# all flat_load (global addresses from the pointer table) re-encoded as global_load so LDS waits (lgkmcnt) no longer stall on outstanding prefetch loads
# baseline (speedup 1.0000x reference)
; __device__ __forceinline__ float silu_f(float x) { return x / (1.f + __expf(-x)); }
; __device__ __forceinline__ void p0_ada(Frame& F, const float* c, const float* ada_w, const float* ada_b, float* mod) {
;     ...
;     for (int i = F.tid; i < NB * D; i += NTHR) { const int b = i / D, k = i % D; cond[k * 8 + b] = silu_f(c[i]); }
;     __syncthreads();
;     const int cq = F.lane & 7, ks = F.lane >> 3;
;     for (int u = blockIdx.x; u < 768; u += F.G) {
;         const int l = u / 384, cb = u % 384;
;         const float* W = ada_w + (size_t)l * D * 6 * D + cb * 32 + cq * 4;
;         f32x4 acc[8];
; #pragma unroll
;         for (int b = 0; b < 8; ++b) acc[b] = (f32x4){0.f, 0.f, 0.f, 0.f};
;         const int kbase = F.wave * 256 + ks;
.LBB0_15:
	global_load_dword v6, v[4:5], off
	v_add_u32_e32 v9, 0x200, v3
	v_lshrrev_b32_e32 v8, 9, v3
	v_cmp_lt_u32_e32 vcc, s10, v3
	v_mov_b32_e32 v3, v9
	v_and_b32_e32 v7, 0x3ff8, v1
	v_lshlrev_b32_e32 v7, 2, v7
	v_and_b32_e32 v8, 0x7ffffc, v8
	v_add3_u32 v7, 0, v7, v8
	s_or_b64 s[6:7], vcc, s[6:7]
	v_add_u32_e32 v1, 0x1000, v1
	v_lshl_add_u64 v[4:5], v[4:5], 0, s[8:9]
	s_waitcnt vmcnt(0) lgkmcnt(0)
	v_mul_f32_e32 v9, 0xbfb8aa3b, v6
	v_exp_f32_e32 v9, v9
	s_nop 0
	v_add_f32_e32 v8, 1.0, v9
	v_div_scale_f32 v9, s[12:13], v8, v8, v6
	v_rcp_f32_e32 v10, v9
	v_div_scale_f32 v11, vcc, v6, v8, v6
	v_fma_f32 v12, -v9, v10, 1.0
	v_fmac_f32_e32 v10, v12, v10
	v_mul_f32_e32 v12, v11, v10
	v_fma_f32 v13, -v9, v12, v11
	v_fmac_f32_e32 v12, v13, v10
	v_fma_f32 v9, -v9, v12, v11
	v_div_fmas_f32 v9, v9, v10, v12
	v_div_fixup_f32 v6, v9, v8, v6
	ds_write_b32 v7, v6
	s_andn2_b64 exec, exec, s[6:7]
	s_cbranch_execnz .LBB0_15
	s_or_b64 exec, exec, s[6:7]
	s_cmpk_gt_i32 s2, 0x2ff
	v_lshrrev_b32_e32 v72, 3, v194
	s_waitcnt lgkmcnt(0)
	s_barrier
	s_cbranch_scc1 .LBB0_25
	v_mbcnt_lo_u32_b32 v1, -1, 0
	v_mbcnt_hi_u32_b32 v3, -1, v1
	v_and_b32_e32 v5, 64, v3
	v_xor_b32_e32 v1, 8, v3
	v_add_u32_e32 v5, 64, v5
	v_cmp_lt_i32_e32 vcc, v1, v5
	v_xor_b32_e32 v6, 16, v3
	s_add_u32 s8, s50, 0x100000
	v_cndmask_b32_e32 v1, v3, v1, vcc
	v_cmp_lt_i32_e32 vcc, v6, v5
	v_readlane_b32 s12, v255, 9
	s_addc_u32 s9, s51, 0
	v_cndmask_b32_e32 v6, v3, v6, vcc
	v_lshlrev_b32_e32 v13, 2, v6
	v_xor_b32_e32 v6, 32, v3
	s_add_i32 s10, 0, 0x10000
	s_lshl_b32 s11, s12, 10
	v_cmp_lt_i32_e32 vcc, v6, v5
	s_add_i32 s11, s11, s10
	v_add_u32_e32 v75, s10, v2
	s_lshl_b32 s10, s12, 13
	v_and_b32_e32 v4, 28, v2
	v_mov_b32_e32 v11, 0
	v_cndmask_b32_e32 v3, v3, v6, vcc
	s_movk_i32 s6, 0x100
	v_and_b32_e32 v6, 31, v0
	s_add_i32 s10, s10, 0
	v_lshlrev_b32_e32 v1, 2, v1
	v_lshlrev_b32_e32 v73, 2, v3
	v_cmp_gt_u32_e32 vcc, 8, v194
	v_cmp_gt_u32_e64 s[6:7], s6, v0
	v_lshl_add_u32 v74, v4, 2, s11
	v_lshrrev_b32_e32 v12, 5, v0
	v_lshl_add_u32 v76, v72, 5, s10
	v_lshl_or_b32 v77, s12, 8, v72
	v_lshlrev_b32_e32 v14, 2, v4
	v_mov_b32_e32 v15, v11
	s_mov_b32 s15, 0xc000
	v_lshlrev_b32_e32 v10, 2, v6
	s_mov_b32 s16, s2
	s_branch .LBB0_19

; __device__ __forceinline__ void p0_ada(Frame& F, const float* c, const float* ada_w, const float* ada_b, float* mod) {
;     ...
; #pragma unroll 4
;         for (int it = 0; it < 32; ++it) {
;             const int k = kbase + 8 * it;
;             const f32x4 w = __builtin_nontemporal_load((const f32x4*)(W + (size_t)k * 6 * D));
;             const f32x4 c0 = *(const f32x4*)(cond + k * 8), c1 = *(const f32x4*)(cond + k * 8 + 4);
;             acc[0] += w * c0[0]; acc[1] += w * c0[1]; acc[2] += w * c0[2]; acc[3] += w * c0[3];
;             acc[4] += w * c1[0]; acc[5] += w * c1[1]; acc[6] += w * c1[2]; acc[7] += w * c1[3];
;         }
.LBB0_20:
	v_add_u32_e32 v51, s12, v77
	v_mad_u64_u32 v[56:57], s[18:19], v51, s15, v[42:43]
	ds_read_b128 v[6:9], v50
	ds_read_b128 v[2:5], v50 offset:16
	ds_read_b128 v[52:55], v50 offset:256
	global_load_dwordx4 v[56:59], v[56:57], off nt
	v_add_u32_e32 v60, 8, v51
	v_add_u32_e32 v61, 16, v51
	v_add_u32_e32 v51, 24, v51
	v_mad_u64_u32 v[78:79], s[18:19], v60, s15, v[42:43]
	v_mad_u64_u32 v[80:81], s[18:19], v61, s15, v[42:43]
	v_mad_u64_u32 v[82:83], s[18:19], v51, s15, v[42:43]
	global_load_dwordx4 v[60:63], v[78:79], off nt
	global_load_dwordx4 v[64:67], v[80:81], off nt
	global_load_dwordx4 v[68:71], v[82:83], off nt
	ds_read_b128 v[78:81], v50 offset:272
	ds_read_b128 v[82:85], v50 offset:512
	ds_read_b128 v[86:89], v50 offset:528
	ds_read_b128 v[90:93], v50 offset:768
	ds_read_b128 v[94:97], v50 offset:784
	s_waitcnt lgkmcnt(0)
	v_mov_b32_e32 v98, v9
	v_mov_b32_e32 v100, v5
	v_mov_b32_e32 v102, v55
	v_mov_b32_e32 v104, v81
	v_mov_b32_e32 v106, v85
	v_mov_b32_e32 v108, v89
	s_add_i32 s12, s12, 32
	v_mov_b32_e32 v110, v93
	v_mov_b32_e32 v112, v97
	v_add_u32_e32 v50, 0x400, v50
	s_cmpk_lg_i32 s12, 0x100
	s_waitcnt vmcnt(0)
	v_pk_fma_f32 v[48:49], v[56:57], v[6:7], v[48:49] op_sel_hi:[1,0,1]
	v_pk_fma_f32 v[46:47], v[58:59], v[6:7], v[46:47] op_sel_hi:[1,0,1]
	v_pk_fma_f32 v[44:45], v[56:57], v[6:7], v[44:45] op_sel:[0,1,0]
	v_pk_fma_f32 v[6:7], v[58:59], v[6:7], v[40:41] op_sel:[0,1,0]
	v_pk_fma_f32 v[38:39], v[56:57], v[8:9], v[38:39] op_sel_hi:[1,0,1]
	v_pk_fma_f32 v[8:9], v[58:59], v[8:9], v[36:37] op_sel_hi:[1,0,1]
	v_pk_fma_f32 v[30:31], v[56:57], v[2:3], v[30:31] op_sel_hi:[1,0,1]
	v_pk_fma_f32 v[28:29], v[58:59], v[2:3], v[28:29] op_sel_hi:[1,0,1]
	v_pk_fma_f32 v[26:27], v[56:57], v[2:3], v[26:27] op_sel:[0,1,0]
	v_pk_fma_f32 v[2:3], v[58:59], v[2:3], v[24:25] op_sel:[0,1,0]
	v_pk_fma_f32 v[22:23], v[56:57], v[4:5], v[22:23] op_sel_hi:[1,0,1]
	v_pk_fma_f32 v[4:5], v[58:59], v[4:5], v[20:21] op_sel_hi:[1,0,1]
	v_pk_fma_f32 v[20:21], v[56:57], v[98:99], v[34:35] op_sel_hi:[1,0,1]
	v_pk_fma_f32 v[24:25], v[58:59], v[98:99], v[32:33] op_sel_hi:[1,0,1]
	v_pk_fma_f32 v[18:19], v[56:57], v[100:101], v[18:19] op_sel_hi:[1,0,1]
	v_pk_fma_f32 v[16:17], v[58:59], v[100:101], v[16:17] op_sel_hi:[1,0,1]
	v_pk_fma_f32 v[32:33], v[62:63], v[52:53], v[46:47] op_sel_hi:[1,0,1]
	v_pk_fma_f32 v[34:35], v[60:61], v[52:53], v[48:49] op_sel_hi:[1,0,1]
	v_pk_fma_f32 v[6:7], v[62:63], v[52:53], v[6:7] op_sel:[0,1,0]
	v_pk_fma_f32 v[36:37], v[60:61], v[52:53], v[44:45] op_sel:[0,1,0]
	v_pk_fma_f32 v[8:9], v[62:63], v[54:55], v[8:9] op_sel_hi:[1,0,1]
	v_pk_fma_f32 v[38:39], v[60:61], v[54:55], v[38:39] op_sel_hi:[1,0,1]
	v_pk_fma_f32 v[28:29], v[62:63], v[78:79], v[28:29] op_sel_hi:[1,0,1]
	v_pk_fma_f32 v[30:31], v[60:61], v[78:79], v[30:31] op_sel_hi:[1,0,1]
	v_pk_fma_f32 v[2:3], v[62:63], v[78:79], v[2:3] op_sel:[0,1,0]
	v_pk_fma_f32 v[26:27], v[60:61], v[78:79], v[26:27] op_sel:[0,1,0]
	v_pk_fma_f32 v[4:5], v[62:63], v[80:81], v[4:5] op_sel_hi:[1,0,1]
	v_pk_fma_f32 v[22:23], v[60:61], v[80:81], v[22:23] op_sel_hi:[1,0,1]
	v_pk_fma_f32 v[24:25], v[62:63], v[102:103], v[24:25] op_sel_hi:[1,0,1]
	v_pk_fma_f32 v[20:21], v[60:61], v[102:103], v[20:21] op_sel_hi:[1,0,1]
	v_pk_fma_f32 v[16:17], v[62:63], v[104:105], v[16:17] op_sel_hi:[1,0,1]
	v_pk_fma_f32 v[18:19], v[60:61], v[104:105], v[18:19] op_sel_hi:[1,0,1]
	v_pk_fma_f32 v[32:33], v[66:67], v[82:83], v[32:33] op_sel_hi:[1,0,1]
	v_pk_fma_f32 v[34:35], v[64:65], v[82:83], v[34:35] op_sel_hi:[1,0,1]
	v_pk_fma_f32 v[6:7], v[66:67], v[82:83], v[6:7] op_sel:[0,1,0]
	v_pk_fma_f32 v[36:37], v[64:65], v[82:83], v[36:37] op_sel:[0,1,0]
	v_pk_fma_f32 v[38:39], v[64:65], v[84:85], v[38:39] op_sel_hi:[1,0,1]
	v_pk_fma_f32 v[8:9], v[66:67], v[84:85], v[8:9] op_sel_hi:[1,0,1]
	v_pk_fma_f32 v[28:29], v[66:67], v[86:87], v[28:29] op_sel_hi:[1,0,1]
	v_pk_fma_f32 v[30:31], v[64:65], v[86:87], v[30:31] op_sel_hi:[1,0,1]
	v_pk_fma_f32 v[2:3], v[66:67], v[86:87], v[2:3] op_sel:[0,1,0]
	v_pk_fma_f32 v[26:27], v[64:65], v[86:87], v[26:27] op_sel:[0,1,0]
	v_pk_fma_f32 v[22:23], v[64:65], v[88:89], v[22:23] op_sel_hi:[1,0,1]
	v_pk_fma_f32 v[4:5], v[66:67], v[88:89], v[4:5] op_sel_hi:[1,0,1]
	v_pk_fma_f32 v[20:21], v[64:65], v[106:107], v[20:21] op_sel_hi:[1,0,1]
	v_pk_fma_f32 v[24:25], v[66:67], v[106:107], v[24:25] op_sel_hi:[1,0,1]
	v_pk_fma_f32 v[18:19], v[64:65], v[108:109], v[18:19] op_sel_hi:[1,0,1]
	v_pk_fma_f32 v[16:17], v[66:67], v[108:109], v[16:17] op_sel_hi:[1,0,1]
	v_pk_fma_f32 v[46:47], v[70:71], v[90:91], v[32:33] op_sel_hi:[1,0,1]
	v_pk_fma_f32 v[48:49], v[68:69], v[90:91], v[34:35] op_sel_hi:[1,0,1]
	v_pk_fma_f32 v[40:41], v[70:71], v[90:91], v[6:7] op_sel:[0,1,0]
	v_pk_fma_f32 v[44:45], v[68:69], v[90:91], v[36:37] op_sel:[0,1,0]
	v_pk_fma_f32 v[36:37], v[70:71], v[92:93], v[8:9] op_sel_hi:[1,0,1]
	v_pk_fma_f32 v[38:39], v[68:69], v[92:93], v[38:39] op_sel_hi:[1,0,1]
	v_pk_fma_f32 v[32:33], v[70:71], v[110:111], v[24:25] op_sel_hi:[1,0,1]
	v_pk_fma_f32 v[34:35], v[68:69], v[110:111], v[20:21] op_sel_hi:[1,0,1]
	v_pk_fma_f32 v[28:29], v[70:71], v[94:95], v[28:29] op_sel_hi:[1,0,1]
	v_pk_fma_f32 v[30:31], v[68:69], v[94:95], v[30:31] op_sel_hi:[1,0,1]
	v_pk_fma_f32 v[24:25], v[70:71], v[94:95], v[2:3] op_sel:[0,1,0]
	v_pk_fma_f32 v[26:27], v[68:69], v[94:95], v[26:27] op_sel:[0,1,0]
	v_pk_fma_f32 v[20:21], v[70:71], v[96:97], v[4:5] op_sel_hi:[1,0,1]
	v_pk_fma_f32 v[22:23], v[68:69], v[96:97], v[22:23] op_sel_hi:[1,0,1]
	v_pk_fma_f32 v[16:17], v[70:71], v[112:113], v[16:17] op_sel_hi:[1,0,1]
	v_pk_fma_f32 v[18:19], v[68:69], v[112:113], v[18:19] op_sel_hi:[1,0,1]
	s_cbranch_scc1 .LBB0_20
; __device__ __forceinline__ void p0_ada(Frame& F, const float* c, const float* ada_w, const float* ada_b, float* mod) {
;     ...
; #pragma unroll
;         for (int b = 0; b < 8; ++b)
; #pragma unroll
;             for (int j = 0; j < 4; ++j) { float v = acc[b][j]; v += __shfl_xor(v, 8); v += __shfl_xor(v, 16); v += __shfl_xor(v, 32); acc[b][j] = v; }
;         if (F.lane < 8) {
; #pragma unroll
;             for (int b = 0; b < 8; ++b) *(f32x4*)(part + (F.wave * 8 + b) * 32 + cq * 4) = acc[b];
;         }
	ds_bpermute_b32 v2, v1, v48
	ds_bpermute_b32 v3, v1, v49
	ds_bpermute_b32 v50, v1, v36
	ds_bpermute_b32 v51, v1, v37
	ds_bpermute_b32 v60, v1, v26
	ds_bpermute_b32 v61, v1, v27
	s_waitcnt lgkmcnt(4)
	v_pk_add_f32 v[2:3], v[48:49], v[2:3]
	ds_bpermute_b32 v48, v1, v40
	ds_bpermute_b32 v49, v1, v41
	s_waitcnt lgkmcnt(4)
	v_pk_add_f32 v[50:51], v[36:37], v[50:51]
	ds_bpermute_b32 v52, v13, v50
	ds_bpermute_b32 v53, v13, v51
	s_waitcnt lgkmcnt(4)
	v_pk_add_f32 v[26:27], v[26:27], v[60:61]
	s_waitcnt lgkmcnt(2)
	v_pk_add_f32 v[40:41], v[40:41], v[48:49]
	ds_bpermute_b32 v48, v1, v38
	ds_bpermute_b32 v49, v1, v39
	ds_bpermute_b32 v64, v1, v22
	ds_bpermute_b32 v65, v1, v23
	ds_bpermute_b32 v4, v1, v46
	ds_bpermute_b32 v5, v1, v47
	s_waitcnt lgkmcnt(4)
	v_pk_add_f32 v[38:39], v[38:39], v[48:49]
	ds_bpermute_b32 v48, v13, v38
	ds_bpermute_b32 v49, v13, v39
	ds_bpermute_b32 v8, v1, v44
	ds_bpermute_b32 v9, v1, v45
	ds_bpermute_b32 v54, v1, v32
	ds_bpermute_b32 v55, v1, v33
	s_waitcnt lgkmcnt(4)
	v_pk_add_f32 v[36:37], v[38:39], v[48:49]
	v_pk_add_f32 v[48:49], v[50:51], v[52:53]
	ds_bpermute_b32 v52, v1, v34
	ds_bpermute_b32 v53, v1, v35
	ds_bpermute_b32 v58, v1, v30
	ds_bpermute_b32 v59, v1, v31
	ds_bpermute_b32 v62, v13, v26
	ds_bpermute_b32 v63, v13, v27
	ds_bpermute_b32 v6, v13, v2
	ds_bpermute_b32 v7, v13, v3
	v_pk_add_f32 v[22:23], v[22:23], v[64:65]
	v_pk_add_f32 v[42:43], v[46:47], v[4:5]
	s_waitcnt lgkmcnt(10)
	v_pk_add_f32 v[8:9], v[44:45], v[8:9]
	s_waitcnt lgkmcnt(6)
	v_pk_add_f32 v[34:35], v[34:35], v[52:53]
	v_pk_add_f32 v[54:55], v[32:33], v[54:55]
	s_waitcnt lgkmcnt(4)
	v_pk_add_f32 v[30:31], v[30:31], v[58:59]
	ds_bpermute_b32 v58, v1, v28
	ds_bpermute_b32 v59, v1, v29
	s_waitcnt lgkmcnt(4)
	v_pk_add_f32 v[26:27], v[26:27], v[62:63]
	ds_bpermute_b32 v62, v1, v24
	ds_bpermute_b32 v63, v1, v25
	ds_bpermute_b32 v64, v13, v22
	ds_bpermute_b32 v65, v13, v23
	ds_bpermute_b32 v66, v1, v20
	ds_bpermute_b32 v67, v1, v21
	ds_bpermute_b32 v68, v1, v18
	ds_bpermute_b32 v69, v1, v19
	ds_bpermute_b32 v70, v1, v16
	ds_bpermute_b32 v71, v1, v17
	s_waitcnt lgkmcnt(12)
	v_pk_add_f32 v[2:3], v[2:3], v[6:7]
	ds_bpermute_b32 v6, v13, v42
	ds_bpermute_b32 v7, v13, v43
	ds_bpermute_b32 v46, v13, v8
	ds_bpermute_b32 v47, v13, v9
	ds_bpermute_b32 v52, v13, v34
	ds_bpermute_b32 v53, v13, v35
	ds_bpermute_b32 v56, v13, v54
	ds_bpermute_b32 v57, v13, v55
	s_waitcnt lgkmcnt(14)
	v_pk_add_f32 v[28:29], v[28:29], v[58:59]
	v_pk_add_f32 v[24:25], v[24:25], v[62:63]
	v_pk_add_f32 v[22:23], v[22:23], v[64:65]
	s_waitcnt lgkmcnt(12)
	v_pk_add_f32 v[64:65], v[20:21], v[66:67]
	s_waitcnt lgkmcnt(10)
	v_pk_add_f32 v[18:19], v[18:19], v[68:69]
	s_waitcnt lgkmcnt(8)
	v_pk_add_f32 v[70:71], v[16:17], v[70:71]
	s_waitcnt lgkmcnt(6)
	v_pk_add_f32 v[42:43], v[42:43], v[6:7]
	s_waitcnt lgkmcnt(4)
	v_pk_add_f32 v[6:7], v[8:9], v[46:47]
	ds_bpermute_b32 v46, v13, v40
	ds_bpermute_b32 v47, v13, v41
	s_waitcnt lgkmcnt(4)
	v_pk_add_f32 v[32:33], v[34:35], v[52:53]
	s_waitcnt lgkmcnt(2)
	v_pk_add_f32 v[52:53], v[54:55], v[56:57]
	ds_bpermute_b32 v56, v13, v30
	ds_bpermute_b32 v57, v13, v31
	ds_bpermute_b32 v58, v13, v28
	ds_bpermute_b32 v59, v13, v29
	ds_bpermute_b32 v62, v13, v24
	ds_bpermute_b32 v63, v13, v25
	ds_bpermute_b32 v66, v13, v64
	ds_bpermute_b32 v67, v13, v65
	ds_bpermute_b32 v68, v13, v18
	ds_bpermute_b32 v69, v13, v19
	ds_bpermute_b32 v78, v13, v70
	ds_bpermute_b32 v79, v13, v71
	s_waitcnt lgkmcnt(12)
	v_pk_add_f32 v[40:41], v[40:41], v[46:47]
	s_waitcnt lgkmcnt(10)
	v_pk_add_f32 v[30:31], v[30:31], v[56:57]
	s_waitcnt lgkmcnt(8)
	v_pk_add_f32 v[58:59], v[28:29], v[58:59]
	s_waitcnt lgkmcnt(6)
	v_pk_add_f32 v[24:25], v[24:25], v[62:63]
	s_waitcnt lgkmcnt(4)
	v_pk_add_f32 v[64:65], v[64:65], v[66:67]
	s_waitcnt lgkmcnt(2)
	v_pk_add_f32 v[16:17], v[18:19], v[68:69]
	s_waitcnt lgkmcnt(0)
	v_pk_add_f32 v[68:69], v[70:71], v[78:79]
	ds_bpermute_b32 v4, v73, v2
	ds_bpermute_b32 v5, v73, v3
	ds_bpermute_b32 v44, v73, v42
	ds_bpermute_b32 v45, v73, v43
	ds_bpermute_b32 v8, v73, v6
	ds_bpermute_b32 v9, v73, v7
	ds_bpermute_b32 v46, v73, v40
	ds_bpermute_b32 v47, v73, v41
	ds_bpermute_b32 v38, v73, v36
	ds_bpermute_b32 v39, v73, v37
	ds_bpermute_b32 v50, v73, v48
	ds_bpermute_b32 v51, v73, v49
	ds_bpermute_b32 v34, v73, v32
	ds_bpermute_b32 v35, v73, v33
	ds_bpermute_b32 v54, v73, v52
	ds_bpermute_b32 v55, v73, v53
	ds_bpermute_b32 v56, v73, v30
	ds_bpermute_b32 v57, v73, v31
	ds_bpermute_b32 v60, v73, v58
	ds_bpermute_b32 v61, v73, v59
	ds_bpermute_b32 v28, v73, v26
	ds_bpermute_b32 v29, v73, v27
	ds_bpermute_b32 v62, v73, v24
	ds_bpermute_b32 v63, v73, v25
	ds_bpermute_b32 v20, v73, v22
	ds_bpermute_b32 v21, v73, v23
	ds_bpermute_b32 v66, v73, v64
	ds_bpermute_b32 v67, v73, v65
	ds_bpermute_b32 v18, v73, v16
	ds_bpermute_b32 v19, v73, v17
	ds_bpermute_b32 v70, v73, v68
	ds_bpermute_b32 v71, v73, v69
	s_and_saveexec_b64 s[12:13], vcc
	s_cbranch_execz .LBB0_23
	s_waitcnt lgkmcnt(14)
	v_pk_add_f32 v[44:45], v[42:43], v[44:45]
	v_pk_add_f32 v[42:43], v[2:3], v[4:5]
	v_pk_add_f32 v[4:5], v[40:41], v[46:47]
	v_pk_add_f32 v[2:3], v[6:7], v[8:9]
	ds_write_b128 v74, v[2:5] offset:128
	v_pk_add_f32 v[4:5], v[48:49], v[50:51]
	v_pk_add_f32 v[2:3], v[36:37], v[38:39]
	ds_write_b128 v74, v[2:5] offset:256
	v_pk_add_f32 v[4:5], v[52:53], v[54:55]
	v_pk_add_f32 v[2:3], v[32:33], v[34:35]
	ds_write_b128 v74, v[2:5] offset:384
	s_waitcnt lgkmcnt(14)
	v_pk_add_f32 v[4:5], v[58:59], v[60:61]
	v_pk_add_f32 v[2:3], v[30:31], v[56:57]
	ds_write_b128 v74, v[2:5] offset:512
	s_waitcnt lgkmcnt(12)
	v_pk_add_f32 v[4:5], v[24:25], v[62:63]
	v_pk_add_f32 v[2:3], v[26:27], v[28:29]
	ds_write_b128 v74, v[2:5] offset:640
	s_waitcnt lgkmcnt(9)
	v_pk_add_f32 v[4:5], v[64:65], v[66:67]
	v_pk_add_f32 v[2:3], v[22:23], v[20:21]
	ds_write_b128 v74, v[2:5] offset:768
	s_waitcnt lgkmcnt(6)
	v_pk_add_f32 v[4:5], v[68:69], v[70:71]
	v_pk_add_f32 v[2:3], v[16:17], v[18:19]
	ds_write_b128 v74, v[42:45]
	ds_write_b128 v74, v[2:5] offset:896
; __device__ __forceinline__ void p0_ada(Frame& F, const float* c, const float* ada_w, const float* ada_b, float* mod) {
;     ...
;         __syncthreads();
;         if (F.tid < 256) { const int b = F.tid >> 5, col = F.tid & 31; float s = ada_b[(size_t)l * 6 * D + cb * 32 + col];
; #pragma unroll
;           for (int w = 0; w < 8; ++w) s += part[(w * 8 + b) * 32 + col];
;           mod[((size_t)l * NB + b) * 6 * D + cb * 32 + col] = s; }
;         __syncthreads();
.LBB0_23:
	s_or_b64 exec, exec, s[12:13]
	s_waitcnt lgkmcnt(0)
	s_barrier
	s_and_saveexec_b64 s[12:13], s[6:7]
	s_cbranch_execz .LBB0_18
	s_mul_i32 s19, s17, 0xc000
	s_mul_hi_i32 s18, s17, 0xc000
	s_add_u32 s19, s5, s19
	s_addc_u32 s20, s14, s18
	s_add_u32 s18, s19, s10
	s_addc_u32 s19, s20, s11
	v_lshl_add_u64 v[2:3], s[18:19], 0, v[10:11]
	global_load_dword v18, v[2:3], off
	ds_read2st64_b32 v[2:3], v75 offset1:4
	ds_read2st64_b32 v[4:5], v75 offset0:8 offset1:12
	ds_read2st64_b32 v[6:7], v75 offset0:16 offset1:20
	ds_read2st64_b32 v[8:9], v75 offset0:24 offset1:28
	v_lshl_or_b32 v19, s17, 3, v12
	v_mov_b64_e32 v[16:17], s[8:9]
	v_mad_i64_i32 v[16:17], s[18:19], v19, s15, v[16:17]
	v_lshl_add_u64 v[16:17], v[16:17], 0, s[10:11]
	s_waitcnt vmcnt(0) lgkmcnt(0)
	v_add_f32_e32 v2, v18, v2
	v_add_f32_e32 v2, v2, v3
	v_add_f32_e32 v2, v2, v4
	v_add_f32_e32 v2, v2, v5
	v_add_f32_e32 v2, v2, v6
	v_add_f32_e32 v2, v2, v7
	v_add_f32_e32 v2, v2, v8
	v_add_f32_e32 v4, v2, v9
	v_lshl_add_u64 v[2:3], v[16:17], 0, v[10:11]
	global_store_dword v[2:3], v4, off
	s_branch .LBB0_18

; __device__ __forceinline__ void colmax_item(const float* src, int ld, int k0, int c0, float* cmx  , int lane) {
;     const int c = lane & 7, q = lane >> 3;
;     f32x4 mx = (f32x4){0.f, 0.f, 0.f, 0.f};
; #pragma unroll
;     for (int g = 0; g < 4; ++g)
; #pragma unroll
;         for (int j = 0; j < 4; ++j) { const f32x4 v = *(const f32x4*)(src + (size_t)(k0 + 32 * g + 4 * q + j) * ld + c0 + 4 * c);
;             mx[0] = fmaxf(mx[0], fabsf(v[0])); mx[1] = fmaxf(mx[1], fabsf(v[1])); mx[2] = fmaxf(mx[2], fabsf(v[2])); mx[3] = fmaxf(mx[3], fabsf(v[3])); }
; #pragma unroll
;     for (int i = 0; i < 4; ++i) { float v = mx[i]; v = fmaxf(v, __shfl_xor(v, 8)); v = fmaxf(v, __shfl_xor(v, 16)); v = fmaxf(v, __shfl_xor(v, 32)); mx[i] = v; }
;     if (q == 0) {
; #pragma unroll
;         for (int i = 0; i < 4; ++i) atomicMax((unsigned*)(cmx + 4 * c + i), __float_as_uint(mx[i] * CMS_F)); }
; }
; template <int GRP>
; __device__ __forceinline__ void conv_item(Frame& F, int r) {
;     ...
;         if (r < NI) { const int kb = r / 152, nb = r % 152, c0 = (nb < 112) ? nb * 32 : SRC_GATE + 8 + (nb - 112) * 32, drow = nb * 32;
;             if (QUANT) cvt_item_i8(inptr(F, IN_WIN) + (size_t)l * D * NIN_SRC, NIN_SRC, kb * 128, c0, ws + WS_WIN + (size_t)l * NIN * D, D, drow, cmx + CMX_WIN + l * NIN + drow, scr, F.lane);
;             else colmax_item(inptr(F, IN_WIN) + (size_t)l * D * NIN_SRC, NIN_SRC, kb * 128, c0, cmx + CMX_WIN + l * NIN + drow, F.lane);
.LBB0_31:
	s_mul_hi_i32 s8, s37, 0x6bca1af3
	s_lshr_b32 s12, s8, 31
	s_ashr_i32 s8, s8, 6
	s_add_i32 s8, s8, s12
	s_mul_i32 s12, s8, 0xffffff68
	s_add_i32 s13, s37, s12
	s_mul_i32 s12, s8, 0xffffed00
	v_mov_b32_e32 v2, s5
	s_waitcnt lgkmcnt(3)
	ds_read_b64 v[2:3], v2
	s_add_i32 s12, s3, s12
	s_add_i32 s14, s12, 8
	s_cmpk_lt_i32 s13, 0x70
	s_cselect_b32 s14, s12, s14
	s_ashr_i32 s15, s14, 31
	s_waitcnt lgkmcnt(0)
	v_readfirstlane_b32 s13, v2
	s_lshl_b64 s[14:15], s[14:15], 2
	v_readfirstlane_b32 s38, v3
	s_add_u32 s14, s13, s14
	v_lshl_or_b32 v73, s8, 7, v1
	s_addc_u32 s15, s38, s15
	v_lshl_add_u64 v[86:87], s[14:15], 0, v[10:11]
	v_or_b32_e32 v4, 1, v73
	v_mad_i64_i32 v[2:3], s[14:15], v73, s16, v[86:87]
	v_mad_i64_i32 v[6:7], s[14:15], v4, s16, v[86:87]
	v_or_b32_e32 v36, 2, v73
	v_or_b32_e32 v38, 3, v73
	global_load_dwordx4 v[2:5], v[2:3], off
	s_nop 0
	global_load_dwordx4 v[6:9], v[6:7], off
	v_mad_i64_i32 v[36:37], s[14:15], v36, s16, v[86:87]
	v_mad_i64_i32 v[40:41], s[14:15], v38, s16, v[86:87]
	v_or_b32_e32 v44, 32, v73
	v_or_b32_e32 v46, 33, v73
	global_load_dwordx4 v[36:39], v[36:37], off
	s_nop 0
	global_load_dwordx4 v[40:43], v[40:41], off
	v_mad_i64_i32 v[44:45], s[14:15], v44, s16, v[86:87]
	v_mad_i64_i32 v[48:49], s[14:15], v46, s16, v[86:87]
	v_or_b32_e32 v52, 34, v73
	v_or_b32_e32 v54, 35, v73
	global_load_dwordx4 v[44:47], v[44:45], off
	s_nop 0
	global_load_dwordx4 v[48:51], v[48:49], off
	v_mad_i64_i32 v[52:53], s[14:15], v52, s16, v[86:87]
	v_mad_i64_i32 v[56:57], s[14:15], v54, s16, v[86:87]
	v_or_b32_e32 v60, 64, v73
	v_or_b32_e32 v62, 0x41, v73
	global_load_dwordx4 v[52:55], v[52:53], off
	s_nop 0
	global_load_dwordx4 v[56:59], v[56:57], off
	v_mad_i64_i32 v[60:61], s[14:15], v60, s16, v[86:87]
	v_mad_i64_i32 v[64:65], s[14:15], v62, s16, v[86:87]
	v_or_b32_e32 v68, 0x42, v73
	v_or_b32_e32 v70, 0x43, v73
	global_load_dwordx4 v[60:63], v[60:61], off
	s_nop 0
	global_load_dwordx4 v[64:67], v[64:65], off
	v_mad_i64_i32 v[68:69], s[14:15], v68, s16, v[86:87]
	v_mad_i64_i32 v[74:75], s[14:15], v70, s16, v[86:87]
	v_or_b32_e32 v78, 0x60, v73
	v_or_b32_e32 v80, 0x61, v73
	global_load_dwordx4 v[68:71], v[68:69], off
	s_nop 0
	global_load_dwordx4 v[74:77], v[74:75], off
	v_mad_i64_i32 v[78:79], s[14:15], v78, s16, v[86:87]
	v_mad_i64_i32 v[82:83], s[14:15], v80, s16, v[86:87]
	v_or_b32_e32 v88, 0x62, v73
	v_or_b32_e32 v73, 0x63, v73
	global_load_dwordx4 v[78:81], v[78:79], off
	s_nop 0
	global_load_dwordx4 v[82:85], v[82:83], off
	v_mad_i64_i32 v[88:89], s[14:15], v88, s16, v[86:87]
	v_mad_i64_i32 v[90:91], s[14:15], v73, s16, v[86:87]
	global_load_dwordx4 v[86:89], v[88:89], off
	s_nop 0
	global_load_dwordx4 v[90:93], v[90:91], off
	v_cmp_lt_i32_e32 vcc, v30, v31
	s_waitcnt vmcnt(0) lgkmcnt(0)
	v_max3_f32 v4, |v4|, 0, |v8|
	v_max3_f32 v2, |v2|, 0, |v6|
	v_max3_f32 v3, |v3|, 0, |v7|
	v_max3_f32 v5, |v5|, 0, |v9|
	v_max3_f32 v4, v4, |v38|, |v42|
	v_max3_f32 v2, v2, |v36|, |v40|
	v_max3_f32 v3, v3, |v37|, |v41|
	v_max3_f32 v5, v5, |v39|, |v43|
	v_max3_f32 v4, v4, |v46|, |v50|
	v_max3_f32 v2, v2, |v44|, |v48|
	v_max3_f32 v3, v3, |v45|, |v49|
	v_max3_f32 v5, v5, |v47|, |v51|
	v_max3_f32 v4, v4, |v54|, |v58|
	v_max3_f32 v2, v2, |v52|, |v56|
	v_max3_f32 v3, v3, |v53|, |v57|
	v_max3_f32 v5, v5, |v55|, |v59|
	v_max3_f32 v4, v4, |v62|, |v66|
	v_max3_f32 v2, v2, |v60|, |v64|
	v_max3_f32 v3, v3, |v61|, |v65|
	v_max3_f32 v5, v5, |v63|, |v67|
	v_max3_f32 v4, v4, |v70|, |v76|
	v_max3_f32 v2, v2, |v68|, |v74|
	v_max3_f32 v3, v3, |v69|, |v75|
	v_max3_f32 v5, v5, |v71|, |v77|
	v_max3_f32 v4, v4, |v80|, |v84|
	v_max3_f32 v2, v2, |v78|, |v82|
	v_max3_f32 v3, v3, |v79|, |v83|
	v_max3_f32 v5, v5, |v81|, |v85|
	v_max3_f32 v6, v4, |v88|, |v92|
	v_cndmask_b32_e32 v4, v29, v30, vcc
	v_max3_f32 v2, v2, |v86|, |v90|
	v_lshlrev_b32_e32 v4, 2, v4
	ds_bpermute_b32 v8, v4, v2
	v_max3_f32 v3, v3, |v87|, |v91|
	v_cmp_lt_i32_e32 vcc, v32, v31
	ds_bpermute_b32 v36, v4, v3
	v_max3_f32 v5, v5, |v89|, |v93|
	v_cndmask_b32_e32 v7, v29, v32, vcc
	s_waitcnt lgkmcnt(1)
	v_max_f32_e32 v8, v8, v8
	v_lshlrev_b32_e32 v7, 2, v7
	v_max_f32_e32 v2, v2, v8
	ds_bpermute_b32 v8, v7, v2
	s_waitcnt lgkmcnt(1)
	v_max_f32_e32 v36, v36, v36
	v_max_f32_e32 v36, v3, v36
	ds_bpermute_b32 v37, v7, v36
	ds_bpermute_b32 v38, v4, v5
	s_waitcnt lgkmcnt(2)
	v_max_f32_e32 v3, v8, v8
	ds_bpermute_b32 v8, v4, v6
	v_cmp_lt_i32_e32 vcc, v33, v31
	s_waitcnt lgkmcnt(2)
	v_max_f32_e32 v37, v37, v37
	v_max_f32_e32 v4, v36, v37
	s_waitcnt lgkmcnt(1)
	v_max_f32_e32 v36, v38, v38
	s_waitcnt lgkmcnt(0)
	v_max_f32_e32 v8, v8, v8
	v_max_f32_e32 v6, v6, v8
	v_max_f32_e32 v36, v5, v36
	ds_bpermute_b32 v8, v7, v6
	ds_bpermute_b32 v37, v7, v36
	v_cndmask_b32_e32 v9, v29, v33, vcc
	v_lshlrev_b32_e32 v9, 2, v9
	v_max_f32_e32 v2, v2, v3
	s_waitcnt lgkmcnt(1)
	v_max_f32_e32 v7, v8, v8
	s_waitcnt lgkmcnt(0)
	v_max_f32_e32 v8, v37, v37
	v_max_f32_e32 v6, v6, v7
	v_max_f32_e32 v8, v36, v8
	ds_bpermute_b32 v3, v9, v2
	ds_bpermute_b32 v5, v9, v4
	ds_bpermute_b32 v7, v9, v6
	ds_bpermute_b32 v9, v9, v8
	s_and_saveexec_b64 s[14:15], s[6:7]
	s_cbranch_execz .LBB0_33
	s_waitcnt lgkmcnt(2)
	v_max_f32_e32 v5, v5, v5
	v_max_f32_e32 v4, v4, v4
	v_max_f32_e32 v3, v3, v3
	v_max_f32_e32 v2, v2, v2
	s_ashr_i32 s13, s12, 31
	v_max_f32_e32 v4, v4, v5
	v_max_f32_e32 v5, v2, v3
	s_waitcnt lgkmcnt(1)
	v_max_f32_e32 v7, v7, v7
	v_max_f32_e32 v6, v6, v6
	v_lshl_add_u64 v[2:3], s[12:13], 2, v[12:13]
	v_mul_f32_e32 v5, 0x3fb33333, v5
	s_waitcnt lgkmcnt(0)
	v_max_f32_e32 v9, v9, v9
	v_max_f32_e32 v8, v8, v8
	v_max_f32_e32 v6, v6, v7
	global_atomic_umax v[2:3], v5, off
	v_mul_f32_e32 v4, 0x3fb33333, v4
	v_max_f32_e32 v8, v8, v9
	global_atomic_umax v[2:3], v4, off offset:4
	v_mul_f32_e32 v4, 0x3fb33333, v6
	global_atomic_umax v[2:3], v4, off offset:8
	v_mul_f32_e32 v4, 0x3fb33333, v8
	global_atomic_umax v[2:3], v4, off offset:12

; __device__ __forceinline__ void colmax_item(const float* src, int ld, int k0, int c0, float* cmx  , int lane) {
;     const int c = lane & 7, q = lane >> 3;
;     f32x4 mx = (f32x4){0.f, 0.f, 0.f, 0.f};
; #pragma unroll
;     for (int g = 0; g < 4; ++g)
; #pragma unroll
;         for (int j = 0; j < 4; ++j) { const f32x4 v = *(const f32x4*)(src + (size_t)(k0 + 32 * g + 4 * q + j) * ld + c0 + 4 * c);
;             mx[0] = fmaxf(mx[0], fabsf(v[0])); mx[1] = fmaxf(mx[1], fabsf(v[1])); mx[2] = fmaxf(mx[2], fabsf(v[2])); mx[3] = fmaxf(mx[3], fabsf(v[3])); }
; #pragma unroll
;     for (int i = 0; i < 4; ++i) { float v = mx[i]; v = fmaxf(v, __shfl_xor(v, 8)); v = fmaxf(v, __shfl_xor(v, 16)); v = fmaxf(v, __shfl_xor(v, 32)); mx[i] = v; }
;     if (q == 0) {
; #pragma unroll
;         for (int i = 0; i < 4; ++i) atomicMax((unsigned*)(cmx + 4 * c + i), __float_as_uint(mx[i] * CMS_F)); }
; }
; template <int GRP>
; __device__ __forceinline__ void conv_item(Frame& F, int r) {
;     ...
;     if (GRP == 0 || GRP == 1) { constexpr int KBN = (GRP == 1) ? 16 : CMS_KB, I_F = KBN * 176; const int up = r / I_F; r %= I_F; const int kb = r / 176, nb = r % 176, n0 = nb * 32, drow = (n0 >> 7) * 256 + up * 128 + (n0 & 127);
;         if (GRP == 1) cvt_item_i8(inptr(F, up ? IN_FU : IN_FG), DFF, kb * 128, n0, ws + WS_WGU, D, drow, cmx + drow, scr, F.lane);
;         else colmax_item(inptr(F, up ? IN_FU : IN_FG), DFF, kb * 128, n0, cmx + drow, F.lane); }
.LBB0_35:
	s_cmpk_gt_i32 s12, 0x3ff
	s_mov_b64 s[10:11], -1
	s_cbranch_scc0 .LBB0_43
	s_cmpk_gt_u32 s12, 0xeff
	s_cbranch_scc0 .LBB0_40
	s_add_i32 s13, s12, 0xfffff100
	s_add_i32 s8, s12, 0xffffefa0
	s_cmpk_lt_u32 s13, 0x160
	s_cselect_b32 s15, s13, s8
	v_sub_co_u32_e32 v2, vcc, s15, v34
	s_and_b64 s[10:11], vcc, exec
	v_readfirstlane_b32 s8, v2
	s_cselect_b32 s14, s15, s8
	s_lshl_b32 s8, s14, 5
	s_add_i32 s10, s12, 0xfffff25f
	s_cmpk_lt_u32 s10, 0x2bf
	s_cselect_b32 s10, s17, 0x88
	s_add_i32 s10, s10, 0
	s_add_i32 s10, s10, 0x20200
	v_mov_b32_e32 v2, s10
	s_waitcnt lgkmcnt(3)
	ds_read_b64 v[2:3], v2
	s_cmpk_gt_u32 s15, 0xaf
	s_cselect_b32 s10, 0x80, 0
	v_or_b32_e32 v4, s10, v1
	s_lshl_b64 s[10:11], s[8:9], 2
	s_waitcnt lgkmcnt(0)
	v_readfirstlane_b32 s15, v2
	v_readfirstlane_b32 s38, v3
	s_add_u32 s10, s15, s10
	s_addc_u32 s11, s38, s11
	v_lshl_add_u64 v[2:3], s[10:11], 0, v[10:11]
	v_mul_u32_u24_e32 v4, 0x5800, v4
	v_mov_b32_e32 v5, v11
	v_lshl_add_u64 v[86:87], v[2:3], 0, v[4:5]
	v_add_co_u32_e32 v6, vcc, s18, v86
	s_nop 1
	v_addc_co_u32_e32 v7, vcc, 0, v87, vcc
	v_add_co_u32_e32 v36, vcc, s19, v86
	global_load_dwordx4 v[2:5], v[86:87], off
	s_nop 0
	global_load_dwordx4 v[6:9], v[6:7], off offset:2048
	v_addc_co_u32_e32 v37, vcc, 0, v87, vcc
	v_add_co_u32_e32 v40, vcc, s20, v86
	s_waitcnt vmcnt(0) lgkmcnt(0)
	v_max3_f32 v4, |v4|, 0, |v8|
	v_addc_co_u32_e32 v41, vcc, 0, v87, vcc
	v_add_co_u32_e32 v44, vcc, s21, v86
	global_load_dwordx4 v[36:39], v[36:37], off
	s_nop 0
	global_load_dwordx4 v[40:43], v[40:41], off offset:2048
	v_addc_co_u32_e32 v45, vcc, 0, v87, vcc
	v_add_co_u32_e32 v48, vcc, s22, v86
	v_max3_f32 v2, |v2|, 0, |v6|
	s_nop 0
	v_addc_co_u32_e32 v49, vcc, 0, v87, vcc
	v_add_co_u32_e32 v52, vcc, s23, v86
	global_load_dwordx4 v[44:47], v[44:45], off
	s_nop 0
	global_load_dwordx4 v[48:51], v[48:49], off offset:2048
	v_addc_co_u32_e32 v53, vcc, 0, v87, vcc
	v_add_co_u32_e32 v56, vcc, s24, v86
	v_max3_f32 v3, |v3|, 0, |v7|
	s_nop 0
	v_addc_co_u32_e32 v57, vcc, 0, v87, vcc
	v_add_co_u32_e32 v60, vcc, s25, v86
	global_load_dwordx4 v[52:55], v[52:53], off
	s_nop 0
	global_load_dwordx4 v[56:59], v[56:57], off offset:2048
	v_addc_co_u32_e32 v61, vcc, 0, v87, vcc
	v_add_co_u32_e32 v64, vcc, s26, v86
	v_max3_f32 v5, |v5|, 0, |v9|
	s_nop 0
	v_addc_co_u32_e32 v65, vcc, 0, v87, vcc
	v_add_co_u32_e32 v68, vcc, s27, v86
	global_load_dwordx4 v[60:63], v[60:61], off
	s_nop 0
	global_load_dwordx4 v[64:67], v[64:65], off offset:2048
	v_addc_co_u32_e32 v69, vcc, 0, v87, vcc
	v_add_co_u32_e32 v74, vcc, s28, v86
	s_waitcnt vmcnt(0) lgkmcnt(0)
	v_max3_f32 v4, v4, |v38|, |v42|
	v_addc_co_u32_e32 v75, vcc, 0, v87, vcc
	v_add_co_u32_e32 v78, vcc, s29, v86
	global_load_dwordx4 v[68:71], v[68:69], off
	s_nop 0
	global_load_dwordx4 v[74:77], v[74:75], off offset:2048
	v_addc_co_u32_e32 v79, vcc, 0, v87, vcc
	v_add_co_u32_e32 v82, vcc, s30, v86
	v_max3_f32 v2, v2, |v36|, |v40|
	s_nop 0
	v_addc_co_u32_e32 v83, vcc, 0, v87, vcc
	v_add_co_u32_e32 v88, vcc, s31, v86
	global_load_dwordx4 v[78:81], v[78:79], off
	s_nop 0
	global_load_dwordx4 v[82:85], v[82:83], off offset:2048
	v_addc_co_u32_e32 v89, vcc, 0, v87, vcc
	v_add_co_u32_e32 v90, vcc, s33, v86
	v_max3_f32 v4, v4, |v46|, |v50|
	s_nop 0
	v_addc_co_u32_e32 v91, vcc, 0, v87, vcc
	global_load_dwordx4 v[86:89], v[88:89], off
	s_nop 0
	global_load_dwordx4 v[90:93], v[90:91], off offset:2048
	v_max3_f32 v2, v2, |v44|, |v48|
	v_max3_f32 v4, v4, |v54|, |v58|
	v_max3_f32 v2, v2, |v52|, |v56|
	v_max3_f32 v3, v3, |v37|, |v41|
	v_cmp_lt_i32_e32 vcc, v30, v31
	v_max3_f32 v3, v3, |v45|, |v49|
	v_max3_f32 v4, v4, |v62|, |v66|
	v_max3_f32 v2, v2, |v60|, |v64|
	v_max3_f32 v3, v3, |v53|, |v57|
	v_max3_f32 v3, v3, |v61|, |v65|
	v_max3_f32 v5, v5, |v39|, |v43|
	v_max3_f32 v5, v5, |v47|, |v51|
	v_max3_f32 v5, v5, |v55|, |v59|
	v_max3_f32 v5, v5, |v63|, |v67|
	s_waitcnt vmcnt(0) lgkmcnt(0)
	v_max3_f32 v4, v4, |v70|, |v76|
	v_max3_f32 v2, v2, |v68|, |v74|
	v_max3_f32 v3, v3, |v69|, |v75|
	v_max3_f32 v5, v5, |v71|, |v77|
	v_max3_f32 v4, v4, |v80|, |v84|
	v_max3_f32 v2, v2, |v78|, |v82|
	v_max3_f32 v3, v3, |v79|, |v83|
	v_max3_f32 v5, v5, |v81|, |v85|
	v_max3_f32 v6, v4, |v88|, |v92|
	v_cndmask_b32_e32 v4, v29, v30, vcc
	v_max3_f32 v2, v2, |v86|, |v90|
	v_lshlrev_b32_e32 v4, 2, v4
	ds_bpermute_b32 v8, v4, v2
	v_max3_f32 v3, v3, |v87|, |v91|
	v_cmp_lt_i32_e32 vcc, v32, v31
	ds_bpermute_b32 v36, v4, v3
	v_max3_f32 v5, v5, |v89|, |v93|
	v_cndmask_b32_e32 v7, v29, v32, vcc
	s_waitcnt lgkmcnt(1)
	v_max_f32_e32 v8, v8, v8
	v_lshlrev_b32_e32 v7, 2, v7
	v_max_f32_e32 v2, v2, v8
	ds_bpermute_b32 v8, v7, v2
	s_waitcnt lgkmcnt(1)
	v_max_f32_e32 v36, v36, v36
	v_max_f32_e32 v36, v3, v36
	ds_bpermute_b32 v37, v7, v36
	ds_bpermute_b32 v38, v4, v5
	s_waitcnt lgkmcnt(2)
	v_max_f32_e32 v3, v8, v8
	ds_bpermute_b32 v8, v4, v6
	v_cmp_lt_i32_e32 vcc, v33, v31
	s_waitcnt lgkmcnt(2)
	v_max_f32_e32 v37, v37, v37
	v_max_f32_e32 v4, v36, v37
	s_waitcnt lgkmcnt(1)
	v_max_f32_e32 v36, v38, v38
	s_waitcnt lgkmcnt(0)
	v_max_f32_e32 v8, v8, v8
	v_max_f32_e32 v6, v6, v8
	v_max_f32_e32 v36, v5, v36
	ds_bpermute_b32 v8, v7, v6
	ds_bpermute_b32 v37, v7, v36
	v_cndmask_b32_e32 v9, v29, v33, vcc
	v_lshlrev_b32_e32 v9, 2, v9
	v_max_f32_e32 v2, v2, v3
	s_waitcnt lgkmcnt(1)
	v_max_f32_e32 v7, v8, v8
	s_waitcnt lgkmcnt(0)
	v_max_f32_e32 v8, v37, v37
	v_max_f32_e32 v6, v6, v7
	v_max_f32_e32 v8, v36, v8
	ds_bpermute_b32 v3, v9, v2
	ds_bpermute_b32 v5, v9, v4
	ds_bpermute_b32 v7, v9, v6
	ds_bpermute_b32 v9, v9, v8
	s_and_saveexec_b64 s[10:11], s[6:7]
	s_cbranch_execz .LBB0_39
	s_lshl_b32 s14, s14, 6
	s_and_b32 s14, s14, 0x7fffff00
	s_cmpk_gt_u32 s13, 0x15f
	s_cselect_b32 s13, 0x80, 0
	s_or_b32 s13, s14, s13
	s_and_b32 s8, s8, 0x60
	s_waitcnt lgkmcnt(2)
	v_max_f32_e32 v5, v5, v5
	v_max_f32_e32 v4, v4, v4
	v_max_f32_e32 v3, v3, v3
	v_max_f32_e32 v2, v2, v2
	s_or_b32 s8, s13, s8
	v_max_f32_e32 v4, v4, v5
	v_max_f32_e32 v5, v2, v3
	s_waitcnt lgkmcnt(1)
	v_max_f32_e32 v7, v7, v7
	v_max_f32_e32 v6, v6, v6
	v_lshl_add_u64 v[2:3], s[8:9], 2, v[14:15]
	v_mul_f32_e32 v5, 0x3fb33333, v5
	s_waitcnt lgkmcnt(0)
	v_max_f32_e32 v9, v9, v9
	v_max_f32_e32 v8, v8, v8
	v_max_f32_e32 v6, v6, v7
	global_atomic_umax v[2:3], v5, off
	v_mul_f32_e32 v4, 0x3fb33333, v4
	v_max_f32_e32 v8, v8, v9
	global_atomic_umax v[2:3], v4, off offset:4
	v_mul_f32_e32 v4, 0x3fb33333, v6
	global_atomic_umax v[2:3], v4, off offset:8
	v_mul_f32_e32 v4, 0x3fb33333, v8
	global_atomic_umax v[2:3], v4, off offset:12

; __device__ __forceinline__ void cvt_item8(const float* src, int ld, int k0, int c0, unsigned char* dst, int Kd, int drow0, unsigned char* scr, int lane) {
;     const int c = lane & 7, q = lane >> 3;
;     f32x4 v[4][4];
; #pragma unroll
;     for (int g = 0; g < 4; ++g)
; #pragma unroll
;         for (int j = 0; j < 4; ++j) v[g][j] = __builtin_nontemporal_load((const f32x4*)(src + (size_t)(k0 + 32 * g + 4 * q + j) * ld + c0 + 4 * c));
; #pragma unroll
;     for (int g = 0; g < 4; ++g)
; #pragma unroll
;         for (int i = 0; i < 4; ++i) *(unsigned*)(scr + (4 * c + i) * 132 + 32 * g + 4 * q) = pg8::pack_fp8x4(v[g][0][i] * WSC, v[g][1][i] * WSC, v[g][2][i] * WSC, v[g][3][i] * WSC);
;     asm volatile("s_waitcnt lgkmcnt(0)" ::: "memory");
; template <int GRP>
; __device__ __forceinline__ void conv_item(Frame& F, int r) {
;     ...
;         if (GRP == 0) {
;             if (r < CI_FD) { const int kb = r / 64, nb = r % 64; cvt_item8(inptr(F, IN_FD), D, kb * 128, nb * 32, ws + WS_WD, DFF, nb * 32, scr, F.lane); return; }
.LBB0_40:
	s_andn2_b64 vcc, exec, s[10:11]
	s_cbranch_vccnz .LBB0_42
	v_mov_b32_e32 v2, s34
	s_waitcnt lgkmcnt(3)
	ds_read_b64 v[2:3], v2
	s_lshl_b32 s8, s12, 1
	s_lshl_b32 s10, s12, 5
	s_add_i32 s8, s8, 0x7ffff800
	s_and_b32 s10, s10, 0x7e0
	s_and_b32 s8, s8, 0x7fffff80
	s_waitcnt lgkmcnt(0)
	v_readfirstlane_b32 s11, v2
	s_lshl_b32 s14, s10, 2
	v_readfirstlane_b32 s13, v3
	v_or_b32_e32 v86, s8, v17
	s_add_u32 s14, s11, s14
	s_addc_u32 s15, s13, 0
	v_lshlrev_b32_e32 v2, 2, v16
	v_mov_b32_e32 v3, v11
	v_mov_b32_e32 v87, v11
	v_or_b32_e32 v4, 1, v86
	v_mov_b32_e32 v5, v11
	v_lshl_add_u64 v[88:89], s[14:15], 0, v[2:3]
	v_lshlrev_b64 v[2:3], 13, v[86:87]
	v_lshlrev_b64 v[4:5], 13, v[4:5]
	v_lshl_add_u64 v[2:3], v[88:89], 0, v[2:3]
	v_lshl_add_u64 v[6:7], v[88:89], 0, v[4:5]
	global_load_dwordx4 v[2:5], v[2:3], off nt
	s_nop 0
	global_load_dwordx4 v[6:9], v[6:7], off nt
	v_or_b32_e32 v36, 2, v86
	v_mov_b32_e32 v37, v11
	v_or_b32_e32 v40, 3, v86
	v_mov_b32_e32 v41, v11
	v_lshlrev_b64 v[36:37], 13, v[36:37]
	v_lshlrev_b64 v[40:41], 13, v[40:41]
	v_lshl_add_u64 v[36:37], v[88:89], 0, v[36:37]
	v_lshl_add_u64 v[40:41], v[88:89], 0, v[40:41]
	global_load_dwordx4 v[36:39], v[36:37], off nt
	v_or_b32_e32 v44, 32, v86
	global_load_dwordx4 v[40:43], v[40:41], off nt
	v_mov_b32_e32 v45, v11
	v_or_b32_e32 v46, 33, v86
	v_mov_b32_e32 v47, v11
	v_lshlrev_b64 v[44:45], 13, v[44:45]
	v_lshlrev_b64 v[46:47], 13, v[46:47]
	v_lshl_add_u64 v[44:45], v[88:89], 0, v[44:45]
	v_lshl_add_u64 v[48:49], v[88:89], 0, v[46:47]
	global_load_dwordx4 v[44:47], v[44:45], off nt
	s_nop 0
	global_load_dwordx4 v[48:51], v[48:49], off nt
	v_or_b32_e32 v52, 34, v86
	v_mov_b32_e32 v53, v11
	v_or_b32_e32 v54, 35, v86
	v_mov_b32_e32 v55, v11
	v_lshlrev_b64 v[52:53], 13, v[52:53]
	v_lshlrev_b64 v[54:55], 13, v[54:55]
	v_lshl_add_u64 v[52:53], v[88:89], 0, v[52:53]
	v_lshl_add_u64 v[56:57], v[88:89], 0, v[54:55]
	global_load_dwordx4 v[52:55], v[52:53], off nt
	s_nop 0
	global_load_dwordx4 v[56:59], v[56:57], off nt
	v_or_b32_e32 v60, 64, v86
	v_mov_b32_e32 v61, v11
	v_or_b32_e32 v62, 0x41, v86
	v_mov_b32_e32 v63, v11
	v_lshlrev_b64 v[60:61], 13, v[60:61]
	v_lshlrev_b64 v[62:63], 13, v[62:63]
	v_lshl_add_u64 v[60:61], v[88:89], 0, v[60:61]
	v_lshl_add_u64 v[64:65], v[88:89], 0, v[62:63]
	global_load_dwordx4 v[60:63], v[60:61], off nt
	s_nop 0
	global_load_dwordx4 v[64:67], v[64:65], off nt
	v_or_b32_e32 v68, 0x42, v86
	v_mov_b32_e32 v69, v11
	v_or_b32_e32 v70, 0x43, v86
	v_mov_b32_e32 v71, v11
	v_lshlrev_b64 v[68:69], 13, v[68:69]
	v_lshlrev_b64 v[70:71], 13, v[70:71]
	v_lshl_add_u64 v[68:69], v[88:89], 0, v[68:69]
	v_lshl_add_u64 v[74:75], v[88:89], 0, v[70:71]
	global_load_dwordx4 v[68:71], v[68:69], off nt
	s_nop 0
	global_load_dwordx4 v[74:77], v[74:75], off nt
	v_or_b32_e32 v78, 0x60, v86
	v_mov_b32_e32 v79, v11
	v_or_b32_e32 v80, 0x61, v86
	v_mov_b32_e32 v81, v11
	v_lshlrev_b64 v[78:79], 13, v[78:79]
	v_lshlrev_b64 v[80:81], 13, v[80:81]
	v_lshl_add_u64 v[78:79], v[88:89], 0, v[78:79]
	v_lshl_add_u64 v[82:83], v[88:89], 0, v[80:81]
	global_load_dwordx4 v[78:81], v[78:79], off nt
	s_nop 0
	global_load_dwordx4 v[82:85], v[82:83], off nt
	v_or_b32_e32 v90, 0x62, v86
	v_mov_b32_e32 v91, v11
	v_or_b32_e32 v86, 0x63, v86
	v_lshlrev_b64 v[90:91], 13, v[90:91]
	v_lshlrev_b64 v[86:87], 13, v[86:87]
	v_lshl_add_u64 v[90:91], v[88:89], 0, v[90:91]
	v_lshl_add_u64 v[92:93], v[88:89], 0, v[86:87]
	global_load_dwordx4 v[86:89], v[90:91], off nt
	s_nop 0
	global_load_dwordx4 v[90:93], v[92:93], off nt
	v_mov_b32_e32 v73, v11
	s_waitcnt vmcnt(0) lgkmcnt(0)
	v_mul_f32_e32 v2, 0x42800000, v2
	v_mul_f32_e32 v6, 0x42800000, v6
	v_med3_f32 v2, v2, s35, v35
	v_med3_f32 v6, v6, s35, v35
	v_cvt_pk_fp8_f32 v73, v2, v6
	v_mul_f32_e32 v3, 0x42800000, v3
	v_med3_f32 v3, v3, s35, v35
	v_mul_f32_e32 v36, 0x42800000, v36
	v_med3_f32 v6, v36, s35, v35
	v_mul_f32_e32 v2, 0x42800000, v40
	v_med3_f32 v2, v2, s35, v35
	v_cvt_pk_fp8_f32 v73, v6, v2 op_sel:[0,0,1]
	v_mul_f32_e32 v6, 0x42800000, v7
	v_med3_f32 v6, v6, s35, v35
	v_mov_b32_e32 v36, v11
	v_cvt_pk_fp8_f32 v36, v3, v6
	v_mul_f32_e32 v7, 0x42800000, v37
	v_mul_f32_e32 v3, 0x42800000, v41
	v_med3_f32 v6, v7, s35, v35
	v_med3_f32 v3, v3, s35, v35
	v_cvt_pk_fp8_f32 v36, v6, v3 op_sel:[0,0,1]
	v_mul_f32_e32 v3, 0x42800000, v4
	v_mul_f32_e32 v4, 0x42800000, v8
	v_med3_f32 v3, v3, s35, v35
	v_med3_f32 v4, v4, s35, v35
	v_mov_b32_e32 v7, v11
	v_cvt_pk_fp8_f32 v7, v3, v4
	v_mul_f32_e32 v6, 0x42800000, v38
	v_mul_f32_e32 v3, 0x42800000, v42
	v_med3_f32 v4, v6, s35, v35
	v_med3_f32 v3, v3, s35, v35
	v_cvt_pk_fp8_f32 v7, v4, v3 op_sel:[0,0,1]
	v_mul_f32_e32 v3, 0x42800000, v5
	v_mul_f32_e32 v4, 0x42800000, v9
	v_med3_f32 v3, v3, s35, v35
	v_med3_f32 v4, v4, s35, v35
	v_mov_b32_e32 v6, v11
	v_cvt_pk_fp8_f32 v6, v3, v4
	v_mul_f32_e32 v5, 0x42800000, v39
	v_mul_f32_e32 v3, 0x42800000, v43
	v_med3_f32 v4, v5, s35, v35
	v_med3_f32 v3, v3, s35, v35
	v_cvt_pk_fp8_f32 v6, v4, v3 op_sel:[0,0,1]
	v_mul_f32_e32 v3, 0x42800000, v44
	v_mul_f32_e32 v4, 0x42800000, v48
	v_med3_f32 v3, v3, s35, v35
	v_med3_f32 v4, v4, s35, v35
	v_mov_b32_e32 v8, v11
	v_cvt_pk_fp8_f32 v8, v3, v4
	v_mul_f32_e32 v5, 0x42800000, v52
	v_mul_f32_e32 v3, 0x42800000, v56
	v_med3_f32 v4, v5, s35, v35
	v_med3_f32 v3, v3, s35, v35
	v_cvt_pk_fp8_f32 v8, v4, v3 op_sel:[0,0,1]
	v_mul_f32_e32 v3, 0x42800000, v45
	v_mul_f32_e32 v4, 0x42800000, v49
	v_med3_f32 v3, v3, s35, v35
	v_med3_f32 v4, v4, s35, v35
	v_mov_b32_e32 v9, v11
	v_cvt_pk_fp8_f32 v9, v3, v4
; __device__ __forceinline__ void cvt_item8(const float* src, int ld, int k0, int c0, unsigned char* dst, int Kd, int drow0, unsigned char* scr, int lane) {
;     ...
;     for (int g = 0; g < 4; ++g)
; #pragma unroll
;         for (int i = 0; i < 4; ++i) *(unsigned*)(scr + (4 * c + i) * 132 + 32 * g + 4 * q) = pg8::pack_fp8x4(v[g][0][i] * WSC, v[g][1][i] * WSC, v[g][2][i] * WSC, v[g][3][i] * WSC);
;     asm volatile("s_waitcnt lgkmcnt(0)" ::: "memory");
; #pragma unroll
;     for (int r = 0; r < 4; ++r) { const int n = 8 * r + (lane >> 3), ch = lane & 7; const unsigned char* p = scr + n * 132 + ch * 16;
;         u32x4 o; o.x = *(const unsigned*)(p); o.y = *(const unsigned*)(p + 4); o.z = *(const unsigned*)(p + 8); o.w = *(const unsigned*)(p + 12);
;         *(u32x4*)(dst + (size_t)(drow0 + n) * Kd + k0 + 16 * ch) = o; }
;     asm volatile("s_waitcnt lgkmcnt(0)" ::: "memory");
	v_mul_f32_e32 v5, 0x42800000, v53
	v_mul_f32_e32 v3, 0x42800000, v57
	v_med3_f32 v4, v5, s35, v35
	v_med3_f32 v3, v3, s35, v35
	v_cvt_pk_fp8_f32 v9, v4, v3 op_sel:[0,0,1]
	v_mul_f32_e32 v3, 0x42800000, v46
	v_mul_f32_e32 v4, 0x42800000, v50
	v_med3_f32 v3, v3, s35, v35
	v_med3_f32 v4, v4, s35, v35
	v_mov_b32_e32 v37, v11
	v_cvt_pk_fp8_f32 v37, v3, v4
	v_mul_f32_e32 v5, 0x42800000, v54
	v_mul_f32_e32 v3, 0x42800000, v58
	v_med3_f32 v4, v5, s35, v35
	v_med3_f32 v3, v3, s35, v35
	v_cvt_pk_fp8_f32 v37, v4, v3 op_sel:[0,0,1]
	v_mul_f32_e32 v3, 0x42800000, v47
	v_mul_f32_e32 v4, 0x42800000, v51
	v_med3_f32 v3, v3, s35, v35
	v_med3_f32 v4, v4, s35, v35
	v_mov_b32_e32 v38, v11
	v_cvt_pk_fp8_f32 v38, v3, v4
	v_mul_f32_e32 v5, 0x42800000, v55
	v_mul_f32_e32 v3, 0x42800000, v59
	v_med3_f32 v4, v5, s35, v35
	v_med3_f32 v3, v3, s35, v35
	v_add_u32_e32 v2, v22, v23
	v_cvt_pk_fp8_f32 v38, v4, v3 op_sel:[0,0,1]
	v_mul_f32_e32 v3, 0x42800000, v60
	v_mul_f32_e32 v4, 0x42800000, v64
	ds_write2_b32 v2, v73, v8 offset1:8
	ds_write2_b32 v2, v36, v9 offset0:33 offset1:41
	ds_write2_b32 v2, v7, v37 offset0:66 offset1:74
	ds_write2_b32 v2, v6, v38 offset0:99 offset1:107
	v_med3_f32 v3, v3, s35, v35
	v_med3_f32 v4, v4, s35, v35
	v_mov_b32_e32 v6, v11
	v_cvt_pk_fp8_f32 v6, v3, v4
	v_mul_f32_e32 v5, 0x42800000, v68
	v_mul_f32_e32 v3, 0x42800000, v74
	v_med3_f32 v4, v5, s35, v35
	v_med3_f32 v3, v3, s35, v35
	v_cvt_pk_fp8_f32 v6, v4, v3 op_sel:[0,0,1]
	v_mul_f32_e32 v3, 0x42800000, v61
	v_mul_f32_e32 v4, 0x42800000, v65
	v_med3_f32 v3, v3, s35, v35
	v_med3_f32 v4, v4, s35, v35
	v_mov_b32_e32 v7, v11
	v_cvt_pk_fp8_f32 v7, v3, v4
	v_mul_f32_e32 v5, 0x42800000, v69
	v_mul_f32_e32 v3, 0x42800000, v75
	v_med3_f32 v4, v5, s35, v35
	v_med3_f32 v3, v3, s35, v35
	v_cvt_pk_fp8_f32 v7, v4, v3 op_sel:[0,0,1]
	v_mul_f32_e32 v3, 0x42800000, v62
	v_mul_f32_e32 v4, 0x42800000, v66
	v_med3_f32 v3, v3, s35, v35
	v_med3_f32 v4, v4, s35, v35
	v_mov_b32_e32 v8, v11
	v_cvt_pk_fp8_f32 v8, v3, v4
	v_mul_f32_e32 v5, 0x42800000, v70
	v_mul_f32_e32 v3, 0x42800000, v76
	v_med3_f32 v4, v5, s35, v35
	v_med3_f32 v3, v3, s35, v35
	v_cvt_pk_fp8_f32 v8, v4, v3 op_sel:[0,0,1]
	v_mul_f32_e32 v3, 0x42800000, v63
	v_mul_f32_e32 v4, 0x42800000, v67
	v_med3_f32 v3, v3, s35, v35
	v_med3_f32 v4, v4, s35, v35
	v_mov_b32_e32 v9, v11
	v_cvt_pk_fp8_f32 v9, v3, v4
	v_mul_f32_e32 v5, 0x42800000, v71
	v_mul_f32_e32 v3, 0x42800000, v77
	v_med3_f32 v4, v5, s35, v35
	v_med3_f32 v3, v3, s35, v35
	v_cvt_pk_fp8_f32 v9, v4, v3 op_sel:[0,0,1]
	v_mul_f32_e32 v3, 0x42800000, v78
	v_mul_f32_e32 v4, 0x42800000, v82
	v_med3_f32 v3, v3, s35, v35
	v_med3_f32 v4, v4, s35, v35
	v_mov_b32_e32 v36, v11
	v_cvt_pk_fp8_f32 v36, v3, v4
	v_mul_f32_e32 v5, 0x42800000, v86
	v_mul_f32_e32 v3, 0x42800000, v90
	v_med3_f32 v4, v5, s35, v35
	v_med3_f32 v3, v3, s35, v35
	v_cvt_pk_fp8_f32 v36, v4, v3 op_sel:[0,0,1]
	v_mul_f32_e32 v3, 0x42800000, v79
	v_mul_f32_e32 v4, 0x42800000, v83
	v_med3_f32 v3, v3, s35, v35
	v_med3_f32 v4, v4, s35, v35
	v_mov_b32_e32 v37, v11
	v_cvt_pk_fp8_f32 v37, v3, v4
	v_mul_f32_e32 v5, 0x42800000, v87
	v_mul_f32_e32 v3, 0x42800000, v91
	v_med3_f32 v4, v5, s35, v35
	v_med3_f32 v3, v3, s35, v35
	v_cvt_pk_fp8_f32 v37, v4, v3 op_sel:[0,0,1]
	v_mul_f32_e32 v3, 0x42800000, v80
	v_mul_f32_e32 v4, 0x42800000, v84
	v_med3_f32 v3, v3, s35, v35
	v_med3_f32 v4, v4, s35, v35
	v_mov_b32_e32 v38, v11
	v_cvt_pk_fp8_f32 v38, v3, v4
	v_mul_f32_e32 v5, 0x42800000, v88
	v_mul_f32_e32 v3, 0x42800000, v92
	v_med3_f32 v4, v5, s35, v35
	v_med3_f32 v3, v3, s35, v35
	v_cvt_pk_fp8_f32 v38, v4, v3 op_sel:[0,0,1]
	v_mul_f32_e32 v3, 0x42800000, v81
	v_mul_f32_e32 v4, 0x42800000, v85
	v_med3_f32 v3, v3, s35, v35
	v_med3_f32 v4, v4, s35, v35
	v_mov_b32_e32 v39, v11
	v_cvt_pk_fp8_f32 v39, v3, v4
	v_mul_f32_e32 v5, 0x42800000, v89
	v_mul_f32_e32 v3, 0x42800000, v93
	v_med3_f32 v4, v5, s35, v35
	v_med3_f32 v3, v3, s35, v35
	v_cvt_pk_fp8_f32 v39, v4, v3 op_sel:[0,0,1]
	ds_write2_b32 v2, v6, v36 offset0:16 offset1:24
	ds_write2_b32 v2, v7, v37 offset0:49 offset1:57
	ds_write2_b32 v2, v8, v38 offset0:82 offset1:90
	ds_write2_b32 v2, v9, v39 offset0:115 offset1:123
	s_waitcnt lgkmcnt(0)
	v_add_u32_e32 v40, v24, v25
	ds_read2_b32 v[2:3], v40 offset1:1
	ds_read2_b32 v[4:5], v40 offset0:2 offset1:3
	v_or_b32_e32 v6, s10, v72
	v_lshl_add_u64 v[36:37], v[18:19], 0, s[8:9]
	v_mul_u32_u24_e32 v6, 0x1600, v6
	v_mov_b32_e32 v7, v11
	v_lshl_add_u64 v[38:39], v[36:37], 0, v[6:7]
	v_add_u32_e32 v6, 0x420, v40
	v_add_u32_e32 v8, 0x428, v40
	ds_read2_b32 v[6:7], v6 offset1:1
	ds_read2_b32 v[8:9], v8 offset1:1
	s_waitcnt lgkmcnt(2)
	global_store_dwordx4 v[38:39], v[2:5], off
	s_nop 1
	v_or_b32_e32 v2, s10, v26
	v_mul_u32_u24_e32 v2, 0x1600, v2
	v_mov_b32_e32 v3, v11
	v_lshl_add_u64 v[2:3], v[36:37], 0, v[2:3]
	s_waitcnt lgkmcnt(0)
	global_store_dwordx4 v[2:3], v[6:9], off
	v_add_u32_e32 v2, 0x840, v40
	v_add_u32_e32 v4, 0x848, v40
	ds_read2_b32 v[2:3], v2 offset1:1
	ds_read2_b32 v[4:5], v4 offset1:1
	v_or_b32_e32 v6, s10, v27
	v_mul_u32_u24_e32 v6, 0x1600, v6
	v_mov_b32_e32 v7, v11
	v_lshl_add_u64 v[38:39], v[36:37], 0, v[6:7]
	v_add_u32_e32 v6, 0xc60, v40
	v_add_u32_e32 v8, 0xc68, v40
	ds_read2_b32 v[6:7], v6 offset1:1
	ds_read2_b32 v[8:9], v8 offset1:1
	s_waitcnt lgkmcnt(2)
	global_store_dwordx4 v[38:39], v[2:5], off
	s_nop 1
	v_or_b32_e32 v2, s10, v28
	v_mul_u32_u24_e32 v2, 0x1600, v2
	v_mov_b32_e32 v3, v11
	v_lshl_add_u64 v[2:3], v[36:37], 0, v[2:3]
	s_waitcnt lgkmcnt(0)
	global_store_dwordx4 v[2:3], v[6:9], off
	s_waitcnt lgkmcnt(0)

; __device__ __forceinline__ void cvt_item8(const float* src, int ld, int k0, int c0, unsigned char* dst, int Kd, int drow0, unsigned char* scr, int lane) {
;     const int c = lane & 7, q = lane >> 3;
;     f32x4 v[4][4];
; #pragma unroll
;     for (int g = 0; g < 4; ++g)
; #pragma unroll
;         for (int j = 0; j < 4; ++j) v[g][j] = __builtin_nontemporal_load((const f32x4*)(src + (size_t)(k0 + 32 * g + 4 * q + j) * ld + c0 + 4 * c));
; #pragma unroll
;     for (int g = 0; g < 4; ++g)
; #pragma unroll
;         for (int i = 0; i < 4; ++i) *(unsigned*)(scr + (4 * c + i) * 132 + 32 * g + 4 * q) = pg8::pack_fp8x4(v[g][0][i] * WSC, v[g][1][i] * WSC, v[g][2][i] * WSC, v[g][3][i] * WSC);
;     asm volatile("s_waitcnt lgkmcnt(0)" ::: "memory");
; template <int GRP>
; __device__ __forceinline__ void conv_item(Frame& F, int r) {
;     ...
;         if (r < CI_WO) { const int kb = r / 64, nb = r % 64;
;             cvt_item8(inptr(F, IN_WOUT) + (size_t)l * D * D, D, kb * 128, nb * 32, ws + WS_WOUT + (size_t)l * D * D, D, nb * 32, scr, F.lane); return; }
.LBB0_43:
	s_andn2_b64 vcc, exec, s[10:11]
	s_cbranch_vccnz .LBB0_27
	s_ashr_i32 s8, s12, 31
	v_mov_b32_e32 v2, s36
	s_lshr_b32 s8, s8, 26
	s_waitcnt lgkmcnt(3)
	ds_read_b64 v[2:3], v2
	s_add_i32 s8, s12, s8
	s_and_b32 s10, s8, 0x7ffffc0
	s_sub_i32 s10, s12, s10
	s_lshl_b32 s10, s10, 5
	s_lshl_b32 s8, s8, 1
	s_ashr_i32 s11, s10, 31
	s_waitcnt lgkmcnt(0)
	v_readfirstlane_b32 s13, v2
	s_and_b32 s12, s8, 0xffffff80
	s_lshl_b64 s[14:15], s[10:11], 2
	v_readfirstlane_b32 s38, v3
	v_or_b32_e32 v86, s12, v17
	s_add_u32 s14, s13, s14
	s_addc_u32 s15, s38, s15
	v_lshlrev_b32_e32 v2, 2, v16
	v_mov_b32_e32 v3, v11
	v_ashrrev_i32_e32 v87, 31, v86
	v_or_b32_e32 v4, 1, v86
	v_lshl_add_u64 v[88:89], s[14:15], 0, v[2:3]
	v_lshlrev_b64 v[2:3], 13, v[86:87]
	v_ashrrev_i32_e32 v5, 31, v4
	v_lshl_add_u64 v[2:3], v[88:89], 0, v[2:3]
	v_lshlrev_b64 v[4:5], 13, v[4:5]
	v_lshl_add_u64 v[4:5], v[88:89], 0, v[4:5]
	global_load_dwordx4 v[36:39], v[2:3], off nt
	global_load_dwordx4 v[40:43], v[4:5], off nt
	v_or_b32_e32 v2, 2, v86
	v_ashrrev_i32_e32 v3, 31, v2
	v_lshlrev_b64 v[2:3], 13, v[2:3]
	v_lshl_add_u64 v[2:3], v[88:89], 0, v[2:3]
	global_load_dwordx4 v[44:47], v[2:3], off nt
	v_or_b32_e32 v2, 3, v86
	v_ashrrev_i32_e32 v3, 31, v2
	v_lshlrev_b64 v[2:3], 13, v[2:3]
	v_lshl_add_u64 v[2:3], v[88:89], 0, v[2:3]
	global_load_dwordx4 v[48:51], v[2:3], off nt
	v_or_b32_e32 v2, 32, v86
	v_ashrrev_i32_e32 v3, 31, v2
	v_or_b32_e32 v4, 33, v86
	v_lshlrev_b64 v[2:3], 13, v[2:3]
	v_ashrrev_i32_e32 v5, 31, v4
	v_lshl_add_u64 v[2:3], v[88:89], 0, v[2:3]
	v_lshlrev_b64 v[4:5], 13, v[4:5]
	v_lshl_add_u64 v[4:5], v[88:89], 0, v[4:5]
	global_load_dwordx4 v[52:55], v[2:3], off nt
	global_load_dwordx4 v[56:59], v[4:5], off nt
	v_or_b32_e32 v2, 34, v86
	v_ashrrev_i32_e32 v3, 31, v2
	v_or_b32_e32 v4, 35, v86
	v_lshlrev_b64 v[2:3], 13, v[2:3]
	v_ashrrev_i32_e32 v5, 31, v4
	v_lshl_add_u64 v[2:3], v[88:89], 0, v[2:3]
	v_lshlrev_b64 v[4:5], 13, v[4:5]
	v_lshl_add_u64 v[4:5], v[88:89], 0, v[4:5]
	global_load_dwordx4 v[60:63], v[2:3], off nt
	global_load_dwordx4 v[64:67], v[4:5], off nt
	v_or_b32_e32 v2, 64, v86
	v_ashrrev_i32_e32 v3, 31, v2
	v_or_b32_e32 v4, 0x41, v86
	v_lshlrev_b64 v[2:3], 13, v[2:3]
	v_ashrrev_i32_e32 v5, 31, v4
	v_lshl_add_u64 v[2:3], v[88:89], 0, v[2:3]
	v_lshlrev_b64 v[4:5], 13, v[4:5]
	v_lshl_add_u64 v[4:5], v[88:89], 0, v[4:5]
	global_load_dwordx4 v[68:71], v[2:3], off nt
	global_load_dwordx4 v[74:77], v[4:5], off nt
	v_or_b32_e32 v2, 0x42, v86
	v_ashrrev_i32_e32 v3, 31, v2
	v_or_b32_e32 v4, 0x43, v86
	v_lshlrev_b64 v[2:3], 13, v[2:3]
	v_ashrrev_i32_e32 v5, 31, v4
	v_lshl_add_u64 v[2:3], v[88:89], 0, v[2:3]
	v_lshlrev_b64 v[4:5], 13, v[4:5]
	v_lshl_add_u64 v[4:5], v[88:89], 0, v[4:5]
	global_load_dwordx4 v[78:81], v[2:3], off nt
	global_load_dwordx4 v[82:85], v[4:5], off nt
	v_or_b32_e32 v2, 0x60, v86
	v_or_b32_e32 v4, 0x61, v86
	v_ashrrev_i32_e32 v3, 31, v2
	v_ashrrev_i32_e32 v5, 31, v4
	v_lshlrev_b64 v[2:3], 13, v[2:3]
	v_lshlrev_b64 v[4:5], 13, v[4:5]
	v_lshl_add_u64 v[2:3], v[88:89], 0, v[2:3]
	v_lshl_add_u64 v[6:7], v[88:89], 0, v[4:5]
	global_load_dwordx4 v[2:5], v[2:3], off nt
	s_nop 0
	global_load_dwordx4 v[6:9], v[6:7], off nt
	v_or_b32_e32 v90, 0x62, v86
	v_or_b32_e32 v86, 0x63, v86
	v_ashrrev_i32_e32 v91, 31, v90
	v_ashrrev_i32_e32 v87, 31, v86
	v_lshlrev_b64 v[90:91], 13, v[90:91]
	v_lshlrev_b64 v[86:87], 13, v[86:87]
	v_lshl_add_u64 v[90:91], v[88:89], 0, v[90:91]
	v_lshl_add_u64 v[92:93], v[88:89], 0, v[86:87]
	global_load_dwordx4 v[86:89], v[90:91], off nt
	s_nop 0
	global_load_dwordx4 v[90:93], v[92:93], off nt
	v_mov_b32_e32 v73, v11
	s_ashr_i32 s13, s12, 31
	s_waitcnt vmcnt(0) lgkmcnt(0)
	v_mul_f32_e32 v36, 0x42800000, v36
	v_mul_f32_e32 v40, 0x42800000, v40
	v_med3_f32 v36, v36, s35, v35
	v_med3_f32 v40, v40, s35, v35
	v_cvt_pk_fp8_f32 v73, v36, v40
	v_mul_f32_e32 v37, 0x42800000, v37
	v_mul_f32_e32 v44, 0x42800000, v44
	v_med3_f32 v40, v44, s35, v35
	v_med3_f32 v37, v37, s35, v35
	v_mov_b32_e32 v44, v11
	v_mul_f32_e32 v36, 0x42800000, v48
	v_med3_f32 v36, v36, s35, v35
	v_cvt_pk_fp8_f32 v73, v40, v36 op_sel:[0,0,1]
	v_mul_f32_e32 v40, 0x42800000, v41
	v_med3_f32 v40, v40, s35, v35
	v_cvt_pk_fp8_f32 v44, v37, v40
	v_mul_f32_e32 v41, 0x42800000, v45
	v_mul_f32_e32 v37, 0x42800000, v49
	v_med3_f32 v40, v41, s35, v35
	v_med3_f32 v37, v37, s35, v35
	v_cvt_pk_fp8_f32 v44, v40, v37 op_sel:[0,0,1]
	v_mul_f32_e32 v37, 0x42800000, v38
	v_mul_f32_e32 v38, 0x42800000, v42
	v_med3_f32 v37, v37, s35, v35
	v_med3_f32 v38, v38, s35, v35
	v_mov_b32_e32 v41, v11
	v_cvt_pk_fp8_f32 v41, v37, v38
	v_mul_f32_e32 v40, 0x42800000, v46
	v_mul_f32_e32 v37, 0x42800000, v50
	v_med3_f32 v38, v40, s35, v35
	v_med3_f32 v37, v37, s35, v35
	v_cvt_pk_fp8_f32 v41, v38, v37 op_sel:[0,0,1]
	v_mul_f32_e32 v37, 0x42800000, v39
	v_mul_f32_e32 v38, 0x42800000, v43
	v_med3_f32 v37, v37, s35, v35
	v_med3_f32 v38, v38, s35, v35
	v_mov_b32_e32 v40, v11
	v_cvt_pk_fp8_f32 v40, v37, v38
	v_mul_f32_e32 v39, 0x42800000, v47
	v_mul_f32_e32 v37, 0x42800000, v51
	v_med3_f32 v38, v39, s35, v35
	v_med3_f32 v37, v37, s35, v35
	v_cvt_pk_fp8_f32 v40, v38, v37 op_sel:[0,0,1]
	v_mul_f32_e32 v37, 0x42800000, v52
	v_mul_f32_e32 v38, 0x42800000, v56
	v_med3_f32 v37, v37, s35, v35
	v_med3_f32 v38, v38, s35, v35
	v_mov_b32_e32 v42, v11
	v_cvt_pk_fp8_f32 v42, v37, v38
	v_mul_f32_e32 v39, 0x42800000, v60
	v_mul_f32_e32 v37, 0x42800000, v64
	v_med3_f32 v38, v39, s35, v35
	v_med3_f32 v37, v37, s35, v35
	v_cvt_pk_fp8_f32 v42, v38, v37 op_sel:[0,0,1]
	v_mul_f32_e32 v37, 0x42800000, v53
	v_mul_f32_e32 v38, 0x42800000, v57
	v_med3_f32 v37, v37, s35, v35
	v_med3_f32 v38, v38, s35, v35
	v_mov_b32_e32 v43, v11
; __device__ __forceinline__ void cvt_item8(const float* src, int ld, int k0, int c0, unsigned char* dst, int Kd, int drow0, unsigned char* scr, int lane) {
;     ...
;     for (int g = 0; g < 4; ++g)
; #pragma unroll
;         for (int i = 0; i < 4; ++i) *(unsigned*)(scr + (4 * c + i) * 132 + 32 * g + 4 * q) = pg8::pack_fp8x4(v[g][0][i] * WSC, v[g][1][i] * WSC, v[g][2][i] * WSC, v[g][3][i] * WSC);
;     asm volatile("s_waitcnt lgkmcnt(0)" ::: "memory");
; #pragma unroll
;     for (int r = 0; r < 4; ++r) { const int n = 8 * r + (lane >> 3), ch = lane & 7; const unsigned char* p = scr + n * 132 + ch * 16;
;         u32x4 o; o.x = *(const unsigned*)(p); o.y = *(const unsigned*)(p + 4); o.z = *(const unsigned*)(p + 8); o.w = *(const unsigned*)(p + 12);
;         *(u32x4*)(dst + (size_t)(drow0 + n) * Kd + k0 + 16 * ch) = o; }
;     asm volatile("s_waitcnt lgkmcnt(0)" ::: "memory");
	v_cvt_pk_fp8_f32 v43, v37, v38
	v_mul_f32_e32 v39, 0x42800000, v61
	v_mul_f32_e32 v37, 0x42800000, v65
	v_med3_f32 v38, v39, s35, v35
	v_med3_f32 v37, v37, s35, v35
	v_cvt_pk_fp8_f32 v43, v38, v37 op_sel:[0,0,1]
	v_mul_f32_e32 v37, 0x42800000, v54
	v_mul_f32_e32 v38, 0x42800000, v58
	v_med3_f32 v37, v37, s35, v35
	v_med3_f32 v38, v38, s35, v35
	v_mov_b32_e32 v45, v11
	v_cvt_pk_fp8_f32 v45, v37, v38
	v_mul_f32_e32 v39, 0x42800000, v62
	v_mul_f32_e32 v37, 0x42800000, v66
	v_med3_f32 v38, v39, s35, v35
	v_med3_f32 v37, v37, s35, v35
	v_cvt_pk_fp8_f32 v45, v38, v37 op_sel:[0,0,1]
	v_mul_f32_e32 v37, 0x42800000, v55
	v_mul_f32_e32 v38, 0x42800000, v59
	v_med3_f32 v37, v37, s35, v35
	v_med3_f32 v38, v38, s35, v35
	v_mov_b32_e32 v46, v11
	v_cvt_pk_fp8_f32 v46, v37, v38
	v_mul_f32_e32 v39, 0x42800000, v63
	v_mul_f32_e32 v37, 0x42800000, v67
	v_med3_f32 v38, v39, s35, v35
	v_med3_f32 v37, v37, s35, v35
	v_add_u32_e32 v36, v22, v23
	v_cvt_pk_fp8_f32 v46, v38, v37 op_sel:[0,0,1]
	v_mul_f32_e32 v37, 0x42800000, v68
	v_mul_f32_e32 v38, 0x42800000, v74
	ds_write2_b32 v36, v73, v42 offset1:8
	ds_write2_b32 v36, v44, v43 offset0:33 offset1:41
	ds_write2_b32 v36, v41, v45 offset0:66 offset1:74
	ds_write2_b32 v36, v40, v46 offset0:99 offset1:107
	v_med3_f32 v37, v37, s35, v35
	v_med3_f32 v38, v38, s35, v35
	v_mov_b32_e32 v40, v11
	v_cvt_pk_fp8_f32 v40, v37, v38
	v_mul_f32_e32 v39, 0x42800000, v78
	v_mul_f32_e32 v37, 0x42800000, v82
	v_med3_f32 v38, v39, s35, v35
	v_med3_f32 v37, v37, s35, v35
	v_cvt_pk_fp8_f32 v40, v38, v37 op_sel:[0,0,1]
	v_mul_f32_e32 v37, 0x42800000, v69
	v_mul_f32_e32 v38, 0x42800000, v75
	v_med3_f32 v37, v37, s35, v35
	v_med3_f32 v38, v38, s35, v35
	v_mov_b32_e32 v41, v11
	v_cvt_pk_fp8_f32 v41, v37, v38
	v_mul_f32_e32 v39, 0x42800000, v79
	v_mul_f32_e32 v37, 0x42800000, v83
	v_med3_f32 v38, v39, s35, v35
	v_med3_f32 v37, v37, s35, v35
	v_cvt_pk_fp8_f32 v41, v38, v37 op_sel:[0,0,1]
	v_mul_f32_e32 v37, 0x42800000, v70
	v_mul_f32_e32 v38, 0x42800000, v76
	v_med3_f32 v37, v37, s35, v35
	v_med3_f32 v38, v38, s35, v35
	v_mov_b32_e32 v42, v11
	v_cvt_pk_fp8_f32 v42, v37, v38
	v_mul_f32_e32 v39, 0x42800000, v80
	v_mul_f32_e32 v37, 0x42800000, v84
	v_med3_f32 v38, v39, s35, v35
	v_med3_f32 v37, v37, s35, v35
	v_cvt_pk_fp8_f32 v42, v38, v37 op_sel:[0,0,1]
	v_mul_f32_e32 v37, 0x42800000, v71
	v_mul_f32_e32 v38, 0x42800000, v77
	v_med3_f32 v37, v37, s35, v35
	v_med3_f32 v38, v38, s35, v35
	v_mov_b32_e32 v43, v11
	v_cvt_pk_fp8_f32 v43, v37, v38
	v_mul_f32_e32 v39, 0x42800000, v81
	v_mul_f32_e32 v37, 0x42800000, v85
	v_med3_f32 v38, v39, s35, v35
	v_med3_f32 v37, v37, s35, v35
	v_mul_f32_e32 v2, 0x42800000, v2
	v_mul_f32_e32 v6, 0x42800000, v6
	v_cvt_pk_fp8_f32 v43, v38, v37 op_sel:[0,0,1]
	v_med3_f32 v2, v2, s35, v35
	v_med3_f32 v6, v6, s35, v35
	v_mov_b32_e32 v38, v11
	v_cvt_pk_fp8_f32 v38, v2, v6
	v_mul_f32_e32 v37, 0x42800000, v86
	v_mul_f32_e32 v2, 0x42800000, v90
	v_med3_f32 v6, v37, s35, v35
	v_med3_f32 v2, v2, s35, v35
	v_cvt_pk_fp8_f32 v38, v6, v2 op_sel:[0,0,1]
	v_mul_f32_e32 v2, 0x42800000, v3
	v_mul_f32_e32 v3, 0x42800000, v7
	v_med3_f32 v2, v2, s35, v35
	v_med3_f32 v3, v3, s35, v35
	v_mov_b32_e32 v7, v11
	v_cvt_pk_fp8_f32 v7, v2, v3
	v_mul_f32_e32 v6, 0x42800000, v87
	v_mul_f32_e32 v2, 0x42800000, v91
	v_med3_f32 v3, v6, s35, v35
	v_med3_f32 v2, v2, s35, v35
	v_cvt_pk_fp8_f32 v7, v3, v2 op_sel:[0,0,1]
	v_mul_f32_e32 v2, 0x42800000, v4
	v_mul_f32_e32 v3, 0x42800000, v8
	v_med3_f32 v2, v2, s35, v35
	v_med3_f32 v3, v3, s35, v35
	v_mov_b32_e32 v6, v11
	v_cvt_pk_fp8_f32 v6, v2, v3
	v_mul_f32_e32 v4, 0x42800000, v88
	v_mul_f32_e32 v2, 0x42800000, v92
	v_med3_f32 v3, v4, s35, v35
	v_med3_f32 v2, v2, s35, v35
	v_cvt_pk_fp8_f32 v6, v3, v2 op_sel:[0,0,1]
	v_mul_f32_e32 v2, 0x42800000, v5
	v_mul_f32_e32 v3, 0x42800000, v9
	v_med3_f32 v2, v2, s35, v35
	v_med3_f32 v3, v3, s35, v35
	v_mov_b32_e32 v5, v11
	v_cvt_pk_fp8_f32 v5, v2, v3
	v_mul_f32_e32 v4, 0x42800000, v89
	v_mul_f32_e32 v2, 0x42800000, v93
	v_med3_f32 v3, v4, s35, v35
	v_med3_f32 v2, v2, s35, v35
	v_cvt_pk_fp8_f32 v5, v3, v2 op_sel:[0,0,1]
	ds_write2_b32 v36, v40, v38 offset0:16 offset1:24
	ds_write2_b32 v36, v41, v7 offset0:49 offset1:57
	ds_write2_b32 v36, v42, v6 offset0:82 offset1:90
	ds_write2_b32 v36, v43, v5 offset0:115 offset1:123
	s_waitcnt lgkmcnt(0)
	v_add_u32_e32 v40, v24, v25
	ds_read2_b32 v[2:3], v40 offset1:1
	ds_read2_b32 v[4:5], v40 offset0:2 offset1:3
	v_or_b32_e32 v6, s10, v72
	v_ashrrev_i32_e32 v7, 31, v6
	v_lshl_add_u64 v[36:37], v[20:21], 0, s[12:13]
	v_lshlrev_b64 v[6:7], 11, v[6:7]
	v_lshl_add_u64 v[38:39], v[36:37], 0, v[6:7]
	v_add_u32_e32 v6, 0x420, v40
	v_add_u32_e32 v8, 0x428, v40
	ds_read2_b32 v[6:7], v6 offset1:1
	ds_read2_b32 v[8:9], v8 offset1:1
	s_waitcnt lgkmcnt(2)
	global_store_dwordx4 v[38:39], v[2:5], off
	s_nop 1
	v_or_b32_e32 v2, s10, v26
	v_ashrrev_i32_e32 v3, 31, v2
	v_lshlrev_b64 v[2:3], 11, v[2:3]
	v_lshl_add_u64 v[2:3], v[36:37], 0, v[2:3]
	s_waitcnt lgkmcnt(0)
	global_store_dwordx4 v[2:3], v[6:9], off
	v_add_u32_e32 v2, 0x840, v40
	v_add_u32_e32 v4, 0x848, v40
	ds_read2_b32 v[2:3], v2 offset1:1
	ds_read2_b32 v[4:5], v4 offset1:1
	v_or_b32_e32 v6, s10, v27
	v_ashrrev_i32_e32 v7, 31, v6
	v_lshlrev_b64 v[6:7], 11, v[6:7]
	v_lshl_add_u64 v[38:39], v[36:37], 0, v[6:7]
	v_add_u32_e32 v6, 0xc60, v40
	v_add_u32_e32 v8, 0xc68, v40
	ds_read2_b32 v[6:7], v6 offset1:1
	ds_read2_b32 v[8:9], v8 offset1:1
	s_waitcnt lgkmcnt(2)
	global_store_dwordx4 v[38:39], v[2:5], off
	s_nop 1
	v_or_b32_e32 v2, s10, v28
	v_ashrrev_i32_e32 v3, 31, v2
	v_lshlrev_b64 v[2:3], 11, v[2:3]
	v_lshl_add_u64 v[2:3], v[36:37], 0, v[2:3]
	s_waitcnt lgkmcnt(0)
	global_store_dwordx4 v[2:3], v[6:9], off
	s_waitcnt lgkmcnt(0)
	s_branch .LBB0_27

; #define LAS __attribute__((address_space(3)))
; template <int YMODE, int EXTRA, bool NORM_OUT, bool XN8  , bool XIN_BF = false  , bool XOUT_BF = false  > ...
;     ...
;         __syncthreads();
;         { const int col = 4 * F.tid;
;             if (YMODE) { const f32x4 g = *(const f32x4*)(gt + (size_t)b * 6 * D + col), p = *(const f32x4*)(gpost + col); *(LAS f32x4*)(vA + col) = g * p; }
;             if (NORM_OUT) { const f32x4 g = *(const f32x4*)(gpre + col), s = *(const f32x4*)(sc + (size_t)b * 6 * D + col); *(LAS f32x4*)(vB + col) = g * (1.f + s); *(LAS f32x4*)(vC + col) = *(const f32x4*)(sh + (size_t)b * 6 * D + col); } }
;         __syncthreads();
;         f32x4 xr[8]; u32x2 xrb[8], yr[8], yr2[8]; float w1n = 0.f, w2n = 0.f;
;     ...
;         RP_LOAD(0);
.LBB0_105:
	s_ashr_i32 s29, s28, 31
	s_lshr_b32 s26, s29, 27
	s_add_i32 s26, s28, s26
	s_ashr_i32 s26, s26, 5
	s_mul_i32 s26, s26, 6
	s_ashr_i32 s27, s26, 31
	s_lshl_b64 s[26:27], s[26:27], 13
	v_lshl_add_u64 v[2:3], v[70:71], 0, s[26:27]
	s_waitcnt lgkmcnt(0)
	s_barrier
	global_load_dwordx4 v[2:5], v[2:3], off
	v_lshl_add_u64 v[6:7], v[72:73], 0, s[26:27]
	global_load_dwordx4 v[6:9], v[6:7], off
	s_nop 0
	global_load_dwordx4 v[10:13], v[68:69], off
	s_lshl_b64 s[30:31], s[28:29], 6
	s_add_u32 s29, s30, s5
	s_addc_u32 s35, s31, 0
	s_and_b32 s26, s28, 7
	s_or_b32 s34, s29, s26
	s_lshl_b64 s[26:27], s[34:35], 13
	v_lshl_add_u64 v[14:15], v[74:75], 0, s[26:27]
	v_add_co_u32_e32 v16, vcc, 0x1000, v14
	s_mov_b32 s59, 0
	s_nop 0
	v_addc_co_u32_e32 v17, vcc, 0, v15, vcc
	s_waitcnt vmcnt(0)
	v_pk_add_f32 v[4:5], v[4:5], 1.0 op_sel_hi:[1,0]
	v_pk_add_f32 v[2:3], v[2:3], 1.0 op_sel_hi:[1,0]
	s_waitcnt lgkmcnt(0)
	v_pk_mul_f32 v[4:5], v[12:13], v[4:5]
	v_pk_mul_f32 v[2:3], v[10:11], v[2:3]
	ds_write_b128 v85, v[6:9]
	ds_write_b128 v84, v[2:5]
	s_waitcnt lgkmcnt(0)
	s_barrier
	global_load_dwordx4 v[62:65], v[14:15], off nt
	global_load_dwordx4 v[58:61], v[14:15], off offset:1024 nt
	global_load_dwordx4 v[54:57], v[14:15], off offset:2048 nt
	global_load_dwordx4 v[50:53], v[14:15], off offset:3072 nt
	global_load_dwordx4 v[46:49], v[16:17], off nt
	global_load_dwordx4 v[42:45], v[16:17], off offset:1024 nt
	global_load_dwordx4 v[38:41], v[16:17], off offset:2048 nt
	global_load_dwordx4 v[34:37], v[16:17], off offset:3072 nt
	s_waitcnt vmcnt(0) lgkmcnt(0)
	v_mov_b64_e32 v[2:3], v[62:63]
	v_mov_b64_e32 v[6:7], v[58:59]
	v_mov_b64_e32 v[10:11], v[54:55]
	v_mov_b64_e32 v[14:15], v[50:51]
	v_mov_b64_e32 v[18:19], v[46:47]
	v_mov_b64_e32 v[22:23], v[42:43]
	v_mov_b64_e32 v[26:27], v[38:39]
	v_mov_b64_e32 v[30:31], v[34:35]
	v_mov_b64_e32 v[4:5], v[64:65]
	v_mov_b64_e32 v[8:9], v[60:61]
	v_mov_b64_e32 v[12:13], v[56:57]
	v_mov_b64_e32 v[16:17], v[52:53]
	v_mov_b64_e32 v[20:21], v[48:49]
	v_mov_b64_e32 v[24:25], v[44:45]
	v_mov_b64_e32 v[28:29], v[40:41]
	v_mov_b64_e32 v[32:33], v[36:37]
	s_branch .LBB0_108

; template <int YMODE, int EXTRA, bool NORM_OUT, bool XN8  , bool XIN_BF = false  , bool XOUT_BF = false  > ...
;     ...
;             if (rr < 7) RP_LOAD(rr + 1);
.LBB0_108:
	s_add_i32 s26, s28, s59
	s_cmp_eq_u32 s59, 7
	s_cbranch_scc1 .LBB0_110
	s_add_i32 s27, s26, 1
	s_and_b32 s27, s27, 7
	s_or_b32 s34, s29, s27
	s_lshl_b64 s[36:37], s[34:35], 13
	v_lshl_add_u64 v[18:19], v[74:75], 0, s[36:37]
	v_add_co_u32_e32 v30, vcc, 0x1000, v18
	global_load_dwordx4 v[2:5], v[18:19], off nt
	global_load_dwordx4 v[6:9], v[18:19], off offset:1024 nt
	global_load_dwordx4 v[10:13], v[18:19], off offset:2048 nt
	global_load_dwordx4 v[14:17], v[18:19], off offset:3072 nt
	v_addc_co_u32_e32 v31, vcc, 0, v19, vcc
	global_load_dwordx4 v[18:21], v[30:31], off nt
	global_load_dwordx4 v[22:25], v[30:31], off offset:1024 nt
	global_load_dwordx4 v[26:29], v[30:31], off offset:2048 nt
	s_nop 0
	global_load_dwordx4 v[30:33], v[30:31], off offset:3072 nt

; #define LAS __attribute__((address_space(3)))
; __device__ __forceinline__ unsigned cvtpk(float lo, float hi) { f32x2 v = {lo, hi}; bf16x2_t b = __builtin_convertvector(v, bf16x2_t); return __builtin_bit_cast(unsigned, b); }
; __device__ __forceinline__ float wave_sum(float v) { return lane63(scan64<false>(v)); }
; template <int YMODE, int EXTRA, bool NORM_OUT, bool XN8  , bool XIN_BF = false  , bool XOUT_BF = false  > ...
;     ...
;                     const float inv = am > 0.f ? 127.f / am : 0.f;
;                     if (F.lane == 0) { rowmax[row] = am; if (EXTRA == 2) route[384 + rl] = am; }
; #pragma unroll
;                     for (int j = 0; j < 8; ++j) *(unsigned*)((unsigned char*)XN + row * D + 256 * j + 4 * F.lane) = pack_i8x4(x[j][0] * inv, x[j][1] * inv, x[j][2] * inv, x[j][3] * inv);
;                 } else {
; #pragma unroll
;                     for (int j = 0; j < 8; ++j) { u32x2 w; w.x = cvtpk(x[j][0], x[j][1]); w.y = cvtpk(x[j][2], x[j][3]); *(u32x2*)(XN + row * D + 256 * j + 4 * F.lane) = w; }
;                 }
;                 if (EXTRA) {
;                     float d8[8];
; #pragma unroll
;                     for (int e = 0; e < 8; ++e) { float s = 0.f;
; #pragma unroll
;                         for (int j = 0; j < 8; ++j) { const f32x4 w = *(const LAS f32x4*)(we + e * D + 256 * j + 4 * F.lane); s += (x[j][0] * w[0] + x[j][1] * w[1]) + (x[j][2] * w[2] + x[j][3] * w[3]); }
;                         d8[e] = wave_sum(s); asm volatile("" ::: "memory"); }
.LBB0_112:
	s_or_b64 exec, exec, s[36:37]
	v_div_scale_f32 v1, s[36:37], s34, s34, v93
	v_rcp_f32_e32 v83, v1
	v_mov_b32_e32 v95, s34
	v_div_scale_f32 v95, vcc, s40, v95, s40
	v_fma_f32 v96, -v1, v83, 1.0
	v_fmac_f32_e32 v83, v96, v83
	v_mul_f32_e32 v96, v95, v83
	v_fma_f32 v97, -v1, v96, v95
	v_fmac_f32_e32 v96, v97, v83
	v_fma_f32 v1, -v1, v96, v95
	v_div_fmas_f32 v1, v1, v83, v96
	v_div_fixup_f32 v1, v1, s34, v93
	v_cmp_gt_f32_e64 vcc, s34, 0
	s_lshl_b64 s[36:37], s[26:27], 11
	v_lshl_add_u64 v[100:101], v[80:81], 0, s[36:37]
	v_cndmask_b32_e32 v1, 0, v1, vcc
	v_mul_f32_e32 v95, v65, v1
	v_mul_f32_e32 v83, v64, v1
	v_mul_f32_e32 v96, v62, v1
	v_mul_f32_e32 v97, v63, v1
	v_med3_f32 v95, v95, s41, v93
	v_med3_f32 v83, v83, s41, v93
	v_rndne_f32_e32 v95, v95
	v_med3_f32 v96, v96, s41, v93
	v_med3_f32 v97, v97, s41, v93
	v_rndne_f32_e32 v83, v83
	v_cvt_i32_f32_e32 v95, v95
	v_rndne_f32_e32 v96, v96
	v_rndne_f32_e32 v97, v97
	v_cvt_i32_f32_e32 v83, v83
	v_cvt_i32_f32_sdwa v96, v96 dst_sel:WORD_1 dst_unused:UNUSED_PAD src0_sel:DWORD
	v_cvt_i32_f32_e32 v97, v97
	v_lshlrev_b32_e32 v95, 8, v95
	v_and_b32_e32 v95, 0xff00, v95
	v_and_b32_e32 v96, 0xff0000, v96
	v_perm_b32 v83, v97, v83, s42
	v_or3_b32 v83, v83, v95, v96
	v_mul_f32_e32 v95, v61, v1
	global_store_dword v[100:101], v83, off
	v_mul_f32_e32 v83, v60, v1
	v_mul_f32_e32 v96, v58, v1
	v_mul_f32_e32 v97, v59, v1
	v_med3_f32 v95, v95, s41, v93
	v_med3_f32 v83, v83, s41, v93
	v_rndne_f32_e32 v95, v95
	v_med3_f32 v96, v96, s41, v93
	v_med3_f32 v97, v97, s41, v93
	v_rndne_f32_e32 v83, v83
	v_cvt_i32_f32_e32 v95, v95
	v_rndne_f32_e32 v96, v96
	v_rndne_f32_e32 v97, v97
	v_cvt_i32_f32_e32 v83, v83
	v_cvt_i32_f32_sdwa v96, v96 dst_sel:WORD_1 dst_unused:UNUSED_PAD src0_sel:DWORD
	v_cvt_i32_f32_e32 v97, v97
	v_lshlrev_b32_e32 v95, 8, v95
	v_and_b32_e32 v95, 0xff00, v95
	v_and_b32_e32 v96, 0xff0000, v96
	v_perm_b32 v83, v97, v83, s42
	v_or3_b32 v83, v83, v95, v96
	v_mul_f32_e32 v95, v57, v1
	global_store_dword v[100:101], v83, off offset:256
	v_mul_f32_e32 v83, v56, v1
	v_mul_f32_e32 v96, v54, v1
	v_mul_f32_e32 v97, v55, v1
	v_med3_f32 v95, v95, s41, v93
	v_med3_f32 v83, v83, s41, v93
	v_rndne_f32_e32 v95, v95
	v_med3_f32 v96, v96, s41, v93
	v_med3_f32 v97, v97, s41, v93
	v_rndne_f32_e32 v83, v83
	v_cvt_i32_f32_e32 v95, v95
	v_rndne_f32_e32 v96, v96
	v_rndne_f32_e32 v97, v97
	v_cvt_i32_f32_e32 v83, v83
	v_cvt_i32_f32_sdwa v96, v96 dst_sel:WORD_1 dst_unused:UNUSED_PAD src0_sel:DWORD
	v_cvt_i32_f32_e32 v97, v97
	v_lshlrev_b32_e32 v95, 8, v95
	v_and_b32_e32 v95, 0xff00, v95
	v_and_b32_e32 v96, 0xff0000, v96
	v_perm_b32 v83, v97, v83, s42
	v_or3_b32 v83, v83, v95, v96
	v_mul_f32_e32 v95, v53, v1
	global_store_dword v[100:101], v83, off offset:512
	v_mul_f32_e32 v83, v52, v1
	v_mul_f32_e32 v96, v50, v1
	v_mul_f32_e32 v97, v51, v1
	v_med3_f32 v95, v95, s41, v93
	v_med3_f32 v83, v83, s41, v93
	v_rndne_f32_e32 v95, v95
	v_med3_f32 v96, v96, s41, v93
	v_med3_f32 v97, v97, s41, v93
	v_rndne_f32_e32 v83, v83
	v_cvt_i32_f32_e32 v95, v95
	v_rndne_f32_e32 v96, v96
	v_rndne_f32_e32 v97, v97
	v_cvt_i32_f32_e32 v83, v83
	v_cvt_i32_f32_sdwa v96, v96 dst_sel:WORD_1 dst_unused:UNUSED_PAD src0_sel:DWORD
	v_cvt_i32_f32_e32 v97, v97
	v_lshlrev_b32_e32 v95, 8, v95
	v_and_b32_e32 v95, 0xff00, v95
	v_and_b32_e32 v96, 0xff0000, v96
	v_perm_b32 v83, v97, v83, s42
	v_or3_b32 v83, v83, v95, v96
	v_mul_f32_e32 v95, v49, v1
	global_store_dword v[100:101], v83, off offset:768
	v_mul_f32_e32 v83, v48, v1
	v_mul_f32_e32 v96, v46, v1
	v_mul_f32_e32 v97, v47, v1
	v_med3_f32 v95, v95, s41, v93
	v_med3_f32 v83, v83, s41, v93
	v_rndne_f32_e32 v95, v95
	v_med3_f32 v96, v96, s41, v93
	v_med3_f32 v97, v97, s41, v93
	v_rndne_f32_e32 v83, v83
	v_cvt_i32_f32_e32 v95, v95
	v_rndne_f32_e32 v96, v96
	v_rndne_f32_e32 v97, v97
	v_cvt_i32_f32_e32 v83, v83
	v_cvt_i32_f32_sdwa v96, v96 dst_sel:WORD_1 dst_unused:UNUSED_PAD src0_sel:DWORD
	v_cvt_i32_f32_e32 v97, v97
	v_lshlrev_b32_e32 v95, 8, v95
	v_and_b32_e32 v95, 0xff00, v95
	v_and_b32_e32 v96, 0xff0000, v96
	v_perm_b32 v83, v97, v83, s42
	v_or3_b32 v83, v83, v95, v96
	v_mul_f32_e32 v95, v45, v1
	global_store_dword v[100:101], v83, off offset:1024
	v_mul_f32_e32 v83, v44, v1
	v_mul_f32_e32 v96, v42, v1
	v_mul_f32_e32 v97, v43, v1
	v_med3_f32 v95, v95, s41, v93
	v_med3_f32 v83, v83, s41, v93
	v_rndne_f32_e32 v95, v95
	v_med3_f32 v96, v96, s41, v93
	v_med3_f32 v97, v97, s41, v93
	v_rndne_f32_e32 v83, v83
	v_cvt_i32_f32_e32 v95, v95
	v_rndne_f32_e32 v96, v96
	v_rndne_f32_e32 v97, v97
	v_cvt_i32_f32_e32 v83, v83
	v_cvt_i32_f32_sdwa v96, v96 dst_sel:WORD_1 dst_unused:UNUSED_PAD src0_sel:DWORD
	v_cvt_i32_f32_e32 v97, v97
	v_lshlrev_b32_e32 v95, 8, v95
	v_and_b32_e32 v95, 0xff00, v95
	v_and_b32_e32 v96, 0xff0000, v96
	v_perm_b32 v83, v97, v83, s42
	v_or3_b32 v83, v83, v95, v96
	v_mul_f32_e32 v95, v41, v1
	global_store_dword v[100:101], v83, off offset:1280
	v_mul_f32_e32 v83, v40, v1
	v_mul_f32_e32 v96, v38, v1
	v_mul_f32_e32 v97, v39, v1
	v_med3_f32 v95, v95, s41, v93
	v_med3_f32 v83, v83, s41, v93
	v_rndne_f32_e32 v95, v95
	v_med3_f32 v96, v96, s41, v93
	v_med3_f32 v97, v97, s41, v93
	v_rndne_f32_e32 v83, v83
	v_cvt_i32_f32_e32 v95, v95
	v_rndne_f32_e32 v96, v96
	v_rndne_f32_e32 v97, v97
	v_cvt_i32_f32_e32 v83, v83
	v_cvt_i32_f32_sdwa v96, v96 dst_sel:WORD_1 dst_unused:UNUSED_PAD src0_sel:DWORD
	v_cvt_i32_f32_e32 v97, v97
	v_lshlrev_b32_e32 v95, 8, v95
	v_and_b32_e32 v95, 0xff00, v95
	v_and_b32_e32 v96, 0xff0000, v96
	v_perm_b32 v83, v97, v83, s42
	v_or3_b32 v83, v83, v95, v96
	v_mul_f32_e32 v95, v37, v1
	v_mul_f32_e32 v96, v34, v1
	global_store_dword v[100:101], v83, off offset:1536
	v_mul_f32_e32 v83, v36, v1
	v_mul_f32_e32 v1, v35, v1
	v_med3_f32 v95, v95, s41, v93
	v_med3_f32 v96, v96, s41, v93
	v_med3_f32 v83, v83, s41, v93
	v_rndne_f32_e32 v95, v95
	v_rndne_f32_e32 v96, v96
	v_med3_f32 v1, v1, s41, v93
	v_rndne_f32_e32 v83, v83
	v_cvt_i32_f32_e32 v95, v95
	v_cvt_i32_f32_sdwa v96, v96 dst_sel:WORD_1 dst_unused:UNUSED_PAD src0_sel:DWORD
	v_rndne_f32_e32 v1, v1
	v_cvt_i32_f32_e32 v83, v83
	v_cvt_i32_f32_e32 v1, v1
	v_lshlrev_b32_e32 v95, 8, v95
	v_and_b32_e32 v102, 0xff0000, v96
	ds_read_b128 v[96:99], v88
	v_and_b32_e32 v95, 0xff00, v95
	v_perm_b32 v1, v1, v83, s42
	v_or3_b32 v1, v1, v95, v102
	global_store_dword v[100:101], v1, off offset:1792
	ds_read_b128 v[100:103], v88 offset:1024
	s_waitcnt lgkmcnt(0)
; #define LAS __attribute__((address_space(3)))
; __device__ __forceinline__ float wave_sum(float v) { return lane63(scan64<false>(v)); }
; template <int YMODE, int EXTRA, bool NORM_OUT, bool XN8  , bool XIN_BF = false  , bool XOUT_BF = false  > ...
;     ...
;                 if (EXTRA) {
;                     float d8[8];
; #pragma unroll
;                     for (int e = 0; e < 8; ++e) { float s = 0.f;
; #pragma unroll
;                         for (int j = 0; j < 8; ++j) { const f32x4 w = *(const LAS f32x4*)(we + e * D + 256 * j + 4 * F.lane); s += (x[j][0] * w[0] + x[j][1] * w[1]) + (x[j][2] * w[2] + x[j][3] * w[3]); }
;                         d8[e] = wave_sum(s); asm volatile("" ::: "memory"); }
	v_mul_f32_e32 v1, v65, v97
	v_mul_f32_e32 v83, v63, v99
	v_fmac_f32_e32 v1, v64, v96
	v_fmac_f32_e32 v83, v62, v98
	ds_read_b128 v[96:99], v88 offset:2048
	v_add_f32_e32 v1, v1, v83
	v_mul_f32_e32 v83, v61, v101
	v_mul_f32_e32 v95, v59, v103
	v_fmac_f32_e32 v83, v60, v100
	v_fmac_f32_e32 v95, v58, v102
	ds_read_b128 v[100:103], v88 offset:3072
	v_add_f32_e32 v1, 0, v1
	v_add_f32_e32 v83, v83, v95
	v_add_f32_e32 v1, v1, v83
	s_waitcnt lgkmcnt(0)
	v_mul_f32_e32 v83, v57, v97
	v_mul_f32_e32 v95, v55, v99
	v_fmac_f32_e32 v83, v56, v96
	v_fmac_f32_e32 v95, v54, v98
	ds_read_b128 v[96:99], v88 offset:4096
	v_add_f32_e32 v83, v83, v95
	v_add_f32_e32 v1, v1, v83
	v_mul_f32_e32 v83, v53, v101
	v_mul_f32_e32 v95, v51, v103
	v_fmac_f32_e32 v83, v52, v100
	v_fmac_f32_e32 v95, v50, v102
	ds_read_b128 v[100:103], v88 offset:5120
	v_add_f32_e32 v83, v83, v95
	v_add_f32_e32 v1, v1, v83
	s_waitcnt lgkmcnt(0)
	v_mul_f32_e32 v83, v49, v97
	v_mul_f32_e32 v95, v47, v99
	v_fmac_f32_e32 v83, v48, v96
	v_fmac_f32_e32 v95, v46, v98
	ds_read_b128 v[96:99], v88 offset:6144
	v_add_f32_e32 v83, v83, v95
	v_add_f32_e32 v1, v1, v83
	v_mul_f32_e32 v83, v45, v101
	v_mul_f32_e32 v95, v43, v103
	v_fmac_f32_e32 v83, v44, v100
	v_fmac_f32_e32 v95, v42, v102
	ds_read_b128 v[100:103], v88 offset:7168
	v_add_f32_e32 v83, v83, v95
	v_add_f32_e32 v1, v1, v83
	s_waitcnt lgkmcnt(0)
	v_mul_f32_e32 v83, v41, v97
	v_mul_f32_e32 v95, v39, v99
	v_fmac_f32_e32 v83, v40, v96
	v_fmac_f32_e32 v95, v38, v98
	v_add_f32_e32 v83, v83, v95
	v_add_f32_e32 v1, v1, v83
	v_mul_f32_e32 v83, v37, v101
	v_mul_f32_e32 v95, v35, v103
	v_fmac_f32_e32 v83, v36, v100
	v_fmac_f32_e32 v95, v34, v102
	v_add_f32_e32 v83, v83, v95
	v_add_f32_e32 v1, v1, v83
	v_mov_b32_e32 v83, 0
	ds_read_b128 v[96:99], v88 offset:8192
	ds_read_b128 v[100:103], v88 offset:9216
	v_add_f32_dpp v1, v1, v1 row_shr:1 row_mask:0xf bank_mask:0xf bound_ctrl:1
	s_waitcnt lgkmcnt(0)
	v_mul_f32_e32 v95, v59, v103
	v_add_f32_dpp v1, v1, v1 row_shr:2 row_mask:0xf bank_mask:0xf bound_ctrl:1
	v_fmac_f32_e32 v95, v58, v102
	s_nop 0
	v_add_f32_dpp v1, v1, v1 row_shr:4 row_mask:0xf bank_mask:0xf bound_ctrl:1
	s_nop 1
	v_add_f32_dpp v1, v1, v1 row_shr:8 row_mask:0xf bank_mask:0xf bound_ctrl:1
	s_nop 1
	v_mov_b32_dpp v83, v1 row_bcast:15 row_mask:0xa bank_mask:0xf
	v_add_f32_e32 v1, v1, v83
	v_mov_b32_e32 v83, 0
	s_nop 1
	v_mov_b32_dpp v83, v1 row_bcast:31 row_mask:0xc bank_mask:0xf
	v_add_f32_e32 v1, v1, v83
	v_mul_f32_e32 v83, v63, v99
	v_readlane_b32 s34, v1, 63
	v_mul_f32_e32 v1, v65, v97
	v_fmac_f32_e32 v1, v64, v96
	v_fmac_f32_e32 v83, v62, v98
	ds_read_b128 v[96:99], v88 offset:10240
	v_add_f32_e32 v1, v1, v83
	v_mul_f32_e32 v83, v61, v101
	v_fmac_f32_e32 v83, v60, v100
	ds_read_b128 v[100:103], v88 offset:11264
	v_add_f32_e32 v1, 0, v1
	v_add_f32_e32 v83, v83, v95
	v_add_f32_e32 v1, v1, v83
	s_waitcnt lgkmcnt(0)
	v_mul_f32_e32 v83, v57, v97
	v_mul_f32_e32 v95, v55, v99
	v_fmac_f32_e32 v83, v56, v96
	v_fmac_f32_e32 v95, v54, v98
	ds_read_b128 v[96:99], v88 offset:12288
	v_add_f32_e32 v83, v83, v95
	v_add_f32_e32 v1, v1, v83
	v_mul_f32_e32 v83, v53, v101
	v_mul_f32_e32 v95, v51, v103
	v_fmac_f32_e32 v83, v52, v100
	v_fmac_f32_e32 v95, v50, v102
	ds_read_b128 v[100:103], v88 offset:13312
	v_add_f32_e32 v83, v83, v95
	v_add_f32_e32 v1, v1, v83
	s_waitcnt lgkmcnt(0)
	v_mul_f32_e32 v83, v49, v97
	v_mul_f32_e32 v95, v47, v99
	v_fmac_f32_e32 v83, v48, v96
	v_fmac_f32_e32 v95, v46, v98
	ds_read_b128 v[96:99], v88 offset:14336
	v_add_f32_e32 v83, v83, v95
	v_add_f32_e32 v1, v1, v83
	v_mul_f32_e32 v83, v45, v101
	v_mul_f32_e32 v95, v43, v103
	v_fmac_f32_e32 v83, v44, v100
	v_fmac_f32_e32 v95, v42, v102
	ds_read_b128 v[100:103], v88 offset:15360
	v_add_f32_e32 v83, v83, v95
	v_add_f32_e32 v1, v1, v83
	s_waitcnt lgkmcnt(0)
	v_mul_f32_e32 v83, v41, v97
	v_mul_f32_e32 v95, v39, v99
	v_fmac_f32_e32 v83, v40, v96
	v_fmac_f32_e32 v95, v38, v98
	v_add_f32_e32 v83, v83, v95
	v_add_f32_e32 v1, v1, v83
	v_mul_f32_e32 v83, v37, v101
	v_mul_f32_e32 v95, v35, v103
	v_fmac_f32_e32 v83, v36, v100
	v_fmac_f32_e32 v95, v34, v102
	v_add_f32_e32 v83, v83, v95
	v_add_f32_e32 v1, v1, v83
	v_mov_b32_e32 v83, 0
	ds_read_b128 v[96:99], v88 offset:16384
	ds_read_b128 v[100:103], v88 offset:17408
	v_add_f32_dpp v1, v1, v1 row_shr:1 row_mask:0xf bank_mask:0xf bound_ctrl:1
	s_waitcnt lgkmcnt(0)
	v_mul_f32_e32 v95, v59, v103
	v_add_f32_dpp v1, v1, v1 row_shr:2 row_mask:0xf bank_mask:0xf bound_ctrl:1
	v_fmac_f32_e32 v95, v58, v102
	s_nop 0
	v_add_f32_dpp v1, v1, v1 row_shr:4 row_mask:0xf bank_mask:0xf bound_ctrl:1
	s_nop 1
	v_add_f32_dpp v1, v1, v1 row_shr:8 row_mask:0xf bank_mask:0xf bound_ctrl:1
	s_nop 1
	v_mov_b32_dpp v83, v1 row_bcast:15 row_mask:0xa bank_mask:0xf
	v_add_f32_e32 v1, v1, v83
	v_mov_b32_e32 v83, 0
	s_nop 1
	v_mov_b32_dpp v83, v1 row_bcast:31 row_mask:0xc bank_mask:0xf
	v_add_f32_e32 v1, v1, v83
	v_mul_f32_e32 v83, v63, v99
	v_readlane_b32 s38, v1, 63
	v_mul_f32_e32 v1, v65, v97
	v_fmac_f32_e32 v1, v64, v96
	v_fmac_f32_e32 v83, v62, v98
	ds_read_b128 v[96:99], v88 offset:18432
	v_add_f32_e32 v1, v1, v83
	v_mul_f32_e32 v83, v61, v101
	v_fmac_f32_e32 v83, v60, v100
	ds_read_b128 v[100:103], v88 offset:19456
	v_add_f32_e32 v1, 0, v1
	v_add_f32_e32 v83, v83, v95
	v_add_f32_e32 v1, v1, v83
	s_waitcnt lgkmcnt(0)
	v_mul_f32_e32 v83, v57, v97
	v_mul_f32_e32 v95, v55, v99
	v_fmac_f32_e32 v83, v56, v96
	v_fmac_f32_e32 v95, v54, v98
	ds_read_b128 v[96:99], v88 offset:20480
	v_add_f32_e32 v83, v83, v95
	v_add_f32_e32 v1, v1, v83
	v_mul_f32_e32 v83, v53, v101
	v_mul_f32_e32 v95, v51, v103
	v_fmac_f32_e32 v83, v52, v100
	v_fmac_f32_e32 v95, v50, v102
	ds_read_b128 v[100:103], v88 offset:21504
	v_add_f32_e32 v83, v83, v95
	v_add_f32_e32 v1, v1, v83
	s_waitcnt lgkmcnt(0)
; #define LAS __attribute__((address_space(3)))
; __device__ __forceinline__ float wave_sum(float v) { return lane63(scan64<false>(v)); }
; template <int YMODE, int EXTRA, bool NORM_OUT, bool XN8  , bool XIN_BF = false  , bool XOUT_BF = false  > ...
;     ...
;                 if (EXTRA) {
;                     float d8[8];
; #pragma unroll
;                     for (int e = 0; e < 8; ++e) { float s = 0.f;
; #pragma unroll
;                         for (int j = 0; j < 8; ++j) { const f32x4 w = *(const LAS f32x4*)(we + e * D + 256 * j + 4 * F.lane); s += (x[j][0] * w[0] + x[j][1] * w[1]) + (x[j][2] * w[2] + x[j][3] * w[3]); }
;                         d8[e] = wave_sum(s); asm volatile("" ::: "memory"); }
	v_mul_f32_e32 v83, v49, v97
	v_mul_f32_e32 v95, v47, v99
	v_fmac_f32_e32 v83, v48, v96
	v_fmac_f32_e32 v95, v46, v98
	ds_read_b128 v[96:99], v88 offset:22528
	v_add_f32_e32 v83, v83, v95
	v_add_f32_e32 v1, v1, v83
	v_mul_f32_e32 v83, v45, v101
	v_mul_f32_e32 v95, v43, v103
	v_fmac_f32_e32 v83, v44, v100
	v_fmac_f32_e32 v95, v42, v102
	ds_read_b128 v[100:103], v88 offset:23552
	v_add_f32_e32 v83, v83, v95
	v_add_f32_e32 v1, v1, v83
	s_waitcnt lgkmcnt(0)
	v_mul_f32_e32 v83, v41, v97
	v_mul_f32_e32 v95, v39, v99
	v_fmac_f32_e32 v83, v40, v96
	v_fmac_f32_e32 v95, v38, v98
	v_add_f32_e32 v83, v83, v95
	v_add_f32_e32 v1, v1, v83
	v_mul_f32_e32 v83, v37, v101
	v_mul_f32_e32 v95, v35, v103
	v_fmac_f32_e32 v83, v36, v100
	v_fmac_f32_e32 v95, v34, v102
	v_add_f32_e32 v83, v83, v95
	v_add_f32_e32 v1, v1, v83
	v_mov_b32_e32 v83, 0
	ds_read_b128 v[96:99], v88 offset:24576
	ds_read_b128 v[100:103], v88 offset:25600
	v_add_f32_dpp v1, v1, v1 row_shr:1 row_mask:0xf bank_mask:0xf bound_ctrl:1
	s_waitcnt lgkmcnt(0)
	v_mul_f32_e32 v95, v59, v103
	v_add_f32_dpp v1, v1, v1 row_shr:2 row_mask:0xf bank_mask:0xf bound_ctrl:1
	v_fmac_f32_e32 v95, v58, v102
	s_nop 0
	v_add_f32_dpp v1, v1, v1 row_shr:4 row_mask:0xf bank_mask:0xf bound_ctrl:1
	s_nop 1
	v_add_f32_dpp v1, v1, v1 row_shr:8 row_mask:0xf bank_mask:0xf bound_ctrl:1
	s_nop 1
	v_mov_b32_dpp v83, v1 row_bcast:15 row_mask:0xa bank_mask:0xf
	v_add_f32_e32 v1, v1, v83
	v_mov_b32_e32 v83, 0
	s_nop 1
	v_mov_b32_dpp v83, v1 row_bcast:31 row_mask:0xc bank_mask:0xf
	v_add_f32_e32 v1, v1, v83
	v_mul_f32_e32 v83, v63, v99
	v_readlane_b32 s39, v1, 63
	v_mul_f32_e32 v1, v65, v97
	v_fmac_f32_e32 v1, v64, v96
	v_fmac_f32_e32 v83, v62, v98
	ds_read_b128 v[96:99], v88 offset:26624
	v_add_f32_e32 v1, v1, v83
	v_mul_f32_e32 v83, v61, v101
	v_fmac_f32_e32 v83, v60, v100
	ds_read_b128 v[100:103], v88 offset:27648
	v_add_f32_e32 v1, 0, v1
	v_add_f32_e32 v83, v83, v95
	v_add_f32_e32 v1, v1, v83
	s_waitcnt lgkmcnt(0)
	v_mul_f32_e32 v83, v57, v97
	v_mul_f32_e32 v95, v55, v99
	v_fmac_f32_e32 v83, v56, v96
	v_fmac_f32_e32 v95, v54, v98
	ds_read_b128 v[96:99], v88 offset:28672
	v_add_f32_e32 v83, v83, v95
	v_add_f32_e32 v1, v1, v83
	v_mul_f32_e32 v83, v53, v101
	v_mul_f32_e32 v95, v51, v103
	v_fmac_f32_e32 v83, v52, v100
	v_fmac_f32_e32 v95, v50, v102
	ds_read_b128 v[100:103], v88 offset:29696
	v_add_f32_e32 v83, v83, v95
	v_add_f32_e32 v1, v1, v83
	s_waitcnt lgkmcnt(0)
	v_mul_f32_e32 v83, v49, v97
	v_mul_f32_e32 v95, v47, v99
	v_fmac_f32_e32 v83, v48, v96
	v_fmac_f32_e32 v95, v46, v98
	ds_read_b128 v[96:99], v88 offset:30720
	v_add_f32_e32 v83, v83, v95
	v_add_f32_e32 v1, v1, v83
	v_mul_f32_e32 v83, v45, v101
	v_mul_f32_e32 v95, v43, v103
	v_fmac_f32_e32 v83, v44, v100
	v_fmac_f32_e32 v95, v42, v102
	ds_read_b128 v[100:103], v88 offset:31744
	v_add_f32_e32 v83, v83, v95
	v_add_f32_e32 v1, v1, v83
	s_waitcnt lgkmcnt(0)
	v_mul_f32_e32 v83, v41, v97
	v_mul_f32_e32 v95, v39, v99
	v_fmac_f32_e32 v83, v40, v96
	v_fmac_f32_e32 v95, v38, v98
	v_add_f32_e32 v83, v83, v95
	v_add_f32_e32 v1, v1, v83
	v_mul_f32_e32 v83, v37, v101
	v_mul_f32_e32 v95, v35, v103
	v_fmac_f32_e32 v83, v36, v100
	v_fmac_f32_e32 v95, v34, v102
	v_add_f32_e32 v83, v83, v95
	v_add_f32_e32 v1, v1, v83
	v_mov_b32_e32 v83, 0
	ds_read_b128 v[96:99], v88 offset:32768
	ds_read_b128 v[100:103], v88 offset:33792
	v_add_f32_dpp v1, v1, v1 row_shr:1 row_mask:0xf bank_mask:0xf bound_ctrl:1
	s_waitcnt lgkmcnt(0)
	v_mul_f32_e32 v95, v59, v103
	v_add_f32_dpp v1, v1, v1 row_shr:2 row_mask:0xf bank_mask:0xf bound_ctrl:1
	v_fmac_f32_e32 v95, v58, v102
	s_nop 0
	v_add_f32_dpp v1, v1, v1 row_shr:4 row_mask:0xf bank_mask:0xf bound_ctrl:1
	s_nop 1
	v_add_f32_dpp v1, v1, v1 row_shr:8 row_mask:0xf bank_mask:0xf bound_ctrl:1
	s_nop 1
	v_mov_b32_dpp v83, v1 row_bcast:15 row_mask:0xa bank_mask:0xf
	v_add_f32_e32 v1, v1, v83
	v_mov_b32_e32 v83, 0
	s_nop 1
	v_mov_b32_dpp v83, v1 row_bcast:31 row_mask:0xc bank_mask:0xf
	v_add_f32_e32 v1, v1, v83
	v_mul_f32_e32 v83, v63, v99
	v_readlane_b32 s60, v1, 63
	v_mul_f32_e32 v1, v65, v97
	v_fmac_f32_e32 v1, v64, v96
	v_fmac_f32_e32 v83, v62, v98
	ds_read_b128 v[96:99], v88 offset:34816
	v_add_f32_e32 v1, v1, v83
	v_mul_f32_e32 v83, v61, v101
	v_fmac_f32_e32 v83, v60, v100
	ds_read_b128 v[100:103], v88 offset:35840
	v_add_f32_e32 v1, 0, v1
	v_add_f32_e32 v83, v83, v95
	v_add_f32_e32 v1, v1, v83
	s_waitcnt lgkmcnt(0)
	v_mul_f32_e32 v83, v57, v97
	v_mul_f32_e32 v95, v55, v99
	v_fmac_f32_e32 v83, v56, v96
	v_fmac_f32_e32 v95, v54, v98
	ds_read_b128 v[96:99], v88 offset:36864
	v_add_f32_e32 v83, v83, v95
	v_add_f32_e32 v1, v1, v83
	v_mul_f32_e32 v83, v53, v101
	v_mul_f32_e32 v95, v51, v103
	v_fmac_f32_e32 v83, v52, v100
	v_fmac_f32_e32 v95, v50, v102
	ds_read_b128 v[100:103], v88 offset:37888
	v_add_f32_e32 v83, v83, v95
	v_add_f32_e32 v1, v1, v83
	s_waitcnt lgkmcnt(0)
	v_mul_f32_e32 v83, v49, v97
	v_mul_f32_e32 v95, v47, v99
	v_fmac_f32_e32 v83, v48, v96
	v_fmac_f32_e32 v95, v46, v98
	ds_read_b128 v[96:99], v88 offset:38912
	v_add_f32_e32 v83, v83, v95
	v_add_f32_e32 v1, v1, v83
	v_mul_f32_e32 v83, v45, v101
	v_mul_f32_e32 v95, v43, v103
	v_fmac_f32_e32 v83, v44, v100
	v_fmac_f32_e32 v95, v42, v102
	ds_read_b128 v[100:103], v88 offset:39936
	v_add_f32_e32 v83, v83, v95
	v_add_f32_e32 v1, v1, v83
	s_waitcnt lgkmcnt(0)
	v_mul_f32_e32 v83, v41, v97
	v_mul_f32_e32 v95, v39, v99
	v_fmac_f32_e32 v83, v40, v96
	v_fmac_f32_e32 v95, v38, v98
	v_add_f32_e32 v83, v83, v95
	v_add_f32_e32 v1, v1, v83
	v_mul_f32_e32 v83, v37, v101
	v_mul_f32_e32 v95, v35, v103
	v_fmac_f32_e32 v83, v36, v100
	v_fmac_f32_e32 v95, v34, v102
	v_add_f32_e32 v83, v83, v95
	v_add_f32_e32 v1, v1, v83
	v_mov_b32_e32 v83, 0
	ds_read_b128 v[96:99], v88 offset:40960
	ds_read_b128 v[100:103], v88 offset:41984
	v_add_f32_dpp v1, v1, v1 row_shr:1 row_mask:0xf bank_mask:0xf bound_ctrl:1
	s_waitcnt lgkmcnt(0)
; #define LAS __attribute__((address_space(3)))
; __device__ __forceinline__ float wave_sum(float v) { return lane63(scan64<false>(v)); }
; template <int YMODE, int EXTRA, bool NORM_OUT, bool XN8  , bool XIN_BF = false  , bool XOUT_BF = false  > ...
;     ...
;                 if (EXTRA) {
;                     float d8[8];
; #pragma unroll
;                     for (int e = 0; e < 8; ++e) { float s = 0.f;
; #pragma unroll
;                         for (int j = 0; j < 8; ++j) { const f32x4 w = *(const LAS f32x4*)(we + e * D + 256 * j + 4 * F.lane); s += (x[j][0] * w[0] + x[j][1] * w[1]) + (x[j][2] * w[2] + x[j][3] * w[3]); }
;                         d8[e] = wave_sum(s); asm volatile("" ::: "memory"); }
	v_mul_f32_e32 v95, v59, v103
	v_add_f32_dpp v1, v1, v1 row_shr:2 row_mask:0xf bank_mask:0xf bound_ctrl:1
	v_fmac_f32_e32 v95, v58, v102
	s_nop 0
	v_add_f32_dpp v1, v1, v1 row_shr:4 row_mask:0xf bank_mask:0xf bound_ctrl:1
	s_nop 1
	v_add_f32_dpp v1, v1, v1 row_shr:8 row_mask:0xf bank_mask:0xf bound_ctrl:1
	s_nop 1
	v_mov_b32_dpp v83, v1 row_bcast:15 row_mask:0xa bank_mask:0xf
	v_add_f32_e32 v1, v1, v83
	v_mov_b32_e32 v83, 0
	s_nop 1
	v_mov_b32_dpp v83, v1 row_bcast:31 row_mask:0xc bank_mask:0xf
	v_add_f32_e32 v1, v1, v83
	v_mul_f32_e32 v83, v63, v99
	v_readlane_b32 s61, v1, 63
	v_mul_f32_e32 v1, v65, v97
	v_fmac_f32_e32 v1, v64, v96
	v_fmac_f32_e32 v83, v62, v98
	ds_read_b128 v[96:99], v88 offset:43008
	v_add_f32_e32 v1, v1, v83
	v_mul_f32_e32 v83, v61, v101
	v_fmac_f32_e32 v83, v60, v100
	ds_read_b128 v[100:103], v88 offset:44032
	v_add_f32_e32 v1, 0, v1
	v_add_f32_e32 v83, v83, v95
	v_add_f32_e32 v1, v1, v83
	s_waitcnt lgkmcnt(0)
	v_mul_f32_e32 v83, v57, v97
	v_mul_f32_e32 v95, v55, v99
	v_fmac_f32_e32 v83, v56, v96
	v_fmac_f32_e32 v95, v54, v98
	ds_read_b128 v[96:99], v88 offset:45056
	v_add_f32_e32 v83, v83, v95
	v_add_f32_e32 v1, v1, v83
	v_mul_f32_e32 v83, v53, v101
	v_mul_f32_e32 v95, v51, v103
	v_fmac_f32_e32 v83, v52, v100
	v_fmac_f32_e32 v95, v50, v102
	ds_read_b128 v[100:103], v88 offset:46080
	v_add_f32_e32 v83, v83, v95
	v_add_f32_e32 v1, v1, v83
	s_waitcnt lgkmcnt(0)
	v_mul_f32_e32 v83, v49, v97
	v_mul_f32_e32 v95, v47, v99
	v_fmac_f32_e32 v83, v48, v96
	v_fmac_f32_e32 v95, v46, v98
	ds_read_b128 v[96:99], v88 offset:47104
	v_add_f32_e32 v83, v83, v95
	v_add_f32_e32 v1, v1, v83
	v_mul_f32_e32 v83, v45, v101
	v_mul_f32_e32 v95, v43, v103
	v_fmac_f32_e32 v83, v44, v100
	v_fmac_f32_e32 v95, v42, v102
	ds_read_b128 v[100:103], v88 offset:48128
	v_add_f32_e32 v83, v83, v95
	v_add_f32_e32 v1, v1, v83
	s_waitcnt lgkmcnt(0)
	v_mul_f32_e32 v83, v41, v97
	v_mul_f32_e32 v95, v39, v99
	v_fmac_f32_e32 v83, v40, v96
	v_fmac_f32_e32 v95, v38, v98
	v_add_f32_e32 v83, v83, v95
	v_add_f32_e32 v1, v1, v83
	v_mul_f32_e32 v83, v37, v101
	v_mul_f32_e32 v95, v35, v103
	v_fmac_f32_e32 v83, v36, v100
	v_fmac_f32_e32 v95, v34, v102
	v_add_f32_e32 v83, v83, v95
	v_add_f32_e32 v1, v1, v83
	v_mov_b32_e32 v83, 0
	ds_read_b128 v[96:99], v88 offset:49152
	ds_read_b128 v[100:103], v88 offset:50176
	v_add_f32_dpp v1, v1, v1 row_shr:1 row_mask:0xf bank_mask:0xf bound_ctrl:1
	s_waitcnt lgkmcnt(0)
	v_mul_f32_e32 v95, v59, v103
	v_add_f32_dpp v1, v1, v1 row_shr:2 row_mask:0xf bank_mask:0xf bound_ctrl:1
	v_fmac_f32_e32 v95, v58, v102
	s_nop 0
	v_add_f32_dpp v1, v1, v1 row_shr:4 row_mask:0xf bank_mask:0xf bound_ctrl:1
	s_nop 1
	v_add_f32_dpp v1, v1, v1 row_shr:8 row_mask:0xf bank_mask:0xf bound_ctrl:1
	s_nop 1
	v_mov_b32_dpp v83, v1 row_bcast:15 row_mask:0xa bank_mask:0xf
	v_add_f32_e32 v1, v1, v83
	v_mov_b32_e32 v83, 0
	s_nop 1
	v_mov_b32_dpp v83, v1 row_bcast:31 row_mask:0xc bank_mask:0xf
	v_add_f32_e32 v1, v1, v83
	v_mul_f32_e32 v83, v63, v99
	v_readlane_b32 s62, v1, 63
	v_mul_f32_e32 v1, v65, v97
	v_fmac_f32_e32 v1, v64, v96
	v_fmac_f32_e32 v83, v62, v98
	ds_read_b128 v[96:99], v88 offset:51200
	v_add_f32_e32 v1, v1, v83
	v_mul_f32_e32 v83, v61, v101
	v_fmac_f32_e32 v83, v60, v100
	ds_read_b128 v[100:103], v88 offset:52224
	v_add_f32_e32 v1, 0, v1
	v_add_f32_e32 v83, v83, v95
	v_add_f32_e32 v1, v1, v83
	s_waitcnt lgkmcnt(0)
	v_mul_f32_e32 v83, v57, v97
	v_mul_f32_e32 v95, v55, v99
	v_fmac_f32_e32 v83, v56, v96
	v_fmac_f32_e32 v95, v54, v98
	ds_read_b128 v[96:99], v88 offset:53248
	v_add_f32_e32 v83, v83, v95
	v_add_f32_e32 v1, v1, v83
	v_mul_f32_e32 v83, v53, v101
	v_mul_f32_e32 v95, v51, v103
	v_fmac_f32_e32 v83, v52, v100
	v_fmac_f32_e32 v95, v50, v102
	ds_read_b128 v[100:103], v88 offset:54272
	v_add_f32_e32 v83, v83, v95
	v_add_f32_e32 v1, v1, v83
	s_waitcnt lgkmcnt(0)
	v_mul_f32_e32 v83, v49, v97
	v_mul_f32_e32 v95, v47, v99
	v_fmac_f32_e32 v83, v48, v96
	v_fmac_f32_e32 v95, v46, v98
	ds_read_b128 v[96:99], v88 offset:55296
	v_add_f32_e32 v83, v83, v95
	v_add_f32_e32 v1, v1, v83
	v_mul_f32_e32 v83, v45, v101
	v_mul_f32_e32 v95, v43, v103
	v_fmac_f32_e32 v83, v44, v100
	v_fmac_f32_e32 v95, v42, v102
	ds_read_b128 v[100:103], v88 offset:56320
	v_add_f32_e32 v83, v83, v95
	v_add_f32_e32 v1, v1, v83
	s_waitcnt lgkmcnt(0)
; #define LAS __attribute__((address_space(3)))
; __device__ __forceinline__ float wave_sum(float v) { return lane63(scan64<false>(v)); }
; template <int YMODE, int EXTRA, bool NORM_OUT, bool XN8  , bool XIN_BF = false  , bool XOUT_BF = false  > ...
;     ...
;                     for (int e = 0; e < 8; ++e) { float s = 0.f;
; #pragma unroll
;                         for (int j = 0; j < 8; ++j) { const f32x4 w = *(const LAS f32x4*)(we + e * D + 256 * j + 4 * F.lane); s += (x[j][0] * w[0] + x[j][1] * w[1]) + (x[j][2] * w[2] + x[j][3] * w[3]); }
;                         d8[e] = wave_sum(s); asm volatile("" ::: "memory"); }
;                     if (EXTRA == 1) {
;                         float v = 0.f;
; #pragma unroll
;                         for (int e = 0; e < 8; ++e) v = (F.lane == e) ? d8[e] : v;
;                         if (F.lane < 8) { const float bb = (F.lane < 4) ? bi[F.lane] : bfg[F.lane - 4]; const float z = 15.f * tanhf((v + bb) * (1.f / 15.f));
;                             const float o = (F.lane < 4) ? z : (fminf(z, 0.f) - log1pf(expf(-fabsf(z)))); gates_out[row * 8 + F.lane] = o; }
	v_mul_f32_e32 v83, v41, v97
	v_mul_f32_e32 v95, v39, v99
	v_fmac_f32_e32 v83, v40, v96
	v_fmac_f32_e32 v95, v38, v98
	v_add_f32_e32 v83, v83, v95
	v_add_f32_e32 v1, v1, v83
	v_mul_f32_e32 v83, v37, v101
	v_mul_f32_e32 v95, v35, v103
	v_fmac_f32_e32 v83, v36, v100
	v_fmac_f32_e32 v95, v34, v102
	v_add_f32_e32 v83, v83, v95
	v_add_f32_e32 v1, v1, v83
	v_mov_b32_e32 v83, 0
	ds_read_b128 v[96:99], v88 offset:57344
	ds_read_b128 v[100:103], v88 offset:58368
	v_add_f32_dpp v1, v1, v1 row_shr:1 row_mask:0xf bank_mask:0xf bound_ctrl:1
	s_waitcnt lgkmcnt(0)
	v_mul_f32_e32 v63, v63, v99
	v_add_f32_dpp v1, v1, v1 row_shr:2 row_mask:0xf bank_mask:0xf bound_ctrl:1
	v_fmac_f32_e32 v63, v62, v98
	v_mul_f32_e32 v59, v59, v103
	v_add_f32_dpp v1, v1, v1 row_shr:4 row_mask:0xf bank_mask:0xf bound_ctrl:1
	v_fmac_f32_e32 v59, v58, v102
	s_nop 0
	v_add_f32_dpp v1, v1, v1 row_shr:8 row_mask:0xf bank_mask:0xf bound_ctrl:1
	s_nop 1
	v_mov_b32_dpp v83, v1 row_bcast:15 row_mask:0xa bank_mask:0xf
	v_add_f32_e32 v1, v1, v83
	v_mov_b32_e32 v83, 0
	s_nop 1
	v_mov_b32_dpp v83, v1 row_bcast:31 row_mask:0xc bank_mask:0xf
	v_add_f32_e32 v1, v1, v83
	s_nop 0
	v_readlane_b32 s63, v1, 63
	v_mul_f32_e32 v1, v65, v97
	v_fmac_f32_e32 v1, v64, v96
	v_mul_f32_e32 v64, v61, v101
	v_add_f32_e32 v1, v1, v63
	v_fmac_f32_e32 v64, v60, v100
	ds_read_b128 v[60:63], v88 offset:59392
	ds_read_b128 v[96:99], v88 offset:60416
	v_add_f32_e32 v1, 0, v1
	v_add_f32_e32 v58, v64, v59
	v_add_f32_e32 v1, v1, v58
	s_waitcnt lgkmcnt(0)
	v_mul_f32_e32 v57, v57, v61
	v_mul_f32_e32 v55, v55, v63
	v_fmac_f32_e32 v57, v56, v60
	v_fmac_f32_e32 v55, v54, v62
	v_add_f32_e32 v54, v57, v55
	v_mul_f32_e32 v56, v53, v97
	v_add_f32_e32 v1, v1, v54
	v_fmac_f32_e32 v56, v52, v96
	v_mul_f32_e32 v51, v51, v99
	ds_read_b128 v[52:55], v88 offset:61440
	v_fmac_f32_e32 v51, v50, v98
	v_add_f32_e32 v50, v56, v51
	ds_read_b128 v[56:59], v88 offset:62464
	v_add_f32_e32 v1, v1, v50
	s_waitcnt lgkmcnt(0)
	v_mul_f32_e32 v49, v49, v53
	v_mul_f32_e32 v47, v47, v55
	v_fmac_f32_e32 v49, v48, v52
	v_fmac_f32_e32 v47, v46, v54
	v_add_f32_e32 v46, v49, v47
	v_mul_f32_e32 v48, v45, v57
	v_mul_f32_e32 v43, v43, v59
	v_add_f32_e32 v1, v1, v46
	v_fmac_f32_e32 v48, v44, v56
	ds_read_b128 v[44:47], v88 offset:63488
	v_fmac_f32_e32 v43, v42, v58
	v_add_f32_e32 v42, v48, v43
	ds_read_b128 v[48:51], v88 offset:64512
	v_add_f32_e32 v1, v1, v42
	s_waitcnt lgkmcnt(0)
	v_mul_f32_e32 v41, v41, v45
	v_mul_f32_e32 v39, v39, v47
	v_fmac_f32_e32 v41, v40, v44
	v_fmac_f32_e32 v39, v38, v46
	v_mul_f32_e32 v37, v37, v49
	v_mul_f32_e32 v35, v35, v51
	v_add_f32_e32 v38, v41, v39
	v_fmac_f32_e32 v37, v36, v48
	v_fmac_f32_e32 v35, v34, v50
	v_add_f32_e32 v1, v1, v38
	v_add_f32_e32 v34, v37, v35
	v_add_f32_e32 v1, v1, v34
	v_mov_b32_e32 v34, 0
	s_nop 0
	v_add_f32_dpp v1, v1, v1 row_shr:1 row_mask:0xf bank_mask:0xf bound_ctrl:1
	s_nop 1
	v_add_f32_dpp v1, v1, v1 row_shr:2 row_mask:0xf bank_mask:0xf bound_ctrl:1
	s_nop 1
	v_add_f32_dpp v1, v1, v1 row_shr:4 row_mask:0xf bank_mask:0xf bound_ctrl:1
	s_nop 1
	v_add_f32_dpp v1, v1, v1 row_shr:8 row_mask:0xf bank_mask:0xf bound_ctrl:1
	s_nop 1
	v_mov_b32_dpp v34, v1 row_bcast:15 row_mask:0xa bank_mask:0xf
	v_add_f32_e32 v1, v1, v34
	v_mov_b32_e32 v34, 0
	s_nop 1
	v_mov_b32_dpp v34, v1 row_bcast:31 row_mask:0xc bank_mask:0xf
	v_add_f32_e32 v1, v1, v34
	s_nop 0
	v_readlane_b32 s64, v1, 63
	s_and_saveexec_b64 s[36:37], s[8:9]
	s_cbranch_execz .LBB0_107
	global_load_dword v1, v[76:77], off
	v_mov_b32_e32 v34, s34
	v_cndmask_b32_e64 v34, 0, v34, s[6:7]
	v_mov_b32_e32 v35, s38
	v_cndmask_b32_e64 v34, v34, v35, s[22:23]
	v_mov_b32_e32 v35, s39
	v_cndmask_b32_e64 v34, v34, v35, s[20:21]
	v_mov_b32_e32 v35, s60
	v_cndmask_b32_e64 v34, v34, v35, s[18:19]
	v_mov_b32_e32 v35, s61
	v_cndmask_b32_e64 v34, v34, v35, s[16:17]
	v_mov_b32_e32 v35, s62
	v_cndmask_b32_e64 v34, v34, v35, s[14:15]
	v_mov_b32_e32 v35, s63
	v_cndmask_b32_e64 v34, v34, v35, s[12:13]
	v_mov_b32_e32 v35, s64
	v_cndmask_b32_e64 v34, v34, v35, s[10:11]
	s_waitcnt vmcnt(0) lgkmcnt(0)
	v_add_f32_e32 v1, v34, v1
	v_mul_f32_e32 v1, 0x3d888889, v1
	v_cmp_nlt_f32_e64 s[38:39], |v1|, s43
	s_and_saveexec_b64 s[60:61], s[38:39]
	s_xor_b64 s[38:39], exec, s[60:61]
	s_cbranch_execz .LBB0_115
	v_add_f32_e64 v34, |v1|, |v1|
	v_mul_f32_e32 v35, 0x3fb8aa3b, v34
	v_rndne_f32_e32 v36, v35
	v_sub_f32_e32 v37, v35, v36
	v_fma_f32 v35, v34, s44, -v35
	v_fmac_f32_e32 v35, 0x32a5705f, v34
	v_add_f32_e32 v35, v37, v35
	v_cvt_i32_f32_e32 v36, v36
	v_exp_f32_e32 v35, v35
	v_cmp_ngt_f32_e32 vcc, s45, v34
	v_ldexp_f32 v35, v35, v36
	s_nop 0
	v_cndmask_b32_e32 v35, 0, v35, vcc
	v_cmp_nlt_f32_e32 vcc, s46, v34
	s_nop 1
	v_cndmask_b32_e32 v34, v94, v35, vcc
	v_add_f32_e32 v34, 1.0, v34
	v_rcp_f32_e32 v34, v34
	s_nop 0
	v_fma_f32 v34, v34, -2.0, 1.0

; __device__ __forceinline__ void cvt_item_i8(const float* src, int ld, int k0, int c0, unsigned char* dst, int Kd, int drow0, const float* cmx  , unsigned char* scr, int lane) {
;     const int c = lane & 7, q = lane >> 3;
;     const f32x4 cm = *(const f32x4*)(cmx + 4 * c);
;     f32x4 inv; inv[0] = cm[0] > 0.f ? 127.f / cm[0] : 0.f; inv[1] = cm[1] > 0.f ? 127.f / cm[1] : 0.f; inv[2] = cm[2] > 0.f ? 127.f / cm[2] : 0.f; inv[3] = cm[3] > 0.f ? 127.f / cm[3] : 0.f;
;     f32x4 v[4][4];
; #pragma unroll
;     for (int g = 0; g < 4; ++g)
; #pragma unroll
;         for (int j = 0; j < 4; ++j) v[g][j] = __builtin_nontemporal_load((const f32x4*)(src + (size_t)(k0 + 32 * g + 4 * q + j) * ld + c0 + 4 * c));
; #pragma unroll
;     for (int g = 0; g < 4; ++g)
; #pragma unroll
;         for (int i = 0; i < 4; ++i) *(unsigned*)(scr + (4 * c + i) * 132 + 32 * g + 4 * q) = pack_i8x4(v[g][0][i] * inv[i], v[g][1][i] * inv[i], v[g][2][i] * inv[i], v[g][3][i] * inv[i]);
; template <int GRP>
; __device__ __forceinline__ void conv_item(Frame& F, int r) {
;     ...
;         if (r < NI) { const int kb = r / 152, nb = r % 152, c0 = (nb < 112) ? nb * 32 : SRC_GATE + 8 + (nb - 112) * 32, drow = nb * 32;
;             if (QUANT) cvt_item_i8(inptr(F, IN_WIN) + (size_t)l * D * NIN_SRC, NIN_SRC, kb * 128, c0, ws + WS_WIN + (size_t)l * NIN * D, D, drow, cmx + CMX_WIN + l * NIN + drow, scr, F.lane);
.LBB0_126:
	s_mul_hi_i32 s6, s24, 0x6bca1af3
	s_lshr_b32 s7, s6, 31
	s_ashr_i32 s6, s6, 6
	s_add_i32 s7, s6, s7
	s_mul_i32 s8, s7, 0xffffed00
	s_mul_i32 s6, s7, 0xffffff68
	s_add_i32 s14, s3, s8
	s_add_i32 s6, s24, s6
	s_add_i32 s8, s14, 8
	s_cmpk_lt_i32 s6, 0x70
	s_cselect_b32 s6, s14, s8
	s_ashr_i32 s15, s14, 31
	v_lshl_add_u64 v[2:3], s[14:15], 2, v[36:37]
	global_load_dwordx4 v[2:5], v[2:3], off
	v_mov_b32_e32 v6, s5
	ds_read_b64 v[6:7], v6
	s_lshl_b32 s16, s7, 7
	s_ashr_i32 s7, s6, 31
	s_lshl_b64 s[6:7], s[6:7], 2
	v_or_b32_e32 v16, s16, v44
	s_waitcnt lgkmcnt(0)
	v_readfirstlane_b32 s8, v6
	v_readfirstlane_b32 s9, v7
	s_add_u32 s6, s8, s6
	s_addc_u32 s7, s9, s7
	v_lshl_add_u64 v[10:11], s[6:7], 0, v[34:35]
	v_or_b32_e32 v8, 1, v16
	v_or_b32_e32 v12, 2, v16
	v_or_b32_e32 v14, 3, v16
	v_mad_i64_i32 v[6:7], s[6:7], v16, s19, v[10:11]
	v_mad_i64_i32 v[8:9], s[6:7], v8, s19, v[10:11]
	v_mad_i64_i32 v[12:13], s[6:7], v12, s19, v[10:11]
	v_mad_i64_i32 v[14:15], s[6:7], v14, s19, v[10:11]
	global_load_dwordx4 v[26:29], v[6:7], off nt
	global_load_dwordx4 v[30:33], v[8:9], off nt
	global_load_dwordx4 v[72:75], v[12:13], off nt
	global_load_dwordx4 v[76:79], v[14:15], off nt
	v_or_b32_e32 v17, 32, v16
	s_ashr_i32 s17, s16, 31
	s_waitcnt vmcnt(0)
	v_div_scale_f32 v6, s[6:7], v2, v2, s18
	v_div_scale_f32 v8, s[6:7], v3, v3, s18
	v_rcp_f32_e32 v18, v6
	v_rcp_f32_e32 v19, v8
	v_div_scale_f32 v12, s[8:9], v4, v4, s18
	v_rcp_f32_e32 v20, v12
	v_div_scale_f32 v14, s[10:11], v5, v5, s18
	v_fma_f32 v22, -v6, v18, 1.0
	v_div_scale_f32 v7, vcc, s18, v2, s18
	v_rcp_f32_e32 v21, v14
	v_fma_f32 v23, -v8, v19, 1.0
	v_fmac_f32_e32 v18, v22, v18
	v_div_scale_f32 v9, s[6:7], s18, v3, s18
	v_fmac_f32_e32 v19, v23, v19
	v_mul_f32_e32 v22, v7, v18
	v_fma_f32 v24, -v12, v20, 1.0
	v_mul_f32_e32 v23, v9, v19
	v_fma_f32 v71, -v6, v22, v7
	v_div_scale_f32 v13, s[8:9], s18, v4, s18
	v_fmac_f32_e32 v20, v24, v20
	v_fma_f32 v80, -v8, v23, v9
	v_fmac_f32_e32 v22, v71, v18
	v_fma_f32 v25, -v14, v21, 1.0
	v_mul_f32_e32 v24, v13, v20
	v_fmac_f32_e32 v23, v80, v19
	v_fma_f32 v6, -v6, v22, v7
	v_div_scale_f32 v15, s[10:11], s18, v5, s18
	v_fmac_f32_e32 v21, v25, v21
	v_fma_f32 v81, -v12, v24, v13
	v_fma_f32 v7, -v8, v23, v9
	v_div_fmas_f32 v6, v6, v18, v22
	s_mov_b64 vcc, s[6:7]
	v_mul_f32_e32 v25, v15, v21
	v_fmac_f32_e32 v24, v81, v20
	v_div_fixup_f32 v6, v6, v2, s18
	v_div_fmas_f32 v7, v7, v19, v23
	v_cmp_lt_f32_e32 vcc, 0, v2
	v_fma_f32 v82, -v14, v25, v15
	v_fma_f32 v8, -v12, v24, v13
	v_cndmask_b32_e32 v71, 0, v6, vcc
	s_mov_b64 vcc, s[8:9]
	v_fmac_f32_e32 v25, v82, v21
	v_div_fixup_f32 v2, v7, v3, s18
	v_div_fmas_f32 v6, v8, v20, v24
	v_cmp_lt_f32_e32 vcc, 0, v3
	v_fma_f32 v9, -v14, v25, v15
	s_waitcnt lgkmcnt(0)
	v_mul_f32_e32 v30, v71, v30
	v_cndmask_b32_e32 v108, 0, v2, vcc
	s_mov_b64 vcc, s[10:11]
	v_div_fixup_f32 v2, v6, v4, s18
	v_div_fmas_f32 v3, v9, v21, v25
	v_cmp_lt_f32_e32 vcc, 0, v4
	v_or_b32_e32 v4, 33, v16
	v_mul_f32_e32 v26, v26, v71
	v_cndmask_b32_e32 v109, 0, v2, vcc
	v_div_fixup_f32 v2, v3, v5, s18
	v_cmp_lt_f32_e32 vcc, 0, v5
	v_mad_i64_i32 v[4:5], s[6:7], v4, s19, v[10:11]
	s_nop 0
	v_cndmask_b32_e32 v110, 0, v2, vcc
	v_mad_i64_i32 v[2:3], s[6:7], v17, s19, v[10:11]
	global_load_dwordx4 v[80:83], v[2:3], off nt
	global_load_dwordx4 v[84:87], v[4:5], off nt
	v_or_b32_e32 v2, 34, v16
	v_mad_i64_i32 v[2:3], s[6:7], v2, s19, v[10:11]
	v_or_b32_e32 v4, 35, v16
	v_mad_i64_i32 v[4:5], s[6:7], v4, s19, v[10:11]
	global_load_dwordx4 v[88:91], v[2:3], off nt
	global_load_dwordx4 v[92:95], v[4:5], off nt
	v_or_b32_e32 v2, 64, v16
	v_mad_i64_i32 v[2:3], s[6:7], v2, s19, v[10:11]
	v_or_b32_e32 v4, 0x41, v16
	v_mad_i64_i32 v[4:5], s[6:7], v4, s19, v[10:11]
	global_load_dwordx4 v[18:21], v[2:3], off nt
	global_load_dwordx4 v[22:25], v[4:5], off nt
	v_or_b32_e32 v2, 0x42, v16
	v_mad_i64_i32 v[2:3], s[6:7], v2, s19, v[10:11]
	v_or_b32_e32 v4, 0x43, v16
	v_mad_i64_i32 v[4:5], s[6:7], v4, s19, v[10:11]
	global_load_dwordx4 v[96:99], v[2:3], off nt
	global_load_dwordx4 v[100:103], v[4:5], off nt
	v_or_b32_e32 v2, 0x60, v16
	v_mad_i64_i32 v[12:13], s[6:7], v2, s19, v[10:11]
	v_or_b32_e32 v2, 0x61, v16
	v_mad_i64_i32 v[14:15], s[6:7], v2, s19, v[10:11]
	global_load_dwordx4 v[2:5], v[12:13], off nt
	global_load_dwordx4 v[6:9], v[14:15], off nt
	v_or_b32_e32 v12, 0x62, v16
	v_mad_i64_i32 v[104:105], s[6:7], v12, s19, v[10:11]
	v_or_b32_e32 v12, 0x63, v16
	v_mad_i64_i32 v[106:107], s[6:7], v12, s19, v[10:11]
	global_load_dwordx4 v[10:13], v[104:105], off nt
	global_load_dwordx4 v[14:17], v[106:107], off nt
	v_mul_f32_e32 v72, v71, v72
	v_med3_f32 v30, v30, s20, v56
	v_mul_f32_e32 v76, v71, v76
	v_med3_f32 v26, v26, s20, v56
	v_rndne_f32_e32 v30, v30
	v_med3_f32 v72, v72, s20, v56
	v_rndne_f32_e32 v26, v26
	v_cvt_i32_f32_e32 v30, v30
	v_rndne_f32_e32 v72, v72
	v_med3_f32 v76, v76, s20, v56
	v_cvt_i32_f32_e32 v26, v26
	v_cvt_i32_f32_sdwa v72, v72 dst_sel:WORD_1 dst_unused:UNUSED_PAD src0_sel:DWORD
	v_rndne_f32_e32 v76, v76
	v_cvt_i32_f32_sdwa v76, v76 dst_sel:BYTE_3 dst_unused:UNUSED_PAD src0_sel:DWORD
	v_lshlrev_b32_e32 v30, 8, v30
	v_perm_b32 v26, v30, v26, s21
	v_and_b32_e32 v30, 0xff0000, v72
	v_or3_b32 v26, v26, v30, v76
	v_mul_f32_e32 v30, v108, v31
	v_mul_f32_e32 v27, v27, v108
	v_mul_f32_e32 v31, v108, v73
	v_med3_f32 v30, v30, s20, v56
	v_mul_f32_e32 v72, v108, v77
	v_med3_f32 v27, v27, s20, v56
	v_rndne_f32_e32 v30, v30
	v_med3_f32 v31, v31, s20, v56
	v_rndne_f32_e32 v27, v27
	v_cvt_i32_f32_e32 v30, v30
	v_rndne_f32_e32 v31, v31
	v_med3_f32 v72, v72, s20, v56
	v_cvt_i32_f32_e32 v27, v27
	v_cvt_i32_f32_sdwa v31, v31 dst_sel:WORD_1 dst_unused:UNUSED_PAD src0_sel:DWORD
; __device__ __forceinline__ void cvt_item_i8(const float* src, int ld, int k0, int c0, unsigned char* dst, int Kd, int drow0, const float* cmx  , unsigned char* scr, int lane) {
;     ...
; #pragma unroll
;     for (int g = 0; g < 4; ++g)
; #pragma unroll
;         for (int i = 0; i < 4; ++i) *(unsigned*)(scr + (4 * c + i) * 132 + 32 * g + 4 * q) = pack_i8x4(v[g][0][i] * inv[i], v[g][1][i] * inv[i], v[g][2][i] * inv[i], v[g][3][i] * inv[i]);
;     asm volatile("s_waitcnt lgkmcnt(0)" ::: "memory");
	v_rndne_f32_e32 v72, v72
	v_cvt_i32_f32_sdwa v72, v72 dst_sel:BYTE_3 dst_unused:UNUSED_PAD src0_sel:DWORD
	v_lshlrev_b32_e32 v30, 8, v30
	v_perm_b32 v27, v30, v27, s21
	v_and_b32_e32 v30, 0xff0000, v31
	v_or3_b32 v27, v27, v30, v72
	v_mul_f32_e32 v30, v109, v32
	v_mul_f32_e32 v28, v28, v109
	v_mul_f32_e32 v31, v109, v74
	v_med3_f32 v30, v30, s20, v56
	v_mul_f32_e32 v32, v109, v78
	v_med3_f32 v28, v28, s20, v56
	v_rndne_f32_e32 v30, v30
	v_med3_f32 v31, v31, s20, v56
	v_rndne_f32_e32 v28, v28
	v_cvt_i32_f32_e32 v30, v30
	v_rndne_f32_e32 v31, v31
	v_med3_f32 v32, v32, s20, v56
	v_cvt_i32_f32_e32 v28, v28
	v_cvt_i32_f32_sdwa v31, v31 dst_sel:WORD_1 dst_unused:UNUSED_PAD src0_sel:DWORD
	v_rndne_f32_e32 v32, v32
	v_cvt_i32_f32_sdwa v32, v32 dst_sel:BYTE_3 dst_unused:UNUSED_PAD src0_sel:DWORD
	v_lshlrev_b32_e32 v30, 8, v30
	v_perm_b32 v28, v30, v28, s21
	v_and_b32_e32 v30, 0xff0000, v31
	v_or3_b32 v28, v28, v30, v32
	v_mul_f32_e32 v30, v110, v33
	v_mul_f32_e32 v29, v29, v110
	v_mul_f32_e32 v31, v110, v75
	v_med3_f32 v30, v30, s20, v56
	v_mul_f32_e32 v32, v110, v79
	v_med3_f32 v29, v29, s20, v56
	v_rndne_f32_e32 v30, v30
	v_med3_f32 v31, v31, s20, v56
	v_rndne_f32_e32 v29, v29
	v_cvt_i32_f32_e32 v30, v30
	v_rndne_f32_e32 v31, v31
	v_med3_f32 v32, v32, s20, v56
	v_cvt_i32_f32_e32 v29, v29
	v_cvt_i32_f32_sdwa v31, v31 dst_sel:WORD_1 dst_unused:UNUSED_PAD src0_sel:DWORD
	v_rndne_f32_e32 v32, v32
	v_cvt_i32_f32_sdwa v32, v32 dst_sel:BYTE_3 dst_unused:UNUSED_PAD src0_sel:DWORD
	v_lshlrev_b32_e32 v30, 8, v30
	v_perm_b32 v29, v30, v29, s21
	v_and_b32_e32 v30, 0xff0000, v31
	s_waitcnt vmcnt(0) lgkmcnt(0)
	v_mul_f32_e32 v31, v71, v84
	v_or3_b32 v29, v29, v30, v32
	v_mul_f32_e32 v30, v71, v80
	v_mul_f32_e32 v32, v71, v88
	v_med3_f32 v31, v31, s20, v56
	v_mul_f32_e32 v33, v71, v92
	v_med3_f32 v30, v30, s20, v56
	v_rndne_f32_e32 v31, v31
	v_med3_f32 v32, v32, s20, v56
	v_rndne_f32_e32 v30, v30
	v_cvt_i32_f32_e32 v31, v31
	v_rndne_f32_e32 v32, v32
	v_med3_f32 v33, v33, s20, v56
	v_cvt_i32_f32_e32 v30, v30
	v_cvt_i32_f32_sdwa v32, v32 dst_sel:WORD_1 dst_unused:UNUSED_PAD src0_sel:DWORD
	v_rndne_f32_e32 v33, v33
	v_cvt_i32_f32_sdwa v33, v33 dst_sel:BYTE_3 dst_unused:UNUSED_PAD src0_sel:DWORD
	v_lshlrev_b32_e32 v31, 8, v31
	v_perm_b32 v30, v31, v30, s21
	v_and_b32_e32 v31, 0xff0000, v32
	v_or3_b32 v30, v30, v31, v33
	ds_write2_b32 v48, v26, v30 offset1:8
	v_mul_f32_e32 v30, v108, v85
	v_mul_f32_e32 v26, v108, v81
	v_mul_f32_e32 v31, v108, v89
	v_med3_f32 v30, v30, s20, v56
	v_mul_f32_e32 v32, v108, v93
	v_med3_f32 v26, v26, s20, v56
	v_rndne_f32_e32 v30, v30
	v_med3_f32 v31, v31, s20, v56
	v_rndne_f32_e32 v26, v26
	v_cvt_i32_f32_e32 v30, v30
	v_rndne_f32_e32 v31, v31
	v_med3_f32 v32, v32, s20, v56
	v_cvt_i32_f32_e32 v26, v26
	v_cvt_i32_f32_sdwa v31, v31 dst_sel:WORD_1 dst_unused:UNUSED_PAD src0_sel:DWORD
	v_rndne_f32_e32 v32, v32
	v_cvt_i32_f32_sdwa v32, v32 dst_sel:BYTE_3 dst_unused:UNUSED_PAD src0_sel:DWORD
	v_lshlrev_b32_e32 v30, 8, v30
	v_perm_b32 v26, v30, v26, s21
	v_and_b32_e32 v30, 0xff0000, v31
	v_or3_b32 v26, v26, v30, v32
	ds_write2_b32 v48, v27, v26 offset0:33 offset1:41
	v_mul_f32_e32 v27, v109, v86
	v_mul_f32_e32 v26, v109, v82
	v_mul_f32_e32 v30, v109, v90
	v_med3_f32 v27, v27, s20, v56
	v_mul_f32_e32 v31, v109, v94
	v_med3_f32 v26, v26, s20, v56
	v_rndne_f32_e32 v27, v27
	v_med3_f32 v30, v30, s20, v56
	v_rndne_f32_e32 v26, v26
	v_cvt_i32_f32_e32 v27, v27
	v_rndne_f32_e32 v30, v30
	v_med3_f32 v31, v31, s20, v56
	v_cvt_i32_f32_e32 v26, v26
	v_cvt_i32_f32_sdwa v30, v30 dst_sel:WORD_1 dst_unused:UNUSED_PAD src0_sel:DWORD
	v_rndne_f32_e32 v31, v31
	v_cvt_i32_f32_sdwa v31, v31 dst_sel:BYTE_3 dst_unused:UNUSED_PAD src0_sel:DWORD
	v_lshlrev_b32_e32 v27, 8, v27
	v_perm_b32 v26, v27, v26, s21
	v_and_b32_e32 v27, 0xff0000, v30
	v_or3_b32 v26, v26, v27, v31
	v_mul_f32_e32 v27, v110, v87
	ds_write2_b32 v48, v28, v26 offset0:66 offset1:74
	v_mul_f32_e32 v26, v110, v83
	v_mul_f32_e32 v28, v110, v91
	v_med3_f32 v27, v27, s20, v56
	v_mul_f32_e32 v30, v110, v95
	v_med3_f32 v26, v26, s20, v56
	v_rndne_f32_e32 v27, v27
	v_med3_f32 v28, v28, s20, v56
	v_rndne_f32_e32 v26, v26
	v_cvt_i32_f32_e32 v27, v27
	v_rndne_f32_e32 v28, v28
	v_med3_f32 v30, v30, s20, v56
	v_cvt_i32_f32_e32 v26, v26
	v_cvt_i32_f32_sdwa v28, v28 dst_sel:WORD_1 dst_unused:UNUSED_PAD src0_sel:DWORD
	v_rndne_f32_e32 v30, v30
	v_cvt_i32_f32_sdwa v30, v30 dst_sel:BYTE_3 dst_unused:UNUSED_PAD src0_sel:DWORD
	v_lshlrev_b32_e32 v27, 8, v27
	v_perm_b32 v26, v27, v26, s21
	v_and_b32_e32 v27, 0xff0000, v28
	v_or3_b32 v26, v26, v27, v30
	v_mul_f32_e32 v22, v71, v22
	v_mul_f32_e32 v6, v71, v6
	ds_write2_b32 v48, v29, v26 offset0:99 offset1:107
	v_mul_f32_e32 v18, v71, v18
	v_mul_f32_e32 v26, v71, v96
	v_med3_f32 v22, v22, s20, v56
	v_mul_f32_e32 v2, v71, v2
	v_mul_f32_e32 v10, v71, v10
	v_med3_f32 v6, v6, s20, v56
	v_mul_f32_e32 v27, v71, v100
	v_med3_f32 v18, v18, s20, v56
	v_rndne_f32_e32 v22, v22
	v_med3_f32 v26, v26, s20, v56
	v_mul_f32_e32 v14, v71, v14
	v_med3_f32 v2, v2, s20, v56
	v_rndne_f32_e32 v6, v6
	v_med3_f32 v10, v10, s20, v56
	v_rndne_f32_e32 v18, v18
	v_cvt_i32_f32_e32 v22, v22
	v_rndne_f32_e32 v26, v26
	v_med3_f32 v27, v27, s20, v56
	v_rndne_f32_e32 v2, v2
	v_cvt_i32_f32_e32 v6, v6
	v_rndne_f32_e32 v10, v10
	v_med3_f32 v14, v14, s20, v56
	v_cvt_i32_f32_e32 v18, v18
	v_cvt_i32_f32_sdwa v26, v26 dst_sel:WORD_1 dst_unused:UNUSED_PAD src0_sel:DWORD
	v_rndne_f32_e32 v27, v27
	v_cvt_i32_f32_e32 v2, v2
	v_cvt_i32_f32_sdwa v10, v10 dst_sel:WORD_1 dst_unused:UNUSED_PAD src0_sel:DWORD
	v_rndne_f32_e32 v14, v14
	v_cvt_i32_f32_sdwa v27, v27 dst_sel:BYTE_3 dst_unused:UNUSED_PAD src0_sel:DWORD
; __device__ __forceinline__ void cvt_item_i8(const float* src, int ld, int k0, int c0, unsigned char* dst, int Kd, int drow0, const float* cmx  , unsigned char* scr, int lane) {
;     ...
; #pragma unroll
;     for (int g = 0; g < 4; ++g)
; #pragma unroll
;         for (int i = 0; i < 4; ++i) *(unsigned*)(scr + (4 * c + i) * 132 + 32 * g + 4 * q) = pack_i8x4(v[g][0][i] * inv[i], v[g][1][i] * inv[i], v[g][2][i] * inv[i], v[g][3][i] * inv[i]);
;     asm volatile("s_waitcnt lgkmcnt(0)" ::: "memory");
; #pragma unroll
;     for (int r = 0; r < 4; ++r) { const int n = 8 * r + (lane >> 3), ch = lane & 7; const unsigned char* p = scr + n * 132 + ch * 16;
;         u32x4 o; o.x = *(const unsigned*)(p); o.y = *(const unsigned*)(p + 4); o.z = *(const unsigned*)(p + 8); o.w = *(const unsigned*)(p + 12);
;         *(u32x4*)(dst + (size_t)(drow0 + n) * Kd + k0 + 16 * ch) = o; }
;     asm volatile("s_waitcnt lgkmcnt(0)" ::: "memory");
	v_cvt_i32_f32_sdwa v14, v14 dst_sel:BYTE_3 dst_unused:UNUSED_PAD src0_sel:DWORD
	v_lshlrev_b32_e32 v22, 8, v22
	v_lshlrev_b32_e32 v6, 8, v6
	v_perm_b32 v18, v22, v18, s21
	v_and_b32_e32 v22, 0xff0000, v26
	v_perm_b32 v2, v6, v2, s21
	v_and_b32_e32 v6, 0xff0000, v10
	v_or3_b32 v18, v18, v22, v27
	v_or3_b32 v2, v2, v6, v14
	v_mul_f32_e32 v22, v108, v23
	ds_write2_b32 v48, v18, v2 offset0:16 offset1:24
	v_mul_f32_e32 v2, v108, v3
	v_mul_f32_e32 v3, v108, v7
	v_mul_f32_e32 v19, v108, v19
	v_mul_f32_e32 v23, v108, v97
	v_med3_f32 v22, v22, s20, v56
	v_mul_f32_e32 v6, v108, v11
	v_med3_f32 v3, v3, s20, v56
	v_mul_f32_e32 v26, v108, v101
	v_med3_f32 v19, v19, s20, v56
	v_rndne_f32_e32 v22, v22
	v_med3_f32 v23, v23, s20, v56
	v_mul_f32_e32 v7, v108, v15
	v_med3_f32 v2, v2, s20, v56
	v_rndne_f32_e32 v3, v3
	v_med3_f32 v6, v6, s20, v56
	v_rndne_f32_e32 v19, v19
	v_cvt_i32_f32_e32 v22, v22
	v_rndne_f32_e32 v23, v23
	v_med3_f32 v26, v26, s20, v56
	v_rndne_f32_e32 v2, v2
	v_cvt_i32_f32_e32 v3, v3
	v_rndne_f32_e32 v6, v6
	v_med3_f32 v7, v7, s20, v56
	v_cvt_i32_f32_e32 v19, v19
	v_cvt_i32_f32_sdwa v23, v23 dst_sel:WORD_1 dst_unused:UNUSED_PAD src0_sel:DWORD
	v_rndne_f32_e32 v26, v26
	v_cvt_i32_f32_e32 v2, v2
	v_cvt_i32_f32_sdwa v6, v6 dst_sel:WORD_1 dst_unused:UNUSED_PAD src0_sel:DWORD
	v_rndne_f32_e32 v7, v7
	v_cvt_i32_f32_sdwa v26, v26 dst_sel:BYTE_3 dst_unused:UNUSED_PAD src0_sel:DWORD
	v_cvt_i32_f32_sdwa v7, v7 dst_sel:BYTE_3 dst_unused:UNUSED_PAD src0_sel:DWORD
	v_lshlrev_b32_e32 v22, 8, v22
	v_lshlrev_b32_e32 v3, 8, v3
	v_perm_b32 v19, v22, v19, s21
	v_and_b32_e32 v22, 0xff0000, v23
	v_perm_b32 v2, v3, v2, s21
	v_and_b32_e32 v3, 0xff0000, v6
	v_or3_b32 v19, v19, v22, v26
	v_mul_f32_e32 v22, v109, v24
	v_or3_b32 v2, v2, v3, v7
	v_mul_f32_e32 v3, v109, v8
	v_mul_f32_e32 v20, v109, v20
	v_mul_f32_e32 v23, v109, v98
	v_med3_f32 v22, v22, s20, v56
	ds_write2_b32 v48, v19, v2 offset0:49 offset1:57
	v_mul_f32_e32 v2, v109, v4
	v_mul_f32_e32 v4, v109, v12
	v_med3_f32 v3, v3, s20, v56
	v_mul_f32_e32 v24, v109, v102
	v_med3_f32 v20, v20, s20, v56
	v_rndne_f32_e32 v22, v22
	v_med3_f32 v23, v23, s20, v56
	v_mul_f32_e32 v6, v109, v16
	v_med3_f32 v2, v2, s20, v56
	v_rndne_f32_e32 v3, v3
	v_med3_f32 v4, v4, s20, v56
	v_rndne_f32_e32 v20, v20
	v_cvt_i32_f32_e32 v22, v22
	v_rndne_f32_e32 v23, v23
	v_med3_f32 v24, v24, s20, v56
	v_rndne_f32_e32 v2, v2
	v_cvt_i32_f32_e32 v3, v3
	v_rndne_f32_e32 v4, v4
	v_med3_f32 v6, v6, s20, v56
	v_cvt_i32_f32_e32 v20, v20
	v_cvt_i32_f32_sdwa v23, v23 dst_sel:WORD_1 dst_unused:UNUSED_PAD src0_sel:DWORD
	v_rndne_f32_e32 v24, v24
	v_cvt_i32_f32_e32 v2, v2
	v_cvt_i32_f32_sdwa v4, v4 dst_sel:WORD_1 dst_unused:UNUSED_PAD src0_sel:DWORD
	v_rndne_f32_e32 v6, v6
	v_cvt_i32_f32_sdwa v24, v24 dst_sel:BYTE_3 dst_unused:UNUSED_PAD src0_sel:DWORD
	v_cvt_i32_f32_sdwa v6, v6 dst_sel:BYTE_3 dst_unused:UNUSED_PAD src0_sel:DWORD
	v_lshlrev_b32_e32 v22, 8, v22
	v_lshlrev_b32_e32 v3, 8, v3
	v_perm_b32 v20, v22, v20, s21
	v_and_b32_e32 v22, 0xff0000, v23
	v_perm_b32 v2, v3, v2, s21
	v_and_b32_e32 v3, 0xff0000, v4
	v_or3_b32 v20, v20, v22, v24
	v_mul_f32_e32 v22, v110, v25
	v_or3_b32 v2, v2, v3, v6
	v_mul_f32_e32 v3, v110, v9
	v_mul_f32_e32 v21, v110, v21
	v_mul_f32_e32 v23, v110, v99
	v_med3_f32 v22, v22, s20, v56
	ds_write2_b32 v48, v20, v2 offset0:82 offset1:90
	v_mul_f32_e32 v2, v110, v5
	v_mul_f32_e32 v4, v110, v13
	v_med3_f32 v3, v3, s20, v56
	v_mul_f32_e32 v24, v110, v103
	v_med3_f32 v21, v21, s20, v56
	v_rndne_f32_e32 v22, v22
	v_med3_f32 v23, v23, s20, v56
	v_mul_f32_e32 v5, v110, v17
	v_med3_f32 v2, v2, s20, v56
	v_rndne_f32_e32 v3, v3
	v_med3_f32 v4, v4, s20, v56
	v_rndne_f32_e32 v21, v21
	v_cvt_i32_f32_e32 v22, v22
	v_rndne_f32_e32 v23, v23
	v_med3_f32 v24, v24, s20, v56
	v_rndne_f32_e32 v2, v2
	v_cvt_i32_f32_e32 v3, v3
	v_rndne_f32_e32 v4, v4
	v_med3_f32 v5, v5, s20, v56
	v_cvt_i32_f32_e32 v21, v21
	v_cvt_i32_f32_sdwa v23, v23 dst_sel:WORD_1 dst_unused:UNUSED_PAD src0_sel:DWORD
	v_rndne_f32_e32 v24, v24
	v_cvt_i32_f32_e32 v2, v2
	v_cvt_i32_f32_sdwa v4, v4 dst_sel:WORD_1 dst_unused:UNUSED_PAD src0_sel:DWORD
	v_rndne_f32_e32 v5, v5
	v_cvt_i32_f32_sdwa v24, v24 dst_sel:BYTE_3 dst_unused:UNUSED_PAD src0_sel:DWORD
	v_cvt_i32_f32_sdwa v5, v5 dst_sel:BYTE_3 dst_unused:UNUSED_PAD src0_sel:DWORD
	v_lshlrev_b32_e32 v22, 8, v22
	v_lshlrev_b32_e32 v3, 8, v3
	v_perm_b32 v21, v22, v21, s21
	v_and_b32_e32 v22, 0xff0000, v23
	v_perm_b32 v2, v3, v2, s21
	v_and_b32_e32 v3, 0xff0000, v4
	v_or3_b32 v21, v21, v22, v24
	v_or3_b32 v2, v2, v3, v5
	ds_write2_b32 v48, v21, v2 offset0:115 offset1:123
	s_waitcnt lgkmcnt(0)
	ds_read2_b32 v[2:3], v49 offset1:1
	ds_read2_b32 v[4:5], v49 offset0:2 offset1:3
	v_add_u32_e32 v12, s14, v1
	v_ashrrev_i32_e32 v13, 31, v12
	v_lshl_add_u64 v[10:11], v[38:39], 0, s[16:17]
	v_lshlrev_b64 v[6:7], 11, v[12:13]
	v_lshl_add_u64 v[14:15], v[10:11], 0, v[6:7]
	ds_read2_b32 v[6:7], v50 offset1:1
	ds_read2_b32 v[8:9], v51 offset1:1
	s_waitcnt lgkmcnt(2)
	global_store_dwordx4 v[14:15], v[2:5], off
	s_nop 1
	v_add_u32_e32 v2, 8, v12
	v_ashrrev_i32_e32 v3, 31, v2
	v_lshlrev_b64 v[2:3], 11, v[2:3]
	v_lshl_add_u64 v[2:3], v[10:11], 0, v[2:3]
	s_waitcnt lgkmcnt(0)
	global_store_dwordx4 v[2:3], v[6:9], off
	ds_read2_b32 v[2:3], v52 offset1:1
	ds_read2_b32 v[4:5], v53 offset1:1
	v_add_u32_e32 v6, 16, v12
	v_ashrrev_i32_e32 v7, 31, v6
	v_lshlrev_b64 v[6:7], 11, v[6:7]
	v_lshl_add_u64 v[14:15], v[10:11], 0, v[6:7]
	ds_read2_b32 v[6:7], v54 offset1:1
	ds_read2_b32 v[8:9], v55 offset1:1
	s_waitcnt lgkmcnt(2)
	global_store_dwordx4 v[14:15], v[2:5], off
	s_nop 1
	v_add_u32_e32 v2, 24, v12
	v_ashrrev_i32_e32 v3, 31, v2
	v_lshlrev_b64 v[2:3], 11, v[2:3]
	v_lshl_add_u64 v[2:3], v[10:11], 0, v[2:3]
	s_waitcnt lgkmcnt(0)
	global_store_dwordx4 v[2:3], v[6:9], off
	s_waitcnt lgkmcnt(0)
	s_mov_b32 s6, s24
	s_cbranch_execnz .LBB0_125

; __device__ __forceinline__ void cvt_item_i8(const float* src, int ld, int k0, int c0, unsigned char* dst, int Kd, int drow0, const float* cmx  , unsigned char* scr, int lane) {
;     const int c = lane & 7, q = lane >> 3;
;     const f32x4 cm = *(const f32x4*)(cmx + 4 * c);
;     f32x4 inv; inv[0] = cm[0] > 0.f ? 127.f / cm[0] : 0.f; inv[1] = cm[1] > 0.f ? 127.f / cm[1] : 0.f; inv[2] = cm[2] > 0.f ? 127.f / cm[2] : 0.f; inv[3] = cm[3] > 0.f ? 127.f / cm[3] : 0.f;
;     f32x4 v[4][4];
; #pragma unroll
;     for (int g = 0; g < 4; ++g)
; #pragma unroll
;         for (int j = 0; j < 4; ++j) v[g][j] = __builtin_nontemporal_load((const f32x4*)(src + (size_t)(k0 + 32 * g + 4 * q + j) * ld + c0 + 4 * c));
; #pragma unroll
;     for (int g = 0; g < 4; ++g)
; #pragma unroll
;         for (int i = 0; i < 4; ++i) *(unsigned*)(scr + (4 * c + i) * 132 + 32 * g + 4 * q) = pack_i8x4(v[g][0][i] * inv[i], v[g][1][i] * inv[i], v[g][2][i] * inv[i], v[g][3][i] * inv[i]);
; template <int GRP>
; __device__ __forceinline__ void conv_item(Frame& F, int r) {
;     ...
;     if (GRP == 0 || GRP == 1) { constexpr int KBN = (GRP == 1) ? 16 : CMS_KB, I_F = KBN * 176; const int up = r / I_F; r %= I_F; const int kb = r / 176, nb = r % 176, n0 = nb * 32, drow = (n0 >> 7) * 256 + up * 128 + (n0 & 127);
;         if (GRP == 1) cvt_item_i8(inptr(F, up ? IN_FU : IN_FG), DFF, kb * 128, n0, ws + WS_WGU, D, drow, cmx + drow, scr, F.lane);
.LBB0_128:
	s_mul_hi_i32 s7, s6, 0x2e8ba2e9
	s_lshr_b32 s8, s7, 31
	s_ashr_i32 s7, s7, 9
	s_add_i32 s7, s7, s8
	s_mul_i32 s8, s7, 0xb00
	s_sub_i32 s8, s6, s8
	s_mul_i32 s9, s8, 0xba3
	s_lshr_b32 s10, s9, 31
	s_ashr_i32 s9, s9, 19
	s_add_i32 s9, s9, s10
	s_mul_i32 s10, s9, 0xb0
	s_sub_i32 s8, s8, s10
	s_sext_i32_i16 s10, s8
	s_lshl_b32 s8, s10, 5
	s_lshl_b32 s10, s10, 6
	s_and_b32 s10, s10, 0xffffff00
	s_lshl_b32 s7, s7, 7
	s_add_i32 s10, s10, s7
	s_and_b32 s7, s8, 0x60
	s_or_b32 s12, s10, s7
	s_addk_i32 s6, 0xaff
	s_cmpk_lt_u32 s6, 0x15ff
	s_cselect_b32 s6, s22, 0x88
	s_ashr_i32 s13, s12, 31
	v_lshl_add_u64 v[2:3], s[12:13], 2, v[40:41]
	global_load_dwordx4 v[2:5], v[2:3], off
	s_sext_i32_i16 s7, s9
	s_ashr_i32 s9, s8, 31
	s_add_i32 s10, s6, 0
	s_lshl_b32 s14, s7, 7
	s_lshl_b64 s[6:7], s[8:9], 2
	s_add_i32 s8, s10, 0x20200
	v_mov_b32_e32 v7, s8
	ds_read_b64 v[14:15], v7
	v_or_b32_e32 v16, s14, v44
	v_mul_i32_i24_e32 v6, 0x5800, v16
	v_mad_i32_i24 v8, v16, s23, s23
	v_mad_i32_i24 v10, v16, s23, v57
	s_waitcnt lgkmcnt(0)
	v_readfirstlane_b32 s8, v14
	v_readfirstlane_b32 s9, v15
	s_add_u32 s6, s8, s6
	s_addc_u32 s7, s9, s7
	v_mad_i32_i24 v12, v16, s23, v58
	v_ashrrev_i32_e32 v7, 31, v6
	v_lshl_add_u64 v[14:15], s[6:7], 0, v[34:35]
	v_ashrrev_i32_e32 v9, 31, v8
	v_ashrrev_i32_e32 v11, 31, v10
	v_ashrrev_i32_e32 v13, 31, v12
	v_lshl_add_u64 v[6:7], v[14:15], 0, v[6:7]
	v_lshl_add_u64 v[8:9], v[14:15], 0, v[8:9]
	v_lshl_add_u64 v[10:11], v[14:15], 0, v[10:11]
	v_lshl_add_u64 v[12:13], v[14:15], 0, v[12:13]
	global_load_dwordx4 v[72:75], v[6:7], off nt
	global_load_dwordx4 v[76:79], v[8:9], off nt
	global_load_dwordx4 v[80:83], v[10:11], off nt
	global_load_dwordx4 v[84:87], v[12:13], off nt
	s_ashr_i32 s15, s14, 31
	s_waitcnt vmcnt(0)
	v_div_scale_f32 v6, s[6:7], v2, v2, s18
	v_div_scale_f32 v8, s[6:7], v3, v3, s18
	v_rcp_f32_e32 v17, v6
	v_rcp_f32_e32 v18, v8
	v_div_scale_f32 v10, s[8:9], v4, v4, s18
	v_rcp_f32_e32 v19, v10
	v_fma_f32 v21, -v6, v17, 1.0
	v_div_scale_f32 v7, vcc, s18, v2, s18
	v_div_scale_f32 v12, s[10:11], v5, v5, s18
	v_fma_f32 v22, -v8, v18, 1.0
	v_fmac_f32_e32 v17, v21, v17
	v_div_scale_f32 v9, s[6:7], s18, v3, s18
	v_rcp_f32_e32 v20, v12
	v_fmac_f32_e32 v18, v22, v18
	v_mul_f32_e32 v21, v7, v17
	v_fma_f32 v23, -v10, v19, 1.0
	v_mul_f32_e32 v22, v9, v18
	v_fma_f32 v25, -v6, v21, v7
	v_div_scale_f32 v11, s[8:9], s18, v4, s18
	v_fmac_f32_e32 v19, v23, v19
	v_fma_f32 v26, -v8, v22, v9
	v_fmac_f32_e32 v21, v25, v17
	v_mul_f32_e32 v23, v11, v19
	v_fmac_f32_e32 v22, v26, v18
	v_fma_f32 v6, -v6, v21, v7
	v_fma_f32 v24, -v12, v20, 1.0
	v_fma_f32 v27, -v10, v23, v11
	v_fma_f32 v7, -v8, v22, v9
	v_div_fmas_f32 v6, v6, v17, v21
	s_mov_b64 vcc, s[6:7]
	v_div_scale_f32 v13, s[10:11], s18, v5, s18
	v_fmac_f32_e32 v20, v24, v20
	v_fmac_f32_e32 v23, v27, v19
	v_div_fixup_f32 v6, v6, v2, s18
	v_div_fmas_f32 v7, v7, v18, v22
	v_cmp_lt_f32_e32 vcc, 0, v2
	v_mul_f32_e32 v24, v13, v20
	v_fma_f32 v8, -v10, v23, v11
	v_cndmask_b32_e32 v71, 0, v6, vcc
	s_mov_b64 vcc, s[8:9]
	v_fma_f32 v28, -v12, v24, v13
	v_div_fixup_f32 v2, v7, v3, s18
	v_div_fmas_f32 v6, v8, v19, v23
	v_cmp_lt_f32_e32 vcc, 0, v3
	v_fmac_f32_e32 v24, v28, v20
	s_waitcnt lgkmcnt(0)
	v_mul_f32_e32 v76, v71, v76
	v_cndmask_b32_e32 v108, 0, v2, vcc
	v_div_fixup_f32 v2, v6, v4, s18
	v_cmp_lt_f32_e32 vcc, 0, v4
	v_mad_i32_i24 v4, v16, s23, v60
	v_mul_f32_e32 v72, v72, v71
	v_cndmask_b32_e32 v109, 0, v2, vcc
	v_fma_f32 v2, -v12, v24, v13
	s_mov_b64 vcc, s[10:11]
	v_div_fmas_f32 v2, v2, v20, v24
	v_div_fixup_f32 v2, v2, v5, s18
	v_cmp_lt_f32_e32 vcc, 0, v5
	v_ashrrev_i32_e32 v5, 31, v4
	v_lshl_add_u64 v[4:5], v[14:15], 0, v[4:5]
	v_cndmask_b32_e32 v110, 0, v2, vcc
	v_mad_i32_i24 v2, v16, s23, v59
	v_ashrrev_i32_e32 v3, 31, v2
	v_lshl_add_u64 v[2:3], v[14:15], 0, v[2:3]
	global_load_dwordx4 v[88:91], v[2:3], off nt
	global_load_dwordx4 v[92:95], v[4:5], off nt
	v_mad_i32_i24 v2, v16, s23, v61
	v_ashrrev_i32_e32 v3, 31, v2
	v_mad_i32_i24 v4, v16, s23, v62
	v_lshl_add_u64 v[2:3], v[14:15], 0, v[2:3]
	v_ashrrev_i32_e32 v5, 31, v4
	v_lshl_add_u64 v[4:5], v[14:15], 0, v[4:5]
	global_load_dwordx4 v[96:99], v[2:3], off nt
	global_load_dwordx4 v[100:103], v[4:5], off nt
	v_mad_i32_i24 v2, v16, s23, v63
	v_ashrrev_i32_e32 v3, 31, v2
	v_mad_i32_i24 v4, v16, s23, v64
	v_lshl_add_u64 v[2:3], v[14:15], 0, v[2:3]
	v_ashrrev_i32_e32 v5, 31, v4
	v_lshl_add_u64 v[4:5], v[14:15], 0, v[4:5]
	global_load_dwordx4 v[18:21], v[2:3], off nt
	global_load_dwordx4 v[22:25], v[4:5], off nt
	v_mad_i32_i24 v2, v16, s23, v65
	v_ashrrev_i32_e32 v3, 31, v2
	v_mad_i32_i24 v4, v16, s23, v66
	v_lshl_add_u64 v[2:3], v[14:15], 0, v[2:3]
	v_ashrrev_i32_e32 v5, 31, v4
	v_lshl_add_u64 v[4:5], v[14:15], 0, v[4:5]
	global_load_dwordx4 v[26:29], v[2:3], off nt
	global_load_dwordx4 v[30:33], v[4:5], off nt
	v_mad_i32_i24 v2, v16, s23, v67
	v_ashrrev_i32_e32 v3, 31, v2
	v_lshl_add_u64 v[10:11], v[14:15], 0, v[2:3]
	v_mad_i32_i24 v2, v16, s23, v68
	v_ashrrev_i32_e32 v3, 31, v2
	v_lshl_add_u64 v[12:13], v[14:15], 0, v[2:3]
	global_load_dwordx4 v[2:5], v[10:11], off nt
	global_load_dwordx4 v[6:9], v[12:13], off nt
	v_mad_i32_i24 v10, v16, s23, v69
	v_ashrrev_i32_e32 v11, 31, v10
	v_lshl_add_u64 v[104:105], v[14:15], 0, v[10:11]
	v_mad_i32_i24 v10, v16, s23, v70
	v_ashrrev_i32_e32 v11, 31, v10
	v_lshl_add_u64 v[106:107], v[14:15], 0, v[10:11]
	global_load_dwordx4 v[10:13], v[104:105], off nt
	global_load_dwordx4 v[14:17], v[106:107], off nt
	v_mul_f32_e32 v80, v71, v80
	v_med3_f32 v76, v76, s20, v56
	v_mul_f32_e32 v84, v71, v84
	v_med3_f32 v72, v72, s20, v56
	v_rndne_f32_e32 v76, v76
	v_med3_f32 v80, v80, s20, v56
	v_rndne_f32_e32 v72, v72
; __device__ __forceinline__ void cvt_item_i8(const float* src, int ld, int k0, int c0, unsigned char* dst, int Kd, int drow0, const float* cmx  , unsigned char* scr, int lane) {
;     ...
; #pragma unroll
;     for (int g = 0; g < 4; ++g)
; #pragma unroll
;         for (int i = 0; i < 4; ++i) *(unsigned*)(scr + (4 * c + i) * 132 + 32 * g + 4 * q) = pack_i8x4(v[g][0][i] * inv[i], v[g][1][i] * inv[i], v[g][2][i] * inv[i], v[g][3][i] * inv[i]);
;     asm volatile("s_waitcnt lgkmcnt(0)" ::: "memory");
	v_cvt_i32_f32_e32 v76, v76
	v_rndne_f32_e32 v80, v80
	v_med3_f32 v84, v84, s20, v56
	v_cvt_i32_f32_e32 v72, v72
	v_cvt_i32_f32_sdwa v80, v80 dst_sel:WORD_1 dst_unused:UNUSED_PAD src0_sel:DWORD
	v_rndne_f32_e32 v84, v84
	v_cvt_i32_f32_sdwa v84, v84 dst_sel:BYTE_3 dst_unused:UNUSED_PAD src0_sel:DWORD
	v_lshlrev_b32_e32 v76, 8, v76
	v_perm_b32 v72, v76, v72, s21
	v_and_b32_e32 v76, 0xff0000, v80
	v_or3_b32 v72, v72, v76, v84
	v_mul_f32_e32 v76, v108, v77
	v_mul_f32_e32 v73, v73, v108
	v_mul_f32_e32 v77, v108, v81
	v_med3_f32 v76, v76, s20, v56
	v_mul_f32_e32 v80, v108, v85
	v_med3_f32 v73, v73, s20, v56
	v_rndne_f32_e32 v76, v76
	v_med3_f32 v77, v77, s20, v56
	v_rndne_f32_e32 v73, v73
	v_cvt_i32_f32_e32 v76, v76
	v_rndne_f32_e32 v77, v77
	v_med3_f32 v80, v80, s20, v56
	v_cvt_i32_f32_e32 v73, v73
	v_cvt_i32_f32_sdwa v77, v77 dst_sel:WORD_1 dst_unused:UNUSED_PAD src0_sel:DWORD
	v_rndne_f32_e32 v80, v80
	v_cvt_i32_f32_sdwa v80, v80 dst_sel:BYTE_3 dst_unused:UNUSED_PAD src0_sel:DWORD
	v_lshlrev_b32_e32 v76, 8, v76
	v_perm_b32 v73, v76, v73, s21
	v_and_b32_e32 v76, 0xff0000, v77
	v_or3_b32 v73, v73, v76, v80
	v_mul_f32_e32 v76, v109, v78
	v_mul_f32_e32 v74, v74, v109
	v_mul_f32_e32 v77, v109, v82
	v_med3_f32 v76, v76, s20, v56
	v_mul_f32_e32 v78, v109, v86
	v_med3_f32 v74, v74, s20, v56
	v_rndne_f32_e32 v76, v76
	v_med3_f32 v77, v77, s20, v56
	v_rndne_f32_e32 v74, v74
	v_cvt_i32_f32_e32 v76, v76
	v_rndne_f32_e32 v77, v77
	v_med3_f32 v78, v78, s20, v56
	v_cvt_i32_f32_e32 v74, v74
	v_cvt_i32_f32_sdwa v77, v77 dst_sel:WORD_1 dst_unused:UNUSED_PAD src0_sel:DWORD
	v_rndne_f32_e32 v78, v78
	v_cvt_i32_f32_sdwa v78, v78 dst_sel:BYTE_3 dst_unused:UNUSED_PAD src0_sel:DWORD
	v_lshlrev_b32_e32 v76, 8, v76
	v_perm_b32 v74, v76, v74, s21
	v_and_b32_e32 v76, 0xff0000, v77
	v_or3_b32 v74, v74, v76, v78
	v_mul_f32_e32 v76, v110, v79
	v_mul_f32_e32 v75, v75, v110
	v_mul_f32_e32 v77, v110, v83
	v_med3_f32 v76, v76, s20, v56
	v_mul_f32_e32 v78, v110, v87
	v_med3_f32 v75, v75, s20, v56
	v_rndne_f32_e32 v76, v76
	v_med3_f32 v77, v77, s20, v56
	v_rndne_f32_e32 v75, v75
	v_cvt_i32_f32_e32 v76, v76
	v_rndne_f32_e32 v77, v77
	v_med3_f32 v78, v78, s20, v56
	v_cvt_i32_f32_e32 v75, v75
	v_cvt_i32_f32_sdwa v77, v77 dst_sel:WORD_1 dst_unused:UNUSED_PAD src0_sel:DWORD
	v_rndne_f32_e32 v78, v78
	v_cvt_i32_f32_sdwa v78, v78 dst_sel:BYTE_3 dst_unused:UNUSED_PAD src0_sel:DWORD
	v_lshlrev_b32_e32 v76, 8, v76
	v_perm_b32 v75, v76, v75, s21
	v_and_b32_e32 v76, 0xff0000, v77
	s_waitcnt vmcnt(0) lgkmcnt(0)
	v_mul_f32_e32 v77, v71, v92
	v_or3_b32 v75, v75, v76, v78
	v_mul_f32_e32 v76, v71, v88
	v_mul_f32_e32 v78, v71, v96
	v_med3_f32 v77, v77, s20, v56
	v_mul_f32_e32 v22, v71, v22
	v_mul_f32_e32 v6, v71, v6
	v_mul_f32_e32 v79, v71, v100
	v_med3_f32 v76, v76, s20, v56
	v_rndne_f32_e32 v77, v77
	v_med3_f32 v78, v78, s20, v56
	v_mul_f32_e32 v18, v71, v18
	v_mul_f32_e32 v26, v71, v26
	v_med3_f32 v22, v22, s20, v56
	v_mul_f32_e32 v2, v71, v2
	v_mul_f32_e32 v10, v71, v10
	v_med3_f32 v6, v6, s20, v56
	v_rndne_f32_e32 v76, v76
	v_cvt_i32_f32_e32 v77, v77
	v_rndne_f32_e32 v78, v78
	v_med3_f32 v79, v79, s20, v56
	v_mul_f32_e32 v30, v71, v30
	v_med3_f32 v18, v18, s20, v56
	v_rndne_f32_e32 v22, v22
	v_med3_f32 v26, v26, s20, v56
	v_mul_f32_e32 v14, v71, v14
	v_med3_f32 v2, v2, s20, v56
	v_rndne_f32_e32 v6, v6
	v_med3_f32 v10, v10, s20, v56
	v_cvt_i32_f32_e32 v76, v76
	v_cvt_i32_f32_sdwa v78, v78 dst_sel:WORD_1 dst_unused:UNUSED_PAD src0_sel:DWORD
	v_rndne_f32_e32 v79, v79
	v_rndne_f32_e32 v18, v18
	v_cvt_i32_f32_e32 v22, v22
	v_rndne_f32_e32 v26, v26
	v_med3_f32 v30, v30, s20, v56
	v_rndne_f32_e32 v2, v2
	v_cvt_i32_f32_e32 v6, v6
	v_rndne_f32_e32 v10, v10
	v_med3_f32 v14, v14, s20, v56
	v_cvt_i32_f32_sdwa v79, v79 dst_sel:BYTE_3 dst_unused:UNUSED_PAD src0_sel:DWORD
	v_cvt_i32_f32_e32 v18, v18
	v_cvt_i32_f32_sdwa v26, v26 dst_sel:WORD_1 dst_unused:UNUSED_PAD src0_sel:DWORD
	v_rndne_f32_e32 v30, v30
	v_cvt_i32_f32_e32 v2, v2
	v_cvt_i32_f32_sdwa v10, v10 dst_sel:WORD_1 dst_unused:UNUSED_PAD src0_sel:DWORD
	v_rndne_f32_e32 v14, v14
	v_cvt_i32_f32_sdwa v30, v30 dst_sel:BYTE_3 dst_unused:UNUSED_PAD src0_sel:DWORD
	v_cvt_i32_f32_sdwa v14, v14 dst_sel:BYTE_3 dst_unused:UNUSED_PAD src0_sel:DWORD
	v_lshlrev_b32_e32 v77, 8, v77
	v_perm_b32 v76, v77, v76, s21
	v_and_b32_e32 v77, 0xff0000, v78
	v_lshlrev_b32_e32 v22, 8, v22
	v_lshlrev_b32_e32 v6, 8, v6
	v_or3_b32 v76, v76, v77, v79
	v_perm_b32 v18, v22, v18, s21
	v_and_b32_e32 v22, 0xff0000, v26
	v_perm_b32 v2, v6, v2, s21
	v_and_b32_e32 v6, 0xff0000, v10
	ds_write2_b32 v48, v72, v76 offset1:8
	v_mul_f32_e32 v76, v108, v93
	v_or3_b32 v18, v18, v22, v30
	v_or3_b32 v2, v2, v6, v14
	v_mul_f32_e32 v72, v108, v89
	v_mul_f32_e32 v77, v108, v97
	v_med3_f32 v76, v76, s20, v56
	v_mul_f32_e32 v22, v108, v23
	ds_write2_b32 v48, v18, v2 offset0:16 offset1:24
	v_mul_f32_e32 v2, v108, v3
	v_mul_f32_e32 v3, v108, v7
	v_mul_f32_e32 v78, v108, v101
	v_med3_f32 v72, v72, s20, v56
	v_rndne_f32_e32 v76, v76
	v_med3_f32 v77, v77, s20, v56
	v_mul_f32_e32 v19, v108, v19
	v_mul_f32_e32 v23, v108, v27
	v_med3_f32 v22, v22, s20, v56
	v_mul_f32_e32 v6, v108, v11
	v_med3_f32 v3, v3, s20, v56
	v_rndne_f32_e32 v72, v72
	v_cvt_i32_f32_e32 v76, v76
	v_rndne_f32_e32 v77, v77
	v_med3_f32 v78, v78, s20, v56
	v_mul_f32_e32 v26, v108, v31
	v_med3_f32 v19, v19, s20, v56
	v_rndne_f32_e32 v22, v22
	v_med3_f32 v23, v23, s20, v56
	v_mul_f32_e32 v7, v108, v15
	v_med3_f32 v2, v2, s20, v56
	v_rndne_f32_e32 v3, v3
	v_med3_f32 v6, v6, s20, v56
	v_cvt_i32_f32_e32 v72, v72
	v_cvt_i32_f32_sdwa v77, v77 dst_sel:WORD_1 dst_unused:UNUSED_PAD src0_sel:DWORD
	v_rndne_f32_e32 v78, v78
	v_rndne_f32_e32 v19, v19
; __device__ __forceinline__ void cvt_item_i8(const float* src, int ld, int k0, int c0, unsigned char* dst, int Kd, int drow0, const float* cmx  , unsigned char* scr, int lane) {
;     ...
; #pragma unroll
;     for (int g = 0; g < 4; ++g)
; #pragma unroll
;         for (int i = 0; i < 4; ++i) *(unsigned*)(scr + (4 * c + i) * 132 + 32 * g + 4 * q) = pack_i8x4(v[g][0][i] * inv[i], v[g][1][i] * inv[i], v[g][2][i] * inv[i], v[g][3][i] * inv[i]);
;     asm volatile("s_waitcnt lgkmcnt(0)" ::: "memory");
; #pragma unroll
;     for (int r = 0; r < 4; ++r) { const int n = 8 * r + (lane >> 3), ch = lane & 7; const unsigned char* p = scr + n * 132 + ch * 16;
;         u32x4 o; o.x = *(const unsigned*)(p); o.y = *(const unsigned*)(p + 4); o.z = *(const unsigned*)(p + 8); o.w = *(const unsigned*)(p + 12);
;         *(u32x4*)(dst + (size_t)(drow0 + n) * Kd + k0 + 16 * ch) = o; }
;     asm volatile("s_waitcnt lgkmcnt(0)" ::: "memory");
	v_cvt_i32_f32_e32 v22, v22
	v_rndne_f32_e32 v23, v23
	v_med3_f32 v26, v26, s20, v56
	v_rndne_f32_e32 v2, v2
	v_cvt_i32_f32_e32 v3, v3
	v_rndne_f32_e32 v6, v6
	v_med3_f32 v7, v7, s20, v56
	v_cvt_i32_f32_sdwa v78, v78 dst_sel:BYTE_3 dst_unused:UNUSED_PAD src0_sel:DWORD
	v_cvt_i32_f32_e32 v19, v19
	v_cvt_i32_f32_sdwa v23, v23 dst_sel:WORD_1 dst_unused:UNUSED_PAD src0_sel:DWORD
	v_rndne_f32_e32 v26, v26
	v_cvt_i32_f32_e32 v2, v2
	v_cvt_i32_f32_sdwa v6, v6 dst_sel:WORD_1 dst_unused:UNUSED_PAD src0_sel:DWORD
	v_rndne_f32_e32 v7, v7
	v_cvt_i32_f32_sdwa v26, v26 dst_sel:BYTE_3 dst_unused:UNUSED_PAD src0_sel:DWORD
	v_cvt_i32_f32_sdwa v7, v7 dst_sel:BYTE_3 dst_unused:UNUSED_PAD src0_sel:DWORD
	v_lshlrev_b32_e32 v76, 8, v76
	v_perm_b32 v72, v76, v72, s21
	v_and_b32_e32 v76, 0xff0000, v77
	v_lshlrev_b32_e32 v22, 8, v22
	v_lshlrev_b32_e32 v3, 8, v3
	v_or3_b32 v72, v72, v76, v78
	v_perm_b32 v19, v22, v19, s21
	v_and_b32_e32 v22, 0xff0000, v23
	v_perm_b32 v2, v3, v2, s21
	v_and_b32_e32 v3, 0xff0000, v6
	ds_write2_b32 v48, v73, v72 offset0:33 offset1:41
	v_mul_f32_e32 v73, v109, v94
	v_or3_b32 v19, v19, v22, v26
	v_mul_f32_e32 v22, v109, v24
	v_or3_b32 v2, v2, v3, v7
	v_mul_f32_e32 v3, v109, v8
	v_mul_f32_e32 v72, v109, v90
	v_mul_f32_e32 v76, v109, v98
	v_med3_f32 v73, v73, s20, v56
	v_mul_f32_e32 v20, v109, v20
	v_mul_f32_e32 v23, v109, v28
	v_med3_f32 v22, v22, s20, v56
	ds_write2_b32 v48, v19, v2 offset0:49 offset1:57
	v_mul_f32_e32 v2, v109, v4
	v_mul_f32_e32 v4, v109, v12
	v_med3_f32 v3, v3, s20, v56
	v_mul_f32_e32 v77, v109, v102
	v_med3_f32 v72, v72, s20, v56
	v_rndne_f32_e32 v73, v73
	v_med3_f32 v76, v76, s20, v56
	v_mul_f32_e32 v24, v109, v32
	v_med3_f32 v20, v20, s20, v56
	v_rndne_f32_e32 v22, v22
	v_med3_f32 v23, v23, s20, v56
	v_mul_f32_e32 v6, v109, v16
	v_med3_f32 v2, v2, s20, v56
	v_rndne_f32_e32 v3, v3
	v_med3_f32 v4, v4, s20, v56
	v_rndne_f32_e32 v72, v72
	v_cvt_i32_f32_e32 v73, v73
	v_rndne_f32_e32 v76, v76
	v_med3_f32 v77, v77, s20, v56
	v_rndne_f32_e32 v20, v20
	v_cvt_i32_f32_e32 v22, v22
	v_rndne_f32_e32 v23, v23
	v_med3_f32 v24, v24, s20, v56
	v_rndne_f32_e32 v2, v2
	v_cvt_i32_f32_e32 v3, v3
	v_rndne_f32_e32 v4, v4
	v_med3_f32 v6, v6, s20, v56
	v_cvt_i32_f32_e32 v72, v72
	v_cvt_i32_f32_sdwa v76, v76 dst_sel:WORD_1 dst_unused:UNUSED_PAD src0_sel:DWORD
	v_rndne_f32_e32 v77, v77
	v_cvt_i32_f32_e32 v20, v20
	v_cvt_i32_f32_sdwa v23, v23 dst_sel:WORD_1 dst_unused:UNUSED_PAD src0_sel:DWORD
	v_rndne_f32_e32 v24, v24
	v_cvt_i32_f32_e32 v2, v2
	v_cvt_i32_f32_sdwa v4, v4 dst_sel:WORD_1 dst_unused:UNUSED_PAD src0_sel:DWORD
	v_rndne_f32_e32 v6, v6
	v_cvt_i32_f32_sdwa v77, v77 dst_sel:BYTE_3 dst_unused:UNUSED_PAD src0_sel:DWORD
	v_cvt_i32_f32_sdwa v24, v24 dst_sel:BYTE_3 dst_unused:UNUSED_PAD src0_sel:DWORD
	v_cvt_i32_f32_sdwa v6, v6 dst_sel:BYTE_3 dst_unused:UNUSED_PAD src0_sel:DWORD
	v_lshlrev_b32_e32 v73, 8, v73
	v_lshlrev_b32_e32 v22, 8, v22
	v_lshlrev_b32_e32 v3, 8, v3
	v_perm_b32 v72, v73, v72, s21
	v_and_b32_e32 v73, 0xff0000, v76
	v_perm_b32 v20, v22, v20, s21
	v_and_b32_e32 v22, 0xff0000, v23
	v_perm_b32 v2, v3, v2, s21
	v_and_b32_e32 v3, 0xff0000, v4
	v_or3_b32 v72, v72, v73, v77
	v_mul_f32_e32 v73, v110, v95
	v_or3_b32 v20, v20, v22, v24
	v_mul_f32_e32 v22, v110, v25
	v_or3_b32 v2, v2, v3, v6
	v_mul_f32_e32 v3, v110, v9
	ds_write2_b32 v48, v74, v72 offset0:66 offset1:74
	v_mul_f32_e32 v72, v110, v91
	v_mul_f32_e32 v74, v110, v99
	v_med3_f32 v73, v73, s20, v56
	v_mul_f32_e32 v21, v110, v21
	v_mul_f32_e32 v23, v110, v29
	v_med3_f32 v22, v22, s20, v56
	ds_write2_b32 v48, v20, v2 offset0:82 offset1:90
	v_mul_f32_e32 v2, v110, v5
	v_mul_f32_e32 v4, v110, v13
	v_med3_f32 v3, v3, s20, v56
	v_mul_f32_e32 v76, v110, v103
	v_med3_f32 v72, v72, s20, v56
	v_rndne_f32_e32 v73, v73
	v_med3_f32 v74, v74, s20, v56
	v_mul_f32_e32 v24, v110, v33
	v_med3_f32 v21, v21, s20, v56
	v_rndne_f32_e32 v22, v22
	v_med3_f32 v23, v23, s20, v56
	v_mul_f32_e32 v5, v110, v17
	v_med3_f32 v2, v2, s20, v56
	v_rndne_f32_e32 v3, v3
	v_med3_f32 v4, v4, s20, v56
	v_rndne_f32_e32 v72, v72
	v_cvt_i32_f32_e32 v73, v73
	v_rndne_f32_e32 v74, v74
	v_med3_f32 v76, v76, s20, v56
	v_rndne_f32_e32 v21, v21
	v_cvt_i32_f32_e32 v22, v22
	v_rndne_f32_e32 v23, v23
	v_med3_f32 v24, v24, s20, v56
	v_rndne_f32_e32 v2, v2
	v_cvt_i32_f32_e32 v3, v3
	v_rndne_f32_e32 v4, v4
	v_med3_f32 v5, v5, s20, v56
	v_cvt_i32_f32_e32 v72, v72
	v_cvt_i32_f32_sdwa v74, v74 dst_sel:WORD_1 dst_unused:UNUSED_PAD src0_sel:DWORD
	v_rndne_f32_e32 v76, v76
	v_cvt_i32_f32_e32 v21, v21
	v_cvt_i32_f32_sdwa v23, v23 dst_sel:WORD_1 dst_unused:UNUSED_PAD src0_sel:DWORD
	v_rndne_f32_e32 v24, v24
	v_cvt_i32_f32_e32 v2, v2
	v_cvt_i32_f32_sdwa v4, v4 dst_sel:WORD_1 dst_unused:UNUSED_PAD src0_sel:DWORD
	v_rndne_f32_e32 v5, v5
	v_cvt_i32_f32_sdwa v76, v76 dst_sel:BYTE_3 dst_unused:UNUSED_PAD src0_sel:DWORD
	v_cvt_i32_f32_sdwa v24, v24 dst_sel:BYTE_3 dst_unused:UNUSED_PAD src0_sel:DWORD
	v_cvt_i32_f32_sdwa v5, v5 dst_sel:BYTE_3 dst_unused:UNUSED_PAD src0_sel:DWORD
	v_lshlrev_b32_e32 v73, 8, v73
	v_lshlrev_b32_e32 v22, 8, v22
	v_lshlrev_b32_e32 v3, 8, v3
	v_perm_b32 v72, v73, v72, s21
	v_and_b32_e32 v73, 0xff0000, v74
	v_perm_b32 v21, v22, v21, s21
	v_and_b32_e32 v22, 0xff0000, v23
	v_perm_b32 v2, v3, v2, s21
	v_and_b32_e32 v3, 0xff0000, v4
	v_or3_b32 v72, v72, v73, v76
	v_or3_b32 v21, v21, v22, v24
	v_or3_b32 v2, v2, v3, v5
	ds_write2_b32 v48, v75, v72 offset0:99 offset1:107
	ds_write2_b32 v48, v21, v2 offset0:115 offset1:123
	s_waitcnt lgkmcnt(0)
	ds_read2_b32 v[2:3], v49 offset1:1
	ds_read2_b32 v[4:5], v49 offset0:2 offset1:3
	v_or_b32_e32 v6, s12, v1
	v_ashrrev_i32_e32 v7, 31, v6
	v_lshl_add_u64 v[10:11], v[42:43], 0, s[14:15]
	v_lshlrev_b64 v[6:7], 11, v[6:7]
	v_lshl_add_u64 v[12:13], v[10:11], 0, v[6:7]
	ds_read2_b32 v[6:7], v50 offset1:1
	ds_read2_b32 v[8:9], v51 offset1:1
	s_waitcnt lgkmcnt(2)
	global_store_dwordx4 v[12:13], v[2:5], off
	s_nop 1
	v_or_b32_e32 v2, s12, v45
	v_ashrrev_i32_e32 v3, 31, v2
	v_lshlrev_b64 v[2:3], 11, v[2:3]
	v_lshl_add_u64 v[2:3], v[10:11], 0, v[2:3]
	s_waitcnt lgkmcnt(0)
	global_store_dwordx4 v[2:3], v[6:9], off
	ds_read2_b32 v[2:3], v52 offset1:1
	ds_read2_b32 v[4:5], v53 offset1:1
	v_or_b32_e32 v6, s12, v46
	v_ashrrev_i32_e32 v7, 31, v6
	v_lshlrev_b64 v[6:7], 11, v[6:7]
	v_lshl_add_u64 v[12:13], v[10:11], 0, v[6:7]
	ds_read2_b32 v[6:7], v54 offset1:1
	ds_read2_b32 v[8:9], v55 offset1:1
	s_waitcnt lgkmcnt(2)
	global_store_dwordx4 v[12:13], v[2:5], off
	s_nop 1
	v_or_b32_e32 v2, s12, v47
	v_ashrrev_i32_e32 v3, 31, v2
	v_lshlrev_b64 v[2:3], 11, v[2:3]
	v_lshl_add_u64 v[2:3], v[10:11], 0, v[2:3]
	s_waitcnt lgkmcnt(0)
	global_store_dwordx4 v[2:3], v[6:9], off
	s_waitcnt lgkmcnt(0)
	s_branch .LBB0_122

; __device__ __forceinline__ void colmax_item(const float* src, int ld, int k0, int c0, float* cmx  , int lane) {
;     const int c = lane & 7, q = lane >> 3;
;     f32x4 mx = (f32x4){0.f, 0.f, 0.f, 0.f};
; #pragma unroll
;     for (int g = 0; g < 4; ++g)
; #pragma unroll
;         for (int j = 0; j < 4; ++j) { const f32x4 v = *(const f32x4*)(src + (size_t)(k0 + 32 * g + 4 * q + j) * ld + c0 + 4 * c);
;             mx[0] = fmaxf(mx[0], fabsf(v[0])); mx[1] = fmaxf(mx[1], fabsf(v[1])); mx[2] = fmaxf(mx[2], fabsf(v[2])); mx[3] = fmaxf(mx[3], fabsf(v[3])); }
; #pragma unroll
;     for (int i = 0; i < 4; ++i) { float v = mx[i]; v = fmaxf(v, __shfl_xor(v, 8)); v = fmaxf(v, __shfl_xor(v, 16)); v = fmaxf(v, __shfl_xor(v, 32)); mx[i] = v; }
;     if (q == 0) {
; #pragma unroll
;         for (int i = 0; i < 4; ++i) atomicMax((unsigned*)(cmx + 4 * c + i), __float_as_uint(mx[i] * CMS_F)); }
; }
; template <int GRP>
; __device__ __forceinline__ void conv_item(Frame& F, int r) {
;     ...
;         if (r < NI) { const int kb = r / 152, nb = r % 152, c0 = (nb < 112) ? nb * 32 : SRC_GATE + 8 + (nb - 112) * 32, drow = nb * 32;
;             if (QUANT) cvt_item_i8(inptr(F, IN_WIN) + (size_t)l * D * NIN_SRC, NIN_SRC, kb * 128, c0, ws + WS_WIN + (size_t)l * NIN * D, D, drow, cmx + CMX_WIN + l * NIN + drow, scr, F.lane);
;             else colmax_item(inptr(F, IN_WIN) + (size_t)l * D * NIN_SRC, NIN_SRC, kb * 128, c0, cmx + CMX_WIN + l * NIN + drow, F.lane);
.LBB0_214:
	s_add_i32 s42, s4, 0xfffff130
	s_cmpk_gt_i32 s42, 0xf12f
	s_cselect_b64 s[16:17], -1, 0
	s_and_b64 vcc, exec, s[16:17]
	s_mov_b32 s18, s4
	s_cbranch_vccnz .LBB0_218
	s_add_i32 s0, s4, 0x130
	s_mul_hi_i32 s18, s0, 0x6bca1af3
	s_lshr_b32 s19, s18, 31
	s_ashr_i32 s18, s18, 6
	s_add_i32 s19, s18, s19
	s_mul_i32 s18, s19, 0x98
	s_sub_i32 s0, s0, s18
	v_mov_b32_e32 v12, s5
	s_waitcnt lgkmcnt(3)
	ds_read_b64 v[12:13], v12
	s_lshl_b32 s18, s0, 5
	s_or_b32 s20, s18, 8
	s_cmpk_lt_i32 s0, 0x70
	s_cselect_b32 s20, s18, s20
	s_ashr_i32 s21, s20, 31
	s_waitcnt lgkmcnt(0)
	v_readfirstlane_b32 s0, v12
	s_lshl_b64 s[20:21], s[20:21], 2
	v_readfirstlane_b32 s43, v13
	s_add_u32 s20, s0, s20
	s_addc_u32 s21, s43, s21
	v_lshl_or_b32 v29, s19, 7, v1
	v_lshl_add_u64 v[12:13], s[20:21], 0, v[2:3]
	v_lshl_add_u64 v[82:83], v[12:13], 0, s[12:13]
	v_or_b32_e32 v14, 1, v29
	v_mad_i64_i32 v[12:13], s[20:21], v29, s22, v[82:83]
	v_mad_i64_i32 v[30:31], s[20:21], v14, s22, v[82:83]
	v_or_b32_e32 v34, 2, v29
	v_or_b32_e32 v36, 3, v29
	global_load_dwordx4 v[12:15], v[12:13], off
	s_nop 0
	global_load_dwordx4 v[30:33], v[30:31], off
	v_mad_i64_i32 v[34:35], s[20:21], v34, s22, v[82:83]
	v_mad_i64_i32 v[38:39], s[20:21], v36, s22, v[82:83]
	v_or_b32_e32 v42, 32, v29
	v_or_b32_e32 v44, 33, v29
	global_load_dwordx4 v[34:37], v[34:35], off
	s_nop 0
	global_load_dwordx4 v[38:41], v[38:39], off
	v_mad_i64_i32 v[42:43], s[20:21], v42, s22, v[82:83]
	v_mad_i64_i32 v[46:47], s[20:21], v44, s22, v[82:83]
	v_or_b32_e32 v50, 34, v29
	v_or_b32_e32 v52, 35, v29
	global_load_dwordx4 v[42:45], v[42:43], off
	s_nop 0
	global_load_dwordx4 v[46:49], v[46:47], off
	v_mad_i64_i32 v[50:51], s[20:21], v50, s22, v[82:83]
	v_mad_i64_i32 v[54:55], s[20:21], v52, s22, v[82:83]
	v_or_b32_e32 v58, 64, v29
	v_or_b32_e32 v60, 0x41, v29
	global_load_dwordx4 v[50:53], v[50:51], off
	s_nop 0
	global_load_dwordx4 v[54:57], v[54:55], off
	v_mad_i64_i32 v[58:59], s[20:21], v58, s22, v[82:83]
	v_mad_i64_i32 v[62:63], s[20:21], v60, s22, v[82:83]
	v_or_b32_e32 v66, 0x42, v29
	v_or_b32_e32 v68, 0x43, v29
	global_load_dwordx4 v[58:61], v[58:59], off
	s_nop 0
	global_load_dwordx4 v[62:65], v[62:63], off
	v_mad_i64_i32 v[66:67], s[20:21], v66, s22, v[82:83]
	v_mad_i64_i32 v[70:71], s[20:21], v68, s22, v[82:83]
	v_or_b32_e32 v74, 0x60, v29
	v_or_b32_e32 v76, 0x61, v29
	global_load_dwordx4 v[66:69], v[66:67], off
	s_nop 0
	global_load_dwordx4 v[70:73], v[70:71], off
	v_mad_i64_i32 v[74:75], s[20:21], v74, s22, v[82:83]
	v_mad_i64_i32 v[78:79], s[20:21], v76, s22, v[82:83]
	v_or_b32_e32 v84, 0x62, v29
	v_or_b32_e32 v29, 0x63, v29
	global_load_dwordx4 v[74:77], v[74:75], off
	s_nop 0
	global_load_dwordx4 v[78:81], v[78:79], off
	v_mad_i64_i32 v[84:85], s[20:21], v84, s22, v[82:83]
	v_mad_i64_i32 v[86:87], s[20:21], v29, s22, v[82:83]
	global_load_dwordx4 v[82:85], v[84:85], off
	s_nop 0
	global_load_dwordx4 v[86:89], v[86:87], off
	v_cmp_lt_i32_e32 vcc, v21, v22
	s_waitcnt vmcnt(0) lgkmcnt(0)
	v_max3_f32 v14, |v14|, 0, |v32|
	v_max3_f32 v12, |v12|, 0, |v30|
	v_max3_f32 v13, |v13|, 0, |v31|
	v_max3_f32 v15, |v15|, 0, |v33|
	v_max3_f32 v14, v14, |v36|, |v40|
	v_max3_f32 v12, v12, |v34|, |v38|
	v_max3_f32 v13, v13, |v35|, |v39|
	v_max3_f32 v15, v15, |v37|, |v41|
	v_max3_f32 v14, v14, |v44|, |v48|
	v_max3_f32 v12, v12, |v42|, |v46|
	v_max3_f32 v13, v13, |v43|, |v47|
	v_max3_f32 v15, v15, |v45|, |v49|
	v_max3_f32 v14, v14, |v52|, |v56|
	v_max3_f32 v12, v12, |v50|, |v54|
	v_max3_f32 v13, v13, |v51|, |v55|
	v_max3_f32 v15, v15, |v53|, |v57|
	v_max3_f32 v14, v14, |v60|, |v64|
	v_max3_f32 v12, v12, |v58|, |v62|
	v_max3_f32 v13, v13, |v59|, |v63|
	v_max3_f32 v15, v15, |v61|, |v65|
	v_max3_f32 v14, v14, |v68|, |v72|
	v_max3_f32 v12, v12, |v66|, |v70|
	v_max3_f32 v13, v13, |v67|, |v71|
	v_max3_f32 v15, v15, |v69|, |v73|
	v_max3_f32 v14, v14, |v76|, |v80|
	v_max3_f32 v12, v12, |v74|, |v78|
	v_max3_f32 v13, v13, |v75|, |v79|
	v_max3_f32 v15, v15, |v77|, |v81|
	v_max3_f32 v29, v14, |v84|, |v88|
	v_cndmask_b32_e32 v14, v20, v21, vcc
	v_max3_f32 v12, v12, |v82|, |v86|
	v_lshlrev_b32_e32 v14, 2, v14
	ds_bpermute_b32 v31, v14, v12
	v_max3_f32 v13, v13, |v83|, |v87|
	v_cmp_lt_i32_e32 vcc, v23, v22
	ds_bpermute_b32 v33, v14, v13
	v_max3_f32 v15, v15, |v85|, |v89|
	v_cndmask_b32_e32 v30, v20, v23, vcc
	s_waitcnt lgkmcnt(1)
	v_max_f32_e32 v31, v31, v31
	v_lshlrev_b32_e32 v30, 2, v30
	v_max_f32_e32 v12, v12, v31
	ds_bpermute_b32 v31, v30, v12
	s_waitcnt lgkmcnt(1)
	v_max_f32_e32 v33, v33, v33
	v_max_f32_e32 v33, v13, v33
	ds_bpermute_b32 v34, v30, v33
	ds_bpermute_b32 v35, v14, v15
	s_waitcnt lgkmcnt(2)
	v_max_f32_e32 v13, v31, v31
	ds_bpermute_b32 v31, v14, v29
	v_cmp_lt_i32_e32 vcc, v24, v22
	s_waitcnt lgkmcnt(2)
	v_max_f32_e32 v34, v34, v34
	v_max_f32_e32 v14, v33, v34
	s_waitcnt lgkmcnt(1)
	v_max_f32_e32 v33, v35, v35
	s_waitcnt lgkmcnt(0)
	v_max_f32_e32 v31, v31, v31
	v_max_f32_e32 v29, v29, v31
	v_max_f32_e32 v33, v15, v33
	ds_bpermute_b32 v31, v30, v29
	ds_bpermute_b32 v34, v30, v33
	v_cndmask_b32_e32 v32, v20, v24, vcc
	v_lshlrev_b32_e32 v32, 2, v32
	v_max_f32_e32 v12, v12, v13
	s_waitcnt lgkmcnt(1)
	v_max_f32_e32 v30, v31, v31
	s_waitcnt lgkmcnt(0)
	v_max_f32_e32 v31, v34, v34
	v_max_f32_e32 v29, v29, v30
	v_max_f32_e32 v31, v33, v31
	ds_bpermute_b32 v13, v32, v12
	ds_bpermute_b32 v15, v32, v14
	ds_bpermute_b32 v30, v32, v29
	ds_bpermute_b32 v32, v32, v31
	s_and_saveexec_b64 s[20:21], s[6:7]
	s_cbranch_execz .LBB0_217
	s_waitcnt lgkmcnt(2)
	v_max_f32_e32 v15, v15, v15
	v_max_f32_e32 v14, v14, v14
	v_max_f32_e32 v13, v13, v13
	v_max_f32_e32 v12, v12, v12
	s_ashr_i32 s19, s18, 31
	v_max_f32_e32 v14, v14, v15
	v_max_f32_e32 v15, v12, v13
	s_waitcnt lgkmcnt(1)
	v_max_f32_e32 v30, v30, v30
	v_max_f32_e32 v29, v29, v29
	v_lshl_add_u64 v[12:13], s[18:19], 2, v[4:5]
	v_mul_f32_e32 v15, 0x3fb33333, v15
	s_waitcnt lgkmcnt(0)
	v_max_f32_e32 v32, v32, v32
	v_max_f32_e32 v31, v31, v31
	v_max_f32_e32 v29, v29, v30
	global_atomic_umax v[12:13], v15, off
	v_mul_f32_e32 v14, 0x3fb33333, v14
	v_max_f32_e32 v31, v31, v32
	global_atomic_umax v[12:13], v14, off offset:4
	v_mul_f32_e32 v14, 0x3fb33333, v29
	global_atomic_umax v[12:13], v14, off offset:8
	v_mul_f32_e32 v14, 0x3fb33333, v31
	global_atomic_umax v[12:13], v14, off offset:12

; __device__ __forceinline__ void cvt_item8(const float* src, int ld, int k0, int c0, unsigned char* dst, int Kd, int drow0, unsigned char* scr, int lane) {
;     const int c = lane & 7, q = lane >> 3;
;     f32x4 v[4][4];
; #pragma unroll
;     for (int g = 0; g < 4; ++g)
; #pragma unroll
;         for (int j = 0; j < 4; ++j) v[g][j] = __builtin_nontemporal_load((const f32x4*)(src + (size_t)(k0 + 32 * g + 4 * q + j) * ld + c0 + 4 * c));
; #pragma unroll
;     for (int g = 0; g < 4; ++g)
; #pragma unroll
;         for (int i = 0; i < 4; ++i) *(unsigned*)(scr + (4 * c + i) * 132 + 32 * g + 4 * q) = pg8::pack_fp8x4(v[g][0][i] * WSC, v[g][1][i] * WSC, v[g][2][i] * WSC, v[g][3][i] * WSC);
;     asm volatile("s_waitcnt lgkmcnt(0)" ::: "memory");
; template <int GRP>
; __device__ __forceinline__ void conv_item(Frame& F, int r) {
;     ...
;             if (r < CI_MD) { const int e = r / (22 * 64); r %= (22 * 64); const int kb = r / 64, nb = r % 64;
;                 cvt_item8(inptr(F, IN_MD) + (size_t)e * DFE * D, D, kb * 128, nb * 32, ws + WS_MD + (size_t)e * D * DFE, DFE, nb * 32, scr, F.lane); return; }
.LBB0_218:
	s_andn2_b64 vcc, exec, s[16:17]
	s_cbranch_vccnz .LBB0_213
	s_mov_b64 s[16:17], -1
	s_cmpk_gt_i32 s18, 0x3ff
	v_lshlrev_b32_e32 v12, 2, v6
	v_add_u32_e32 v33, 0x420, v26
	v_add_u32_e32 v34, 0x428, v26
	v_add_u32_e32 v31, 0x840, v26
	s_waitcnt lgkmcnt(0)
	v_add_u32_e32 v32, 0x848, v26
	v_add_u32_e32 v29, 0xc60, v26
	v_add_u32_e32 v30, 0xc68, v26
	s_cbranch_scc0 .LBB0_221
	s_add_i32 s0, s18, 0xfc00
	v_mov_b32_e32 v13, s23
	s_and_b32 s16, s0, 0xffff
	ds_read_b64 v[14:15], v13
	s_mul_i32 s16, s16, 0xba2f
	s_lshr_b32 s17, s16, 26
	s_mul_i32 s16, s17, 0x580
	s_sub_i32 s0, s0, s16
	s_and_b32 s16, s0, 0xffff
	s_waitcnt lgkmcnt(0)
	v_readfirstlane_b32 s0, v14
	s_mul_i32 s20, s17, 0x1600000
	v_readfirstlane_b32 s19, v15
	s_add_u32 s20, s0, s20
	s_addc_u32 s19, s19, 0
	s_lshl_b32 s0, s16, 1
	s_lshl_b32 s16, s16, 5
	s_and_b32 s16, s16, 0x7e0
	s_and_b32 s0, s0, 0xf80
	s_lshl_b32 s21, s16, 2
	s_add_u32 s20, s20, s21
	v_or_b32_e32 v35, s0, v16
	s_addc_u32 s21, s19, 0
	v_mov_b32_e32 v13, v3
	v_lshl_add_u64 v[14:15], s[20:21], 0, v[12:13]
	v_lshlrev_b32_e32 v36, 13, v35
	v_mov_b32_e32 v37, v3
	v_lshl_add_u64 v[92:93], v[14:15], 0, v[36:37]
	v_add_co_u32_e32 v14, vcc, s24, v92
	s_nop 1
	v_addc_co_u32_e32 v15, vcc, 0, v93, vcc
	global_load_dwordx4 v[36:39], v[92:93], off nt
	global_load_dwordx4 v[40:43], v[14:15], off nt
	v_add_co_u32_e32 v14, vcc, s25, v92
	s_waitcnt vmcnt(0) lgkmcnt(0)
	v_mul_f32_e32 v13, 0x42800000, v36
	v_addc_co_u32_e32 v15, vcc, 0, v93, vcc
	global_load_dwordx4 v[44:47], v[14:15], off nt
	v_add_co_u32_e32 v14, vcc, s26, v92
	v_mul_f32_e32 v35, 0x42800000, v40
	s_nop 0
	v_addc_co_u32_e32 v15, vcc, 0, v93, vcc
	global_load_dwordx4 v[48:51], v[14:15], off nt
	v_add_co_u32_e32 v52, vcc, s27, v92
	v_med3_f32 v13, v13, s40, v28
	s_nop 0
	v_addc_co_u32_e32 v53, vcc, 0, v93, vcc
	v_add_co_u32_e32 v56, vcc, s28, v92
	v_med3_f32 v35, v35, s40, v28
	s_nop 0
	v_addc_co_u32_e32 v57, vcc, 0, v93, vcc
	global_load_dwordx4 v[52:55], v[52:53], off nt
	s_nop 0
	global_load_dwordx4 v[56:59], v[56:57], off nt
	v_add_co_u32_e32 v60, vcc, s29, v92
	v_mov_b32_e32 v40, v3
	s_nop 0
	v_addc_co_u32_e32 v61, vcc, 0, v93, vcc
	v_add_co_u32_e32 v64, vcc, s30, v92
	v_cvt_pk_fp8_f32 v40, v13, v35
	s_nop 0
	v_addc_co_u32_e32 v65, vcc, 0, v93, vcc
	global_load_dwordx4 v[60:63], v[60:61], off nt
	s_nop 0
	global_load_dwordx4 v[64:67], v[64:65], off nt
	v_add_co_u32_e32 v68, vcc, s31, v92
	v_mov_b64_e32 v[14:15], s[8:9]
	s_nop 0
	v_addc_co_u32_e32 v69, vcc, 0, v93, vcc
	v_add_co_u32_e32 v72, vcc, s33, v92
	v_mad_u64_u32 v[14:15], s[20:21], s17, v27, v[14:15]
	s_nop 0
	v_addc_co_u32_e32 v73, vcc, 0, v93, vcc
	global_load_dwordx4 v[68:71], v[68:69], off nt
	s_nop 0
	global_load_dwordx4 v[72:75], v[72:73], off nt
	v_add_co_u32_e32 v76, vcc, s34, v92
	v_lshl_add_u64 v[14:15], v[14:15], 0, s[0:1]
	s_nop 0
	v_addc_co_u32_e32 v77, vcc, 0, v93, vcc
	v_add_co_u32_e32 v80, vcc, s35, v92
	v_lshl_add_u64 v[14:15], v[14:15], 0, v[8:9]
	s_nop 0
	v_addc_co_u32_e32 v81, vcc, 0, v93, vcc
	global_load_dwordx4 v[76:79], v[76:77], off nt
	s_nop 0
	global_load_dwordx4 v[80:83], v[80:81], off nt
	v_add_co_u32_e32 v84, vcc, s36, v92
	s_waitcnt vmcnt(0) lgkmcnt(0)
	v_mul_f32_e32 v36, 0x42800000, v44
	v_addc_co_u32_e32 v85, vcc, 0, v93, vcc
	v_add_co_u32_e32 v88, vcc, s37, v92
	v_med3_f32 v35, v36, s40, v28
	s_nop 0
	v_addc_co_u32_e32 v89, vcc, 0, v93, vcc
	global_load_dwordx4 v[84:87], v[84:85], off nt
	s_nop 0
	global_load_dwordx4 v[88:91], v[88:89], off nt
	v_add_co_u32_e32 v94, vcc, s38, v92
	v_mul_f32_e32 v13, 0x42800000, v48
	s_nop 0
	v_addc_co_u32_e32 v95, vcc, 0, v93, vcc
	v_add_co_u32_e32 v96, vcc, s39, v92
	v_med3_f32 v13, v13, s40, v28
	s_nop 0
	v_addc_co_u32_e32 v97, vcc, 0, v93, vcc
	global_load_dwordx4 v[92:95], v[94:95], off nt
	s_nop 0
	global_load_dwordx4 v[96:99], v[96:97], off nt
	v_cvt_pk_fp8_f32 v40, v35, v13 op_sel:[0,0,1]
	v_mul_f32_e32 v13, 0x42800000, v37
	v_mul_f32_e32 v35, 0x42800000, v41
	v_med3_f32 v13, v13, s40, v28
	v_med3_f32 v35, v35, s40, v28
	v_mov_b32_e32 v37, v3
	v_cvt_pk_fp8_f32 v37, v13, v35
	v_mul_f32_e32 v36, 0x42800000, v45
	v_mul_f32_e32 v13, 0x42800000, v49
	v_med3_f32 v35, v36, s40, v28
	v_med3_f32 v13, v13, s40, v28
	v_cvt_pk_fp8_f32 v37, v35, v13 op_sel:[0,0,1]
	v_mul_f32_e32 v13, 0x42800000, v38
	v_mul_f32_e32 v35, 0x42800000, v42
	v_med3_f32 v13, v13, s40, v28
	v_med3_f32 v35, v35, s40, v28
	v_mov_b32_e32 v38, v3
	v_cvt_pk_fp8_f32 v38, v13, v35
	v_mul_f32_e32 v36, 0x42800000, v46
	v_mul_f32_e32 v13, 0x42800000, v50
	v_med3_f32 v35, v36, s40, v28
	v_med3_f32 v13, v13, s40, v28
	v_cvt_pk_fp8_f32 v38, v35, v13 op_sel:[0,0,1]
	v_mul_f32_e32 v13, 0x42800000, v39
	v_mul_f32_e32 v35, 0x42800000, v43
	v_med3_f32 v13, v13, s40, v28
	v_med3_f32 v35, v35, s40, v28
	v_mov_b32_e32 v39, v3
	v_cvt_pk_fp8_f32 v39, v13, v35
	v_mul_f32_e32 v36, 0x42800000, v47
	v_mul_f32_e32 v13, 0x42800000, v51
	v_med3_f32 v35, v36, s40, v28
	v_med3_f32 v13, v13, s40, v28
	v_cvt_pk_fp8_f32 v39, v35, v13 op_sel:[0,0,1]
	v_mul_f32_e32 v13, 0x42800000, v52
	v_mul_f32_e32 v35, 0x42800000, v56
	v_med3_f32 v13, v13, s40, v28
	v_med3_f32 v35, v35, s40, v28
	v_mov_b32_e32 v41, v3
	v_cvt_pk_fp8_f32 v41, v13, v35
	v_mul_f32_e32 v36, 0x42800000, v60
	v_mul_f32_e32 v13, 0x42800000, v64
	v_med3_f32 v35, v36, s40, v28
	v_med3_f32 v13, v13, s40, v28
	v_cvt_pk_fp8_f32 v41, v35, v13 op_sel:[0,0,1]
	v_mul_f32_e32 v13, 0x42800000, v53
	v_mul_f32_e32 v35, 0x42800000, v57
	v_med3_f32 v13, v13, s40, v28
	v_med3_f32 v35, v35, s40, v28
	v_mov_b32_e32 v42, v3
	v_cvt_pk_fp8_f32 v42, v13, v35
	v_mul_f32_e32 v36, 0x42800000, v61
	v_mul_f32_e32 v13, 0x42800000, v65
	v_med3_f32 v35, v36, s40, v28
; __device__ __forceinline__ void cvt_item8(const float* src, int ld, int k0, int c0, unsigned char* dst, int Kd, int drow0, unsigned char* scr, int lane) {
;     ...
;     for (int g = 0; g < 4; ++g)
; #pragma unroll
;         for (int i = 0; i < 4; ++i) *(unsigned*)(scr + (4 * c + i) * 132 + 32 * g + 4 * q) = pg8::pack_fp8x4(v[g][0][i] * WSC, v[g][1][i] * WSC, v[g][2][i] * WSC, v[g][3][i] * WSC);
;     asm volatile("s_waitcnt lgkmcnt(0)" ::: "memory");
; #pragma unroll
;     for (int r = 0; r < 4; ++r) { const int n = 8 * r + (lane >> 3), ch = lane & 7; const unsigned char* p = scr + n * 132 + ch * 16;
;         u32x4 o; o.x = *(const unsigned*)(p); o.y = *(const unsigned*)(p + 4); o.z = *(const unsigned*)(p + 8); o.w = *(const unsigned*)(p + 12);
;         *(u32x4*)(dst + (size_t)(drow0 + n) * Kd + k0 + 16 * ch) = o; }
;     asm volatile("s_waitcnt lgkmcnt(0)" ::: "memory");
	v_med3_f32 v13, v13, s40, v28
	v_cvt_pk_fp8_f32 v42, v35, v13 op_sel:[0,0,1]
	v_mul_f32_e32 v13, 0x42800000, v54
	v_mul_f32_e32 v35, 0x42800000, v58
	v_med3_f32 v13, v13, s40, v28
	v_med3_f32 v35, v35, s40, v28
	v_mov_b32_e32 v43, v3
	v_cvt_pk_fp8_f32 v43, v13, v35
	v_mul_f32_e32 v36, 0x42800000, v62
	v_mul_f32_e32 v13, 0x42800000, v66
	v_med3_f32 v35, v36, s40, v28
	v_med3_f32 v13, v13, s40, v28
	v_cvt_pk_fp8_f32 v43, v35, v13 op_sel:[0,0,1]
	v_mul_f32_e32 v13, 0x42800000, v55
	v_mul_f32_e32 v35, 0x42800000, v59
	v_med3_f32 v13, v13, s40, v28
	v_med3_f32 v35, v35, s40, v28
	v_mov_b32_e32 v44, v3
	v_cvt_pk_fp8_f32 v44, v13, v35
	v_mul_f32_e32 v36, 0x42800000, v63
	v_mul_f32_e32 v13, 0x42800000, v67
	v_med3_f32 v35, v36, s40, v28
	v_med3_f32 v13, v13, s40, v28
	v_cvt_pk_fp8_f32 v44, v35, v13 op_sel:[0,0,1]
	v_mul_f32_e32 v13, 0x42800000, v68
	v_mul_f32_e32 v35, 0x42800000, v72
	ds_write2_b32 v25, v40, v41 offset1:8
	ds_write2_b32 v25, v37, v42 offset0:33 offset1:41
	ds_write2_b32 v25, v38, v43 offset0:66 offset1:74
	ds_write2_b32 v25, v39, v44 offset0:99 offset1:107
	v_med3_f32 v13, v13, s40, v28
	v_med3_f32 v35, v35, s40, v28
	v_mov_b32_e32 v37, v3
	v_cvt_pk_fp8_f32 v37, v13, v35
	v_mul_f32_e32 v36, 0x42800000, v76
	v_mul_f32_e32 v13, 0x42800000, v80
	v_med3_f32 v35, v36, s40, v28
	v_med3_f32 v13, v13, s40, v28
	v_cvt_pk_fp8_f32 v37, v35, v13 op_sel:[0,0,1]
	v_mul_f32_e32 v13, 0x42800000, v69
	v_mul_f32_e32 v35, 0x42800000, v73
	v_med3_f32 v13, v13, s40, v28
	v_med3_f32 v35, v35, s40, v28
	v_mov_b32_e32 v38, v3
	v_cvt_pk_fp8_f32 v38, v13, v35
	v_mul_f32_e32 v36, 0x42800000, v77
	v_mul_f32_e32 v13, 0x42800000, v81
	v_med3_f32 v35, v36, s40, v28
	v_med3_f32 v13, v13, s40, v28
	v_cvt_pk_fp8_f32 v38, v35, v13 op_sel:[0,0,1]
	v_mul_f32_e32 v13, 0x42800000, v70
	v_mul_f32_e32 v35, 0x42800000, v74
	v_med3_f32 v13, v13, s40, v28
	v_med3_f32 v35, v35, s40, v28
	v_mov_b32_e32 v39, v3
	v_cvt_pk_fp8_f32 v39, v13, v35
	v_mul_f32_e32 v36, 0x42800000, v78
	v_mul_f32_e32 v13, 0x42800000, v82
	v_med3_f32 v35, v36, s40, v28
	v_med3_f32 v13, v13, s40, v28
	v_cvt_pk_fp8_f32 v39, v35, v13 op_sel:[0,0,1]
	v_mul_f32_e32 v13, 0x42800000, v71
	v_mul_f32_e32 v35, 0x42800000, v75
	v_med3_f32 v13, v13, s40, v28
	v_med3_f32 v35, v35, s40, v28
	v_mov_b32_e32 v40, v3
	v_cvt_pk_fp8_f32 v40, v13, v35
	v_mul_f32_e32 v36, 0x42800000, v79
	v_mul_f32_e32 v13, 0x42800000, v83
	v_med3_f32 v35, v36, s40, v28
	v_med3_f32 v13, v13, s40, v28
	v_cvt_pk_fp8_f32 v40, v35, v13 op_sel:[0,0,1]
	s_waitcnt vmcnt(0) lgkmcnt(0)
	v_mul_f32_e32 v13, 0x42800000, v84
	v_mul_f32_e32 v35, 0x42800000, v88
	v_med3_f32 v13, v13, s40, v28
	v_med3_f32 v35, v35, s40, v28
	v_mov_b32_e32 v41, v3
	v_cvt_pk_fp8_f32 v41, v13, v35
	v_mul_f32_e32 v36, 0x42800000, v92
	v_mul_f32_e32 v13, 0x42800000, v96
	v_med3_f32 v35, v36, s40, v28
	v_med3_f32 v13, v13, s40, v28
	v_cvt_pk_fp8_f32 v41, v35, v13 op_sel:[0,0,1]
	v_mul_f32_e32 v13, 0x42800000, v85
	v_mul_f32_e32 v35, 0x42800000, v89
	v_med3_f32 v13, v13, s40, v28
	v_med3_f32 v35, v35, s40, v28
	v_mov_b32_e32 v42, v3
	v_cvt_pk_fp8_f32 v42, v13, v35
	v_mul_f32_e32 v36, 0x42800000, v93
	v_mul_f32_e32 v13, 0x42800000, v97
	v_med3_f32 v35, v36, s40, v28
	v_med3_f32 v13, v13, s40, v28
	v_cvt_pk_fp8_f32 v42, v35, v13 op_sel:[0,0,1]
	v_mul_f32_e32 v13, 0x42800000, v86
	v_mul_f32_e32 v35, 0x42800000, v90
	v_med3_f32 v13, v13, s40, v28
	v_med3_f32 v35, v35, s40, v28
	v_mov_b32_e32 v43, v3
	v_cvt_pk_fp8_f32 v43, v13, v35
	v_mul_f32_e32 v36, 0x42800000, v94
	v_mul_f32_e32 v13, 0x42800000, v98
	v_med3_f32 v35, v36, s40, v28
	v_med3_f32 v13, v13, s40, v28
	v_cvt_pk_fp8_f32 v43, v35, v13 op_sel:[0,0,1]
	v_mul_f32_e32 v13, 0x42800000, v87
	v_mul_f32_e32 v35, 0x42800000, v91
	v_med3_f32 v13, v13, s40, v28
	v_med3_f32 v35, v35, s40, v28
	v_mov_b32_e32 v44, v3
	v_cvt_pk_fp8_f32 v44, v13, v35
	v_mul_f32_e32 v36, 0x42800000, v95
	v_mul_f32_e32 v13, 0x42800000, v99
	v_med3_f32 v35, v36, s40, v28
	v_med3_f32 v13, v13, s40, v28
	v_cvt_pk_fp8_f32 v44, v35, v13 op_sel:[0,0,1]
	ds_write2_b32 v25, v37, v41 offset0:16 offset1:24
	ds_write2_b32 v25, v38, v42 offset0:49 offset1:57
	ds_write2_b32 v25, v39, v43 offset0:82 offset1:90
	ds_write2_b32 v25, v40, v44 offset0:115 offset1:123
	s_waitcnt lgkmcnt(0)
	ds_read2_b32 v[36:37], v26 offset1:1
	ds_read2_b32 v[38:39], v26 offset0:2 offset1:3
	v_or_b32_e32 v13, s16, v7
	v_mul_u32_u24_e32 v40, 0xb00, v13
	v_mov_b32_e32 v41, v3
	v_lshl_add_u64 v[44:45], v[14:15], 0, v[40:41]
	ds_read2_b32 v[40:41], v33 offset1:1
	ds_read2_b32 v[42:43], v34 offset1:1
	v_or_b32_e32 v13, s16, v17
	s_waitcnt lgkmcnt(2)
	global_store_dwordx4 v[44:45], v[36:39], off
	s_nop 1
	v_mul_u32_u24_e32 v36, 0xb00, v13
	v_mov_b32_e32 v37, v3
	v_lshl_add_u64 v[36:37], v[14:15], 0, v[36:37]
	s_waitcnt lgkmcnt(0)
	global_store_dwordx4 v[36:37], v[40:43], off
	ds_read2_b32 v[36:37], v31 offset1:1
	ds_read2_b32 v[38:39], v32 offset1:1
	v_or_b32_e32 v13, s16, v18
	v_mul_u32_u24_e32 v40, 0xb00, v13
	v_mov_b32_e32 v41, v3
	v_lshl_add_u64 v[44:45], v[14:15], 0, v[40:41]
	ds_read2_b32 v[40:41], v29 offset1:1
	ds_read2_b32 v[42:43], v30 offset1:1
	v_or_b32_e32 v13, s16, v19
	s_waitcnt lgkmcnt(2)
	global_store_dwordx4 v[44:45], v[36:39], off
	s_mov_b64 s[16:17], 0
	s_nop 0
	v_mul_u32_u24_e32 v36, 0xb00, v13
	v_mov_b32_e32 v37, v3
	v_lshl_add_u64 v[14:15], v[14:15], 0, v[36:37]
	s_waitcnt lgkmcnt(0)
	global_store_dwordx4 v[14:15], v[40:43], off
	s_waitcnt lgkmcnt(0)
; __device__ __forceinline__ void cvt_item8(const float* src, int ld, int k0, int c0, unsigned char* dst, int Kd, int drow0, unsigned char* scr, int lane) {
;     const int c = lane & 7, q = lane >> 3;
;     f32x4 v[4][4];
; #pragma unroll
;     for (int g = 0; g < 4; ++g)
; #pragma unroll
;         for (int j = 0; j < 4; ++j) v[g][j] = __builtin_nontemporal_load((const f32x4*)(src + (size_t)(k0 + 32 * g + 4 * q + j) * ld + c0 + 4 * c));
; #pragma unroll
;     for (int g = 0; g < 4; ++g)
; #pragma unroll
;         for (int i = 0; i < 4; ++i) *(unsigned*)(scr + (4 * c + i) * 132 + 32 * g + 4 * q) = pg8::pack_fp8x4(v[g][0][i] * WSC, v[g][1][i] * WSC, v[g][2][i] * WSC, v[g][3][i] * WSC);
;     asm volatile("s_waitcnt lgkmcnt(0)" ::: "memory");
; template <int GRP>
; __device__ __forceinline__ void conv_item(Frame& F, int r) {
;     ...
;         if (r < CI_WO) { const int kb = r / 64, nb = r % 64;
;             cvt_item8(inptr(F, IN_WOUT) + (size_t)l * D * D, D, kb * 128, nb * 32, ws + WS_WOUT + (size_t)l * D * D, D, nb * 32, scr, F.lane); return; }
.LBB0_221:
	s_andn2_b64 vcc, exec, s[16:17]
	s_cbranch_vccnz .LBB0_213
	s_ashr_i32 s0, s18, 31
	v_mov_b32_e32 v13, s41
	s_lshr_b32 s0, s0, 26
	ds_read_b64 v[14:15], v13
	s_add_i32 s0, s18, s0
	s_and_b32 s16, s0, 0x7ffffc0
	s_sub_i32 s16, s18, s16
	s_lshl_b32 s16, s16, 5
	s_lshl_b32 s0, s0, 1
	s_ashr_i32 s17, s16, 31
	s_waitcnt lgkmcnt(0)
	v_readfirstlane_b32 s19, v14
	s_and_b32 s18, s0, 0xffffff80
	s_lshl_b64 s[20:21], s[16:17], 2
	v_readfirstlane_b32 s43, v15
	v_or_b32_e32 v88, s18, v16
	s_add_u32 s20, s19, s20
	s_addc_u32 s21, s43, s21
	v_mov_b32_e32 v13, v3
	v_or_b32_e32 v14, 1, v88
	v_lshl_add_u64 v[12:13], s[20:21], 0, v[12:13]
	v_ashrrev_i32_e32 v89, 31, v88
	v_ashrrev_i32_e32 v15, 31, v14
	v_or_b32_e32 v40, 2, v88
	v_lshl_add_u64 v[90:91], v[12:13], 0, s[14:15]
	v_lshlrev_b64 v[12:13], 13, v[88:89]
	v_lshlrev_b64 v[14:15], 13, v[14:15]
	v_ashrrev_i32_e32 v41, 31, v40
	v_lshl_add_u64 v[12:13], v[90:91], 0, v[12:13]
	v_lshl_add_u64 v[36:37], v[90:91], 0, v[14:15]
	v_lshlrev_b64 v[40:41], 13, v[40:41]
	global_load_dwordx4 v[12:15], v[12:13], off nt
	s_nop 0
	global_load_dwordx4 v[36:39], v[36:37], off nt
	v_lshl_add_u64 v[40:41], v[90:91], 0, v[40:41]
	v_or_b32_e32 v44, 3, v88
	global_load_dwordx4 v[40:43], v[40:41], off nt
	v_ashrrev_i32_e32 v45, 31, v44
	v_lshlrev_b64 v[44:45], 13, v[44:45]
	v_lshl_add_u64 v[44:45], v[90:91], 0, v[44:45]
	global_load_dwordx4 v[44:47], v[44:45], off nt
	v_or_b32_e32 v48, 32, v88
	v_or_b32_e32 v50, 33, v88
	v_ashrrev_i32_e32 v49, 31, v48
	v_ashrrev_i32_e32 v51, 31, v50
	v_lshlrev_b64 v[48:49], 13, v[48:49]
	v_lshlrev_b64 v[50:51], 13, v[50:51]
	v_lshl_add_u64 v[48:49], v[90:91], 0, v[48:49]
	v_lshl_add_u64 v[52:53], v[90:91], 0, v[50:51]
	global_load_dwordx4 v[48:51], v[48:49], off nt
	s_nop 0
	global_load_dwordx4 v[52:55], v[52:53], off nt
	v_or_b32_e32 v56, 34, v88
	v_or_b32_e32 v58, 35, v88
	v_ashrrev_i32_e32 v57, 31, v56
	v_ashrrev_i32_e32 v59, 31, v58
	v_lshlrev_b64 v[56:57], 13, v[56:57]
	v_lshlrev_b64 v[58:59], 13, v[58:59]
	v_lshl_add_u64 v[56:57], v[90:91], 0, v[56:57]
	v_lshl_add_u64 v[60:61], v[90:91], 0, v[58:59]
	global_load_dwordx4 v[56:59], v[56:57], off nt
	s_nop 0
	global_load_dwordx4 v[60:63], v[60:61], off nt
	v_or_b32_e32 v64, 64, v88
	v_or_b32_e32 v66, 0x41, v88
	v_ashrrev_i32_e32 v65, 31, v64
	v_ashrrev_i32_e32 v67, 31, v66
	v_lshlrev_b64 v[64:65], 13, v[64:65]
	v_lshlrev_b64 v[66:67], 13, v[66:67]
	v_lshl_add_u64 v[64:65], v[90:91], 0, v[64:65]
	v_lshl_add_u64 v[68:69], v[90:91], 0, v[66:67]
	global_load_dwordx4 v[64:67], v[64:65], off nt
	s_nop 0
	global_load_dwordx4 v[68:71], v[68:69], off nt
	v_or_b32_e32 v72, 0x42, v88
	v_or_b32_e32 v74, 0x43, v88
	v_ashrrev_i32_e32 v73, 31, v72
	v_ashrrev_i32_e32 v75, 31, v74
	v_lshlrev_b64 v[72:73], 13, v[72:73]
	v_lshlrev_b64 v[74:75], 13, v[74:75]
	v_lshl_add_u64 v[72:73], v[90:91], 0, v[72:73]
	v_lshl_add_u64 v[76:77], v[90:91], 0, v[74:75]
	global_load_dwordx4 v[72:75], v[72:73], off nt
	s_nop 0
	global_load_dwordx4 v[76:79], v[76:77], off nt
	v_or_b32_e32 v80, 0x60, v88
	v_or_b32_e32 v82, 0x61, v88
	v_ashrrev_i32_e32 v81, 31, v80
	v_ashrrev_i32_e32 v83, 31, v82
	v_lshlrev_b64 v[80:81], 13, v[80:81]
	v_lshlrev_b64 v[82:83], 13, v[82:83]
	v_lshl_add_u64 v[80:81], v[90:91], 0, v[80:81]
	v_lshl_add_u64 v[84:85], v[90:91], 0, v[82:83]
	global_load_dwordx4 v[80:83], v[80:81], off nt
	s_nop 0
	global_load_dwordx4 v[84:87], v[84:85], off nt
	v_or_b32_e32 v92, 0x62, v88
	v_or_b32_e32 v88, 0x63, v88
	v_ashrrev_i32_e32 v93, 31, v92
	v_ashrrev_i32_e32 v89, 31, v88
	v_lshlrev_b64 v[92:93], 13, v[92:93]
	v_lshlrev_b64 v[88:89], 13, v[88:89]
	v_lshl_add_u64 v[92:93], v[90:91], 0, v[92:93]
	v_lshl_add_u64 v[94:95], v[90:91], 0, v[88:89]
	global_load_dwordx4 v[88:91], v[92:93], off nt
	s_nop 0
	global_load_dwordx4 v[92:95], v[94:95], off nt
	s_ashr_i32 s19, s18, 31
	s_waitcnt vmcnt(0) lgkmcnt(0)
	v_mul_f32_e32 v12, 0x42800000, v12
	v_mul_f32_e32 v35, 0x42800000, v36
	v_med3_f32 v12, v12, s40, v28
	v_med3_f32 v35, v35, s40, v28
	v_mul_f32_e32 v36, 0x42800000, v40
	v_mov_b32_e32 v40, v3
	v_cvt_pk_fp8_f32 v40, v12, v35
	v_med3_f32 v35, v36, s40, v28
	v_mul_f32_e32 v12, 0x42800000, v44
	v_med3_f32 v12, v12, s40, v28
	v_cvt_pk_fp8_f32 v40, v35, v12 op_sel:[0,0,1]
	v_mul_f32_e32 v12, 0x42800000, v13
	v_mul_f32_e32 v13, 0x42800000, v37
	v_med3_f32 v12, v12, s40, v28
	v_med3_f32 v13, v13, s40, v28
	v_mov_b32_e32 v36, v3
	v_cvt_pk_fp8_f32 v36, v12, v13
	v_mul_f32_e32 v35, 0x42800000, v41
	v_mul_f32_e32 v12, 0x42800000, v45
	v_med3_f32 v13, v35, s40, v28
	v_med3_f32 v12, v12, s40, v28
	v_cvt_pk_fp8_f32 v36, v13, v12 op_sel:[0,0,1]
	v_mul_f32_e32 v12, 0x42800000, v14
	v_mul_f32_e32 v13, 0x42800000, v38
	v_med3_f32 v12, v12, s40, v28
	v_med3_f32 v13, v13, s40, v28
	v_mov_b32_e32 v35, v3
	v_cvt_pk_fp8_f32 v35, v12, v13
	v_mul_f32_e32 v14, 0x42800000, v42
	v_mul_f32_e32 v12, 0x42800000, v46
	v_med3_f32 v13, v14, s40, v28
	v_med3_f32 v12, v12, s40, v28
	v_cvt_pk_fp8_f32 v35, v13, v12 op_sel:[0,0,1]
	v_mul_f32_e32 v12, 0x42800000, v15
	v_mul_f32_e32 v13, 0x42800000, v39
	v_med3_f32 v12, v12, s40, v28
	v_med3_f32 v13, v13, s40, v28
	v_mov_b32_e32 v15, v3
	v_cvt_pk_fp8_f32 v15, v12, v13
	v_mul_f32_e32 v14, 0x42800000, v43
	v_mul_f32_e32 v12, 0x42800000, v47
	v_med3_f32 v13, v14, s40, v28
	v_med3_f32 v12, v12, s40, v28
	v_cvt_pk_fp8_f32 v15, v13, v12 op_sel:[0,0,1]
	v_mul_f32_e32 v12, 0x42800000, v48
	v_mul_f32_e32 v13, 0x42800000, v52
	v_med3_f32 v12, v12, s40, v28
	v_med3_f32 v13, v13, s40, v28
	v_mov_b32_e32 v37, v3
	v_cvt_pk_fp8_f32 v37, v12, v13
	v_mul_f32_e32 v14, 0x42800000, v56
	v_mul_f32_e32 v12, 0x42800000, v60
	v_med3_f32 v13, v14, s40, v28
; __device__ __forceinline__ void cvt_item8(const float* src, int ld, int k0, int c0, unsigned char* dst, int Kd, int drow0, unsigned char* scr, int lane) {
;     ...
;     for (int g = 0; g < 4; ++g)
; #pragma unroll
;         for (int i = 0; i < 4; ++i) *(unsigned*)(scr + (4 * c + i) * 132 + 32 * g + 4 * q) = pg8::pack_fp8x4(v[g][0][i] * WSC, v[g][1][i] * WSC, v[g][2][i] * WSC, v[g][3][i] * WSC);
;     asm volatile("s_waitcnt lgkmcnt(0)" ::: "memory");
; #pragma unroll
;     for (int r = 0; r < 4; ++r) { const int n = 8 * r + (lane >> 3), ch = lane & 7; const unsigned char* p = scr + n * 132 + ch * 16;
;         u32x4 o; o.x = *(const unsigned*)(p); o.y = *(const unsigned*)(p + 4); o.z = *(const unsigned*)(p + 8); o.w = *(const unsigned*)(p + 12);
;         *(u32x4*)(dst + (size_t)(drow0 + n) * Kd + k0 + 16 * ch) = o; }
;     asm volatile("s_waitcnt lgkmcnt(0)" ::: "memory");
	v_med3_f32 v12, v12, s40, v28
	v_cvt_pk_fp8_f32 v37, v13, v12 op_sel:[0,0,1]
	v_mul_f32_e32 v12, 0x42800000, v49
	v_mul_f32_e32 v13, 0x42800000, v53
	v_med3_f32 v12, v12, s40, v28
	v_med3_f32 v13, v13, s40, v28
	v_mov_b32_e32 v38, v3
	v_cvt_pk_fp8_f32 v38, v12, v13
	v_mul_f32_e32 v14, 0x42800000, v57
	v_mul_f32_e32 v12, 0x42800000, v61
	v_med3_f32 v13, v14, s40, v28
	v_med3_f32 v12, v12, s40, v28
	v_cvt_pk_fp8_f32 v38, v13, v12 op_sel:[0,0,1]
	v_mul_f32_e32 v12, 0x42800000, v50
	v_mul_f32_e32 v13, 0x42800000, v54
	v_med3_f32 v12, v12, s40, v28
	v_med3_f32 v13, v13, s40, v28
	v_mov_b32_e32 v39, v3
	v_cvt_pk_fp8_f32 v39, v12, v13
	v_mul_f32_e32 v14, 0x42800000, v58
	v_mul_f32_e32 v12, 0x42800000, v62
	v_med3_f32 v13, v14, s40, v28
	v_med3_f32 v12, v12, s40, v28
	v_cvt_pk_fp8_f32 v39, v13, v12 op_sel:[0,0,1]
	v_mul_f32_e32 v12, 0x42800000, v51
	v_mul_f32_e32 v13, 0x42800000, v55
	v_med3_f32 v12, v12, s40, v28
	v_med3_f32 v13, v13, s40, v28
	v_mov_b32_e32 v41, v3
	v_cvt_pk_fp8_f32 v41, v12, v13
	v_mul_f32_e32 v14, 0x42800000, v59
	v_mul_f32_e32 v12, 0x42800000, v63
	v_med3_f32 v13, v14, s40, v28
	v_med3_f32 v12, v12, s40, v28
	v_cvt_pk_fp8_f32 v41, v13, v12 op_sel:[0,0,1]
	v_mul_f32_e32 v12, 0x42800000, v64
	v_mul_f32_e32 v13, 0x42800000, v68
	ds_write2_b32 v25, v40, v37 offset1:8
	ds_write2_b32 v25, v36, v38 offset0:33 offset1:41
	ds_write2_b32 v25, v35, v39 offset0:66 offset1:74
	ds_write2_b32 v25, v15, v41 offset0:99 offset1:107
	v_med3_f32 v12, v12, s40, v28
	v_med3_f32 v13, v13, s40, v28
	v_mov_b32_e32 v15, v3
	v_cvt_pk_fp8_f32 v15, v12, v13
	v_mul_f32_e32 v14, 0x42800000, v72
	v_mul_f32_e32 v12, 0x42800000, v76
	v_med3_f32 v13, v14, s40, v28
	v_med3_f32 v12, v12, s40, v28
	v_cvt_pk_fp8_f32 v15, v13, v12 op_sel:[0,0,1]
	v_mul_f32_e32 v12, 0x42800000, v65
	v_mul_f32_e32 v13, 0x42800000, v69
	v_med3_f32 v12, v12, s40, v28
	v_med3_f32 v13, v13, s40, v28
	v_mov_b32_e32 v35, v3
	v_cvt_pk_fp8_f32 v35, v12, v13
	v_mul_f32_e32 v14, 0x42800000, v73
	v_mul_f32_e32 v12, 0x42800000, v77
	v_med3_f32 v13, v14, s40, v28
	v_med3_f32 v12, v12, s40, v28
	v_cvt_pk_fp8_f32 v35, v13, v12 op_sel:[0,0,1]
	v_mul_f32_e32 v12, 0x42800000, v66
	v_mul_f32_e32 v13, 0x42800000, v70
	v_med3_f32 v12, v12, s40, v28
	v_med3_f32 v13, v13, s40, v28
	v_mov_b32_e32 v36, v3
	v_cvt_pk_fp8_f32 v36, v12, v13
	v_mul_f32_e32 v14, 0x42800000, v74
	v_mul_f32_e32 v12, 0x42800000, v78
	v_med3_f32 v13, v14, s40, v28
	v_med3_f32 v12, v12, s40, v28
	v_cvt_pk_fp8_f32 v36, v13, v12 op_sel:[0,0,1]
	v_mul_f32_e32 v12, 0x42800000, v67
	v_mul_f32_e32 v13, 0x42800000, v71
	v_med3_f32 v12, v12, s40, v28
	v_med3_f32 v13, v13, s40, v28
	v_mov_b32_e32 v37, v3
	v_cvt_pk_fp8_f32 v37, v12, v13
	v_mul_f32_e32 v14, 0x42800000, v75
	v_mul_f32_e32 v12, 0x42800000, v79
	v_med3_f32 v13, v14, s40, v28
	v_med3_f32 v12, v12, s40, v28
	v_cvt_pk_fp8_f32 v37, v13, v12 op_sel:[0,0,1]
	v_mul_f32_e32 v12, 0x42800000, v80
	v_mul_f32_e32 v13, 0x42800000, v84
	v_med3_f32 v12, v12, s40, v28
	v_med3_f32 v13, v13, s40, v28
	v_mov_b32_e32 v38, v3
	v_cvt_pk_fp8_f32 v38, v12, v13
	v_mul_f32_e32 v14, 0x42800000, v88
	v_mul_f32_e32 v12, 0x42800000, v92
	v_med3_f32 v13, v14, s40, v28
	v_med3_f32 v12, v12, s40, v28
	v_cvt_pk_fp8_f32 v38, v13, v12 op_sel:[0,0,1]
	v_mul_f32_e32 v12, 0x42800000, v81
	v_mul_f32_e32 v13, 0x42800000, v85
	v_med3_f32 v12, v12, s40, v28
	v_med3_f32 v13, v13, s40, v28
	v_mov_b32_e32 v39, v3
	v_cvt_pk_fp8_f32 v39, v12, v13
	v_mul_f32_e32 v14, 0x42800000, v89
	v_mul_f32_e32 v12, 0x42800000, v93
	v_med3_f32 v13, v14, s40, v28
	v_med3_f32 v12, v12, s40, v28
	v_cvt_pk_fp8_f32 v39, v13, v12 op_sel:[0,0,1]
	v_mul_f32_e32 v12, 0x42800000, v82
	v_mul_f32_e32 v13, 0x42800000, v86
	v_med3_f32 v12, v12, s40, v28
	v_med3_f32 v13, v13, s40, v28
	v_mov_b32_e32 v40, v3
	v_cvt_pk_fp8_f32 v40, v12, v13
	v_mul_f32_e32 v14, 0x42800000, v90
	v_mul_f32_e32 v12, 0x42800000, v94
	v_med3_f32 v13, v14, s40, v28
	v_med3_f32 v12, v12, s40, v28
	v_cvt_pk_fp8_f32 v40, v13, v12 op_sel:[0,0,1]
	v_mul_f32_e32 v12, 0x42800000, v83
	v_mul_f32_e32 v13, 0x42800000, v87
	v_med3_f32 v12, v12, s40, v28
	v_med3_f32 v13, v13, s40, v28
	v_mov_b32_e32 v41, v3
	v_cvt_pk_fp8_f32 v41, v12, v13
	v_mul_f32_e32 v14, 0x42800000, v91
	v_mul_f32_e32 v12, 0x42800000, v95
	v_med3_f32 v13, v14, s40, v28
	v_med3_f32 v12, v12, s40, v28
	v_cvt_pk_fp8_f32 v41, v13, v12 op_sel:[0,0,1]
	ds_write2_b32 v25, v15, v38 offset0:16 offset1:24
	ds_write2_b32 v25, v35, v39 offset0:49 offset1:57
	ds_write2_b32 v25, v36, v40 offset0:82 offset1:90
	ds_write2_b32 v25, v37, v41 offset0:115 offset1:123
	s_waitcnt lgkmcnt(0)
	ds_read2_b32 v[12:13], v26 offset1:1
	ds_read2_b32 v[14:15], v26 offset0:2 offset1:3
	v_or_b32_e32 v36, s16, v7
	v_ashrrev_i32_e32 v37, 31, v36
	v_lshl_add_u64 v[40:41], v[10:11], 0, s[18:19]
	v_lshlrev_b64 v[36:37], 11, v[36:37]
	v_lshl_add_u64 v[42:43], v[40:41], 0, v[36:37]
	ds_read2_b32 v[36:37], v33 offset1:1
	ds_read2_b32 v[38:39], v34 offset1:1
	s_waitcnt lgkmcnt(2)
	global_store_dwordx4 v[42:43], v[12:15], off
	s_nop 1
	v_or_b32_e32 v12, s16, v17
	v_ashrrev_i32_e32 v13, 31, v12
	v_lshlrev_b64 v[12:13], 11, v[12:13]
	v_lshl_add_u64 v[12:13], v[40:41], 0, v[12:13]
	s_waitcnt lgkmcnt(0)
	global_store_dwordx4 v[12:13], v[36:39], off
	ds_read2_b32 v[12:13], v31 offset1:1
	ds_read2_b32 v[14:15], v32 offset1:1
	v_or_b32_e32 v32, s16, v18
	v_ashrrev_i32_e32 v33, 31, v32
	v_lshlrev_b64 v[32:33], 11, v[32:33]
	v_lshl_add_u64 v[36:37], v[40:41], 0, v[32:33]
	ds_read2_b32 v[32:33], v29 offset1:1
	ds_read2_b32 v[34:35], v30 offset1:1
	s_waitcnt lgkmcnt(2)
	global_store_dwordx4 v[36:37], v[12:15], off
	s_nop 1
	v_or_b32_e32 v12, s16, v19
	v_ashrrev_i32_e32 v13, 31, v12
	v_lshlrev_b64 v[12:13], 11, v[12:13]
	v_lshl_add_u64 v[12:13], v[40:41], 0, v[12:13]
	s_waitcnt lgkmcnt(0)
	global_store_dwordx4 v[12:13], v[32:35], off
	s_waitcnt lgkmcnt(0)
	s_branch .LBB0_213

; __device__ __forceinline__ void colmax_item(const float* src, int ld, int k0, int c0, float* cmx  , int lane) {
;     const int c = lane & 7, q = lane >> 3;
;     f32x4 mx = (f32x4){0.f, 0.f, 0.f, 0.f};
; #pragma unroll
;     for (int g = 0; g < 4; ++g)
; #pragma unroll
;         for (int j = 0; j < 4; ++j) { const f32x4 v = *(const f32x4*)(src + (size_t)(k0 + 32 * g + 4 * q + j) * ld + c0 + 4 * c);
;             mx[0] = fmaxf(mx[0], fabsf(v[0])); mx[1] = fmaxf(mx[1], fabsf(v[1])); mx[2] = fmaxf(mx[2], fabsf(v[2])); mx[3] = fmaxf(mx[3], fabsf(v[3])); }
; #pragma unroll
;     for (int i = 0; i < 4; ++i) { float v = mx[i]; v = fmaxf(v, __shfl_xor(v, 8)); v = fmaxf(v, __shfl_xor(v, 16)); v = fmaxf(v, __shfl_xor(v, 32)); mx[i] = v; }
;     if (q == 0) {
; #pragma unroll
;         for (int i = 0; i < 4; ++i) atomicMax((unsigned*)(cmx + 4 * c + i), __float_as_uint(mx[i] * CMS_F)); }
; }
; template <int GRP>
; __device__ __forceinline__ void conv_item(Frame& F, int r) {
;     ...
;         if (r < NI) { const int kb = r / 152, nb = r % 152, c0 = (nb < 112) ? nb * 32 : SRC_GATE + 8 + (nb - 112) * 32, drow = nb * 32;
;             if (QUANT) cvt_item_i8(inptr(F, IN_WIN) + (size_t)l * D * NIN_SRC, NIN_SRC, kb * 128, c0, ws + WS_WIN + (size_t)l * NIN * D, D, drow, cmx + CMX_WIN + l * NIN + drow, scr, F.lane);
;             else colmax_item(inptr(F, IN_WIN) + (size_t)l * D * NIN_SRC, NIN_SRC, kb * 128, c0, cmx + CMX_WIN + l * NIN + drow, F.lane);
.LBB0_437:
	s_mul_hi_i32 s14, s23, 0x6bca1af3
	s_lshr_b32 s15, s14, 31
	s_ashr_i32 s14, s14, 6
	s_add_i32 s15, s14, s15
	s_mul_i32 s14, s15, 0x98
	s_sub_i32 s20, s23, s14
	v_mov_b32_e32 v1, s3
	s_waitcnt lgkmcnt(3)
	ds_read_b64 v[126:127], v1
	s_lshl_b32 s14, s20, 5
	s_or_b32 s21, s14, 8
	s_cmpk_lt_i32 s20, 0x70
	s_cselect_b32 s20, s14, s21
	s_ashr_i32 s21, s20, 31
	s_waitcnt lgkmcnt(0)
	v_readfirstlane_b32 s24, v126
	s_lshl_b64 s[20:21], s[20:21], 2
	v_readfirstlane_b32 s25, v127
	s_add_u32 s20, s24, s20
	s_addc_u32 s21, s25, s21
	v_lshlrev_b32_e32 v136, 2, v142
	v_lshl_or_b32 v1, s15, 7, v135
	v_lshl_add_u64 v[126:127], s[20:21], 0, v[136:137]
	s_mov_b64 s[20:21], 0x2610000
	v_lshl_add_u64 v[192:193], v[126:127], 0, s[20:21]
	v_or_b32_e32 v136, 2, v1
	v_mad_i64_i32 v[152:153], s[20:21], v136, s4, v[192:193]
	v_or_b32_e32 v136, 3, v1
	v_mad_i64_i32 v[156:157], s[20:21], v136, s4, v[192:193]
	v_or_b32_e32 v136, 32, v1
	v_mad_i64_i32 v[160:161], s[20:21], v136, s4, v[192:193]
	v_or_b32_e32 v136, 33, v1
	v_mad_i64_i32 v[164:165], s[20:21], v136, s4, v[192:193]
	v_or_b32_e32 v136, 34, v1
	v_or_b32_e32 v128, 1, v1
	v_mad_i64_i32 v[168:169], s[20:21], v136, s4, v[192:193]
	v_or_b32_e32 v136, 35, v1
	v_mad_i64_i32 v[126:127], s[20:21], v1, s4, v[192:193]
	v_mad_i64_i32 v[130:131], s[20:21], v128, s4, v[192:193]
	v_mad_i64_i32 v[172:173], s[20:21], v136, s4, v[192:193]
	v_or_b32_e32 v136, 64, v1
	global_load_dwordx4 v[126:129], v[126:127], off
	s_nop 0
	global_load_dwordx4 v[130:133], v[130:131], off
	v_mad_i64_i32 v[176:177], s[20:21], v136, s4, v[192:193]
	v_or_b32_e32 v136, 0x41, v1
	global_load_dwordx4 v[152:155], v[152:153], off
	s_nop 0
	global_load_dwordx4 v[156:159], v[156:157], off
	v_mad_i64_i32 v[180:181], s[20:21], v136, s4, v[192:193]
	v_or_b32_e32 v136, 0x42, v1
	global_load_dwordx4 v[160:163], v[160:161], off
	s_nop 0
	global_load_dwordx4 v[164:167], v[164:165], off
	v_mad_i64_i32 v[184:185], s[20:21], v136, s4, v[192:193]
	v_or_b32_e32 v136, 0x43, v1
	global_load_dwordx4 v[168:171], v[168:169], off
	s_nop 0
	global_load_dwordx4 v[172:175], v[172:173], off
	v_mad_i64_i32 v[188:189], s[20:21], v136, s4, v[192:193]
	v_or_b32_e32 v136, 0x60, v1
	global_load_dwordx4 v[176:179], v[176:177], off
	s_nop 0
	global_load_dwordx4 v[180:183], v[180:181], off
	v_mad_i64_i32 v[196:197], s[20:21], v136, s4, v[192:193]
	v_or_b32_e32 v136, 0x61, v1
	global_load_dwordx4 v[184:187], v[184:185], off
	s_nop 0
	global_load_dwordx4 v[188:191], v[188:189], off
	v_mad_i64_i32 v[200:201], s[20:21], v136, s4, v[192:193]
	v_or_b32_e32 v136, 0x62, v1
	global_load_dwordx4 v[196:199], v[196:197], off
	s_nop 0
	global_load_dwordx4 v[200:203], v[200:201], off
	v_mad_i64_i32 v[204:205], s[20:21], v136, s4, v[192:193]
	v_or_b32_e32 v1, 0x63, v1
	v_mad_i64_i32 v[192:193], s[20:21], v1, s4, v[192:193]
	global_load_dwordx4 v[204:207], v[204:205], off
	s_nop 0
	global_load_dwordx4 v[208:211], v[192:193], off
	s_waitcnt vmcnt(0) lgkmcnt(0)
	v_max3_f32 v1, |v126|, 0, |v130|
	v_max3_f32 v126, |v127|, 0, |v131|
	v_max3_f32 v127, |v128|, 0, |v132|
	v_and_b32_e32 v130, 64, v232
	v_max3_f32 v127, v127, |v154|, |v158|
	v_max3_f32 v1, v1, |v152|, |v156|
	v_max3_f32 v128, |v129|, 0, |v133|
	v_add_u32_e32 v130, 64, v130
	v_max3_f32 v127, v127, |v162|, |v166|
	v_max3_f32 v1, v1, |v160|, |v164|
	v_max3_f32 v126, v126, |v153|, |v157|
	v_max3_f32 v126, v126, |v161|, |v165|
	v_max3_f32 v127, v127, |v170|, |v174|
	v_max3_f32 v1, v1, |v168|, |v172|
	v_max3_f32 v126, v126, |v169|, |v173|
	v_xor_b32_e32 v131, 16, v232
	v_max3_f32 v127, v127, |v178|, |v182|
	v_max3_f32 v1, v1, |v176|, |v180|
	v_max3_f32 v126, v126, |v177|, |v181|
	v_xor_b32_e32 v133, 32, v232
	v_max3_f32 v127, v127, |v186|, |v190|
	v_max3_f32 v1, v1, |v184|, |v188|
	v_max3_f32 v126, v126, |v185|, |v189|
	v_max3_f32 v128, v128, |v155|, |v159|
	v_max3_f32 v127, v127, |v198|, |v202|
	v_max3_f32 v1, v1, |v196|, |v200|
	v_max3_f32 v126, v126, |v197|, |v201|
	v_max3_f32 v128, v128, |v163|, |v167|
	v_max3_f32 v128, v128, |v171|, |v175|
	v_max3_f32 v128, v128, |v179|, |v183|
	v_max3_f32 v129, v127, |v206|, |v210|
	v_xor_b32_e32 v127, 8, v232
	v_cmp_lt_i32_e32 vcc, v127, v130
	v_max3_f32 v1, v1, |v204|, |v208|
	v_max3_f32 v126, v126, |v205|, |v209|
	v_cndmask_b32_e32 v127, v232, v127, vcc
	v_lshlrev_b32_e32 v127, 2, v127
	ds_bpermute_b32 v132, v127, v1
	v_cmp_lt_i32_e32 vcc, v131, v130
	v_max3_f32 v128, v128, |v187|, |v191|
	v_max3_f32 v128, v128, |v199|, |v203|
	v_cndmask_b32_e32 v131, v232, v131, vcc
	v_cmp_lt_i32_e32 vcc, v133, v130
	s_waitcnt lgkmcnt(0)
	v_max_f32_e32 v132, v132, v132
	v_lshlrev_b32_e32 v131, 2, v131
	v_cndmask_b32_e32 v130, v232, v133, vcc
	ds_bpermute_b32 v133, v127, v126
	v_max_f32_e32 v1, v1, v132
	ds_bpermute_b32 v132, v131, v1
	v_lshlrev_b32_e32 v136, 2, v130
	v_max3_f32 v128, v128, |v207|, |v211|
	s_waitcnt lgkmcnt(1)
	v_max_f32_e32 v130, v133, v133
	v_max_f32_e32 v130, v126, v130
	ds_bpermute_b32 v133, v131, v130
	s_waitcnt lgkmcnt(1)
	v_max_f32_e32 v126, v132, v132
	ds_bpermute_b32 v132, v127, v129
	ds_bpermute_b32 v152, v127, v128
	v_max_f32_e32 v1, v1, v126
	s_waitcnt lgkmcnt(2)
	v_max_f32_e32 v133, v133, v133
	v_max_f32_e32 v127, v130, v133
	s_waitcnt lgkmcnt(1)
	v_max_f32_e32 v130, v132, v132
	s_waitcnt lgkmcnt(0)
	v_max_f32_e32 v132, v152, v152
	v_max_f32_e32 v129, v129, v130
	v_max_f32_e32 v132, v128, v132
	ds_bpermute_b32 v130, v131, v129
	ds_bpermute_b32 v131, v131, v132
	ds_bpermute_b32 v126, v136, v1
	ds_bpermute_b32 v128, v136, v127
	s_waitcnt lgkmcnt(3)
	v_max_f32_e32 v130, v130, v130
	s_waitcnt lgkmcnt(2)
	v_max_f32_e32 v131, v131, v131
	v_max_f32_e32 v129, v129, v130
	v_max_f32_e32 v131, v132, v131
	ds_bpermute_b32 v130, v136, v129
	ds_bpermute_b32 v132, v136, v131
	s_and_saveexec_b64 s[20:21], s[8:9]
	s_cbranch_execz .LBB0_439
	s_waitcnt lgkmcnt(3)
	v_max_f32_e32 v126, v126, v126
	v_max_f32_e32 v1, v1, v1
	s_ashr_i32 s15, s14, 31
	s_waitcnt lgkmcnt(2)
	v_max_f32_e32 v128, v128, v128
	v_max_f32_e32 v127, v127, v127
	v_max_f32_e32 v1, v1, v126
	s_waitcnt lgkmcnt(1)
	v_max_f32_e32 v130, v130, v130
	v_max_f32_e32 v129, v129, v129
	v_max_f32_e32 v128, v127, v128
	v_lshl_add_u64 v[126:127], s[14:15], 2, v[144:145]
	v_mul_f32_e32 v1, 0x3fb33333, v1
	s_waitcnt lgkmcnt(0)
	v_max_f32_e32 v132, v132, v132
	v_max_f32_e32 v131, v131, v131
	v_max_f32_e32 v129, v129, v130
	global_atomic_umax v[126:127], v1, off
	v_mul_f32_e32 v1, 0x3fb33333, v128
	v_max_f32_e32 v131, v131, v132
	global_atomic_umax v[126:127], v1, off offset:4
	v_mul_f32_e32 v1, 0x3fb33333, v129
	global_atomic_umax v[126:127], v1, off offset:8
	v_mul_f32_e32 v1, 0x3fb33333, v131
	global_atomic_umax v[126:127], v1, off offset:12

; __device__ __forceinline__ void colmax_item(const float* src, int ld, int k0, int c0, float* cmx  , int lane) {
;     const int c = lane & 7, q = lane >> 3;
;     f32x4 mx = (f32x4){0.f, 0.f, 0.f, 0.f};
; #pragma unroll
;     for (int g = 0; g < 4; ++g)
; #pragma unroll
;         for (int j = 0; j < 4; ++j) { const f32x4 v = *(const f32x4*)(src + (size_t)(k0 + 32 * g + 4 * q + j) * ld + c0 + 4 * c);
;             mx[0] = fmaxf(mx[0], fabsf(v[0])); mx[1] = fmaxf(mx[1], fabsf(v[1])); mx[2] = fmaxf(mx[2], fabsf(v[2])); mx[3] = fmaxf(mx[3], fabsf(v[3])); }
; #pragma unroll
;     for (int i = 0; i < 4; ++i) { float v = mx[i]; v = fmaxf(v, __shfl_xor(v, 8)); v = fmaxf(v, __shfl_xor(v, 16)); v = fmaxf(v, __shfl_xor(v, 32)); mx[i] = v; }
; template <int GRP>
; __device__ __forceinline__ void conv_item(Frame& F, int r) {
;     ...
;     else { constexpr int KBN = (GRP == 3) ? 16 : CMS_KB, I_E = KBN * 88; const int up = r / (8 * I_E); r %= (8 * I_E); const int e = r / I_E; r %= I_E; const int kb = r / 88, nb = r % 88, n0 = nb * 32, drow = (n0 >> 7) * 256 + up * 128 + (n0 & 127);
;         if (GRP == 3) cvt_item_i8(inptr(F, up ? IN_MU : IN_MG) + (size_t)e * D * DFE, DFE, kb * 128, n0, ws + WS_MGU + (size_t)e * 2 * DFE * D, D, drow, cmx + 2 * DFF + e * 2 * DFE + drow, scr, F.lane);
;         else colmax_item(inptr(F, up ? IN_MU : IN_MG) + (size_t)e * D * DFE, DFE, kb * 128, n0, cmx + 2 * DFF + e * 2 * DFE + drow, F.lane); }
.LBB0_441:
	s_cmpk_gt_i32 s23, 0x3ff
	s_mov_b64 s[10:11], -1
	s_cbranch_scc0 .LBB0_449
	s_cmpk_gt_u32 s23, 0x2fff
	s_cbranch_scc0 .LBB0_446
	s_add_i32 s10, s23, 0xffffd000
	s_mul_hi_u32 s11, s10, 0xba2e8ba3
	s_lshr_b32 s20, s11, 10
	v_mul_u32_u24_e32 v1, s20, v233
	s_add_i32 s14, s23, 0xffffd57f
	v_readfirstlane_b32 s11, v1
	s_sub_i32 s10, s10, s11
	s_mul_i32 s11, s10, 0xba2f
	s_lshr_b32 s21, s11, 23
	s_mul_i32 s11, s21, 0xb0
	s_sub_i32 s10, s10, s11
	s_and_b32 s11, s10, 0xffff
	s_add_i32 s10, s11, 0xffffffa8
	s_min_u32 s24, s11, s10
	s_lshl_b32 s10, s24, 5
	s_cmpk_lt_u32 s14, 0xaff
	s_movk_i32 s14, 0xa0
	s_cselect_b32 s14, s14, 0xa8
	s_add_i32 s14, s14, 0
	s_add_i32 s14, s14, 0x20200
	v_mov_b32_e32 v1, s14
	s_waitcnt lgkmcnt(3)
	ds_read_b64 v[126:127], v1
	s_cmpk_gt_u32 s11, 0x57
	v_mul_u32_u24_e32 v136, s21, v234
	s_cselect_b32 s11, 0x80, 0
	v_or_b32_e32 v1, s11, v135
	s_waitcnt lgkmcnt(0)
	v_readfirstlane_b32 s14, v126
	v_readfirstlane_b32 s15, v127
	v_lshlrev_b64 v[126:127], 2, v[136:137]
	s_ashr_i32 s11, s10, 31
	v_lshl_add_u64 v[126:127], s[14:15], 0, v[126:127]
	s_lshl_b64 s[14:15], s[10:11], 2
	v_lshl_add_u64 v[126:127], v[126:127], 0, s[14:15]
	v_lshlrev_b32_e32 v136, 2, v142
	v_lshl_add_u64 v[126:127], v[126:127], 0, v[136:137]
	v_mul_u32_u24_e32 v136, 0x2c00, v1
	v_lshl_add_u64 v[192:193], v[126:127], 0, v[136:137]
	s_movk_i32 s11, 0x2000
	v_add_co_u32_e32 v130, vcc, s11, v192
	s_movk_i32 s11, 0x5000
	s_nop 0
	v_addc_co_u32_e32 v131, vcc, 0, v193, vcc
	v_add_co_u32_e32 v152, vcc, s11, v192
	s_mov_b32 s11, 0x8000
	s_nop 0
	v_addc_co_u32_e32 v153, vcc, 0, v193, vcc
	v_add_co_u32_e32 v156, vcc, s11, v192
	s_mov_b32 s11, 0x58000
	s_nop 0
	v_addc_co_u32_e32 v157, vcc, 0, v193, vcc
	v_add_co_u32_e32 v160, vcc, s11, v192
	s_mov_b32 s11, 0x5a000
	s_nop 0
	v_addc_co_u32_e32 v161, vcc, 0, v193, vcc
	v_add_co_u32_e32 v164, vcc, s11, v192
	s_mov_b32 s11, 0x5d000
	s_nop 0
	v_addc_co_u32_e32 v165, vcc, 0, v193, vcc
	v_add_co_u32_e32 v168, vcc, s11, v192
	s_mov_b32 s11, 0x60000
	s_nop 0
	v_addc_co_u32_e32 v169, vcc, 0, v193, vcc
	v_add_co_u32_e32 v172, vcc, s11, v192
	s_mov_b32 s11, 0xb0000
	s_nop 0
	v_addc_co_u32_e32 v173, vcc, 0, v193, vcc
	v_add_co_u32_e32 v176, vcc, s11, v192
	s_mov_b32 s11, 0xb2000
	s_nop 0
	v_addc_co_u32_e32 v177, vcc, 0, v193, vcc
	v_add_co_u32_e32 v180, vcc, s11, v192
	s_mov_b32 s11, 0xb5000
	s_nop 0
	v_addc_co_u32_e32 v181, vcc, 0, v193, vcc
	v_add_co_u32_e32 v184, vcc, s11, v192
	s_mov_b32 s11, 0xb8000
	s_nop 0
	v_addc_co_u32_e32 v185, vcc, 0, v193, vcc
	v_add_co_u32_e32 v188, vcc, s11, v192
	s_mov_b32 s11, 0x108000
	s_nop 0
	v_addc_co_u32_e32 v189, vcc, 0, v193, vcc
	global_load_dwordx4 v[126:129], v[192:193], off
	s_nop 0
	global_load_dwordx4 v[130:133], v[130:131], off offset:3072
	v_add_co_u32_e32 v196, vcc, s11, v192
	global_load_dwordx4 v[152:155], v[152:153], off offset:2048
	s_nop 0
	global_load_dwordx4 v[156:159], v[156:157], off offset:1024
	v_addc_co_u32_e32 v197, vcc, 0, v193, vcc
	s_mov_b32 s11, 0x10a000
	global_load_dwordx4 v[160:163], v[160:161], off
	s_nop 0
	global_load_dwordx4 v[164:167], v[164:165], off offset:3072
	v_add_co_u32_e32 v200, vcc, s11, v192
	global_load_dwordx4 v[168:171], v[168:169], off offset:2048
	s_nop 0
	global_load_dwordx4 v[172:175], v[172:173], off offset:1024
	v_addc_co_u32_e32 v201, vcc, 0, v193, vcc
	s_mov_b32 s11, 0x10d000
	global_load_dwordx4 v[176:179], v[176:177], off
	s_nop 0
	global_load_dwordx4 v[180:183], v[180:181], off offset:3072
	v_add_co_u32_e32 v204, vcc, s11, v192
	global_load_dwordx4 v[184:187], v[184:185], off offset:2048
	s_nop 0
	global_load_dwordx4 v[188:191], v[188:189], off offset:1024
	v_addc_co_u32_e32 v205, vcc, 0, v193, vcc
	s_mov_b32 s11, 0x110000
	global_load_dwordx4 v[196:199], v[196:197], off
	s_nop 0
	global_load_dwordx4 v[200:203], v[200:201], off offset:3072
	v_add_co_u32_e32 v192, vcc, s11, v192
	s_waitcnt vmcnt(0) lgkmcnt(0)
	v_max3_f32 v1, |v126|, 0, |v130|
	v_addc_co_u32_e32 v193, vcc, 0, v193, vcc
	global_load_dwordx4 v[204:207], v[204:205], off offset:2048
	s_nop 0
	global_load_dwordx4 v[208:211], v[192:193], off offset:1024
	v_max3_f32 v126, |v127|, 0, |v131|
	v_max3_f32 v127, |v128|, 0, |v132|
	v_max3_f32 v127, v127, |v154|, |v158|
	v_max3_f32 v127, v127, |v162|, |v166|
	v_max3_f32 v1, v1, |v152|, |v156|
	v_max3_f32 v1, v1, |v160|, |v164|
	v_max3_f32 v127, v127, |v170|, |v174|
	v_max3_f32 v1, v1, |v168|, |v172|
	v_and_b32_e32 v130, 64, v232
	v_max3_f32 v128, |v129|, 0, |v133|
	v_max3_f32 v127, v127, |v178|, |v182|
	v_max3_f32 v1, v1, |v176|, |v180|
	v_add_u32_e32 v130, 64, v130
	v_max3_f32 v127, v127, |v186|, |v190|
	v_max3_f32 v126, v126, |v153|, |v157|
	v_max3_f32 v1, v1, |v184|, |v188|
	v_max3_f32 v126, v126, |v161|, |v165|
	v_max3_f32 v127, v127, |v198|, |v202|
	v_max3_f32 v1, v1, |v196|, |v200|
	v_max3_f32 v126, v126, |v169|, |v173|
	v_max3_f32 v126, v126, |v177|, |v181|
	v_max3_f32 v126, v126, |v185|, |v189|
	v_xor_b32_e32 v131, 16, v232
	v_max3_f32 v126, v126, |v197|, |v201|
	v_xor_b32_e32 v133, 32, v232
	v_max3_f32 v128, v128, |v155|, |v159|
	v_max3_f32 v128, v128, |v163|, |v167|
	v_max3_f32 v128, v128, |v171|, |v175|
	v_max3_f32 v128, v128, |v179|, |v183|
	v_max3_f32 v128, v128, |v187|, |v191|
	v_max3_f32 v128, v128, |v199|, |v203|
	s_waitcnt vmcnt(0) lgkmcnt(0)
	v_max3_f32 v129, v127, |v206|, |v210|
	v_xor_b32_e32 v127, 8, v232
	v_cmp_lt_i32_e32 vcc, v127, v130
	v_max3_f32 v1, v1, |v204|, |v208|
	v_max3_f32 v126, v126, |v205|, |v209|
	v_cndmask_b32_e32 v127, v232, v127, vcc
	v_lshlrev_b32_e32 v127, 2, v127
	ds_bpermute_b32 v132, v127, v1
	v_cmp_lt_i32_e32 vcc, v131, v130
	v_max3_f32 v128, v128, |v207|, |v211|
	ds_bpermute_b32 v152, v127, v128
	v_cndmask_b32_e32 v131, v232, v131, vcc
	v_cmp_lt_i32_e32 vcc, v133, v130
	s_waitcnt lgkmcnt(1)
	v_max_f32_e32 v132, v132, v132
	v_lshlrev_b32_e32 v131, 2, v131
	v_cndmask_b32_e32 v130, v232, v133, vcc
	ds_bpermute_b32 v133, v127, v126
	v_max_f32_e32 v1, v1, v132
	ds_bpermute_b32 v132, v131, v1
	v_lshlrev_b32_e32 v136, 2, v130
	s_waitcnt lgkmcnt(1)
	v_max_f32_e32 v130, v133, v133
	v_max_f32_e32 v130, v126, v130
	ds_bpermute_b32 v133, v131, v130
	s_waitcnt lgkmcnt(1)
	v_max_f32_e32 v126, v132, v132
	ds_bpermute_b32 v132, v127, v129
	v_max_f32_e32 v1, v1, v126
	ds_bpermute_b32 v126, v136, v1
	s_waitcnt lgkmcnt(2)
	v_max_f32_e32 v133, v133, v133
	v_max_f32_e32 v127, v130, v133
	s_waitcnt lgkmcnt(1)
	v_max_f32_e32 v130, v132, v132
	v_max_f32_e32 v132, v152, v152
	v_max_f32_e32 v129, v129, v130
	v_max_f32_e32 v132, v128, v132
	ds_bpermute_b32 v130, v131, v129
	ds_bpermute_b32 v131, v131, v132
	ds_bpermute_b32 v128, v136, v127
	s_waitcnt lgkmcnt(2)
	v_max_f32_e32 v130, v130, v130
	s_waitcnt lgkmcnt(1)
	v_max_f32_e32 v131, v131, v131
	v_max_f32_e32 v129, v129, v130
	v_max_f32_e32 v131, v132, v131
	ds_bpermute_b32 v130, v136, v129
	ds_bpermute_b32 v132, v136, v131
	s_and_saveexec_b64 s[14:15], s[8:9]
	s_cbranch_execz .LBB0_445
; __device__ __forceinline__ void colmax_item(const float* src, int ld, int k0, int c0, float* cmx  , int lane) {
;     ...
;     if (q == 0) {
; #pragma unroll
;         for (int i = 0; i < 4; ++i) atomicMax((unsigned*)(cmx + 4 * c + i), __float_as_uint(mx[i] * CMS_F)); }
	s_lshl_b32 s11, s24, 6
	s_and_b32 s11, s11, 0x3fff00
	s_lshl_b32 s20, s20, 7
	v_mul_u32_u24_e32 v133, s21, v235
	v_readlane_b32 s26, v255, 37
	s_add_i32 s11, s11, s20
	s_and_b32 s10, s10, 0x60
	v_lshlrev_b32_e32 v136, 2, v133
	v_readlane_b32 s27, v255, 38
	s_or_b32 s10, s11, s10
	s_lshl_b32 s70, s10, 2
	v_lshl_add_u64 v[152:153], s[26:27], 0, v[136:137]
	v_max_f32_e32 v126, v126, v126
	v_max_f32_e32 v1, v1, v1
	v_lshl_add_u64 v[152:153], v[152:153], 0, s[70:71]
	s_waitcnt lgkmcnt(2)
	v_max_f32_e32 v128, v128, v128
	v_max_f32_e32 v127, v127, v127
	v_max_f32_e32 v1, v1, v126
	s_waitcnt lgkmcnt(1)
	v_max_f32_e32 v130, v130, v130
	v_max_f32_e32 v129, v129, v129
	v_max_f32_e32 v127, v127, v128
	v_mul_f32_e32 v1, 0x3fb33333, v1
	v_readfirstlane_b32 s10, v152
	v_readfirstlane_b32 s11, v153
	s_waitcnt lgkmcnt(0)
	v_max_f32_e32 v132, v132, v132
	v_max_f32_e32 v131, v131, v131
	v_max_f32_e32 v129, v129, v130
	v_max_f32_e32 v131, v131, v132
	global_atomic_umax v230, v1, s[10:11]
	v_mul_f32_e32 v1, 0x3fb33333, v127
	global_atomic_umax v230, v1, s[10:11] offset:4
	v_mul_f32_e32 v1, 0x3fb33333, v129
	global_atomic_umax v230, v1, s[10:11] offset:8
	v_mul_f32_e32 v1, 0x3fb33333, v131
	global_atomic_umax v230, v1, s[10:11] offset:12

; __device__ __forceinline__ void cvt_item8(const float* src, int ld, int k0, int c0, unsigned char* dst, int Kd, int drow0, unsigned char* scr, int lane) {
;     const int c = lane & 7, q = lane >> 3;
;     f32x4 v[4][4];
; #pragma unroll
;     for (int g = 0; g < 4; ++g)
; #pragma unroll
;         for (int j = 0; j < 4; ++j) v[g][j] = __builtin_nontemporal_load((const f32x4*)(src + (size_t)(k0 + 32 * g + 4 * q + j) * ld + c0 + 4 * c));
; #pragma unroll
;     for (int g = 0; g < 4; ++g)
; #pragma unroll
;         for (int i = 0; i < 4; ++i) *(unsigned*)(scr + (4 * c + i) * 132 + 32 * g + 4 * q) = pg8::pack_fp8x4(v[g][0][i] * WSC, v[g][1][i] * WSC, v[g][2][i] * WSC, v[g][3][i] * WSC);
; template <int GRP>
; __device__ __forceinline__ void conv_item(Frame& F, int r) {
;     ...
;             if (r < CI_MD) { const int e = r / (22 * 64); r %= (22 * 64); const int kb = r / 64, nb = r % 64;
;                 cvt_item8(inptr(F, IN_MD) + (size_t)e * DFE * D, D, kb * 128, nb * 32, ws + WS_MD + (size_t)e * D * DFE, DFE, nb * 32, scr, F.lane); return; }
.LBB0_446:
	s_andn2_b64 vcc, exec, s[10:11]
	s_cbranch_vccnz .LBB0_448
	s_add_i32 s10, s23, 0xfc00
	v_mov_b32_e32 v1, s16
	s_and_b32 s11, s10, 0xffff
	s_waitcnt lgkmcnt(3)
	ds_read_b64 v[126:127], v1
	s_mul_i32 s11, s11, 0xba2f
	s_lshr_b32 s11, s11, 26
	s_mul_i32 s14, s11, 0x580
	s_sub_i32 s10, s10, s14
	s_and_b32 s10, s10, 0xffff
	s_waitcnt lgkmcnt(0)
	v_readfirstlane_b32 s14, v126
	s_mul_i32 s20, s11, 0x1600000
	v_readfirstlane_b32 s15, v127
	s_add_u32 s14, s14, s20
	s_addc_u32 s15, s15, 0
	s_lshl_b32 s20, s10, 1
	s_lshl_b32 s10, s10, 5
	s_and_b32 s10, s10, 0x7e0
	s_and_b32 s70, s20, 0xf80
	s_lshl_b32 s20, s10, 2
	s_add_u32 s14, s14, s20
	v_or_b32_e32 v1, s70, v143
	s_addc_u32 s15, s15, 0
	v_lshlrev_b32_e32 v136, 2, v146
	v_lshl_add_u64 v[126:127], s[14:15], 0, v[136:137]
	v_lshlrev_b32_e32 v136, 13, v1
	v_lshl_add_u64 v[132:133], v[126:127], 0, v[136:137]
	s_movk_i32 s14, 0x2000
	v_add_co_u32_e32 v126, vcc, s14, v132
	s_movk_i32 s14, 0x4000
	s_nop 0
	v_addc_co_u32_e32 v127, vcc, 0, v133, vcc
	global_load_dwordx4 v[152:155], v[132:133], off nt
	global_load_dwordx4 v[156:159], v[126:127], off nt
	v_add_co_u32_e32 v126, vcc, s14, v132
	s_movk_i32 s14, 0x6000
	s_nop 0
	v_addc_co_u32_e32 v127, vcc, 0, v133, vcc
	global_load_dwordx4 v[160:163], v[126:127], off nt
	v_add_co_u32_e32 v126, vcc, s14, v132
	v_mov_b32_e32 v136, v137
	s_nop 0
	v_addc_co_u32_e32 v127, vcc, 0, v133, vcc
	global_load_dwordx4 v[164:167], v[126:127], off nt
	v_mov_b64_e32 v[126:127], s[18:19]
	v_mad_u64_u32 v[130:131], s[14:15], s11, v234, v[126:127]
	s_mov_b32 s11, 0x40000
	v_add_co_u32_e32 v126, vcc, s11, v132
	s_mov_b32 s11, 0x42000
	s_nop 0
	v_addc_co_u32_e32 v127, vcc, 0, v133, vcc
	v_add_co_u32_e32 v128, vcc, s11, v132
	s_mov_b32 s11, 0x44000
	s_nop 0
	v_addc_co_u32_e32 v129, vcc, 0, v133, vcc
	global_load_dwordx4 v[168:171], v[126:127], off nt
	global_load_dwordx4 v[172:175], v[128:129], off nt
	v_add_co_u32_e32 v126, vcc, s11, v132
	s_mov_b32 s11, 0x46000
	s_nop 0
	v_addc_co_u32_e32 v127, vcc, 0, v133, vcc
	v_add_co_u32_e32 v128, vcc, s11, v132
	s_mov_b32 s11, 0x80000
	s_nop 0
	v_addc_co_u32_e32 v129, vcc, 0, v133, vcc
	global_load_dwordx4 v[176:179], v[126:127], off nt
	global_load_dwordx4 v[180:183], v[128:129], off nt
	v_add_co_u32_e32 v126, vcc, s11, v132
	s_mov_b32 s11, 0x82000
	s_nop 0
	v_addc_co_u32_e32 v127, vcc, 0, v133, vcc
	v_add_co_u32_e32 v128, vcc, s11, v132
	s_mov_b32 s11, 0x84000
	s_nop 0
	v_addc_co_u32_e32 v129, vcc, 0, v133, vcc
	global_load_dwordx4 v[184:187], v[126:127], off nt
	global_load_dwordx4 v[188:191], v[128:129], off nt
	v_add_co_u32_e32 v126, vcc, s11, v132
	s_mov_b32 s11, 0x86000
	s_nop 0
	v_addc_co_u32_e32 v127, vcc, 0, v133, vcc
	v_add_co_u32_e32 v128, vcc, s11, v132
	s_mov_b32 s11, 0xc0000
	s_nop 0
	v_addc_co_u32_e32 v129, vcc, 0, v133, vcc
	global_load_dwordx4 v[196:199], v[126:127], off nt
	global_load_dwordx4 v[200:203], v[128:129], off nt
	v_add_co_u32_e32 v126, vcc, s11, v132
	s_mov_b32 s11, 0xc2000
	s_nop 0
	v_addc_co_u32_e32 v127, vcc, 0, v133, vcc
	v_add_co_u32_e32 v192, vcc, s11, v132
	s_mov_b32 s11, 0xc4000
	s_nop 0
	v_addc_co_u32_e32 v193, vcc, 0, v133, vcc
	global_load_dwordx4 v[126:129], v[126:127], off nt
	s_nop 0
	global_load_dwordx4 v[204:207], v[192:193], off nt
	v_add_co_u32_e32 v192, vcc, s11, v132
	s_mov_b32 s11, 0xc6000
	s_nop 0
	v_addc_co_u32_e32 v193, vcc, 0, v133, vcc
	v_add_co_u32_e32 v132, vcc, s11, v132
	s_waitcnt vmcnt(0) lgkmcnt(0)
	v_mul_f32_e32 v1, 0x42800000, v152
	v_addc_co_u32_e32 v133, vcc, 0, v133, vcc
	global_load_dwordx4 v[208:211], v[192:193], off nt
	global_load_dwordx4 v[212:215], v[132:133], off nt
	v_mul_f32_e32 v132, 0x42800000, v156
	v_med3_f32 v1, v1, s17, v231
	v_med3_f32 v132, v132, s17, v231
	v_cvt_pk_fp8_f32 v136, v1, v132
	v_mul_f32_e32 v133, 0x42800000, v160
	v_med3_f32 v132, v133, s17, v231
	v_mul_f32_e32 v133, 0x42800000, v157
	v_med3_f32 v133, v133, s17, v231
	v_mul_f32_e32 v152, 0x42800000, v161
	v_mul_f32_e32 v1, 0x42800000, v164
	v_med3_f32 v1, v1, s17, v231
	v_cvt_pk_fp8_f32 v136, v132, v1 op_sel:[0,0,1]
	v_mul_f32_e32 v132, 0x42800000, v153
	v_med3_f32 v132, v132, s17, v231
	v_mov_b32_e32 v153, v137
	v_cvt_pk_fp8_f32 v153, v132, v133
	v_mul_f32_e32 v132, 0x42800000, v165
	v_med3_f32 v133, v152, s17, v231
	v_med3_f32 v132, v132, s17, v231
	v_cvt_pk_fp8_f32 v153, v133, v132 op_sel:[0,0,1]
	v_mul_f32_e32 v132, 0x42800000, v154
	v_mul_f32_e32 v133, 0x42800000, v158
	v_med3_f32 v132, v132, s17, v231
	v_med3_f32 v133, v133, s17, v231
	v_mov_b32_e32 v154, v137
	v_cvt_pk_fp8_f32 v154, v132, v133
	v_mul_f32_e32 v152, 0x42800000, v162
	v_mul_f32_e32 v132, 0x42800000, v166
	v_med3_f32 v133, v152, s17, v231
	v_med3_f32 v132, v132, s17, v231
	v_cvt_pk_fp8_f32 v154, v133, v132 op_sel:[0,0,1]
	v_mul_f32_e32 v132, 0x42800000, v155
	v_mul_f32_e32 v133, 0x42800000, v159
	v_med3_f32 v132, v132, s17, v231
	v_med3_f32 v133, v133, s17, v231
	v_mov_b32_e32 v155, v137
	v_cvt_pk_fp8_f32 v155, v132, v133
	v_mul_f32_e32 v152, 0x42800000, v163
	v_mul_f32_e32 v132, 0x42800000, v167
	v_med3_f32 v133, v152, s17, v231
	v_med3_f32 v132, v132, s17, v231
	v_cvt_pk_fp8_f32 v155, v133, v132 op_sel:[0,0,1]
	v_mul_f32_e32 v132, 0x42800000, v168
	v_mul_f32_e32 v133, 0x42800000, v172
	v_med3_f32 v132, v132, s17, v231
	v_med3_f32 v133, v133, s17, v231
	v_mov_b32_e32 v156, v137
	v_cvt_pk_fp8_f32 v156, v132, v133
	v_mul_f32_e32 v152, 0x42800000, v176
	v_mul_f32_e32 v132, 0x42800000, v180
	v_med3_f32 v133, v152, s17, v231
	v_med3_f32 v132, v132, s17, v231
	v_cvt_pk_fp8_f32 v156, v133, v132 op_sel:[0,0,1]
	v_mul_f32_e32 v132, 0x42800000, v169
	v_mul_f32_e32 v133, 0x42800000, v173
	v_med3_f32 v132, v132, s17, v231
; __device__ __forceinline__ void cvt_item8(const float* src, int ld, int k0, int c0, unsigned char* dst, int Kd, int drow0, unsigned char* scr, int lane) {
;     ...
;     for (int g = 0; g < 4; ++g)
; #pragma unroll
;         for (int i = 0; i < 4; ++i) *(unsigned*)(scr + (4 * c + i) * 132 + 32 * g + 4 * q) = pg8::pack_fp8x4(v[g][0][i] * WSC, v[g][1][i] * WSC, v[g][2][i] * WSC, v[g][3][i] * WSC);
;     asm volatile("s_waitcnt lgkmcnt(0)" ::: "memory");
; #pragma unroll
;     for (int r = 0; r < 4; ++r) { const int n = 8 * r + (lane >> 3), ch = lane & 7; const unsigned char* p = scr + n * 132 + ch * 16;
;         u32x4 o; o.x = *(const unsigned*)(p); o.y = *(const unsigned*)(p + 4); o.z = *(const unsigned*)(p + 8); o.w = *(const unsigned*)(p + 12);
;         *(u32x4*)(dst + (size_t)(drow0 + n) * Kd + k0 + 16 * ch) = o; }
;     asm volatile("s_waitcnt lgkmcnt(0)" ::: "memory");
	v_med3_f32 v133, v133, s17, v231
	v_mov_b32_e32 v157, v137
	v_cvt_pk_fp8_f32 v157, v132, v133
	v_mul_f32_e32 v152, 0x42800000, v177
	v_mul_f32_e32 v132, 0x42800000, v181
	v_med3_f32 v133, v152, s17, v231
	v_med3_f32 v132, v132, s17, v231
	v_cvt_pk_fp8_f32 v157, v133, v132 op_sel:[0,0,1]
	v_mul_f32_e32 v132, 0x42800000, v170
	v_mul_f32_e32 v133, 0x42800000, v174
	v_med3_f32 v132, v132, s17, v231
	v_med3_f32 v133, v133, s17, v231
	v_mov_b32_e32 v158, v137
	v_cvt_pk_fp8_f32 v158, v132, v133
	v_mul_f32_e32 v152, 0x42800000, v178
	v_mul_f32_e32 v132, 0x42800000, v182
	v_med3_f32 v133, v152, s17, v231
	v_med3_f32 v132, v132, s17, v231
	v_cvt_pk_fp8_f32 v158, v133, v132 op_sel:[0,0,1]
	v_mul_f32_e32 v132, 0x42800000, v171
	v_mul_f32_e32 v133, 0x42800000, v175
	v_med3_f32 v132, v132, s17, v231
	v_med3_f32 v133, v133, s17, v231
	v_mov_b32_e32 v159, v137
	v_cvt_pk_fp8_f32 v159, v132, v133
	v_mul_f32_e32 v152, 0x42800000, v179
	v_mul_f32_e32 v132, 0x42800000, v183
	v_med3_f32 v133, v152, s17, v231
	v_med3_f32 v132, v132, s17, v231
	v_cvt_pk_fp8_f32 v159, v133, v132 op_sel:[0,0,1]
	v_mul_f32_e32 v132, 0x42800000, v184
	v_mul_f32_e32 v133, 0x42800000, v188
	v_med3_f32 v132, v132, s17, v231
	v_med3_f32 v133, v133, s17, v231
	v_mov_b32_e32 v152, v137
	v_cvt_pk_fp8_f32 v152, v132, v133
	v_add_u32_e32 v1, v147, v224
	ds_write2_b32 v1, v136, v156 offset1:8
	ds_write2_b32 v1, v153, v157 offset0:33 offset1:41
	ds_write2_b32 v1, v154, v158 offset0:66 offset1:74
	ds_write2_b32 v1, v155, v159 offset0:99 offset1:107
	v_mul_f32_e32 v136, 0x42800000, v196
	v_mul_f32_e32 v132, 0x42800000, v200
	v_med3_f32 v133, v136, s17, v231
	v_med3_f32 v132, v132, s17, v231
	v_cvt_pk_fp8_f32 v152, v133, v132 op_sel:[0,0,1]
	v_mul_f32_e32 v132, 0x42800000, v185
	v_mul_f32_e32 v133, 0x42800000, v189
	v_med3_f32 v132, v132, s17, v231
	v_med3_f32 v133, v133, s17, v231
	v_mov_b32_e32 v153, v137
	v_cvt_pk_fp8_f32 v153, v132, v133
	v_mul_f32_e32 v136, 0x42800000, v197
	v_mul_f32_e32 v132, 0x42800000, v201
	v_med3_f32 v133, v136, s17, v231
	v_med3_f32 v132, v132, s17, v231
	v_cvt_pk_fp8_f32 v153, v133, v132 op_sel:[0,0,1]
	v_mul_f32_e32 v132, 0x42800000, v186
	v_mul_f32_e32 v133, 0x42800000, v190
	v_med3_f32 v132, v132, s17, v231
	v_med3_f32 v133, v133, s17, v231
	v_mov_b32_e32 v154, v137
	v_cvt_pk_fp8_f32 v154, v132, v133
	v_mul_f32_e32 v136, 0x42800000, v198
	v_mul_f32_e32 v132, 0x42800000, v202
	v_med3_f32 v133, v136, s17, v231
	v_med3_f32 v132, v132, s17, v231
	v_cvt_pk_fp8_f32 v154, v133, v132 op_sel:[0,0,1]
	v_mul_f32_e32 v132, 0x42800000, v187
	v_mul_f32_e32 v133, 0x42800000, v191
	v_med3_f32 v132, v132, s17, v231
	v_med3_f32 v133, v133, s17, v231
	v_mov_b32_e32 v155, v137
	v_cvt_pk_fp8_f32 v155, v132, v133
	v_mul_f32_e32 v136, 0x42800000, v199
	v_mul_f32_e32 v132, 0x42800000, v203
	v_med3_f32 v133, v136, s17, v231
	v_med3_f32 v132, v132, s17, v231
	v_cvt_pk_fp8_f32 v155, v133, v132 op_sel:[0,0,1]
	v_mul_f32_e32 v126, 0x42800000, v126
	v_mul_f32_e32 v132, 0x42800000, v204
	v_med3_f32 v126, v126, s17, v231
	v_med3_f32 v132, v132, s17, v231
	v_mov_b32_e32 v136, v137
	v_cvt_pk_fp8_f32 v136, v126, v132
	s_waitcnt vmcnt(0) lgkmcnt(0)
	v_mul_f32_e32 v133, 0x42800000, v208
	v_mul_f32_e32 v126, 0x42800000, v212
	v_med3_f32 v132, v133, s17, v231
	v_med3_f32 v126, v126, s17, v231
	v_cvt_pk_fp8_f32 v136, v132, v126 op_sel:[0,0,1]
	v_mul_f32_e32 v126, 0x42800000, v127
	v_mul_f32_e32 v127, 0x42800000, v205
	v_med3_f32 v126, v126, s17, v231
	v_med3_f32 v127, v127, s17, v231
	v_mov_b32_e32 v133, v137
	v_cvt_pk_fp8_f32 v133, v126, v127
	v_mul_f32_e32 v132, 0x42800000, v209
	v_mul_f32_e32 v126, 0x42800000, v213
	v_med3_f32 v127, v132, s17, v231
	v_med3_f32 v126, v126, s17, v231
	v_cvt_pk_fp8_f32 v133, v127, v126 op_sel:[0,0,1]
	v_mul_f32_e32 v126, 0x42800000, v128
	v_mul_f32_e32 v127, 0x42800000, v206
	v_med3_f32 v126, v126, s17, v231
	v_med3_f32 v127, v127, s17, v231
	v_mov_b32_e32 v132, v137
	v_cvt_pk_fp8_f32 v132, v126, v127
	v_mul_f32_e32 v128, 0x42800000, v210
	v_mul_f32_e32 v126, 0x42800000, v214
	v_med3_f32 v127, v128, s17, v231
	v_med3_f32 v126, v126, s17, v231
	v_cvt_pk_fp8_f32 v132, v127, v126 op_sel:[0,0,1]
	v_mul_f32_e32 v126, 0x42800000, v129
	v_mul_f32_e32 v127, 0x42800000, v207
	v_med3_f32 v126, v126, s17, v231
	v_med3_f32 v127, v127, s17, v231
	v_mov_b32_e32 v129, v137
	v_cvt_pk_fp8_f32 v129, v126, v127
	v_mul_f32_e32 v128, 0x42800000, v211
	v_mul_f32_e32 v126, 0x42800000, v215
	v_med3_f32 v127, v128, s17, v231
	v_med3_f32 v126, v126, s17, v231
	v_cvt_pk_fp8_f32 v129, v127, v126 op_sel:[0,0,1]
	ds_write2_b32 v1, v152, v136 offset0:16 offset1:24
	ds_write2_b32 v1, v153, v133 offset0:49 offset1:57
	ds_write2_b32 v1, v154, v132 offset0:82 offset1:90
	ds_write2_b32 v1, v155, v129 offset0:115 offset1:123
	s_waitcnt lgkmcnt(0)
	v_lshl_add_u64 v[126:127], v[130:131], 0, s[70:71]
	v_add_u32_e32 v1, v225, v226
	v_lshl_add_u64 v[152:153], v[126:127], 0, v[148:149]
	ds_read2_b32 v[126:127], v1 offset1:1
	ds_read2_b32 v[128:129], v1 offset0:2 offset1:3
	v_or_b32_e32 v130, s10, v139
	v_mul_u32_u24_e32 v136, 0xb00, v130
	v_add_u32_e32 v130, 0x420, v1
	v_add_u32_e32 v132, 0x428, v1
	ds_read2_b32 v[130:131], v130 offset1:1
	ds_read2_b32 v[132:133], v132 offset1:1
	v_lshl_add_u64 v[154:155], v[152:153], 0, v[136:137]
	s_waitcnt lgkmcnt(2)
	global_store_dwordx4 v[154:155], v[126:129], off
	s_nop 1
	v_or_b32_e32 v126, s10, v227
	v_mul_u32_u24_e32 v136, 0xb00, v126
	v_lshl_add_u64 v[126:127], v[152:153], 0, v[136:137]
	s_waitcnt lgkmcnt(0)
	global_store_dwordx4 v[126:127], v[130:133], off
	v_add_u32_e32 v126, 0x840, v1
	v_add_u32_e32 v128, 0x848, v1
	v_or_b32_e32 v130, s10, v228
	ds_read2_b32 v[126:127], v126 offset1:1
	ds_read2_b32 v[128:129], v128 offset1:1
	v_mul_u32_u24_e32 v136, 0xb00, v130
	v_add_u32_e32 v130, 0xc60, v1
	v_add_u32_e32 v1, 0xc68, v1
	ds_read2_b32 v[130:131], v130 offset1:1
	ds_read2_b32 v[132:133], v1 offset1:1
	v_or_b32_e32 v1, s10, v229
	v_lshl_add_u64 v[154:155], v[152:153], 0, v[136:137]
	v_mul_u32_u24_e32 v136, 0xb00, v1
	s_waitcnt lgkmcnt(2)
	global_store_dwordx4 v[154:155], v[126:129], off
	s_nop 1
	v_lshl_add_u64 v[126:127], v[152:153], 0, v[136:137]
	s_waitcnt lgkmcnt(0)
	global_store_dwordx4 v[126:127], v[130:133], off
	s_waitcnt lgkmcnt(0)

; __device__ __forceinline__ void cvt_item8(const float* src, int ld, int k0, int c0, unsigned char* dst, int Kd, int drow0, unsigned char* scr, int lane) {
;     const int c = lane & 7, q = lane >> 3;
;     f32x4 v[4][4];
; #pragma unroll
;     for (int g = 0; g < 4; ++g)
; #pragma unroll
;         for (int j = 0; j < 4; ++j) v[g][j] = __builtin_nontemporal_load((const f32x4*)(src + (size_t)(k0 + 32 * g + 4 * q + j) * ld + c0 + 4 * c));
; #pragma unroll
;     for (int g = 0; g < 4; ++g)
; #pragma unroll
;         for (int i = 0; i < 4; ++i) *(unsigned*)(scr + (4 * c + i) * 132 + 32 * g + 4 * q) = pg8::pack_fp8x4(v[g][0][i] * WSC, v[g][1][i] * WSC, v[g][2][i] * WSC, v[g][3][i] * WSC);
; template <int GRP>
; __device__ __forceinline__ void conv_item(Frame& F, int r) {
;     ...
;         if (r < CI_WO) { const int kb = r / 64, nb = r % 64;
;             cvt_item8(inptr(F, IN_WOUT) + (size_t)l * D * D, D, kb * 128, nb * 32, ws + WS_WOUT + (size_t)l * D * D, D, nb * 32, scr, F.lane); return; }
.LBB0_449:
	s_andn2_b64 vcc, exec, s[10:11]
	s_cbranch_vccnz .LBB0_433
	s_ashr_i32 s10, s23, 31
	v_mov_b32_e32 v1, s6
	s_lshr_b32 s10, s10, 26
	s_waitcnt lgkmcnt(3)
	ds_read_b64 v[126:127], v1
	s_add_i32 s10, s23, s10
	s_and_b32 s11, s10, 0x7ffffc0
	s_sub_i32 s11, s23, s11
	s_lshl_b32 s10, s10, 1
	s_and_b32 s14, s10, 0xffffff80
	s_lshl_b32 s10, s11, 5
	s_ashr_i32 s11, s10, 31
	s_waitcnt lgkmcnt(0)
	v_readfirstlane_b32 s15, v126
	s_lshl_b64 s[20:21], s[10:11], 2
	v_readfirstlane_b32 s23, v127
	s_add_u32 s20, s15, s20
	v_or_b32_e32 v192, s14, v143
	s_addc_u32 s21, s23, s21
	v_lshlrev_b32_e32 v136, 2, v146
	v_lshl_add_u64 v[126:127], s[20:21], 0, v[136:137]
	s_mov_b64 s[20:21], 0x1000000
	v_ashrrev_i32_e32 v193, 31, v192
	v_or_b32_e32 v128, 1, v192
	v_lshl_add_u64 v[204:205], v[126:127], 0, s[20:21]
	v_lshlrev_b64 v[126:127], 13, v[192:193]
	v_ashrrev_i32_e32 v129, 31, v128
	v_lshl_add_u64 v[126:127], v[204:205], 0, v[126:127]
	v_lshlrev_b64 v[128:129], 13, v[128:129]
	v_lshl_add_u64 v[128:129], v[204:205], 0, v[128:129]
	global_load_dwordx4 v[152:155], v[126:127], off nt
	global_load_dwordx4 v[156:159], v[128:129], off nt
	v_or_b32_e32 v126, 2, v192
	v_ashrrev_i32_e32 v127, 31, v126
	v_lshlrev_b64 v[126:127], 13, v[126:127]
	v_lshl_add_u64 v[126:127], v[204:205], 0, v[126:127]
	global_load_dwordx4 v[160:163], v[126:127], off nt
	v_or_b32_e32 v126, 3, v192
	v_ashrrev_i32_e32 v127, 31, v126
	v_lshlrev_b64 v[126:127], 13, v[126:127]
	v_lshl_add_u64 v[126:127], v[204:205], 0, v[126:127]
	global_load_dwordx4 v[164:167], v[126:127], off nt
	v_or_b32_e32 v126, 32, v192
	v_ashrrev_i32_e32 v127, 31, v126
	v_or_b32_e32 v128, 33, v192
	v_lshlrev_b64 v[126:127], 13, v[126:127]
	v_ashrrev_i32_e32 v129, 31, v128
	v_lshl_add_u64 v[126:127], v[204:205], 0, v[126:127]
	v_lshlrev_b64 v[128:129], 13, v[128:129]
	v_lshl_add_u64 v[128:129], v[204:205], 0, v[128:129]
	global_load_dwordx4 v[168:171], v[126:127], off nt
	global_load_dwordx4 v[172:175], v[128:129], off nt
	v_or_b32_e32 v126, 34, v192
	v_ashrrev_i32_e32 v127, 31, v126
	v_or_b32_e32 v128, 35, v192
	v_lshlrev_b64 v[126:127], 13, v[126:127]
	v_ashrrev_i32_e32 v129, 31, v128
	v_lshl_add_u64 v[126:127], v[204:205], 0, v[126:127]
	v_lshlrev_b64 v[128:129], 13, v[128:129]
	v_lshl_add_u64 v[128:129], v[204:205], 0, v[128:129]
	global_load_dwordx4 v[176:179], v[126:127], off nt
	global_load_dwordx4 v[180:183], v[128:129], off nt
	v_or_b32_e32 v126, 64, v192
	v_ashrrev_i32_e32 v127, 31, v126
	v_or_b32_e32 v128, 0x41, v192
	v_lshlrev_b64 v[126:127], 13, v[126:127]
	v_ashrrev_i32_e32 v129, 31, v128
	v_lshl_add_u64 v[126:127], v[204:205], 0, v[126:127]
	v_lshlrev_b64 v[128:129], 13, v[128:129]
	v_lshl_add_u64 v[128:129], v[204:205], 0, v[128:129]
	global_load_dwordx4 v[184:187], v[126:127], off nt
	global_load_dwordx4 v[188:191], v[128:129], off nt
	v_or_b32_e32 v126, 0x42, v192
	v_ashrrev_i32_e32 v127, 31, v126
	v_or_b32_e32 v128, 0x43, v192
	v_lshlrev_b64 v[126:127], 13, v[126:127]
	v_ashrrev_i32_e32 v129, 31, v128
	v_lshl_add_u64 v[126:127], v[204:205], 0, v[126:127]
	v_lshlrev_b64 v[128:129], 13, v[128:129]
	v_lshl_add_u64 v[128:129], v[204:205], 0, v[128:129]
	global_load_dwordx4 v[196:199], v[126:127], off nt
	global_load_dwordx4 v[200:203], v[128:129], off nt
	v_or_b32_e32 v126, 0x60, v192
	v_or_b32_e32 v128, 0x61, v192
	v_ashrrev_i32_e32 v127, 31, v126
	v_ashrrev_i32_e32 v129, 31, v128
	v_lshlrev_b64 v[126:127], 13, v[126:127]
	v_lshlrev_b64 v[128:129], 13, v[128:129]
	v_lshl_add_u64 v[126:127], v[204:205], 0, v[126:127]
	v_lshl_add_u64 v[130:131], v[204:205], 0, v[128:129]
	global_load_dwordx4 v[126:129], v[126:127], off nt
	s_nop 0
	global_load_dwordx4 v[130:133], v[130:131], off nt
	v_or_b32_e32 v206, 0x62, v192
	v_ashrrev_i32_e32 v207, 31, v206
	v_or_b32_e32 v192, 0x63, v192
	v_lshlrev_b64 v[206:207], 13, v[206:207]
	v_ashrrev_i32_e32 v193, 31, v192
	v_lshl_add_u64 v[206:207], v[204:205], 0, v[206:207]
	v_lshlrev_b64 v[192:193], 13, v[192:193]
	v_lshl_add_u64 v[192:193], v[204:205], 0, v[192:193]
	global_load_dwordx4 v[204:207], v[206:207], off nt
	s_nop 0
	global_load_dwordx4 v[208:211], v[192:193], off nt
	s_ashr_i32 s15, s14, 31
	s_waitcnt vmcnt(0) lgkmcnt(0)
	v_mul_f32_e32 v1, 0x42800000, v152
	v_mul_f32_e32 v136, 0x42800000, v156
	v_med3_f32 v1, v1, s17, v231
	v_med3_f32 v136, v136, s17, v231
	v_mov_b32_e32 v156, v137
	v_cvt_pk_fp8_f32 v156, v1, v136
	v_mul_f32_e32 v152, 0x42800000, v160
	v_med3_f32 v136, v152, s17, v231
	v_mul_f32_e32 v152, 0x42800000, v157
	v_med3_f32 v152, v152, s17, v231
	v_mov_b32_e32 v157, v137
	v_mul_f32_e32 v1, 0x42800000, v164
	v_med3_f32 v1, v1, s17, v231
	v_cvt_pk_fp8_f32 v156, v136, v1 op_sel:[0,0,1]
	v_mul_f32_e32 v136, 0x42800000, v153
	v_med3_f32 v136, v136, s17, v231
	v_cvt_pk_fp8_f32 v157, v136, v152
	v_mul_f32_e32 v153, 0x42800000, v161
	v_mul_f32_e32 v136, 0x42800000, v165
	v_med3_f32 v152, v153, s17, v231
	v_med3_f32 v136, v136, s17, v231
	v_cvt_pk_fp8_f32 v157, v152, v136 op_sel:[0,0,1]
	v_mul_f32_e32 v136, 0x42800000, v154
	v_mul_f32_e32 v152, 0x42800000, v158
	v_med3_f32 v136, v136, s17, v231
	v_med3_f32 v152, v152, s17, v231
	v_mov_b32_e32 v154, v137
	v_cvt_pk_fp8_f32 v154, v136, v152
	v_mul_f32_e32 v153, 0x42800000, v162
	v_mul_f32_e32 v136, 0x42800000, v166
	v_med3_f32 v152, v153, s17, v231
	v_med3_f32 v136, v136, s17, v231
	v_cvt_pk_fp8_f32 v154, v152, v136 op_sel:[0,0,1]
	v_mul_f32_e32 v136, 0x42800000, v155
	v_mul_f32_e32 v152, 0x42800000, v159
	v_med3_f32 v136, v136, s17, v231
	v_med3_f32 v152, v152, s17, v231
	v_mov_b32_e32 v155, v137
	v_cvt_pk_fp8_f32 v155, v136, v152
	v_mul_f32_e32 v153, 0x42800000, v163
	v_mul_f32_e32 v136, 0x42800000, v167
; __device__ __forceinline__ void cvt_item8(const float* src, int ld, int k0, int c0, unsigned char* dst, int Kd, int drow0, unsigned char* scr, int lane) {
;     ...
;     for (int g = 0; g < 4; ++g)
; #pragma unroll
;         for (int i = 0; i < 4; ++i) *(unsigned*)(scr + (4 * c + i) * 132 + 32 * g + 4 * q) = pg8::pack_fp8x4(v[g][0][i] * WSC, v[g][1][i] * WSC, v[g][2][i] * WSC, v[g][3][i] * WSC);
;     asm volatile("s_waitcnt lgkmcnt(0)" ::: "memory");
; #pragma unroll
;     for (int r = 0; r < 4; ++r) { const int n = 8 * r + (lane >> 3), ch = lane & 7; const unsigned char* p = scr + n * 132 + ch * 16;
;         u32x4 o; o.x = *(const unsigned*)(p); o.y = *(const unsigned*)(p + 4); o.z = *(const unsigned*)(p + 8); o.w = *(const unsigned*)(p + 12);
;         *(u32x4*)(dst + (size_t)(drow0 + n) * Kd + k0 + 16 * ch) = o; }
;     asm volatile("s_waitcnt lgkmcnt(0)" ::: "memory");
	v_med3_f32 v152, v153, s17, v231
	v_med3_f32 v136, v136, s17, v231
	v_cvt_pk_fp8_f32 v155, v152, v136 op_sel:[0,0,1]
	v_mul_f32_e32 v136, 0x42800000, v168
	v_mul_f32_e32 v152, 0x42800000, v172
	v_med3_f32 v136, v136, s17, v231
	v_med3_f32 v152, v152, s17, v231
	v_mov_b32_e32 v158, v137
	v_cvt_pk_fp8_f32 v158, v136, v152
	v_mul_f32_e32 v153, 0x42800000, v176
	v_mul_f32_e32 v136, 0x42800000, v180
	v_med3_f32 v152, v153, s17, v231
	v_med3_f32 v136, v136, s17, v231
	v_cvt_pk_fp8_f32 v158, v152, v136 op_sel:[0,0,1]
	v_mul_f32_e32 v136, 0x42800000, v169
	v_mul_f32_e32 v152, 0x42800000, v173
	v_med3_f32 v136, v136, s17, v231
	v_med3_f32 v152, v152, s17, v231
	v_mov_b32_e32 v159, v137
	v_cvt_pk_fp8_f32 v159, v136, v152
	v_mul_f32_e32 v153, 0x42800000, v177
	v_mul_f32_e32 v136, 0x42800000, v181
	v_med3_f32 v152, v153, s17, v231
	v_med3_f32 v136, v136, s17, v231
	v_cvt_pk_fp8_f32 v159, v152, v136 op_sel:[0,0,1]
	v_mul_f32_e32 v136, 0x42800000, v170
	v_mul_f32_e32 v152, 0x42800000, v174
	v_med3_f32 v136, v136, s17, v231
	v_med3_f32 v152, v152, s17, v231
	v_mov_b32_e32 v160, v137
	v_cvt_pk_fp8_f32 v160, v136, v152
	v_mul_f32_e32 v153, 0x42800000, v178
	v_mul_f32_e32 v136, 0x42800000, v182
	v_med3_f32 v152, v153, s17, v231
	v_med3_f32 v136, v136, s17, v231
	v_cvt_pk_fp8_f32 v160, v152, v136 op_sel:[0,0,1]
	v_mul_f32_e32 v136, 0x42800000, v171
	v_mul_f32_e32 v152, 0x42800000, v175
	v_med3_f32 v136, v136, s17, v231
	v_med3_f32 v152, v152, s17, v231
	v_mov_b32_e32 v161, v137
	v_cvt_pk_fp8_f32 v161, v136, v152
	v_mul_f32_e32 v153, 0x42800000, v179
	v_mul_f32_e32 v136, 0x42800000, v183
	v_med3_f32 v152, v153, s17, v231
	v_med3_f32 v136, v136, s17, v231
	v_add_u32_e32 v1, v147, v224
	v_cvt_pk_fp8_f32 v161, v152, v136 op_sel:[0,0,1]
	v_mul_f32_e32 v136, 0x42800000, v184
	v_mul_f32_e32 v152, 0x42800000, v188
	ds_write2_b32 v1, v156, v158 offset1:8
	ds_write2_b32 v1, v157, v159 offset0:33 offset1:41
	ds_write2_b32 v1, v154, v160 offset0:66 offset1:74
	ds_write2_b32 v1, v155, v161 offset0:99 offset1:107
	v_med3_f32 v136, v136, s17, v231
	v_med3_f32 v152, v152, s17, v231
	v_mov_b32_e32 v154, v137
	v_cvt_pk_fp8_f32 v154, v136, v152
	v_mul_f32_e32 v153, 0x42800000, v196
	v_mul_f32_e32 v136, 0x42800000, v200
	v_med3_f32 v152, v153, s17, v231
	v_med3_f32 v136, v136, s17, v231
	v_cvt_pk_fp8_f32 v154, v152, v136 op_sel:[0,0,1]
	v_mul_f32_e32 v136, 0x42800000, v185
	v_mul_f32_e32 v152, 0x42800000, v189
	v_med3_f32 v136, v136, s17, v231
	v_med3_f32 v152, v152, s17, v231
	v_mov_b32_e32 v155, v137
	v_cvt_pk_fp8_f32 v155, v136, v152
	v_mul_f32_e32 v153, 0x42800000, v197
	v_mul_f32_e32 v136, 0x42800000, v201
	v_med3_f32 v152, v153, s17, v231
	v_med3_f32 v136, v136, s17, v231
	v_cvt_pk_fp8_f32 v155, v152, v136 op_sel:[0,0,1]
	v_mul_f32_e32 v136, 0x42800000, v186
	v_mul_f32_e32 v152, 0x42800000, v190
	v_med3_f32 v136, v136, s17, v231
	v_med3_f32 v152, v152, s17, v231
	v_mov_b32_e32 v156, v137
	v_cvt_pk_fp8_f32 v156, v136, v152
	v_mul_f32_e32 v153, 0x42800000, v198
	v_mul_f32_e32 v136, 0x42800000, v202
	v_med3_f32 v152, v153, s17, v231
	v_med3_f32 v136, v136, s17, v231
	v_cvt_pk_fp8_f32 v156, v152, v136 op_sel:[0,0,1]
	v_mul_f32_e32 v136, 0x42800000, v187
	v_mul_f32_e32 v152, 0x42800000, v191
	v_med3_f32 v136, v136, s17, v231
	v_med3_f32 v152, v152, s17, v231
	v_mov_b32_e32 v157, v137
	v_cvt_pk_fp8_f32 v157, v136, v152
	v_mul_f32_e32 v153, 0x42800000, v199
	v_mul_f32_e32 v136, 0x42800000, v203
	v_med3_f32 v152, v153, s17, v231
	v_med3_f32 v136, v136, s17, v231
	v_mul_f32_e32 v126, 0x42800000, v126
	v_mul_f32_e32 v130, 0x42800000, v130
	v_cvt_pk_fp8_f32 v157, v152, v136 op_sel:[0,0,1]
	v_med3_f32 v126, v126, s17, v231
	v_med3_f32 v130, v130, s17, v231
	v_mov_b32_e32 v152, v137
	v_cvt_pk_fp8_f32 v152, v126, v130
	v_mul_f32_e32 v136, 0x42800000, v204
	v_mul_f32_e32 v126, 0x42800000, v208
	v_med3_f32 v130, v136, s17, v231
	v_med3_f32 v126, v126, s17, v231
	v_cvt_pk_fp8_f32 v152, v130, v126 op_sel:[0,0,1]
	v_mul_f32_e32 v126, 0x42800000, v127
	v_mul_f32_e32 v127, 0x42800000, v131
	v_med3_f32 v126, v126, s17, v231
	v_med3_f32 v127, v127, s17, v231
	v_mov_b32_e32 v131, v137
	v_cvt_pk_fp8_f32 v131, v126, v127
	v_mul_f32_e32 v130, 0x42800000, v205
	v_mul_f32_e32 v126, 0x42800000, v209
	v_med3_f32 v127, v130, s17, v231
	v_med3_f32 v126, v126, s17, v231
	v_cvt_pk_fp8_f32 v131, v127, v126 op_sel:[0,0,1]
	v_mul_f32_e32 v126, 0x42800000, v128
	v_mul_f32_e32 v127, 0x42800000, v132
	v_med3_f32 v126, v126, s17, v231
	v_med3_f32 v127, v127, s17, v231
	v_mov_b32_e32 v130, v137
	v_cvt_pk_fp8_f32 v130, v126, v127
	v_mul_f32_e32 v128, 0x42800000, v206
	v_mul_f32_e32 v126, 0x42800000, v210
	v_med3_f32 v127, v128, s17, v231
	v_med3_f32 v126, v126, s17, v231
	v_cvt_pk_fp8_f32 v130, v127, v126 op_sel:[0,0,1]
	v_mul_f32_e32 v126, 0x42800000, v129
	v_mul_f32_e32 v127, 0x42800000, v133
	v_med3_f32 v126, v126, s17, v231
	v_med3_f32 v127, v127, s17, v231
	v_mov_b32_e32 v129, v137
	v_cvt_pk_fp8_f32 v129, v126, v127
	v_mul_f32_e32 v128, 0x42800000, v207
	v_mul_f32_e32 v126, 0x42800000, v211
	v_med3_f32 v127, v128, s17, v231
	v_med3_f32 v126, v126, s17, v231
	v_cvt_pk_fp8_f32 v129, v127, v126 op_sel:[0,0,1]
	ds_write2_b32 v1, v154, v152 offset0:16 offset1:24
	ds_write2_b32 v1, v155, v131 offset0:49 offset1:57
	ds_write2_b32 v1, v156, v130 offset0:82 offset1:90
	ds_write2_b32 v1, v157, v129 offset0:115 offset1:123
	s_waitcnt lgkmcnt(0)
	v_add_u32_e32 v1, v225, v226
	ds_read2_b32 v[126:127], v1 offset1:1
	ds_read2_b32 v[128:129], v1 offset0:2 offset1:3
	v_or_b32_e32 v130, s10, v139
	v_ashrrev_i32_e32 v131, 31, v130
	v_lshl_add_u64 v[152:153], v[150:151], 0, s[14:15]
	v_lshlrev_b64 v[130:131], 11, v[130:131]
	v_lshl_add_u64 v[154:155], v[152:153], 0, v[130:131]
	v_add_u32_e32 v130, 0x420, v1
	v_add_u32_e32 v132, 0x428, v1
	ds_read2_b32 v[130:131], v130 offset1:1
	ds_read2_b32 v[132:133], v132 offset1:1
	s_waitcnt lgkmcnt(2)
	global_store_dwordx4 v[154:155], v[126:129], off
	s_nop 1
	v_or_b32_e32 v126, s10, v227
	v_ashrrev_i32_e32 v127, 31, v126
	v_lshlrev_b64 v[126:127], 11, v[126:127]
	v_lshl_add_u64 v[126:127], v[152:153], 0, v[126:127]
	s_waitcnt lgkmcnt(0)
	global_store_dwordx4 v[126:127], v[130:133], off
	v_add_u32_e32 v126, 0x840, v1
	v_add_u32_e32 v128, 0x848, v1
	ds_read2_b32 v[126:127], v126 offset1:1
	ds_read2_b32 v[128:129], v128 offset1:1
	v_or_b32_e32 v130, s10, v228
	v_ashrrev_i32_e32 v131, 31, v130
	v_lshlrev_b64 v[130:131], 11, v[130:131]
	v_lshl_add_u64 v[154:155], v[152:153], 0, v[130:131]
	v_add_u32_e32 v130, 0xc60, v1
	v_add_u32_e32 v1, 0xc68, v1
	ds_read2_b32 v[130:131], v130 offset1:1
	ds_read2_b32 v[132:133], v1 offset1:1
	s_waitcnt lgkmcnt(2)
	global_store_dwordx4 v[154:155], v[126:129], off
	s_nop 1
	v_or_b32_e32 v126, s10, v229
	v_ashrrev_i32_e32 v127, 31, v126
	v_lshlrev_b64 v[126:127], 11, v[126:127]
	v_lshl_add_u64 v[126:127], v[152:153], 0, v[126:127]
	s_waitcnt lgkmcnt(0)
	global_store_dwordx4 v[126:127], v[130:133], off
	s_waitcnt lgkmcnt(0)
	s_branch .LBB0_433

; __device__ __forceinline__ void colmax_item(const float* src, int ld, int k0, int c0, float* cmx  , int lane) {
;     const int c = lane & 7, q = lane >> 3;
;     f32x4 mx = (f32x4){0.f, 0.f, 0.f, 0.f};
; #pragma unroll
;     for (int g = 0; g < 4; ++g)
; #pragma unroll
;         for (int j = 0; j < 4; ++j) { const f32x4 v = *(const f32x4*)(src + (size_t)(k0 + 32 * g + 4 * q + j) * ld + c0 + 4 * c);
;             mx[0] = fmaxf(mx[0], fabsf(v[0])); mx[1] = fmaxf(mx[1], fabsf(v[1])); mx[2] = fmaxf(mx[2], fabsf(v[2])); mx[3] = fmaxf(mx[3], fabsf(v[3])); }
; #pragma unroll
;     for (int i = 0; i < 4; ++i) { float v = mx[i]; v = fmaxf(v, __shfl_xor(v, 8)); v = fmaxf(v, __shfl_xor(v, 16)); v = fmaxf(v, __shfl_xor(v, 32)); mx[i] = v; }
;     if (q == 0) {
; #pragma unroll
;         for (int i = 0; i < 4; ++i) atomicMax((unsigned*)(cmx + 4 * c + i), __float_as_uint(mx[i] * CMS_F)); }
; }
; template <int GRP>
; __device__ __forceinline__ void conv_item(Frame& F, int r) {
;     ...
;         if (r < NI) { const int kb = r / 152, nb = r % 152, c0 = (nb < 112) ? nb * 32 : SRC_GATE + 8 + (nb - 112) * 32, drow = nb * 32;
;             if (QUANT) cvt_item_i8(inptr(F, IN_WIN) + (size_t)l * D * NIN_SRC, NIN_SRC, kb * 128, c0, ws + WS_WIN + (size_t)l * NIN * D, D, drow, cmx + CMX_WIN + l * NIN + drow, scr, F.lane);
;             else colmax_item(inptr(F, IN_WIN) + (size_t)l * D * NIN_SRC, NIN_SRC, kb * 128, c0, cmx + CMX_WIN + l * NIN + drow, F.lane);
.LBB0_510:
	s_mul_hi_i32 s8, s3, 0x6bca1af3
	s_lshr_b32 s18, s8, 31
	s_ashr_i32 s8, s8, 6
	s_add_i32 s8, s8, s18
	s_mul_i32 s18, s8, 0xffffff68
	s_add_i32 s19, s3, s18
	s_mul_i32 s18, s8, 0xffffed00
	v_mov_b32_e32 v1, s23
	s_add_i32 s18, s4, s18
	s_waitcnt lgkmcnt(3)
	ds_read_b64 v[2:3], v1
	s_add_i32 s20, s18, 8
	s_cmpk_lt_i32 s19, 0x70
	s_cselect_b32 s20, s18, s20
	s_ashr_i32 s21, s20, 31
	s_waitcnt lgkmcnt(0)
	v_readfirstlane_b32 s19, v2
	s_lshl_b64 s[20:21], s[20:21], 2
	v_readfirstlane_b32 s69, v3
	s_add_u32 s20, s19, s20
	s_addc_u32 s21, s69, s21
	v_lshl_or_b32 v1, s8, 7, v15
	v_lshl_add_u64 v[2:3], s[20:21], 0, v[10:11]
	s_mov_b64 s[20:21], 0x2610000
	v_lshl_add_u64 v[38:39], v[2:3], 0, s[20:21]
	v_or_b32_e32 v6, 1, v1
	v_mad_i64_i32 v[2:3], s[20:21], v1, s24, v[38:39]
	v_mad_i64_i32 v[6:7], s[20:21], v6, s24, v[38:39]
	global_load_dwordx4 v[2:5], v[2:3], off
	v_cmp_lt_i32_e32 vcc, v31, v32
	global_load_dwordx4 v[6:9], v[6:7], off
	s_waitcnt vmcnt(0) lgkmcnt(0)
	v_max3_f32 v40, |v2|, 0, |v6|
	v_or_b32_e32 v2, 2, v1
	v_or_b32_e32 v6, 3, v1
	v_max3_f32 v41, |v3|, 0, |v7|
	v_mad_i64_i32 v[2:3], s[20:21], v2, s24, v[38:39]
	v_mad_i64_i32 v[6:7], s[20:21], v6, s24, v[38:39]
	v_max3_f32 v42, |v4|, 0, |v8|
	v_max3_f32 v43, |v5|, 0, |v9|
	global_load_dwordx4 v[2:5], v[2:3], off
	s_nop 0
	global_load_dwordx4 v[6:9], v[6:7], off
	s_waitcnt vmcnt(0) lgkmcnt(0)
	v_max3_f32 v40, v40, |v2|, |v6|
	v_or_b32_e32 v2, 32, v1
	v_or_b32_e32 v6, 33, v1
	v_max3_f32 v41, v41, |v3|, |v7|
	v_mad_i64_i32 v[2:3], s[20:21], v2, s24, v[38:39]
	v_mad_i64_i32 v[6:7], s[20:21], v6, s24, v[38:39]
	v_max3_f32 v42, v42, |v4|, |v8|
	v_max3_f32 v43, v43, |v5|, |v9|
	global_load_dwordx4 v[2:5], v[2:3], off
	s_nop 0
	global_load_dwordx4 v[6:9], v[6:7], off
	s_waitcnt vmcnt(0) lgkmcnt(0)
	v_max3_f32 v40, v40, |v2|, |v6|
	v_or_b32_e32 v2, 34, v1
	v_or_b32_e32 v6, 35, v1
	v_max3_f32 v41, v41, |v3|, |v7|
	v_mad_i64_i32 v[2:3], s[20:21], v2, s24, v[38:39]
	v_mad_i64_i32 v[6:7], s[20:21], v6, s24, v[38:39]
	v_max3_f32 v42, v42, |v4|, |v8|
	v_max3_f32 v43, v43, |v5|, |v9|
	global_load_dwordx4 v[2:5], v[2:3], off
	s_nop 0
	global_load_dwordx4 v[6:9], v[6:7], off
	s_waitcnt vmcnt(0) lgkmcnt(0)
	v_max3_f32 v40, v40, |v2|, |v6|
	v_or_b32_e32 v2, 64, v1
	v_or_b32_e32 v6, 0x41, v1
	v_max3_f32 v41, v41, |v3|, |v7|
	v_mad_i64_i32 v[2:3], s[20:21], v2, s24, v[38:39]
	v_mad_i64_i32 v[6:7], s[20:21], v6, s24, v[38:39]
	v_max3_f32 v42, v42, |v4|, |v8|
	v_max3_f32 v43, v43, |v5|, |v9|
	global_load_dwordx4 v[2:5], v[2:3], off
	s_nop 0
	global_load_dwordx4 v[6:9], v[6:7], off
	s_waitcnt vmcnt(0) lgkmcnt(0)
	v_max3_f32 v40, v40, |v2|, |v6|
	v_or_b32_e32 v2, 0x42, v1
	v_or_b32_e32 v6, 0x43, v1
	v_max3_f32 v41, v41, |v3|, |v7|
	v_mad_i64_i32 v[2:3], s[20:21], v2, s24, v[38:39]
	v_mad_i64_i32 v[6:7], s[20:21], v6, s24, v[38:39]
	v_max3_f32 v42, v42, |v4|, |v8|
	v_max3_f32 v43, v43, |v5|, |v9|
	global_load_dwordx4 v[2:5], v[2:3], off
	s_nop 0
	global_load_dwordx4 v[6:9], v[6:7], off
	s_waitcnt vmcnt(0) lgkmcnt(0)
	v_max3_f32 v40, v40, |v2|, |v6|
	v_or_b32_e32 v2, 0x60, v1
	v_or_b32_e32 v6, 0x61, v1
	v_max3_f32 v41, v41, |v3|, |v7|
	v_mad_i64_i32 v[2:3], s[20:21], v2, s24, v[38:39]
	v_mad_i64_i32 v[6:7], s[20:21], v6, s24, v[38:39]
	v_max3_f32 v42, v42, |v4|, |v8|
	v_max3_f32 v43, v43, |v5|, |v9|
	global_load_dwordx4 v[2:5], v[2:3], off
	s_nop 0
	global_load_dwordx4 v[6:9], v[6:7], off
	s_waitcnt vmcnt(0) lgkmcnt(0)
	v_max3_f32 v40, v40, |v2|, |v6|
	v_or_b32_e32 v2, 0x62, v1
	v_or_b32_e32 v1, 0x63, v1
	v_max3_f32 v41, v41, |v3|, |v7|
	v_mad_i64_i32 v[2:3], s[20:21], v2, s24, v[38:39]
	v_mad_i64_i32 v[6:7], s[20:21], v1, s24, v[38:39]
	v_max3_f32 v42, v42, |v4|, |v8|
	v_max3_f32 v43, v43, |v5|, |v9|
	global_load_dwordx4 v[2:5], v[2:3], off
	s_nop 0
	global_load_dwordx4 v[6:9], v[6:7], off
	s_waitcnt vmcnt(0) lgkmcnt(0)
	v_max3_f32 v1, v40, |v2|, |v6|
	v_cndmask_b32_e32 v2, v30, v31, vcc
	v_cmp_lt_i32_e32 vcc, v33, v32
	v_max3_f32 v6, v42, |v4|, |v8|
	v_lshlrev_b32_e32 v8, 2, v2
	v_cndmask_b32_e32 v2, v30, v33, vcc
	v_cmp_lt_i32_e32 vcc, v34, v32
	v_max3_f32 v3, v41, |v3|, |v7|
	v_max3_f32 v7, v43, |v5|, |v9|
	v_lshlrev_b32_e32 v9, 2, v2
	v_cndmask_b32_e32 v2, v30, v34, vcc
	v_lshlrev_b32_e32 v38, 2, v2
	ds_bpermute_b32 v2, v8, v1
	ds_bpermute_b32 v4, v8, v3
	ds_bpermute_b32 v5, v8, v6
	ds_bpermute_b32 v8, v8, v7
	s_waitcnt lgkmcnt(3)
	v_max_f32_e32 v2, v2, v2
	s_waitcnt lgkmcnt(2)
	v_max_f32_e32 v4, v4, v4
	s_waitcnt lgkmcnt(1)
	v_max_f32_e32 v5, v5, v5
	s_waitcnt lgkmcnt(0)
	v_max_f32_e32 v8, v8, v8
	v_max_f32_e32 v1, v1, v2
	v_max_f32_e32 v3, v3, v4
	v_max_f32_e32 v5, v6, v5
	v_max_f32_e32 v7, v7, v8
	ds_bpermute_b32 v2, v9, v1
	ds_bpermute_b32 v4, v9, v3
	ds_bpermute_b32 v6, v9, v5
	ds_bpermute_b32 v8, v9, v7
	s_waitcnt lgkmcnt(3)
	v_max_f32_e32 v2, v2, v2
	s_waitcnt lgkmcnt(2)
	v_max_f32_e32 v4, v4, v4
	s_waitcnt lgkmcnt(1)
	v_max_f32_e32 v6, v6, v6
	s_waitcnt lgkmcnt(0)
	v_max_f32_e32 v8, v8, v8
	v_max_f32_e32 v1, v1, v2
	v_max_f32_e32 v3, v3, v4
	v_max_f32_e32 v5, v5, v6
	v_max_f32_e32 v7, v7, v8
	ds_bpermute_b32 v2, v38, v1
	ds_bpermute_b32 v4, v38, v3
	ds_bpermute_b32 v6, v38, v5
	ds_bpermute_b32 v8, v38, v7
	s_and_saveexec_b64 s[20:21], s[6:7]
	s_cbranch_execz .LBB0_512
	s_waitcnt lgkmcnt(3)
	v_max_f32_e32 v2, v2, v2
	v_max_f32_e32 v1, v1, v1
	s_ashr_i32 s19, s18, 31
	s_waitcnt lgkmcnt(2)
	v_max_f32_e32 v4, v4, v4
	v_max_f32_e32 v3, v3, v3
	v_max_f32_e32 v1, v1, v2
	s_waitcnt lgkmcnt(1)
	v_max_f32_e32 v6, v6, v6
	v_max_f32_e32 v5, v5, v5
	v_max_f32_e32 v4, v3, v4
	v_lshl_add_u64 v[2:3], s[18:19], 2, v[12:13]
	v_mul_f32_e32 v1, 0x3fb33333, v1
	s_waitcnt lgkmcnt(0)
	v_max_f32_e32 v8, v8, v8
	v_max_f32_e32 v7, v7, v7
	v_max_f32_e32 v5, v5, v6
	global_atomic_umax v[2:3], v1, off
	v_mul_f32_e32 v1, 0x3fb33333, v4
	v_max_f32_e32 v7, v7, v8
	global_atomic_umax v[2:3], v1, off offset:4
	v_mul_f32_e32 v1, 0x3fb33333, v5
	global_atomic_umax v[2:3], v1, off offset:8
	v_mul_f32_e32 v1, 0x3fb33333, v7
	global_atomic_umax v[2:3], v1, off offset:12

; __device__ __forceinline__ void colmax_item(const float* src, int ld, int k0, int c0, float* cmx  , int lane) {
;     const int c = lane & 7, q = lane >> 3;
;     f32x4 mx = (f32x4){0.f, 0.f, 0.f, 0.f};
; #pragma unroll
;     for (int g = 0; g < 4; ++g)
; #pragma unroll
;         for (int j = 0; j < 4; ++j) { const f32x4 v = *(const f32x4*)(src + (size_t)(k0 + 32 * g + 4 * q + j) * ld + c0 + 4 * c);
;             mx[0] = fmaxf(mx[0], fabsf(v[0])); mx[1] = fmaxf(mx[1], fabsf(v[1])); mx[2] = fmaxf(mx[2], fabsf(v[2])); mx[3] = fmaxf(mx[3], fabsf(v[3])); }
; #pragma unroll
;     for (int i = 0; i < 4; ++i) { float v = mx[i]; v = fmaxf(v, __shfl_xor(v, 8)); v = fmaxf(v, __shfl_xor(v, 16)); v = fmaxf(v, __shfl_xor(v, 32)); mx[i] = v; }
; template <int GRP>
; __device__ __forceinline__ void conv_item(Frame& F, int r) {
;     ...
;     else { constexpr int KBN = (GRP == 3) ? 16 : CMS_KB, I_E = KBN * 88; const int up = r / (8 * I_E); r %= (8 * I_E); const int e = r / I_E; r %= I_E; const int kb = r / 88, nb = r % 88, n0 = nb * 32, drow = (n0 >> 7) * 256 + up * 128 + (n0 & 127);
;         if (GRP == 3) cvt_item_i8(inptr(F, up ? IN_MU : IN_MG) + (size_t)e * D * DFE, DFE, kb * 128, n0, ws + WS_MGU + (size_t)e * 2 * DFE * D, D, drow, cmx + 2 * DFF + e * 2 * DFE + drow, scr, F.lane);
;         else colmax_item(inptr(F, up ? IN_MU : IN_MG) + (size_t)e * D * DFE, DFE, kb * 128, n0, cmx + 2 * DFF + e * 2 * DFE + drow, F.lane); }
.LBB0_514:
	s_cmpk_gt_i32 s20, 0x3ff
	s_mov_b64 s[16:17], -1
	s_cbranch_scc0 .LBB0_522
	s_cmpk_gt_u32 s20, 0x2fff
	s_cbranch_scc0 .LBB0_519
	s_add_i32 s8, s20, 0xffffd000
	s_add_i32 s16, s20, 0xca80
	s_cmpk_lt_u32 s8, 0x580
	s_cselect_b32 s16, s8, s16
	s_and_b32 s17, s16, 0xffff
	s_mul_i32 s17, s17, 0xba2f
	s_lshr_b32 s21, s17, 23
	s_mul_i32 s17, s21, 0xb0
	s_sub_i32 s16, s16, s17
	s_and_b32 s17, s16, 0xffff
	s_add_i32 s16, s17, 0xffffffa8
	s_min_u32 s69, s17, s16
	s_lshl_b32 s16, s69, 5
	s_cmpk_lt_u32 s20, 0x3580
	s_cselect_b32 s18, s25, 0xa8
	s_add_i32 s18, s18, 0
	s_add_i32 s18, s18, 0x20200
	v_mov_b32_e32 v1, s18
	s_waitcnt lgkmcnt(3)
	ds_read_b64 v[2:3], v1
	s_cmpk_gt_u32 s17, 0x57
	s_cselect_b32 s17, 0x80, 0
	v_or_b32_e32 v1, s17, v15
	s_ashr_i32 s17, s16, 31
	s_waitcnt lgkmcnt(0)
	v_readfirstlane_b32 s18, v2
	v_readfirstlane_b32 s19, v3
	v_mul_u32_u24_e32 v2, s21, v35
	v_mov_b32_e32 v3, v11
	v_lshlrev_b64 v[2:3], 2, v[2:3]
	v_lshl_add_u64 v[2:3], s[18:19], 0, v[2:3]
	s_lshl_b64 s[18:19], s[16:17], 2
	v_lshl_add_u64 v[2:3], v[2:3], 0, s[18:19]
	v_lshl_add_u64 v[2:3], v[2:3], 0, v[10:11]
	v_mul_u32_u24_e32 v4, 0x2c00, v1
	v_mov_b32_e32 v5, v11
	v_lshl_add_u64 v[2:3], v[2:3], 0, v[4:5]
	v_add_co_u32_e32 v8, vcc, s26, v2
	global_load_dwordx4 v[4:7], v[2:3], off
	s_nop 0
	v_addc_co_u32_e32 v9, vcc, 0, v3, vcc
	global_load_dwordx4 v[38:41], v[8:9], off offset:3072
	s_waitcnt vmcnt(0) lgkmcnt(0)
	v_max3_f32 v1, |v4|, 0, |v38|
	v_add_co_u32_e32 v4, vcc, s27, v2
	v_max3_f32 v42, |v5|, 0, |v39|
	s_nop 0
	v_addc_co_u32_e32 v5, vcc, 0, v3, vcc
	v_add_co_u32_e32 v8, vcc, s28, v2
	v_max3_f32 v43, |v6|, 0, |v40|
	s_nop 0
	v_addc_co_u32_e32 v9, vcc, 0, v3, vcc
	v_max3_f32 v44, |v7|, 0, |v41|
	global_load_dwordx4 v[4:7], v[4:5], off offset:2048
	s_nop 0
	global_load_dwordx4 v[38:41], v[8:9], off offset:1024
	s_waitcnt vmcnt(0) lgkmcnt(0)
	v_max3_f32 v1, v1, |v4|, |v38|
	v_add_co_u32_e32 v4, vcc, s29, v2
	v_max3_f32 v42, v42, |v5|, |v39|
	s_nop 0
	v_addc_co_u32_e32 v5, vcc, 0, v3, vcc
	v_add_co_u32_e32 v8, vcc, s30, v2
	v_max3_f32 v43, v43, |v6|, |v40|
	s_nop 0
	v_addc_co_u32_e32 v9, vcc, 0, v3, vcc
	v_max3_f32 v44, v44, |v7|, |v41|
	global_load_dwordx4 v[4:7], v[4:5], off
	s_nop 0
	global_load_dwordx4 v[38:41], v[8:9], off offset:3072
	s_waitcnt vmcnt(0) lgkmcnt(0)
	v_max3_f32 v1, v1, |v4|, |v38|
	v_add_co_u32_e32 v4, vcc, s31, v2
	v_max3_f32 v42, v42, |v5|, |v39|
	s_nop 0
	v_addc_co_u32_e32 v5, vcc, 0, v3, vcc
	v_add_co_u32_e32 v8, vcc, s34, v2
	v_max3_f32 v43, v43, |v6|, |v40|
	s_nop 0
	v_addc_co_u32_e32 v9, vcc, 0, v3, vcc
	v_max3_f32 v44, v44, |v7|, |v41|
	global_load_dwordx4 v[4:7], v[4:5], off offset:2048
	s_nop 0
	global_load_dwordx4 v[38:41], v[8:9], off offset:1024
	s_waitcnt vmcnt(0) lgkmcnt(0)
	v_max3_f32 v1, v1, |v4|, |v38|
	v_add_co_u32_e32 v4, vcc, s35, v2
	v_max3_f32 v42, v42, |v5|, |v39|
	s_nop 0
	v_addc_co_u32_e32 v5, vcc, 0, v3, vcc
	v_add_co_u32_e32 v8, vcc, s36, v2
	v_max3_f32 v43, v43, |v6|, |v40|
	s_nop 0
	v_addc_co_u32_e32 v9, vcc, 0, v3, vcc
	v_max3_f32 v44, v44, |v7|, |v41|
	global_load_dwordx4 v[4:7], v[4:5], off
	s_nop 0
	global_load_dwordx4 v[38:41], v[8:9], off offset:3072
	s_waitcnt vmcnt(0) lgkmcnt(0)
	v_max3_f32 v1, v1, |v4|, |v38|
	v_add_co_u32_e32 v4, vcc, s37, v2
	v_max3_f32 v42, v42, |v5|, |v39|
	s_nop 0
	v_addc_co_u32_e32 v5, vcc, 0, v3, vcc
	v_add_co_u32_e32 v8, vcc, s38, v2
	v_max3_f32 v43, v43, |v6|, |v40|
	s_nop 0
	v_addc_co_u32_e32 v9, vcc, 0, v3, vcc
	v_max3_f32 v44, v44, |v7|, |v41|
	global_load_dwordx4 v[4:7], v[4:5], off offset:2048
	s_nop 0
	global_load_dwordx4 v[38:41], v[8:9], off offset:1024
	s_waitcnt vmcnt(0) lgkmcnt(0)
	v_max3_f32 v1, v1, |v4|, |v38|
	v_add_co_u32_e32 v4, vcc, s39, v2
	v_max3_f32 v42, v42, |v5|, |v39|
	s_nop 0
	v_addc_co_u32_e32 v5, vcc, 0, v3, vcc
	v_add_co_u32_e32 v8, vcc, s40, v2
	v_max3_f32 v43, v43, |v6|, |v40|
	s_nop 0
	v_addc_co_u32_e32 v9, vcc, 0, v3, vcc
	v_max3_f32 v44, v44, |v7|, |v41|
	global_load_dwordx4 v[4:7], v[4:5], off
	s_nop 0
	global_load_dwordx4 v[38:41], v[8:9], off offset:3072
	s_waitcnt vmcnt(0) lgkmcnt(0)
	v_max3_f32 v1, v1, |v4|, |v38|
	v_add_co_u32_e32 v4, vcc, s41, v2
	v_max3_f32 v8, v42, |v5|, |v39|
	s_nop 0
	v_addc_co_u32_e32 v5, vcc, 0, v3, vcc
	v_add_co_u32_e32 v2, vcc, s42, v2
	v_max3_f32 v9, v43, |v6|, |v40|
	s_nop 0
	v_addc_co_u32_e32 v3, vcc, 0, v3, vcc
	v_max3_f32 v42, v44, |v7|, |v41|
	global_load_dwordx4 v[4:7], v[4:5], off offset:2048
	v_cmp_lt_i32_e32 vcc, v31, v32
	global_load_dwordx4 v[38:41], v[2:3], off offset:1024
	s_waitcnt vmcnt(0) lgkmcnt(0)
	v_max3_f32 v3, v8, |v5|, |v39|
	v_cndmask_b32_e32 v2, v30, v31, vcc
	v_cmp_lt_i32_e32 vcc, v33, v32
	v_lshlrev_b32_e32 v8, 2, v2
	v_max3_f32 v1, v1, |v4|, |v38|
	v_cndmask_b32_e32 v2, v30, v33, vcc
	v_cmp_lt_i32_e32 vcc, v34, v32
	v_max3_f32 v5, v9, |v6|, |v40|
	v_max3_f32 v7, v42, |v7|, |v41|
	v_lshlrev_b32_e32 v9, 2, v2
	v_cndmask_b32_e32 v2, v30, v34, vcc
	v_lshlrev_b32_e32 v38, 2, v2
	ds_bpermute_b32 v2, v8, v1
	ds_bpermute_b32 v4, v8, v3
	ds_bpermute_b32 v6, v8, v5
	ds_bpermute_b32 v8, v8, v7
	s_waitcnt lgkmcnt(3)
	v_max_f32_e32 v2, v2, v2
	s_waitcnt lgkmcnt(2)
	v_max_f32_e32 v4, v4, v4
	s_waitcnt lgkmcnt(1)
	v_max_f32_e32 v6, v6, v6
	s_waitcnt lgkmcnt(0)
	v_max_f32_e32 v8, v8, v8
	v_max_f32_e32 v1, v1, v2
	v_max_f32_e32 v3, v3, v4
	v_max_f32_e32 v5, v5, v6
	v_max_f32_e32 v7, v7, v8
	ds_bpermute_b32 v2, v9, v1
	ds_bpermute_b32 v4, v9, v3
	ds_bpermute_b32 v6, v9, v5
	ds_bpermute_b32 v8, v9, v7
	s_waitcnt lgkmcnt(3)
	v_max_f32_e32 v2, v2, v2
	s_waitcnt lgkmcnt(2)
	v_max_f32_e32 v4, v4, v4
	s_waitcnt lgkmcnt(1)
	v_max_f32_e32 v6, v6, v6
	s_waitcnt lgkmcnt(0)
	v_max_f32_e32 v8, v8, v8
	v_max_f32_e32 v1, v1, v2
	v_max_f32_e32 v3, v3, v4
	v_max_f32_e32 v5, v5, v6
	v_max_f32_e32 v7, v7, v8
	ds_bpermute_b32 v2, v38, v1
	ds_bpermute_b32 v4, v38, v3
	ds_bpermute_b32 v6, v38, v5
	ds_bpermute_b32 v8, v38, v7
	s_and_saveexec_b64 s[18:19], s[6:7]
	s_cbranch_execz .LBB0_518
; __device__ __forceinline__ void colmax_item(const float* src, int ld, int k0, int c0, float* cmx  , int lane) {
;     ...
;     if (q == 0) {
; #pragma unroll
;         for (int i = 0; i < 4; ++i) atomicMax((unsigned*)(cmx + 4 * c + i), __float_as_uint(mx[i] * CMS_F)); }
	s_lshl_b32 s17, s69, 6
	s_and_b32 s17, s17, 0x3fff00
	s_cmpk_gt_u32 s8, 0x57f
	s_cselect_b32 s8, 0x80, 0
	v_mul_u32_u24_e32 v9, s21, v36
	s_or_b32 s8, s17, s8
	s_and_b32 s16, s16, 0x60
	v_lshlrev_b32_e32 v38, 2, v9
	v_mov_b32_e32 v39, v11
	s_or_b32 s8, s8, s16
	v_lshl_add_u64 v[38:39], s[10:11], 0, v[38:39]
	s_lshl_b32 s8, s8, 2
	s_waitcnt lgkmcnt(3)
	v_max_f32_e32 v2, v2, v2
	v_max_f32_e32 v1, v1, v1
	v_lshl_add_u64 v[38:39], v[38:39], 0, s[8:9]
	s_waitcnt lgkmcnt(2)
	v_max_f32_e32 v4, v4, v4
	v_max_f32_e32 v3, v3, v3
	v_max_f32_e32 v1, v1, v2
	s_waitcnt lgkmcnt(1)
	v_max_f32_e32 v6, v6, v6
	v_max_f32_e32 v5, v5, v5
	v_max_f32_e32 v3, v3, v4
	v_mul_f32_e32 v1, 0x3fb33333, v1
	v_readfirstlane_b32 s16, v38
	v_readfirstlane_b32 s17, v39
	s_waitcnt lgkmcnt(0)
	v_max_f32_e32 v8, v8, v8
	v_max_f32_e32 v7, v7, v7
	v_max_f32_e32 v5, v5, v6
	v_max_f32_e32 v7, v7, v8
	global_atomic_umax v29, v1, s[16:17]
	v_mul_f32_e32 v1, 0x3fb33333, v3
	global_atomic_umax v29, v1, s[16:17] offset:4
	v_mul_f32_e32 v1, 0x3fb33333, v5
	global_atomic_umax v29, v1, s[16:17] offset:8
	v_mul_f32_e32 v1, 0x3fb33333, v7
	global_atomic_umax v29, v1, s[16:17] offset:12

; __device__ __forceinline__ void cvt_item8(const float* src, int ld, int k0, int c0, unsigned char* dst, int Kd, int drow0, unsigned char* scr, int lane) {
;     const int c = lane & 7, q = lane >> 3;
;     f32x4 v[4][4];
; #pragma unroll
;     for (int g = 0; g < 4; ++g)
; #pragma unroll
;         for (int j = 0; j < 4; ++j) v[g][j] = __builtin_nontemporal_load((const f32x4*)(src + (size_t)(k0 + 32 * g + 4 * q + j) * ld + c0 + 4 * c));
; #pragma unroll
;     for (int g = 0; g < 4; ++g)
; #pragma unroll
;         for (int i = 0; i < 4; ++i) *(unsigned*)(scr + (4 * c + i) * 132 + 32 * g + 4 * q) = pg8::pack_fp8x4(v[g][0][i] * WSC, v[g][1][i] * WSC, v[g][2][i] * WSC, v[g][3][i] * WSC);
; template <int GRP>
; __device__ __forceinline__ void conv_item(Frame& F, int r) {
;     ...
;             if (r < CI_MD) { const int e = r / (22 * 64); r %= (22 * 64); const int kb = r / 64, nb = r % 64;
;                 cvt_item8(inptr(F, IN_MD) + (size_t)e * DFE * D, D, kb * 128, nb * 32, ws + WS_MD + (size_t)e * D * DFE, DFE, nb * 32, scr, F.lane); return; }
.LBB0_519:
	s_andn2_b64 vcc, exec, s[16:17]
	s_cbranch_vccnz .LBB0_521
	s_add_i32 s8, s20, 0xfc00
	v_mov_b32_e32 v1, s43
	s_and_b32 s16, s8, 0xffff
	s_waitcnt lgkmcnt(3)
	ds_read_b64 v[2:3], v1
	s_mul_i32 s16, s16, 0xba2f
	s_lshr_b32 s17, s16, 26
	s_mul_i32 s16, s17, 0x580
	s_sub_i32 s8, s8, s16
	s_and_b32 s16, s8, 0xffff
	s_waitcnt lgkmcnt(0)
	v_readfirstlane_b32 s8, v2
	s_mul_i32 s19, s17, 0x1600000
	v_readfirstlane_b32 s18, v3
	s_add_u32 s19, s8, s19
	s_addc_u32 s21, s18, 0
	s_lshl_b32 s8, s16, 1
	s_lshl_b32 s16, s16, 5
	s_and_b32 s16, s16, 0x7e0
	s_and_b32 s8, s8, 0xf80
	s_lshl_b32 s18, s16, 2
	s_add_u32 s18, s19, s18
	v_or_b32_e32 v1, s8, v21
	s_addc_u32 s19, s21, 0
	v_lshlrev_b32_e32 v2, 2, v14
	v_mov_b32_e32 v3, v11
	v_lshl_add_u64 v[2:3], s[18:19], 0, v[2:3]
	v_lshlrev_b32_e32 v4, 13, v1
	v_mov_b32_e32 v5, v11
	v_lshl_add_u64 v[8:9], v[2:3], 0, v[4:5]
	v_add_co_u32_e32 v2, vcc, s26, v8
	s_nop 1
	v_addc_co_u32_e32 v3, vcc, 0, v9, vcc
	global_load_dwordx4 v[4:7], v[8:9], off nt
	global_load_dwordx4 v[38:41], v[2:3], off nt
	v_add_co_u32_e32 v2, vcc, s44, v8
	s_waitcnt vmcnt(0) lgkmcnt(0)
	v_mul_f32_e32 v1, 0x42800000, v4
	v_addc_co_u32_e32 v3, vcc, 0, v9, vcc
	global_load_dwordx4 v[42:45], v[2:3], off nt
	v_add_co_u32_e32 v2, vcc, s45, v8
	v_mul_f32_e32 v4, 0x42800000, v38
	s_nop 0
	v_addc_co_u32_e32 v3, vcc, 0, v9, vcc
	global_load_dwordx4 v[46:49], v[2:3], off nt
	v_add_co_u32_e32 v50, vcc, s46, v8
	v_med3_f32 v1, v1, s67, v37
	s_nop 0
	v_addc_co_u32_e32 v51, vcc, 0, v9, vcc
	v_add_co_u32_e32 v54, vcc, s47, v8
	v_med3_f32 v4, v4, s67, v37
	s_nop 0
	v_addc_co_u32_e32 v55, vcc, 0, v9, vcc
	global_load_dwordx4 v[50:53], v[50:51], off nt
	s_nop 0
	global_load_dwordx4 v[54:57], v[54:55], off nt
	v_add_co_u32_e32 v58, vcc, s49, v8
	v_mov_b32_e32 v38, v11
	s_nop 0
	v_addc_co_u32_e32 v59, vcc, 0, v9, vcc
	v_add_co_u32_e32 v62, vcc, s52, v8
	v_mov_b64_e32 v[2:3], s[12:13]
	s_nop 0
	v_addc_co_u32_e32 v63, vcc, 0, v9, vcc
	global_load_dwordx4 v[58:61], v[58:59], off nt
	s_nop 0
	global_load_dwordx4 v[62:65], v[62:63], off nt
	v_add_co_u32_e32 v66, vcc, s53, v8
	v_mad_u64_u32 v[2:3], s[18:19], s17, v35, v[2:3]
	s_nop 0
	v_addc_co_u32_e32 v67, vcc, 0, v9, vcc
	v_add_co_u32_e32 v70, vcc, s54, v8
	v_lshl_add_u64 v[2:3], v[2:3], 0, s[8:9]
	s_nop 0
	v_addc_co_u32_e32 v71, vcc, 0, v9, vcc
	global_load_dwordx4 v[66:69], v[66:67], off nt
	s_nop 0
	global_load_dwordx4 v[70:73], v[70:71], off nt
	v_add_co_u32_e32 v74, vcc, s55, v8
	s_nop 1
	v_addc_co_u32_e32 v75, vcc, 0, v9, vcc
	v_add_co_u32_e32 v78, vcc, s56, v8
	s_nop 1
	v_addc_co_u32_e32 v79, vcc, 0, v9, vcc
	global_load_dwordx4 v[74:77], v[74:75], off nt
	s_nop 0
	global_load_dwordx4 v[78:81], v[78:79], off nt
	v_add_co_u32_e32 v82, vcc, s57, v8
	s_nop 1
	v_addc_co_u32_e32 v83, vcc, 0, v9, vcc
	v_add_co_u32_e32 v86, vcc, s62, v8
	s_nop 1
	v_addc_co_u32_e32 v87, vcc, 0, v9, vcc
	global_load_dwordx4 v[82:85], v[82:83], off nt
	s_nop 0
	global_load_dwordx4 v[86:89], v[86:87], off nt
	v_add_co_u32_e32 v90, vcc, s63, v8
	s_nop 1
	v_addc_co_u32_e32 v91, vcc, 0, v9, vcc
	v_add_co_u32_e32 v8, vcc, s66, v8
	s_nop 1
	v_addc_co_u32_e32 v9, vcc, 0, v9, vcc
	global_load_dwordx4 v[90:93], v[90:91], off nt
	s_nop 0
	global_load_dwordx4 v[94:97], v[8:9], off nt
	v_mov_b32_e32 v9, v11
	v_cvt_pk_fp8_f32 v9, v1, v4
	s_waitcnt vmcnt(0) lgkmcnt(0)
	v_mul_f32_e32 v8, 0x42800000, v42
	v_med3_f32 v4, v8, s67, v37
	v_mul_f32_e32 v8, 0x42800000, v43
	v_mov_b32_e32 v42, v11
	v_mul_f32_e32 v1, 0x42800000, v46
	v_med3_f32 v1, v1, s67, v37
	v_cvt_pk_fp8_f32 v9, v4, v1 op_sel:[0,0,1]
	v_mul_f32_e32 v4, 0x42800000, v5
	v_mul_f32_e32 v5, 0x42800000, v39
	v_med3_f32 v4, v4, s67, v37
	v_med3_f32 v5, v5, s67, v37
	v_cvt_pk_fp8_f32 v38, v4, v5
	v_mul_f32_e32 v4, 0x42800000, v47
	v_med3_f32 v5, v8, s67, v37
	v_med3_f32 v4, v4, s67, v37
	v_cvt_pk_fp8_f32 v38, v5, v4 op_sel:[0,0,1]
	v_mul_f32_e32 v4, 0x42800000, v6
	v_mul_f32_e32 v5, 0x42800000, v40
	v_med3_f32 v4, v4, s67, v37
	v_med3_f32 v5, v5, s67, v37
	v_mov_b32_e32 v8, v11
	v_cvt_pk_fp8_f32 v8, v4, v5
	v_mul_f32_e32 v6, 0x42800000, v44
	v_mul_f32_e32 v4, 0x42800000, v48
	v_med3_f32 v5, v6, s67, v37
	v_med3_f32 v4, v4, s67, v37
	v_cvt_pk_fp8_f32 v8, v5, v4 op_sel:[0,0,1]
	v_mul_f32_e32 v4, 0x42800000, v7
	v_mul_f32_e32 v5, 0x42800000, v41
	v_med3_f32 v4, v4, s67, v37
	v_med3_f32 v5, v5, s67, v37
	v_mov_b32_e32 v7, v11
	v_cvt_pk_fp8_f32 v7, v4, v5
	v_mul_f32_e32 v6, 0x42800000, v45
	v_mul_f32_e32 v4, 0x42800000, v49
	v_med3_f32 v5, v6, s67, v37
	v_med3_f32 v4, v4, s67, v37
	v_cvt_pk_fp8_f32 v7, v5, v4 op_sel:[0,0,1]
	v_mul_f32_e32 v4, 0x42800000, v50
	v_mul_f32_e32 v5, 0x42800000, v54
	v_med3_f32 v4, v4, s67, v37
	v_med3_f32 v5, v5, s67, v37
	v_mov_b32_e32 v39, v11
	v_cvt_pk_fp8_f32 v39, v4, v5
	v_mul_f32_e32 v6, 0x42800000, v58
	v_mul_f32_e32 v4, 0x42800000, v62
	v_med3_f32 v5, v6, s67, v37
	v_med3_f32 v4, v4, s67, v37
	v_cvt_pk_fp8_f32 v39, v5, v4 op_sel:[0,0,1]
	v_mul_f32_e32 v4, 0x42800000, v51
	v_mul_f32_e32 v5, 0x42800000, v55
	v_med3_f32 v4, v4, s67, v37
	v_med3_f32 v5, v5, s67, v37
	v_mov_b32_e32 v40, v11
	v_cvt_pk_fp8_f32 v40, v4, v5
	v_mul_f32_e32 v6, 0x42800000, v59
	v_mul_f32_e32 v4, 0x42800000, v63
	v_med3_f32 v5, v6, s67, v37
	v_med3_f32 v4, v4, s67, v37
	v_cvt_pk_fp8_f32 v40, v5, v4 op_sel:[0,0,1]
; __device__ __forceinline__ void cvt_item8(const float* src, int ld, int k0, int c0, unsigned char* dst, int Kd, int drow0, unsigned char* scr, int lane) {
;     ...
;     for (int g = 0; g < 4; ++g)
; #pragma unroll
;         for (int i = 0; i < 4; ++i) *(unsigned*)(scr + (4 * c + i) * 132 + 32 * g + 4 * q) = pg8::pack_fp8x4(v[g][0][i] * WSC, v[g][1][i] * WSC, v[g][2][i] * WSC, v[g][3][i] * WSC);
;     asm volatile("s_waitcnt lgkmcnt(0)" ::: "memory");
; #pragma unroll
;     for (int r = 0; r < 4; ++r) { const int n = 8 * r + (lane >> 3), ch = lane & 7; const unsigned char* p = scr + n * 132 + ch * 16;
;         u32x4 o; o.x = *(const unsigned*)(p); o.y = *(const unsigned*)(p + 4); o.z = *(const unsigned*)(p + 8); o.w = *(const unsigned*)(p + 12);
;         *(u32x4*)(dst + (size_t)(drow0 + n) * Kd + k0 + 16 * ch) = o; }
;     asm volatile("s_waitcnt lgkmcnt(0)" ::: "memory");
	v_mul_f32_e32 v4, 0x42800000, v52
	v_mul_f32_e32 v5, 0x42800000, v56
	v_med3_f32 v4, v4, s67, v37
	v_med3_f32 v5, v5, s67, v37
	v_mov_b32_e32 v41, v11
	v_cvt_pk_fp8_f32 v41, v4, v5
	v_mul_f32_e32 v6, 0x42800000, v60
	v_mul_f32_e32 v4, 0x42800000, v64
	v_med3_f32 v5, v6, s67, v37
	v_med3_f32 v4, v4, s67, v37
	v_cvt_pk_fp8_f32 v41, v5, v4 op_sel:[0,0,1]
	v_mul_f32_e32 v4, 0x42800000, v53
	v_mul_f32_e32 v5, 0x42800000, v57
	v_med3_f32 v4, v4, s67, v37
	v_med3_f32 v5, v5, s67, v37
	v_cvt_pk_fp8_f32 v42, v4, v5
	v_mul_f32_e32 v6, 0x42800000, v61
	v_mul_f32_e32 v4, 0x42800000, v65
	v_med3_f32 v5, v6, s67, v37
	v_med3_f32 v4, v4, s67, v37
	v_add_u32_e32 v1, v22, v23
	v_cvt_pk_fp8_f32 v42, v5, v4 op_sel:[0,0,1]
	v_mul_f32_e32 v4, 0x42800000, v66
	v_mul_f32_e32 v5, 0x42800000, v70
	ds_write2_b32 v1, v9, v39 offset1:8
	ds_write2_b32 v1, v38, v40 offset0:33 offset1:41
	ds_write2_b32 v1, v8, v41 offset0:66 offset1:74
	ds_write2_b32 v1, v7, v42 offset0:99 offset1:107
	v_med3_f32 v4, v4, s67, v37
	v_med3_f32 v5, v5, s67, v37
	v_mov_b32_e32 v7, v11
	v_cvt_pk_fp8_f32 v7, v4, v5
	v_mul_f32_e32 v6, 0x42800000, v74
	v_mul_f32_e32 v4, 0x42800000, v78
	v_med3_f32 v5, v6, s67, v37
	v_med3_f32 v4, v4, s67, v37
	v_cvt_pk_fp8_f32 v7, v5, v4 op_sel:[0,0,1]
	v_mul_f32_e32 v4, 0x42800000, v67
	v_mul_f32_e32 v5, 0x42800000, v71
	v_med3_f32 v4, v4, s67, v37
	v_med3_f32 v5, v5, s67, v37
	v_mov_b32_e32 v8, v11
	v_cvt_pk_fp8_f32 v8, v4, v5
	v_mul_f32_e32 v6, 0x42800000, v75
	v_mul_f32_e32 v4, 0x42800000, v79
	v_med3_f32 v5, v6, s67, v37
	v_med3_f32 v4, v4, s67, v37
	v_cvt_pk_fp8_f32 v8, v5, v4 op_sel:[0,0,1]
	v_mul_f32_e32 v4, 0x42800000, v68
	v_mul_f32_e32 v5, 0x42800000, v72
	v_med3_f32 v4, v4, s67, v37
	v_med3_f32 v5, v5, s67, v37
	v_mov_b32_e32 v9, v11
	v_cvt_pk_fp8_f32 v9, v4, v5
	v_mul_f32_e32 v6, 0x42800000, v76
	v_mul_f32_e32 v4, 0x42800000, v80
	v_med3_f32 v5, v6, s67, v37
	v_med3_f32 v4, v4, s67, v37
	v_cvt_pk_fp8_f32 v9, v5, v4 op_sel:[0,0,1]
	v_mul_f32_e32 v4, 0x42800000, v69
	v_mul_f32_e32 v5, 0x42800000, v73
	v_med3_f32 v4, v4, s67, v37
	v_med3_f32 v5, v5, s67, v37
	v_mov_b32_e32 v38, v11
	v_cvt_pk_fp8_f32 v38, v4, v5
	v_mul_f32_e32 v6, 0x42800000, v77
	v_mul_f32_e32 v4, 0x42800000, v81
	v_med3_f32 v5, v6, s67, v37
	v_med3_f32 v4, v4, s67, v37
	v_cvt_pk_fp8_f32 v38, v5, v4 op_sel:[0,0,1]
	v_mul_f32_e32 v4, 0x42800000, v82
	v_mul_f32_e32 v5, 0x42800000, v86
	v_med3_f32 v4, v4, s67, v37
	v_med3_f32 v5, v5, s67, v37
	v_mov_b32_e32 v39, v11
	v_cvt_pk_fp8_f32 v39, v4, v5
	v_mul_f32_e32 v6, 0x42800000, v90
	v_mul_f32_e32 v4, 0x42800000, v94
	v_med3_f32 v5, v6, s67, v37
	v_med3_f32 v4, v4, s67, v37
	v_cvt_pk_fp8_f32 v39, v5, v4 op_sel:[0,0,1]
	v_mul_f32_e32 v4, 0x42800000, v83
	v_mul_f32_e32 v5, 0x42800000, v87
	v_med3_f32 v4, v4, s67, v37
	v_med3_f32 v5, v5, s67, v37
	v_mov_b32_e32 v40, v11
	v_cvt_pk_fp8_f32 v40, v4, v5
	v_mul_f32_e32 v6, 0x42800000, v91
	v_mul_f32_e32 v4, 0x42800000, v95
	v_med3_f32 v5, v6, s67, v37
	v_med3_f32 v4, v4, s67, v37
	v_cvt_pk_fp8_f32 v40, v5, v4 op_sel:[0,0,1]
	v_mul_f32_e32 v4, 0x42800000, v84
	v_mul_f32_e32 v5, 0x42800000, v88
	v_med3_f32 v4, v4, s67, v37
	v_med3_f32 v5, v5, s67, v37
	v_mov_b32_e32 v41, v11
	v_cvt_pk_fp8_f32 v41, v4, v5
	v_mul_f32_e32 v6, 0x42800000, v92
	v_mul_f32_e32 v4, 0x42800000, v96
	v_med3_f32 v5, v6, s67, v37
	v_med3_f32 v4, v4, s67, v37
	v_cvt_pk_fp8_f32 v41, v5, v4 op_sel:[0,0,1]
	v_mul_f32_e32 v4, 0x42800000, v85
	v_mul_f32_e32 v5, 0x42800000, v89
	v_med3_f32 v4, v4, s67, v37
	v_med3_f32 v5, v5, s67, v37
	v_mov_b32_e32 v42, v11
	v_cvt_pk_fp8_f32 v42, v4, v5
	v_mul_f32_e32 v6, 0x42800000, v93
	v_mul_f32_e32 v4, 0x42800000, v97
	v_med3_f32 v5, v6, s67, v37
	v_med3_f32 v4, v4, s67, v37
	v_cvt_pk_fp8_f32 v42, v5, v4 op_sel:[0,0,1]
	ds_write2_b32 v1, v7, v39 offset0:16 offset1:24
	ds_write2_b32 v1, v8, v40 offset0:49 offset1:57
	ds_write2_b32 v1, v9, v41 offset0:82 offset1:90
	ds_write2_b32 v1, v38, v42 offset0:115 offset1:123
	s_waitcnt lgkmcnt(0)
	v_add_u32_e32 v1, v24, v25
	v_lshl_add_u64 v[38:39], v[2:3], 0, v[16:17]
	ds_read2_b32 v[2:3], v1 offset1:1
	ds_read2_b32 v[4:5], v1 offset0:2 offset1:3
	v_or_b32_e32 v6, s16, v20
	v_mul_u32_u24_e32 v6, 0xb00, v6
	v_mov_b32_e32 v7, v11
	v_lshl_add_u64 v[40:41], v[38:39], 0, v[6:7]
	v_add_u32_e32 v6, 0x420, v1
	v_add_u32_e32 v8, 0x428, v1
	ds_read2_b32 v[6:7], v6 offset1:1
	ds_read2_b32 v[8:9], v8 offset1:1
	s_waitcnt lgkmcnt(2)
	global_store_dwordx4 v[40:41], v[2:5], off
	s_nop 1
	v_or_b32_e32 v2, s16, v26
	v_mul_u32_u24_e32 v2, 0xb00, v2
	v_mov_b32_e32 v3, v11
	v_lshl_add_u64 v[2:3], v[38:39], 0, v[2:3]
	s_waitcnt lgkmcnt(0)
	global_store_dwordx4 v[2:3], v[6:9], off
	v_add_u32_e32 v2, 0x840, v1
	v_add_u32_e32 v4, 0x848, v1
	v_or_b32_e32 v6, s16, v27
	ds_read2_b32 v[2:3], v2 offset1:1
	ds_read2_b32 v[4:5], v4 offset1:1
	v_mul_u32_u24_e32 v6, 0xb00, v6
	v_mov_b32_e32 v7, v11
	v_lshl_add_u64 v[40:41], v[38:39], 0, v[6:7]
	v_add_u32_e32 v6, 0xc60, v1
	v_add_u32_e32 v1, 0xc68, v1
	ds_read2_b32 v[6:7], v6 offset1:1
	ds_read2_b32 v[8:9], v1 offset1:1
	v_or_b32_e32 v1, s16, v28
	s_waitcnt lgkmcnt(2)
	global_store_dwordx4 v[40:41], v[2:5], off
	s_nop 1
	v_mul_u32_u24_e32 v2, 0xb00, v1
	v_mov_b32_e32 v3, v11
	v_lshl_add_u64 v[2:3], v[38:39], 0, v[2:3]
	s_waitcnt lgkmcnt(0)
	global_store_dwordx4 v[2:3], v[6:9], off
	s_waitcnt lgkmcnt(0)

; __device__ __forceinline__ void cvt_item8(const float* src, int ld, int k0, int c0, unsigned char* dst, int Kd, int drow0, unsigned char* scr, int lane) {
;     const int c = lane & 7, q = lane >> 3;
;     f32x4 v[4][4];
; #pragma unroll
;     for (int g = 0; g < 4; ++g)
; #pragma unroll
;         for (int j = 0; j < 4; ++j) v[g][j] = __builtin_nontemporal_load((const f32x4*)(src + (size_t)(k0 + 32 * g + 4 * q + j) * ld + c0 + 4 * c));
; #pragma unroll
;     for (int g = 0; g < 4; ++g)
; #pragma unroll
;         for (int i = 0; i < 4; ++i) *(unsigned*)(scr + (4 * c + i) * 132 + 32 * g + 4 * q) = pg8::pack_fp8x4(v[g][0][i] * WSC, v[g][1][i] * WSC, v[g][2][i] * WSC, v[g][3][i] * WSC);
; template <int GRP>
; __device__ __forceinline__ void conv_item(Frame& F, int r) {
;     ...
;         if (r < CI_WO) { const int kb = r / 64, nb = r % 64;
;             cvt_item8(inptr(F, IN_WOUT) + (size_t)l * D * D, D, kb * 128, nb * 32, ws + WS_WOUT + (size_t)l * D * D, D, nb * 32, scr, F.lane); return; }
.LBB0_522:
	s_andn2_b64 vcc, exec, s[16:17]
	s_cbranch_vccnz .LBB0_506
	s_ashr_i32 s8, s20, 31
	v_mov_b32_e32 v1, s68
	s_lshr_b32 s8, s8, 26
	s_waitcnt lgkmcnt(3)
	ds_read_b64 v[2:3], v1
	s_add_i32 s8, s20, s8
	s_and_b32 s16, s8, 0x7ffffc0
	s_sub_i32 s16, s20, s16
	s_lshl_b32 s16, s16, 5
	s_lshl_b32 s8, s8, 1
	s_ashr_i32 s17, s16, 31
	s_waitcnt lgkmcnt(0)
	v_readfirstlane_b32 s19, v2
	s_and_b32 s18, s8, 0xffffff80
	s_lshl_b64 s[20:21], s[16:17], 2
	v_readfirstlane_b32 s69, v3
	s_add_u32 s20, s19, s20
	v_or_b32_e32 v86, s18, v21
	s_addc_u32 s21, s69, s21
	v_lshlrev_b32_e32 v2, 2, v14
	v_mov_b32_e32 v3, v11
	v_lshl_add_u64 v[2:3], s[20:21], 0, v[2:3]
	v_ashrrev_i32_e32 v87, 31, v86
	v_or_b32_e32 v4, 1, v86
	v_lshl_add_u64 v[88:89], v[2:3], 0, s[14:15]
	v_lshlrev_b64 v[2:3], 13, v[86:87]
	v_ashrrev_i32_e32 v5, 31, v4
	v_lshl_add_u64 v[2:3], v[88:89], 0, v[2:3]
	v_lshlrev_b64 v[4:5], 13, v[4:5]
	v_lshl_add_u64 v[4:5], v[88:89], 0, v[4:5]
	global_load_dwordx4 v[38:41], v[2:3], off nt
	s_waitcnt vmcnt(0)
	global_load_dwordx4 v[42:45], v[4:5], off nt
	v_or_b32_e32 v2, 2, v86
	v_ashrrev_i32_e32 v3, 31, v2
	v_lshlrev_b64 v[2:3], 13, v[2:3]
	v_lshl_add_u64 v[2:3], v[88:89], 0, v[2:3]
	global_load_dwordx4 v[46:49], v[2:3], off nt
	v_or_b32_e32 v2, 3, v86
	v_ashrrev_i32_e32 v3, 31, v2
	v_lshlrev_b64 v[2:3], 13, v[2:3]
	v_lshl_add_u64 v[2:3], v[88:89], 0, v[2:3]
	global_load_dwordx4 v[50:53], v[2:3], off nt
	v_or_b32_e32 v2, 32, v86
	v_ashrrev_i32_e32 v3, 31, v2
	v_or_b32_e32 v4, 33, v86
	v_lshlrev_b64 v[2:3], 13, v[2:3]
	v_ashrrev_i32_e32 v5, 31, v4
	v_lshl_add_u64 v[2:3], v[88:89], 0, v[2:3]
	v_lshlrev_b64 v[4:5], 13, v[4:5]
	v_lshl_add_u64 v[4:5], v[88:89], 0, v[4:5]
	global_load_dwordx4 v[54:57], v[2:3], off nt
	global_load_dwordx4 v[58:61], v[4:5], off nt
	v_or_b32_e32 v2, 34, v86
	v_ashrrev_i32_e32 v3, 31, v2
	v_or_b32_e32 v4, 35, v86
	v_lshlrev_b64 v[2:3], 13, v[2:3]
	v_ashrrev_i32_e32 v5, 31, v4
	v_lshl_add_u64 v[2:3], v[88:89], 0, v[2:3]
	v_lshlrev_b64 v[4:5], 13, v[4:5]
	v_lshl_add_u64 v[4:5], v[88:89], 0, v[4:5]
	global_load_dwordx4 v[62:65], v[2:3], off nt
	global_load_dwordx4 v[66:69], v[4:5], off nt
	v_or_b32_e32 v2, 64, v86
	v_ashrrev_i32_e32 v3, 31, v2
	v_or_b32_e32 v4, 0x41, v86
	v_lshlrev_b64 v[2:3], 13, v[2:3]
	v_ashrrev_i32_e32 v5, 31, v4
	v_lshl_add_u64 v[2:3], v[88:89], 0, v[2:3]
	v_lshlrev_b64 v[4:5], 13, v[4:5]
	v_lshl_add_u64 v[4:5], v[88:89], 0, v[4:5]
	global_load_dwordx4 v[70:73], v[2:3], off nt
	global_load_dwordx4 v[74:77], v[4:5], off nt
	v_or_b32_e32 v2, 0x42, v86
	v_ashrrev_i32_e32 v3, 31, v2
	v_or_b32_e32 v4, 0x43, v86
	v_lshlrev_b64 v[2:3], 13, v[2:3]
	v_ashrrev_i32_e32 v5, 31, v4
	v_lshl_add_u64 v[2:3], v[88:89], 0, v[2:3]
	v_lshlrev_b64 v[4:5], 13, v[4:5]
	v_lshl_add_u64 v[4:5], v[88:89], 0, v[4:5]
	global_load_dwordx4 v[78:81], v[2:3], off nt
	global_load_dwordx4 v[82:85], v[4:5], off nt
	v_or_b32_e32 v2, 0x60, v86
	v_or_b32_e32 v4, 0x61, v86
	v_ashrrev_i32_e32 v3, 31, v2
	v_ashrrev_i32_e32 v5, 31, v4
	v_lshlrev_b64 v[2:3], 13, v[2:3]
	v_lshlrev_b64 v[4:5], 13, v[4:5]
	v_lshl_add_u64 v[2:3], v[88:89], 0, v[2:3]
	v_lshl_add_u64 v[6:7], v[88:89], 0, v[4:5]
	global_load_dwordx4 v[2:5], v[2:3], off nt
	s_nop 0
	global_load_dwordx4 v[6:9], v[6:7], off nt
	v_or_b32_e32 v90, 0x62, v86
	v_or_b32_e32 v86, 0x63, v86
	v_ashrrev_i32_e32 v91, 31, v90
	v_ashrrev_i32_e32 v87, 31, v86
	v_lshlrev_b64 v[90:91], 13, v[90:91]
	v_lshlrev_b64 v[86:87], 13, v[86:87]
	v_lshl_add_u64 v[90:91], v[88:89], 0, v[90:91]
	v_lshl_add_u64 v[92:93], v[88:89], 0, v[86:87]
	global_load_dwordx4 v[86:89], v[90:91], off nt
	s_nop 0
	global_load_dwordx4 v[90:93], v[92:93], off nt
	s_ashr_i32 s19, s18, 31
	s_waitcnt lgkmcnt(0)
	v_mul_f32_e32 v1, 0x42800000, v38
	s_waitcnt vmcnt(0)
	v_mul_f32_e32 v38, 0x42800000, v42
	v_med3_f32 v1, v1, s67, v37
	v_med3_f32 v38, v38, s67, v37
	v_mul_f32_e32 v42, 0x42800000, v46
	v_mov_b32_e32 v46, v11
	v_cvt_pk_fp8_f32 v46, v1, v38
	v_med3_f32 v38, v42, s67, v37
	v_mul_f32_e32 v42, 0x42800000, v47
	v_mul_f32_e32 v1, 0x42800000, v50
	v_med3_f32 v1, v1, s67, v37
	v_cvt_pk_fp8_f32 v46, v38, v1 op_sel:[0,0,1]
	v_mul_f32_e32 v38, 0x42800000, v39
	v_mul_f32_e32 v39, 0x42800000, v43
	v_med3_f32 v38, v38, s67, v37
	v_med3_f32 v39, v39, s67, v37
	v_mov_b32_e32 v43, v11
	v_cvt_pk_fp8_f32 v43, v38, v39
	v_mul_f32_e32 v38, 0x42800000, v51
	v_med3_f32 v39, v42, s67, v37
	v_med3_f32 v38, v38, s67, v37
	v_cvt_pk_fp8_f32 v43, v39, v38 op_sel:[0,0,1]
	v_mul_f32_e32 v38, 0x42800000, v40
	v_mul_f32_e32 v39, 0x42800000, v44
	v_med3_f32 v38, v38, s67, v37
	v_med3_f32 v39, v39, s67, v37
	v_mov_b32_e32 v42, v11
	v_cvt_pk_fp8_f32 v42, v38, v39
	v_mul_f32_e32 v40, 0x42800000, v48
	v_mul_f32_e32 v38, 0x42800000, v52
	v_med3_f32 v39, v40, s67, v37
	v_med3_f32 v38, v38, s67, v37
	v_cvt_pk_fp8_f32 v42, v39, v38 op_sel:[0,0,1]
	v_mul_f32_e32 v38, 0x42800000, v41
	v_mul_f32_e32 v39, 0x42800000, v45
	v_med3_f32 v38, v38, s67, v37
	v_med3_f32 v39, v39, s67, v37
	v_mov_b32_e32 v41, v11
	v_cvt_pk_fp8_f32 v41, v38, v39
	v_mul_f32_e32 v40, 0x42800000, v49
	v_mul_f32_e32 v38, 0x42800000, v53
	v_med3_f32 v39, v40, s67, v37
	v_med3_f32 v38, v38, s67, v37
	v_cvt_pk_fp8_f32 v41, v39, v38 op_sel:[0,0,1]
	v_mul_f32_e32 v38, 0x42800000, v54
	v_mul_f32_e32 v39, 0x42800000, v58
	v_med3_f32 v38, v38, s67, v37
	v_med3_f32 v39, v39, s67, v37
	v_mov_b32_e32 v44, v11
	v_cvt_pk_fp8_f32 v44, v38, v39
	v_mul_f32_e32 v40, 0x42800000, v62
	v_mul_f32_e32 v38, 0x42800000, v66
	v_med3_f32 v39, v40, s67, v37
	v_med3_f32 v38, v38, s67, v37
	v_cvt_pk_fp8_f32 v44, v39, v38 op_sel:[0,0,1]
	v_mul_f32_e32 v38, 0x42800000, v55
	v_mul_f32_e32 v39, 0x42800000, v59
	v_med3_f32 v38, v38, s67, v37
; __device__ __forceinline__ void cvt_item8(const float* src, int ld, int k0, int c0, unsigned char* dst, int Kd, int drow0, unsigned char* scr, int lane) {
;     ...
;     for (int g = 0; g < 4; ++g)
; #pragma unroll
;         for (int i = 0; i < 4; ++i) *(unsigned*)(scr + (4 * c + i) * 132 + 32 * g + 4 * q) = pg8::pack_fp8x4(v[g][0][i] * WSC, v[g][1][i] * WSC, v[g][2][i] * WSC, v[g][3][i] * WSC);
;     asm volatile("s_waitcnt lgkmcnt(0)" ::: "memory");
; #pragma unroll
;     for (int r = 0; r < 4; ++r) { const int n = 8 * r + (lane >> 3), ch = lane & 7; const unsigned char* p = scr + n * 132 + ch * 16;
;         u32x4 o; o.x = *(const unsigned*)(p); o.y = *(const unsigned*)(p + 4); o.z = *(const unsigned*)(p + 8); o.w = *(const unsigned*)(p + 12);
;         *(u32x4*)(dst + (size_t)(drow0 + n) * Kd + k0 + 16 * ch) = o; }
;     asm volatile("s_waitcnt lgkmcnt(0)" ::: "memory");
	v_med3_f32 v39, v39, s67, v37
	v_mov_b32_e32 v45, v11
	v_cvt_pk_fp8_f32 v45, v38, v39
	v_mul_f32_e32 v40, 0x42800000, v63
	v_mul_f32_e32 v38, 0x42800000, v67
	v_med3_f32 v39, v40, s67, v37
	v_med3_f32 v38, v38, s67, v37
	v_cvt_pk_fp8_f32 v45, v39, v38 op_sel:[0,0,1]
	v_mul_f32_e32 v38, 0x42800000, v56
	v_mul_f32_e32 v39, 0x42800000, v60
	v_med3_f32 v38, v38, s67, v37
	v_med3_f32 v39, v39, s67, v37
	v_mov_b32_e32 v47, v11
	v_cvt_pk_fp8_f32 v47, v38, v39
	v_mul_f32_e32 v40, 0x42800000, v64
	v_mul_f32_e32 v38, 0x42800000, v68
	v_med3_f32 v39, v40, s67, v37
	v_med3_f32 v38, v38, s67, v37
	v_cvt_pk_fp8_f32 v47, v39, v38 op_sel:[0,0,1]
	v_mul_f32_e32 v38, 0x42800000, v57
	v_mul_f32_e32 v39, 0x42800000, v61
	v_med3_f32 v38, v38, s67, v37
	v_med3_f32 v39, v39, s67, v37
	v_mov_b32_e32 v48, v11
	v_cvt_pk_fp8_f32 v48, v38, v39
	v_mul_f32_e32 v40, 0x42800000, v65
	v_mul_f32_e32 v38, 0x42800000, v69
	v_med3_f32 v39, v40, s67, v37
	v_med3_f32 v38, v38, s67, v37
	v_add_u32_e32 v1, v22, v23
	v_cvt_pk_fp8_f32 v48, v39, v38 op_sel:[0,0,1]
	v_mul_f32_e32 v38, 0x42800000, v70
	v_mul_f32_e32 v39, 0x42800000, v74
	ds_write2_b32 v1, v46, v44 offset1:8
	ds_write2_b32 v1, v43, v45 offset0:33 offset1:41
	ds_write2_b32 v1, v42, v47 offset0:66 offset1:74
	ds_write2_b32 v1, v41, v48 offset0:99 offset1:107
	v_med3_f32 v38, v38, s67, v37
	v_med3_f32 v39, v39, s67, v37
	v_mov_b32_e32 v41, v11
	v_cvt_pk_fp8_f32 v41, v38, v39
	v_mul_f32_e32 v40, 0x42800000, v78
	v_mul_f32_e32 v38, 0x42800000, v82
	v_med3_f32 v39, v40, s67, v37
	v_med3_f32 v38, v38, s67, v37
	v_cvt_pk_fp8_f32 v41, v39, v38 op_sel:[0,0,1]
	v_mul_f32_e32 v38, 0x42800000, v71
	v_mul_f32_e32 v39, 0x42800000, v75
	v_med3_f32 v38, v38, s67, v37
	v_med3_f32 v39, v39, s67, v37
	v_mov_b32_e32 v42, v11
	v_cvt_pk_fp8_f32 v42, v38, v39
	v_mul_f32_e32 v40, 0x42800000, v79
	v_mul_f32_e32 v38, 0x42800000, v83
	v_med3_f32 v39, v40, s67, v37
	v_med3_f32 v38, v38, s67, v37
	v_cvt_pk_fp8_f32 v42, v39, v38 op_sel:[0,0,1]
	v_mul_f32_e32 v38, 0x42800000, v72
	v_mul_f32_e32 v39, 0x42800000, v76
	v_med3_f32 v38, v38, s67, v37
	v_med3_f32 v39, v39, s67, v37
	v_mov_b32_e32 v43, v11
	v_cvt_pk_fp8_f32 v43, v38, v39
	v_mul_f32_e32 v40, 0x42800000, v80
	v_mul_f32_e32 v38, 0x42800000, v84
	v_med3_f32 v39, v40, s67, v37
	v_med3_f32 v38, v38, s67, v37
	v_cvt_pk_fp8_f32 v43, v39, v38 op_sel:[0,0,1]
	v_mul_f32_e32 v38, 0x42800000, v73
	v_mul_f32_e32 v39, 0x42800000, v77
	v_med3_f32 v38, v38, s67, v37
	v_med3_f32 v39, v39, s67, v37
	v_mov_b32_e32 v44, v11
	v_cvt_pk_fp8_f32 v44, v38, v39
	v_mul_f32_e32 v40, 0x42800000, v81
	v_mul_f32_e32 v38, 0x42800000, v85
	v_med3_f32 v39, v40, s67, v37
	v_med3_f32 v38, v38, s67, v37
	v_mul_f32_e32 v2, 0x42800000, v2
	v_mul_f32_e32 v6, 0x42800000, v6
	v_cvt_pk_fp8_f32 v44, v39, v38 op_sel:[0,0,1]
	v_med3_f32 v2, v2, s67, v37
	v_med3_f32 v6, v6, s67, v37
	v_mov_b32_e32 v39, v11
	v_cvt_pk_fp8_f32 v39, v2, v6
	v_mul_f32_e32 v38, 0x42800000, v86
	v_mul_f32_e32 v2, 0x42800000, v90
	v_med3_f32 v6, v38, s67, v37
	v_med3_f32 v2, v2, s67, v37
	v_cvt_pk_fp8_f32 v39, v6, v2 op_sel:[0,0,1]
	v_mul_f32_e32 v2, 0x42800000, v3
	v_mul_f32_e32 v3, 0x42800000, v7
	v_med3_f32 v2, v2, s67, v37
	v_med3_f32 v3, v3, s67, v37
	v_mov_b32_e32 v7, v11
	v_cvt_pk_fp8_f32 v7, v2, v3
	v_mul_f32_e32 v6, 0x42800000, v87
	v_mul_f32_e32 v2, 0x42800000, v91
	v_med3_f32 v3, v6, s67, v37
	v_med3_f32 v2, v2, s67, v37
	v_cvt_pk_fp8_f32 v7, v3, v2 op_sel:[0,0,1]
	v_mul_f32_e32 v2, 0x42800000, v4
	v_mul_f32_e32 v3, 0x42800000, v8
	v_med3_f32 v2, v2, s67, v37
	v_med3_f32 v3, v3, s67, v37
	v_mov_b32_e32 v6, v11
	v_cvt_pk_fp8_f32 v6, v2, v3
	v_mul_f32_e32 v4, 0x42800000, v88
	v_mul_f32_e32 v2, 0x42800000, v92
	v_med3_f32 v3, v4, s67, v37
	v_med3_f32 v2, v2, s67, v37
	v_cvt_pk_fp8_f32 v6, v3, v2 op_sel:[0,0,1]
	v_mul_f32_e32 v2, 0x42800000, v5
	v_mul_f32_e32 v3, 0x42800000, v9
	v_med3_f32 v2, v2, s67, v37
	v_med3_f32 v3, v3, s67, v37
	v_mov_b32_e32 v5, v11
	v_cvt_pk_fp8_f32 v5, v2, v3
	v_mul_f32_e32 v4, 0x42800000, v89
	v_mul_f32_e32 v2, 0x42800000, v93
	v_med3_f32 v3, v4, s67, v37
	v_med3_f32 v2, v2, s67, v37
	v_cvt_pk_fp8_f32 v5, v3, v2 op_sel:[0,0,1]
	ds_write2_b32 v1, v41, v39 offset0:16 offset1:24
	ds_write2_b32 v1, v42, v7 offset0:49 offset1:57
	ds_write2_b32 v1, v43, v6 offset0:82 offset1:90
	ds_write2_b32 v1, v44, v5 offset0:115 offset1:123
	s_waitcnt lgkmcnt(0)
	v_add_u32_e32 v1, v24, v25
	ds_read2_b32 v[2:3], v1 offset1:1
	ds_read2_b32 v[4:5], v1 offset0:2 offset1:3
	v_or_b32_e32 v6, s16, v20
	v_ashrrev_i32_e32 v7, 31, v6
	v_lshl_add_u64 v[38:39], v[18:19], 0, s[18:19]
	v_lshlrev_b64 v[6:7], 11, v[6:7]
	v_lshl_add_u64 v[40:41], v[38:39], 0, v[6:7]
	v_add_u32_e32 v6, 0x420, v1
	v_add_u32_e32 v8, 0x428, v1
	ds_read2_b32 v[6:7], v6 offset1:1
	ds_read2_b32 v[8:9], v8 offset1:1
	s_waitcnt lgkmcnt(2)
	global_store_dwordx4 v[40:41], v[2:5], off
	s_nop 1
	v_or_b32_e32 v2, s16, v26
	v_ashrrev_i32_e32 v3, 31, v2
	v_lshlrev_b64 v[2:3], 11, v[2:3]
	v_lshl_add_u64 v[2:3], v[38:39], 0, v[2:3]
	s_waitcnt lgkmcnt(0)
	global_store_dwordx4 v[2:3], v[6:9], off
	v_add_u32_e32 v2, 0x840, v1
	v_add_u32_e32 v4, 0x848, v1
	ds_read2_b32 v[2:3], v2 offset1:1
	ds_read2_b32 v[4:5], v4 offset1:1
	v_or_b32_e32 v6, s16, v27
	v_ashrrev_i32_e32 v7, 31, v6
	v_lshlrev_b64 v[6:7], 11, v[6:7]
	v_lshl_add_u64 v[40:41], v[38:39], 0, v[6:7]
	v_add_u32_e32 v6, 0xc60, v1
	v_add_u32_e32 v1, 0xc68, v1
	ds_read2_b32 v[6:7], v6 offset1:1
	ds_read2_b32 v[8:9], v1 offset1:1
	s_waitcnt lgkmcnt(2)
	global_store_dwordx4 v[40:41], v[2:5], off
	s_nop 1
	v_or_b32_e32 v2, s16, v28
	v_ashrrev_i32_e32 v3, 31, v2
	v_lshlrev_b64 v[2:3], 11, v[2:3]
	v_lshl_add_u64 v[2:3], v[38:39], 0, v[2:3]
	s_waitcnt lgkmcnt(0)
	global_store_dwordx4 v[2:3], v[6:9], off
	s_waitcnt lgkmcnt(0)
	s_branch .LBB0_506
; __device__ __forceinline__ void cvt_item_i8(const float* src, int ld, int k0, int c0, unsigned char* dst, int Kd, int drow0, const float* cmx  , unsigned char* scr, int lane) {
;     const int c = lane & 7, q = lane >> 3;
;     const f32x4 cm = *(const f32x4*)(cmx + 4 * c);
;     f32x4 inv; inv[0] = cm[0] > 0.f ? 127.f / cm[0] : 0.f; inv[1] = cm[1] > 0.f ? 127.f / cm[1] : 0.f; inv[2] = cm[2] > 0.f ? 127.f / cm[2] : 0.f; inv[3] = cm[3] > 0.f ? 127.f / cm[3] : 0.f;
;     f32x4 v[4][4];
; #pragma unroll
;     for (int g = 0; g < 4; ++g)
; #pragma unroll
;         for (int j = 0; j < 4; ++j) v[g][j] = __builtin_nontemporal_load((const f32x4*)(src + (size_t)(k0 + 32 * g + 4 * q + j) * ld + c0 + 4 * c));
; template <int L>
; __device__ __forceinline__ void layer(Frame& F, const XcdBarrier& bar, float* out, const int lo, const int hi) {
;     ...
;         if (cls == 0) { conv_all<GRP>(F, (F.G == 256) ? ((L == 0) ? SLOT_FIRST0 : SLOT_FIRST1) : 0); if (L == 0 && F.G == 256) { const int e4 = F.gw - G4_SLACK0; if (e4 >= 0 && e4 < G4_TAIL) conv_item<4>(F, 2048 + e4); } __syncthreads(); }
.LBB0_524:
	v_readlane_b32 s3, v255, 10
	s_addk_i32 s3, 0xf980
	s_cmpk_gt_u32 s3, 0x17f
	s_cselect_b64 s[6:7], -1, 0
	s_xor_b64 s[0:1], s[0:1], -1
	s_or_b64 s[0:1], s[0:1], s[6:7]
	s_and_b64 vcc, exec, s[0:1]
	s_cbranch_vccnz .LBB0_526
	v_readlane_b32 s1, v255, 10
	s_addk_i32 s1, 0x180
	s_and_b32 s3, s1, 0xffff
	s_mul_i32 s3, s3, 0xd795
	s_lshr_b32 s4, s3, 16
	s_lshr_b32 s3, s3, 23
	s_mulk_i32 s3, 0x98
	s_sub_i32 s1, s1, s3
	v_readlane_b32 s0, v255, 9
	s_and_b32 s3, s1, 0xffff
	s_lshl_b32 s1, s1, 5
	s_mulk_i32 s0, 0x2200
	s_and_b32 s1, s1, 0xffe0
	s_add_i32 s0, s0, 0
	s_or_b32 s6, s1, 8
	s_cmpk_lt_u32 s3, 0x70
	s_cselect_b32 s8, s1, s6
	s_add_i32 s3, 0, 0x20240
	s_lshl_b32 s6, s1, 2
	s_add_u32 s6, s50, s6
	v_and_b32_e32 v68, 7, v0
	s_addc_u32 s7, s51, 0
	s_waitcnt vmcnt(14)
	v_lshlrev_b32_e32 v34, 4, v68
	v_mov_b32_e32 v35, 0
	s_waitcnt lgkmcnt(3)
	v_lshl_add_u64 v[2:3], s[6:7], 0, v[34:35]
	s_mov_b32 s6, 0xbb000
	v_add_co_u32_e32 v2, vcc, s6, v2
	s_waitcnt lgkmcnt(1)
	v_mov_b32_e32 v6, s3
	v_addc_co_u32_e32 v3, vcc, 0, v3, vcc
	global_load_dwordx4 v[2:5], v[2:3], off offset:3072
	s_waitcnt lgkmcnt(0)
	ds_read_b64 v[8:9], v6
	v_lshrrev_b32_e32 v1, 3, v194
	s_and_b32 s3, s4, 0xff80
	s_lshl_b32 s4, s8, 2
	v_lshlrev_b32_e32 v69, 2, v1
	s_waitcnt lgkmcnt(0)
	v_readfirstlane_b32 s6, v8
	v_readfirstlane_b32 s7, v9
	s_add_u32 s6, s6, s4
	v_or_b32_e32 v6, s3, v69
	s_addc_u32 s7, s7, 0
	s_mov_b32 s12, 0x42fe0000
	v_mov_b32_e32 v7, v35
	v_mul_u32_u24_e32 v6, 0x4c20, v6
	v_lshl_add_u64 v[8:9], s[6:7], 0, v[34:35]
	v_lshl_add_u64 v[10:11], v[8:9], 0, v[6:7]
	s_mov_b32 s9, 0x2610000
	v_add_co_u32_e32 v6, vcc, s9, v10
	s_mov_b32 s13, 0x2614000
	s_nop 0
	v_addc_co_u32_e32 v7, vcc, 0, v11, vcc
	s_mov_b32 s4, 0x2619000
	v_mov_b32_e32 v74, 0x42fe0000
	s_waitcnt vmcnt(0)
	v_div_scale_f32 v8, s[6:7], v2, v2, s12
	v_div_scale_f32 v12, s[6:7], v3, v3, s12
	v_rcp_f32_e32 v18, v8
	v_rcp_f32_e32 v19, v12
	v_div_scale_f32 v14, s[8:9], v4, v4, s12
	v_rcp_f32_e32 v20, v14
	v_fma_f32 v22, -v8, v18, 1.0
	v_div_scale_f32 v9, vcc, s12, v2, s12
	v_fma_f32 v23, -v12, v19, 1.0
	v_fmac_f32_e32 v18, v22, v18
	v_div_scale_f32 v13, s[6:7], s12, v3, s12
	v_fmac_f32_e32 v19, v23, v19
	v_mul_f32_e32 v22, v9, v18
	v_fma_f32 v24, -v14, v20, 1.0
	v_mul_f32_e32 v23, v13, v19
	v_fma_f32 v26, -v8, v22, v9
	v_div_scale_f32 v15, s[8:9], s12, v4, s12
	v_fmac_f32_e32 v20, v24, v20
	v_fma_f32 v27, -v12, v23, v13
	v_fmac_f32_e32 v22, v26, v18
	v_mul_f32_e32 v24, v15, v20
	v_fmac_f32_e32 v23, v27, v19
	v_fma_f32 v8, -v8, v22, v9
	v_fma_f32 v28, -v14, v24, v15
	v_fma_f32 v9, -v12, v23, v13
	v_div_fmas_f32 v8, v8, v18, v22
	s_mov_b64 vcc, s[6:7]
	v_fmac_f32_e32 v24, v28, v20
	v_div_fixup_f32 v8, v8, v2, s12
	v_div_fmas_f32 v9, v9, v19, v23
	v_cmp_lt_f32_e32 vcc, 0, v2
	v_fma_f32 v12, -v14, v24, v15
	v_div_fixup_f32 v2, v9, v3, s12
	v_cndmask_b32_e32 v70, 0, v8, vcc
	s_mov_b64 vcc, s[8:9]
	v_div_fmas_f32 v8, v12, v20, v24
	v_cmp_lt_f32_e32 vcc, 0, v3
	v_div_scale_f32 v16, s[10:11], v5, v5, s12
	s_nop 0
	v_cndmask_b32_e32 v71, 0, v2, vcc
	v_div_fixup_f32 v2, v8, v4, s12
	v_cmp_lt_f32_e32 vcc, 0, v4
	v_rcp_f32_e32 v21, v16
	v_div_scale_f32 v17, s[10:11], s12, v5, s12
	v_cndmask_b32_e32 v72, 0, v2, vcc
	v_add_co_u32_e32 v2, vcc, s13, v10
	v_fma_f32 v25, -v16, v21, 1.0
	s_nop 0
	v_addc_co_u32_e32 v3, vcc, 0, v11, vcc
	global_load_dwordx4 v[36:39], v[6:7], off nt
	global_load_dwordx4 v[40:43], v[2:3], off offset:3104 nt
	v_add_co_u32_e32 v2, vcc, s4, v10
	s_mov_b32 s4, 0x261e000
	s_nop 0
	v_addc_co_u32_e32 v3, vcc, 0, v11, vcc
	v_add_co_u32_e32 v6, vcc, s4, v10
	v_fmac_f32_e32 v21, v25, v21
	s_nop 0
	v_addc_co_u32_e32 v7, vcc, 0, v11, vcc
	global_load_dwordx4 v[44:47], v[2:3], off offset:2112 nt
	global_load_dwordx4 v[48:51], v[6:7], off offset:1120 nt
	v_mul_f32_e32 v25, v17, v21
	v_fma_f32 v29, -v16, v25, v17
	v_fmac_f32_e32 v25, v29, v21
	v_fma_f32 v13, -v16, v25, v17
	s_mov_b64 vcc, s[10:11]
	v_div_fmas_f32 v2, v13, v21, v25
	v_div_fixup_f32 v2, v2, v5, s12
	v_cmp_lt_f32_e32 vcc, 0, v5
	s_mov_b32 s4, 0x26a8000
	s_mov_b32 s6, 0xc0c0500
	v_cndmask_b32_e32 v73, 0, v2, vcc
	v_add_co_u32_e32 v2, vcc, s4, v10
	s_mov_b32 s4, 0x26ad000
	s_nop 0
	v_addc_co_u32_e32 v3, vcc, 0, v11, vcc
	v_add_co_u32_e32 v4, vcc, s4, v10
	s_mov_b32 s4, 0x26b1000
	s_nop 0
	v_addc_co_u32_e32 v5, vcc, 0, v11, vcc
	global_load_dwordx4 v[52:55], v[2:3], off offset:1024 nt
	global_load_dwordx4 v[56:59], v[4:5], off offset:32 nt
	v_add_co_u32_e32 v2, vcc, s4, v10
	s_mov_b32 s4, 0x26b6000
	s_nop 0
	v_addc_co_u32_e32 v3, vcc, 0, v11, vcc
	v_add_co_u32_e32 v4, vcc, s4, v10
	s_mov_b32 s4, 0x2740000
	s_nop 0
	v_addc_co_u32_e32 v5, vcc, 0, v11, vcc
	global_load_dwordx4 v[60:63], v[2:3], off offset:3136 nt
	global_load_dwordx4 v[64:67], v[4:5], off offset:2144 nt
	v_add_co_u32_e32 v2, vcc, s4, v10
	s_mov_b32 s4, 0x2745000
	s_nop 0
	v_addc_co_u32_e32 v3, vcc, 0, v11, vcc
	v_add_co_u32_e32 v4, vcc, s4, v10
	s_mov_b32 s4, 0x274a000
	s_nop 0
	v_addc_co_u32_e32 v5, vcc, 0, v11, vcc
	global_load_dwordx4 v[18:21], v[2:3], off offset:2048 nt
	global_load_dwordx4 v[22:25], v[4:5], off offset:1056 nt
	v_add_co_u32_e32 v2, vcc, s4, v10
	s_mov_b32 s4, 0x274e000
	s_nop 0
	v_addc_co_u32_e32 v3, vcc, 0, v11, vcc
	v_add_co_u32_e32 v4, vcc, s4, v10
	s_mov_b32 s4, 0x27d8000
	s_nop 0
	v_addc_co_u32_e32 v5, vcc, 0, v11, vcc
	global_load_dwordx4 v[26:29], v[2:3], off offset:64 nt
	global_load_dwordx4 v[30:33], v[4:5], off offset:3168 nt
	v_add_co_u32_e32 v2, vcc, s4, v10
	s_mov_b32 s4, 0x27dd000
	s_nop 0
	v_addc_co_u32_e32 v3, vcc, 0, v11, vcc
	v_add_co_u32_e32 v6, vcc, s4, v10
	s_mov_b32 s4, 0x27e2000
	s_nop 0
	v_addc_co_u32_e32 v7, vcc, 0, v11, vcc
	v_add_co_u32_e32 v12, vcc, s4, v10
	s_mov_b32 s4, 0x27e7000
	s_nop 0
	v_addc_co_u32_e32 v13, vcc, 0, v11, vcc
	global_load_dwordx4 v[2:5], v[2:3], off offset:3072 nt
	s_nop 0
	global_load_dwordx4 v[6:9], v[6:7], off offset:2080 nt
	v_add_co_u32_e32 v14, vcc, s4, v10
	s_waitcnt vmcnt(0) lgkmcnt(0)
; __device__ __forceinline__ void cvt_item_i8(const float* src, int ld, int k0, int c0, unsigned char* dst, int Kd, int drow0, const float* cmx  , unsigned char* scr, int lane) {
;     ...
;         for (int j = 0; j < 4; ++j) v[g][j] = __builtin_nontemporal_load((const f32x4*)(src + (size_t)(k0 + 32 * g + 4 * q + j) * ld + c0 + 4 * c));
; #pragma unroll
;     for (int g = 0; g < 4; ++g)
; #pragma unroll
;         for (int i = 0; i < 4; ++i) *(unsigned*)(scr + (4 * c + i) * 132 + 32 * g + 4 * q) = pack_i8x4(v[g][0][i] * inv[i], v[g][1][i] * inv[i], v[g][2][i] * inv[i], v[g][3][i] * inv[i]);
	v_mul_f32_e32 v40, v70, v40
	v_addc_co_u32_e32 v15, vcc, 0, v11, vcc
	global_load_dwordx4 v[10:13], v[12:13], off offset:1088 nt
	s_nop 0
	global_load_dwordx4 v[14:17], v[14:15], off offset:96 nt
	s_mov_b32 s4, 0xc2fe0000
	v_mul_f32_e32 v36, v36, v70
	v_mul_f32_e32 v44, v70, v44
	v_med3_f32 v40, v40, s4, v74
	v_med3_f32 v36, v36, s4, v74
	v_rndne_f32_e32 v40, v40
	v_med3_f32 v44, v44, s4, v74
	v_rndne_f32_e32 v36, v36
	v_cvt_i32_f32_e32 v40, v40
	v_rndne_f32_e32 v44, v44
	v_cvt_i32_f32_e32 v36, v36
	v_cvt_i32_f32_sdwa v44, v44 dst_sel:WORD_1 dst_unused:UNUSED_PAD src0_sel:DWORD
	v_lshlrev_b32_e32 v40, 8, v40
	v_mul_f32_e32 v41, v71, v41
	v_perm_b32 v36, v40, v36, s6
	v_and_b32_e32 v40, 0xff0000, v44
	v_mul_f32_e32 v37, v37, v71
	v_mul_f32_e32 v44, v71, v45
	v_med3_f32 v41, v41, s4, v74
	v_mul_f32_e32 v45, v71, v49
	v_med3_f32 v37, v37, s4, v74
	v_rndne_f32_e32 v41, v41
	v_med3_f32 v44, v44, s4, v74
	v_rndne_f32_e32 v37, v37
	v_cvt_i32_f32_e32 v41, v41
	v_rndne_f32_e32 v44, v44
	v_med3_f32 v45, v45, s4, v74
	v_cvt_i32_f32_e32 v37, v37
	v_cvt_i32_f32_sdwa v44, v44 dst_sel:WORD_1 dst_unused:UNUSED_PAD src0_sel:DWORD
	v_rndne_f32_e32 v45, v45
	v_cvt_i32_f32_sdwa v45, v45 dst_sel:BYTE_3 dst_unused:UNUSED_PAD src0_sel:DWORD
	v_lshlrev_b32_e32 v41, 8, v41
	v_perm_b32 v37, v41, v37, s6
	v_and_b32_e32 v41, 0xff0000, v44
	v_or3_b32 v37, v37, v41, v45
	v_mul_f32_e32 v41, v72, v42
	v_mul_f32_e32 v38, v38, v72
	v_mul_f32_e32 v42, v72, v46
	v_med3_f32 v41, v41, s4, v74
	v_mul_f32_e32 v44, v72, v50
	v_med3_f32 v38, v38, s4, v74
	v_rndne_f32_e32 v41, v41
	v_med3_f32 v42, v42, s4, v74
	v_rndne_f32_e32 v38, v38
	v_cvt_i32_f32_e32 v41, v41
	v_rndne_f32_e32 v42, v42
	v_med3_f32 v44, v44, s4, v74
	v_cvt_i32_f32_e32 v38, v38
	v_cvt_i32_f32_sdwa v42, v42 dst_sel:WORD_1 dst_unused:UNUSED_PAD src0_sel:DWORD
	v_rndne_f32_e32 v44, v44
	v_cvt_i32_f32_sdwa v44, v44 dst_sel:BYTE_3 dst_unused:UNUSED_PAD src0_sel:DWORD
	v_lshlrev_b32_e32 v41, 8, v41
	v_perm_b32 v38, v41, v38, s6
	v_and_b32_e32 v41, 0xff0000, v42
	v_or3_b32 v38, v38, v41, v44
	v_mul_f32_e32 v41, v73, v43
	v_mul_f32_e32 v39, v39, v73
	v_mul_f32_e32 v42, v73, v47
	v_med3_f32 v41, v41, s4, v74
	v_mul_f32_e32 v43, v73, v51
	v_med3_f32 v39, v39, s4, v74
	v_rndne_f32_e32 v41, v41
	v_med3_f32 v42, v42, s4, v74
	v_rndne_f32_e32 v39, v39
	v_cvt_i32_f32_e32 v41, v41
	v_rndne_f32_e32 v42, v42
	v_med3_f32 v43, v43, s4, v74
	v_cvt_i32_f32_e32 v39, v39
	v_cvt_i32_f32_sdwa v42, v42 dst_sel:WORD_1 dst_unused:UNUSED_PAD src0_sel:DWORD
	v_rndne_f32_e32 v43, v43
	v_cvt_i32_f32_sdwa v43, v43 dst_sel:BYTE_3 dst_unused:UNUSED_PAD src0_sel:DWORD
	v_lshlrev_b32_e32 v41, 8, v41
	v_perm_b32 v39, v41, v39, s6
	v_and_b32_e32 v41, 0xff0000, v42
	v_mul_f32_e32 v42, v70, v56
	v_mul_f32_e32 v48, v70, v48
	v_or3_b32 v39, v39, v41, v43
	v_mul_f32_e32 v41, v70, v52
	v_mul_f32_e32 v43, v70, v60
	v_med3_f32 v42, v42, s4, v74
	v_mul_f32_e32 v22, v70, v22
	v_mul_f32_e32 v6, v70, v6
	v_med3_f32 v48, v48, s4, v74
	v_mul_f32_e32 v44, v70, v64
	v_med3_f32 v41, v41, s4, v74
	v_rndne_f32_e32 v42, v42
	v_med3_f32 v43, v43, s4, v74
	v_mul_f32_e32 v18, v70, v18
	v_mul_f32_e32 v26, v70, v26
	v_med3_f32 v22, v22, s4, v74
	v_mul_f32_e32 v2, v70, v2
	s_waitcnt vmcnt(0) lgkmcnt(0)
	v_mul_f32_e32 v10, v70, v10
	v_med3_f32 v6, v6, s4, v74
	v_rndne_f32_e32 v48, v48
	v_rndne_f32_e32 v41, v41
	v_cvt_i32_f32_e32 v42, v42
	v_rndne_f32_e32 v43, v43
	v_med3_f32 v44, v44, s4, v74
	v_mul_f32_e32 v30, v70, v30
	v_med3_f32 v18, v18, s4, v74
	v_rndne_f32_e32 v22, v22
	v_med3_f32 v26, v26, s4, v74
	v_mul_f32_e32 v14, v70, v14
	v_med3_f32 v2, v2, s4, v74
	v_rndne_f32_e32 v6, v6
	v_med3_f32 v10, v10, s4, v74
	v_cvt_i32_f32_sdwa v48, v48 dst_sel:BYTE_3 dst_unused:UNUSED_PAD src0_sel:DWORD
	v_cvt_i32_f32_e32 v41, v41
	v_cvt_i32_f32_sdwa v43, v43 dst_sel:WORD_1 dst_unused:UNUSED_PAD src0_sel:DWORD
	v_rndne_f32_e32 v44, v44
	v_rndne_f32_e32 v18, v18
	v_cvt_i32_f32_e32 v22, v22
	v_rndne_f32_e32 v26, v26
	v_med3_f32 v30, v30, s4, v74
	v_rndne_f32_e32 v2, v2
	v_cvt_i32_f32_e32 v6, v6
	v_rndne_f32_e32 v10, v10
	v_med3_f32 v14, v14, s4, v74
	v_cvt_i32_f32_sdwa v44, v44 dst_sel:BYTE_3 dst_unused:UNUSED_PAD src0_sel:DWORD
	v_cvt_i32_f32_e32 v18, v18
	v_cvt_i32_f32_sdwa v26, v26 dst_sel:WORD_1 dst_unused:UNUSED_PAD src0_sel:DWORD
	v_rndne_f32_e32 v30, v30
	v_cvt_i32_f32_e32 v2, v2
	v_cvt_i32_f32_sdwa v10, v10 dst_sel:WORD_1 dst_unused:UNUSED_PAD src0_sel:DWORD
	v_rndne_f32_e32 v14, v14
	v_cvt_i32_f32_sdwa v30, v30 dst_sel:BYTE_3 dst_unused:UNUSED_PAD src0_sel:DWORD
	v_cvt_i32_f32_sdwa v14, v14 dst_sel:BYTE_3 dst_unused:UNUSED_PAD src0_sel:DWORD
	v_lshlrev_b32_e32 v42, 8, v42
	v_or3_b32 v36, v36, v40, v48
	v_mul_u32_u24_e32 v40, 0x210, v68
	v_perm_b32 v41, v42, v41, s6
	v_and_b32_e32 v42, 0xff0000, v43
	v_lshlrev_b32_e32 v22, 8, v22
	v_lshlrev_b32_e32 v6, 8, v6
	v_add3_u32 v40, s0, v69, v40
	v_or3_b32 v41, v41, v42, v44
	v_perm_b32 v18, v22, v18, s6
	v_and_b32_e32 v22, 0xff0000, v26
	v_perm_b32 v2, v6, v2, s6
	v_and_b32_e32 v6, 0xff0000, v10
	ds_write2_b32 v40, v36, v41 offset1:8
	v_mul_f32_e32 v41, v71, v57
	v_or3_b32 v18, v18, v22, v30
	v_or3_b32 v2, v2, v6, v14
	v_mul_f32_e32 v36, v71, v53
	v_mul_f32_e32 v42, v71, v61
	v_med3_f32 v41, v41, s4, v74
	v_mul_f32_e32 v22, v71, v23
	ds_write2_b32 v40, v18, v2 offset0:16 offset1:24
	v_mul_f32_e32 v2, v71, v3
	v_mul_f32_e32 v3, v71, v7
	v_mul_f32_e32 v43, v71, v65
	v_med3_f32 v36, v36, s4, v74
	v_rndne_f32_e32 v41, v41
	v_med3_f32 v42, v42, s4, v74
	v_mul_f32_e32 v19, v71, v19
	v_mul_f32_e32 v23, v71, v27
	v_med3_f32 v22, v22, s4, v74
	v_mul_f32_e32 v6, v71, v11
	v_med3_f32 v3, v3, s4, v74
	v_rndne_f32_e32 v36, v36
	v_cvt_i32_f32_e32 v41, v41
; __device__ __forceinline__ void cvt_item_i8(const float* src, int ld, int k0, int c0, unsigned char* dst, int Kd, int drow0, const float* cmx  , unsigned char* scr, int lane) {
;     ...
;     for (int g = 0; g < 4; ++g)
; #pragma unroll
;         for (int i = 0; i < 4; ++i) *(unsigned*)(scr + (4 * c + i) * 132 + 32 * g + 4 * q) = pack_i8x4(v[g][0][i] * inv[i], v[g][1][i] * inv[i], v[g][2][i] * inv[i], v[g][3][i] * inv[i]);
;     asm volatile("s_waitcnt lgkmcnt(0)" ::: "memory");
	v_rndne_f32_e32 v42, v42
	v_med3_f32 v43, v43, s4, v74
	v_mul_f32_e32 v26, v71, v31
	v_med3_f32 v19, v19, s4, v74
	v_rndne_f32_e32 v22, v22
	v_med3_f32 v23, v23, s4, v74
	v_mul_f32_e32 v7, v71, v15
	v_med3_f32 v2, v2, s4, v74
	v_rndne_f32_e32 v3, v3
	v_med3_f32 v6, v6, s4, v74
	v_cvt_i32_f32_e32 v36, v36
	v_cvt_i32_f32_sdwa v42, v42 dst_sel:WORD_1 dst_unused:UNUSED_PAD src0_sel:DWORD
	v_rndne_f32_e32 v43, v43
	v_rndne_f32_e32 v19, v19
	v_cvt_i32_f32_e32 v22, v22
	v_rndne_f32_e32 v23, v23
	v_med3_f32 v26, v26, s4, v74
	v_rndne_f32_e32 v2, v2
	v_cvt_i32_f32_e32 v3, v3
	v_rndne_f32_e32 v6, v6
	v_med3_f32 v7, v7, s4, v74
	v_cvt_i32_f32_sdwa v43, v43 dst_sel:BYTE_3 dst_unused:UNUSED_PAD src0_sel:DWORD
	v_cvt_i32_f32_e32 v19, v19
	v_cvt_i32_f32_sdwa v23, v23 dst_sel:WORD_1 dst_unused:UNUSED_PAD src0_sel:DWORD
	v_rndne_f32_e32 v26, v26
	v_cvt_i32_f32_e32 v2, v2
	v_cvt_i32_f32_sdwa v6, v6 dst_sel:WORD_1 dst_unused:UNUSED_PAD src0_sel:DWORD
	v_rndne_f32_e32 v7, v7
	v_cvt_i32_f32_sdwa v26, v26 dst_sel:BYTE_3 dst_unused:UNUSED_PAD src0_sel:DWORD
	v_cvt_i32_f32_sdwa v7, v7 dst_sel:BYTE_3 dst_unused:UNUSED_PAD src0_sel:DWORD
	v_lshlrev_b32_e32 v41, 8, v41
	v_perm_b32 v36, v41, v36, s6
	v_and_b32_e32 v41, 0xff0000, v42
	v_lshlrev_b32_e32 v22, 8, v22
	v_lshlrev_b32_e32 v3, 8, v3
	v_or3_b32 v36, v36, v41, v43
	v_perm_b32 v19, v22, v19, s6
	v_and_b32_e32 v22, 0xff0000, v23
	v_perm_b32 v2, v3, v2, s6
	v_and_b32_e32 v3, 0xff0000, v6
	ds_write2_b32 v40, v37, v36 offset0:33 offset1:41
	v_mul_f32_e32 v37, v72, v58
	v_or3_b32 v19, v19, v22, v26
	v_mul_f32_e32 v22, v72, v24
	v_or3_b32 v2, v2, v3, v7
	v_mul_f32_e32 v3, v72, v8
	v_mul_f32_e32 v36, v72, v54
	v_mul_f32_e32 v41, v72, v62
	v_med3_f32 v37, v37, s4, v74
	v_mul_f32_e32 v20, v72, v20
	v_mul_f32_e32 v23, v72, v28
	v_med3_f32 v22, v22, s4, v74
	ds_write2_b32 v40, v19, v2 offset0:49 offset1:57
	v_mul_f32_e32 v2, v72, v4
	v_mul_f32_e32 v4, v72, v12
	v_med3_f32 v3, v3, s4, v74
	v_mul_f32_e32 v42, v72, v66
	v_med3_f32 v36, v36, s4, v74
	v_rndne_f32_e32 v37, v37
	v_med3_f32 v41, v41, s4, v74
	v_mul_f32_e32 v24, v72, v32
	v_med3_f32 v20, v20, s4, v74
	v_rndne_f32_e32 v22, v22
	v_med3_f32 v23, v23, s4, v74
	v_mul_f32_e32 v6, v72, v16
	v_med3_f32 v2, v2, s4, v74
	v_rndne_f32_e32 v3, v3
	v_med3_f32 v4, v4, s4, v74
	v_rndne_f32_e32 v36, v36
	v_cvt_i32_f32_e32 v37, v37
	v_rndne_f32_e32 v41, v41
	v_med3_f32 v42, v42, s4, v74
	v_rndne_f32_e32 v20, v20
	v_cvt_i32_f32_e32 v22, v22
	v_rndne_f32_e32 v23, v23
	v_med3_f32 v24, v24, s4, v74
	v_rndne_f32_e32 v2, v2
	v_cvt_i32_f32_e32 v3, v3
	v_rndne_f32_e32 v4, v4
	v_med3_f32 v6, v6, s4, v74
	v_cvt_i32_f32_e32 v36, v36
	v_cvt_i32_f32_sdwa v41, v41 dst_sel:WORD_1 dst_unused:UNUSED_PAD src0_sel:DWORD
	v_rndne_f32_e32 v42, v42
	v_cvt_i32_f32_e32 v20, v20
	v_cvt_i32_f32_sdwa v23, v23 dst_sel:WORD_1 dst_unused:UNUSED_PAD src0_sel:DWORD
	v_rndne_f32_e32 v24, v24
	v_cvt_i32_f32_e32 v2, v2
	v_cvt_i32_f32_sdwa v4, v4 dst_sel:WORD_1 dst_unused:UNUSED_PAD src0_sel:DWORD
	v_rndne_f32_e32 v6, v6
	v_cvt_i32_f32_sdwa v42, v42 dst_sel:BYTE_3 dst_unused:UNUSED_PAD src0_sel:DWORD
	v_cvt_i32_f32_sdwa v24, v24 dst_sel:BYTE_3 dst_unused:UNUSED_PAD src0_sel:DWORD
	v_cvt_i32_f32_sdwa v6, v6 dst_sel:BYTE_3 dst_unused:UNUSED_PAD src0_sel:DWORD
	v_lshlrev_b32_e32 v37, 8, v37
	v_lshlrev_b32_e32 v22, 8, v22
	v_lshlrev_b32_e32 v3, 8, v3
	v_perm_b32 v36, v37, v36, s6
	v_and_b32_e32 v37, 0xff0000, v41
	v_perm_b32 v20, v22, v20, s6
	v_and_b32_e32 v22, 0xff0000, v23
	v_perm_b32 v2, v3, v2, s6
	v_and_b32_e32 v3, 0xff0000, v4
	v_or3_b32 v36, v36, v37, v42
	v_mul_f32_e32 v37, v73, v59
	v_or3_b32 v20, v20, v22, v24
	v_mul_f32_e32 v22, v73, v25
	v_or3_b32 v2, v2, v3, v6
	v_mul_f32_e32 v3, v73, v9
	ds_write2_b32 v40, v38, v36 offset0:66 offset1:74
	v_mul_f32_e32 v36, v73, v55
	v_med3_f32 v37, v37, s4, v74
	v_mul_f32_e32 v21, v73, v21
	v_mul_f32_e32 v23, v73, v29
	v_med3_f32 v22, v22, s4, v74
	ds_write2_b32 v40, v20, v2 offset0:82 offset1:90
	v_mul_f32_e32 v2, v73, v5
	v_mul_f32_e32 v4, v73, v13
	v_med3_f32 v3, v3, s4, v74
	v_mul_f32_e32 v38, v73, v63
	v_med3_f32 v36, v36, s4, v74
	v_rndne_f32_e32 v37, v37
	v_mul_f32_e32 v24, v73, v33
	v_med3_f32 v21, v21, s4, v74
	v_rndne_f32_e32 v22, v22
	v_med3_f32 v23, v23, s4, v74
	v_mul_f32_e32 v5, v73, v17
	v_med3_f32 v2, v2, s4, v74
	v_rndne_f32_e32 v3, v3
	v_med3_f32 v4, v4, s4, v74
	v_mul_f32_e32 v41, v73, v67
	v_rndne_f32_e32 v36, v36
	v_cvt_i32_f32_e32 v37, v37
	v_med3_f32 v38, v38, s4, v74
	v_rndne_f32_e32 v21, v21
	v_cvt_i32_f32_e32 v22, v22
	v_rndne_f32_e32 v23, v23
	v_med3_f32 v24, v24, s4, v74
	v_rndne_f32_e32 v2, v2
	v_cvt_i32_f32_e32 v3, v3
	v_rndne_f32_e32 v4, v4
	v_med3_f32 v5, v5, s4, v74
	v_cvt_i32_f32_e32 v36, v36
	v_rndne_f32_e32 v38, v38
	v_med3_f32 v41, v41, s4, v74
	v_cvt_i32_f32_e32 v21, v21
	v_cvt_i32_f32_sdwa v23, v23 dst_sel:WORD_1 dst_unused:UNUSED_PAD src0_sel:DWORD
	v_rndne_f32_e32 v24, v24
	v_cvt_i32_f32_e32 v2, v2
	v_cvt_i32_f32_sdwa v4, v4 dst_sel:WORD_1 dst_unused:UNUSED_PAD src0_sel:DWORD
	v_rndne_f32_e32 v5, v5
	v_cvt_i32_f32_sdwa v38, v38 dst_sel:WORD_1 dst_unused:UNUSED_PAD src0_sel:DWORD
	v_rndne_f32_e32 v41, v41
	v_cvt_i32_f32_sdwa v24, v24 dst_sel:BYTE_3 dst_unused:UNUSED_PAD src0_sel:DWORD
	v_cvt_i32_f32_sdwa v5, v5 dst_sel:BYTE_3 dst_unused:UNUSED_PAD src0_sel:DWORD
	v_cvt_i32_f32_sdwa v41, v41 dst_sel:BYTE_3 dst_unused:UNUSED_PAD src0_sel:DWORD
	v_lshlrev_b32_e32 v37, 8, v37
	v_lshlrev_b32_e32 v22, 8, v22
	v_lshlrev_b32_e32 v3, 8, v3
	v_perm_b32 v36, v37, v36, s6
	v_perm_b32 v21, v22, v21, s6
	v_and_b32_e32 v22, 0xff0000, v23
	v_perm_b32 v2, v3, v2, s6
	v_and_b32_e32 v3, 0xff0000, v4
	s_add_u32 s6, s50, s3
	v_and_b32_e32 v37, 0xff0000, v38
	v_or3_b32 v21, v21, v22, v24
	v_or3_b32 v2, v2, v3, v5
	s_addc_u32 s7, s51, 0
	v_or3_b32 v36, v36, v37, v41
	ds_write2_b32 v40, v21, v2 offset0:115 offset1:123
	v_lshl_add_u64 v[2:3], s[6:7], 0, v[34:35]
	s_mov_b64 s[6:7], 0x1180000
	ds_write2_b32 v40, v39, v36 offset0:99 offset1:107
	v_lshl_add_u64 v[10:11], v[2:3], 0, s[6:7]
	v_mul_u32_u24_e32 v2, 0x84, v1
	s_waitcnt lgkmcnt(0)
; __device__ __forceinline__ void cvt_item_i8(const float* src, int ld, int k0, int c0, unsigned char* dst, int Kd, int drow0, const float* cmx  , unsigned char* scr, int lane) {
;     ...
;     asm volatile("s_waitcnt lgkmcnt(0)" ::: "memory");
; #pragma unroll
;     for (int r = 0; r < 4; ++r) { const int n = 8 * r + (lane >> 3), ch = lane & 7; const unsigned char* p = scr + n * 132 + ch * 16;
;         u32x4 o; o.x = *(const unsigned*)(p); o.y = *(const unsigned*)(p + 4); o.z = *(const unsigned*)(p + 8); o.w = *(const unsigned*)(p + 12);
;         *(u32x4*)(dst + (size_t)(drow0 + n) * Kd + k0 + 16 * ch) = o; }
;     asm volatile("s_waitcnt lgkmcnt(0)" ::: "memory");
	v_add3_u32 v14, s0, v34, v2
	ds_read2_b32 v[2:3], v14 offset1:1
	ds_read2_b32 v[4:5], v14 offset0:2 offset1:3
	v_or_b32_e32 v1, s1, v1
	v_lshlrev_b32_e32 v34, 11, v1
	v_add_u32_e32 v1, 0x420, v14
	v_add_u32_e32 v8, 0x428, v14
	ds_read2_b32 v[6:7], v1 offset1:1
	ds_read2_b32 v[8:9], v8 offset1:1
	v_lshl_add_u64 v[12:13], v[10:11], 0, v[34:35]
	s_waitcnt lgkmcnt(2)
	global_store_dwordx4 v[12:13], v[2:5], off
	v_add_u32_e32 v1, 0x840, v14
	v_or_b32_e32 v12, 0x8000, v34
	v_or_b32_e32 v2, 0x4000, v34
	v_mov_b32_e32 v3, v35
	v_lshl_add_u64 v[2:3], v[10:11], 0, v[2:3]
	s_waitcnt lgkmcnt(0)
	global_store_dwordx4 v[2:3], v[6:9], off
	v_add_u32_e32 v4, 0x848, v14
	ds_read2_b32 v[2:3], v1 offset1:1
	ds_read2_b32 v[4:5], v4 offset1:1
	v_add_u32_e32 v1, 0xc60, v14
	v_add_u32_e32 v8, 0xc68, v14
	ds_read2_b32 v[6:7], v1 offset1:1
	ds_read2_b32 v[8:9], v8 offset1:1
	v_mov_b32_e32 v13, v35
	v_lshl_add_u64 v[12:13], v[10:11], 0, v[12:13]
	v_or_b32_e32 v34, 0xc000, v34
	s_waitcnt lgkmcnt(2)
	global_store_dwordx4 v[12:13], v[2:5], off
	s_nop 1
	v_lshl_add_u64 v[2:3], v[10:11], 0, v[34:35]
	s_waitcnt lgkmcnt(0)
	global_store_dwordx4 v[2:3], v[6:9], off
	s_waitcnt lgkmcnt(0)

; __device__ __forceinline__ void colmax_item(const float* src, int ld, int k0, int c0, float* cmx  , int lane) {
;     const int c = lane & 7, q = lane >> 3;
;     f32x4 mx = (f32x4){0.f, 0.f, 0.f, 0.f};
; #pragma unroll
;     for (int g = 0; g < 4; ++g)
; #pragma unroll
;         for (int j = 0; j < 4; ++j) { const f32x4 v = *(const f32x4*)(src + (size_t)(k0 + 32 * g + 4 * q + j) * ld + c0 + 4 * c);
;             mx[0] = fmaxf(mx[0], fabsf(v[0])); mx[1] = fmaxf(mx[1], fabsf(v[1])); mx[2] = fmaxf(mx[2], fabsf(v[2])); mx[3] = fmaxf(mx[3], fabsf(v[3])); }
; #pragma unroll
;     for (int i = 0; i < 4; ++i) { float v = mx[i]; v = fmaxf(v, __shfl_xor(v, 8)); v = fmaxf(v, __shfl_xor(v, 16)); v = fmaxf(v, __shfl_xor(v, 32)); mx[i] = v; }
;     if (q == 0) {
; #pragma unroll
;         for (int i = 0; i < 4; ++i) atomicMax((unsigned*)(cmx + 4 * c + i), __float_as_uint(mx[i] * CMS_F)); }
; }
; template <int GRP>
; __device__ __forceinline__ void conv_item(Frame& F, int r) {
;     ...
;         if (r < NI) { const int kb = r / 152, nb = r % 152, c0 = (nb < 112) ? nb * 32 : SRC_GATE + 8 + (nb - 112) * 32, drow = nb * 32;
;             if (QUANT) cvt_item_i8(inptr(F, IN_WIN) + (size_t)l * D * NIN_SRC, NIN_SRC, kb * 128, c0, ws + WS_WIN + (size_t)l * NIN * D, D, drow, cmx + CMX_WIN + l * NIN + drow, scr, F.lane);
;             else colmax_item(inptr(F, IN_WIN) + (size_t)l * D * NIN_SRC, NIN_SRC, kb * 128, c0, cmx + CMX_WIN + l * NIN + drow, F.lane);
.LBB0_627:
	s_mul_hi_i32 s8, s3, 0x6bca1af3
	s_lshr_b32 s18, s8, 31
	s_ashr_i32 s8, s8, 6
	s_add_i32 s8, s8, s18
	s_mul_i32 s18, s8, 0xffffff68
	s_add_i32 s19, s3, s18
	s_mul_i32 s18, s8, 0xffffed00
	v_mov_b32_e32 v1, s23
	s_add_i32 s18, s4, s18
	s_waitcnt lgkmcnt(3)
	ds_read_b64 v[2:3], v1
	s_add_i32 s20, s18, 8
	s_cmpk_lt_i32 s19, 0x70
	s_cselect_b32 s20, s18, s20
	s_ashr_i32 s21, s20, 31
	s_waitcnt lgkmcnt(0)
	v_readfirstlane_b32 s19, v2
	s_lshl_b64 s[20:21], s[20:21], 2
	v_readfirstlane_b32 s67, v3
	s_add_u32 s20, s19, s20
	s_addc_u32 s21, s67, s21
	v_lshl_or_b32 v1, s8, 7, v15
	v_lshl_add_u64 v[2:3], s[20:21], 0, v[10:11]
	s_mov_b64 s[20:21], 0x2610000
	v_lshl_add_u64 v[38:39], v[2:3], 0, s[20:21]
	v_or_b32_e32 v6, 1, v1
	v_mad_i64_i32 v[2:3], s[20:21], v1, s24, v[38:39]
	v_mad_i64_i32 v[6:7], s[20:21], v6, s24, v[38:39]
	global_load_dwordx4 v[2:5], v[2:3], off
	v_cmp_lt_i32_e32 vcc, v31, v32
	global_load_dwordx4 v[6:9], v[6:7], off
	s_waitcnt vmcnt(0) lgkmcnt(0)
	v_max3_f32 v40, |v2|, 0, |v6|
	v_or_b32_e32 v2, 2, v1
	v_or_b32_e32 v6, 3, v1
	v_max3_f32 v41, |v3|, 0, |v7|
	v_mad_i64_i32 v[2:3], s[20:21], v2, s24, v[38:39]
	v_mad_i64_i32 v[6:7], s[20:21], v6, s24, v[38:39]
	v_max3_f32 v42, |v4|, 0, |v8|
	v_max3_f32 v43, |v5|, 0, |v9|
	global_load_dwordx4 v[2:5], v[2:3], off
	s_nop 0
	global_load_dwordx4 v[6:9], v[6:7], off
	s_waitcnt vmcnt(0) lgkmcnt(0)
	v_max3_f32 v40, v40, |v2|, |v6|
	v_or_b32_e32 v2, 32, v1
	v_or_b32_e32 v6, 33, v1
	v_max3_f32 v41, v41, |v3|, |v7|
	v_mad_i64_i32 v[2:3], s[20:21], v2, s24, v[38:39]
	v_mad_i64_i32 v[6:7], s[20:21], v6, s24, v[38:39]
	v_max3_f32 v42, v42, |v4|, |v8|
	v_max3_f32 v43, v43, |v5|, |v9|
	global_load_dwordx4 v[2:5], v[2:3], off
	s_nop 0
	global_load_dwordx4 v[6:9], v[6:7], off
	s_waitcnt vmcnt(0) lgkmcnt(0)
	v_max3_f32 v40, v40, |v2|, |v6|
	v_or_b32_e32 v2, 34, v1
	v_or_b32_e32 v6, 35, v1
	v_max3_f32 v41, v41, |v3|, |v7|
	v_mad_i64_i32 v[2:3], s[20:21], v2, s24, v[38:39]
	v_mad_i64_i32 v[6:7], s[20:21], v6, s24, v[38:39]
	v_max3_f32 v42, v42, |v4|, |v8|
	v_max3_f32 v43, v43, |v5|, |v9|
	global_load_dwordx4 v[2:5], v[2:3], off
	s_nop 0
	global_load_dwordx4 v[6:9], v[6:7], off
	s_waitcnt vmcnt(0) lgkmcnt(0)
	v_max3_f32 v40, v40, |v2|, |v6|
	v_or_b32_e32 v2, 64, v1
	v_or_b32_e32 v6, 0x41, v1
	v_max3_f32 v41, v41, |v3|, |v7|
	v_mad_i64_i32 v[2:3], s[20:21], v2, s24, v[38:39]
	v_mad_i64_i32 v[6:7], s[20:21], v6, s24, v[38:39]
	v_max3_f32 v42, v42, |v4|, |v8|
	v_max3_f32 v43, v43, |v5|, |v9|
	global_load_dwordx4 v[2:5], v[2:3], off
	s_nop 0
	global_load_dwordx4 v[6:9], v[6:7], off
	s_waitcnt vmcnt(0) lgkmcnt(0)
	v_max3_f32 v40, v40, |v2|, |v6|
	v_or_b32_e32 v2, 0x42, v1
	v_or_b32_e32 v6, 0x43, v1
	v_max3_f32 v41, v41, |v3|, |v7|
	v_mad_i64_i32 v[2:3], s[20:21], v2, s24, v[38:39]
	v_mad_i64_i32 v[6:7], s[20:21], v6, s24, v[38:39]
	v_max3_f32 v42, v42, |v4|, |v8|
	v_max3_f32 v43, v43, |v5|, |v9|
	global_load_dwordx4 v[2:5], v[2:3], off
	s_nop 0
	global_load_dwordx4 v[6:9], v[6:7], off
	s_waitcnt vmcnt(0) lgkmcnt(0)
	v_max3_f32 v40, v40, |v2|, |v6|
	v_or_b32_e32 v2, 0x60, v1
	v_or_b32_e32 v6, 0x61, v1
	v_max3_f32 v41, v41, |v3|, |v7|
	v_mad_i64_i32 v[2:3], s[20:21], v2, s24, v[38:39]
	v_mad_i64_i32 v[6:7], s[20:21], v6, s24, v[38:39]
	v_max3_f32 v42, v42, |v4|, |v8|
	v_max3_f32 v43, v43, |v5|, |v9|
	global_load_dwordx4 v[2:5], v[2:3], off
	s_nop 0
	global_load_dwordx4 v[6:9], v[6:7], off
	s_waitcnt vmcnt(0) lgkmcnt(0)
	v_max3_f32 v40, v40, |v2|, |v6|
	v_or_b32_e32 v2, 0x62, v1
	v_or_b32_e32 v1, 0x63, v1
	v_max3_f32 v41, v41, |v3|, |v7|
	v_mad_i64_i32 v[2:3], s[20:21], v2, s24, v[38:39]
	v_mad_i64_i32 v[6:7], s[20:21], v1, s24, v[38:39]
	v_max3_f32 v42, v42, |v4|, |v8|
	v_max3_f32 v43, v43, |v5|, |v9|
	global_load_dwordx4 v[2:5], v[2:3], off
	s_nop 0
	global_load_dwordx4 v[6:9], v[6:7], off
	s_waitcnt vmcnt(0) lgkmcnt(0)
	v_max3_f32 v1, v40, |v2|, |v6|
	v_cndmask_b32_e32 v2, v30, v31, vcc
	v_cmp_lt_i32_e32 vcc, v33, v32
	v_max3_f32 v6, v42, |v4|, |v8|
	v_lshlrev_b32_e32 v8, 2, v2
	v_cndmask_b32_e32 v2, v30, v33, vcc
	v_cmp_lt_i32_e32 vcc, v34, v32
	v_max3_f32 v3, v41, |v3|, |v7|
	v_max3_f32 v7, v43, |v5|, |v9|
	v_lshlrev_b32_e32 v9, 2, v2
	v_cndmask_b32_e32 v2, v30, v34, vcc
	v_lshlrev_b32_e32 v38, 2, v2
	ds_bpermute_b32 v2, v8, v1
	ds_bpermute_b32 v4, v8, v3
	ds_bpermute_b32 v5, v8, v6
	ds_bpermute_b32 v8, v8, v7
	s_waitcnt lgkmcnt(3)
	v_max_f32_e32 v2, v2, v2
	s_waitcnt lgkmcnt(2)
	v_max_f32_e32 v4, v4, v4
	s_waitcnt lgkmcnt(1)
	v_max_f32_e32 v5, v5, v5
	s_waitcnt lgkmcnt(0)
	v_max_f32_e32 v8, v8, v8
	v_max_f32_e32 v1, v1, v2
	v_max_f32_e32 v3, v3, v4
	v_max_f32_e32 v5, v6, v5
	v_max_f32_e32 v7, v7, v8
	ds_bpermute_b32 v2, v9, v1
	ds_bpermute_b32 v4, v9, v3
	ds_bpermute_b32 v6, v9, v5
	ds_bpermute_b32 v8, v9, v7
	s_waitcnt lgkmcnt(3)
	v_max_f32_e32 v2, v2, v2
	s_waitcnt lgkmcnt(2)
	v_max_f32_e32 v4, v4, v4
	s_waitcnt lgkmcnt(1)
	v_max_f32_e32 v6, v6, v6
	s_waitcnt lgkmcnt(0)
	v_max_f32_e32 v8, v8, v8
	v_max_f32_e32 v1, v1, v2
	v_max_f32_e32 v3, v3, v4
	v_max_f32_e32 v5, v5, v6
	v_max_f32_e32 v7, v7, v8
	ds_bpermute_b32 v2, v38, v1
	ds_bpermute_b32 v4, v38, v3
	ds_bpermute_b32 v6, v38, v5
	ds_bpermute_b32 v8, v38, v7
	s_and_saveexec_b64 s[20:21], s[6:7]
	s_cbranch_execz .LBB0_629
	s_waitcnt lgkmcnt(3)
	v_max_f32_e32 v2, v2, v2
	v_max_f32_e32 v1, v1, v1
	s_ashr_i32 s19, s18, 31
	s_waitcnt lgkmcnt(2)
	v_max_f32_e32 v4, v4, v4
	v_max_f32_e32 v3, v3, v3
	v_max_f32_e32 v1, v1, v2
	s_waitcnt lgkmcnt(1)
	v_max_f32_e32 v6, v6, v6
	v_max_f32_e32 v5, v5, v5
	v_max_f32_e32 v4, v3, v4
	v_lshl_add_u64 v[2:3], s[18:19], 2, v[12:13]
	v_mul_f32_e32 v1, 0x3fb33333, v1
	s_waitcnt lgkmcnt(0)
	v_max_f32_e32 v8, v8, v8
	v_max_f32_e32 v7, v7, v7
	v_max_f32_e32 v5, v5, v6
	global_atomic_umax v[2:3], v1, off
	v_mul_f32_e32 v1, 0x3fb33333, v4
	v_max_f32_e32 v7, v7, v8
	global_atomic_umax v[2:3], v1, off offset:4
	v_mul_f32_e32 v1, 0x3fb33333, v5
	global_atomic_umax v[2:3], v1, off offset:8
	v_mul_f32_e32 v1, 0x3fb33333, v7
	global_atomic_umax v[2:3], v1, off offset:12

; __device__ __forceinline__ void colmax_item(const float* src, int ld, int k0, int c0, float* cmx  , int lane) {
;     const int c = lane & 7, q = lane >> 3;
;     f32x4 mx = (f32x4){0.f, 0.f, 0.f, 0.f};
; #pragma unroll
;     for (int g = 0; g < 4; ++g)
; #pragma unroll
;         for (int j = 0; j < 4; ++j) { const f32x4 v = *(const f32x4*)(src + (size_t)(k0 + 32 * g + 4 * q + j) * ld + c0 + 4 * c);
;             mx[0] = fmaxf(mx[0], fabsf(v[0])); mx[1] = fmaxf(mx[1], fabsf(v[1])); mx[2] = fmaxf(mx[2], fabsf(v[2])); mx[3] = fmaxf(mx[3], fabsf(v[3])); }
; #pragma unroll
;     for (int i = 0; i < 4; ++i) { float v = mx[i]; v = fmaxf(v, __shfl_xor(v, 8)); v = fmaxf(v, __shfl_xor(v, 16)); v = fmaxf(v, __shfl_xor(v, 32)); mx[i] = v; }
; template <int GRP>
; __device__ __forceinline__ void conv_item(Frame& F, int r) {
;     ...
;     else { constexpr int KBN = (GRP == 3) ? 16 : CMS_KB, I_E = KBN * 88; const int up = r / (8 * I_E); r %= (8 * I_E); const int e = r / I_E; r %= I_E; const int kb = r / 88, nb = r % 88, n0 = nb * 32, drow = (n0 >> 7) * 256 + up * 128 + (n0 & 127);
;         if (GRP == 3) cvt_item_i8(inptr(F, up ? IN_MU : IN_MG) + (size_t)e * D * DFE, DFE, kb * 128, n0, ws + WS_MGU + (size_t)e * 2 * DFE * D, D, drow, cmx + 2 * DFF + e * 2 * DFE + drow, scr, F.lane);
;         else colmax_item(inptr(F, up ? IN_MU : IN_MG) + (size_t)e * D * DFE, DFE, kb * 128, n0, cmx + 2 * DFF + e * 2 * DFE + drow, F.lane); }
.LBB0_631:
	s_cmpk_gt_i32 s20, 0x3ff
	s_mov_b64 s[16:17], -1
	s_cbranch_scc0 .LBB0_639
	s_cmpk_gt_u32 s20, 0x2fff
	s_cbranch_scc0 .LBB0_636
	s_add_i32 s8, s20, 0xffffd000
	s_add_i32 s16, s20, 0xca80
	s_cmpk_lt_u32 s8, 0x580
	s_cselect_b32 s16, s8, s16
	s_and_b32 s17, s16, 0xffff
	s_mul_i32 s17, s17, 0xba2f
	s_lshr_b32 s21, s17, 23
	s_mul_i32 s17, s21, 0xb0
	s_sub_i32 s16, s16, s17
	s_and_b32 s17, s16, 0xffff
	s_add_i32 s16, s17, 0xffffffa8
	s_min_u32 s67, s17, s16
	s_lshl_b32 s16, s67, 5
	s_cmpk_lt_u32 s20, 0x3580
	s_movk_i32 s18, 0xa0
	s_cselect_b32 s18, s18, 0xa8
	s_add_i32 s18, s18, 0
	s_add_i32 s18, s18, 0x20200
	v_mov_b32_e32 v1, s18
	s_waitcnt lgkmcnt(3)
	ds_read_b64 v[2:3], v1
	s_cmpk_gt_u32 s17, 0x57
	s_cselect_b32 s17, 0x80, 0
	v_or_b32_e32 v1, s17, v15
	s_ashr_i32 s17, s16, 31
	s_waitcnt lgkmcnt(0)
	v_readfirstlane_b32 s18, v2
	v_readfirstlane_b32 s19, v3
	v_mul_u32_u24_e32 v2, s21, v35
	v_mov_b32_e32 v3, v11
	v_lshlrev_b64 v[2:3], 2, v[2:3]
	v_lshl_add_u64 v[2:3], s[18:19], 0, v[2:3]
	s_lshl_b64 s[18:19], s[16:17], 2
	v_lshl_add_u64 v[2:3], v[2:3], 0, s[18:19]
	v_lshl_add_u64 v[2:3], v[2:3], 0, v[10:11]
	v_mul_u32_u24_e32 v4, 0x2c00, v1
	v_mov_b32_e32 v5, v11
	v_lshl_add_u64 v[2:3], v[2:3], 0, v[4:5]
	v_add_co_u32_e32 v8, vcc, s25, v2
	global_load_dwordx4 v[4:7], v[2:3], off
	s_nop 0
	v_addc_co_u32_e32 v9, vcc, 0, v3, vcc
	global_load_dwordx4 v[38:41], v[8:9], off offset:3072
	s_movk_i32 s17, 0x5000
	s_waitcnt vmcnt(0) lgkmcnt(0)
	v_max3_f32 v1, |v4|, 0, |v38|
	v_add_co_u32_e32 v4, vcc, s17, v2
	v_max3_f32 v42, |v5|, 0, |v39|
	s_nop 0
	v_addc_co_u32_e32 v5, vcc, 0, v3, vcc
	v_add_co_u32_e32 v8, vcc, s26, v2
	v_max3_f32 v43, |v6|, 0, |v40|
	s_nop 0
	v_addc_co_u32_e32 v9, vcc, 0, v3, vcc
	v_max3_f32 v44, |v7|, 0, |v41|
	global_load_dwordx4 v[4:7], v[4:5], off offset:2048
	s_nop 0
	global_load_dwordx4 v[38:41], v[8:9], off offset:1024
	s_waitcnt vmcnt(0) lgkmcnt(0)
	v_max3_f32 v1, v1, |v4|, |v38|
	v_add_co_u32_e32 v4, vcc, s27, v2
	v_max3_f32 v42, v42, |v5|, |v39|
	s_nop 0
	v_addc_co_u32_e32 v5, vcc, 0, v3, vcc
	v_add_co_u32_e32 v8, vcc, s28, v2
	v_max3_f32 v43, v43, |v6|, |v40|
	s_nop 0
	v_addc_co_u32_e32 v9, vcc, 0, v3, vcc
	v_max3_f32 v44, v44, |v7|, |v41|
	global_load_dwordx4 v[4:7], v[4:5], off
	s_nop 0
	global_load_dwordx4 v[38:41], v[8:9], off offset:3072
	s_waitcnt vmcnt(0) lgkmcnt(0)
	v_max3_f32 v1, v1, |v4|, |v38|
	v_add_co_u32_e32 v4, vcc, s29, v2
	v_max3_f32 v42, v42, |v5|, |v39|
	s_nop 0
	v_addc_co_u32_e32 v5, vcc, 0, v3, vcc
	v_add_co_u32_e32 v8, vcc, s30, v2
	v_max3_f32 v43, v43, |v6|, |v40|
	s_nop 0
	v_addc_co_u32_e32 v9, vcc, 0, v3, vcc
	v_max3_f32 v44, v44, |v7|, |v41|
	global_load_dwordx4 v[4:7], v[4:5], off offset:2048
	s_nop 0
	global_load_dwordx4 v[38:41], v[8:9], off offset:1024
	s_waitcnt vmcnt(0) lgkmcnt(0)
	v_max3_f32 v1, v1, |v4|, |v38|
	v_add_co_u32_e32 v4, vcc, s31, v2
	v_max3_f32 v42, v42, |v5|, |v39|
	s_nop 0
	v_addc_co_u32_e32 v5, vcc, 0, v3, vcc
	v_add_co_u32_e32 v8, vcc, s34, v2
	v_max3_f32 v43, v43, |v6|, |v40|
	s_nop 0
	v_addc_co_u32_e32 v9, vcc, 0, v3, vcc
	v_max3_f32 v44, v44, |v7|, |v41|
	global_load_dwordx4 v[4:7], v[4:5], off
	s_nop 0
	global_load_dwordx4 v[38:41], v[8:9], off offset:3072
	s_waitcnt vmcnt(0) lgkmcnt(0)
	v_max3_f32 v1, v1, |v4|, |v38|
	v_add_co_u32_e32 v4, vcc, s35, v2
	v_max3_f32 v42, v42, |v5|, |v39|
	s_nop 0
	v_addc_co_u32_e32 v5, vcc, 0, v3, vcc
	v_add_co_u32_e32 v8, vcc, s36, v2
	v_max3_f32 v43, v43, |v6|, |v40|
	s_nop 0
	v_addc_co_u32_e32 v9, vcc, 0, v3, vcc
	v_max3_f32 v44, v44, |v7|, |v41|
	global_load_dwordx4 v[4:7], v[4:5], off offset:2048
	s_nop 0
	global_load_dwordx4 v[38:41], v[8:9], off offset:1024
	s_waitcnt vmcnt(0) lgkmcnt(0)
	v_max3_f32 v1, v1, |v4|, |v38|
	v_add_co_u32_e32 v4, vcc, s37, v2
	v_max3_f32 v42, v42, |v5|, |v39|
	s_nop 0
	v_addc_co_u32_e32 v5, vcc, 0, v3, vcc
	v_add_co_u32_e32 v8, vcc, s38, v2
	v_max3_f32 v43, v43, |v6|, |v40|
	s_nop 0
	v_addc_co_u32_e32 v9, vcc, 0, v3, vcc
	v_max3_f32 v44, v44, |v7|, |v41|
	global_load_dwordx4 v[4:7], v[4:5], off
	s_nop 0
	global_load_dwordx4 v[38:41], v[8:9], off offset:3072
	s_waitcnt vmcnt(0) lgkmcnt(0)
	v_max3_f32 v1, v1, |v4|, |v38|
	v_add_co_u32_e32 v4, vcc, s39, v2
	v_max3_f32 v8, v42, |v5|, |v39|
	s_nop 0
	v_addc_co_u32_e32 v5, vcc, 0, v3, vcc
	v_add_co_u32_e32 v2, vcc, s40, v2
	v_max3_f32 v9, v43, |v6|, |v40|
	s_nop 0
	v_addc_co_u32_e32 v3, vcc, 0, v3, vcc
	v_max3_f32 v42, v44, |v7|, |v41|
	global_load_dwordx4 v[4:7], v[4:5], off offset:2048
	v_cmp_lt_i32_e32 vcc, v31, v32
	global_load_dwordx4 v[38:41], v[2:3], off offset:1024
	s_waitcnt vmcnt(0) lgkmcnt(0)
	v_max3_f32 v3, v8, |v5|, |v39|
	v_cndmask_b32_e32 v2, v30, v31, vcc
	v_cmp_lt_i32_e32 vcc, v33, v32
	v_lshlrev_b32_e32 v8, 2, v2
	v_max3_f32 v1, v1, |v4|, |v38|
	v_cndmask_b32_e32 v2, v30, v33, vcc
	v_cmp_lt_i32_e32 vcc, v34, v32
	v_max3_f32 v5, v9, |v6|, |v40|
	v_max3_f32 v7, v42, |v7|, |v41|
	v_lshlrev_b32_e32 v9, 2, v2
	v_cndmask_b32_e32 v2, v30, v34, vcc
	v_lshlrev_b32_e32 v38, 2, v2
	ds_bpermute_b32 v2, v8, v1
	ds_bpermute_b32 v4, v8, v3
	ds_bpermute_b32 v6, v8, v5
	ds_bpermute_b32 v8, v8, v7
	s_waitcnt lgkmcnt(3)
	v_max_f32_e32 v2, v2, v2
	s_waitcnt lgkmcnt(2)
	v_max_f32_e32 v4, v4, v4
	s_waitcnt lgkmcnt(1)
	v_max_f32_e32 v6, v6, v6
	s_waitcnt lgkmcnt(0)
	v_max_f32_e32 v8, v8, v8
	v_max_f32_e32 v1, v1, v2
	v_max_f32_e32 v3, v3, v4
	v_max_f32_e32 v5, v5, v6
	v_max_f32_e32 v7, v7, v8
	ds_bpermute_b32 v2, v9, v1
	ds_bpermute_b32 v4, v9, v3
	ds_bpermute_b32 v6, v9, v5
	ds_bpermute_b32 v8, v9, v7
	s_waitcnt lgkmcnt(3)
	v_max_f32_e32 v2, v2, v2
	s_waitcnt lgkmcnt(2)
	v_max_f32_e32 v4, v4, v4
	s_waitcnt lgkmcnt(1)
	v_max_f32_e32 v6, v6, v6
	s_waitcnt lgkmcnt(0)
	v_max_f32_e32 v8, v8, v8
	v_max_f32_e32 v1, v1, v2
	v_max_f32_e32 v3, v3, v4
	v_max_f32_e32 v5, v5, v6
	v_max_f32_e32 v7, v7, v8
	ds_bpermute_b32 v2, v38, v1
	ds_bpermute_b32 v4, v38, v3
	ds_bpermute_b32 v6, v38, v5
	ds_bpermute_b32 v8, v38, v7
	s_and_saveexec_b64 s[18:19], s[6:7]
	s_cbranch_execz .LBB0_635
; __device__ __forceinline__ void colmax_item(const float* src, int ld, int k0, int c0, float* cmx  , int lane) {
;     ...
;     if (q == 0) {
; #pragma unroll
;         for (int i = 0; i < 4; ++i) atomicMax((unsigned*)(cmx + 4 * c + i), __float_as_uint(mx[i] * CMS_F)); }
	s_lshl_b32 s17, s67, 6
	s_and_b32 s17, s17, 0x3fff00
	s_cmpk_gt_u32 s8, 0x57f
	s_cselect_b32 s8, 0x80, 0
	v_mul_u32_u24_e32 v9, s21, v36
	s_or_b32 s8, s17, s8
	s_and_b32 s16, s16, 0x60
	v_lshlrev_b32_e32 v38, 2, v9
	v_mov_b32_e32 v39, v11
	s_or_b32 s8, s8, s16
	v_lshl_add_u64 v[38:39], s[10:11], 0, v[38:39]
	s_lshl_b32 s8, s8, 2
	s_waitcnt lgkmcnt(3)
	v_max_f32_e32 v2, v2, v2
	v_max_f32_e32 v1, v1, v1
	v_lshl_add_u64 v[38:39], v[38:39], 0, s[8:9]
	s_waitcnt lgkmcnt(2)
	v_max_f32_e32 v4, v4, v4
	v_max_f32_e32 v3, v3, v3
	v_max_f32_e32 v1, v1, v2
	s_waitcnt lgkmcnt(1)
	v_max_f32_e32 v6, v6, v6
	v_max_f32_e32 v5, v5, v5
	v_max_f32_e32 v3, v3, v4
	v_mul_f32_e32 v1, 0x3fb33333, v1
	v_readfirstlane_b32 s16, v38
	v_readfirstlane_b32 s17, v39
	s_waitcnt lgkmcnt(0)
	v_max_f32_e32 v8, v8, v8
	v_max_f32_e32 v7, v7, v7
	v_max_f32_e32 v5, v5, v6
	v_max_f32_e32 v7, v7, v8
	global_atomic_umax v29, v1, s[16:17]
	v_mul_f32_e32 v1, 0x3fb33333, v3
	global_atomic_umax v29, v1, s[16:17] offset:4
	v_mul_f32_e32 v1, 0x3fb33333, v5
	global_atomic_umax v29, v1, s[16:17] offset:8
	v_mul_f32_e32 v1, 0x3fb33333, v7
	global_atomic_umax v29, v1, s[16:17] offset:12

; __device__ __forceinline__ void cvt_item8(const float* src, int ld, int k0, int c0, unsigned char* dst, int Kd, int drow0, unsigned char* scr, int lane) {
;     const int c = lane & 7, q = lane >> 3;
;     f32x4 v[4][4];
; #pragma unroll
;     for (int g = 0; g < 4; ++g)
; #pragma unroll
;         for (int j = 0; j < 4; ++j) v[g][j] = __builtin_nontemporal_load((const f32x4*)(src + (size_t)(k0 + 32 * g + 4 * q + j) * ld + c0 + 4 * c));
; #pragma unroll
;     for (int g = 0; g < 4; ++g)
; #pragma unroll
;         for (int i = 0; i < 4; ++i) *(unsigned*)(scr + (4 * c + i) * 132 + 32 * g + 4 * q) = pg8::pack_fp8x4(v[g][0][i] * WSC, v[g][1][i] * WSC, v[g][2][i] * WSC, v[g][3][i] * WSC);
; template <int GRP>
; __device__ __forceinline__ void conv_item(Frame& F, int r) {
;     ...
;             if (r < CI_MD) { const int e = r / (22 * 64); r %= (22 * 64); const int kb = r / 64, nb = r % 64;
;                 cvt_item8(inptr(F, IN_MD) + (size_t)e * DFE * D, D, kb * 128, nb * 32, ws + WS_MD + (size_t)e * D * DFE, DFE, nb * 32, scr, F.lane); return; }
.LBB0_636:
	s_andn2_b64 vcc, exec, s[16:17]
	s_cbranch_vccnz .LBB0_638
	s_add_i32 s8, s20, 0xfc00
	v_mov_b32_e32 v1, s41
	s_and_b32 s16, s8, 0xffff
	s_waitcnt lgkmcnt(3)
	ds_read_b64 v[2:3], v1
	s_mul_i32 s16, s16, 0xba2f
	s_lshr_b32 s17, s16, 26
	s_mul_i32 s16, s17, 0x580
	s_sub_i32 s8, s8, s16
	s_and_b32 s16, s8, 0xffff
	s_waitcnt lgkmcnt(0)
	v_readfirstlane_b32 s8, v2
	s_mul_i32 s19, s17, 0x1600000
	v_readfirstlane_b32 s18, v3
	s_add_u32 s19, s8, s19
	s_addc_u32 s21, s18, 0
	s_lshl_b32 s8, s16, 1
	s_lshl_b32 s16, s16, 5
	s_and_b32 s16, s16, 0x7e0
	s_and_b32 s8, s8, 0xf80
	s_lshl_b32 s18, s16, 2
	s_add_u32 s18, s19, s18
	v_or_b32_e32 v1, s8, v21
	s_addc_u32 s19, s21, 0
	v_lshlrev_b32_e32 v2, 2, v14
	v_mov_b32_e32 v3, v11
	v_lshl_add_u64 v[2:3], s[18:19], 0, v[2:3]
	v_lshlrev_b32_e32 v4, 13, v1
	v_mov_b32_e32 v5, v11
	v_lshl_add_u64 v[8:9], v[2:3], 0, v[4:5]
	v_add_co_u32_e32 v2, vcc, s25, v8
	s_nop 1
	v_addc_co_u32_e32 v3, vcc, 0, v9, vcc
	global_load_dwordx4 v[4:7], v[8:9], off nt
	global_load_dwordx4 v[38:41], v[2:3], off nt
	v_add_co_u32_e32 v2, vcc, s42, v8
	s_waitcnt vmcnt(0) lgkmcnt(0)
	v_mul_f32_e32 v1, 0x42800000, v4
	v_addc_co_u32_e32 v3, vcc, 0, v9, vcc
	global_load_dwordx4 v[42:45], v[2:3], off nt
	v_add_co_u32_e32 v2, vcc, s43, v8
	v_mul_f32_e32 v4, 0x42800000, v38
	s_nop 0
	v_addc_co_u32_e32 v3, vcc, 0, v9, vcc
	global_load_dwordx4 v[46:49], v[2:3], off nt
	v_add_co_u32_e32 v50, vcc, s44, v8
	v_med3_f32 v1, v1, s63, v37
	s_nop 0
	v_addc_co_u32_e32 v51, vcc, 0, v9, vcc
	v_add_co_u32_e32 v54, vcc, s45, v8
	v_med3_f32 v4, v4, s63, v37
	s_nop 0
	v_addc_co_u32_e32 v55, vcc, 0, v9, vcc
	global_load_dwordx4 v[50:53], v[50:51], off nt
	s_nop 0
	global_load_dwordx4 v[54:57], v[54:55], off nt
	v_add_co_u32_e32 v58, vcc, s46, v8
	v_mov_b32_e32 v38, v11
	s_nop 0
	v_addc_co_u32_e32 v59, vcc, 0, v9, vcc
	v_add_co_u32_e32 v62, vcc, s47, v8
	v_mov_b64_e32 v[2:3], s[12:13]
	s_nop 0
	v_addc_co_u32_e32 v63, vcc, 0, v9, vcc
	global_load_dwordx4 v[58:61], v[58:59], off nt
	s_nop 0
	global_load_dwordx4 v[62:65], v[62:63], off nt
	v_add_co_u32_e32 v66, vcc, s49, v8
	v_mad_u64_u32 v[2:3], s[18:19], s17, v35, v[2:3]
	s_nop 0
	v_addc_co_u32_e32 v67, vcc, 0, v9, vcc
	v_add_co_u32_e32 v70, vcc, s52, v8
	v_lshl_add_u64 v[2:3], v[2:3], 0, s[8:9]
	s_nop 0
	v_addc_co_u32_e32 v71, vcc, 0, v9, vcc
	global_load_dwordx4 v[66:69], v[66:67], off nt
	s_nop 0
	global_load_dwordx4 v[70:73], v[70:71], off nt
	v_add_co_u32_e32 v74, vcc, s53, v8
	s_nop 1
	v_addc_co_u32_e32 v75, vcc, 0, v9, vcc
	v_add_co_u32_e32 v78, vcc, s54, v8
	s_nop 1
	v_addc_co_u32_e32 v79, vcc, 0, v9, vcc
	global_load_dwordx4 v[74:77], v[74:75], off nt
	s_nop 0
	global_load_dwordx4 v[78:81], v[78:79], off nt
	v_add_co_u32_e32 v82, vcc, s55, v8
	s_nop 1
	v_addc_co_u32_e32 v83, vcc, 0, v9, vcc
	v_add_co_u32_e32 v86, vcc, s56, v8
	s_nop 1
	v_addc_co_u32_e32 v87, vcc, 0, v9, vcc
	global_load_dwordx4 v[82:85], v[82:83], off nt
	s_nop 0
	global_load_dwordx4 v[86:89], v[86:87], off nt
	v_add_co_u32_e32 v90, vcc, s57, v8
	s_nop 1
	v_addc_co_u32_e32 v91, vcc, 0, v9, vcc
	v_add_co_u32_e32 v8, vcc, s62, v8
	s_nop 1
	v_addc_co_u32_e32 v9, vcc, 0, v9, vcc
	global_load_dwordx4 v[90:93], v[90:91], off nt
	s_nop 0
	global_load_dwordx4 v[94:97], v[8:9], off nt
	v_mov_b32_e32 v9, v11
	v_cvt_pk_fp8_f32 v9, v1, v4
	s_waitcnt vmcnt(0) lgkmcnt(0)
	v_mul_f32_e32 v8, 0x42800000, v42
	v_med3_f32 v4, v8, s63, v37
	v_mul_f32_e32 v8, 0x42800000, v43
	v_mov_b32_e32 v42, v11
	v_mul_f32_e32 v1, 0x42800000, v46
	v_med3_f32 v1, v1, s63, v37
	v_cvt_pk_fp8_f32 v9, v4, v1 op_sel:[0,0,1]
	v_mul_f32_e32 v4, 0x42800000, v5
	v_mul_f32_e32 v5, 0x42800000, v39
	v_med3_f32 v4, v4, s63, v37
	v_med3_f32 v5, v5, s63, v37
	v_cvt_pk_fp8_f32 v38, v4, v5
	v_mul_f32_e32 v4, 0x42800000, v47
	v_med3_f32 v5, v8, s63, v37
	v_med3_f32 v4, v4, s63, v37
	v_cvt_pk_fp8_f32 v38, v5, v4 op_sel:[0,0,1]
	v_mul_f32_e32 v4, 0x42800000, v6
	v_mul_f32_e32 v5, 0x42800000, v40
	v_med3_f32 v4, v4, s63, v37
	v_med3_f32 v5, v5, s63, v37
	v_mov_b32_e32 v8, v11
	v_cvt_pk_fp8_f32 v8, v4, v5
	v_mul_f32_e32 v6, 0x42800000, v44
	v_mul_f32_e32 v4, 0x42800000, v48
	v_med3_f32 v5, v6, s63, v37
	v_med3_f32 v4, v4, s63, v37
	v_cvt_pk_fp8_f32 v8, v5, v4 op_sel:[0,0,1]
	v_mul_f32_e32 v4, 0x42800000, v7
	v_mul_f32_e32 v5, 0x42800000, v41
	v_med3_f32 v4, v4, s63, v37
	v_med3_f32 v5, v5, s63, v37
	v_mov_b32_e32 v7, v11
	v_cvt_pk_fp8_f32 v7, v4, v5
	v_mul_f32_e32 v6, 0x42800000, v45
	v_mul_f32_e32 v4, 0x42800000, v49
	v_med3_f32 v5, v6, s63, v37
	v_med3_f32 v4, v4, s63, v37
	v_cvt_pk_fp8_f32 v7, v5, v4 op_sel:[0,0,1]
	v_mul_f32_e32 v4, 0x42800000, v50
	v_mul_f32_e32 v5, 0x42800000, v54
	v_med3_f32 v4, v4, s63, v37
	v_med3_f32 v5, v5, s63, v37
	v_mov_b32_e32 v39, v11
	v_cvt_pk_fp8_f32 v39, v4, v5
	v_mul_f32_e32 v6, 0x42800000, v58
	v_mul_f32_e32 v4, 0x42800000, v62
	v_med3_f32 v5, v6, s63, v37
	v_med3_f32 v4, v4, s63, v37
	v_cvt_pk_fp8_f32 v39, v5, v4 op_sel:[0,0,1]
	v_mul_f32_e32 v4, 0x42800000, v51
	v_mul_f32_e32 v5, 0x42800000, v55
	v_med3_f32 v4, v4, s63, v37
	v_med3_f32 v5, v5, s63, v37
	v_mov_b32_e32 v40, v11
	v_cvt_pk_fp8_f32 v40, v4, v5
	v_mul_f32_e32 v6, 0x42800000, v59
	v_mul_f32_e32 v4, 0x42800000, v63
	v_med3_f32 v5, v6, s63, v37
	v_med3_f32 v4, v4, s63, v37
	v_cvt_pk_fp8_f32 v40, v5, v4 op_sel:[0,0,1]
; __device__ __forceinline__ void cvt_item8(const float* src, int ld, int k0, int c0, unsigned char* dst, int Kd, int drow0, unsigned char* scr, int lane) {
;     ...
;     for (int g = 0; g < 4; ++g)
; #pragma unroll
;         for (int i = 0; i < 4; ++i) *(unsigned*)(scr + (4 * c + i) * 132 + 32 * g + 4 * q) = pg8::pack_fp8x4(v[g][0][i] * WSC, v[g][1][i] * WSC, v[g][2][i] * WSC, v[g][3][i] * WSC);
;     asm volatile("s_waitcnt lgkmcnt(0)" ::: "memory");
; #pragma unroll
;     for (int r = 0; r < 4; ++r) { const int n = 8 * r + (lane >> 3), ch = lane & 7; const unsigned char* p = scr + n * 132 + ch * 16;
;         u32x4 o; o.x = *(const unsigned*)(p); o.y = *(const unsigned*)(p + 4); o.z = *(const unsigned*)(p + 8); o.w = *(const unsigned*)(p + 12);
;         *(u32x4*)(dst + (size_t)(drow0 + n) * Kd + k0 + 16 * ch) = o; }
;     asm volatile("s_waitcnt lgkmcnt(0)" ::: "memory");
	v_mul_f32_e32 v4, 0x42800000, v52
	v_mul_f32_e32 v5, 0x42800000, v56
	v_med3_f32 v4, v4, s63, v37
	v_med3_f32 v5, v5, s63, v37
	v_mov_b32_e32 v41, v11
	v_cvt_pk_fp8_f32 v41, v4, v5
	v_mul_f32_e32 v6, 0x42800000, v60
	v_mul_f32_e32 v4, 0x42800000, v64
	v_med3_f32 v5, v6, s63, v37
	v_med3_f32 v4, v4, s63, v37
	v_cvt_pk_fp8_f32 v41, v5, v4 op_sel:[0,0,1]
	v_mul_f32_e32 v4, 0x42800000, v53
	v_mul_f32_e32 v5, 0x42800000, v57
	v_med3_f32 v4, v4, s63, v37
	v_med3_f32 v5, v5, s63, v37
	v_cvt_pk_fp8_f32 v42, v4, v5
	v_mul_f32_e32 v6, 0x42800000, v61
	v_mul_f32_e32 v4, 0x42800000, v65
	v_med3_f32 v5, v6, s63, v37
	v_med3_f32 v4, v4, s63, v37
	v_add_u32_e32 v1, v22, v23
	v_cvt_pk_fp8_f32 v42, v5, v4 op_sel:[0,0,1]
	v_mul_f32_e32 v4, 0x42800000, v66
	v_mul_f32_e32 v5, 0x42800000, v70
	ds_write2_b32 v1, v9, v39 offset1:8
	ds_write2_b32 v1, v38, v40 offset0:33 offset1:41
	ds_write2_b32 v1, v8, v41 offset0:66 offset1:74
	ds_write2_b32 v1, v7, v42 offset0:99 offset1:107
	v_med3_f32 v4, v4, s63, v37
	v_med3_f32 v5, v5, s63, v37
	v_mov_b32_e32 v7, v11
	v_cvt_pk_fp8_f32 v7, v4, v5
	v_mul_f32_e32 v6, 0x42800000, v74
	v_mul_f32_e32 v4, 0x42800000, v78
	v_med3_f32 v5, v6, s63, v37
	v_med3_f32 v4, v4, s63, v37
	v_cvt_pk_fp8_f32 v7, v5, v4 op_sel:[0,0,1]
	v_mul_f32_e32 v4, 0x42800000, v67
	v_mul_f32_e32 v5, 0x42800000, v71
	v_med3_f32 v4, v4, s63, v37
	v_med3_f32 v5, v5, s63, v37
	v_mov_b32_e32 v8, v11
	v_cvt_pk_fp8_f32 v8, v4, v5
	v_mul_f32_e32 v6, 0x42800000, v75
	v_mul_f32_e32 v4, 0x42800000, v79
	v_med3_f32 v5, v6, s63, v37
	v_med3_f32 v4, v4, s63, v37
	v_cvt_pk_fp8_f32 v8, v5, v4 op_sel:[0,0,1]
	v_mul_f32_e32 v4, 0x42800000, v68
	v_mul_f32_e32 v5, 0x42800000, v72
	v_med3_f32 v4, v4, s63, v37
	v_med3_f32 v5, v5, s63, v37
	v_mov_b32_e32 v9, v11
	v_cvt_pk_fp8_f32 v9, v4, v5
	v_mul_f32_e32 v6, 0x42800000, v76
	v_mul_f32_e32 v4, 0x42800000, v80
	v_med3_f32 v5, v6, s63, v37
	v_med3_f32 v4, v4, s63, v37
	v_cvt_pk_fp8_f32 v9, v5, v4 op_sel:[0,0,1]
	v_mul_f32_e32 v4, 0x42800000, v69
	v_mul_f32_e32 v5, 0x42800000, v73
	v_med3_f32 v4, v4, s63, v37
	v_med3_f32 v5, v5, s63, v37
	v_mov_b32_e32 v38, v11
	v_cvt_pk_fp8_f32 v38, v4, v5
	v_mul_f32_e32 v6, 0x42800000, v77
	v_mul_f32_e32 v4, 0x42800000, v81
	v_med3_f32 v5, v6, s63, v37
	v_med3_f32 v4, v4, s63, v37
	v_cvt_pk_fp8_f32 v38, v5, v4 op_sel:[0,0,1]
	v_mul_f32_e32 v4, 0x42800000, v82
	v_mul_f32_e32 v5, 0x42800000, v86
	v_med3_f32 v4, v4, s63, v37
	v_med3_f32 v5, v5, s63, v37
	v_mov_b32_e32 v39, v11
	v_cvt_pk_fp8_f32 v39, v4, v5
	v_mul_f32_e32 v6, 0x42800000, v90
	v_mul_f32_e32 v4, 0x42800000, v94
	v_med3_f32 v5, v6, s63, v37
	v_med3_f32 v4, v4, s63, v37
	v_cvt_pk_fp8_f32 v39, v5, v4 op_sel:[0,0,1]
	v_mul_f32_e32 v4, 0x42800000, v83
	v_mul_f32_e32 v5, 0x42800000, v87
	v_med3_f32 v4, v4, s63, v37
	v_med3_f32 v5, v5, s63, v37
	v_mov_b32_e32 v40, v11
	v_cvt_pk_fp8_f32 v40, v4, v5
	v_mul_f32_e32 v6, 0x42800000, v91
	v_mul_f32_e32 v4, 0x42800000, v95
	v_med3_f32 v5, v6, s63, v37
	v_med3_f32 v4, v4, s63, v37
	v_cvt_pk_fp8_f32 v40, v5, v4 op_sel:[0,0,1]
	v_mul_f32_e32 v4, 0x42800000, v84
	v_mul_f32_e32 v5, 0x42800000, v88
	v_med3_f32 v4, v4, s63, v37
	v_med3_f32 v5, v5, s63, v37
	v_mov_b32_e32 v41, v11
	v_cvt_pk_fp8_f32 v41, v4, v5
	v_mul_f32_e32 v6, 0x42800000, v92
	v_mul_f32_e32 v4, 0x42800000, v96
	v_med3_f32 v5, v6, s63, v37
	v_med3_f32 v4, v4, s63, v37
	v_cvt_pk_fp8_f32 v41, v5, v4 op_sel:[0,0,1]
	v_mul_f32_e32 v4, 0x42800000, v85
	v_mul_f32_e32 v5, 0x42800000, v89
	v_med3_f32 v4, v4, s63, v37
	v_med3_f32 v5, v5, s63, v37
	v_mov_b32_e32 v42, v11
	v_cvt_pk_fp8_f32 v42, v4, v5
	v_mul_f32_e32 v6, 0x42800000, v93
	v_mul_f32_e32 v4, 0x42800000, v97
	v_med3_f32 v5, v6, s63, v37
	v_med3_f32 v4, v4, s63, v37
	v_cvt_pk_fp8_f32 v42, v5, v4 op_sel:[0,0,1]
	ds_write2_b32 v1, v7, v39 offset0:16 offset1:24
	ds_write2_b32 v1, v8, v40 offset0:49 offset1:57
	ds_write2_b32 v1, v9, v41 offset0:82 offset1:90
	ds_write2_b32 v1, v38, v42 offset0:115 offset1:123
	s_waitcnt lgkmcnt(0)
	v_add_u32_e32 v1, v24, v25
	v_lshl_add_u64 v[38:39], v[2:3], 0, v[16:17]
	ds_read2_b32 v[2:3], v1 offset1:1
	ds_read2_b32 v[4:5], v1 offset0:2 offset1:3
	v_or_b32_e32 v6, s16, v20
	v_mul_u32_u24_e32 v6, 0xb00, v6
	v_mov_b32_e32 v7, v11
	v_lshl_add_u64 v[40:41], v[38:39], 0, v[6:7]
	v_add_u32_e32 v6, 0x420, v1
	v_add_u32_e32 v8, 0x428, v1
	ds_read2_b32 v[6:7], v6 offset1:1
	ds_read2_b32 v[8:9], v8 offset1:1
	s_waitcnt lgkmcnt(2)
	global_store_dwordx4 v[40:41], v[2:5], off
	s_nop 1
	v_or_b32_e32 v2, s16, v26
	v_mul_u32_u24_e32 v2, 0xb00, v2
	v_mov_b32_e32 v3, v11
	v_lshl_add_u64 v[2:3], v[38:39], 0, v[2:3]
	s_waitcnt lgkmcnt(0)
	global_store_dwordx4 v[2:3], v[6:9], off
	v_add_u32_e32 v2, 0x840, v1
	v_add_u32_e32 v4, 0x848, v1
	v_or_b32_e32 v6, s16, v27
	ds_read2_b32 v[2:3], v2 offset1:1
	ds_read2_b32 v[4:5], v4 offset1:1
	v_mul_u32_u24_e32 v6, 0xb00, v6
	v_mov_b32_e32 v7, v11
	v_lshl_add_u64 v[40:41], v[38:39], 0, v[6:7]
	v_add_u32_e32 v6, 0xc60, v1
	v_add_u32_e32 v1, 0xc68, v1
	ds_read2_b32 v[6:7], v6 offset1:1
	ds_read2_b32 v[8:9], v1 offset1:1
	v_or_b32_e32 v1, s16, v28
	s_waitcnt lgkmcnt(2)
	global_store_dwordx4 v[40:41], v[2:5], off
	s_nop 1
	v_mul_u32_u24_e32 v2, 0xb00, v1
	v_mov_b32_e32 v3, v11
	v_lshl_add_u64 v[2:3], v[38:39], 0, v[2:3]
	s_waitcnt lgkmcnt(0)
	global_store_dwordx4 v[2:3], v[6:9], off
	s_waitcnt lgkmcnt(0)

; __device__ __forceinline__ void cvt_item8(const float* src, int ld, int k0, int c0, unsigned char* dst, int Kd, int drow0, unsigned char* scr, int lane) {
;     const int c = lane & 7, q = lane >> 3;
;     f32x4 v[4][4];
; #pragma unroll
;     for (int g = 0; g < 4; ++g)
; #pragma unroll
;         for (int j = 0; j < 4; ++j) v[g][j] = __builtin_nontemporal_load((const f32x4*)(src + (size_t)(k0 + 32 * g + 4 * q + j) * ld + c0 + 4 * c));
; #pragma unroll
;     for (int g = 0; g < 4; ++g)
; #pragma unroll
;         for (int i = 0; i < 4; ++i) *(unsigned*)(scr + (4 * c + i) * 132 + 32 * g + 4 * q) = pg8::pack_fp8x4(v[g][0][i] * WSC, v[g][1][i] * WSC, v[g][2][i] * WSC, v[g][3][i] * WSC);
; template <int GRP>
; __device__ __forceinline__ void conv_item(Frame& F, int r) {
;     ...
;         if (r < CI_WO) { const int kb = r / 64, nb = r % 64;
;             cvt_item8(inptr(F, IN_WOUT) + (size_t)l * D * D, D, kb * 128, nb * 32, ws + WS_WOUT + (size_t)l * D * D, D, nb * 32, scr, F.lane); return; }
.LBB0_639:
	s_andn2_b64 vcc, exec, s[16:17]
	s_cbranch_vccnz .LBB0_623
	s_ashr_i32 s8, s20, 31
	v_mov_b32_e32 v1, s66
	s_lshr_b32 s8, s8, 26
	s_waitcnt lgkmcnt(3)
	ds_read_b64 v[2:3], v1
	s_add_i32 s8, s20, s8
	s_and_b32 s16, s8, 0x7ffffc0
	s_sub_i32 s16, s20, s16
	s_lshl_b32 s16, s16, 5
	s_lshl_b32 s8, s8, 1
	s_ashr_i32 s17, s16, 31
	s_waitcnt lgkmcnt(0)
	v_readfirstlane_b32 s19, v2
	s_and_b32 s18, s8, 0xffffff80
	s_lshl_b64 s[20:21], s[16:17], 2
	v_readfirstlane_b32 s67, v3
	s_add_u32 s20, s19, s20
	v_or_b32_e32 v86, s18, v21
	s_addc_u32 s21, s67, s21
	v_lshlrev_b32_e32 v2, 2, v14
	v_mov_b32_e32 v3, v11
	v_lshl_add_u64 v[2:3], s[20:21], 0, v[2:3]
	v_ashrrev_i32_e32 v87, 31, v86
	v_or_b32_e32 v4, 1, v86
	v_lshl_add_u64 v[88:89], v[2:3], 0, s[14:15]
	v_lshlrev_b64 v[2:3], 13, v[86:87]
	v_ashrrev_i32_e32 v5, 31, v4
	v_lshl_add_u64 v[2:3], v[88:89], 0, v[2:3]
	v_lshlrev_b64 v[4:5], 13, v[4:5]
	v_lshl_add_u64 v[4:5], v[88:89], 0, v[4:5]
	global_load_dwordx4 v[38:41], v[2:3], off nt
	s_waitcnt vmcnt(0)
	global_load_dwordx4 v[42:45], v[4:5], off nt
	v_or_b32_e32 v2, 2, v86
	v_ashrrev_i32_e32 v3, 31, v2
	v_lshlrev_b64 v[2:3], 13, v[2:3]
	v_lshl_add_u64 v[2:3], v[88:89], 0, v[2:3]
	global_load_dwordx4 v[46:49], v[2:3], off nt
	v_or_b32_e32 v2, 3, v86
	v_ashrrev_i32_e32 v3, 31, v2
	v_lshlrev_b64 v[2:3], 13, v[2:3]
	v_lshl_add_u64 v[2:3], v[88:89], 0, v[2:3]
	global_load_dwordx4 v[50:53], v[2:3], off nt
	v_or_b32_e32 v2, 32, v86
	v_ashrrev_i32_e32 v3, 31, v2
	v_or_b32_e32 v4, 33, v86
	v_lshlrev_b64 v[2:3], 13, v[2:3]
	v_ashrrev_i32_e32 v5, 31, v4
	v_lshl_add_u64 v[2:3], v[88:89], 0, v[2:3]
	v_lshlrev_b64 v[4:5], 13, v[4:5]
	v_lshl_add_u64 v[4:5], v[88:89], 0, v[4:5]
	global_load_dwordx4 v[54:57], v[2:3], off nt
	global_load_dwordx4 v[58:61], v[4:5], off nt
	v_or_b32_e32 v2, 34, v86
	v_ashrrev_i32_e32 v3, 31, v2
	v_or_b32_e32 v4, 35, v86
	v_lshlrev_b64 v[2:3], 13, v[2:3]
	v_ashrrev_i32_e32 v5, 31, v4
	v_lshl_add_u64 v[2:3], v[88:89], 0, v[2:3]
	v_lshlrev_b64 v[4:5], 13, v[4:5]
	v_lshl_add_u64 v[4:5], v[88:89], 0, v[4:5]
	global_load_dwordx4 v[62:65], v[2:3], off nt
	global_load_dwordx4 v[66:69], v[4:5], off nt
	v_or_b32_e32 v2, 64, v86
	v_ashrrev_i32_e32 v3, 31, v2
	v_or_b32_e32 v4, 0x41, v86
	v_lshlrev_b64 v[2:3], 13, v[2:3]
	v_ashrrev_i32_e32 v5, 31, v4
	v_lshl_add_u64 v[2:3], v[88:89], 0, v[2:3]
	v_lshlrev_b64 v[4:5], 13, v[4:5]
	v_lshl_add_u64 v[4:5], v[88:89], 0, v[4:5]
	global_load_dwordx4 v[70:73], v[2:3], off nt
	global_load_dwordx4 v[74:77], v[4:5], off nt
	v_or_b32_e32 v2, 0x42, v86
	v_ashrrev_i32_e32 v3, 31, v2
	v_or_b32_e32 v4, 0x43, v86
	v_lshlrev_b64 v[2:3], 13, v[2:3]
	v_ashrrev_i32_e32 v5, 31, v4
	v_lshl_add_u64 v[2:3], v[88:89], 0, v[2:3]
	v_lshlrev_b64 v[4:5], 13, v[4:5]
	v_lshl_add_u64 v[4:5], v[88:89], 0, v[4:5]
	global_load_dwordx4 v[78:81], v[2:3], off nt
	global_load_dwordx4 v[82:85], v[4:5], off nt
	v_or_b32_e32 v2, 0x60, v86
	v_or_b32_e32 v4, 0x61, v86
	v_ashrrev_i32_e32 v3, 31, v2
	v_ashrrev_i32_e32 v5, 31, v4
	v_lshlrev_b64 v[2:3], 13, v[2:3]
	v_lshlrev_b64 v[4:5], 13, v[4:5]
	v_lshl_add_u64 v[2:3], v[88:89], 0, v[2:3]
	v_lshl_add_u64 v[6:7], v[88:89], 0, v[4:5]
	global_load_dwordx4 v[2:5], v[2:3], off nt
	s_nop 0
	global_load_dwordx4 v[6:9], v[6:7], off nt
	v_or_b32_e32 v90, 0x62, v86
	v_or_b32_e32 v86, 0x63, v86
	v_ashrrev_i32_e32 v91, 31, v90
	v_ashrrev_i32_e32 v87, 31, v86
	v_lshlrev_b64 v[90:91], 13, v[90:91]
	v_lshlrev_b64 v[86:87], 13, v[86:87]
	v_lshl_add_u64 v[90:91], v[88:89], 0, v[90:91]
	v_lshl_add_u64 v[92:93], v[88:89], 0, v[86:87]
	global_load_dwordx4 v[86:89], v[90:91], off nt
	s_nop 0
	global_load_dwordx4 v[90:93], v[92:93], off nt
	s_ashr_i32 s19, s18, 31
	s_waitcnt lgkmcnt(0)
	v_mul_f32_e32 v1, 0x42800000, v38
	s_waitcnt vmcnt(0)
	v_mul_f32_e32 v38, 0x42800000, v42
	v_med3_f32 v1, v1, s63, v37
	v_med3_f32 v38, v38, s63, v37
	v_mul_f32_e32 v42, 0x42800000, v46
	v_mov_b32_e32 v46, v11
	v_cvt_pk_fp8_f32 v46, v1, v38
	v_med3_f32 v38, v42, s63, v37
	v_mul_f32_e32 v42, 0x42800000, v47
	v_mul_f32_e32 v1, 0x42800000, v50
	v_med3_f32 v1, v1, s63, v37
	v_cvt_pk_fp8_f32 v46, v38, v1 op_sel:[0,0,1]
	v_mul_f32_e32 v38, 0x42800000, v39
	v_mul_f32_e32 v39, 0x42800000, v43
	v_med3_f32 v38, v38, s63, v37
	v_med3_f32 v39, v39, s63, v37
	v_mov_b32_e32 v43, v11
	v_cvt_pk_fp8_f32 v43, v38, v39
	v_mul_f32_e32 v38, 0x42800000, v51
	v_med3_f32 v39, v42, s63, v37
	v_med3_f32 v38, v38, s63, v37
	v_cvt_pk_fp8_f32 v43, v39, v38 op_sel:[0,0,1]
	v_mul_f32_e32 v38, 0x42800000, v40
	v_mul_f32_e32 v39, 0x42800000, v44
	v_med3_f32 v38, v38, s63, v37
	v_med3_f32 v39, v39, s63, v37
	v_mov_b32_e32 v42, v11
	v_cvt_pk_fp8_f32 v42, v38, v39
	v_mul_f32_e32 v40, 0x42800000, v48
	v_mul_f32_e32 v38, 0x42800000, v52
	v_med3_f32 v39, v40, s63, v37
	v_med3_f32 v38, v38, s63, v37
	v_cvt_pk_fp8_f32 v42, v39, v38 op_sel:[0,0,1]
	v_mul_f32_e32 v38, 0x42800000, v41
	v_mul_f32_e32 v39, 0x42800000, v45
	v_med3_f32 v38, v38, s63, v37
	v_med3_f32 v39, v39, s63, v37
	v_mov_b32_e32 v41, v11
	v_cvt_pk_fp8_f32 v41, v38, v39
	v_mul_f32_e32 v40, 0x42800000, v49
	v_mul_f32_e32 v38, 0x42800000, v53
	v_med3_f32 v39, v40, s63, v37
	v_med3_f32 v38, v38, s63, v37
	v_cvt_pk_fp8_f32 v41, v39, v38 op_sel:[0,0,1]
	v_mul_f32_e32 v38, 0x42800000, v54
	v_mul_f32_e32 v39, 0x42800000, v58
	v_med3_f32 v38, v38, s63, v37
	v_med3_f32 v39, v39, s63, v37
	v_mov_b32_e32 v44, v11
	v_cvt_pk_fp8_f32 v44, v38, v39
	v_mul_f32_e32 v40, 0x42800000, v62
	v_mul_f32_e32 v38, 0x42800000, v66
	v_med3_f32 v39, v40, s63, v37
	v_med3_f32 v38, v38, s63, v37
	v_cvt_pk_fp8_f32 v44, v39, v38 op_sel:[0,0,1]
	v_mul_f32_e32 v38, 0x42800000, v55
	v_mul_f32_e32 v39, 0x42800000, v59
	v_med3_f32 v38, v38, s63, v37
; __device__ __forceinline__ void cvt_item8(const float* src, int ld, int k0, int c0, unsigned char* dst, int Kd, int drow0, unsigned char* scr, int lane) {
;     ...
;     for (int g = 0; g < 4; ++g)
; #pragma unroll
;         for (int i = 0; i < 4; ++i) *(unsigned*)(scr + (4 * c + i) * 132 + 32 * g + 4 * q) = pg8::pack_fp8x4(v[g][0][i] * WSC, v[g][1][i] * WSC, v[g][2][i] * WSC, v[g][3][i] * WSC);
;     asm volatile("s_waitcnt lgkmcnt(0)" ::: "memory");
; #pragma unroll
;     for (int r = 0; r < 4; ++r) { const int n = 8 * r + (lane >> 3), ch = lane & 7; const unsigned char* p = scr + n * 132 + ch * 16;
;         u32x4 o; o.x = *(const unsigned*)(p); o.y = *(const unsigned*)(p + 4); o.z = *(const unsigned*)(p + 8); o.w = *(const unsigned*)(p + 12);
;         *(u32x4*)(dst + (size_t)(drow0 + n) * Kd + k0 + 16 * ch) = o; }
;     asm volatile("s_waitcnt lgkmcnt(0)" ::: "memory");
	v_med3_f32 v39, v39, s63, v37
	v_mov_b32_e32 v45, v11
	v_cvt_pk_fp8_f32 v45, v38, v39
	v_mul_f32_e32 v40, 0x42800000, v63
	v_mul_f32_e32 v38, 0x42800000, v67
	v_med3_f32 v39, v40, s63, v37
	v_med3_f32 v38, v38, s63, v37
	v_cvt_pk_fp8_f32 v45, v39, v38 op_sel:[0,0,1]
	v_mul_f32_e32 v38, 0x42800000, v56
	v_mul_f32_e32 v39, 0x42800000, v60
	v_med3_f32 v38, v38, s63, v37
	v_med3_f32 v39, v39, s63, v37
	v_mov_b32_e32 v47, v11
	v_cvt_pk_fp8_f32 v47, v38, v39
	v_mul_f32_e32 v40, 0x42800000, v64
	v_mul_f32_e32 v38, 0x42800000, v68
	v_med3_f32 v39, v40, s63, v37
	v_med3_f32 v38, v38, s63, v37
	v_cvt_pk_fp8_f32 v47, v39, v38 op_sel:[0,0,1]
	v_mul_f32_e32 v38, 0x42800000, v57
	v_mul_f32_e32 v39, 0x42800000, v61
	v_med3_f32 v38, v38, s63, v37
	v_med3_f32 v39, v39, s63, v37
	v_mov_b32_e32 v48, v11
	v_cvt_pk_fp8_f32 v48, v38, v39
	v_mul_f32_e32 v40, 0x42800000, v65
	v_mul_f32_e32 v38, 0x42800000, v69
	v_med3_f32 v39, v40, s63, v37
	v_med3_f32 v38, v38, s63, v37
	v_add_u32_e32 v1, v22, v23
	v_cvt_pk_fp8_f32 v48, v39, v38 op_sel:[0,0,1]
	v_mul_f32_e32 v38, 0x42800000, v70
	v_mul_f32_e32 v39, 0x42800000, v74
	ds_write2_b32 v1, v46, v44 offset1:8
	ds_write2_b32 v1, v43, v45 offset0:33 offset1:41
	ds_write2_b32 v1, v42, v47 offset0:66 offset1:74
	ds_write2_b32 v1, v41, v48 offset0:99 offset1:107
	v_med3_f32 v38, v38, s63, v37
	v_med3_f32 v39, v39, s63, v37
	v_mov_b32_e32 v41, v11
	v_cvt_pk_fp8_f32 v41, v38, v39
	v_mul_f32_e32 v40, 0x42800000, v78
	v_mul_f32_e32 v38, 0x42800000, v82
	v_med3_f32 v39, v40, s63, v37
	v_med3_f32 v38, v38, s63, v37
	v_cvt_pk_fp8_f32 v41, v39, v38 op_sel:[0,0,1]
	v_mul_f32_e32 v38, 0x42800000, v71
	v_mul_f32_e32 v39, 0x42800000, v75
	v_med3_f32 v38, v38, s63, v37
	v_med3_f32 v39, v39, s63, v37
	v_mov_b32_e32 v42, v11
	v_cvt_pk_fp8_f32 v42, v38, v39
	v_mul_f32_e32 v40, 0x42800000, v79
	v_mul_f32_e32 v38, 0x42800000, v83
	v_med3_f32 v39, v40, s63, v37
	v_med3_f32 v38, v38, s63, v37
	v_cvt_pk_fp8_f32 v42, v39, v38 op_sel:[0,0,1]
	v_mul_f32_e32 v38, 0x42800000, v72
	v_mul_f32_e32 v39, 0x42800000, v76
	v_med3_f32 v38, v38, s63, v37
	v_med3_f32 v39, v39, s63, v37
	v_mov_b32_e32 v43, v11
	v_cvt_pk_fp8_f32 v43, v38, v39
	v_mul_f32_e32 v40, 0x42800000, v80
	v_mul_f32_e32 v38, 0x42800000, v84
	v_med3_f32 v39, v40, s63, v37
	v_med3_f32 v38, v38, s63, v37
	v_cvt_pk_fp8_f32 v43, v39, v38 op_sel:[0,0,1]
	v_mul_f32_e32 v38, 0x42800000, v73
	v_mul_f32_e32 v39, 0x42800000, v77
	v_med3_f32 v38, v38, s63, v37
	v_med3_f32 v39, v39, s63, v37
	v_mov_b32_e32 v44, v11
	v_cvt_pk_fp8_f32 v44, v38, v39
	v_mul_f32_e32 v40, 0x42800000, v81
	v_mul_f32_e32 v38, 0x42800000, v85
	v_med3_f32 v39, v40, s63, v37
	v_med3_f32 v38, v38, s63, v37
	v_mul_f32_e32 v2, 0x42800000, v2
	v_mul_f32_e32 v6, 0x42800000, v6
	v_cvt_pk_fp8_f32 v44, v39, v38 op_sel:[0,0,1]
	v_med3_f32 v2, v2, s63, v37
	v_med3_f32 v6, v6, s63, v37
	v_mov_b32_e32 v39, v11
	v_cvt_pk_fp8_f32 v39, v2, v6
	v_mul_f32_e32 v38, 0x42800000, v86
	v_mul_f32_e32 v2, 0x42800000, v90
	v_med3_f32 v6, v38, s63, v37
	v_med3_f32 v2, v2, s63, v37
	v_cvt_pk_fp8_f32 v39, v6, v2 op_sel:[0,0,1]
	v_mul_f32_e32 v2, 0x42800000, v3
	v_mul_f32_e32 v3, 0x42800000, v7
	v_med3_f32 v2, v2, s63, v37
	v_med3_f32 v3, v3, s63, v37
	v_mov_b32_e32 v7, v11
	v_cvt_pk_fp8_f32 v7, v2, v3
	v_mul_f32_e32 v6, 0x42800000, v87
	v_mul_f32_e32 v2, 0x42800000, v91
	v_med3_f32 v3, v6, s63, v37
	v_med3_f32 v2, v2, s63, v37
	v_cvt_pk_fp8_f32 v7, v3, v2 op_sel:[0,0,1]
	v_mul_f32_e32 v2, 0x42800000, v4
	v_mul_f32_e32 v3, 0x42800000, v8
	v_med3_f32 v2, v2, s63, v37
	v_med3_f32 v3, v3, s63, v37
	v_mov_b32_e32 v6, v11
	v_cvt_pk_fp8_f32 v6, v2, v3
	v_mul_f32_e32 v4, 0x42800000, v88
	v_mul_f32_e32 v2, 0x42800000, v92
	v_med3_f32 v3, v4, s63, v37
	v_med3_f32 v2, v2, s63, v37
	v_cvt_pk_fp8_f32 v6, v3, v2 op_sel:[0,0,1]
	v_mul_f32_e32 v2, 0x42800000, v5
	v_mul_f32_e32 v3, 0x42800000, v9
	v_med3_f32 v2, v2, s63, v37
	v_med3_f32 v3, v3, s63, v37
	v_mov_b32_e32 v5, v11
	v_cvt_pk_fp8_f32 v5, v2, v3
	v_mul_f32_e32 v4, 0x42800000, v89
	v_mul_f32_e32 v2, 0x42800000, v93
	v_med3_f32 v3, v4, s63, v37
	v_med3_f32 v2, v2, s63, v37
	v_cvt_pk_fp8_f32 v5, v3, v2 op_sel:[0,0,1]
	ds_write2_b32 v1, v41, v39 offset0:16 offset1:24
	ds_write2_b32 v1, v42, v7 offset0:49 offset1:57
	ds_write2_b32 v1, v43, v6 offset0:82 offset1:90
	ds_write2_b32 v1, v44, v5 offset0:115 offset1:123
	s_waitcnt lgkmcnt(0)
	v_add_u32_e32 v1, v24, v25
	ds_read2_b32 v[2:3], v1 offset1:1
	ds_read2_b32 v[4:5], v1 offset0:2 offset1:3
	v_or_b32_e32 v6, s16, v20
	v_ashrrev_i32_e32 v7, 31, v6
	v_lshl_add_u64 v[38:39], v[18:19], 0, s[18:19]
	v_lshlrev_b64 v[6:7], 11, v[6:7]
	v_lshl_add_u64 v[40:41], v[38:39], 0, v[6:7]
	v_add_u32_e32 v6, 0x420, v1
	v_add_u32_e32 v8, 0x428, v1
	ds_read2_b32 v[6:7], v6 offset1:1
	ds_read2_b32 v[8:9], v8 offset1:1
	s_waitcnt lgkmcnt(2)
	global_store_dwordx4 v[40:41], v[2:5], off
	s_nop 1
	v_or_b32_e32 v2, s16, v26
	v_ashrrev_i32_e32 v3, 31, v2
	v_lshlrev_b64 v[2:3], 11, v[2:3]
	v_lshl_add_u64 v[2:3], v[38:39], 0, v[2:3]
	s_waitcnt lgkmcnt(0)
	global_store_dwordx4 v[2:3], v[6:9], off
	v_add_u32_e32 v2, 0x840, v1
	v_add_u32_e32 v4, 0x848, v1
	ds_read2_b32 v[2:3], v2 offset1:1
	ds_read2_b32 v[4:5], v4 offset1:1
	v_or_b32_e32 v6, s16, v27
	v_ashrrev_i32_e32 v7, 31, v6
	v_lshlrev_b64 v[6:7], 11, v[6:7]
	v_lshl_add_u64 v[40:41], v[38:39], 0, v[6:7]
	v_add_u32_e32 v6, 0xc60, v1
	v_add_u32_e32 v1, 0xc68, v1
	ds_read2_b32 v[6:7], v6 offset1:1
	ds_read2_b32 v[8:9], v1 offset1:1
	s_waitcnt lgkmcnt(2)
	global_store_dwordx4 v[40:41], v[2:5], off
	s_nop 1
	v_or_b32_e32 v2, s16, v28
	v_ashrrev_i32_e32 v3, 31, v2
	v_lshlrev_b64 v[2:3], 11, v[2:3]
	v_lshl_add_u64 v[2:3], v[38:39], 0, v[2:3]
	s_waitcnt lgkmcnt(0)
	global_store_dwordx4 v[2:3], v[6:9], off
	s_waitcnt lgkmcnt(0)
	s_branch .LBB0_623

; #define LAS __attribute__((address_space(3)))
; __device__ __forceinline__ void prefetch(Pre& P, const bf16_t* proj, const float* gates, size_t rb, int c, int h, int tid, int lane) {
;     const int cc = tid & 31, rg = tid >> 5;
;     const int col = (cc < 16) ? (C_LQ + h * 128 + 8 * cc) : (C_LK + h * 128 + 8 * (cc - 16));
; #pragma unroll
;     for (int i = 0; i < 7; ++i) { const int pos = c * 64 + 4 * rg - 3 + i;
;         if (pos >= 0) P.raw[i] = *(const u32x4*)(proj + (rb + pos) * NIN + col); else P.raw[i] = (u32x4){0u, 0u, 0u, 0u}; }
; __device__ __forceinline__ void z_setup(Frame& F, const float* conv_w, const float* conv_b, const float* normw) {
;     __syncthreads();
;     for (int i = F.tid; i < 5 * 1024; i += NTHR) { const int j = i >> 10, ch = i & 1023; ((LAS float*)(F.lds + ZCW))[i] = (j < 4) ? conv_w[j * 1024 + ch] : conv_b[ch]; }
;     ((LAS float*)(F.lds + ZNW))[F.tid] = normw[F.tid];
;     __syncthreads();
; }
.LBB0_645:
	s_mov_b64 s[8:9], 0x1000
	v_lshl_add_u64 v[10:11], v[4:5], 0, s[8:9]
	v_lshl_add_u64 v[12:13], v[10:11], 0, s[8:9]
	v_lshl_add_u64 v[14:15], v[12:13], 0, s[8:9]
	v_lshl_add_u64 v[16:17], s[6:7], 0, v[2:3]
	global_load_dword v20, v[4:5], off
	global_load_dword v21, v[4:5], off offset:2048
	global_load_dword v22, v[10:11], off
	global_load_dword v23, v[10:11], off offset:2048
	global_load_dword v24, v[12:13], off
	global_load_dword v25, v[12:13], off offset:2048
	global_load_dword v26, v[14:15], off
	global_load_dword v27, v[14:15], off offset:2048
	global_load_dword v28, v[16:17], off
	global_load_dword v29, v[16:17], off offset:2048
	s_waitcnt vmcnt(0)
	ds_write_b32 v1, v20
	ds_write_b32 v1, v21 offset:2048
	ds_write_b32 v1, v22 offset:4096
	ds_write_b32 v1, v23 offset:6144
	ds_write_b32 v1, v24 offset:8192
	ds_write_b32 v1, v25 offset:10240
	ds_write_b32 v1, v26 offset:12288
	ds_write_b32 v1, v27 offset:14336
	ds_write_b32 v1, v28 offset:16384
	ds_write_b32 v1, v29 offset:18432
	v_mov_b32_e32 v34, 0
	v_lshlrev_b32_e32 v110, 2, v0
	v_mov_b32_e32 v111, v34
	v_lshl_add_u64 v[2:3], s[0:1], 0, v[110:111]
	global_load_dword v1, v[2:3], off
	v_lshl_add_u32 v2, v0, 2, 0
	s_cmpk_lt_i32 s2, 0x400
	v_add_u32_e32 v2, 0x1f300, v2
	s_cselect_b64 s[0:1], -1, 0
	s_cmpk_gt_i32 s2, 0x3ff
	s_waitcnt vmcnt(0) lgkmcnt(0)
	ds_write_b32 v2, v1
	s_waitcnt lgkmcnt(0)
	s_barrier
	s_cbranch_scc1 .LBB0_656
	s_ashr_i32 s3, s2, 5
	s_and_b32 s4, s3, 3
	v_and_b32_e32 v1, 31, v0
	s_lshl_b32 s11, s4, 7
	v_lshlrev_b32_e32 v2, 3, v1
	v_or_b32_e32 v3, s11, v2
	v_add_u32_e32 v2, s11, v2
	s_lshl_b32 s8, s2, 6
	v_or_b32_e32 v3, 0x600, v3
	v_add_u32_e32 v2, 0x780, v2
	v_cmp_gt_u32_e32 vcc, 16, v1
	s_ashr_i32 s6, s2, 7
	s_and_b32 s10, s8, 0x7c0
	v_lshrrev_b32_e32 v8, 5, v0
	v_cndmask_b32_e32 v3, v2, v3, vcc
	s_ashr_i32 s7, s6, 31
	v_lshl_or_b32 v2, v8, 2, s10
	v_lshlrev_b32_e32 v4, 1, v3
	v_mov_b32_e32 v5, v34
	s_lshl_b64 s[6:7], s[6:7], 11
	v_add_u32_e32 v6, -3, v2
	v_lshl_add_u64 v[4:5], s[58:59], 0, v[4:5]
	v_cmp_ne_u32_e32 vcc, 0, v2
	v_mov_b32_e32 v35, 0
	v_mov_b32_e32 v36, 0
	v_mov_b32_e32 v37, 0
	s_and_saveexec_b64 s[8:9], vcc
	s_cbranch_execz .LBB0_649
	v_mov_b32_e32 v7, 0
	v_lshl_add_u64 v[10:11], s[6:7], 0, v[6:7]
	s_movk_i32 s14, 0x2600
	v_mad_u64_u32 v[12:13], s[12:13], v10, s14, v[4:5]
	v_mad_i32_i24 v13, v11, s14, v13
	global_load_dwordx4 v[34:37], v[12:13], off

; __device__ __forceinline__ void colmax_item(const float* src, int ld, int k0, int c0, float* cmx  , int lane) {
;     const int c = lane & 7, q = lane >> 3;
;     f32x4 mx = (f32x4){0.f, 0.f, 0.f, 0.f};
; #pragma unroll
;     for (int g = 0; g < 4; ++g)
; #pragma unroll
;         for (int j = 0; j < 4; ++j) { const f32x4 v = *(const f32x4*)(src + (size_t)(k0 + 32 * g + 4 * q + j) * ld + c0 + 4 * c);
;             mx[0] = fmaxf(mx[0], fabsf(v[0])); mx[1] = fmaxf(mx[1], fabsf(v[1])); mx[2] = fmaxf(mx[2], fabsf(v[2])); mx[3] = fmaxf(mx[3], fabsf(v[3])); }
; #pragma unroll
;     for (int i = 0; i < 4; ++i) { float v = mx[i]; v = fmaxf(v, __shfl_xor(v, 8)); v = fmaxf(v, __shfl_xor(v, 16)); v = fmaxf(v, __shfl_xor(v, 32)); mx[i] = v; }
;     if (q == 0) {
; #pragma unroll
;         for (int i = 0; i < 4; ++i) atomicMax((unsigned*)(cmx + 4 * c + i), __float_as_uint(mx[i] * CMS_F)); }
; }
; template <int GRP>
; __device__ __forceinline__ void conv_item(Frame& F, int r) {
;     ...
;         if (r < NI) { const int kb = r / 152, nb = r % 152, c0 = (nb < 112) ? nb * 32 : SRC_GATE + 8 + (nb - 112) * 32, drow = nb * 32;
;             if (QUANT) cvt_item_i8(inptr(F, IN_WIN) + (size_t)l * D * NIN_SRC, NIN_SRC, kb * 128, c0, ws + WS_WIN + (size_t)l * NIN * D, D, drow, cmx + CMX_WIN + l * NIN + drow, scr, F.lane);
;             else colmax_item(inptr(F, IN_WIN) + (size_t)l * D * NIN_SRC, NIN_SRC, kb * 128, c0, cmx + CMX_WIN + l * NIN + drow, F.lane);
.LBB0_785:
	s_mul_hi_i32 s8, s3, 0x6bca1af3
	s_lshr_b32 s20, s8, 31
	s_ashr_i32 s8, s8, 6
	s_add_i32 s8, s8, s20
	s_mul_i32 s20, s8, 0xffffff68
	s_add_i32 s21, s3, s20
	s_mul_i32 s20, s8, 0xffffed00
	v_mov_b32_e32 v1, s25
	s_add_i32 s20, s4, s20
	s_waitcnt lgkmcnt(3)
	ds_read_b64 v[2:3], v1
	s_add_i32 s22, s20, 8
	s_cmpk_lt_i32 s21, 0x70
	s_cselect_b32 s22, s20, s22
	s_ashr_i32 s23, s22, 31
	s_waitcnt lgkmcnt(0)
	v_readfirstlane_b32 s21, v2
	s_lshl_b64 s[22:23], s[22:23], 2
	v_readfirstlane_b32 s69, v3
	s_add_u32 s22, s21, s22
	s_addc_u32 s23, s69, s23
	v_lshl_or_b32 v1, s8, 7, v15
	v_lshl_add_u64 v[2:3], s[22:23], 0, v[10:11]
	s_mov_b64 s[22:23], 0x2610000
	v_lshl_add_u64 v[38:39], v[2:3], 0, s[22:23]
	v_or_b32_e32 v6, 1, v1
	v_mad_i64_i32 v[2:3], s[22:23], v1, s26, v[38:39]
	v_mad_i64_i32 v[6:7], s[22:23], v6, s26, v[38:39]
	global_load_dwordx4 v[2:5], v[2:3], off
	v_cmp_lt_i32_e32 vcc, v31, v32
	global_load_dwordx4 v[6:9], v[6:7], off
	s_waitcnt vmcnt(0) lgkmcnt(0)
	v_max3_f32 v40, |v2|, 0, |v6|
	v_or_b32_e32 v2, 2, v1
	v_or_b32_e32 v6, 3, v1
	v_max3_f32 v41, |v3|, 0, |v7|
	v_mad_i64_i32 v[2:3], s[22:23], v2, s26, v[38:39]
	v_mad_i64_i32 v[6:7], s[22:23], v6, s26, v[38:39]
	v_max3_f32 v42, |v4|, 0, |v8|
	v_max3_f32 v43, |v5|, 0, |v9|
	global_load_dwordx4 v[2:5], v[2:3], off
	s_nop 0
	global_load_dwordx4 v[6:9], v[6:7], off
	s_waitcnt vmcnt(0) lgkmcnt(0)
	v_max3_f32 v40, v40, |v2|, |v6|
	v_or_b32_e32 v2, 32, v1
	v_or_b32_e32 v6, 33, v1
	v_max3_f32 v41, v41, |v3|, |v7|
	v_mad_i64_i32 v[2:3], s[22:23], v2, s26, v[38:39]
	v_mad_i64_i32 v[6:7], s[22:23], v6, s26, v[38:39]
	v_max3_f32 v42, v42, |v4|, |v8|
	v_max3_f32 v43, v43, |v5|, |v9|
	global_load_dwordx4 v[2:5], v[2:3], off
	s_nop 0
	global_load_dwordx4 v[6:9], v[6:7], off
	s_waitcnt vmcnt(0) lgkmcnt(0)
	v_max3_f32 v40, v40, |v2|, |v6|
	v_or_b32_e32 v2, 34, v1
	v_or_b32_e32 v6, 35, v1
	v_max3_f32 v41, v41, |v3|, |v7|
	v_mad_i64_i32 v[2:3], s[22:23], v2, s26, v[38:39]
	v_mad_i64_i32 v[6:7], s[22:23], v6, s26, v[38:39]
	v_max3_f32 v42, v42, |v4|, |v8|
	v_max3_f32 v43, v43, |v5|, |v9|
	global_load_dwordx4 v[2:5], v[2:3], off
	s_nop 0
	global_load_dwordx4 v[6:9], v[6:7], off
	s_waitcnt vmcnt(0) lgkmcnt(0)
	v_max3_f32 v40, v40, |v2|, |v6|
	v_or_b32_e32 v2, 64, v1
	v_or_b32_e32 v6, 0x41, v1
	v_max3_f32 v41, v41, |v3|, |v7|
	v_mad_i64_i32 v[2:3], s[22:23], v2, s26, v[38:39]
	v_mad_i64_i32 v[6:7], s[22:23], v6, s26, v[38:39]
	v_max3_f32 v42, v42, |v4|, |v8|
	v_max3_f32 v43, v43, |v5|, |v9|
	global_load_dwordx4 v[2:5], v[2:3], off
	s_nop 0
	global_load_dwordx4 v[6:9], v[6:7], off
	s_waitcnt vmcnt(0) lgkmcnt(0)
	v_max3_f32 v40, v40, |v2|, |v6|
	v_or_b32_e32 v2, 0x42, v1
	v_or_b32_e32 v6, 0x43, v1
	v_max3_f32 v41, v41, |v3|, |v7|
	v_mad_i64_i32 v[2:3], s[22:23], v2, s26, v[38:39]
	v_mad_i64_i32 v[6:7], s[22:23], v6, s26, v[38:39]
	v_max3_f32 v42, v42, |v4|, |v8|
	v_max3_f32 v43, v43, |v5|, |v9|
	global_load_dwordx4 v[2:5], v[2:3], off
	s_nop 0
	global_load_dwordx4 v[6:9], v[6:7], off
	s_waitcnt vmcnt(0) lgkmcnt(0)
	v_max3_f32 v40, v40, |v2|, |v6|
	v_or_b32_e32 v2, 0x60, v1
	v_or_b32_e32 v6, 0x61, v1
	v_max3_f32 v41, v41, |v3|, |v7|
	v_mad_i64_i32 v[2:3], s[22:23], v2, s26, v[38:39]
	v_mad_i64_i32 v[6:7], s[22:23], v6, s26, v[38:39]
	v_max3_f32 v42, v42, |v4|, |v8|
	v_max3_f32 v43, v43, |v5|, |v9|
	global_load_dwordx4 v[2:5], v[2:3], off
	s_nop 0
	global_load_dwordx4 v[6:9], v[6:7], off
	s_waitcnt vmcnt(0) lgkmcnt(0)
	v_max3_f32 v40, v40, |v2|, |v6|
	v_or_b32_e32 v2, 0x62, v1
	v_or_b32_e32 v1, 0x63, v1
	v_max3_f32 v41, v41, |v3|, |v7|
	v_mad_i64_i32 v[2:3], s[22:23], v2, s26, v[38:39]
	v_mad_i64_i32 v[6:7], s[22:23], v1, s26, v[38:39]
	v_max3_f32 v42, v42, |v4|, |v8|
	v_max3_f32 v43, v43, |v5|, |v9|
	global_load_dwordx4 v[2:5], v[2:3], off
	s_nop 0
	global_load_dwordx4 v[6:9], v[6:7], off
	s_waitcnt vmcnt(0) lgkmcnt(0)
	v_max3_f32 v1, v40, |v2|, |v6|
	v_cndmask_b32_e32 v2, v30, v31, vcc
	v_cmp_lt_i32_e32 vcc, v33, v32
	v_max3_f32 v6, v42, |v4|, |v8|
	v_lshlrev_b32_e32 v8, 2, v2
	v_cndmask_b32_e32 v2, v30, v33, vcc
	v_cmp_lt_i32_e32 vcc, v34, v32
	v_max3_f32 v3, v41, |v3|, |v7|
	v_max3_f32 v7, v43, |v5|, |v9|
	v_lshlrev_b32_e32 v9, 2, v2
	v_cndmask_b32_e32 v2, v30, v34, vcc
	v_lshlrev_b32_e32 v38, 2, v2
	ds_bpermute_b32 v2, v8, v1
	ds_bpermute_b32 v4, v8, v3
	ds_bpermute_b32 v5, v8, v6
	ds_bpermute_b32 v8, v8, v7
	s_waitcnt lgkmcnt(3)
	v_max_f32_e32 v2, v2, v2
	s_waitcnt lgkmcnt(2)
	v_max_f32_e32 v4, v4, v4
	s_waitcnt lgkmcnt(1)
	v_max_f32_e32 v5, v5, v5
	s_waitcnt lgkmcnt(0)
	v_max_f32_e32 v8, v8, v8
	v_max_f32_e32 v1, v1, v2
	v_max_f32_e32 v3, v3, v4
	v_max_f32_e32 v5, v6, v5
	v_max_f32_e32 v7, v7, v8
	ds_bpermute_b32 v2, v9, v1
	ds_bpermute_b32 v4, v9, v3
	ds_bpermute_b32 v6, v9, v5
	ds_bpermute_b32 v8, v9, v7
	s_waitcnt lgkmcnt(3)
	v_max_f32_e32 v2, v2, v2
	s_waitcnt lgkmcnt(2)
	v_max_f32_e32 v4, v4, v4
	s_waitcnt lgkmcnt(1)
	v_max_f32_e32 v6, v6, v6
	s_waitcnt lgkmcnt(0)
	v_max_f32_e32 v8, v8, v8
	v_max_f32_e32 v1, v1, v2
	v_max_f32_e32 v3, v3, v4
	v_max_f32_e32 v5, v5, v6
	v_max_f32_e32 v7, v7, v8
	ds_bpermute_b32 v2, v38, v1
	ds_bpermute_b32 v4, v38, v3
	ds_bpermute_b32 v6, v38, v5
	ds_bpermute_b32 v8, v38, v7
	s_and_saveexec_b64 s[22:23], s[6:7]
	s_cbranch_execz .LBB0_787
	s_waitcnt lgkmcnt(3)
	v_max_f32_e32 v2, v2, v2
	v_max_f32_e32 v1, v1, v1
	s_ashr_i32 s21, s20, 31
	s_waitcnt lgkmcnt(2)
	v_max_f32_e32 v4, v4, v4
	v_max_f32_e32 v3, v3, v3
	v_max_f32_e32 v1, v1, v2
	s_waitcnt lgkmcnt(1)
	v_max_f32_e32 v6, v6, v6
	v_max_f32_e32 v5, v5, v5
	v_max_f32_e32 v4, v3, v4
	v_lshl_add_u64 v[2:3], s[20:21], 2, v[12:13]
	v_mul_f32_e32 v1, 0x3fb33333, v1
	s_waitcnt lgkmcnt(0)
	v_max_f32_e32 v8, v8, v8
	v_max_f32_e32 v7, v7, v7
	v_max_f32_e32 v5, v5, v6
	global_atomic_umax v[2:3], v1, off
	v_mul_f32_e32 v1, 0x3fb33333, v4
	v_max_f32_e32 v7, v7, v8
	global_atomic_umax v[2:3], v1, off offset:4
	v_mul_f32_e32 v1, 0x3fb33333, v5
	global_atomic_umax v[2:3], v1, off offset:8
	v_mul_f32_e32 v1, 0x3fb33333, v7
	global_atomic_umax v[2:3], v1, off offset:12

; __device__ __forceinline__ void colmax_item(const float* src, int ld, int k0, int c0, float* cmx  , int lane) {
;     const int c = lane & 7, q = lane >> 3;
;     f32x4 mx = (f32x4){0.f, 0.f, 0.f, 0.f};
; #pragma unroll
;     for (int g = 0; g < 4; ++g)
; #pragma unroll
;         for (int j = 0; j < 4; ++j) { const f32x4 v = *(const f32x4*)(src + (size_t)(k0 + 32 * g + 4 * q + j) * ld + c0 + 4 * c);
;             mx[0] = fmaxf(mx[0], fabsf(v[0])); mx[1] = fmaxf(mx[1], fabsf(v[1])); mx[2] = fmaxf(mx[2], fabsf(v[2])); mx[3] = fmaxf(mx[3], fabsf(v[3])); }
; #pragma unroll
;     for (int i = 0; i < 4; ++i) { float v = mx[i]; v = fmaxf(v, __shfl_xor(v, 8)); v = fmaxf(v, __shfl_xor(v, 16)); v = fmaxf(v, __shfl_xor(v, 32)); mx[i] = v; }
;     if (q == 0) {
; #pragma unroll
;         for (int i = 0; i < 4; ++i) atomicMax((unsigned*)(cmx + 4 * c + i), __float_as_uint(mx[i] * CMS_F)); }
; }
; template <int GRP>
; __device__ __forceinline__ void conv_item(Frame& F, int r) {
;     ...
;     else { constexpr int KBN = (GRP == 3) ? 16 : CMS_KB, I_E = KBN * 88; const int up = r / (8 * I_E); r %= (8 * I_E); const int e = r / I_E; r %= I_E; const int kb = r / 88, nb = r % 88, n0 = nb * 32, drow = (n0 >> 7) * 256 + up * 128 + (n0 & 127);
;         if (GRP == 3) cvt_item_i8(inptr(F, up ? IN_MU : IN_MG) + (size_t)e * D * DFE, DFE, kb * 128, n0, ws + WS_MGU + (size_t)e * 2 * DFE * D, D, drow, cmx + 2 * DFF + e * 2 * DFE + drow, scr, F.lane);
;         else colmax_item(inptr(F, up ? IN_MU : IN_MG) + (size_t)e * D * DFE, DFE, kb * 128, n0, cmx + 2 * DFF + e * 2 * DFE + drow, F.lane); }
.LBB0_789:
	s_cmpk_gt_i32 s22, 0x3ff
	s_mov_b64 s[16:17], -1
	s_cbranch_scc0 .LBB0_797
	s_cmpk_gt_u32 s22, 0x2fff
	s_cbranch_scc0 .LBB0_794
	s_add_i32 s8, s22, 0xffffd000
	s_add_i32 s16, s22, 0xca80
	s_cmpk_lt_u32 s8, 0x580
	s_cselect_b32 s16, s8, s16
	s_and_b32 s17, s16, 0xffff
	s_mul_i32 s17, s17, 0xba2f
	s_lshr_b32 s23, s17, 23
	s_mul_i32 s17, s23, 0xb0
	s_sub_i32 s16, s16, s17
	s_and_b32 s17, s16, 0xffff
	s_add_i32 s16, s17, 0xffffffa8
	s_min_u32 s69, s17, s16
	s_lshl_b32 s16, s69, 5
	s_cmpk_lt_u32 s22, 0x3580
	s_movk_i32 s20, 0xa0
	s_cselect_b32 s20, s20, 0xa8
	s_add_i32 s20, s20, 0
	s_add_i32 s20, s20, 0x20200
	v_mov_b32_e32 v1, s20
	s_waitcnt lgkmcnt(3)
	ds_read_b64 v[2:3], v1
	s_cmpk_gt_u32 s17, 0x57
	s_cselect_b32 s17, 0x80, 0
	v_or_b32_e32 v1, s17, v15
	s_ashr_i32 s17, s16, 31
	s_waitcnt lgkmcnt(0)
	v_readfirstlane_b32 s20, v2
	v_readfirstlane_b32 s21, v3
	v_mul_u32_u24_e32 v2, s23, v35
	v_mov_b32_e32 v3, v11
	v_lshlrev_b64 v[2:3], 2, v[2:3]
	v_lshl_add_u64 v[2:3], s[20:21], 0, v[2:3]
	s_lshl_b64 s[20:21], s[16:17], 2
	v_lshl_add_u64 v[2:3], v[2:3], 0, s[20:21]
	v_lshl_add_u64 v[2:3], v[2:3], 0, v[10:11]
	v_mul_u32_u24_e32 v4, 0x2c00, v1
	v_mov_b32_e32 v5, v11
	v_lshl_add_u64 v[2:3], v[2:3], 0, v[4:5]
	v_add_co_u32_e32 v8, vcc, s27, v2
	global_load_dwordx4 v[4:7], v[2:3], off
	s_nop 0
	v_addc_co_u32_e32 v9, vcc, 0, v3, vcc
	global_load_dwordx4 v[38:41], v[8:9], off offset:3072
	s_movk_i32 s17, 0x5000
	s_waitcnt vmcnt(0) lgkmcnt(0)
	v_max3_f32 v1, |v4|, 0, |v38|
	v_add_co_u32_e32 v4, vcc, s17, v2
	v_max3_f32 v42, |v5|, 0, |v39|
	s_nop 0
	v_addc_co_u32_e32 v5, vcc, 0, v3, vcc
	v_add_co_u32_e32 v8, vcc, s28, v2
	v_max3_f32 v43, |v6|, 0, |v40|
	s_nop 0
	v_addc_co_u32_e32 v9, vcc, 0, v3, vcc
	v_max3_f32 v44, |v7|, 0, |v41|
	global_load_dwordx4 v[4:7], v[4:5], off offset:2048
	s_nop 0
	global_load_dwordx4 v[38:41], v[8:9], off offset:1024
	s_waitcnt vmcnt(0) lgkmcnt(0)
	v_max3_f32 v1, v1, |v4|, |v38|
	v_add_co_u32_e32 v4, vcc, s29, v2
	v_max3_f32 v42, v42, |v5|, |v39|
	s_nop 0
	v_addc_co_u32_e32 v5, vcc, 0, v3, vcc
	v_add_co_u32_e32 v8, vcc, s30, v2
	v_max3_f32 v43, v43, |v6|, |v40|
	s_nop 0
	v_addc_co_u32_e32 v9, vcc, 0, v3, vcc
	v_max3_f32 v44, v44, |v7|, |v41|
	global_load_dwordx4 v[4:7], v[4:5], off
	s_nop 0
	global_load_dwordx4 v[38:41], v[8:9], off offset:3072
	s_waitcnt vmcnt(0) lgkmcnt(0)
	v_max3_f32 v1, v1, |v4|, |v38|
	v_add_co_u32_e32 v4, vcc, s31, v2
	v_max3_f32 v42, v42, |v5|, |v39|
	s_nop 0
	v_addc_co_u32_e32 v5, vcc, 0, v3, vcc
	v_add_co_u32_e32 v8, vcc, s34, v2
	v_max3_f32 v43, v43, |v6|, |v40|
	s_nop 0
	v_addc_co_u32_e32 v9, vcc, 0, v3, vcc
	v_max3_f32 v44, v44, |v7|, |v41|
	global_load_dwordx4 v[4:7], v[4:5], off offset:2048
	s_nop 0
	global_load_dwordx4 v[38:41], v[8:9], off offset:1024
	s_waitcnt vmcnt(0) lgkmcnt(0)
	v_max3_f32 v1, v1, |v4|, |v38|
	v_add_co_u32_e32 v4, vcc, s35, v2
	v_max3_f32 v42, v42, |v5|, |v39|
	s_nop 0
	v_addc_co_u32_e32 v5, vcc, 0, v3, vcc
	v_add_co_u32_e32 v8, vcc, s36, v2
	v_max3_f32 v43, v43, |v6|, |v40|
	s_nop 0
	v_addc_co_u32_e32 v9, vcc, 0, v3, vcc
	v_max3_f32 v44, v44, |v7|, |v41|
	global_load_dwordx4 v[4:7], v[4:5], off
	s_nop 0
	global_load_dwordx4 v[38:41], v[8:9], off offset:3072
	s_waitcnt vmcnt(0) lgkmcnt(0)
	v_max3_f32 v1, v1, |v4|, |v38|
	v_add_co_u32_e32 v4, vcc, s37, v2
	v_max3_f32 v42, v42, |v5|, |v39|
	s_nop 0
	v_addc_co_u32_e32 v5, vcc, 0, v3, vcc
	v_add_co_u32_e32 v8, vcc, s38, v2
	v_max3_f32 v43, v43, |v6|, |v40|
	s_nop 0
	v_addc_co_u32_e32 v9, vcc, 0, v3, vcc
	v_max3_f32 v44, v44, |v7|, |v41|
	global_load_dwordx4 v[4:7], v[4:5], off offset:2048
	s_nop 0
	global_load_dwordx4 v[38:41], v[8:9], off offset:1024
	s_waitcnt vmcnt(0) lgkmcnt(0)
	v_max3_f32 v1, v1, |v4|, |v38|
	v_add_co_u32_e32 v4, vcc, s39, v2
	v_max3_f32 v42, v42, |v5|, |v39|
	s_nop 0
	v_addc_co_u32_e32 v5, vcc, 0, v3, vcc
	v_add_co_u32_e32 v8, vcc, s40, v2
	v_max3_f32 v43, v43, |v6|, |v40|
	s_nop 0
	v_addc_co_u32_e32 v9, vcc, 0, v3, vcc
	v_max3_f32 v44, v44, |v7|, |v41|
	global_load_dwordx4 v[4:7], v[4:5], off
	s_nop 0
	global_load_dwordx4 v[38:41], v[8:9], off offset:3072
	s_waitcnt vmcnt(0) lgkmcnt(0)
	v_max3_f32 v1, v1, |v4|, |v38|
	v_add_co_u32_e32 v4, vcc, s41, v2
	v_max3_f32 v8, v42, |v5|, |v39|
	s_nop 0
	v_addc_co_u32_e32 v5, vcc, 0, v3, vcc
	v_add_co_u32_e32 v2, vcc, s42, v2
	v_max3_f32 v9, v43, |v6|, |v40|
	s_nop 0
	v_addc_co_u32_e32 v3, vcc, 0, v3, vcc
	v_max3_f32 v42, v44, |v7|, |v41|
	global_load_dwordx4 v[4:7], v[4:5], off offset:2048
	v_cmp_lt_i32_e32 vcc, v31, v32
	global_load_dwordx4 v[38:41], v[2:3], off offset:1024
	s_waitcnt vmcnt(0) lgkmcnt(0)
	v_max3_f32 v3, v8, |v5|, |v39|
	v_cndmask_b32_e32 v2, v30, v31, vcc
	v_cmp_lt_i32_e32 vcc, v33, v32
	v_lshlrev_b32_e32 v8, 2, v2
	v_max3_f32 v1, v1, |v4|, |v38|
	v_cndmask_b32_e32 v2, v30, v33, vcc
	v_cmp_lt_i32_e32 vcc, v34, v32
	v_max3_f32 v5, v9, |v6|, |v40|
	v_max3_f32 v7, v42, |v7|, |v41|
	v_lshlrev_b32_e32 v9, 2, v2
	v_cndmask_b32_e32 v2, v30, v34, vcc
	v_lshlrev_b32_e32 v38, 2, v2
	ds_bpermute_b32 v2, v8, v1
	ds_bpermute_b32 v4, v8, v3
	ds_bpermute_b32 v6, v8, v5
	ds_bpermute_b32 v8, v8, v7
	s_waitcnt lgkmcnt(3)
	v_max_f32_e32 v2, v2, v2
	s_waitcnt lgkmcnt(2)
	v_max_f32_e32 v4, v4, v4
	s_waitcnt lgkmcnt(1)
	v_max_f32_e32 v6, v6, v6
	s_waitcnt lgkmcnt(0)
	v_max_f32_e32 v8, v8, v8
	v_max_f32_e32 v1, v1, v2
	v_max_f32_e32 v3, v3, v4
	v_max_f32_e32 v5, v5, v6
	v_max_f32_e32 v7, v7, v8
	ds_bpermute_b32 v2, v9, v1
	ds_bpermute_b32 v4, v9, v3
	ds_bpermute_b32 v6, v9, v5
	ds_bpermute_b32 v8, v9, v7
	s_waitcnt lgkmcnt(3)
	v_max_f32_e32 v2, v2, v2
	s_waitcnt lgkmcnt(2)
	v_max_f32_e32 v4, v4, v4
	s_waitcnt lgkmcnt(1)
	v_max_f32_e32 v6, v6, v6
	s_waitcnt lgkmcnt(0)
	v_max_f32_e32 v8, v8, v8
	v_max_f32_e32 v1, v1, v2
	v_max_f32_e32 v3, v3, v4
	v_max_f32_e32 v5, v5, v6
	v_max_f32_e32 v7, v7, v8
	ds_bpermute_b32 v2, v38, v1
	ds_bpermute_b32 v4, v38, v3
	ds_bpermute_b32 v6, v38, v5
	ds_bpermute_b32 v8, v38, v7
	s_and_saveexec_b64 s[20:21], s[6:7]
	s_cbranch_execz .LBB0_793
; __device__ __forceinline__ void colmax_item(const float* src, int ld, int k0, int c0, float* cmx  , int lane) {
;     ...
;     for (int i = 0; i < 4; ++i) { float v = mx[i]; v = fmaxf(v, __shfl_xor(v, 8)); v = fmaxf(v, __shfl_xor(v, 16)); v = fmaxf(v, __shfl_xor(v, 32)); mx[i] = v; }
;     if (q == 0) {
; #pragma unroll
;         for (int i = 0; i < 4; ++i) atomicMax((unsigned*)(cmx + 4 * c + i), __float_as_uint(mx[i] * CMS_F)); }
; template <int GRP>
; __device__ __forceinline__ void conv_item(Frame& F, int r) {
;     ...
;         else colmax_item(inptr(F, up ? IN_MU : IN_MG) + (size_t)e * D * DFE, DFE, kb * 128, n0, cmx + 2 * DFF + e * 2 * DFE + drow, F.lane); }
	s_lshl_b32 s17, s69, 6
	s_and_b32 s17, s17, 0x3fff00
	s_cmpk_gt_u32 s8, 0x57f
	s_cselect_b32 s8, 0x80, 0
	v_mul_u32_u24_e32 v9, s23, v36
	s_or_b32 s8, s17, s8
	s_and_b32 s16, s16, 0x60
	v_lshlrev_b32_e32 v38, 2, v9
	v_mov_b32_e32 v39, v11
	s_or_b32 s8, s8, s16
	v_lshl_add_u64 v[38:39], s[10:11], 0, v[38:39]
	s_lshl_b32 s8, s8, 2
	s_waitcnt lgkmcnt(3)
	v_max_f32_e32 v2, v2, v2
	v_max_f32_e32 v1, v1, v1
	v_lshl_add_u64 v[38:39], v[38:39], 0, s[8:9]
	s_waitcnt lgkmcnt(2)
	v_max_f32_e32 v4, v4, v4
	v_max_f32_e32 v3, v3, v3
	v_max_f32_e32 v1, v1, v2
	s_waitcnt lgkmcnt(1)
	v_max_f32_e32 v6, v6, v6
	v_max_f32_e32 v5, v5, v5
	v_max_f32_e32 v3, v3, v4
	v_mul_f32_e32 v1, 0x3fb33333, v1
	v_readfirstlane_b32 s16, v38
	v_readfirstlane_b32 s17, v39
	s_waitcnt lgkmcnt(0)
	v_max_f32_e32 v8, v8, v8
	v_max_f32_e32 v7, v7, v7
	v_max_f32_e32 v5, v5, v6
	v_max_f32_e32 v7, v7, v8
	global_atomic_umax v29, v1, s[16:17]
	v_mul_f32_e32 v1, 0x3fb33333, v3
	global_atomic_umax v29, v1, s[16:17] offset:4
	v_mul_f32_e32 v1, 0x3fb33333, v5
	global_atomic_umax v29, v1, s[16:17] offset:8
	v_mul_f32_e32 v1, 0x3fb33333, v7
	global_atomic_umax v29, v1, s[16:17] offset:12

; __device__ __forceinline__ void cvt_item8(const float* src, int ld, int k0, int c0, unsigned char* dst, int Kd, int drow0, unsigned char* scr, int lane) {
;     const int c = lane & 7, q = lane >> 3;
;     f32x4 v[4][4];
; #pragma unroll
;     for (int g = 0; g < 4; ++g)
; #pragma unroll
;         for (int j = 0; j < 4; ++j) v[g][j] = __builtin_nontemporal_load((const f32x4*)(src + (size_t)(k0 + 32 * g + 4 * q + j) * ld + c0 + 4 * c));
; #pragma unroll
;     for (int g = 0; g < 4; ++g)
; #pragma unroll
;         for (int i = 0; i < 4; ++i) *(unsigned*)(scr + (4 * c + i) * 132 + 32 * g + 4 * q) = pg8::pack_fp8x4(v[g][0][i] * WSC, v[g][1][i] * WSC, v[g][2][i] * WSC, v[g][3][i] * WSC);
; template <int GRP>
; __device__ __forceinline__ void conv_item(Frame& F, int r) {
;     ...
;             if (r < CI_MD) { const int e = r / (22 * 64); r %= (22 * 64); const int kb = r / 64, nb = r % 64;
;                 cvt_item8(inptr(F, IN_MD) + (size_t)e * DFE * D, D, kb * 128, nb * 32, ws + WS_MD + (size_t)e * D * DFE, DFE, nb * 32, scr, F.lane); return; }
.LBB0_794:
	s_andn2_b64 vcc, exec, s[16:17]
	s_cbranch_vccnz .LBB0_796
	s_add_i32 s8, s22, 0xfc00
	v_mov_b32_e32 v1, s43
	s_and_b32 s16, s8, 0xffff
	s_waitcnt lgkmcnt(3)
	ds_read_b64 v[2:3], v1
	s_mul_i32 s16, s16, 0xba2f
	s_lshr_b32 s17, s16, 26
	s_mul_i32 s16, s17, 0x580
	s_sub_i32 s8, s8, s16
	s_and_b32 s16, s8, 0xffff
	s_waitcnt lgkmcnt(0)
	v_readfirstlane_b32 s8, v2
	s_mul_i32 s21, s17, 0x1600000
	v_readfirstlane_b32 s20, v3
	s_add_u32 s21, s8, s21
	s_addc_u32 s23, s20, 0
	s_lshl_b32 s8, s16, 1
	s_lshl_b32 s16, s16, 5
	s_and_b32 s16, s16, 0x7e0
	s_and_b32 s8, s8, 0xf80
	s_lshl_b32 s20, s16, 2
	s_add_u32 s20, s21, s20
	v_or_b32_e32 v1, s8, v21
	s_addc_u32 s21, s23, 0
	v_lshlrev_b32_e32 v2, 2, v14
	v_mov_b32_e32 v3, v11
	v_lshl_add_u64 v[2:3], s[20:21], 0, v[2:3]
	v_lshlrev_b32_e32 v4, 13, v1
	v_mov_b32_e32 v5, v11
	v_lshl_add_u64 v[8:9], v[2:3], 0, v[4:5]
	v_add_co_u32_e32 v2, vcc, s27, v8
	s_nop 1
	v_addc_co_u32_e32 v3, vcc, 0, v9, vcc
	global_load_dwordx4 v[4:7], v[8:9], off nt
	global_load_dwordx4 v[38:41], v[2:3], off nt
	v_add_co_u32_e32 v2, vcc, s44, v8
	s_waitcnt vmcnt(0) lgkmcnt(0)
	v_mul_f32_e32 v1, 0x42800000, v4
	v_addc_co_u32_e32 v3, vcc, 0, v9, vcc
	global_load_dwordx4 v[42:45], v[2:3], off nt
	v_add_co_u32_e32 v2, vcc, s45, v8
	v_mul_f32_e32 v4, 0x42800000, v38
	s_nop 0
	v_addc_co_u32_e32 v3, vcc, 0, v9, vcc
	global_load_dwordx4 v[46:49], v[2:3], off nt
	v_add_co_u32_e32 v50, vcc, s46, v8
	v_med3_f32 v1, v1, s67, v37
	s_nop 0
	v_addc_co_u32_e32 v51, vcc, 0, v9, vcc
	v_add_co_u32_e32 v54, vcc, s47, v8
	v_med3_f32 v4, v4, s67, v37
	s_nop 0
	v_addc_co_u32_e32 v55, vcc, 0, v9, vcc
	global_load_dwordx4 v[50:53], v[50:51], off nt
	s_nop 0
	global_load_dwordx4 v[54:57], v[54:55], off nt
	v_add_co_u32_e32 v58, vcc, s49, v8
	v_mov_b32_e32 v38, v11
	s_nop 0
	v_addc_co_u32_e32 v59, vcc, 0, v9, vcc
	v_add_co_u32_e32 v62, vcc, s52, v8
	v_mov_b64_e32 v[2:3], s[12:13]
	s_nop 0
	v_addc_co_u32_e32 v63, vcc, 0, v9, vcc
	global_load_dwordx4 v[58:61], v[58:59], off nt
	s_nop 0
	global_load_dwordx4 v[62:65], v[62:63], off nt
	v_add_co_u32_e32 v66, vcc, s53, v8
	v_mad_u64_u32 v[2:3], s[20:21], s17, v35, v[2:3]
	s_nop 0
	v_addc_co_u32_e32 v67, vcc, 0, v9, vcc
	v_add_co_u32_e32 v70, vcc, s54, v8
	v_lshl_add_u64 v[2:3], v[2:3], 0, s[8:9]
	s_nop 0
	v_addc_co_u32_e32 v71, vcc, 0, v9, vcc
	global_load_dwordx4 v[66:69], v[66:67], off nt
	s_nop 0
	global_load_dwordx4 v[70:73], v[70:71], off nt
	v_add_co_u32_e32 v74, vcc, s55, v8
	s_nop 1
	v_addc_co_u32_e32 v75, vcc, 0, v9, vcc
	v_add_co_u32_e32 v78, vcc, s56, v8
	s_nop 1
	v_addc_co_u32_e32 v79, vcc, 0, v9, vcc
	global_load_dwordx4 v[74:77], v[74:75], off nt
	s_nop 0
	global_load_dwordx4 v[78:81], v[78:79], off nt
	v_add_co_u32_e32 v82, vcc, s57, v8
	s_nop 1
	v_addc_co_u32_e32 v83, vcc, 0, v9, vcc
	v_add_co_u32_e32 v86, vcc, s62, v8
	s_nop 1
	v_addc_co_u32_e32 v87, vcc, 0, v9, vcc
	global_load_dwordx4 v[82:85], v[82:83], off nt
	s_nop 0
	global_load_dwordx4 v[86:89], v[86:87], off nt
	v_add_co_u32_e32 v90, vcc, s63, v8
	s_nop 1
	v_addc_co_u32_e32 v91, vcc, 0, v9, vcc
	v_add_co_u32_e32 v8, vcc, s66, v8
	s_nop 1
	v_addc_co_u32_e32 v9, vcc, 0, v9, vcc
	global_load_dwordx4 v[90:93], v[90:91], off nt
	s_nop 0
	global_load_dwordx4 v[94:97], v[8:9], off nt
	v_mov_b32_e32 v9, v11
	v_cvt_pk_fp8_f32 v9, v1, v4
	s_waitcnt vmcnt(0) lgkmcnt(0)
	v_mul_f32_e32 v8, 0x42800000, v42
	v_med3_f32 v4, v8, s67, v37
	v_mul_f32_e32 v8, 0x42800000, v43
	v_mov_b32_e32 v42, v11
	v_mul_f32_e32 v1, 0x42800000, v46
	v_med3_f32 v1, v1, s67, v37
	v_cvt_pk_fp8_f32 v9, v4, v1 op_sel:[0,0,1]
	v_mul_f32_e32 v4, 0x42800000, v5
	v_mul_f32_e32 v5, 0x42800000, v39
	v_med3_f32 v4, v4, s67, v37
	v_med3_f32 v5, v5, s67, v37
	v_cvt_pk_fp8_f32 v38, v4, v5
	v_mul_f32_e32 v4, 0x42800000, v47
	v_med3_f32 v5, v8, s67, v37
	v_med3_f32 v4, v4, s67, v37
	v_cvt_pk_fp8_f32 v38, v5, v4 op_sel:[0,0,1]
	v_mul_f32_e32 v4, 0x42800000, v6
	v_mul_f32_e32 v5, 0x42800000, v40
	v_med3_f32 v4, v4, s67, v37
	v_med3_f32 v5, v5, s67, v37
	v_mov_b32_e32 v8, v11
	v_cvt_pk_fp8_f32 v8, v4, v5
	v_mul_f32_e32 v6, 0x42800000, v44
	v_mul_f32_e32 v4, 0x42800000, v48
	v_med3_f32 v5, v6, s67, v37
	v_med3_f32 v4, v4, s67, v37
	v_cvt_pk_fp8_f32 v8, v5, v4 op_sel:[0,0,1]
	v_mul_f32_e32 v4, 0x42800000, v7
	v_mul_f32_e32 v5, 0x42800000, v41
	v_med3_f32 v4, v4, s67, v37
	v_med3_f32 v5, v5, s67, v37
	v_mov_b32_e32 v7, v11
	v_cvt_pk_fp8_f32 v7, v4, v5
	v_mul_f32_e32 v6, 0x42800000, v45
	v_mul_f32_e32 v4, 0x42800000, v49
	v_med3_f32 v5, v6, s67, v37
	v_med3_f32 v4, v4, s67, v37
	v_cvt_pk_fp8_f32 v7, v5, v4 op_sel:[0,0,1]
	v_mul_f32_e32 v4, 0x42800000, v50
	v_mul_f32_e32 v5, 0x42800000, v54
	v_med3_f32 v4, v4, s67, v37
	v_med3_f32 v5, v5, s67, v37
	v_mov_b32_e32 v39, v11
	v_cvt_pk_fp8_f32 v39, v4, v5
	v_mul_f32_e32 v6, 0x42800000, v58
	v_mul_f32_e32 v4, 0x42800000, v62
	v_med3_f32 v5, v6, s67, v37
	v_med3_f32 v4, v4, s67, v37
	v_cvt_pk_fp8_f32 v39, v5, v4 op_sel:[0,0,1]
	v_mul_f32_e32 v4, 0x42800000, v51
	v_mul_f32_e32 v5, 0x42800000, v55
	v_med3_f32 v4, v4, s67, v37
	v_med3_f32 v5, v5, s67, v37
	v_mov_b32_e32 v40, v11
	v_cvt_pk_fp8_f32 v40, v4, v5
	v_mul_f32_e32 v6, 0x42800000, v59
	v_mul_f32_e32 v4, 0x42800000, v63
	v_med3_f32 v5, v6, s67, v37
	v_med3_f32 v4, v4, s67, v37
	v_cvt_pk_fp8_f32 v40, v5, v4 op_sel:[0,0,1]
; __device__ __forceinline__ void cvt_item8(const float* src, int ld, int k0, int c0, unsigned char* dst, int Kd, int drow0, unsigned char* scr, int lane) {
;     ...
;     for (int g = 0; g < 4; ++g)
; #pragma unroll
;         for (int i = 0; i < 4; ++i) *(unsigned*)(scr + (4 * c + i) * 132 + 32 * g + 4 * q) = pg8::pack_fp8x4(v[g][0][i] * WSC, v[g][1][i] * WSC, v[g][2][i] * WSC, v[g][3][i] * WSC);
;     asm volatile("s_waitcnt lgkmcnt(0)" ::: "memory");
; #pragma unroll
;     for (int r = 0; r < 4; ++r) { const int n = 8 * r + (lane >> 3), ch = lane & 7; const unsigned char* p = scr + n * 132 + ch * 16;
;         u32x4 o; o.x = *(const unsigned*)(p); o.y = *(const unsigned*)(p + 4); o.z = *(const unsigned*)(p + 8); o.w = *(const unsigned*)(p + 12);
;         *(u32x4*)(dst + (size_t)(drow0 + n) * Kd + k0 + 16 * ch) = o; }
;     asm volatile("s_waitcnt lgkmcnt(0)" ::: "memory");
	v_mul_f32_e32 v4, 0x42800000, v52
	v_mul_f32_e32 v5, 0x42800000, v56
	v_med3_f32 v4, v4, s67, v37
	v_med3_f32 v5, v5, s67, v37
	v_mov_b32_e32 v41, v11
	v_cvt_pk_fp8_f32 v41, v4, v5
	v_mul_f32_e32 v6, 0x42800000, v60
	v_mul_f32_e32 v4, 0x42800000, v64
	v_med3_f32 v5, v6, s67, v37
	v_med3_f32 v4, v4, s67, v37
	v_cvt_pk_fp8_f32 v41, v5, v4 op_sel:[0,0,1]
	v_mul_f32_e32 v4, 0x42800000, v53
	v_mul_f32_e32 v5, 0x42800000, v57
	v_med3_f32 v4, v4, s67, v37
	v_med3_f32 v5, v5, s67, v37
	v_cvt_pk_fp8_f32 v42, v4, v5
	v_mul_f32_e32 v6, 0x42800000, v61
	v_mul_f32_e32 v4, 0x42800000, v65
	v_med3_f32 v5, v6, s67, v37
	v_med3_f32 v4, v4, s67, v37
	v_add_u32_e32 v1, v22, v23
	v_cvt_pk_fp8_f32 v42, v5, v4 op_sel:[0,0,1]
	v_mul_f32_e32 v4, 0x42800000, v66
	v_mul_f32_e32 v5, 0x42800000, v70
	ds_write2_b32 v1, v9, v39 offset1:8
	ds_write2_b32 v1, v38, v40 offset0:33 offset1:41
	ds_write2_b32 v1, v8, v41 offset0:66 offset1:74
	ds_write2_b32 v1, v7, v42 offset0:99 offset1:107
	v_med3_f32 v4, v4, s67, v37
	v_med3_f32 v5, v5, s67, v37
	v_mov_b32_e32 v7, v11
	v_cvt_pk_fp8_f32 v7, v4, v5
	v_mul_f32_e32 v6, 0x42800000, v74
	v_mul_f32_e32 v4, 0x42800000, v78
	v_med3_f32 v5, v6, s67, v37
	v_med3_f32 v4, v4, s67, v37
	v_cvt_pk_fp8_f32 v7, v5, v4 op_sel:[0,0,1]
	v_mul_f32_e32 v4, 0x42800000, v67
	v_mul_f32_e32 v5, 0x42800000, v71
	v_med3_f32 v4, v4, s67, v37
	v_med3_f32 v5, v5, s67, v37
	v_mov_b32_e32 v8, v11
	v_cvt_pk_fp8_f32 v8, v4, v5
	v_mul_f32_e32 v6, 0x42800000, v75
	v_mul_f32_e32 v4, 0x42800000, v79
	v_med3_f32 v5, v6, s67, v37
	v_med3_f32 v4, v4, s67, v37
	v_cvt_pk_fp8_f32 v8, v5, v4 op_sel:[0,0,1]
	v_mul_f32_e32 v4, 0x42800000, v68
	v_mul_f32_e32 v5, 0x42800000, v72
	v_med3_f32 v4, v4, s67, v37
	v_med3_f32 v5, v5, s67, v37
	v_mov_b32_e32 v9, v11
	v_cvt_pk_fp8_f32 v9, v4, v5
	v_mul_f32_e32 v6, 0x42800000, v76
	v_mul_f32_e32 v4, 0x42800000, v80
	v_med3_f32 v5, v6, s67, v37
	v_med3_f32 v4, v4, s67, v37
	v_cvt_pk_fp8_f32 v9, v5, v4 op_sel:[0,0,1]
	v_mul_f32_e32 v4, 0x42800000, v69
	v_mul_f32_e32 v5, 0x42800000, v73
	v_med3_f32 v4, v4, s67, v37
	v_med3_f32 v5, v5, s67, v37
	v_mov_b32_e32 v38, v11
	v_cvt_pk_fp8_f32 v38, v4, v5
	v_mul_f32_e32 v6, 0x42800000, v77
	v_mul_f32_e32 v4, 0x42800000, v81
	v_med3_f32 v5, v6, s67, v37
	v_med3_f32 v4, v4, s67, v37
	v_cvt_pk_fp8_f32 v38, v5, v4 op_sel:[0,0,1]
	v_mul_f32_e32 v4, 0x42800000, v82
	v_mul_f32_e32 v5, 0x42800000, v86
	v_med3_f32 v4, v4, s67, v37
	v_med3_f32 v5, v5, s67, v37
	v_mov_b32_e32 v39, v11
	v_cvt_pk_fp8_f32 v39, v4, v5
	v_mul_f32_e32 v6, 0x42800000, v90
	v_mul_f32_e32 v4, 0x42800000, v94
	v_med3_f32 v5, v6, s67, v37
	v_med3_f32 v4, v4, s67, v37
	v_cvt_pk_fp8_f32 v39, v5, v4 op_sel:[0,0,1]
	v_mul_f32_e32 v4, 0x42800000, v83
	v_mul_f32_e32 v5, 0x42800000, v87
	v_med3_f32 v4, v4, s67, v37
	v_med3_f32 v5, v5, s67, v37
	v_mov_b32_e32 v40, v11
	v_cvt_pk_fp8_f32 v40, v4, v5
	v_mul_f32_e32 v6, 0x42800000, v91
	v_mul_f32_e32 v4, 0x42800000, v95
	v_med3_f32 v5, v6, s67, v37
	v_med3_f32 v4, v4, s67, v37
	v_cvt_pk_fp8_f32 v40, v5, v4 op_sel:[0,0,1]
	v_mul_f32_e32 v4, 0x42800000, v84
	v_mul_f32_e32 v5, 0x42800000, v88
	v_med3_f32 v4, v4, s67, v37
	v_med3_f32 v5, v5, s67, v37
	v_mov_b32_e32 v41, v11
	v_cvt_pk_fp8_f32 v41, v4, v5
	v_mul_f32_e32 v6, 0x42800000, v92
	v_mul_f32_e32 v4, 0x42800000, v96
	v_med3_f32 v5, v6, s67, v37
	v_med3_f32 v4, v4, s67, v37
	v_cvt_pk_fp8_f32 v41, v5, v4 op_sel:[0,0,1]
	v_mul_f32_e32 v4, 0x42800000, v85
	v_mul_f32_e32 v5, 0x42800000, v89
	v_med3_f32 v4, v4, s67, v37
	v_med3_f32 v5, v5, s67, v37
	v_mov_b32_e32 v42, v11
	v_cvt_pk_fp8_f32 v42, v4, v5
	v_mul_f32_e32 v6, 0x42800000, v93
	v_mul_f32_e32 v4, 0x42800000, v97
	v_med3_f32 v5, v6, s67, v37
	v_med3_f32 v4, v4, s67, v37
	v_cvt_pk_fp8_f32 v42, v5, v4 op_sel:[0,0,1]
	ds_write2_b32 v1, v7, v39 offset0:16 offset1:24
	ds_write2_b32 v1, v8, v40 offset0:49 offset1:57
	ds_write2_b32 v1, v9, v41 offset0:82 offset1:90
	ds_write2_b32 v1, v38, v42 offset0:115 offset1:123
	s_waitcnt lgkmcnt(0)
	v_add_u32_e32 v1, v24, v25
	v_lshl_add_u64 v[38:39], v[2:3], 0, v[16:17]
	ds_read2_b32 v[2:3], v1 offset1:1
	ds_read2_b32 v[4:5], v1 offset0:2 offset1:3
	v_or_b32_e32 v6, s16, v20
	v_mul_u32_u24_e32 v6, 0xb00, v6
	v_mov_b32_e32 v7, v11
	v_lshl_add_u64 v[40:41], v[38:39], 0, v[6:7]
	v_add_u32_e32 v6, 0x420, v1
	v_add_u32_e32 v8, 0x428, v1
	ds_read2_b32 v[6:7], v6 offset1:1
	ds_read2_b32 v[8:9], v8 offset1:1
	s_waitcnt lgkmcnt(2)
	global_store_dwordx4 v[40:41], v[2:5], off
	s_nop 1
	v_or_b32_e32 v2, s16, v26
	v_mul_u32_u24_e32 v2, 0xb00, v2
	v_mov_b32_e32 v3, v11
	v_lshl_add_u64 v[2:3], v[38:39], 0, v[2:3]
	s_waitcnt lgkmcnt(0)
	global_store_dwordx4 v[2:3], v[6:9], off
	v_add_u32_e32 v2, 0x840, v1
	v_add_u32_e32 v4, 0x848, v1
	v_or_b32_e32 v6, s16, v27
	ds_read2_b32 v[2:3], v2 offset1:1
	ds_read2_b32 v[4:5], v4 offset1:1
	v_mul_u32_u24_e32 v6, 0xb00, v6
	v_mov_b32_e32 v7, v11
	v_lshl_add_u64 v[40:41], v[38:39], 0, v[6:7]
	v_add_u32_e32 v6, 0xc60, v1
	v_add_u32_e32 v1, 0xc68, v1
	ds_read2_b32 v[6:7], v6 offset1:1
	ds_read2_b32 v[8:9], v1 offset1:1
	v_or_b32_e32 v1, s16, v28
	s_waitcnt lgkmcnt(2)
	global_store_dwordx4 v[40:41], v[2:5], off
	s_nop 1
	v_mul_u32_u24_e32 v2, 0xb00, v1
	v_mov_b32_e32 v3, v11
	v_lshl_add_u64 v[2:3], v[38:39], 0, v[2:3]
	s_waitcnt lgkmcnt(0)
	global_store_dwordx4 v[2:3], v[6:9], off
	s_waitcnt lgkmcnt(0)

; __device__ __forceinline__ void cvt_item8(const float* src, int ld, int k0, int c0, unsigned char* dst, int Kd, int drow0, unsigned char* scr, int lane) {
;     const int c = lane & 7, q = lane >> 3;
;     f32x4 v[4][4];
; #pragma unroll
;     for (int g = 0; g < 4; ++g)
; #pragma unroll
;         for (int j = 0; j < 4; ++j) v[g][j] = __builtin_nontemporal_load((const f32x4*)(src + (size_t)(k0 + 32 * g + 4 * q + j) * ld + c0 + 4 * c));
; #pragma unroll
;     for (int g = 0; g < 4; ++g)
; #pragma unroll
;         for (int i = 0; i < 4; ++i) *(unsigned*)(scr + (4 * c + i) * 132 + 32 * g + 4 * q) = pg8::pack_fp8x4(v[g][0][i] * WSC, v[g][1][i] * WSC, v[g][2][i] * WSC, v[g][3][i] * WSC);
; template <int GRP>
; __device__ __forceinline__ void conv_item(Frame& F, int r) {
;     ...
;         if (r < CI_WO) { const int kb = r / 64, nb = r % 64;
;             cvt_item8(inptr(F, IN_WOUT) + (size_t)l * D * D, D, kb * 128, nb * 32, ws + WS_WOUT + (size_t)l * D * D, D, nb * 32, scr, F.lane); return; }
.LBB0_797:
	s_andn2_b64 vcc, exec, s[16:17]
	s_cbranch_vccnz .LBB0_781
	s_ashr_i32 s8, s22, 31
	v_mov_b32_e32 v1, s68
	s_lshr_b32 s8, s8, 26
	s_waitcnt lgkmcnt(3)
	ds_read_b64 v[2:3], v1
	s_add_i32 s8, s22, s8
	s_and_b32 s16, s8, 0x7ffffc0
	s_sub_i32 s16, s22, s16
	s_lshl_b32 s16, s16, 5
	s_lshl_b32 s8, s8, 1
	s_ashr_i32 s17, s16, 31
	s_waitcnt lgkmcnt(0)
	v_readfirstlane_b32 s21, v2
	s_and_b32 s20, s8, 0xffffff80
	s_lshl_b64 s[22:23], s[16:17], 2
	v_readfirstlane_b32 s69, v3
	s_add_u32 s22, s21, s22
	v_or_b32_e32 v86, s20, v21
	s_addc_u32 s23, s69, s23
	v_lshlrev_b32_e32 v2, 2, v14
	v_mov_b32_e32 v3, v11
	v_lshl_add_u64 v[2:3], s[22:23], 0, v[2:3]
	v_ashrrev_i32_e32 v87, 31, v86
	v_or_b32_e32 v4, 1, v86
	v_lshl_add_u64 v[88:89], v[2:3], 0, s[14:15]
	v_lshlrev_b64 v[2:3], 13, v[86:87]
	v_ashrrev_i32_e32 v5, 31, v4
	v_lshl_add_u64 v[2:3], v[88:89], 0, v[2:3]
	v_lshlrev_b64 v[4:5], 13, v[4:5]
	v_lshl_add_u64 v[4:5], v[88:89], 0, v[4:5]
	global_load_dwordx4 v[38:41], v[2:3], off nt
	global_load_dwordx4 v[42:45], v[4:5], off nt
	v_or_b32_e32 v2, 2, v86
	v_ashrrev_i32_e32 v3, 31, v2
	v_lshlrev_b64 v[2:3], 13, v[2:3]
	v_lshl_add_u64 v[2:3], v[88:89], 0, v[2:3]
	s_waitcnt vmcnt(0)
	global_load_dwordx4 v[46:49], v[2:3], off nt
	v_or_b32_e32 v2, 3, v86
	v_ashrrev_i32_e32 v3, 31, v2
	v_lshlrev_b64 v[2:3], 13, v[2:3]
	v_lshl_add_u64 v[2:3], v[88:89], 0, v[2:3]
	global_load_dwordx4 v[50:53], v[2:3], off nt
	v_or_b32_e32 v2, 32, v86
	v_ashrrev_i32_e32 v3, 31, v2
	v_or_b32_e32 v4, 33, v86
	v_lshlrev_b64 v[2:3], 13, v[2:3]
	v_ashrrev_i32_e32 v5, 31, v4
	v_lshl_add_u64 v[2:3], v[88:89], 0, v[2:3]
	v_lshlrev_b64 v[4:5], 13, v[4:5]
	v_lshl_add_u64 v[4:5], v[88:89], 0, v[4:5]
	global_load_dwordx4 v[54:57], v[2:3], off nt
	global_load_dwordx4 v[58:61], v[4:5], off nt
	v_or_b32_e32 v2, 34, v86
	v_ashrrev_i32_e32 v3, 31, v2
	v_or_b32_e32 v4, 35, v86
	v_lshlrev_b64 v[2:3], 13, v[2:3]
	v_ashrrev_i32_e32 v5, 31, v4
	v_lshl_add_u64 v[2:3], v[88:89], 0, v[2:3]
	v_lshlrev_b64 v[4:5], 13, v[4:5]
	v_lshl_add_u64 v[4:5], v[88:89], 0, v[4:5]
	global_load_dwordx4 v[62:65], v[2:3], off nt
	global_load_dwordx4 v[66:69], v[4:5], off nt
	v_or_b32_e32 v2, 64, v86
	v_ashrrev_i32_e32 v3, 31, v2
	v_or_b32_e32 v4, 0x41, v86
	v_lshlrev_b64 v[2:3], 13, v[2:3]
	v_ashrrev_i32_e32 v5, 31, v4
	v_lshl_add_u64 v[2:3], v[88:89], 0, v[2:3]
	v_lshlrev_b64 v[4:5], 13, v[4:5]
	v_lshl_add_u64 v[4:5], v[88:89], 0, v[4:5]
	global_load_dwordx4 v[70:73], v[2:3], off nt
	global_load_dwordx4 v[74:77], v[4:5], off nt
	v_or_b32_e32 v2, 0x42, v86
	v_ashrrev_i32_e32 v3, 31, v2
	v_or_b32_e32 v4, 0x43, v86
	v_lshlrev_b64 v[2:3], 13, v[2:3]
	v_ashrrev_i32_e32 v5, 31, v4
	v_lshl_add_u64 v[2:3], v[88:89], 0, v[2:3]
	v_lshlrev_b64 v[4:5], 13, v[4:5]
	v_lshl_add_u64 v[4:5], v[88:89], 0, v[4:5]
	global_load_dwordx4 v[78:81], v[2:3], off nt
	global_load_dwordx4 v[82:85], v[4:5], off nt
	v_or_b32_e32 v2, 0x60, v86
	v_or_b32_e32 v4, 0x61, v86
	v_ashrrev_i32_e32 v3, 31, v2
	v_ashrrev_i32_e32 v5, 31, v4
	v_lshlrev_b64 v[2:3], 13, v[2:3]
	v_lshlrev_b64 v[4:5], 13, v[4:5]
	v_lshl_add_u64 v[2:3], v[88:89], 0, v[2:3]
	v_lshl_add_u64 v[6:7], v[88:89], 0, v[4:5]
	global_load_dwordx4 v[2:5], v[2:3], off nt
	s_nop 0
	global_load_dwordx4 v[6:9], v[6:7], off nt
	v_or_b32_e32 v90, 0x62, v86
	v_or_b32_e32 v86, 0x63, v86
	v_ashrrev_i32_e32 v91, 31, v90
	v_ashrrev_i32_e32 v87, 31, v86
	v_lshlrev_b64 v[90:91], 13, v[90:91]
	v_lshlrev_b64 v[86:87], 13, v[86:87]
	v_lshl_add_u64 v[90:91], v[88:89], 0, v[90:91]
	v_lshl_add_u64 v[92:93], v[88:89], 0, v[86:87]
	global_load_dwordx4 v[86:89], v[90:91], off nt
	s_nop 0
	global_load_dwordx4 v[90:93], v[92:93], off nt
	s_ashr_i32 s21, s20, 31
	s_waitcnt lgkmcnt(0)
	v_mul_f32_e32 v1, 0x42800000, v38
	v_mul_f32_e32 v38, 0x42800000, v42
	v_med3_f32 v1, v1, s67, v37
	v_med3_f32 v38, v38, s67, v37
	s_waitcnt vmcnt(0)
	v_mul_f32_e32 v42, 0x42800000, v46
	v_mov_b32_e32 v46, v11
	v_cvt_pk_fp8_f32 v46, v1, v38
	v_med3_f32 v38, v42, s67, v37
	v_mul_f32_e32 v42, 0x42800000, v47
	v_mul_f32_e32 v1, 0x42800000, v50
	v_med3_f32 v1, v1, s67, v37
	v_cvt_pk_fp8_f32 v46, v38, v1 op_sel:[0,0,1]
	v_mul_f32_e32 v38, 0x42800000, v39
	v_mul_f32_e32 v39, 0x42800000, v43
	v_med3_f32 v38, v38, s67, v37
	v_med3_f32 v39, v39, s67, v37
	v_mov_b32_e32 v43, v11
	v_cvt_pk_fp8_f32 v43, v38, v39
	v_mul_f32_e32 v38, 0x42800000, v51
	v_med3_f32 v39, v42, s67, v37
	v_med3_f32 v38, v38, s67, v37
	v_cvt_pk_fp8_f32 v43, v39, v38 op_sel:[0,0,1]
	v_mul_f32_e32 v38, 0x42800000, v40
	v_mul_f32_e32 v39, 0x42800000, v44
	v_med3_f32 v38, v38, s67, v37
	v_med3_f32 v39, v39, s67, v37
	v_mov_b32_e32 v42, v11
	v_cvt_pk_fp8_f32 v42, v38, v39
	v_mul_f32_e32 v40, 0x42800000, v48
	v_mul_f32_e32 v38, 0x42800000, v52
	v_med3_f32 v39, v40, s67, v37
	v_med3_f32 v38, v38, s67, v37
	v_cvt_pk_fp8_f32 v42, v39, v38 op_sel:[0,0,1]
	v_mul_f32_e32 v38, 0x42800000, v41
	v_mul_f32_e32 v39, 0x42800000, v45
	v_med3_f32 v38, v38, s67, v37
	v_med3_f32 v39, v39, s67, v37
	v_mov_b32_e32 v41, v11
	v_cvt_pk_fp8_f32 v41, v38, v39
	v_mul_f32_e32 v40, 0x42800000, v49
	v_mul_f32_e32 v38, 0x42800000, v53
	v_med3_f32 v39, v40, s67, v37
	v_med3_f32 v38, v38, s67, v37
	v_cvt_pk_fp8_f32 v41, v39, v38 op_sel:[0,0,1]
	v_mul_f32_e32 v38, 0x42800000, v54
	v_mul_f32_e32 v39, 0x42800000, v58
	v_med3_f32 v38, v38, s67, v37
	v_med3_f32 v39, v39, s67, v37
	v_mov_b32_e32 v44, v11
	v_cvt_pk_fp8_f32 v44, v38, v39
	v_mul_f32_e32 v40, 0x42800000, v62
	v_mul_f32_e32 v38, 0x42800000, v66
	v_med3_f32 v39, v40, s67, v37
	v_med3_f32 v38, v38, s67, v37
	v_cvt_pk_fp8_f32 v44, v39, v38 op_sel:[0,0,1]
	v_mul_f32_e32 v38, 0x42800000, v55
	v_mul_f32_e32 v39, 0x42800000, v59
	v_med3_f32 v38, v38, s67, v37
; __device__ __forceinline__ void cvt_item8(const float* src, int ld, int k0, int c0, unsigned char* dst, int Kd, int drow0, unsigned char* scr, int lane) {
;     ...
;     for (int g = 0; g < 4; ++g)
; #pragma unroll
;         for (int i = 0; i < 4; ++i) *(unsigned*)(scr + (4 * c + i) * 132 + 32 * g + 4 * q) = pg8::pack_fp8x4(v[g][0][i] * WSC, v[g][1][i] * WSC, v[g][2][i] * WSC, v[g][3][i] * WSC);
;     asm volatile("s_waitcnt lgkmcnt(0)" ::: "memory");
; #pragma unroll
;     for (int r = 0; r < 4; ++r) { const int n = 8 * r + (lane >> 3), ch = lane & 7; const unsigned char* p = scr + n * 132 + ch * 16;
;         u32x4 o; o.x = *(const unsigned*)(p); o.y = *(const unsigned*)(p + 4); o.z = *(const unsigned*)(p + 8); o.w = *(const unsigned*)(p + 12);
;         *(u32x4*)(dst + (size_t)(drow0 + n) * Kd + k0 + 16 * ch) = o; }
;     asm volatile("s_waitcnt lgkmcnt(0)" ::: "memory");
	v_med3_f32 v39, v39, s67, v37
	v_mov_b32_e32 v45, v11
	v_cvt_pk_fp8_f32 v45, v38, v39
	v_mul_f32_e32 v40, 0x42800000, v63
	v_mul_f32_e32 v38, 0x42800000, v67
	v_med3_f32 v39, v40, s67, v37
	v_med3_f32 v38, v38, s67, v37
	v_cvt_pk_fp8_f32 v45, v39, v38 op_sel:[0,0,1]
	v_mul_f32_e32 v38, 0x42800000, v56
	v_mul_f32_e32 v39, 0x42800000, v60
	v_med3_f32 v38, v38, s67, v37
	v_med3_f32 v39, v39, s67, v37
	v_mov_b32_e32 v47, v11
	v_cvt_pk_fp8_f32 v47, v38, v39
	v_mul_f32_e32 v40, 0x42800000, v64
	v_mul_f32_e32 v38, 0x42800000, v68
	v_med3_f32 v39, v40, s67, v37
	v_med3_f32 v38, v38, s67, v37
	v_cvt_pk_fp8_f32 v47, v39, v38 op_sel:[0,0,1]
	v_mul_f32_e32 v38, 0x42800000, v57
	v_mul_f32_e32 v39, 0x42800000, v61
	v_med3_f32 v38, v38, s67, v37
	v_med3_f32 v39, v39, s67, v37
	v_mov_b32_e32 v48, v11
	v_cvt_pk_fp8_f32 v48, v38, v39
	v_mul_f32_e32 v40, 0x42800000, v65
	v_mul_f32_e32 v38, 0x42800000, v69
	v_med3_f32 v39, v40, s67, v37
	v_med3_f32 v38, v38, s67, v37
	v_add_u32_e32 v1, v22, v23
	v_cvt_pk_fp8_f32 v48, v39, v38 op_sel:[0,0,1]
	v_mul_f32_e32 v38, 0x42800000, v70
	v_mul_f32_e32 v39, 0x42800000, v74
	ds_write2_b32 v1, v46, v44 offset1:8
	ds_write2_b32 v1, v43, v45 offset0:33 offset1:41
	ds_write2_b32 v1, v42, v47 offset0:66 offset1:74
	ds_write2_b32 v1, v41, v48 offset0:99 offset1:107
	v_med3_f32 v38, v38, s67, v37
	v_med3_f32 v39, v39, s67, v37
	v_mov_b32_e32 v41, v11
	v_cvt_pk_fp8_f32 v41, v38, v39
	v_mul_f32_e32 v40, 0x42800000, v78
	v_mul_f32_e32 v38, 0x42800000, v82
	v_med3_f32 v39, v40, s67, v37
	v_med3_f32 v38, v38, s67, v37
	v_cvt_pk_fp8_f32 v41, v39, v38 op_sel:[0,0,1]
	v_mul_f32_e32 v38, 0x42800000, v71
	v_mul_f32_e32 v39, 0x42800000, v75
	v_med3_f32 v38, v38, s67, v37
	v_med3_f32 v39, v39, s67, v37
	v_mov_b32_e32 v42, v11
	v_cvt_pk_fp8_f32 v42, v38, v39
	v_mul_f32_e32 v40, 0x42800000, v79
	v_mul_f32_e32 v38, 0x42800000, v83
	v_med3_f32 v39, v40, s67, v37
	v_med3_f32 v38, v38, s67, v37
	v_cvt_pk_fp8_f32 v42, v39, v38 op_sel:[0,0,1]
	v_mul_f32_e32 v38, 0x42800000, v72
	v_mul_f32_e32 v39, 0x42800000, v76
	v_med3_f32 v38, v38, s67, v37
	v_med3_f32 v39, v39, s67, v37
	v_mov_b32_e32 v43, v11
	v_cvt_pk_fp8_f32 v43, v38, v39
	v_mul_f32_e32 v40, 0x42800000, v80
	v_mul_f32_e32 v38, 0x42800000, v84
	v_med3_f32 v39, v40, s67, v37
	v_med3_f32 v38, v38, s67, v37
	v_cvt_pk_fp8_f32 v43, v39, v38 op_sel:[0,0,1]
	v_mul_f32_e32 v38, 0x42800000, v73
	v_mul_f32_e32 v39, 0x42800000, v77
	v_med3_f32 v38, v38, s67, v37
	v_med3_f32 v39, v39, s67, v37
	v_mov_b32_e32 v44, v11
	v_cvt_pk_fp8_f32 v44, v38, v39
	v_mul_f32_e32 v40, 0x42800000, v81
	v_mul_f32_e32 v38, 0x42800000, v85
	v_med3_f32 v39, v40, s67, v37
	v_med3_f32 v38, v38, s67, v37
	v_mul_f32_e32 v2, 0x42800000, v2
	v_mul_f32_e32 v6, 0x42800000, v6
	v_cvt_pk_fp8_f32 v44, v39, v38 op_sel:[0,0,1]
	v_med3_f32 v2, v2, s67, v37
	v_med3_f32 v6, v6, s67, v37
	v_mov_b32_e32 v39, v11
	v_cvt_pk_fp8_f32 v39, v2, v6
	v_mul_f32_e32 v38, 0x42800000, v86
	v_mul_f32_e32 v2, 0x42800000, v90
	v_med3_f32 v6, v38, s67, v37
	v_med3_f32 v2, v2, s67, v37
	v_cvt_pk_fp8_f32 v39, v6, v2 op_sel:[0,0,1]
	v_mul_f32_e32 v2, 0x42800000, v3
	v_mul_f32_e32 v3, 0x42800000, v7
	v_med3_f32 v2, v2, s67, v37
	v_med3_f32 v3, v3, s67, v37
	v_mov_b32_e32 v7, v11
	v_cvt_pk_fp8_f32 v7, v2, v3
	v_mul_f32_e32 v6, 0x42800000, v87
	v_mul_f32_e32 v2, 0x42800000, v91
	v_med3_f32 v3, v6, s67, v37
	v_med3_f32 v2, v2, s67, v37
	v_cvt_pk_fp8_f32 v7, v3, v2 op_sel:[0,0,1]
	v_mul_f32_e32 v2, 0x42800000, v4
	v_mul_f32_e32 v3, 0x42800000, v8
	v_med3_f32 v2, v2, s67, v37
	v_med3_f32 v3, v3, s67, v37
	v_mov_b32_e32 v6, v11
	v_cvt_pk_fp8_f32 v6, v2, v3
	v_mul_f32_e32 v4, 0x42800000, v88
	v_mul_f32_e32 v2, 0x42800000, v92
	v_med3_f32 v3, v4, s67, v37
	v_med3_f32 v2, v2, s67, v37
	v_cvt_pk_fp8_f32 v6, v3, v2 op_sel:[0,0,1]
	v_mul_f32_e32 v2, 0x42800000, v5
	v_mul_f32_e32 v3, 0x42800000, v9
	v_med3_f32 v2, v2, s67, v37
	v_med3_f32 v3, v3, s67, v37
	v_mov_b32_e32 v5, v11
	v_cvt_pk_fp8_f32 v5, v2, v3
	v_mul_f32_e32 v4, 0x42800000, v89
	v_mul_f32_e32 v2, 0x42800000, v93
	v_med3_f32 v3, v4, s67, v37
	v_med3_f32 v2, v2, s67, v37
	v_cvt_pk_fp8_f32 v5, v3, v2 op_sel:[0,0,1]
	ds_write2_b32 v1, v41, v39 offset0:16 offset1:24
	ds_write2_b32 v1, v42, v7 offset0:49 offset1:57
	ds_write2_b32 v1, v43, v6 offset0:82 offset1:90
	ds_write2_b32 v1, v44, v5 offset0:115 offset1:123
	s_waitcnt lgkmcnt(0)
	v_add_u32_e32 v1, v24, v25
	ds_read2_b32 v[2:3], v1 offset1:1
	ds_read2_b32 v[4:5], v1 offset0:2 offset1:3
	v_or_b32_e32 v6, s16, v20
	v_ashrrev_i32_e32 v7, 31, v6
	v_lshl_add_u64 v[38:39], v[18:19], 0, s[20:21]
	v_lshlrev_b64 v[6:7], 11, v[6:7]
	v_lshl_add_u64 v[40:41], v[38:39], 0, v[6:7]
	v_add_u32_e32 v6, 0x420, v1
	v_add_u32_e32 v8, 0x428, v1
	ds_read2_b32 v[6:7], v6 offset1:1
	ds_read2_b32 v[8:9], v8 offset1:1
	s_waitcnt lgkmcnt(2)
	global_store_dwordx4 v[40:41], v[2:5], off
	s_nop 1
	v_or_b32_e32 v2, s16, v26
	v_ashrrev_i32_e32 v3, 31, v2
	v_lshlrev_b64 v[2:3], 11, v[2:3]
	v_lshl_add_u64 v[2:3], v[38:39], 0, v[2:3]
	s_waitcnt lgkmcnt(0)
	global_store_dwordx4 v[2:3], v[6:9], off
	v_add_u32_e32 v2, 0x840, v1
	v_add_u32_e32 v4, 0x848, v1
	ds_read2_b32 v[2:3], v2 offset1:1
	ds_read2_b32 v[4:5], v4 offset1:1
	v_or_b32_e32 v6, s16, v27
	v_ashrrev_i32_e32 v7, 31, v6
	v_lshlrev_b64 v[6:7], 11, v[6:7]
	v_lshl_add_u64 v[40:41], v[38:39], 0, v[6:7]
	v_add_u32_e32 v6, 0xc60, v1
	v_add_u32_e32 v1, 0xc68, v1
	ds_read2_b32 v[6:7], v6 offset1:1
	ds_read2_b32 v[8:9], v1 offset1:1
	s_waitcnt lgkmcnt(2)
	global_store_dwordx4 v[40:41], v[2:5], off
	s_nop 1
	v_or_b32_e32 v2, s16, v28
	v_ashrrev_i32_e32 v3, 31, v2
	v_lshlrev_b64 v[2:3], 11, v[2:3]
	v_lshl_add_u64 v[2:3], v[38:39], 0, v[2:3]
	s_waitcnt lgkmcnt(0)
	global_store_dwordx4 v[2:3], v[6:9], off
	s_waitcnt lgkmcnt(0)
	s_branch .LBB0_781
; __device__ __forceinline__ void cvt_item_i8(const float* src, int ld, int k0, int c0, unsigned char* dst, int Kd, int drow0, const float* cmx  , unsigned char* scr, int lane) {
;     const int c = lane & 7, q = lane >> 3;
;     const f32x4 cm = *(const f32x4*)(cmx + 4 * c);
;     f32x4 inv; inv[0] = cm[0] > 0.f ? 127.f / cm[0] : 0.f; inv[1] = cm[1] > 0.f ? 127.f / cm[1] : 0.f; inv[2] = cm[2] > 0.f ? 127.f / cm[2] : 0.f; inv[3] = cm[3] > 0.f ? 127.f / cm[3] : 0.f;
;     f32x4 v[4][4];
; #pragma unroll
;     for (int g = 0; g < 4; ++g)
; #pragma unroll
;         for (int j = 0; j < 4; ++j) v[g][j] = __builtin_nontemporal_load((const f32x4*)(src + (size_t)(k0 + 32 * g + 4 * q + j) * ld + c0 + 4 * c));
; template <int GRP>
; __device__ __forceinline__ void conv_item(Frame& F, int r) {
;     ...
;         if (r < NI) { const int kb = r / 152, nb = r % 152, c0 = (nb < 112) ? nb * 32 : SRC_GATE + 8 + (nb - 112) * 32, drow = nb * 32;
;             if (QUANT) cvt_item_i8(inptr(F, IN_WIN) + (size_t)l * D * NIN_SRC, NIN_SRC, kb * 128, c0, ws + WS_WIN + (size_t)l * NIN * D, D, drow, cmx + CMX_WIN + l * NIN + drow, scr, F.lane);
.LBB0_799:
	v_readlane_b32 s3, v255, 10
	s_addk_i32 s3, 0xf980
	s_cmpk_gt_u32 s3, 0x17f
	s_cselect_b64 s[6:7], -1, 0
	s_xor_b64 s[0:1], s[0:1], -1
	s_or_b64 s[0:1], s[0:1], s[6:7]
	s_and_b64 vcc, exec, s[0:1]
	s_cbranch_vccnz .LBB0_801
	v_readlane_b32 s1, v255, 10
	s_addk_i32 s1, 0x180
	s_and_b32 s3, s1, 0xffff
	s_mul_i32 s3, s3, 0xd795
	s_lshr_b32 s4, s3, 16
	s_lshr_b32 s3, s3, 23
	s_mulk_i32 s3, 0x98
	s_sub_i32 s1, s1, s3
	v_readlane_b32 s0, v255, 9
	s_and_b32 s3, s1, 0xffff
	s_lshl_b32 s1, s1, 5
	s_mulk_i32 s0, 0x2200
	s_and_b32 s1, s1, 0xffe0
	s_add_i32 s0, s0, 0
	s_or_b32 s6, s1, 8
	s_cmpk_lt_u32 s3, 0x70
	s_cselect_b32 s8, s1, s6
	s_add_i32 s3, 0, 0x20240
	s_lshl_b32 s6, s1, 2
	s_add_u32 s6, s50, s6
	s_waitcnt vmcnt(7)
	v_and_b32_e32 v68, 7, v0
	s_addc_u32 s7, s51, 0
	v_lshlrev_b32_e32 v34, 4, v68
	v_mov_b32_e32 v35, 0
	s_waitcnt lgkmcnt(3)
	v_lshl_add_u64 v[2:3], s[6:7], 0, v[34:35]
	s_mov_b32 s6, 0xbb000
	v_add_co_u32_e32 v2, vcc, s6, v2
	s_waitcnt lgkmcnt(1)
	v_mov_b32_e32 v6, s3
	v_addc_co_u32_e32 v3, vcc, 0, v3, vcc
	global_load_dwordx4 v[2:5], v[2:3], off offset:3072
	s_waitcnt lgkmcnt(0)
	ds_read_b64 v[8:9], v6
	v_lshrrev_b32_e32 v1, 3, v194
	s_and_b32 s3, s4, 0xff80
	s_lshl_b32 s4, s8, 2
	v_lshlrev_b32_e32 v69, 2, v1
	s_waitcnt lgkmcnt(0)
	v_readfirstlane_b32 s6, v8
	v_readfirstlane_b32 s7, v9
	s_add_u32 s6, s6, s4
	v_or_b32_e32 v6, s3, v69
	s_addc_u32 s7, s7, 0
	s_mov_b32 s12, 0x42fe0000
	v_mov_b32_e32 v7, v35
	v_mul_u32_u24_e32 v6, 0x4c20, v6
	v_lshl_add_u64 v[8:9], s[6:7], 0, v[34:35]
	v_lshl_add_u64 v[10:11], v[8:9], 0, v[6:7]
	s_mov_b32 s9, 0x2610000
	v_add_co_u32_e32 v6, vcc, s9, v10
	s_mov_b32 s13, 0x2614000
	s_nop 0
	v_addc_co_u32_e32 v7, vcc, 0, v11, vcc
	s_mov_b32 s4, 0x2619000
	s_waitcnt vmcnt(7)
	v_mov_b32_e32 v74, 0x42fe0000
	s_waitcnt vmcnt(0)
	v_div_scale_f32 v8, s[6:7], v2, v2, s12
	v_div_scale_f32 v12, s[6:7], v3, v3, s12
	v_rcp_f32_e32 v18, v8
	v_rcp_f32_e32 v19, v12
	v_div_scale_f32 v14, s[8:9], v4, v4, s12
	v_rcp_f32_e32 v20, v14
	v_fma_f32 v22, -v8, v18, 1.0
	v_div_scale_f32 v9, vcc, s12, v2, s12
	v_fma_f32 v23, -v12, v19, 1.0
	v_fmac_f32_e32 v18, v22, v18
	v_div_scale_f32 v13, s[6:7], s12, v3, s12
	v_fmac_f32_e32 v19, v23, v19
	v_mul_f32_e32 v22, v9, v18
	v_fma_f32 v24, -v14, v20, 1.0
	v_mul_f32_e32 v23, v13, v19
	v_fma_f32 v26, -v8, v22, v9
	v_div_scale_f32 v15, s[8:9], s12, v4, s12
	v_fmac_f32_e32 v20, v24, v20
	v_fma_f32 v27, -v12, v23, v13
	v_fmac_f32_e32 v22, v26, v18
	v_mul_f32_e32 v24, v15, v20
	v_fmac_f32_e32 v23, v27, v19
	v_fma_f32 v8, -v8, v22, v9
	v_fma_f32 v28, -v14, v24, v15
	v_fma_f32 v9, -v12, v23, v13
	v_div_fmas_f32 v8, v8, v18, v22
	s_mov_b64 vcc, s[6:7]
	v_fmac_f32_e32 v24, v28, v20
	v_div_fixup_f32 v8, v8, v2, s12
	v_div_fmas_f32 v9, v9, v19, v23
	v_cmp_lt_f32_e32 vcc, 0, v2
	v_fma_f32 v12, -v14, v24, v15
	v_div_fixup_f32 v2, v9, v3, s12
	v_cndmask_b32_e32 v70, 0, v8, vcc
	s_mov_b64 vcc, s[8:9]
	v_div_fmas_f32 v8, v12, v20, v24
	v_cmp_lt_f32_e32 vcc, 0, v3
	v_div_scale_f32 v16, s[10:11], v5, v5, s12
	s_nop 0
	v_cndmask_b32_e32 v71, 0, v2, vcc
	v_div_fixup_f32 v2, v8, v4, s12
	v_cmp_lt_f32_e32 vcc, 0, v4
	v_rcp_f32_e32 v21, v16
	v_div_scale_f32 v17, s[10:11], s12, v5, s12
	v_cndmask_b32_e32 v72, 0, v2, vcc
	v_add_co_u32_e32 v2, vcc, s13, v10
	v_fma_f32 v25, -v16, v21, 1.0
	s_nop 0
	v_addc_co_u32_e32 v3, vcc, 0, v11, vcc
	global_load_dwordx4 v[36:39], v[6:7], off nt
	global_load_dwordx4 v[40:43], v[2:3], off offset:3104 nt
	v_add_co_u32_e32 v2, vcc, s4, v10
	s_mov_b32 s4, 0x261e000
	s_nop 0
	v_addc_co_u32_e32 v3, vcc, 0, v11, vcc
	v_add_co_u32_e32 v6, vcc, s4, v10
	v_fmac_f32_e32 v21, v25, v21
	s_nop 0
	v_addc_co_u32_e32 v7, vcc, 0, v11, vcc
	global_load_dwordx4 v[44:47], v[2:3], off offset:2112 nt
	global_load_dwordx4 v[48:51], v[6:7], off offset:1120 nt
	v_mul_f32_e32 v25, v17, v21
	v_fma_f32 v29, -v16, v25, v17
	v_fmac_f32_e32 v25, v29, v21
	v_fma_f32 v13, -v16, v25, v17
	s_mov_b64 vcc, s[10:11]
	v_div_fmas_f32 v2, v13, v21, v25
	v_div_fixup_f32 v2, v2, v5, s12
	v_cmp_lt_f32_e32 vcc, 0, v5
	s_mov_b32 s4, 0x26a8000
	s_mov_b32 s6, 0xc0c0500
	v_cndmask_b32_e32 v73, 0, v2, vcc
	v_add_co_u32_e32 v2, vcc, s4, v10
	s_mov_b32 s4, 0x26ad000
	s_nop 0
	v_addc_co_u32_e32 v3, vcc, 0, v11, vcc
	v_add_co_u32_e32 v4, vcc, s4, v10
	s_mov_b32 s4, 0x26b1000
	s_nop 0
	v_addc_co_u32_e32 v5, vcc, 0, v11, vcc
	global_load_dwordx4 v[52:55], v[2:3], off offset:1024 nt
	global_load_dwordx4 v[56:59], v[4:5], off offset:32 nt
	v_add_co_u32_e32 v2, vcc, s4, v10
	s_mov_b32 s4, 0x26b6000
	s_nop 0
	v_addc_co_u32_e32 v3, vcc, 0, v11, vcc
	v_add_co_u32_e32 v4, vcc, s4, v10
	s_mov_b32 s4, 0x2740000
	s_nop 0
	v_addc_co_u32_e32 v5, vcc, 0, v11, vcc
	global_load_dwordx4 v[60:63], v[2:3], off offset:3136 nt
	global_load_dwordx4 v[64:67], v[4:5], off offset:2144 nt
	v_add_co_u32_e32 v2, vcc, s4, v10
	s_mov_b32 s4, 0x2745000
	s_nop 0
	v_addc_co_u32_e32 v3, vcc, 0, v11, vcc
	v_add_co_u32_e32 v4, vcc, s4, v10
	s_mov_b32 s4, 0x274a000
	s_nop 0
	v_addc_co_u32_e32 v5, vcc, 0, v11, vcc
	global_load_dwordx4 v[18:21], v[2:3], off offset:2048 nt
	global_load_dwordx4 v[22:25], v[4:5], off offset:1056 nt
	v_add_co_u32_e32 v2, vcc, s4, v10
	s_mov_b32 s4, 0x274e000
	s_nop 0
	v_addc_co_u32_e32 v3, vcc, 0, v11, vcc
	v_add_co_u32_e32 v4, vcc, s4, v10
	s_mov_b32 s4, 0x27d8000
	s_nop 0
	v_addc_co_u32_e32 v5, vcc, 0, v11, vcc
	global_load_dwordx4 v[26:29], v[2:3], off offset:64 nt
	global_load_dwordx4 v[30:33], v[4:5], off offset:3168 nt
	v_add_co_u32_e32 v2, vcc, s4, v10
	s_mov_b32 s4, 0x27dd000
	s_nop 0
	v_addc_co_u32_e32 v3, vcc, 0, v11, vcc
	v_add_co_u32_e32 v6, vcc, s4, v10
	s_mov_b32 s4, 0x27e2000
	s_nop 0
	v_addc_co_u32_e32 v7, vcc, 0, v11, vcc
	v_add_co_u32_e32 v12, vcc, s4, v10
	s_mov_b32 s4, 0x27e7000
	s_nop 0
	v_addc_co_u32_e32 v13, vcc, 0, v11, vcc
	global_load_dwordx4 v[2:5], v[2:3], off offset:3072 nt
	s_nop 0
	global_load_dwordx4 v[6:9], v[6:7], off offset:2080 nt
	v_add_co_u32_e32 v14, vcc, s4, v10
	s_waitcnt vmcnt(0) lgkmcnt(0)
; __device__ __forceinline__ void cvt_item_i8(const float* src, int ld, int k0, int c0, unsigned char* dst, int Kd, int drow0, const float* cmx  , unsigned char* scr, int lane) {
;     ...
;         for (int j = 0; j < 4; ++j) v[g][j] = __builtin_nontemporal_load((const f32x4*)(src + (size_t)(k0 + 32 * g + 4 * q + j) * ld + c0 + 4 * c));
; #pragma unroll
;     for (int g = 0; g < 4; ++g)
; #pragma unroll
;         for (int i = 0; i < 4; ++i) *(unsigned*)(scr + (4 * c + i) * 132 + 32 * g + 4 * q) = pack_i8x4(v[g][0][i] * inv[i], v[g][1][i] * inv[i], v[g][2][i] * inv[i], v[g][3][i] * inv[i]);
	v_mul_f32_e32 v40, v70, v40
	v_addc_co_u32_e32 v15, vcc, 0, v11, vcc
	global_load_dwordx4 v[10:13], v[12:13], off offset:1088 nt
	s_nop 0
	global_load_dwordx4 v[14:17], v[14:15], off offset:96 nt
	s_mov_b32 s4, 0xc2fe0000
	v_mul_f32_e32 v36, v36, v70
	v_mul_f32_e32 v44, v70, v44
	v_med3_f32 v40, v40, s4, v74
	v_med3_f32 v36, v36, s4, v74
	v_rndne_f32_e32 v40, v40
	v_med3_f32 v44, v44, s4, v74
	v_rndne_f32_e32 v36, v36
	v_cvt_i32_f32_e32 v40, v40
	v_rndne_f32_e32 v44, v44
	v_cvt_i32_f32_e32 v36, v36
	v_cvt_i32_f32_sdwa v44, v44 dst_sel:WORD_1 dst_unused:UNUSED_PAD src0_sel:DWORD
	v_lshlrev_b32_e32 v40, 8, v40
	v_mul_f32_e32 v41, v71, v41
	v_perm_b32 v36, v40, v36, s6
	v_and_b32_e32 v40, 0xff0000, v44
	v_mul_f32_e32 v37, v37, v71
	v_mul_f32_e32 v44, v71, v45
	v_med3_f32 v41, v41, s4, v74
	v_mul_f32_e32 v45, v71, v49
	v_med3_f32 v37, v37, s4, v74
	v_rndne_f32_e32 v41, v41
	v_med3_f32 v44, v44, s4, v74
	v_rndne_f32_e32 v37, v37
	v_cvt_i32_f32_e32 v41, v41
	v_rndne_f32_e32 v44, v44
	v_med3_f32 v45, v45, s4, v74
	v_cvt_i32_f32_e32 v37, v37
	v_cvt_i32_f32_sdwa v44, v44 dst_sel:WORD_1 dst_unused:UNUSED_PAD src0_sel:DWORD
	v_rndne_f32_e32 v45, v45
	v_cvt_i32_f32_sdwa v45, v45 dst_sel:BYTE_3 dst_unused:UNUSED_PAD src0_sel:DWORD
	v_lshlrev_b32_e32 v41, 8, v41
	v_perm_b32 v37, v41, v37, s6
	v_and_b32_e32 v41, 0xff0000, v44
	v_or3_b32 v37, v37, v41, v45
	v_mul_f32_e32 v41, v72, v42
	v_mul_f32_e32 v38, v38, v72
	v_mul_f32_e32 v42, v72, v46
	v_med3_f32 v41, v41, s4, v74
	v_mul_f32_e32 v44, v72, v50
	v_med3_f32 v38, v38, s4, v74
	v_rndne_f32_e32 v41, v41
	v_med3_f32 v42, v42, s4, v74
	v_rndne_f32_e32 v38, v38
	v_cvt_i32_f32_e32 v41, v41
	v_rndne_f32_e32 v42, v42
	v_med3_f32 v44, v44, s4, v74
	v_cvt_i32_f32_e32 v38, v38
	v_cvt_i32_f32_sdwa v42, v42 dst_sel:WORD_1 dst_unused:UNUSED_PAD src0_sel:DWORD
	v_rndne_f32_e32 v44, v44
	v_cvt_i32_f32_sdwa v44, v44 dst_sel:BYTE_3 dst_unused:UNUSED_PAD src0_sel:DWORD
	v_lshlrev_b32_e32 v41, 8, v41
	v_perm_b32 v38, v41, v38, s6
	v_and_b32_e32 v41, 0xff0000, v42
	v_or3_b32 v38, v38, v41, v44
	v_mul_f32_e32 v41, v73, v43
	v_mul_f32_e32 v39, v39, v73
	v_mul_f32_e32 v42, v73, v47
	v_med3_f32 v41, v41, s4, v74
	v_mul_f32_e32 v43, v73, v51
	v_med3_f32 v39, v39, s4, v74
	v_rndne_f32_e32 v41, v41
	v_med3_f32 v42, v42, s4, v74
	v_rndne_f32_e32 v39, v39
	v_cvt_i32_f32_e32 v41, v41
	v_rndne_f32_e32 v42, v42
	v_med3_f32 v43, v43, s4, v74
	v_cvt_i32_f32_e32 v39, v39
	v_cvt_i32_f32_sdwa v42, v42 dst_sel:WORD_1 dst_unused:UNUSED_PAD src0_sel:DWORD
	v_rndne_f32_e32 v43, v43
	v_cvt_i32_f32_sdwa v43, v43 dst_sel:BYTE_3 dst_unused:UNUSED_PAD src0_sel:DWORD
	v_lshlrev_b32_e32 v41, 8, v41
	v_perm_b32 v39, v41, v39, s6
	v_and_b32_e32 v41, 0xff0000, v42
	v_mul_f32_e32 v42, v70, v56
	v_mul_f32_e32 v48, v70, v48
	v_or3_b32 v39, v39, v41, v43
	v_mul_f32_e32 v41, v70, v52
	v_mul_f32_e32 v43, v70, v60
	v_med3_f32 v42, v42, s4, v74
	v_mul_f32_e32 v22, v70, v22
	v_mul_f32_e32 v6, v70, v6
	v_med3_f32 v48, v48, s4, v74
	v_mul_f32_e32 v44, v70, v64
	v_med3_f32 v41, v41, s4, v74
	v_rndne_f32_e32 v42, v42
	v_med3_f32 v43, v43, s4, v74
	v_mul_f32_e32 v18, v70, v18
	v_mul_f32_e32 v26, v70, v26
	v_med3_f32 v22, v22, s4, v74
	v_mul_f32_e32 v2, v70, v2
	s_waitcnt vmcnt(0) lgkmcnt(0)
	v_mul_f32_e32 v10, v70, v10
	v_med3_f32 v6, v6, s4, v74
	v_rndne_f32_e32 v48, v48
	v_rndne_f32_e32 v41, v41
	v_cvt_i32_f32_e32 v42, v42
	v_rndne_f32_e32 v43, v43
	v_med3_f32 v44, v44, s4, v74
	v_mul_f32_e32 v30, v70, v30
	v_med3_f32 v18, v18, s4, v74
	v_rndne_f32_e32 v22, v22
	v_med3_f32 v26, v26, s4, v74
	v_mul_f32_e32 v14, v70, v14
	v_med3_f32 v2, v2, s4, v74
	v_rndne_f32_e32 v6, v6
	v_med3_f32 v10, v10, s4, v74
	v_cvt_i32_f32_sdwa v48, v48 dst_sel:BYTE_3 dst_unused:UNUSED_PAD src0_sel:DWORD
	v_cvt_i32_f32_e32 v41, v41
	v_cvt_i32_f32_sdwa v43, v43 dst_sel:WORD_1 dst_unused:UNUSED_PAD src0_sel:DWORD
	v_rndne_f32_e32 v44, v44
	v_rndne_f32_e32 v18, v18
	v_cvt_i32_f32_e32 v22, v22
	v_rndne_f32_e32 v26, v26
	v_med3_f32 v30, v30, s4, v74
	v_rndne_f32_e32 v2, v2
	v_cvt_i32_f32_e32 v6, v6
	v_rndne_f32_e32 v10, v10
	v_med3_f32 v14, v14, s4, v74
	v_cvt_i32_f32_sdwa v44, v44 dst_sel:BYTE_3 dst_unused:UNUSED_PAD src0_sel:DWORD
	v_cvt_i32_f32_e32 v18, v18
	v_cvt_i32_f32_sdwa v26, v26 dst_sel:WORD_1 dst_unused:UNUSED_PAD src0_sel:DWORD
	v_rndne_f32_e32 v30, v30
	v_cvt_i32_f32_e32 v2, v2
	v_cvt_i32_f32_sdwa v10, v10 dst_sel:WORD_1 dst_unused:UNUSED_PAD src0_sel:DWORD
	v_rndne_f32_e32 v14, v14
	v_cvt_i32_f32_sdwa v30, v30 dst_sel:BYTE_3 dst_unused:UNUSED_PAD src0_sel:DWORD
	v_cvt_i32_f32_sdwa v14, v14 dst_sel:BYTE_3 dst_unused:UNUSED_PAD src0_sel:DWORD
	v_lshlrev_b32_e32 v42, 8, v42
	v_or3_b32 v36, v36, v40, v48
	v_mul_u32_u24_e32 v40, 0x210, v68
	v_perm_b32 v41, v42, v41, s6
	v_and_b32_e32 v42, 0xff0000, v43
	v_lshlrev_b32_e32 v22, 8, v22
	v_lshlrev_b32_e32 v6, 8, v6
	v_add3_u32 v40, s0, v69, v40
	v_or3_b32 v41, v41, v42, v44
	v_perm_b32 v18, v22, v18, s6
	v_and_b32_e32 v22, 0xff0000, v26
	v_perm_b32 v2, v6, v2, s6
	v_and_b32_e32 v6, 0xff0000, v10
	ds_write2_b32 v40, v36, v41 offset1:8
	v_mul_f32_e32 v41, v71, v57
	v_or3_b32 v18, v18, v22, v30
	v_or3_b32 v2, v2, v6, v14
	v_mul_f32_e32 v36, v71, v53
	v_mul_f32_e32 v42, v71, v61
	v_med3_f32 v41, v41, s4, v74
	v_mul_f32_e32 v22, v71, v23
	ds_write2_b32 v40, v18, v2 offset0:16 offset1:24
	v_mul_f32_e32 v2, v71, v3
	v_mul_f32_e32 v3, v71, v7
	v_mul_f32_e32 v43, v71, v65
	v_med3_f32 v36, v36, s4, v74
	v_rndne_f32_e32 v41, v41
	v_med3_f32 v42, v42, s4, v74
	v_mul_f32_e32 v19, v71, v19
	v_mul_f32_e32 v23, v71, v27
	v_med3_f32 v22, v22, s4, v74
	v_mul_f32_e32 v6, v71, v11
	v_med3_f32 v3, v3, s4, v74
	v_rndne_f32_e32 v36, v36
	v_cvt_i32_f32_e32 v41, v41
; __device__ __forceinline__ void cvt_item_i8(const float* src, int ld, int k0, int c0, unsigned char* dst, int Kd, int drow0, const float* cmx  , unsigned char* scr, int lane) {
;     ...
; #pragma unroll
;     for (int g = 0; g < 4; ++g)
; #pragma unroll
;         for (int i = 0; i < 4; ++i) *(unsigned*)(scr + (4 * c + i) * 132 + 32 * g + 4 * q) = pack_i8x4(v[g][0][i] * inv[i], v[g][1][i] * inv[i], v[g][2][i] * inv[i], v[g][3][i] * inv[i]);
;     asm volatile("s_waitcnt lgkmcnt(0)" ::: "memory");
	v_rndne_f32_e32 v42, v42
	v_med3_f32 v43, v43, s4, v74
	v_mul_f32_e32 v26, v71, v31
	v_med3_f32 v19, v19, s4, v74
	v_rndne_f32_e32 v22, v22
	v_med3_f32 v23, v23, s4, v74
	v_mul_f32_e32 v7, v71, v15
	v_med3_f32 v2, v2, s4, v74
	v_rndne_f32_e32 v3, v3
	v_med3_f32 v6, v6, s4, v74
	v_cvt_i32_f32_e32 v36, v36
	v_cvt_i32_f32_sdwa v42, v42 dst_sel:WORD_1 dst_unused:UNUSED_PAD src0_sel:DWORD
	v_rndne_f32_e32 v43, v43
	v_rndne_f32_e32 v19, v19
	v_cvt_i32_f32_e32 v22, v22
	v_rndne_f32_e32 v23, v23
	v_med3_f32 v26, v26, s4, v74
	v_rndne_f32_e32 v2, v2
	v_cvt_i32_f32_e32 v3, v3
	v_rndne_f32_e32 v6, v6
	v_med3_f32 v7, v7, s4, v74
	v_cvt_i32_f32_sdwa v43, v43 dst_sel:BYTE_3 dst_unused:UNUSED_PAD src0_sel:DWORD
	v_cvt_i32_f32_e32 v19, v19
	v_cvt_i32_f32_sdwa v23, v23 dst_sel:WORD_1 dst_unused:UNUSED_PAD src0_sel:DWORD
	v_rndne_f32_e32 v26, v26
	v_cvt_i32_f32_e32 v2, v2
	v_cvt_i32_f32_sdwa v6, v6 dst_sel:WORD_1 dst_unused:UNUSED_PAD src0_sel:DWORD
	v_rndne_f32_e32 v7, v7
	v_cvt_i32_f32_sdwa v26, v26 dst_sel:BYTE_3 dst_unused:UNUSED_PAD src0_sel:DWORD
	v_cvt_i32_f32_sdwa v7, v7 dst_sel:BYTE_3 dst_unused:UNUSED_PAD src0_sel:DWORD
	v_lshlrev_b32_e32 v41, 8, v41
	v_perm_b32 v36, v41, v36, s6
	v_and_b32_e32 v41, 0xff0000, v42
	v_lshlrev_b32_e32 v22, 8, v22
	v_lshlrev_b32_e32 v3, 8, v3
	v_or3_b32 v36, v36, v41, v43
	v_perm_b32 v19, v22, v19, s6
	v_and_b32_e32 v22, 0xff0000, v23
	v_perm_b32 v2, v3, v2, s6
	v_and_b32_e32 v3, 0xff0000, v6
	ds_write2_b32 v40, v37, v36 offset0:33 offset1:41
	v_mul_f32_e32 v37, v72, v58
	v_or3_b32 v19, v19, v22, v26
	v_mul_f32_e32 v22, v72, v24
	v_or3_b32 v2, v2, v3, v7
	v_mul_f32_e32 v3, v72, v8
	v_mul_f32_e32 v36, v72, v54
	v_mul_f32_e32 v41, v72, v62
	v_med3_f32 v37, v37, s4, v74
	v_mul_f32_e32 v20, v72, v20
	v_mul_f32_e32 v23, v72, v28
	v_med3_f32 v22, v22, s4, v74
	ds_write2_b32 v40, v19, v2 offset0:49 offset1:57
	v_mul_f32_e32 v2, v72, v4
	v_mul_f32_e32 v4, v72, v12
	v_med3_f32 v3, v3, s4, v74
	v_mul_f32_e32 v42, v72, v66
	v_med3_f32 v36, v36, s4, v74
	v_rndne_f32_e32 v37, v37
	v_med3_f32 v41, v41, s4, v74
	v_mul_f32_e32 v24, v72, v32
	v_med3_f32 v20, v20, s4, v74
	v_rndne_f32_e32 v22, v22
	v_med3_f32 v23, v23, s4, v74
	v_mul_f32_e32 v6, v72, v16
	v_med3_f32 v2, v2, s4, v74
	v_rndne_f32_e32 v3, v3
	v_med3_f32 v4, v4, s4, v74
	v_rndne_f32_e32 v36, v36
	v_cvt_i32_f32_e32 v37, v37
	v_rndne_f32_e32 v41, v41
	v_med3_f32 v42, v42, s4, v74
	v_rndne_f32_e32 v20, v20
	v_cvt_i32_f32_e32 v22, v22
	v_rndne_f32_e32 v23, v23
	v_med3_f32 v24, v24, s4, v74
	v_rndne_f32_e32 v2, v2
	v_cvt_i32_f32_e32 v3, v3
	v_rndne_f32_e32 v4, v4
	v_med3_f32 v6, v6, s4, v74
	v_cvt_i32_f32_e32 v36, v36
	v_cvt_i32_f32_sdwa v41, v41 dst_sel:WORD_1 dst_unused:UNUSED_PAD src0_sel:DWORD
	v_rndne_f32_e32 v42, v42
	v_cvt_i32_f32_e32 v20, v20
	v_cvt_i32_f32_sdwa v23, v23 dst_sel:WORD_1 dst_unused:UNUSED_PAD src0_sel:DWORD
	v_rndne_f32_e32 v24, v24
	v_cvt_i32_f32_e32 v2, v2
	v_cvt_i32_f32_sdwa v4, v4 dst_sel:WORD_1 dst_unused:UNUSED_PAD src0_sel:DWORD
	v_rndne_f32_e32 v6, v6
	v_cvt_i32_f32_sdwa v42, v42 dst_sel:BYTE_3 dst_unused:UNUSED_PAD src0_sel:DWORD
	v_cvt_i32_f32_sdwa v24, v24 dst_sel:BYTE_3 dst_unused:UNUSED_PAD src0_sel:DWORD
	v_cvt_i32_f32_sdwa v6, v6 dst_sel:BYTE_3 dst_unused:UNUSED_PAD src0_sel:DWORD
	v_lshlrev_b32_e32 v37, 8, v37
	v_lshlrev_b32_e32 v22, 8, v22
	v_lshlrev_b32_e32 v3, 8, v3
	v_perm_b32 v36, v37, v36, s6
	v_and_b32_e32 v37, 0xff0000, v41
	v_perm_b32 v20, v22, v20, s6
	v_and_b32_e32 v22, 0xff0000, v23
	v_perm_b32 v2, v3, v2, s6
	v_and_b32_e32 v3, 0xff0000, v4
	v_or3_b32 v36, v36, v37, v42
	v_mul_f32_e32 v37, v73, v59
	v_or3_b32 v20, v20, v22, v24
	v_mul_f32_e32 v22, v73, v25
	v_or3_b32 v2, v2, v3, v6
	v_mul_f32_e32 v3, v73, v9
	ds_write2_b32 v40, v38, v36 offset0:66 offset1:74
	v_mul_f32_e32 v36, v73, v55
	v_med3_f32 v37, v37, s4, v74
	v_mul_f32_e32 v21, v73, v21
	v_mul_f32_e32 v23, v73, v29
	v_med3_f32 v22, v22, s4, v74
	ds_write2_b32 v40, v20, v2 offset0:82 offset1:90
	v_mul_f32_e32 v2, v73, v5
	v_mul_f32_e32 v4, v73, v13
	v_med3_f32 v3, v3, s4, v74
	v_mul_f32_e32 v38, v73, v63
	v_med3_f32 v36, v36, s4, v74
	v_rndne_f32_e32 v37, v37
	v_mul_f32_e32 v24, v73, v33
	v_med3_f32 v21, v21, s4, v74
	v_rndne_f32_e32 v22, v22
	v_med3_f32 v23, v23, s4, v74
	v_mul_f32_e32 v5, v73, v17
	v_med3_f32 v2, v2, s4, v74
	v_rndne_f32_e32 v3, v3
	v_med3_f32 v4, v4, s4, v74
	v_mul_f32_e32 v41, v73, v67
	v_rndne_f32_e32 v36, v36
	v_cvt_i32_f32_e32 v37, v37
	v_med3_f32 v38, v38, s4, v74
	v_rndne_f32_e32 v21, v21
	v_cvt_i32_f32_e32 v22, v22
	v_rndne_f32_e32 v23, v23
	v_med3_f32 v24, v24, s4, v74
	v_rndne_f32_e32 v2, v2
	v_cvt_i32_f32_e32 v3, v3
	v_rndne_f32_e32 v4, v4
	v_med3_f32 v5, v5, s4, v74
	v_cvt_i32_f32_e32 v36, v36
	v_rndne_f32_e32 v38, v38
	v_med3_f32 v41, v41, s4, v74
	v_cvt_i32_f32_e32 v21, v21
	v_cvt_i32_f32_sdwa v23, v23 dst_sel:WORD_1 dst_unused:UNUSED_PAD src0_sel:DWORD
	v_rndne_f32_e32 v24, v24
	v_cvt_i32_f32_e32 v2, v2
	v_cvt_i32_f32_sdwa v4, v4 dst_sel:WORD_1 dst_unused:UNUSED_PAD src0_sel:DWORD
	v_rndne_f32_e32 v5, v5
	v_cvt_i32_f32_sdwa v38, v38 dst_sel:WORD_1 dst_unused:UNUSED_PAD src0_sel:DWORD
	v_rndne_f32_e32 v41, v41
	v_cvt_i32_f32_sdwa v24, v24 dst_sel:BYTE_3 dst_unused:UNUSED_PAD src0_sel:DWORD
	v_cvt_i32_f32_sdwa v5, v5 dst_sel:BYTE_3 dst_unused:UNUSED_PAD src0_sel:DWORD
	v_cvt_i32_f32_sdwa v41, v41 dst_sel:BYTE_3 dst_unused:UNUSED_PAD src0_sel:DWORD
	v_lshlrev_b32_e32 v37, 8, v37
	v_lshlrev_b32_e32 v22, 8, v22
	v_lshlrev_b32_e32 v3, 8, v3
	v_perm_b32 v36, v37, v36, s6
	v_perm_b32 v21, v22, v21, s6
	v_and_b32_e32 v22, 0xff0000, v23
	v_perm_b32 v2, v3, v2, s6
	v_and_b32_e32 v3, 0xff0000, v4
	s_add_u32 s6, s50, s3
	v_and_b32_e32 v37, 0xff0000, v38
	v_or3_b32 v21, v21, v22, v24
	v_or3_b32 v2, v2, v3, v5
	s_addc_u32 s7, s51, 0
	v_or3_b32 v36, v36, v37, v41
	ds_write2_b32 v40, v21, v2 offset0:115 offset1:123
	v_lshl_add_u64 v[2:3], s[6:7], 0, v[34:35]
	s_mov_b64 s[6:7], 0x1180000
	ds_write2_b32 v40, v39, v36 offset0:99 offset1:107
	v_lshl_add_u64 v[10:11], v[2:3], 0, s[6:7]
	v_mul_u32_u24_e32 v2, 0x84, v1
	s_waitcnt lgkmcnt(0)
; __device__ __forceinline__ void cvt_item_i8(const float* src, int ld, int k0, int c0, unsigned char* dst, int Kd, int drow0, const float* cmx  , unsigned char* scr, int lane) {
;     ...
;     asm volatile("s_waitcnt lgkmcnt(0)" ::: "memory");
; #pragma unroll
;     for (int r = 0; r < 4; ++r) { const int n = 8 * r + (lane >> 3), ch = lane & 7; const unsigned char* p = scr + n * 132 + ch * 16;
;         u32x4 o; o.x = *(const unsigned*)(p); o.y = *(const unsigned*)(p + 4); o.z = *(const unsigned*)(p + 8); o.w = *(const unsigned*)(p + 12);
;         *(u32x4*)(dst + (size_t)(drow0 + n) * Kd + k0 + 16 * ch) = o; }
;     asm volatile("s_waitcnt lgkmcnt(0)" ::: "memory");
	v_add3_u32 v14, s0, v34, v2
	ds_read2_b32 v[2:3], v14 offset1:1
	ds_read2_b32 v[4:5], v14 offset0:2 offset1:3
	v_or_b32_e32 v1, s1, v1
	v_lshlrev_b32_e32 v34, 11, v1
	v_add_u32_e32 v1, 0x420, v14
	v_add_u32_e32 v8, 0x428, v14
	ds_read2_b32 v[6:7], v1 offset1:1
	ds_read2_b32 v[8:9], v8 offset1:1
	v_lshl_add_u64 v[12:13], v[10:11], 0, v[34:35]
	s_waitcnt lgkmcnt(2)
	global_store_dwordx4 v[12:13], v[2:5], off
	v_add_u32_e32 v1, 0x840, v14
	v_or_b32_e32 v12, 0x8000, v34
	v_or_b32_e32 v2, 0x4000, v34
	v_mov_b32_e32 v3, v35
	v_lshl_add_u64 v[2:3], v[10:11], 0, v[2:3]
	s_waitcnt lgkmcnt(0)
	global_store_dwordx4 v[2:3], v[6:9], off
	v_add_u32_e32 v4, 0x848, v14
	ds_read2_b32 v[2:3], v1 offset1:1
	ds_read2_b32 v[4:5], v4 offset1:1
	v_add_u32_e32 v1, 0xc60, v14
	v_add_u32_e32 v8, 0xc68, v14
	ds_read2_b32 v[6:7], v1 offset1:1
	ds_read2_b32 v[8:9], v8 offset1:1
	v_mov_b32_e32 v13, v35
	v_lshl_add_u64 v[12:13], v[10:11], 0, v[12:13]
	v_or_b32_e32 v34, 0xc000, v34
	s_waitcnt lgkmcnt(2)
	global_store_dwordx4 v[12:13], v[2:5], off
	s_nop 1
	v_lshl_add_u64 v[2:3], v[10:11], 0, v[34:35]
	s_waitcnt lgkmcnt(0)
	global_store_dwordx4 v[2:3], v[6:9], off
	s_waitcnt lgkmcnt(0)

; #define LAS __attribute__((address_space(3)))
; #define LBAR() do { asm volatile("s_waitcnt lgkmcnt(0)" ::: "memory"); __builtin_amdgcn_s_barrier(); asm volatile("" ::: "memory"); } while (0)
; __device__ __forceinline__ void swa_unit(Frame& F, const bf16_t* proj, const float* sinks, unsigned char* Y, int b, int kvh, int qb) {
;     LAS unsigned char* lds = F.lds; int lane = F.lane; asm volatile("" : "+v"(lane));
;     const int r32 = lane & 31, hh = lane >> 5, w = F.wave, hq = kvh * 8 + w;
;     const size_t rb = (size_t)b * SEQ;
;     const bf16_t* kcol = proj + C_SK + kvh * 64; const bf16_t* vcol = proj + C_SV + kvh * 64;
;     LBAR();
;     if (qb > 0) stage_kv(lds, kcol, vcol, rb + (size_t)qb * 128 - 128, 256, 0, F.tid);
;     else        stage_kv(lds, kcol, vcol, rb, 128, 128, F.tid);
;     LBAR();
;     const float sk = sinks[hq] * 1.4426950408889634f;
;     for (int sb = 0; sb < 4; ++sb) {
;         const int t = qb * 128 + sb * 32 + r32;
;         bf16x8 qf[4];
;         { const bf16_t* qrow = proj + (rb + t) * NIN + C_SQ + hq * 64 + hh * 8;
; #pragma unroll
;           for (int s = 0; s < 4; ++s) qf[s] = *(const bf16x8*)(qrow + s * 16); }
;         State st; init(st);
;         int kt0 = sb; if (qb == 0 && kt0 < 4) kt0 = 4;
;         if (kt0 == sb) tile<2>(lds, sb, qf, st, lane);
;         for (int kt = (kt0 > sb + 1 ? kt0 : sb + 1); kt < sb + 4; ++kt) tile<3>(lds, kt, qf, st, lane);
;         tile<1>(lds, sb + 4, qf, st, lane);
.LBB0_905:
	s_lshl_b32 s0, s19, 3
	v_readlane_b32 s8, v255, 9
	s_add_i32 s0, s0, s8
	s_lshl_b32 s8, s0, 2
	s_add_u32 s8, s17, s8
	s_addc_u32 s9, s18, 0
	s_waitcnt lgkmcnt(0)
	s_barrier
	v_mov_b64_e32 v[4:5], s[8:9]
	global_load_dword v3, v[4:5], off
	v_and_b32_e32 v139, 31, v1
	v_ashrrev_i32_e32 v15, 5, v1
	v_add_u32_e32 v4, -9, v139
	v_lshlrev_b32_e32 v16, 2, v15
	s_lshl_b32 s0, s0, 6
	v_add_u32_e32 v6, -11, v139
	v_or_b32_e32 v17, 2, v16
	v_cmp_gt_i32_e64 s[18:19], v16, v4
	v_lshlrev_b32_e32 v4, 3, v15
	s_movk_i32 s52, 0x208
	v_add_u32_e32 v5, -10, v139
	v_add_u32_e32 v7, -16, v139
	v_subrev_u32_e32 v8, 17, v139
	v_subrev_u32_e32 v9, 18, v139
	v_subrev_u32_e32 v10, 19, v139
	v_subrev_u32_e32 v11, 24, v139
	v_subrev_u32_e32 v12, 25, v139
	v_subrev_u32_e32 v13, 26, v139
	v_subrev_u32_e32 v14, 27, v139
	v_cmp_gt_i32_e64 s[12:13], v17, v139
	v_or_b32_e32 v17, 3, v16
	v_cmp_gt_i32_e64 s[22:23], v16, v6
	v_mad_u32_u24 v6, v139, s52, v4
	s_add_u32 s52, s5, s0
	v_lshl_or_b32 v156, s16, 7, v139
	v_cmp_gt_i32_e64 s[8:9], v16, v139
	v_cmp_lt_i32_e64 s[10:11], v16, v139
	v_cmp_gt_i32_e64 s[14:15], v17, v139
	v_cmp_gt_i32_e64 s[20:21], v16, v5
	v_cmp_gt_i32_e64 s[24:25], v16, v7
	v_cmp_gt_i32_e64 s[26:27], v16, v8
	v_cmp_gt_i32_e64 s[28:29], v16, v9
	v_cmp_gt_i32_e64 s[30:31], v16, v10
	v_cmp_gt_i32_e64 s[34:35], v16, v11
	v_cmp_gt_i32_e64 s[36:37], v16, v12
	v_cmp_gt_i32_e64 s[38:39], v16, v13
	v_cmp_gt_i32_e64 s[40:41], v16, v14
	s_addc_u32 s53, s33, 0
	v_cndmask_b32_e64 v34, v153, v18, s[8:9]
	v_cndmask_b32_e64 v35, v18, v153, s[10:11]
	v_cndmask_b32_e64 v36, v153, v18, s[12:13]
	v_cndmask_b32_e64 v37, v153, v18, s[14:15]
	v_cndmask_b32_e64 v39, v153, v18, s[18:19]
	v_cndmask_b32_e64 v40, v153, v18, s[20:21]
	v_cndmask_b32_e64 v41, v153, v18, s[22:23]
	v_cndmask_b32_e64 v42, v153, v18, s[24:25]
	v_cndmask_b32_e64 v43, v153, v18, s[26:27]
	v_cndmask_b32_e64 v44, v153, v18, s[28:29]
	v_cndmask_b32_e64 v45, v153, v18, s[30:31]
	v_cndmask_b32_e64 v46, v153, v18, s[34:35]
	v_cndmask_b32_e64 v47, v153, v18, s[36:37]
	v_cndmask_b32_e64 v48, v153, v18, s[38:39]
	v_cndmask_b32_e64 v49, v153, v18, s[40:41]
	v_add_u32_e32 v157, 0, v6
	v_add_u32_e32 v158, s62, v6
	s_mov_b32 s71, 0
	s_mov_b32 s70, 1
	s_lshl_b32 s0, s0, 1
	s_waitcnt vmcnt(0) lgkmcnt(0)
	v_mul_f32_e32 v155, 0x3fb8aa3b, v3
	v_ashrrev_i32_e32 v3, 2, v1
	v_ashrrev_i32_e32 v1, 3, v1
	v_and_b32_e32 v140, -8, v3
	v_add_u32_e32 v3, -8, v139
	v_and_b32_e32 v4, -4, v1
	v_cmp_gt_i32_e64 s[16:17], v16, v3
	v_lshlrev_b32_e32 v3, 4, v15
	v_ashrrev_i32_e32 v5, 31, v4
	v_mul_u32_u24_e32 v1, 0x90, v139
	v_ashrrev_i32_e32 v141, 31, v140
	v_cndmask_b32_e64 v38, v153, v18, s[16:17]
	v_add_u32_e32 v142, 0, v3
	v_lshl_add_u64 v[144:145], s[52:53], 0, v[4:5]
	v_add3_u32 v159, v1, v3, 0
	s_branch .LBB0_907

; __device__ __forceinline__ void cvt_item8(const float* src, int ld, int k0, int c0, unsigned char* dst, int Kd, int drow0, unsigned char* scr, int lane) {
;     const int c = lane & 7, q = lane >> 3;
;     f32x4 v[4][4];
; #pragma unroll
;     for (int g = 0; g < 4; ++g)
; #pragma unroll
;         for (int j = 0; j < 4; ++j) v[g][j] = __builtin_nontemporal_load((const f32x4*)(src + (size_t)(k0 + 32 * g + 4 * q + j) * ld + c0 + 4 * c));
; #pragma unroll
;     for (int g = 0; g < 4; ++g)
; #pragma unroll
;         for (int i = 0; i < 4; ++i) *(unsigned*)(scr + (4 * c + i) * 132 + 32 * g + 4 * q) = pg8::pack_fp8x4(v[g][0][i] * WSC, v[g][1][i] * WSC, v[g][2][i] * WSC, v[g][3][i] * WSC);
; template <int GRP>
; __device__ __forceinline__ void conv_item(Frame& F, int r) {
;     ...
;         if (r < CI_WO) { const int kb = r / 64, nb = r % 64;
;             cvt_item8(inptr(F, IN_WOUT) + (size_t)l * D * D, D, kb * 128, nb * 32, ws + WS_WOUT + (size_t)l * D * D, D, nb * 32, scr, F.lane); return; }
.LBB0_941:
	s_andn2_b64 vcc, exec, s[16:17]
	s_cbranch_vccnz .LBB0_925
	s_ashr_i32 s8, s20, 31
	v_mov_b32_e32 v1, s68
	s_lshr_b32 s8, s8, 26
	s_waitcnt lgkmcnt(3)
	ds_read_b64 v[2:3], v1
	s_add_i32 s8, s20, s8
	s_and_b32 s16, s8, 0x7ffffc0
	s_sub_i32 s16, s20, s16
	s_lshl_b32 s16, s16, 5
	s_lshl_b32 s8, s8, 1
	s_ashr_i32 s17, s16, 31
	s_waitcnt lgkmcnt(0)
	v_readfirstlane_b32 s19, v2
	s_and_b32 s18, s8, 0xffffff80
	s_lshl_b64 s[20:21], s[16:17], 2
	v_readfirstlane_b32 s69, v3
	s_add_u32 s20, s19, s20
	v_or_b32_e32 v86, s18, v21
	s_addc_u32 s21, s69, s21
	v_lshlrev_b32_e32 v2, 2, v14
	v_mov_b32_e32 v3, v11
	v_lshl_add_u64 v[2:3], s[20:21], 0, v[2:3]
	v_ashrrev_i32_e32 v87, 31, v86
	v_or_b32_e32 v4, 1, v86
	v_lshl_add_u64 v[88:89], v[2:3], 0, s[14:15]
	v_lshlrev_b64 v[2:3], 13, v[86:87]
	v_ashrrev_i32_e32 v5, 31, v4
	v_lshl_add_u64 v[2:3], v[88:89], 0, v[2:3]
	v_lshlrev_b64 v[4:5], 13, v[4:5]
	v_lshl_add_u64 v[4:5], v[88:89], 0, v[4:5]
	global_load_dwordx4 v[38:41], v[2:3], off nt
	global_load_dwordx4 v[42:45], v[4:5], off nt
	v_or_b32_e32 v2, 2, v86
	v_ashrrev_i32_e32 v3, 31, v2
	v_lshlrev_b64 v[2:3], 13, v[2:3]
	v_lshl_add_u64 v[2:3], v[88:89], 0, v[2:3]
	s_waitcnt vmcnt(0)
	global_load_dwordx4 v[46:49], v[2:3], off nt
	v_or_b32_e32 v2, 3, v86
	v_ashrrev_i32_e32 v3, 31, v2
	v_lshlrev_b64 v[2:3], 13, v[2:3]
	v_lshl_add_u64 v[2:3], v[88:89], 0, v[2:3]
	global_load_dwordx4 v[50:53], v[2:3], off nt
	v_or_b32_e32 v2, 32, v86
	v_ashrrev_i32_e32 v3, 31, v2
	v_or_b32_e32 v4, 33, v86
	v_lshlrev_b64 v[2:3], 13, v[2:3]
	v_ashrrev_i32_e32 v5, 31, v4
	v_lshl_add_u64 v[2:3], v[88:89], 0, v[2:3]
	v_lshlrev_b64 v[4:5], 13, v[4:5]
	v_lshl_add_u64 v[4:5], v[88:89], 0, v[4:5]
	global_load_dwordx4 v[54:57], v[2:3], off nt
	global_load_dwordx4 v[58:61], v[4:5], off nt
	v_or_b32_e32 v2, 34, v86
	v_ashrrev_i32_e32 v3, 31, v2
	v_or_b32_e32 v4, 35, v86
	v_lshlrev_b64 v[2:3], 13, v[2:3]
	v_ashrrev_i32_e32 v5, 31, v4
	v_lshl_add_u64 v[2:3], v[88:89], 0, v[2:3]
	v_lshlrev_b64 v[4:5], 13, v[4:5]
	v_lshl_add_u64 v[4:5], v[88:89], 0, v[4:5]
	global_load_dwordx4 v[62:65], v[2:3], off nt
	global_load_dwordx4 v[66:69], v[4:5], off nt
	v_or_b32_e32 v2, 64, v86
	v_ashrrev_i32_e32 v3, 31, v2
	v_or_b32_e32 v4, 0x41, v86
	v_lshlrev_b64 v[2:3], 13, v[2:3]
	v_ashrrev_i32_e32 v5, 31, v4
	v_lshl_add_u64 v[2:3], v[88:89], 0, v[2:3]
	v_lshlrev_b64 v[4:5], 13, v[4:5]
	v_lshl_add_u64 v[4:5], v[88:89], 0, v[4:5]
	global_load_dwordx4 v[70:73], v[2:3], off nt
	global_load_dwordx4 v[74:77], v[4:5], off nt
	v_or_b32_e32 v2, 0x42, v86
	v_ashrrev_i32_e32 v3, 31, v2
	v_or_b32_e32 v4, 0x43, v86
	v_lshlrev_b64 v[2:3], 13, v[2:3]
	v_ashrrev_i32_e32 v5, 31, v4
	v_lshl_add_u64 v[2:3], v[88:89], 0, v[2:3]
	v_lshlrev_b64 v[4:5], 13, v[4:5]
	v_lshl_add_u64 v[4:5], v[88:89], 0, v[4:5]
	global_load_dwordx4 v[78:81], v[2:3], off nt
	global_load_dwordx4 v[82:85], v[4:5], off nt
	v_or_b32_e32 v2, 0x60, v86
	v_or_b32_e32 v4, 0x61, v86
	v_ashrrev_i32_e32 v3, 31, v2
	v_ashrrev_i32_e32 v5, 31, v4
	v_lshlrev_b64 v[2:3], 13, v[2:3]
	v_lshlrev_b64 v[4:5], 13, v[4:5]
	v_lshl_add_u64 v[2:3], v[88:89], 0, v[2:3]
	v_lshl_add_u64 v[6:7], v[88:89], 0, v[4:5]
	global_load_dwordx4 v[2:5], v[2:3], off nt
	s_nop 0
	global_load_dwordx4 v[6:9], v[6:7], off nt
	v_or_b32_e32 v90, 0x62, v86
	v_or_b32_e32 v86, 0x63, v86
	v_ashrrev_i32_e32 v91, 31, v90
	v_ashrrev_i32_e32 v87, 31, v86
	v_lshlrev_b64 v[90:91], 13, v[90:91]
	v_lshlrev_b64 v[86:87], 13, v[86:87]
	v_lshl_add_u64 v[90:91], v[88:89], 0, v[90:91]
	v_lshl_add_u64 v[92:93], v[88:89], 0, v[86:87]
	global_load_dwordx4 v[86:89], v[90:91], off nt
	s_nop 0
	global_load_dwordx4 v[90:93], v[92:93], off nt
	s_ashr_i32 s19, s18, 31
	s_waitcnt lgkmcnt(0)
	v_mul_f32_e32 v1, 0x42800000, v38
	v_mul_f32_e32 v38, 0x42800000, v42
	v_med3_f32 v1, v1, s67, v37
	v_med3_f32 v38, v38, s67, v37
	s_waitcnt vmcnt(0)
	v_mul_f32_e32 v42, 0x42800000, v46
	v_mov_b32_e32 v46, v11
	v_cvt_pk_fp8_f32 v46, v1, v38
	v_med3_f32 v38, v42, s67, v37
	v_mul_f32_e32 v42, 0x42800000, v47
	v_mul_f32_e32 v1, 0x42800000, v50
	v_med3_f32 v1, v1, s67, v37
	v_cvt_pk_fp8_f32 v46, v38, v1 op_sel:[0,0,1]
	v_mul_f32_e32 v38, 0x42800000, v39
	v_mul_f32_e32 v39, 0x42800000, v43
	v_med3_f32 v38, v38, s67, v37
	v_med3_f32 v39, v39, s67, v37
	v_mov_b32_e32 v43, v11
	v_cvt_pk_fp8_f32 v43, v38, v39
	v_mul_f32_e32 v38, 0x42800000, v51
	v_med3_f32 v39, v42, s67, v37
	v_med3_f32 v38, v38, s67, v37
	v_cvt_pk_fp8_f32 v43, v39, v38 op_sel:[0,0,1]
	v_mul_f32_e32 v38, 0x42800000, v40
	v_mul_f32_e32 v39, 0x42800000, v44
	v_med3_f32 v38, v38, s67, v37
	v_med3_f32 v39, v39, s67, v37
	v_mov_b32_e32 v42, v11
	v_cvt_pk_fp8_f32 v42, v38, v39
	v_mul_f32_e32 v40, 0x42800000, v48
	v_mul_f32_e32 v38, 0x42800000, v52
	v_med3_f32 v39, v40, s67, v37
	v_med3_f32 v38, v38, s67, v37
	v_cvt_pk_fp8_f32 v42, v39, v38 op_sel:[0,0,1]
	v_mul_f32_e32 v38, 0x42800000, v41
	v_mul_f32_e32 v39, 0x42800000, v45
	v_med3_f32 v38, v38, s67, v37
	v_med3_f32 v39, v39, s67, v37
	v_mov_b32_e32 v41, v11
	v_cvt_pk_fp8_f32 v41, v38, v39
	v_mul_f32_e32 v40, 0x42800000, v49
	v_mul_f32_e32 v38, 0x42800000, v53
	v_med3_f32 v39, v40, s67, v37
	v_med3_f32 v38, v38, s67, v37
	v_cvt_pk_fp8_f32 v41, v39, v38 op_sel:[0,0,1]
	v_mul_f32_e32 v38, 0x42800000, v54
	v_mul_f32_e32 v39, 0x42800000, v58
	v_med3_f32 v38, v38, s67, v37
	v_med3_f32 v39, v39, s67, v37
	v_mov_b32_e32 v44, v11
	v_cvt_pk_fp8_f32 v44, v38, v39
	v_mul_f32_e32 v40, 0x42800000, v62
	v_mul_f32_e32 v38, 0x42800000, v66
	v_med3_f32 v39, v40, s67, v37
	v_med3_f32 v38, v38, s67, v37
	v_cvt_pk_fp8_f32 v44, v39, v38 op_sel:[0,0,1]
	v_mul_f32_e32 v38, 0x42800000, v55
	v_mul_f32_e32 v39, 0x42800000, v59
	v_med3_f32 v38, v38, s67, v37
; __device__ __forceinline__ void cvt_item8(const float* src, int ld, int k0, int c0, unsigned char* dst, int Kd, int drow0, unsigned char* scr, int lane) {
;     ...
;     for (int g = 0; g < 4; ++g)
; #pragma unroll
;         for (int i = 0; i < 4; ++i) *(unsigned*)(scr + (4 * c + i) * 132 + 32 * g + 4 * q) = pg8::pack_fp8x4(v[g][0][i] * WSC, v[g][1][i] * WSC, v[g][2][i] * WSC, v[g][3][i] * WSC);
;     asm volatile("s_waitcnt lgkmcnt(0)" ::: "memory");
; #pragma unroll
;     for (int r = 0; r < 4; ++r) { const int n = 8 * r + (lane >> 3), ch = lane & 7; const unsigned char* p = scr + n * 132 + ch * 16;
;         u32x4 o; o.x = *(const unsigned*)(p); o.y = *(const unsigned*)(p + 4); o.z = *(const unsigned*)(p + 8); o.w = *(const unsigned*)(p + 12);
;         *(u32x4*)(dst + (size_t)(drow0 + n) * Kd + k0 + 16 * ch) = o; }
;     asm volatile("s_waitcnt lgkmcnt(0)" ::: "memory");
	v_med3_f32 v39, v39, s67, v37
	v_mov_b32_e32 v45, v11
	v_cvt_pk_fp8_f32 v45, v38, v39
	v_mul_f32_e32 v40, 0x42800000, v63
	v_mul_f32_e32 v38, 0x42800000, v67
	v_med3_f32 v39, v40, s67, v37
	v_med3_f32 v38, v38, s67, v37
	v_cvt_pk_fp8_f32 v45, v39, v38 op_sel:[0,0,1]
	v_mul_f32_e32 v38, 0x42800000, v56
	v_mul_f32_e32 v39, 0x42800000, v60
	v_med3_f32 v38, v38, s67, v37
	v_med3_f32 v39, v39, s67, v37
	v_mov_b32_e32 v47, v11
	v_cvt_pk_fp8_f32 v47, v38, v39
	v_mul_f32_e32 v40, 0x42800000, v64
	v_mul_f32_e32 v38, 0x42800000, v68
	v_med3_f32 v39, v40, s67, v37
	v_med3_f32 v38, v38, s67, v37
	v_cvt_pk_fp8_f32 v47, v39, v38 op_sel:[0,0,1]
	v_mul_f32_e32 v38, 0x42800000, v57
	v_mul_f32_e32 v39, 0x42800000, v61
	v_med3_f32 v38, v38, s67, v37
	v_med3_f32 v39, v39, s67, v37
	v_mov_b32_e32 v48, v11
	v_cvt_pk_fp8_f32 v48, v38, v39
	v_mul_f32_e32 v40, 0x42800000, v65
	v_mul_f32_e32 v38, 0x42800000, v69
	v_med3_f32 v39, v40, s67, v37
	v_med3_f32 v38, v38, s67, v37
	v_add_u32_e32 v1, v22, v23
	v_cvt_pk_fp8_f32 v48, v39, v38 op_sel:[0,0,1]
	v_mul_f32_e32 v38, 0x42800000, v70
	v_mul_f32_e32 v39, 0x42800000, v74
	ds_write2_b32 v1, v46, v44 offset1:8
	ds_write2_b32 v1, v43, v45 offset0:33 offset1:41
	ds_write2_b32 v1, v42, v47 offset0:66 offset1:74
	ds_write2_b32 v1, v41, v48 offset0:99 offset1:107
	v_med3_f32 v38, v38, s67, v37
	v_med3_f32 v39, v39, s67, v37
	v_mov_b32_e32 v41, v11
	v_cvt_pk_fp8_f32 v41, v38, v39
	v_mul_f32_e32 v40, 0x42800000, v78
	v_mul_f32_e32 v38, 0x42800000, v82
	v_med3_f32 v39, v40, s67, v37
	v_med3_f32 v38, v38, s67, v37
	v_cvt_pk_fp8_f32 v41, v39, v38 op_sel:[0,0,1]
	v_mul_f32_e32 v38, 0x42800000, v71
	v_mul_f32_e32 v39, 0x42800000, v75
	v_med3_f32 v38, v38, s67, v37
	v_med3_f32 v39, v39, s67, v37
	v_mov_b32_e32 v42, v11
	v_cvt_pk_fp8_f32 v42, v38, v39
	v_mul_f32_e32 v40, 0x42800000, v79
	v_mul_f32_e32 v38, 0x42800000, v83
	v_med3_f32 v39, v40, s67, v37
	v_med3_f32 v38, v38, s67, v37
	v_cvt_pk_fp8_f32 v42, v39, v38 op_sel:[0,0,1]
	v_mul_f32_e32 v38, 0x42800000, v72
	v_mul_f32_e32 v39, 0x42800000, v76
	v_med3_f32 v38, v38, s67, v37
	v_med3_f32 v39, v39, s67, v37
	v_mov_b32_e32 v43, v11
	v_cvt_pk_fp8_f32 v43, v38, v39
	v_mul_f32_e32 v40, 0x42800000, v80
	v_mul_f32_e32 v38, 0x42800000, v84
	v_med3_f32 v39, v40, s67, v37
	v_med3_f32 v38, v38, s67, v37
	v_cvt_pk_fp8_f32 v43, v39, v38 op_sel:[0,0,1]
	v_mul_f32_e32 v38, 0x42800000, v73
	v_mul_f32_e32 v39, 0x42800000, v77
	v_med3_f32 v38, v38, s67, v37
	v_med3_f32 v39, v39, s67, v37
	v_mov_b32_e32 v44, v11
	v_cvt_pk_fp8_f32 v44, v38, v39
	v_mul_f32_e32 v40, 0x42800000, v81
	v_mul_f32_e32 v38, 0x42800000, v85
	v_med3_f32 v39, v40, s67, v37
	v_med3_f32 v38, v38, s67, v37
	v_mul_f32_e32 v2, 0x42800000, v2
	v_mul_f32_e32 v6, 0x42800000, v6
	v_cvt_pk_fp8_f32 v44, v39, v38 op_sel:[0,0,1]
	v_med3_f32 v2, v2, s67, v37
	v_med3_f32 v6, v6, s67, v37
	v_mov_b32_e32 v39, v11
	v_cvt_pk_fp8_f32 v39, v2, v6
	v_mul_f32_e32 v38, 0x42800000, v86
	v_mul_f32_e32 v2, 0x42800000, v90
	v_med3_f32 v6, v38, s67, v37
	v_med3_f32 v2, v2, s67, v37
	v_cvt_pk_fp8_f32 v39, v6, v2 op_sel:[0,0,1]
	v_mul_f32_e32 v2, 0x42800000, v3
	v_mul_f32_e32 v3, 0x42800000, v7
	v_med3_f32 v2, v2, s67, v37
	v_med3_f32 v3, v3, s67, v37
	v_mov_b32_e32 v7, v11
	v_cvt_pk_fp8_f32 v7, v2, v3
	v_mul_f32_e32 v6, 0x42800000, v87
	v_mul_f32_e32 v2, 0x42800000, v91
	v_med3_f32 v3, v6, s67, v37
	v_med3_f32 v2, v2, s67, v37
	v_cvt_pk_fp8_f32 v7, v3, v2 op_sel:[0,0,1]
	v_mul_f32_e32 v2, 0x42800000, v4
	v_mul_f32_e32 v3, 0x42800000, v8
	v_med3_f32 v2, v2, s67, v37
	v_med3_f32 v3, v3, s67, v37
	v_mov_b32_e32 v6, v11
	v_cvt_pk_fp8_f32 v6, v2, v3
	v_mul_f32_e32 v4, 0x42800000, v88
	v_mul_f32_e32 v2, 0x42800000, v92
	v_med3_f32 v3, v4, s67, v37
	v_med3_f32 v2, v2, s67, v37
	v_cvt_pk_fp8_f32 v6, v3, v2 op_sel:[0,0,1]
	v_mul_f32_e32 v2, 0x42800000, v5
	v_mul_f32_e32 v3, 0x42800000, v9
	v_med3_f32 v2, v2, s67, v37
	v_med3_f32 v3, v3, s67, v37
	v_mov_b32_e32 v5, v11
	v_cvt_pk_fp8_f32 v5, v2, v3
	v_mul_f32_e32 v4, 0x42800000, v89
	v_mul_f32_e32 v2, 0x42800000, v93
	v_med3_f32 v3, v4, s67, v37
	v_med3_f32 v2, v2, s67, v37
	v_cvt_pk_fp8_f32 v5, v3, v2 op_sel:[0,0,1]
	ds_write2_b32 v1, v41, v39 offset0:16 offset1:24
	ds_write2_b32 v1, v42, v7 offset0:49 offset1:57
	ds_write2_b32 v1, v43, v6 offset0:82 offset1:90
	ds_write2_b32 v1, v44, v5 offset0:115 offset1:123
	s_waitcnt lgkmcnt(0)
	v_add_u32_e32 v1, v24, v25
	ds_read2_b32 v[2:3], v1 offset1:1
	ds_read2_b32 v[4:5], v1 offset0:2 offset1:3
	v_or_b32_e32 v6, s16, v20
	v_ashrrev_i32_e32 v7, 31, v6
	v_lshl_add_u64 v[38:39], v[18:19], 0, s[18:19]
	v_lshlrev_b64 v[6:7], 11, v[6:7]
	v_lshl_add_u64 v[40:41], v[38:39], 0, v[6:7]
	v_add_u32_e32 v6, 0x420, v1
	v_add_u32_e32 v8, 0x428, v1
	ds_read2_b32 v[6:7], v6 offset1:1
	ds_read2_b32 v[8:9], v8 offset1:1
	s_waitcnt lgkmcnt(2)
	global_store_dwordx4 v[40:41], v[2:5], off
	s_nop 1
	v_or_b32_e32 v2, s16, v26
	v_ashrrev_i32_e32 v3, 31, v2
	v_lshlrev_b64 v[2:3], 11, v[2:3]
	v_lshl_add_u64 v[2:3], v[38:39], 0, v[2:3]
	s_waitcnt lgkmcnt(0)
	global_store_dwordx4 v[2:3], v[6:9], off
	v_add_u32_e32 v2, 0x840, v1
	v_add_u32_e32 v4, 0x848, v1
	ds_read2_b32 v[2:3], v2 offset1:1
	ds_read2_b32 v[4:5], v4 offset1:1
	v_or_b32_e32 v6, s16, v27
	v_ashrrev_i32_e32 v7, 31, v6
	v_lshlrev_b64 v[6:7], 11, v[6:7]
	v_lshl_add_u64 v[40:41], v[38:39], 0, v[6:7]
	v_add_u32_e32 v6, 0xc60, v1
	v_add_u32_e32 v1, 0xc68, v1
	ds_read2_b32 v[6:7], v6 offset1:1
	ds_read2_b32 v[8:9], v1 offset1:1
	s_waitcnt lgkmcnt(2)
	global_store_dwordx4 v[40:41], v[2:5], off
	s_nop 1
	v_or_b32_e32 v2, s16, v28
	v_ashrrev_i32_e32 v3, 31, v2
	v_lshlrev_b64 v[2:3], 11, v[2:3]
	v_lshl_add_u64 v[2:3], v[38:39], 0, v[2:3]
	s_waitcnt lgkmcnt(0)
	global_store_dwordx4 v[2:3], v[6:9], off
	s_waitcnt lgkmcnt(0)
	s_branch .LBB0_925

; #define LAS __attribute__((address_space(3)))
; template <int YMODE, int EXTRA, bool NORM_OUT, bool XN8  , bool XIN_BF = false  , bool XOUT_BF = false  > ...
;     ...
;     for (int blk = blockIdx.x; blk < M / 64; blk += F.G) {
;         const int b = (blk * 64) / SEQ;
;         __syncthreads();
;         { const int col = 4 * F.tid;
;             if (YMODE) { const f32x4 g = *(const f32x4*)(gt + (size_t)b * 6 * D + col), p = *(const f32x4*)(gpost + col); *(LAS f32x4*)(vA + col) = g * p; }
;             if (NORM_OUT) { const f32x4 g = *(const f32x4*)(gpre + col), s = *(const f32x4*)(sc + (size_t)b * 6 * D + col); *(LAS f32x4*)(vB + col) = g * (1.f + s); *(LAS f32x4*)(vC + col) = *(const f32x4*)(sh + (size_t)b * 6 * D + col); } }
;         __syncthreads();
;         f32x4 xr[8]; u32x2 xrb[8], yr[8], yr2[8]; float w1n = 0.f, w2n = 0.f;
;     ...
;         RP_LOAD(0);
.LBB0_1083:
	s_ashr_i32 s11, s10, 31
	s_lshr_b32 s8, s11, 27
	s_add_i32 s8, s10, s8
	s_ashr_i32 s8, s8, 5
	s_mul_i32 s8, s8, 6
	s_ashr_i32 s9, s8, 31
	s_lshl_b64 s[8:9], s[8:9], 13
	v_lshl_add_u64 v[6:7], v[68:69], 0, s[8:9]
	s_barrier
	global_load_dwordx4 v[2:5], v[70:71], off
	s_nop 0
	global_load_dwordx4 v[6:9], v[6:7], off
	v_lshl_add_u64 v[10:11], v[74:75], 0, s[8:9]
	v_lshl_add_u64 v[14:15], v[76:77], 0, s[8:9]
	global_load_dwordx4 v[10:13], v[10:11], off
	s_nop 0
	global_load_dwordx4 v[14:17], v[14:15], off
	s_lshl_b64 s[12:13], s[10:11], 6
	s_add_u32 s11, s12, s18
	s_addc_u32 s15, s13, 0
	s_and_b32 s8, s10, 7
	s_or_b32 s14, s11, s8
	s_lshl_b64 s[8:9], s[14:15], 13
	s_lshl_b64 s[16:17], s[14:15], 12
	s_mov_b32 s24, 0
	s_waitcnt vmcnt(0) lgkmcnt(0)
	v_pk_mul_f32 v[4:5], v[8:9], v[4:5]
	v_pk_mul_f32 v[2:3], v[6:7], v[2:3]
	ds_write_b128 v1, v[2:5]
	global_load_dwordx4 v[2:5], v[72:73], off
	v_pk_add_f32 v[12:13], v[12:13], 1.0 op_sel_hi:[1,0]
	v_pk_add_f32 v[10:11], v[10:11], 1.0 op_sel_hi:[1,0]
	v_lshl_add_u64 v[6:7], v[80:81], 0, s[8:9]
	v_lshl_add_u64 v[8:9], v[82:83], 0, s[16:17]
	ds_write_b128 v121, v[14:17]
	s_waitcnt vmcnt(0) lgkmcnt(0)
	v_pk_mul_f32 v[4:5], v[4:5], v[12:13]
	v_pk_mul_f32 v[2:3], v[2:3], v[10:11]
	ds_write_b128 v120, v[2:5]
	v_add_co_u32_e32 v2, vcc, s19, v6
	s_waitcnt lgkmcnt(0)
	s_barrier
	global_load_dwordx2 v[110:111], v[8:9], off offset:2048 nt
	global_load_dwordx2 v[108:109], v[8:9], off offset:2560 nt
	global_load_dwordx2 v[106:107], v[8:9], off offset:3072 nt
	global_load_dwordx2 v[104:105], v[8:9], off offset:3584 nt
	global_load_dwordx2 v[118:119], v[8:9], off nt
	global_load_dwordx2 v[116:117], v[8:9], off offset:512 nt
	global_load_dwordx2 v[114:115], v[8:9], off offset:1024 nt
	global_load_dwordx2 v[112:113], v[8:9], off offset:1536 nt
	v_addc_co_u32_e32 v3, vcc, 0, v7, vcc
	global_load_dwordx4 v[62:65], v[6:7], off nt
	global_load_dwordx4 v[58:61], v[6:7], off offset:1024 nt
	global_load_dwordx4 v[54:57], v[6:7], off offset:2048 nt
	global_load_dwordx4 v[50:53], v[6:7], off offset:3072 nt
	global_load_dwordx4 v[46:49], v[2:3], off nt
	global_load_dwordx4 v[42:45], v[2:3], off offset:1024 nt
	global_load_dwordx4 v[38:41], v[2:3], off offset:2048 nt
	global_load_dwordx4 v[34:37], v[2:3], off offset:3072 nt
	s_waitcnt vmcnt(0)
	v_mov_b64_e32 v[94:95], v[110:111]
	v_mov_b64_e32 v[92:93], v[108:109]
	v_mov_b64_e32 v[90:91], v[106:107]
	s_waitcnt lgkmcnt(0)
	v_mov_b64_e32 v[2:3], v[62:63]
	v_mov_b64_e32 v[6:7], v[58:59]
	v_mov_b64_e32 v[10:11], v[54:55]
	v_mov_b64_e32 v[14:15], v[50:51]
	v_mov_b64_e32 v[18:19], v[46:47]
	v_mov_b64_e32 v[22:23], v[42:43]
	v_mov_b64_e32 v[26:27], v[38:39]
	v_mov_b64_e32 v[30:31], v[34:35]
	v_mov_b64_e32 v[88:89], v[104:105]
	v_mov_b64_e32 v[96:97], v[112:113]
	v_mov_b64_e32 v[98:99], v[114:115]
	v_mov_b64_e32 v[100:101], v[116:117]
	v_mov_b64_e32 v[102:103], v[118:119]
	v_mov_b64_e32 v[4:5], v[64:65]
	v_mov_b64_e32 v[8:9], v[60:61]
	v_mov_b64_e32 v[12:13], v[56:57]
	v_mov_b64_e32 v[16:17], v[52:53]
	v_mov_b64_e32 v[20:21], v[48:49]
	v_mov_b64_e32 v[24:25], v[44:45]
	v_mov_b64_e32 v[28:29], v[40:41]
	v_mov_b64_e32 v[32:33], v[36:37]
	s_branch .LBB0_1085

; __device__ __forceinline__ float bflo(unsigned u) { return __uint_as_float(u << 16); }
; __device__ __forceinline__ float bfhi(unsigned u) { return __uint_as_float(u & 0xffff0000u); }
; template <int YMODE, int EXTRA, bool NORM_OUT, bool XN8  , bool XIN_BF = false  , bool XOUT_BF = false  > ...
;     ...
;         RP_LOAD(0);
; #pragma unroll 1
;         for (int rr = 0; rr < 8; ++rr) {
;             const int rl = F.wave * 8 + ((rr + blk) & 7); const size_t row = (size_t)blk * 64 + rl;
;             asm volatile("" ::: "memory");
;             f32x4 x[8];
; #pragma unroll
;             for (int j = 0; j < 8; ++j) x[j] = XIN_BF ? (f32x4){bflo(xrb[j].x), bfhi(xrb[j].x), bflo(xrb[j].y), bfhi(xrb[j].y)} : xr[j];
;             f32x4 y[8];
;             if (YMODE == 1) {
; #pragma unroll
;                 for (int j = 0; j < 8; ++j) y[j] = (f32x4){bflo(yr[j].x), bfhi(yr[j].x), bflo(yr[j].y), bfhi(yr[j].y)};
;             }
;             if (YMODE == 2) {
; #pragma unroll
;                 for (int j = 0; j < 8; ++j) y[j] = (f32x4){bflo(yr[j].x), bfhi(yr[j].x), bflo(yr[j].y), bfhi(yr[j].y)} * w1n + (f32x4){bflo(yr2[j].x), bfhi(yr2[j].x), bflo(yr2[j].y), bfhi(yr2[j].y)} * w2n;
;             }
;             if (rr < 7) RP_LOAD(rr + 1);
.LBB0_1085:
	s_add_i32 s8, s10, s24
	s_cmp_eq_u32 s24, 7
	s_cbranch_scc1 .LBB0_1087
	s_add_i32 s9, s8, 1
	s_and_b32 s9, s9, 7
	s_or_b32 s14, s11, s9
	s_lshl_b64 s[16:17], s[14:15], 13
	v_lshl_add_u64 v[18:19], v[80:81], 0, s[16:17]
	v_add_co_u32_e32 v30, vcc, 0x1000, v18
	s_lshl_b64 s[16:17], s[14:15], 12
	s_nop 0
	v_addc_co_u32_e32 v31, vcc, 0, v19, vcc
	v_lshl_add_u64 v[88:89], v[82:83], 0, s[16:17]
	global_load_dwordx4 v[2:5], v[18:19], off nt
	global_load_dwordx4 v[6:9], v[18:19], off offset:1024 nt
	global_load_dwordx4 v[10:13], v[18:19], off offset:2048 nt
	global_load_dwordx4 v[14:17], v[18:19], off offset:3072 nt
	s_nop 0
	global_load_dwordx4 v[18:21], v[30:31], off nt
	global_load_dwordx4 v[22:25], v[30:31], off offset:1024 nt
	global_load_dwordx4 v[26:29], v[30:31], off offset:2048 nt
	s_nop 0
	global_load_dwordx4 v[30:33], v[30:31], off offset:3072 nt
	s_nop 0
	global_load_dwordx2 v[102:103], v[88:89], off nt
	global_load_dwordx2 v[100:101], v[88:89], off offset:512 nt
	global_load_dwordx2 v[98:99], v[88:89], off offset:1024 nt
	global_load_dwordx2 v[96:97], v[88:89], off offset:1536 nt
	global_load_dwordx2 v[94:95], v[88:89], off offset:2048 nt
	global_load_dwordx2 v[92:93], v[88:89], off offset:2560 nt
	global_load_dwordx2 v[90:91], v[88:89], off offset:3072 nt
	s_nop 0
	global_load_dwordx2 v[88:89], v[88:89], off offset:3584 nt

; #define LAS __attribute__((address_space(3)))
; template <int YMODE, int EXTRA, bool NORM_OUT, bool XN8  , bool XIN_BF = false  , bool XOUT_BF = false  > ...
;     ...
;     for (int blk = blockIdx.x; blk < M / 64; blk += F.G) {
;         const int b = (blk * 64) / SEQ;
;         __syncthreads();
;         { const int col = 4 * F.tid;
;             if (YMODE) { const f32x4 g = *(const f32x4*)(gt + (size_t)b * 6 * D + col), p = *(const f32x4*)(gpost + col); *(LAS f32x4*)(vA + col) = g * p; }
;             if (NORM_OUT) { const f32x4 g = *(const f32x4*)(gpre + col), s = *(const f32x4*)(sc + (size_t)b * 6 * D + col); *(LAS f32x4*)(vB + col) = g * (1.f + s); *(LAS f32x4*)(vC + col) = *(const f32x4*)(sh + (size_t)b * 6 * D + col); } }
;         __syncthreads();
;         f32x4 xr[8]; u32x2 xrb[8], yr[8], yr2[8]; float w1n = 0.f, w2n = 0.f;
;     ...
;         RP_LOAD(0);
.LBB0_1304:
	s_ashr_i32 s1, s0, 31
	s_lshr_b32 s26, s1, 27
	s_add_i32 s26, s0, s26
	s_ashr_i32 s26, s26, 5
	s_mul_i32 s26, s26, 6
	s_ashr_i32 s27, s26, 31
	s_lshl_b64 s[26:27], s[26:27], 13
	v_lshl_add_u64 v[30:31], v[4:5], 0, s[26:27]
	s_waitcnt lgkmcnt(0)
	s_barrier
	global_load_dwordx4 v[26:29], v[6:7], off
	s_nop 0
	global_load_dwordx4 v[30:33], v[30:31], off
	v_lshl_add_u64 v[34:35], v[10:11], 0, s[26:27]
	v_lshl_add_u64 v[38:39], v[12:13], 0, s[26:27]
	global_load_dwordx4 v[34:37], v[34:35], off
	s_nop 0
	global_load_dwordx4 v[38:41], v[38:39], off
	s_lshl_b64 s[30:31], s[0:1], 6
	s_add_u32 s1, s30, s40
	s_addc_u32 s35, s31, 0
	s_and_b32 s26, s0, 7
	s_or_b32 s34, s1, s26
	s_lshl_b64 s[26:27], s[34:35], 12
	s_mov_b32 s57, 0
	s_waitcnt vmcnt(0) lgkmcnt(0)
	v_pk_mul_f32 v[28:29], v[32:33], v[28:29]
	v_pk_mul_f32 v[26:27], v[30:31], v[26:27]
	ds_write_b128 v100, v[26:29]
	global_load_dwordx4 v[26:29], v[8:9], off
	v_pk_add_f32 v[36:37], v[36:37], 1.0 op_sel_hi:[1,0]
	v_pk_add_f32 v[34:35], v[34:35], 1.0 op_sel_hi:[1,0]
	v_lshl_add_u64 v[32:33], v[16:17], 0, s[26:27]
	v_lshl_add_u64 v[30:31], v[14:15], 0, s[26:27]
	ds_write_b128 v102, v[38:41]
	s_waitcnt vmcnt(0) lgkmcnt(0)
	v_pk_mul_f32 v[28:29], v[28:29], v[36:37]
	v_pk_mul_f32 v[26:27], v[26:27], v[34:35]
	ds_write_b128 v101, v[26:29]
	s_waitcnt lgkmcnt(0)
	s_barrier
	global_load_dwordx2 v[88:89], v[32:33], off nt
	global_load_dwordx2 v[84:85], v[32:33], off offset:512 nt
	global_load_dwordx2 v[82:83], v[32:33], off offset:1024 nt
	global_load_dwordx2 v[80:81], v[32:33], off offset:1536 nt
	global_load_dwordx2 v[78:79], v[32:33], off offset:2048 nt
	global_load_dwordx2 v[76:77], v[32:33], off offset:2560 nt
	global_load_dwordx2 v[70:71], v[32:33], off offset:3072 nt
	global_load_dwordx2 v[68:69], v[32:33], off offset:3584 nt
	global_load_dwordx2 v[86:87], v[30:31], off nt
	global_load_dwordx2 v[74:75], v[30:31], off offset:512 nt
	global_load_dwordx2 v[72:73], v[30:31], off offset:1024 nt
	global_load_dwordx2 v[66:67], v[30:31], off offset:1536 nt
	global_load_dwordx2 v[64:65], v[30:31], off offset:2048 nt
	global_load_dwordx2 v[58:59], v[30:31], off offset:2560 nt
	global_load_dwordx2 v[60:61], v[30:31], off offset:3072 nt
	global_load_dwordx2 v[62:63], v[30:31], off offset:3584 nt
	s_waitcnt vmcnt(15)
	v_mov_b64_e32 v[28:29], v[88:89]
	s_waitcnt vmcnt(14)
	v_mov_b64_e32 v[32:33], v[84:85]
	s_waitcnt vmcnt(13)
	v_mov_b64_e32 v[36:37], v[82:83]
	s_waitcnt vmcnt(12)
	v_mov_b64_e32 v[40:41], v[80:81]
	s_waitcnt vmcnt(11)
	v_mov_b64_e32 v[44:45], v[78:79]
	s_waitcnt vmcnt(10)
	v_mov_b64_e32 v[48:49], v[76:77]
	s_waitcnt vmcnt(9)
	v_mov_b64_e32 v[52:53], v[70:71]
	s_waitcnt vmcnt(8)
	v_mov_b64_e32 v[56:57], v[68:69]
	s_waitcnt vmcnt(7)
	v_mov_b64_e32 v[26:27], v[86:87]
	s_waitcnt vmcnt(6)
	v_mov_b64_e32 v[30:31], v[74:75]
	s_waitcnt vmcnt(5)
	v_mov_b64_e32 v[34:35], v[72:73]
	s_waitcnt vmcnt(4)
	v_mov_b64_e32 v[38:39], v[66:67]
	s_waitcnt vmcnt(3)
	v_mov_b64_e32 v[42:43], v[64:65]
	s_waitcnt vmcnt(2)
	v_mov_b64_e32 v[46:47], v[58:59]
	s_waitcnt vmcnt(1)
	v_mov_b64_e32 v[50:51], v[60:61]
	s_waitcnt vmcnt(0)
	v_mov_b64_e32 v[54:55], v[62:63]
	s_branch .LBB0_1307

; __device__ __forceinline__ float wave_max(float v) { return lane63(scan64<true>(v)); }
; template <int YMODE, int EXTRA, bool NORM_OUT, bool XN8  , bool XIN_BF = false  , bool XOUT_BF = false  > ...
;     ...
;                 if (XN8) {
;                     float am = 0.f;
; #pragma unroll
;                     for (int j = 0; j < 8; ++j) am = fmaxf(fmaxf(am, fmaxf(fabsf(x[j][0]), fabsf(x[j][1]))), fmaxf(fabsf(x[j][2]), fabsf(x[j][3])));
;                     am = wave_max(am);
;                     const float inv = am > 0.f ? 127.f / am : 0.f;
;                     if (F.lane == 0) { rowmax[row] = am; if (EXTRA == 2) route[384 + rl] = am; }
; #pragma unroll
;                     for (int j = 0; j < 8; ++j) *(unsigned*)((unsigned char*)XN + row * D + 256 * j + 4 * F.lane) = pack_i8x4(x[j][0] * inv, x[j][1] * inv, x[j][2] * inv, x[j][3] * inv);
.LBB0_1311:
	s_or_b64 exec, exec, s[26:27]
	v_div_scale_f32 v1, s[26:27], s34, s34, v110
	v_rcp_f32_e32 v25, v1
	v_mov_b32_e32 v90, s34
	s_mov_b32 s26, 0x42fe0000
	v_div_scale_f32 v90, vcc, s26, v90, s26
	v_fma_f32 v91, -v1, v25, 1.0
	v_fmac_f32_e32 v25, v91, v25
	v_mul_f32_e32 v91, v90, v25
	v_fma_f32 v92, -v1, v91, v90
	v_fmac_f32_e32 v91, v92, v25
	v_fma_f32 v1, -v1, v91, v90
	v_div_fmas_f32 v1, v1, v25, v91
	v_div_fixup_f32 v1, v1, s34, v110
	v_cmp_gt_f32_e64 vcc, s34, 0
	s_lshl_b64 s[26:27], s[36:37], 11
	v_lshl_add_u64 v[94:95], v[22:23], 0, s[26:27]
	v_cndmask_b32_e32 v1, 0, v1, vcc
	v_mul_f32_e32 v90, v85, v1
	v_mul_f32_e32 v25, v84, v1
	v_mul_f32_e32 v91, v72, v1
	v_mul_f32_e32 v92, v73, v1
	v_med3_f32 v90, v90, s42, v110
	v_med3_f32 v25, v25, s42, v110
	v_rndne_f32_e32 v90, v90
	v_med3_f32 v91, v91, s42, v110
	v_med3_f32 v92, v92, s42, v110
	v_rndne_f32_e32 v25, v25
	v_cvt_i32_f32_e32 v90, v90
	v_rndne_f32_e32 v91, v91
	v_rndne_f32_e32 v92, v92
	v_cvt_i32_f32_e32 v25, v25
	v_cvt_i32_f32_sdwa v91, v91 dst_sel:WORD_1 dst_unused:UNUSED_PAD src0_sel:DWORD
	v_cvt_i32_f32_e32 v92, v92
	v_lshlrev_b32_e32 v90, 8, v90
	v_and_b32_e32 v90, 0xff00, v90
	v_and_b32_e32 v91, 0xff0000, v91
	v_perm_b32 v25, v92, v25, s43
	v_or3_b32 v25, v25, v90, v91
	v_mul_f32_e32 v90, v89, v1
	global_store_dword v[94:95], v25, off
	v_mul_f32_e32 v25, v88, v1
	v_mul_f32_e32 v91, v62, v1
	v_mul_f32_e32 v92, v63, v1
	v_med3_f32 v90, v90, s42, v110
	v_med3_f32 v25, v25, s42, v110
	v_rndne_f32_e32 v90, v90
	v_med3_f32 v91, v91, s42, v110
	v_med3_f32 v92, v92, s42, v110
	v_rndne_f32_e32 v25, v25
	v_cvt_i32_f32_e32 v90, v90
	v_rndne_f32_e32 v91, v91
	v_rndne_f32_e32 v92, v92
	v_cvt_i32_f32_e32 v25, v25
	v_cvt_i32_f32_sdwa v91, v91 dst_sel:WORD_1 dst_unused:UNUSED_PAD src0_sel:DWORD
	v_cvt_i32_f32_e32 v92, v92
	v_lshlrev_b32_e32 v90, 8, v90
	v_and_b32_e32 v90, 0xff00, v90
	v_and_b32_e32 v91, 0xff0000, v91
	v_perm_b32 v25, v92, v25, s43
	v_or3_b32 v25, v25, v90, v91
	v_mul_f32_e32 v90, v81, v1
	global_store_dword v[94:95], v25, off offset:256
	v_mul_f32_e32 v25, v80, v1
	v_mul_f32_e32 v91, v70, v1
	v_mul_f32_e32 v92, v71, v1
	v_med3_f32 v90, v90, s42, v110
	v_med3_f32 v25, v25, s42, v110
	v_rndne_f32_e32 v90, v90
	v_med3_f32 v91, v91, s42, v110
	v_med3_f32 v92, v92, s42, v110
	v_rndne_f32_e32 v25, v25
	v_cvt_i32_f32_e32 v90, v90
	v_rndne_f32_e32 v91, v91
	v_rndne_f32_e32 v92, v92
	v_cvt_i32_f32_e32 v25, v25
	v_cvt_i32_f32_sdwa v91, v91 dst_sel:WORD_1 dst_unused:UNUSED_PAD src0_sel:DWORD
	v_cvt_i32_f32_e32 v92, v92
	v_lshlrev_b32_e32 v90, 8, v90
	v_and_b32_e32 v90, 0xff00, v90
	v_and_b32_e32 v91, 0xff0000, v91
	v_perm_b32 v25, v92, v25, s43
	v_or3_b32 v25, v25, v90, v91
	v_mul_f32_e32 v90, v87, v1
	global_store_dword v[94:95], v25, off offset:512
	v_mul_f32_e32 v25, v86, v1
	v_mul_f32_e32 v91, v60, v1
	v_mul_f32_e32 v92, v61, v1
	v_med3_f32 v90, v90, s42, v110
	v_med3_f32 v25, v25, s42, v110
	v_rndne_f32_e32 v90, v90
	v_med3_f32 v91, v91, s42, v110
	v_med3_f32 v92, v92, s42, v110
	v_rndne_f32_e32 v25, v25
	v_cvt_i32_f32_e32 v90, v90
	v_rndne_f32_e32 v91, v91
	v_rndne_f32_e32 v92, v92
	v_cvt_i32_f32_e32 v25, v25
	v_cvt_i32_f32_sdwa v91, v91 dst_sel:WORD_1 dst_unused:UNUSED_PAD src0_sel:DWORD
	v_cvt_i32_f32_e32 v92, v92
	v_lshlrev_b32_e32 v90, 8, v90
	v_and_b32_e32 v90, 0xff00, v90
	v_and_b32_e32 v91, 0xff0000, v91
	v_perm_b32 v25, v92, v25, s43
	v_or3_b32 v25, v25, v90, v91
	v_mul_f32_e32 v90, v77, v1
	global_store_dword v[94:95], v25, off offset:768
	v_mul_f32_e32 v25, v76, v1
	v_mul_f32_e32 v91, v68, v1
	v_mul_f32_e32 v92, v69, v1
	v_med3_f32 v90, v90, s42, v110
	v_med3_f32 v25, v25, s42, v110
	v_rndne_f32_e32 v90, v90
	v_med3_f32 v91, v91, s42, v110
	v_med3_f32 v92, v92, s42, v110
	v_rndne_f32_e32 v25, v25
	v_cvt_i32_f32_e32 v90, v90
	v_rndne_f32_e32 v91, v91
	v_rndne_f32_e32 v92, v92
	v_cvt_i32_f32_e32 v25, v25
	v_cvt_i32_f32_sdwa v91, v91 dst_sel:WORD_1 dst_unused:UNUSED_PAD src0_sel:DWORD
	v_cvt_i32_f32_e32 v92, v92
	v_lshlrev_b32_e32 v90, 8, v90
	v_and_b32_e32 v90, 0xff00, v90
	v_and_b32_e32 v91, 0xff0000, v91
	v_perm_b32 v25, v92, v25, s43
	v_or3_b32 v25, v25, v90, v91
	v_mul_f32_e32 v90, v83, v1
	global_store_dword v[94:95], v25, off offset:1024
	v_mul_f32_e32 v25, v82, v1
	v_mul_f32_e32 v91, v58, v1
	v_mul_f32_e32 v92, v59, v1
	v_med3_f32 v90, v90, s42, v110
	v_med3_f32 v25, v25, s42, v110
	v_rndne_f32_e32 v90, v90
	v_med3_f32 v91, v91, s42, v110
	v_med3_f32 v92, v92, s42, v110
	v_rndne_f32_e32 v25, v25
	v_cvt_i32_f32_e32 v90, v90
	v_rndne_f32_e32 v91, v91
	v_rndne_f32_e32 v92, v92
	v_cvt_i32_f32_e32 v25, v25
	v_cvt_i32_f32_sdwa v91, v91 dst_sel:WORD_1 dst_unused:UNUSED_PAD src0_sel:DWORD
	v_cvt_i32_f32_e32 v92, v92
	v_lshlrev_b32_e32 v90, 8, v90
	v_and_b32_e32 v90, 0xff00, v90
	v_and_b32_e32 v91, 0xff0000, v91
	v_perm_b32 v25, v92, v25, s43
	v_or3_b32 v25, v25, v90, v91
	v_mul_f32_e32 v90, v75, v1
	global_store_dword v[94:95], v25, off offset:1280
	v_mul_f32_e32 v25, v74, v1
	v_mul_f32_e32 v91, v64, v1
	v_mul_f32_e32 v92, v65, v1
	v_med3_f32 v90, v90, s42, v110
	v_med3_f32 v25, v25, s42, v110
	v_rndne_f32_e32 v90, v90
	v_med3_f32 v91, v91, s42, v110
	v_med3_f32 v92, v92, s42, v110
	v_rndne_f32_e32 v25, v25
	v_cvt_i32_f32_e32 v90, v90
	v_rndne_f32_e32 v91, v91
	v_rndne_f32_e32 v92, v92
	v_cvt_i32_f32_e32 v25, v25
	v_cvt_i32_f32_sdwa v91, v91 dst_sel:WORD_1 dst_unused:UNUSED_PAD src0_sel:DWORD
	v_cvt_i32_f32_e32 v92, v92
	v_lshlrev_b32_e32 v90, 8, v90
	v_and_b32_e32 v90, 0xff00, v90
	v_and_b32_e32 v91, 0xff0000, v91
	v_perm_b32 v25, v92, v25, s43
	v_or3_b32 v25, v25, v90, v91
	v_mul_f32_e32 v90, v79, v1
	global_store_dword v[94:95], v25, off offset:1536
	v_mul_f32_e32 v25, v78, v1
	v_mul_f32_e32 v91, v66, v1
	v_mul_f32_e32 v1, v67, v1
	v_med3_f32 v90, v90, s42, v110
	v_med3_f32 v25, v25, s42, v110
	v_rndne_f32_e32 v90, v90
	v_med3_f32 v91, v91, s42, v110
	v_med3_f32 v1, v1, s42, v110
	v_rndne_f32_e32 v25, v25
	v_cvt_i32_f32_e32 v90, v90
	v_rndne_f32_e32 v91, v91
	v_rndne_f32_e32 v1, v1
	v_cvt_i32_f32_e32 v25, v25
	v_cvt_i32_f32_sdwa v91, v91 dst_sel:WORD_1 dst_unused:UNUSED_PAD src0_sel:DWORD
	v_cvt_i32_f32_e32 v1, v1
	v_lshlrev_b32_e32 v90, 8, v90
	v_and_b32_e32 v96, 0xff00, v90
	v_and_b32_e32 v97, 0xff0000, v91
	ds_read_b128 v[90:93], v105
	v_perm_b32 v1, v1, v25, s43
	v_or3_b32 v1, v1, v96, v97
	global_store_dword v[94:95], v1, off offset:1792
	ds_read_b128 v[94:97], v105 offset:1024
	s_waitcnt lgkmcnt(1)
; #define LAS __attribute__((address_space(3)))
; #define SCAN_STEP(ctrl, rm) { const float tf = __int_as_float(__builtin_amdgcn_update_dpp(ident, __float_as_int(v), ctrl, rm, 0xf, false)); v = MAX ? fmaxf(v, tf) : v + tf; }
; template <bool MAX>
; __device__ __forceinline__ float scan64(float v) {
;     constexpr int ident = MAX ? (int)0xff800000 : 0;
;     ...
;     SCAN_STEP(0x111, 0xf) SCAN_STEP(0x112, 0xf) SCAN_STEP(0x114, 0xf) SCAN_STEP(0x118, 0xf) SCAN_STEP(0x142, 0xa) SCAN_STEP(0x143, 0xc)
;     ...
;     return v;
; }
; __device__ __forceinline__ float lane63(float v) { return __int_as_float(__builtin_amdgcn_readlane(__float_as_int(v), 63)); }
; __device__ __forceinline__ float wave_sum(float v) { return lane63(scan64<false>(v)); }
; template <int YMODE, int EXTRA, bool NORM_OUT, bool XN8  , bool XIN_BF = false  , bool XOUT_BF = false  > ...
;     ...
;                 if (EXTRA) {
;                     float d8[8];
; #pragma unroll
;                     for (int e = 0; e < 8; ++e) { float s = 0.f;
; #pragma unroll
;                         for (int j = 0; j < 8; ++j) { const f32x4 w = *(const LAS f32x4*)(we + e * D + 256 * j + 4 * F.lane); s += (x[j][0] * w[0] + x[j][1] * w[1]) + (x[j][2] * w[2] + x[j][3] * w[3]); }
;                         d8[e] = wave_sum(s); asm volatile("" ::: "memory"); }
	v_mul_f32_e32 v1, v85, v91
	v_mul_f32_e32 v25, v73, v93
	v_fmac_f32_e32 v1, v84, v90
	v_fmac_f32_e32 v25, v72, v92
	ds_read_b128 v[90:93], v105 offset:2048
	v_add_f32_e32 v1, v1, v25
	s_waitcnt lgkmcnt(1)
	v_mul_f32_e32 v25, v89, v95
	v_fmac_f32_e32 v25, v88, v94
	v_mul_f32_e32 v94, v63, v97
	v_fmac_f32_e32 v94, v62, v96
	v_add_f32_e32 v1, 0, v1
	v_add_f32_e32 v25, v25, v94
	ds_read_b128 v[94:97], v105 offset:3072
	v_add_f32_e32 v1, v1, v25
	s_waitcnt lgkmcnt(1)
	v_mul_f32_e32 v25, v81, v91
	v_fmac_f32_e32 v25, v80, v90
	v_mul_f32_e32 v90, v71, v93
	v_fmac_f32_e32 v90, v70, v92
	v_add_f32_e32 v25, v25, v90
	ds_read_b128 v[90:93], v105 offset:4096
	v_add_f32_e32 v1, v1, v25
	s_waitcnt lgkmcnt(1)
	v_mul_f32_e32 v25, v87, v95
	v_fmac_f32_e32 v25, v86, v94
	v_mul_f32_e32 v94, v61, v97
	v_fmac_f32_e32 v94, v60, v96
	v_add_f32_e32 v25, v25, v94
	ds_read_b128 v[94:97], v105 offset:5120
	v_add_f32_e32 v1, v1, v25
	s_waitcnt lgkmcnt(1)
	v_mul_f32_e32 v25, v77, v91
	v_fmac_f32_e32 v25, v76, v90
	v_mul_f32_e32 v90, v69, v93
	v_fmac_f32_e32 v90, v68, v92
	v_add_f32_e32 v25, v25, v90
	ds_read_b128 v[90:93], v105 offset:6144
	v_add_f32_e32 v1, v1, v25
	s_waitcnt lgkmcnt(1)
	v_mul_f32_e32 v25, v83, v95
	v_fmac_f32_e32 v25, v82, v94
	v_mul_f32_e32 v94, v59, v97
	v_fmac_f32_e32 v94, v58, v96
	v_add_f32_e32 v25, v25, v94
	ds_read_b128 v[94:97], v105 offset:7168
	v_add_f32_e32 v1, v1, v25
	s_waitcnt lgkmcnt(1)
	v_mul_f32_e32 v25, v75, v91
	v_fmac_f32_e32 v25, v74, v90
	v_mul_f32_e32 v90, v65, v93
	v_fmac_f32_e32 v90, v64, v92
	v_add_f32_e32 v25, v25, v90
	v_add_f32_e32 v1, v1, v25
	s_waitcnt lgkmcnt(0)
	v_mul_f32_e32 v25, v79, v95
	v_mul_f32_e32 v90, v67, v97
	v_fmac_f32_e32 v25, v78, v94
	v_fmac_f32_e32 v90, v66, v96
	v_add_f32_e32 v25, v25, v90
	v_add_f32_e32 v1, v1, v25
	v_mov_b32_e32 v25, 0
	ds_read_b128 v[90:93], v105 offset:8192
	ds_read_b128 v[94:97], v105 offset:9216
	v_add_f32_dpp v1, v1, v1 row_shr:1 row_mask:0xf bank_mask:0xf bound_ctrl:1
	s_nop 1
	v_add_f32_dpp v1, v1, v1 row_shr:2 row_mask:0xf bank_mask:0xf bound_ctrl:1
	s_nop 1
	v_add_f32_dpp v1, v1, v1 row_shr:4 row_mask:0xf bank_mask:0xf bound_ctrl:1
	s_nop 1
	v_add_f32_dpp v1, v1, v1 row_shr:8 row_mask:0xf bank_mask:0xf bound_ctrl:1
	s_nop 1
	v_mov_b32_dpp v25, v1 row_bcast:15 row_mask:0xa bank_mask:0xf
	v_add_f32_e32 v1, v1, v25
	v_mov_b32_e32 v25, 0
	s_nop 1
	v_mov_b32_dpp v25, v1 row_bcast:31 row_mask:0xc bank_mask:0xf
	v_add_f32_e32 v1, v1, v25
	s_waitcnt lgkmcnt(1)
	v_mul_f32_e32 v25, v73, v93
	v_readlane_b32 s34, v1, 63
	v_mul_f32_e32 v1, v85, v91
	v_fmac_f32_e32 v1, v84, v90
	v_fmac_f32_e32 v25, v72, v92
	ds_read_b128 v[90:93], v105 offset:10240
	v_add_f32_e32 v1, v1, v25
	s_waitcnt lgkmcnt(1)
	v_mul_f32_e32 v25, v89, v95
	v_fmac_f32_e32 v25, v88, v94
	v_mul_f32_e32 v94, v63, v97
	v_fmac_f32_e32 v94, v62, v96
	v_add_f32_e32 v1, 0, v1
	v_add_f32_e32 v25, v25, v94
	ds_read_b128 v[94:97], v105 offset:11264
	v_add_f32_e32 v1, v1, v25
	s_waitcnt lgkmcnt(1)
	v_mul_f32_e32 v25, v81, v91
	v_fmac_f32_e32 v25, v80, v90
	v_mul_f32_e32 v90, v71, v93
	v_fmac_f32_e32 v90, v70, v92
	v_add_f32_e32 v25, v25, v90
	ds_read_b128 v[90:93], v105 offset:12288
	v_add_f32_e32 v1, v1, v25
	s_waitcnt lgkmcnt(1)
	v_mul_f32_e32 v25, v87, v95
	v_fmac_f32_e32 v25, v86, v94
	v_mul_f32_e32 v94, v61, v97
	v_fmac_f32_e32 v94, v60, v96
	v_add_f32_e32 v25, v25, v94
	ds_read_b128 v[94:97], v105 offset:13312
	v_add_f32_e32 v1, v1, v25
	s_waitcnt lgkmcnt(1)
	v_mul_f32_e32 v25, v77, v91
	v_fmac_f32_e32 v25, v76, v90
	v_mul_f32_e32 v90, v69, v93
	v_fmac_f32_e32 v90, v68, v92
	v_add_f32_e32 v25, v25, v90
	ds_read_b128 v[90:93], v105 offset:14336
	v_add_f32_e32 v1, v1, v25
	s_waitcnt lgkmcnt(1)
	v_mul_f32_e32 v25, v83, v95
	v_fmac_f32_e32 v25, v82, v94
	v_mul_f32_e32 v94, v59, v97
	v_fmac_f32_e32 v94, v58, v96
	v_add_f32_e32 v25, v25, v94
	ds_read_b128 v[94:97], v105 offset:15360
	v_add_f32_e32 v1, v1, v25
	s_waitcnt lgkmcnt(1)
	v_mul_f32_e32 v25, v75, v91
	v_fmac_f32_e32 v25, v74, v90
	v_mul_f32_e32 v90, v65, v93
	v_fmac_f32_e32 v90, v64, v92
	v_add_f32_e32 v25, v25, v90
	v_add_f32_e32 v1, v1, v25
	s_waitcnt lgkmcnt(0)
	v_mul_f32_e32 v25, v79, v95
	v_mul_f32_e32 v90, v67, v97
	v_fmac_f32_e32 v25, v78, v94
	v_fmac_f32_e32 v90, v66, v96
	v_add_f32_e32 v25, v25, v90
	v_add_f32_e32 v1, v1, v25
	v_mov_b32_e32 v25, 0
	ds_read_b128 v[90:93], v105 offset:16384
	ds_read_b128 v[94:97], v105 offset:17408
	v_add_f32_dpp v1, v1, v1 row_shr:1 row_mask:0xf bank_mask:0xf bound_ctrl:1
	s_nop 1
	v_add_f32_dpp v1, v1, v1 row_shr:2 row_mask:0xf bank_mask:0xf bound_ctrl:1
	s_nop 1
	v_add_f32_dpp v1, v1, v1 row_shr:4 row_mask:0xf bank_mask:0xf bound_ctrl:1
	s_nop 1
	v_add_f32_dpp v1, v1, v1 row_shr:8 row_mask:0xf bank_mask:0xf bound_ctrl:1
	s_nop 1
	v_mov_b32_dpp v25, v1 row_bcast:15 row_mask:0xa bank_mask:0xf
	v_add_f32_e32 v1, v1, v25
	v_mov_b32_e32 v25, 0
	s_nop 1
	v_mov_b32_dpp v25, v1 row_bcast:31 row_mask:0xc bank_mask:0xf
	v_add_f32_e32 v1, v1, v25
	s_waitcnt lgkmcnt(1)
	v_mul_f32_e32 v25, v73, v93
	v_readlane_b32 s38, v1, 63
	v_mul_f32_e32 v1, v85, v91
	v_fmac_f32_e32 v1, v84, v90
	v_fmac_f32_e32 v25, v72, v92
	ds_read_b128 v[90:93], v105 offset:18432
	v_add_f32_e32 v1, v1, v25
	s_waitcnt lgkmcnt(1)
	v_mul_f32_e32 v25, v89, v95
	v_fmac_f32_e32 v25, v88, v94
	v_mul_f32_e32 v94, v63, v97
	v_fmac_f32_e32 v94, v62, v96
	v_add_f32_e32 v1, 0, v1
	v_add_f32_e32 v25, v25, v94
	ds_read_b128 v[94:97], v105 offset:19456
	v_add_f32_e32 v1, v1, v25
	s_waitcnt lgkmcnt(1)
	v_mul_f32_e32 v25, v81, v91
	v_fmac_f32_e32 v25, v80, v90
	v_mul_f32_e32 v90, v71, v93
	v_fmac_f32_e32 v90, v70, v92
	v_add_f32_e32 v25, v25, v90
	ds_read_b128 v[90:93], v105 offset:20480
	v_add_f32_e32 v1, v1, v25
	s_waitcnt lgkmcnt(1)
; #define LAS __attribute__((address_space(3)))
; __device__ __forceinline__ float wave_sum(float v) { return lane63(scan64<false>(v)); }
; template <int YMODE, int EXTRA, bool NORM_OUT, bool XN8  , bool XIN_BF = false  , bool XOUT_BF = false  > ...
;     ...
;                 if (EXTRA) {
;                     float d8[8];
; #pragma unroll
;                     for (int e = 0; e < 8; ++e) { float s = 0.f;
; #pragma unroll
;                         for (int j = 0; j < 8; ++j) { const f32x4 w = *(const LAS f32x4*)(we + e * D + 256 * j + 4 * F.lane); s += (x[j][0] * w[0] + x[j][1] * w[1]) + (x[j][2] * w[2] + x[j][3] * w[3]); }
;                         d8[e] = wave_sum(s); asm volatile("" ::: "memory"); }
	v_mul_f32_e32 v25, v87, v95
	v_fmac_f32_e32 v25, v86, v94
	v_mul_f32_e32 v94, v61, v97
	v_fmac_f32_e32 v94, v60, v96
	v_add_f32_e32 v25, v25, v94
	ds_read_b128 v[94:97], v105 offset:21504
	v_add_f32_e32 v1, v1, v25
	s_waitcnt lgkmcnt(1)
	v_mul_f32_e32 v25, v77, v91
	v_fmac_f32_e32 v25, v76, v90
	v_mul_f32_e32 v90, v69, v93
	v_fmac_f32_e32 v90, v68, v92
	v_add_f32_e32 v25, v25, v90
	ds_read_b128 v[90:93], v105 offset:22528
	v_add_f32_e32 v1, v1, v25
	s_waitcnt lgkmcnt(1)
	v_mul_f32_e32 v25, v83, v95
	v_fmac_f32_e32 v25, v82, v94
	v_mul_f32_e32 v94, v59, v97
	v_fmac_f32_e32 v94, v58, v96
	v_add_f32_e32 v25, v25, v94
	ds_read_b128 v[94:97], v105 offset:23552
	v_add_f32_e32 v1, v1, v25
	s_waitcnt lgkmcnt(1)
	v_mul_f32_e32 v25, v75, v91
	v_fmac_f32_e32 v25, v74, v90
	v_mul_f32_e32 v90, v65, v93
	v_fmac_f32_e32 v90, v64, v92
	v_add_f32_e32 v25, v25, v90
	v_add_f32_e32 v1, v1, v25
	s_waitcnt lgkmcnt(0)
	v_mul_f32_e32 v25, v79, v95
	v_mul_f32_e32 v90, v67, v97
	v_fmac_f32_e32 v25, v78, v94
	v_fmac_f32_e32 v90, v66, v96
	v_add_f32_e32 v25, v25, v90
	v_add_f32_e32 v1, v1, v25
	v_mov_b32_e32 v25, 0
	ds_read_b128 v[90:93], v105 offset:24576
	ds_read_b128 v[94:97], v105 offset:25600
	v_add_f32_dpp v1, v1, v1 row_shr:1 row_mask:0xf bank_mask:0xf bound_ctrl:1
	s_nop 1
	v_add_f32_dpp v1, v1, v1 row_shr:2 row_mask:0xf bank_mask:0xf bound_ctrl:1
	s_nop 1
	v_add_f32_dpp v1, v1, v1 row_shr:4 row_mask:0xf bank_mask:0xf bound_ctrl:1
	s_nop 1
	v_add_f32_dpp v1, v1, v1 row_shr:8 row_mask:0xf bank_mask:0xf bound_ctrl:1
	s_nop 1
	v_mov_b32_dpp v25, v1 row_bcast:15 row_mask:0xa bank_mask:0xf
	v_add_f32_e32 v1, v1, v25
	v_mov_b32_e32 v25, 0
	s_nop 1
	v_mov_b32_dpp v25, v1 row_bcast:31 row_mask:0xc bank_mask:0xf
	v_add_f32_e32 v1, v1, v25
	s_waitcnt lgkmcnt(1)
	v_mul_f32_e32 v25, v73, v93
	v_readlane_b32 s39, v1, 63
	v_mul_f32_e32 v1, v85, v91
	v_fmac_f32_e32 v1, v84, v90
	v_fmac_f32_e32 v25, v72, v92
	ds_read_b128 v[90:93], v105 offset:26624
	v_add_f32_e32 v1, v1, v25
	s_waitcnt lgkmcnt(1)
	v_mul_f32_e32 v25, v89, v95
	v_fmac_f32_e32 v25, v88, v94
	v_mul_f32_e32 v94, v63, v97
	v_fmac_f32_e32 v94, v62, v96
	v_add_f32_e32 v1, 0, v1
	v_add_f32_e32 v25, v25, v94
	ds_read_b128 v[94:97], v105 offset:27648
	v_add_f32_e32 v1, v1, v25
	s_waitcnt lgkmcnt(1)
	v_mul_f32_e32 v25, v81, v91
	v_fmac_f32_e32 v25, v80, v90
	v_mul_f32_e32 v90, v71, v93
	v_fmac_f32_e32 v90, v70, v92
	v_add_f32_e32 v25, v25, v90
	ds_read_b128 v[90:93], v105 offset:28672
	v_add_f32_e32 v1, v1, v25
	s_waitcnt lgkmcnt(1)
	v_mul_f32_e32 v25, v87, v95
	v_fmac_f32_e32 v25, v86, v94
	v_mul_f32_e32 v94, v61, v97
	v_fmac_f32_e32 v94, v60, v96
	v_add_f32_e32 v25, v25, v94
	ds_read_b128 v[94:97], v105 offset:29696
	v_add_f32_e32 v1, v1, v25
	s_waitcnt lgkmcnt(1)
	v_mul_f32_e32 v25, v77, v91
	v_fmac_f32_e32 v25, v76, v90
	v_mul_f32_e32 v90, v69, v93
	v_fmac_f32_e32 v90, v68, v92
	v_add_f32_e32 v25, v25, v90
	ds_read_b128 v[90:93], v105 offset:30720
	v_add_f32_e32 v1, v1, v25
	s_waitcnt lgkmcnt(1)
	v_mul_f32_e32 v25, v83, v95
	v_fmac_f32_e32 v25, v82, v94
	v_mul_f32_e32 v94, v59, v97
	v_fmac_f32_e32 v94, v58, v96
	v_add_f32_e32 v25, v25, v94
	ds_read_b128 v[94:97], v105 offset:31744
	v_add_f32_e32 v1, v1, v25
	s_waitcnt lgkmcnt(1)
	v_mul_f32_e32 v25, v75, v91
	v_fmac_f32_e32 v25, v74, v90
	v_mul_f32_e32 v90, v65, v93
	v_fmac_f32_e32 v90, v64, v92
	v_add_f32_e32 v25, v25, v90
	v_add_f32_e32 v1, v1, v25
	s_waitcnt lgkmcnt(0)
	v_mul_f32_e32 v25, v79, v95
	v_mul_f32_e32 v90, v67, v97
	v_fmac_f32_e32 v25, v78, v94
	v_fmac_f32_e32 v90, v66, v96
	v_add_f32_e32 v25, v25, v90
	v_add_f32_e32 v1, v1, v25
	v_mov_b32_e32 v25, 0
	ds_read_b128 v[90:93], v105 offset:32768
	ds_read_b128 v[94:97], v105 offset:33792
	v_add_f32_dpp v1, v1, v1 row_shr:1 row_mask:0xf bank_mask:0xf bound_ctrl:1
	s_nop 1
	v_add_f32_dpp v1, v1, v1 row_shr:2 row_mask:0xf bank_mask:0xf bound_ctrl:1
	s_nop 1
	v_add_f32_dpp v1, v1, v1 row_shr:4 row_mask:0xf bank_mask:0xf bound_ctrl:1
	s_nop 1
	v_add_f32_dpp v1, v1, v1 row_shr:8 row_mask:0xf bank_mask:0xf bound_ctrl:1
	s_nop 1
	v_mov_b32_dpp v25, v1 row_bcast:15 row_mask:0xa bank_mask:0xf
	v_add_f32_e32 v1, v1, v25
	v_mov_b32_e32 v25, 0
	s_nop 1
	v_mov_b32_dpp v25, v1 row_bcast:31 row_mask:0xc bank_mask:0xf
	v_add_f32_e32 v1, v1, v25
	s_waitcnt lgkmcnt(1)
	v_mul_f32_e32 v25, v73, v93
	v_readlane_b32 s62, v1, 63
	v_mul_f32_e32 v1, v85, v91
	v_fmac_f32_e32 v1, v84, v90
	v_fmac_f32_e32 v25, v72, v92
	ds_read_b128 v[90:93], v105 offset:34816
	v_add_f32_e32 v1, v1, v25
	s_waitcnt lgkmcnt(1)
	v_mul_f32_e32 v25, v89, v95
	v_fmac_f32_e32 v25, v88, v94
	v_mul_f32_e32 v94, v63, v97
	v_fmac_f32_e32 v94, v62, v96
	v_add_f32_e32 v1, 0, v1
	v_add_f32_e32 v25, v25, v94
	ds_read_b128 v[94:97], v105 offset:35840
	v_add_f32_e32 v1, v1, v25
	s_waitcnt lgkmcnt(1)
	v_mul_f32_e32 v25, v81, v91
	v_fmac_f32_e32 v25, v80, v90
	v_mul_f32_e32 v90, v71, v93
	v_fmac_f32_e32 v90, v70, v92
	v_add_f32_e32 v25, v25, v90
	ds_read_b128 v[90:93], v105 offset:36864
	v_add_f32_e32 v1, v1, v25
	s_waitcnt lgkmcnt(1)
	v_mul_f32_e32 v25, v87, v95
	v_fmac_f32_e32 v25, v86, v94
	v_mul_f32_e32 v94, v61, v97
	v_fmac_f32_e32 v94, v60, v96
	v_add_f32_e32 v25, v25, v94
	ds_read_b128 v[94:97], v105 offset:37888
	v_add_f32_e32 v1, v1, v25
	s_waitcnt lgkmcnt(1)
	v_mul_f32_e32 v25, v77, v91
	v_fmac_f32_e32 v25, v76, v90
	v_mul_f32_e32 v90, v69, v93
	v_fmac_f32_e32 v90, v68, v92
	v_add_f32_e32 v25, v25, v90
	ds_read_b128 v[90:93], v105 offset:38912
	v_add_f32_e32 v1, v1, v25
	s_waitcnt lgkmcnt(1)
	v_mul_f32_e32 v25, v83, v95
	v_fmac_f32_e32 v25, v82, v94
	v_mul_f32_e32 v94, v59, v97
	v_fmac_f32_e32 v94, v58, v96
	v_add_f32_e32 v25, v25, v94
	ds_read_b128 v[94:97], v105 offset:39936
	v_add_f32_e32 v1, v1, v25
	s_waitcnt lgkmcnt(1)
; #define LAS __attribute__((address_space(3)))
; __device__ __forceinline__ float wave_sum(float v) { return lane63(scan64<false>(v)); }
; template <int YMODE, int EXTRA, bool NORM_OUT, bool XN8  , bool XIN_BF = false  , bool XOUT_BF = false  > ...
;     ...
;                 if (EXTRA) {
;                     float d8[8];
; #pragma unroll
;                     for (int e = 0; e < 8; ++e) { float s = 0.f;
; #pragma unroll
;                         for (int j = 0; j < 8; ++j) { const f32x4 w = *(const LAS f32x4*)(we + e * D + 256 * j + 4 * F.lane); s += (x[j][0] * w[0] + x[j][1] * w[1]) + (x[j][2] * w[2] + x[j][3] * w[3]); }
;                         d8[e] = wave_sum(s); asm volatile("" ::: "memory"); }
	v_mul_f32_e32 v25, v75, v91
	v_fmac_f32_e32 v25, v74, v90
	v_mul_f32_e32 v90, v65, v93
	v_fmac_f32_e32 v90, v64, v92
	v_add_f32_e32 v25, v25, v90
	v_add_f32_e32 v1, v1, v25
	s_waitcnt lgkmcnt(0)
	v_mul_f32_e32 v25, v79, v95
	v_mul_f32_e32 v90, v67, v97
	v_fmac_f32_e32 v25, v78, v94
	v_fmac_f32_e32 v90, v66, v96
	v_add_f32_e32 v25, v25, v90
	v_add_f32_e32 v1, v1, v25
	v_mov_b32_e32 v25, 0
	ds_read_b128 v[90:93], v105 offset:40960
	ds_read_b128 v[94:97], v105 offset:41984
	v_add_f32_dpp v1, v1, v1 row_shr:1 row_mask:0xf bank_mask:0xf bound_ctrl:1
	s_nop 1
	v_add_f32_dpp v1, v1, v1 row_shr:2 row_mask:0xf bank_mask:0xf bound_ctrl:1
	s_nop 1
	v_add_f32_dpp v1, v1, v1 row_shr:4 row_mask:0xf bank_mask:0xf bound_ctrl:1
	s_nop 1
	v_add_f32_dpp v1, v1, v1 row_shr:8 row_mask:0xf bank_mask:0xf bound_ctrl:1
	s_nop 1
	v_mov_b32_dpp v25, v1 row_bcast:15 row_mask:0xa bank_mask:0xf
	v_add_f32_e32 v1, v1, v25
	v_mov_b32_e32 v25, 0
	s_nop 1
	v_mov_b32_dpp v25, v1 row_bcast:31 row_mask:0xc bank_mask:0xf
	v_add_f32_e32 v1, v1, v25
	s_waitcnt lgkmcnt(1)
	v_mul_f32_e32 v25, v73, v93
	v_readlane_b32 s63, v1, 63
	v_mul_f32_e32 v1, v85, v91
	v_fmac_f32_e32 v1, v84, v90
	v_fmac_f32_e32 v25, v72, v92
	ds_read_b128 v[90:93], v105 offset:43008
	v_add_f32_e32 v1, v1, v25
	s_waitcnt lgkmcnt(1)
	v_mul_f32_e32 v25, v89, v95
	v_fmac_f32_e32 v25, v88, v94
	v_mul_f32_e32 v94, v63, v97
	v_fmac_f32_e32 v94, v62, v96
	v_add_f32_e32 v1, 0, v1
	v_add_f32_e32 v25, v25, v94
	ds_read_b128 v[94:97], v105 offset:44032
	v_add_f32_e32 v1, v1, v25
	s_waitcnt lgkmcnt(1)
	v_mul_f32_e32 v25, v81, v91
	v_fmac_f32_e32 v25, v80, v90
	v_mul_f32_e32 v90, v71, v93
	v_fmac_f32_e32 v90, v70, v92
	v_add_f32_e32 v25, v25, v90
	ds_read_b128 v[90:93], v105 offset:45056
	v_add_f32_e32 v1, v1, v25
	s_waitcnt lgkmcnt(1)
	v_mul_f32_e32 v25, v87, v95
	v_fmac_f32_e32 v25, v86, v94
	v_mul_f32_e32 v94, v61, v97
	v_fmac_f32_e32 v94, v60, v96
	v_add_f32_e32 v25, v25, v94
	ds_read_b128 v[94:97], v105 offset:46080
	v_add_f32_e32 v1, v1, v25
	s_waitcnt lgkmcnt(1)
	v_mul_f32_e32 v25, v77, v91
	v_fmac_f32_e32 v25, v76, v90
	v_mul_f32_e32 v90, v69, v93
	v_fmac_f32_e32 v90, v68, v92
	v_add_f32_e32 v25, v25, v90
	ds_read_b128 v[90:93], v105 offset:47104
	v_add_f32_e32 v1, v1, v25
	s_waitcnt lgkmcnt(1)
	v_mul_f32_e32 v25, v83, v95
	v_fmac_f32_e32 v25, v82, v94
	v_mul_f32_e32 v94, v59, v97
	v_fmac_f32_e32 v94, v58, v96
	v_add_f32_e32 v25, v25, v94
	ds_read_b128 v[94:97], v105 offset:48128
	v_add_f32_e32 v1, v1, v25
	s_waitcnt lgkmcnt(1)
	v_mul_f32_e32 v25, v75, v91
	v_fmac_f32_e32 v25, v74, v90
	v_mul_f32_e32 v90, v65, v93
	v_fmac_f32_e32 v90, v64, v92
	v_add_f32_e32 v25, v25, v90
	v_add_f32_e32 v1, v1, v25
	s_waitcnt lgkmcnt(0)
	v_mul_f32_e32 v25, v79, v95
	v_mul_f32_e32 v90, v67, v97
	v_fmac_f32_e32 v25, v78, v94
	v_fmac_f32_e32 v90, v66, v96
	v_add_f32_e32 v25, v25, v90
	v_add_f32_e32 v1, v1, v25
	v_mov_b32_e32 v25, 0
	ds_read_b128 v[90:93], v105 offset:49152
	ds_read_b128 v[94:97], v105 offset:50176
	v_add_f32_dpp v1, v1, v1 row_shr:1 row_mask:0xf bank_mask:0xf bound_ctrl:1
	s_nop 1
	v_add_f32_dpp v1, v1, v1 row_shr:2 row_mask:0xf bank_mask:0xf bound_ctrl:1
	s_nop 1
	v_add_f32_dpp v1, v1, v1 row_shr:4 row_mask:0xf bank_mask:0xf bound_ctrl:1
	s_nop 1
	v_add_f32_dpp v1, v1, v1 row_shr:8 row_mask:0xf bank_mask:0xf bound_ctrl:1
	s_nop 1
	v_mov_b32_dpp v25, v1 row_bcast:15 row_mask:0xa bank_mask:0xf
	v_add_f32_e32 v1, v1, v25
	v_mov_b32_e32 v25, 0
	s_nop 1
	v_mov_b32_dpp v25, v1 row_bcast:31 row_mask:0xc bank_mask:0xf
	v_add_f32_e32 v1, v1, v25
	s_waitcnt lgkmcnt(1)
	v_mul_f32_e32 v25, v73, v93
	v_readlane_b32 s66, v1, 63
	v_mul_f32_e32 v1, v85, v91
	v_fmac_f32_e32 v1, v84, v90
	v_fmac_f32_e32 v25, v72, v92
	ds_read_b128 v[90:93], v105 offset:51200
	v_add_f32_e32 v1, v1, v25
	s_waitcnt lgkmcnt(1)
	v_mul_f32_e32 v25, v89, v95
	v_fmac_f32_e32 v25, v88, v94
	v_mul_f32_e32 v94, v63, v97
	v_fmac_f32_e32 v94, v62, v96
	v_add_f32_e32 v1, 0, v1
	v_add_f32_e32 v25, v25, v94
	ds_read_b128 v[94:97], v105 offset:52224
	v_add_f32_e32 v1, v1, v25
	s_waitcnt lgkmcnt(1)
	v_mul_f32_e32 v25, v81, v91
	v_fmac_f32_e32 v25, v80, v90
	v_mul_f32_e32 v90, v71, v93
	v_fmac_f32_e32 v90, v70, v92
	v_add_f32_e32 v25, v25, v90
	ds_read_b128 v[90:93], v105 offset:53248
	v_add_f32_e32 v1, v1, v25
	s_waitcnt lgkmcnt(1)
	v_mul_f32_e32 v25, v87, v95
	v_fmac_f32_e32 v25, v86, v94
	v_mul_f32_e32 v94, v61, v97
	v_fmac_f32_e32 v94, v60, v96
	v_add_f32_e32 v25, v25, v94
	ds_read_b128 v[94:97], v105 offset:54272
	v_add_f32_e32 v1, v1, v25
	s_waitcnt lgkmcnt(1)
	v_mul_f32_e32 v25, v77, v91
	v_fmac_f32_e32 v25, v76, v90
	v_mul_f32_e32 v90, v69, v93
	v_fmac_f32_e32 v90, v68, v92
	v_add_f32_e32 v25, v25, v90
	ds_read_b128 v[90:93], v105 offset:55296
	v_add_f32_e32 v1, v1, v25
	s_waitcnt lgkmcnt(1)
	v_mul_f32_e32 v25, v83, v95
	v_fmac_f32_e32 v25, v82, v94
	v_mul_f32_e32 v94, v59, v97
	v_fmac_f32_e32 v94, v58, v96
	v_add_f32_e32 v25, v25, v94
	ds_read_b128 v[94:97], v105 offset:56320
	v_add_f32_e32 v1, v1, v25
	s_waitcnt lgkmcnt(1)
; #define LAS __attribute__((address_space(3)))
; __device__ __forceinline__ float wave_sum(float v) { return lane63(scan64<false>(v)); }
; template <int YMODE, int EXTRA, bool NORM_OUT, bool XN8  , bool XIN_BF = false  , bool XOUT_BF = false  > ...
;     ...
;                     for (int e = 0; e < 8; ++e) { float s = 0.f;
; #pragma unroll
;                         for (int j = 0; j < 8; ++j) { const f32x4 w = *(const LAS f32x4*)(we + e * D + 256 * j + 4 * F.lane); s += (x[j][0] * w[0] + x[j][1] * w[1]) + (x[j][2] * w[2] + x[j][3] * w[3]); }
;                         d8[e] = wave_sum(s); asm volatile("" ::: "memory"); }
;                     if (EXTRA == 1) {
;                         float v = 0.f;
; #pragma unroll
;                         for (int e = 0; e < 8; ++e) v = (F.lane == e) ? d8[e] : v;
;                         if (F.lane < 8) { const float bb = (F.lane < 4) ? bi[F.lane] : bfg[F.lane - 4]; const float z = 15.f * tanhf((v + bb) * (1.f / 15.f));
;                             const float o = (F.lane < 4) ? z : (fminf(z, 0.f) - log1pf(expf(-fabsf(z)))); gates_out[row * 8 + F.lane] = o; }
	v_mul_f32_e32 v25, v75, v91
	v_fmac_f32_e32 v25, v74, v90
	v_mul_f32_e32 v90, v65, v93
	v_fmac_f32_e32 v90, v64, v92
	v_add_f32_e32 v25, v25, v90
	v_add_f32_e32 v1, v1, v25
	s_waitcnt lgkmcnt(0)
	v_mul_f32_e32 v25, v79, v95
	v_mul_f32_e32 v90, v67, v97
	v_fmac_f32_e32 v25, v78, v94
	v_fmac_f32_e32 v90, v66, v96
	v_add_f32_e32 v25, v25, v90
	v_add_f32_e32 v1, v1, v25
	v_mov_b32_e32 v25, 0
	ds_read_b128 v[90:93], v105 offset:57344
	ds_read_b128 v[94:97], v105 offset:58368
	v_add_f32_dpp v1, v1, v1 row_shr:1 row_mask:0xf bank_mask:0xf bound_ctrl:1
	s_waitcnt lgkmcnt(0)
	v_mul_f32_e32 v63, v63, v97
	v_add_f32_dpp v1, v1, v1 row_shr:2 row_mask:0xf bank_mask:0xf bound_ctrl:1
	v_fmac_f32_e32 v63, v62, v96
	s_nop 0
	v_add_f32_dpp v1, v1, v1 row_shr:4 row_mask:0xf bank_mask:0xf bound_ctrl:1
	s_nop 1
	v_add_f32_dpp v1, v1, v1 row_shr:8 row_mask:0xf bank_mask:0xf bound_ctrl:1
	s_nop 1
	v_mov_b32_dpp v25, v1 row_bcast:15 row_mask:0xa bank_mask:0xf
	v_add_f32_e32 v1, v1, v25
	v_mov_b32_e32 v25, 0
	s_nop 1
	v_mov_b32_dpp v25, v1 row_bcast:31 row_mask:0xc bank_mask:0xf
	v_add_f32_e32 v1, v1, v25
	v_mul_f32_e32 v25, v73, v93
	v_readlane_b32 s67, v1, 63
	v_mul_f32_e32 v1, v85, v91
	v_fmac_f32_e32 v1, v84, v90
	v_fmac_f32_e32 v25, v72, v92
	v_add_f32_e32 v1, v1, v25
	v_mul_f32_e32 v25, v89, v95
	v_fmac_f32_e32 v25, v88, v94
	ds_read_b128 v[88:91], v105 offset:59392
	ds_read_b128 v[92:95], v105 offset:60416
	v_add_f32_e32 v1, 0, v1
	v_add_f32_e32 v25, v25, v63
	v_add_f32_e32 v1, v1, v25
	s_waitcnt lgkmcnt(1)
	v_mul_f32_e32 v25, v81, v89
	v_mul_f32_e32 v62, v71, v91
	v_fmac_f32_e32 v25, v80, v88
	v_fmac_f32_e32 v62, v70, v90
	v_add_f32_e32 v25, v25, v62
	ds_read_b128 v[70:73], v105 offset:61440
	v_add_f32_e32 v1, v1, v25
	s_waitcnt lgkmcnt(1)
	v_mul_f32_e32 v25, v87, v93
	v_mul_f32_e32 v61, v61, v95
	v_fmac_f32_e32 v25, v86, v92
	v_fmac_f32_e32 v61, v60, v94
	v_add_f32_e32 v25, v25, v61
	ds_read_b128 v[60:63], v105 offset:62464
	v_add_f32_e32 v1, v1, v25
	s_waitcnt lgkmcnt(1)
	v_mul_f32_e32 v25, v77, v71
	v_mul_f32_e32 v69, v69, v73
	v_fmac_f32_e32 v25, v76, v70
	v_fmac_f32_e32 v69, v68, v72
	v_add_f32_e32 v25, v25, v69
	ds_read_b128 v[68:71], v105 offset:63488
	v_add_f32_e32 v1, v1, v25
	s_waitcnt lgkmcnt(1)
	v_mul_f32_e32 v25, v83, v61
	v_mul_f32_e32 v59, v59, v63
	v_fmac_f32_e32 v25, v82, v60
	v_fmac_f32_e32 v59, v58, v62
	v_add_f32_e32 v25, v25, v59
	ds_read_b128 v[58:61], v105 offset:64512
	v_add_f32_e32 v1, v1, v25
	s_waitcnt lgkmcnt(1)
	v_mul_f32_e32 v25, v75, v69
	v_mul_f32_e32 v62, v65, v71
	v_fmac_f32_e32 v25, v74, v68
	v_fmac_f32_e32 v62, v64, v70
	v_add_f32_e32 v25, v25, v62
	v_add_f32_e32 v1, v1, v25
	s_waitcnt lgkmcnt(0)
	v_mul_f32_e32 v25, v79, v59
	v_fmac_f32_e32 v25, v78, v58
	v_mul_f32_e32 v58, v67, v61
	v_fmac_f32_e32 v58, v66, v60
	v_add_f32_e32 v25, v25, v58
	v_add_f32_e32 v1, v1, v25
	v_mov_b32_e32 v25, 0
	s_nop 0
	v_add_f32_dpp v1, v1, v1 row_shr:1 row_mask:0xf bank_mask:0xf bound_ctrl:1
	s_nop 1
	v_add_f32_dpp v1, v1, v1 row_shr:2 row_mask:0xf bank_mask:0xf bound_ctrl:1
	s_nop 1
	v_add_f32_dpp v1, v1, v1 row_shr:4 row_mask:0xf bank_mask:0xf bound_ctrl:1
	s_nop 1
	v_add_f32_dpp v1, v1, v1 row_shr:8 row_mask:0xf bank_mask:0xf bound_ctrl:1
	s_nop 1
	v_mov_b32_dpp v25, v1 row_bcast:15 row_mask:0xa bank_mask:0xf
	v_add_f32_e32 v1, v1, v25
	v_mov_b32_e32 v25, 0
	s_nop 1
	v_mov_b32_dpp v25, v1 row_bcast:31 row_mask:0xc bank_mask:0xf
	v_add_f32_e32 v1, v1, v25
	s_nop 0
	v_readlane_b32 s68, v1, 63
	s_and_saveexec_b64 s[26:27], s[8:9]
	s_cbranch_execz .LBB0_1306
	v_mov_b32_e32 v1, s34
	v_cndmask_b32_e64 v1, 0, v1, s[6:7]
	v_mov_b32_e32 v25, s38
	v_cndmask_b32_e64 v1, v1, v25, s[22:23]
	v_mov_b32_e32 v25, s39
	v_cndmask_b32_e64 v1, v1, v25, s[20:21]
	v_mov_b32_e32 v25, s62
	v_cndmask_b32_e64 v1, v1, v25, s[18:19]
	v_mov_b32_e32 v25, s63
	v_cndmask_b32_e64 v1, v1, v25, s[16:17]
	v_mov_b32_e32 v25, s66
	v_cndmask_b32_e64 v1, v1, v25, s[14:15]
	v_mov_b32_e32 v25, s67
	v_cndmask_b32_e64 v1, v1, v25, s[12:13]
	v_mov_b32_e32 v25, s68
	v_cndmask_b32_e64 v1, v1, v25, s[10:11]
	global_load_dword v25, v[18:19], off
	s_mov_b32 s34, 0x3f200000
	s_waitcnt vmcnt(0) lgkmcnt(0)
	v_add_f32_e32 v1, v1, v25
	v_mul_f32_e32 v1, 0x3d888889, v1
	v_cmp_nlt_f32_e64 s[38:39], |v1|, s34
	s_and_saveexec_b64 s[62:63], s[38:39]
	s_xor_b64 s[38:39], exec, s[62:63]
	s_cbranch_execz .LBB0_1314
	v_add_f32_e64 v25, |v1|, |v1|
	v_mul_f32_e32 v58, 0x3fb8aa3b, v25
	v_rndne_f32_e32 v59, v58
	s_mov_b32 s34, 0x3fb8aa3b
	v_sub_f32_e32 v60, v58, v59
	v_fma_f32 v58, v25, s34, -v58
	v_fmac_f32_e32 v58, 0x32a5705f, v25
	v_add_f32_e32 v58, v60, v58
	v_cvt_i32_f32_e32 v59, v59
	v_exp_f32_e32 v58, v58
	s_mov_b32 s34, 0xc2ce8ed0
	v_cmp_ngt_f32_e32 vcc, s34, v25
	v_ldexp_f32 v58, v58, v59
	s_nop 0
	v_cndmask_b32_e32 v58, 0, v58, vcc
	v_cmp_nlt_f32_e32 vcc, s44, v25
	s_nop 1
	v_cndmask_b32_e32 v25, v111, v58, vcc
	v_add_f32_e32 v25, 1.0, v25
	v_rcp_f32_e32 v25, v25
	s_nop 0
	v_fma_f32 v25, v25, -2.0, 1.0

; __device__ __forceinline__ unsigned pack_i8x4(float a, float b, float c, float d) {
;     const int ia = (int)rintf(fminf(fmaxf(a, -127.f), 127.f)), ib = (int)rintf(fminf(fmaxf(b, -127.f), 127.f)), ic = (int)rintf(fminf(fmaxf(c, -127.f), 127.f)), id = (int)rintf(fminf(fmaxf(d, -127.f), 127.f));
;     return (unsigned)(ia & 0xff) | ((unsigned)(ib & 0xff) << 8) | ((unsigned)(ic & 0xff) << 16) | ((unsigned)(id & 0xff) << 24);
; }
; __device__ __forceinline__ void cvt_item_i8(const float* src, int ld, int k0, int c0, unsigned char* dst, int Kd, int drow0, const float* cmx  , unsigned char* scr, int lane) {
;     const int c = lane & 7, q = lane >> 3;
;     const f32x4 cm = *(const f32x4*)(cmx + 4 * c);
;     f32x4 inv; inv[0] = cm[0] > 0.f ? 127.f / cm[0] : 0.f; inv[1] = cm[1] > 0.f ? 127.f / cm[1] : 0.f; inv[2] = cm[2] > 0.f ? 127.f / cm[2] : 0.f; inv[3] = cm[3] > 0.f ? 127.f / cm[3] : 0.f;
;     f32x4 v[4][4];
; #pragma unroll
;     for (int g = 0; g < 4; ++g)
; #pragma unroll
;         for (int j = 0; j < 4; ++j) v[g][j] = __builtin_nontemporal_load((const f32x4*)(src + (size_t)(k0 + 32 * g + 4 * q + j) * ld + c0 + 4 * c));
; #pragma unroll
;     for (int g = 0; g < 4; ++g)
; #pragma unroll
;         for (int i = 0; i < 4; ++i) *(unsigned*)(scr + (4 * c + i) * 132 + 32 * g + 4 * q) = pack_i8x4(v[g][0][i] * inv[i], v[g][1][i] * inv[i], v[g][2][i] * inv[i], v[g][3][i] * inv[i]);
;     asm volatile("s_waitcnt lgkmcnt(0)" ::: "memory");
; #pragma unroll
;     for (int r = 0; r < 4; ++r) { const int n = 8 * r + (lane >> 3), ch = lane & 7; const unsigned char* p = scr + n * 132 + ch * 16;
;         u32x4 o; o.x = *(const unsigned*)(p); o.y = *(const unsigned*)(p + 4); o.z = *(const unsigned*)(p + 8); o.w = *(const unsigned*)(p + 12);
;         *(u32x4*)(dst + (size_t)(drow0 + n) * Kd + k0 + 16 * ch) = o; }
;     asm volatile("s_waitcnt lgkmcnt(0)" ::: "memory");
; }
; template <int GRP>
; __device__ __forceinline__ void conv_item(Frame& F, int r) {
;     ...
;         if (r < NI) { const int kb = r / 152, nb = r % 152, c0 = (nb < 112) ? nb * 32 : SRC_GATE + 8 + (nb - 112) * 32, drow = nb * 32;
;             if (QUANT) cvt_item_i8(inptr(F, IN_WIN) + (size_t)l * D * NIN_SRC, NIN_SRC, kb * 128, c0, ws + WS_WIN + (size_t)l * NIN * D, D, drow, cmx + CMX_WIN + l * NIN + drow, scr, F.lane);
.LBB0_1320:
	s_mul_hi_i32 s6, s17, 0x6bca1af3
	s_lshr_b32 s7, s6, 31
	s_ashr_i32 s6, s6, 6
	s_add_i32 s7, s6, s7
	s_mul_i32 s6, s7, 0xffffff68
	s_mul_i32 s8, s7, 0xffffed00
	s_add_i32 s11, s17, s6
	s_add_i32 s6, s4, s8
	s_add_i32 s10, s6, 8
	s_cmpk_lt_i32 s11, 0x70
	s_cselect_b32 s10, s6, s10
	s_lshl_b32 s18, s7, 7
	s_ashr_i32 s7, s6, 31
	v_lshl_add_u64 v[30:31], s[6:7], 2, v[4:5]
	global_load_dwordx4 v[30:33], v[30:31], off
	ds_read_b64 v[8:9], v19
	s_ashr_i32 s11, s10, 31
	v_or_b32_e32 v29, s18, v18
	v_or_b32_e32 v40, 1, v29
	v_or_b32_e32 v42, 2, v29
	s_waitcnt lgkmcnt(0)
	v_readfirstlane_b32 s8, v8
	v_add_u32_e32 v8, s6, v1
	s_lshl_b64 s[6:7], s[10:11], 2
	v_readfirstlane_b32 s9, v9
	v_add_u32_e32 v12, 16, v8
	s_add_u32 s6, s8, s6
	v_add_u32_e32 v10, 8, v8
	v_ashrrev_i32_e32 v13, 31, v12
	s_addc_u32 s7, s9, s7
	v_add_u32_e32 v14, 24, v8
	v_ashrrev_i32_e32 v11, 31, v10
	v_lshlrev_b64 v[36:37], 11, v[12:13]
	s_ashr_i32 s19, s18, 31
	v_lshl_add_u64 v[12:13], s[6:7], 0, v[2:3]
	v_ashrrev_i32_e32 v9, 31, v8
	v_ashrrev_i32_e32 v15, 31, v14
	v_lshlrev_b64 v[34:35], 11, v[10:11]
	v_or_b32_e32 v44, 3, v29
	v_or_b32_e32 v45, 32, v29
	v_or_b32_e32 v48, 33, v29
	v_or_b32_e32 v49, 34, v29
	v_or_b32_e32 v52, 35, v29
	v_or_b32_e32 v53, 64, v29
	v_or_b32_e32 v56, 0x41, v29
	v_or_b32_e32 v57, 0x42, v29
	v_or_b32_e32 v60, 0x43, v29
	v_or_b32_e32 v61, 0x60, v29
	v_or_b32_e32 v64, 0x61, v29
	v_or_b32_e32 v65, 0x62, v29
	v_or_b32_e32 v68, 0x63, v29
	v_lshl_add_u64 v[10:11], v[6:7], 0, s[18:19]
	v_lshl_add_u64 v[38:39], v[12:13], 0, s[0:1]
	v_lshlrev_b64 v[16:17], 11, v[8:9]
	v_lshlrev_b64 v[8:9], 11, v[14:15]
	v_lshl_add_u64 v[14:15], v[10:11], 0, v[34:35]
	v_mad_i64_i32 v[34:35], s[6:7], v29, s14, v[38:39]
	v_mad_i64_i32 v[40:41], s[6:7], v40, s14, v[38:39]
	v_mad_i64_i32 v[42:43], s[6:7], v42, s14, v[38:39]
	v_mad_i64_i32 v[46:47], s[6:7], v44, s14, v[38:39]
	v_mad_i64_i32 v[50:51], s[6:7], v45, s14, v[38:39]
	v_mad_i64_i32 v[54:55], s[6:7], v48, s14, v[38:39]
	v_mad_i64_i32 v[58:59], s[6:7], v49, s14, v[38:39]
	v_mad_i64_i32 v[62:63], s[6:7], v52, s14, v[38:39]
	v_mad_i64_i32 v[66:67], s[6:7], v53, s14, v[38:39]
	v_mad_i64_i32 v[70:71], s[6:7], v56, s14, v[38:39]
	v_mad_i64_i32 v[74:75], s[6:7], v57, s14, v[38:39]
	v_mad_i64_i32 v[78:79], s[6:7], v60, s14, v[38:39]
	v_mad_i64_i32 v[82:83], s[6:7], v61, s14, v[38:39]
	v_mad_i64_i32 v[86:87], s[6:7], v64, s14, v[38:39]
	v_mad_i64_i32 v[90:91], s[6:7], v65, s14, v[38:39]
	v_mad_i64_i32 v[94:95], s[6:7], v68, s14, v[38:39]
	v_lshl_add_u64 v[12:13], v[10:11], 0, v[16:17]
	v_lshl_add_u64 v[16:17], v[10:11], 0, v[36:37]
	global_load_dwordx4 v[34:37], v[34:35], off nt
	s_nop 0
	global_load_dwordx4 v[38:41], v[40:41], off nt
	s_nop 0
	global_load_dwordx4 v[42:45], v[42:43], off nt
	s_nop 0
	global_load_dwordx4 v[46:49], v[46:47], off nt
	s_nop 0
	global_load_dwordx4 v[50:53], v[50:51], off nt
	s_nop 0
	global_load_dwordx4 v[54:57], v[54:55], off nt
	s_nop 0
	global_load_dwordx4 v[58:61], v[58:59], off nt
	s_nop 0
	global_load_dwordx4 v[62:65], v[62:63], off nt
	s_nop 0
	global_load_dwordx4 v[66:69], v[66:67], off nt
	s_nop 0
	global_load_dwordx4 v[70:73], v[70:71], off nt
	s_nop 0
	global_load_dwordx4 v[74:77], v[74:75], off nt
	s_nop 0
	global_load_dwordx4 v[78:81], v[78:79], off nt
	s_nop 0
	global_load_dwordx4 v[82:85], v[82:83], off nt
	s_nop 0
	global_load_dwordx4 v[86:89], v[86:87], off nt
	s_nop 0
	global_load_dwordx4 v[90:93], v[90:91], off nt
	s_nop 0
	global_load_dwordx4 v[94:97], v[94:95], off nt
	v_lshl_add_u64 v[8:9], v[10:11], 0, v[8:9]
	s_add_i32 s17, s17, s20
	s_add_i32 s4, s4, s12
	s_cmp_lt_i32 s17, s3
	s_waitcnt vmcnt(0)
	v_div_scale_f32 v29, s[6:7], v30, v30, s13
	v_div_scale_f32 v99, s[6:7], v31, v31, s13
	v_rcp_f32_e32 v105, v29
	v_rcp_f32_e32 v106, v99
	v_div_scale_f32 v101, s[8:9], v32, v32, s13
	v_rcp_f32_e32 v107, v101
	v_div_scale_f32 v103, s[10:11], v33, v33, s13
	v_fma_f32 v109, -v29, v105, 1.0
	v_div_scale_f32 v98, vcc, s13, v30, s13
	v_rcp_f32_e32 v108, v103
	v_fma_f32 v110, -v99, v106, 1.0
	v_fmac_f32_e32 v105, v109, v105
	v_div_scale_f32 v100, s[6:7], s13, v31, s13
	v_fmac_f32_e32 v106, v110, v106
	v_mul_f32_e32 v109, v98, v105
	v_fma_f32 v111, -v101, v107, 1.0
	v_mul_f32_e32 v110, v100, v106
	v_fma_f32 v113, -v29, v109, v98
	v_div_scale_f32 v102, s[8:9], s13, v32, s13
	v_fmac_f32_e32 v107, v111, v107
	v_fma_f32 v114, -v99, v110, v100
	v_fmac_f32_e32 v109, v113, v105
	v_fma_f32 v112, -v103, v108, 1.0
	v_mul_f32_e32 v111, v102, v107
	v_fmac_f32_e32 v110, v114, v106
	v_fma_f32 v29, -v29, v109, v98
	v_div_scale_f32 v104, s[10:11], s13, v33, s13
	v_fmac_f32_e32 v108, v112, v108
	v_fma_f32 v115, -v101, v111, v102
	v_fma_f32 v98, -v99, v110, v100
	v_div_fmas_f32 v29, v29, v105, v109
	s_mov_b64 vcc, s[6:7]
	v_mul_f32_e32 v112, v104, v108
	v_fmac_f32_e32 v111, v115, v107
	v_div_fixup_f32 v29, v29, v30, s13
	v_div_fmas_f32 v98, v98, v106, v110
	v_cmp_lt_f32_e32 vcc, 0, v30
	v_fma_f32 v116, -v103, v112, v104
	v_fma_f32 v99, -v101, v111, v102
	v_cndmask_b32_e32 v29, 0, v29, vcc
	s_mov_b64 vcc, s[8:9]
	v_fmac_f32_e32 v112, v116, v108
	v_div_fixup_f32 v30, v98, v31, s13
	v_div_fmas_f32 v98, v99, v107, v111
	v_cmp_lt_f32_e32 vcc, 0, v31
	v_fma_f32 v100, -v103, v112, v104
	v_div_fixup_f32 v31, v98, v32, s13
	v_cndmask_b32_e32 v30, 0, v30, vcc
	s_mov_b64 vcc, s[10:11]
	v_div_fmas_f32 v98, v100, v108, v112
	v_cmp_lt_f32_e32 vcc, 0, v32
	v_div_fixup_f32 v32, v98, v33, s13
	s_waitcnt lgkmcnt(0)
; __device__ __forceinline__ unsigned pack_i8x4(float a, float b, float c, float d) {
;     const int ia = (int)rintf(fminf(fmaxf(a, -127.f), 127.f)), ib = (int)rintf(fminf(fmaxf(b, -127.f), 127.f)), ic = (int)rintf(fminf(fmaxf(c, -127.f), 127.f)), id = (int)rintf(fminf(fmaxf(d, -127.f), 127.f));
;     return (unsigned)(ia & 0xff) | ((unsigned)(ib & 0xff) << 8) | ((unsigned)(ic & 0xff) << 16) | ((unsigned)(id & 0xff) << 24);
; }
; __device__ __forceinline__ void cvt_item_i8(const float* src, int ld, int k0, int c0, unsigned char* dst, int Kd, int drow0, const float* cmx  , unsigned char* scr, int lane) {
;     const int c = lane & 7, q = lane >> 3;
;     const f32x4 cm = *(const f32x4*)(cmx + 4 * c);
;     f32x4 inv; inv[0] = cm[0] > 0.f ? 127.f / cm[0] : 0.f; inv[1] = cm[1] > 0.f ? 127.f / cm[1] : 0.f; inv[2] = cm[2] > 0.f ? 127.f / cm[2] : 0.f; inv[3] = cm[3] > 0.f ? 127.f / cm[3] : 0.f;
;     f32x4 v[4][4];
; #pragma unroll
;     for (int g = 0; g < 4; ++g)
; #pragma unroll
;         for (int j = 0; j < 4; ++j) v[g][j] = __builtin_nontemporal_load((const f32x4*)(src + (size_t)(k0 + 32 * g + 4 * q + j) * ld + c0 + 4 * c));
; #pragma unroll
;     for (int g = 0; g < 4; ++g)
; #pragma unroll
;         for (int i = 0; i < 4; ++i) *(unsigned*)(scr + (4 * c + i) * 132 + 32 * g + 4 * q) = pack_i8x4(v[g][0][i] * inv[i], v[g][1][i] * inv[i], v[g][2][i] * inv[i], v[g][3][i] * inv[i]);
	v_mul_f32_e32 v34, v34, v29
	v_mul_f32_e32 v38, v29, v38
	v_mul_f32_e32 v42, v29, v42
	v_mul_f32_e32 v46, v29, v46
	v_mul_f32_e32 v50, v29, v50
	v_mul_f32_e32 v54, v29, v54
	v_mul_f32_e32 v58, v29, v58
	v_mul_f32_e32 v62, v29, v62
	v_mul_f32_e32 v66, v29, v66
	v_mul_f32_e32 v70, v29, v70
	v_mul_f32_e32 v74, v29, v74
	v_mul_f32_e32 v78, v29, v78
	v_mul_f32_e32 v82, v29, v82
	v_mul_f32_e32 v86, v29, v86
	v_cndmask_b32_e32 v31, 0, v31, vcc
	v_med3_f32 v34, v34, s15, v20
	v_med3_f32 v38, v38, s15, v20
	v_med3_f32 v42, v42, s15, v20
	v_med3_f32 v46, v46, s15, v20
	v_mul_f32_e32 v39, v30, v39
	v_mul_f32_e32 v43, v30, v43
	v_mul_f32_e32 v47, v30, v47
	v_med3_f32 v50, v50, s15, v20
	v_med3_f32 v54, v54, s15, v20
	v_mul_f32_e32 v55, v30, v55
	v_cmp_lt_f32_e32 vcc, 0, v33
	v_mul_f32_e32 v90, v29, v90
	v_mul_f32_e32 v35, v35, v30
	v_med3_f32 v58, v58, s15, v20
	v_med3_f32 v62, v62, s15, v20
	v_mul_f32_e32 v51, v30, v51
	v_mul_f32_e32 v59, v30, v59
	v_mul_f32_e32 v63, v30, v63
	v_med3_f32 v66, v66, s15, v20
	v_med3_f32 v70, v70, s15, v20
	v_med3_f32 v74, v74, s15, v20
	v_med3_f32 v78, v78, s15, v20
	v_mul_f32_e32 v71, v30, v71
	v_mul_f32_e32 v79, v30, v79
	v_med3_f32 v82, v82, s15, v20
	v_med3_f32 v86, v86, s15, v20
	v_mul_f32_e32 v87, v30, v87
	v_cndmask_b32_e32 v32, 0, v32, vcc
	v_rndne_f32_e32 v33, v34
	v_rndne_f32_e32 v34, v38
	v_rndne_f32_e32 v38, v42
	v_rndne_f32_e32 v42, v46
	v_med3_f32 v39, v39, s15, v20
	v_med3_f32 v43, v43, s15, v20
	v_med3_f32 v46, v47, s15, v20
	v_mul_f32_e32 v40, v31, v40
	v_mul_f32_e32 v47, v31, v48
	v_rndne_f32_e32 v48, v50
	v_rndne_f32_e32 v50, v54
	v_med3_f32 v55, v55, s15, v20
	v_mul_f32_e32 v56, v31, v56
	v_mul_f32_e32 v29, v29, v94
	v_mul_f32_e32 v67, v30, v67
	v_mul_f32_e32 v75, v30, v75
	v_med3_f32 v90, v90, s15, v20
	v_mul_f32_e32 v83, v30, v83
	v_mul_f32_e32 v91, v30, v91
	v_med3_f32 v35, v35, s15, v20
	v_mul_f32_e32 v36, v36, v31
	v_mul_f32_e32 v44, v31, v44
	v_rndne_f32_e32 v54, v58
	v_rndne_f32_e32 v58, v62
	v_med3_f32 v51, v51, s15, v20
	v_med3_f32 v59, v59, s15, v20
	v_med3_f32 v62, v63, s15, v20
	v_mul_f32_e32 v52, v31, v52
	v_mul_f32_e32 v60, v31, v60
	v_mul_f32_e32 v63, v31, v64
	v_rndne_f32_e32 v64, v66
	v_rndne_f32_e32 v66, v70
	v_rndne_f32_e32 v70, v74
	v_rndne_f32_e32 v74, v78
	v_med3_f32 v71, v71, s15, v20
	v_med3_f32 v78, v79, s15, v20
	v_mul_f32_e32 v72, v31, v72
	v_mul_f32_e32 v79, v31, v80
	v_rndne_f32_e32 v80, v82
	v_rndne_f32_e32 v82, v86
	v_med3_f32 v87, v87, s15, v20
	v_mul_f32_e32 v88, v31, v88
	v_cvt_i32_f32_e32 v34, v34
	v_rndne_f32_e32 v39, v39
	v_rndne_f32_e32 v43, v43
	v_med3_f32 v40, v40, s15, v20
	v_mul_f32_e32 v41, v32, v41
	v_cvt_i32_f32_e32 v50, v50
	v_rndne_f32_e32 v55, v55
	v_med3_f32 v56, v56, s15, v20
	v_mul_f32_e32 v57, v32, v57
	v_med3_f32 v29, v29, s15, v20
	v_mul_f32_e32 v30, v30, v95
	v_med3_f32 v67, v67, s15, v20
	v_med3_f32 v75, v75, s15, v20
	v_mul_f32_e32 v68, v31, v68
	v_mul_f32_e32 v76, v31, v76
	v_rndne_f32_e32 v86, v90
	v_med3_f32 v83, v83, s15, v20
	v_med3_f32 v90, v91, s15, v20
	v_mul_f32_e32 v84, v31, v84
	v_mul_f32_e32 v91, v31, v92
	v_cvt_i32_f32_e32 v33, v33
	v_cvt_i32_f32_sdwa v38, v38 dst_sel:WORD_1 dst_unused:UNUSED_PAD src0_sel:DWORD
	v_rndne_f32_e32 v35, v35
	v_med3_f32 v36, v36, s15, v20
	v_med3_f32 v44, v44, s15, v20
	v_mul_f32_e32 v37, v37, v32
	v_mul_f32_e32 v45, v32, v45
	v_cvt_i32_f32_e32 v48, v48
	v_cvt_i32_f32_sdwa v54, v54 dst_sel:WORD_1 dst_unused:UNUSED_PAD src0_sel:DWORD
	v_rndne_f32_e32 v51, v51
	v_rndne_f32_e32 v59, v59
	v_med3_f32 v52, v52, s15, v20
	v_med3_f32 v60, v60, s15, v20
	v_mul_f32_e32 v53, v32, v53
	v_mul_f32_e32 v61, v32, v61
	v_cvt_i32_f32_e32 v66, v66
	v_rndne_f32_e32 v71, v71
	v_med3_f32 v72, v72, s15, v20
	v_mul_f32_e32 v73, v32, v73
	v_cvt_i32_f32_e32 v82, v82
	v_rndne_f32_e32 v87, v87
	v_med3_f32 v88, v88, s15, v20
	v_mul_f32_e32 v89, v32, v89
	v_cvt_i32_f32_e32 v39, v39
	v_cvt_i32_f32_sdwa v43, v43 dst_sel:WORD_1 dst_unused:UNUSED_PAD src0_sel:DWORD
	v_rndne_f32_e32 v40, v40
	v_med3_f32 v41, v41, s15, v20
	v_cvt_i32_f32_e32 v55, v55
	v_rndne_f32_e32 v56, v56
	v_med3_f32 v57, v57, s15, v20
	v_rndne_f32_e32 v29, v29
	v_med3_f32 v30, v30, s15, v20
	v_mul_f32_e32 v31, v31, v96
	v_cvt_i32_f32_sdwa v42, v42 dst_sel:BYTE_3 dst_unused:UNUSED_PAD src0_sel:DWORD
	v_rndne_f32_e32 v46, v46
	v_med3_f32 v47, v47, s15, v20
	v_mul_f32_e32 v49, v32, v49
	v_cvt_i32_f32_sdwa v58, v58 dst_sel:BYTE_3 dst_unused:UNUSED_PAD src0_sel:DWORD
	v_rndne_f32_e32 v62, v62
	v_med3_f32 v63, v63, s15, v20
	v_mul_f32_e32 v65, v32, v65
	v_cvt_i32_f32_e32 v64, v64
	v_cvt_i32_f32_sdwa v70, v70 dst_sel:WORD_1 dst_unused:UNUSED_PAD src0_sel:DWORD
	v_rndne_f32_e32 v67, v67
	v_rndne_f32_e32 v75, v75
	v_med3_f32 v68, v68, s15, v20
	v_med3_f32 v76, v76, s15, v20
	v_mul_f32_e32 v69, v32, v69
	v_mul_f32_e32 v77, v32, v77
	v_cvt_i32_f32_e32 v80, v80
	v_cvt_i32_f32_sdwa v86, v86 dst_sel:WORD_1 dst_unused:UNUSED_PAD src0_sel:DWORD
	v_rndne_f32_e32 v83, v83
	v_rndne_f32_e32 v90, v90
	v_med3_f32 v84, v84, s15, v20
	v_med3_f32 v91, v91, s15, v20
	v_mul_f32_e32 v85, v32, v85
	v_mul_f32_e32 v92, v32, v93
	v_cvt_i32_f32_e32 v35, v35
	v_rndne_f32_e32 v36, v36
	v_rndne_f32_e32 v44, v44
	v_med3_f32 v37, v37, s15, v20
	v_med3_f32 v45, v45, s15, v20
	v_cvt_i32_f32_e32 v51, v51
	v_cvt_i32_f32_sdwa v59, v59 dst_sel:WORD_1 dst_unused:UNUSED_PAD src0_sel:DWORD
	v_rndne_f32_e32 v52, v52
	v_rndne_f32_e32 v60, v60
	v_med3_f32 v53, v53, s15, v20
	v_med3_f32 v61, v61, s15, v20
	v_cvt_i32_f32_e32 v71, v71
	v_rndne_f32_e32 v72, v72
	v_med3_f32 v73, v73, s15, v20
	v_cvt_i32_f32_e32 v87, v87
	v_rndne_f32_e32 v88, v88
	v_med3_f32 v89, v89, s15, v20
	v_cvt_i32_f32_e32 v40, v40
; __device__ __forceinline__ unsigned pack_i8x4(float a, float b, float c, float d) {
;     const int ia = (int)rintf(fminf(fmaxf(a, -127.f), 127.f)), ib = (int)rintf(fminf(fmaxf(b, -127.f), 127.f)), ic = (int)rintf(fminf(fmaxf(c, -127.f), 127.f)), id = (int)rintf(fminf(fmaxf(d, -127.f), 127.f));
;     return (unsigned)(ia & 0xff) | ((unsigned)(ib & 0xff) << 8) | ((unsigned)(ic & 0xff) << 16) | ((unsigned)(id & 0xff) << 24);
; }
; __device__ __forceinline__ void cvt_item_i8(const float* src, int ld, int k0, int c0, unsigned char* dst, int Kd, int drow0, const float* cmx  , unsigned char* scr, int lane) {
;     const int c = lane & 7, q = lane >> 3;
;     const f32x4 cm = *(const f32x4*)(cmx + 4 * c);
;     f32x4 inv; inv[0] = cm[0] > 0.f ? 127.f / cm[0] : 0.f; inv[1] = cm[1] > 0.f ? 127.f / cm[1] : 0.f; inv[2] = cm[2] > 0.f ? 127.f / cm[2] : 0.f; inv[3] = cm[3] > 0.f ? 127.f / cm[3] : 0.f;
;     f32x4 v[4][4];
; #pragma unroll
;     for (int g = 0; g < 4; ++g)
; #pragma unroll
;         for (int j = 0; j < 4; ++j) v[g][j] = __builtin_nontemporal_load((const f32x4*)(src + (size_t)(k0 + 32 * g + 4 * q + j) * ld + c0 + 4 * c));
; #pragma unroll
;     for (int g = 0; g < 4; ++g)
; #pragma unroll
;         for (int i = 0; i < 4; ++i) *(unsigned*)(scr + (4 * c + i) * 132 + 32 * g + 4 * q) = pack_i8x4(v[g][0][i] * inv[i], v[g][1][i] * inv[i], v[g][2][i] * inv[i], v[g][3][i] * inv[i]);
;     asm volatile("s_waitcnt lgkmcnt(0)" ::: "memory");
; #pragma unroll
;     for (int r = 0; r < 4; ++r) { const int n = 8 * r + (lane >> 3), ch = lane & 7; const unsigned char* p = scr + n * 132 + ch * 16;
;         u32x4 o; o.x = *(const unsigned*)(p); o.y = *(const unsigned*)(p + 4); o.z = *(const unsigned*)(p + 8); o.w = *(const unsigned*)(p + 12);
;         *(u32x4*)(dst + (size_t)(drow0 + n) * Kd + k0 + 16 * ch) = o; }
;     asm volatile("s_waitcnt lgkmcnt(0)" ::: "memory");
; }
	v_rndne_f32_e32 v41, v41
	v_cvt_i32_f32_e32 v56, v56
	v_rndne_f32_e32 v57, v57
	v_cvt_i32_f32_sdwa v74, v74 dst_sel:BYTE_3 dst_unused:UNUSED_PAD src0_sel:DWORD
	v_rndne_f32_e32 v78, v78
	v_med3_f32 v79, v79, s15, v20
	v_mul_f32_e32 v81, v32, v81
	v_cvt_i32_f32_sdwa v29, v29 dst_sel:BYTE_3 dst_unused:UNUSED_PAD src0_sel:DWORD
	v_rndne_f32_e32 v30, v30
	v_med3_f32 v31, v31, s15, v20
	v_mul_f32_e32 v32, v32, v97
	v_cvt_i32_f32_sdwa v46, v46 dst_sel:BYTE_3 dst_unused:UNUSED_PAD src0_sel:DWORD
	v_rndne_f32_e32 v47, v47
	v_med3_f32 v49, v49, s15, v20
	v_cvt_i32_f32_sdwa v62, v62 dst_sel:BYTE_3 dst_unused:UNUSED_PAD src0_sel:DWORD
	v_rndne_f32_e32 v63, v63
	v_med3_f32 v65, v65, s15, v20
	v_cvt_i32_f32_e32 v67, v67
	v_cvt_i32_f32_sdwa v75, v75 dst_sel:WORD_1 dst_unused:UNUSED_PAD src0_sel:DWORD
	v_rndne_f32_e32 v68, v68
	v_rndne_f32_e32 v76, v76
	v_med3_f32 v69, v69, s15, v20
	v_med3_f32 v77, v77, s15, v20
	v_cvt_i32_f32_e32 v83, v83
	v_cvt_i32_f32_sdwa v90, v90 dst_sel:WORD_1 dst_unused:UNUSED_PAD src0_sel:DWORD
	v_rndne_f32_e32 v84, v84
	v_rndne_f32_e32 v91, v91
	v_med3_f32 v85, v85, s15, v20
	v_med3_f32 v92, v92, s15, v20
	v_cvt_i32_f32_e32 v36, v36
	v_cvt_i32_f32_sdwa v44, v44 dst_sel:WORD_1 dst_unused:UNUSED_PAD src0_sel:DWORD
	v_rndne_f32_e32 v37, v37
	v_rndne_f32_e32 v45, v45
	v_cvt_i32_f32_e32 v52, v52
	v_cvt_i32_f32_sdwa v60, v60 dst_sel:WORD_1 dst_unused:UNUSED_PAD src0_sel:DWORD
	v_rndne_f32_e32 v53, v53
	v_rndne_f32_e32 v61, v61
	v_cvt_i32_f32_e32 v72, v72
	v_rndne_f32_e32 v73, v73
	v_cvt_i32_f32_e32 v88, v88
	v_rndne_f32_e32 v89, v89
	v_cvt_i32_f32_e32 v41, v41
	v_cvt_i32_f32_e32 v57, v57
	v_cvt_i32_f32_sdwa v78, v78 dst_sel:BYTE_3 dst_unused:UNUSED_PAD src0_sel:DWORD
	v_rndne_f32_e32 v79, v79
	v_med3_f32 v81, v81, s15, v20
	v_cvt_i32_f32_sdwa v30, v30 dst_sel:BYTE_3 dst_unused:UNUSED_PAD src0_sel:DWORD
	v_rndne_f32_e32 v31, v31
	v_med3_f32 v32, v32, s15, v20
	v_cvt_i32_f32_sdwa v47, v47 dst_sel:BYTE_3 dst_unused:UNUSED_PAD src0_sel:DWORD
	v_rndne_f32_e32 v49, v49
	v_cvt_i32_f32_sdwa v63, v63 dst_sel:BYTE_3 dst_unused:UNUSED_PAD src0_sel:DWORD
	v_rndne_f32_e32 v65, v65
	v_cvt_i32_f32_e32 v68, v68
	v_cvt_i32_f32_sdwa v76, v76 dst_sel:WORD_1 dst_unused:UNUSED_PAD src0_sel:DWORD
	v_rndne_f32_e32 v69, v69
	v_rndne_f32_e32 v77, v77
	v_cvt_i32_f32_e32 v84, v84
	v_cvt_i32_f32_sdwa v91, v91 dst_sel:WORD_1 dst_unused:UNUSED_PAD src0_sel:DWORD
	v_rndne_f32_e32 v85, v85
	v_rndne_f32_e32 v92, v92
	v_cvt_i32_f32_e32 v37, v37
	v_cvt_i32_f32_sdwa v45, v45 dst_sel:WORD_1 dst_unused:UNUSED_PAD src0_sel:DWORD
	v_cvt_i32_f32_e32 v53, v53
	v_cvt_i32_f32_sdwa v61, v61 dst_sel:WORD_1 dst_unused:UNUSED_PAD src0_sel:DWORD
	v_cvt_i32_f32_e32 v73, v73
	v_cvt_i32_f32_e32 v89, v89
	v_lshlrev_b32_e32 v34, 8, v34
	v_lshlrev_b32_e32 v50, 8, v50
	v_cvt_i32_f32_sdwa v79, v79 dst_sel:BYTE_3 dst_unused:UNUSED_PAD src0_sel:DWORD
	v_rndne_f32_e32 v81, v81
	v_cvt_i32_f32_sdwa v31, v31 dst_sel:BYTE_3 dst_unused:UNUSED_PAD src0_sel:DWORD
	v_rndne_f32_e32 v32, v32
	v_cvt_i32_f32_sdwa v49, v49 dst_sel:BYTE_3 dst_unused:UNUSED_PAD src0_sel:DWORD
	v_cvt_i32_f32_sdwa v65, v65 dst_sel:BYTE_3 dst_unused:UNUSED_PAD src0_sel:DWORD
	v_cvt_i32_f32_e32 v69, v69
	v_cvt_i32_f32_sdwa v77, v77 dst_sel:WORD_1 dst_unused:UNUSED_PAD src0_sel:DWORD
	v_cvt_i32_f32_e32 v85, v85
	v_cvt_i32_f32_sdwa v92, v92 dst_sel:WORD_1 dst_unused:UNUSED_PAD src0_sel:DWORD
	v_and_b32_e32 v38, 0xff0000, v38
	v_and_b32_e32 v54, 0xff0000, v54
	v_lshlrev_b32_e32 v66, 8, v66
	v_lshlrev_b32_e32 v82, 8, v82
	v_perm_b32 v33, v34, v33, s16
	v_lshlrev_b32_e32 v34, 8, v39
	v_and_b32_e32 v39, 0xff0000, v43
	v_perm_b32 v43, v50, v48, s16
	v_lshlrev_b32_e32 v48, 8, v55
	v_cvt_i32_f32_sdwa v81, v81 dst_sel:BYTE_3 dst_unused:UNUSED_PAD src0_sel:DWORD
	v_cvt_i32_f32_sdwa v32, v32 dst_sel:BYTE_3 dst_unused:UNUSED_PAD src0_sel:DWORD
	v_and_b32_e32 v70, 0xff0000, v70
	v_and_b32_e32 v86, 0xff0000, v86
	v_and_b32_e32 v50, 0xff0000, v59
	v_perm_b32 v55, v66, v64, s16
	v_lshlrev_b32_e32 v59, 8, v71
	v_perm_b32 v66, v82, v80, s16
	v_lshlrev_b32_e32 v71, 8, v87
	v_or3_b32 v33, v33, v38, v42
	v_perm_b32 v34, v34, v35, s16
	v_lshlrev_b32_e32 v35, 8, v40
	v_or3_b32 v40, v43, v54, v58
	v_perm_b32 v42, v48, v51, s16
	v_lshlrev_b32_e32 v43, 8, v56
	v_and_b32_e32 v64, 0xff0000, v75
	v_and_b32_e32 v75, 0xff0000, v90
	v_and_b32_e32 v38, 0xff0000, v44
	v_and_b32_e32 v44, 0xff0000, v60
	v_or3_b32 v48, v55, v70, v74
	v_perm_b32 v51, v59, v67, s16
	v_lshlrev_b32_e32 v54, 8, v72
	v_or3_b32 v29, v66, v86, v29
	v_perm_b32 v56, v71, v83, s16
	v_lshlrev_b32_e32 v58, 8, v88
	v_or3_b32 v34, v34, v39, v46
	v_perm_b32 v35, v35, v36, s16
	v_lshlrev_b32_e32 v36, 8, v41
	ds_write2_b32 v21, v33, v40 offset1:8
	v_or3_b32 v33, v42, v50, v62
	v_perm_b32 v40, v43, v52, s16
	v_lshlrev_b32_e32 v41, 8, v57
	v_and_b32_e32 v55, 0xff0000, v76
	v_and_b32_e32 v59, 0xff0000, v91
	v_and_b32_e32 v39, 0xff0000, v45
	v_and_b32_e32 v42, 0xff0000, v61
	v_or3_b32 v43, v51, v64, v78
	v_perm_b32 v45, v54, v68, s16
	v_lshlrev_b32_e32 v46, 8, v73
	ds_write2_b32 v21, v48, v29 offset0:16 offset1:24
	v_or3_b32 v29, v56, v75, v30
	v_perm_b32 v30, v58, v84, s16
	v_lshlrev_b32_e32 v48, 8, v89
	v_or3_b32 v35, v35, v38, v47
	v_perm_b32 v36, v36, v37, s16
	ds_write2_b32 v21, v34, v33 offset0:33 offset1:41
	v_or3_b32 v33, v40, v44, v63
	v_perm_b32 v34, v41, v53, s16
	v_and_b32_e32 v50, 0xff0000, v77
	v_and_b32_e32 v51, 0xff0000, v92
	v_or3_b32 v37, v45, v55, v79
	v_perm_b32 v38, v46, v69, s16
	ds_write2_b32 v21, v43, v29 offset0:49 offset1:57
	v_or3_b32 v29, v30, v59, v31
	v_perm_b32 v30, v48, v85, s16
	v_or3_b32 v31, v36, v39, v49
	ds_write2_b32 v21, v35, v33 offset0:66 offset1:74
	v_or3_b32 v33, v34, v42, v65
	v_or3_b32 v34, v38, v50, v81
	ds_write2_b32 v21, v37, v29 offset0:82 offset1:90
	v_or3_b32 v29, v30, v51, v32
	ds_write2_b32 v21, v31, v33 offset0:99 offset1:107
	ds_write2_b32 v21, v34, v29 offset0:115 offset1:123
	s_waitcnt lgkmcnt(0)
	ds_read2_b32 v[30:31], v22 offset1:1
	ds_read2_b32 v[32:33], v22 offset0:2 offset1:3
	ds_read2_b32 v[34:35], v23 offset1:1
	ds_read2_b32 v[36:37], v24 offset1:1
	ds_read2_b32 v[38:39], v25 offset1:1
	ds_read2_b32 v[40:41], v26 offset1:1
	ds_read2_b32 v[42:43], v27 offset1:1
	ds_read2_b32 v[44:45], v28 offset1:1
	s_waitcnt lgkmcnt(6)
	global_store_dwordx4 v[12:13], v[30:33], off
	s_waitcnt lgkmcnt(4)
	global_store_dwordx4 v[14:15], v[34:37], off
	s_waitcnt lgkmcnt(2)
	global_store_dwordx4 v[16:17], v[38:41], off
	s_waitcnt lgkmcnt(0)
	global_store_dwordx4 v[8:9], v[42:45], off
	s_waitcnt lgkmcnt(0)
	s_cbranch_scc1 .LBB0_1320

; __device__ __forceinline__ void cvt_item_i8(const float* src, int ld, int k0, int c0, unsigned char* dst, int Kd, int drow0, const float* cmx  , unsigned char* scr, int lane) {
;     const int c = lane & 7, q = lane >> 3;
;     const f32x4 cm = *(const f32x4*)(cmx + 4 * c);
;     f32x4 inv; inv[0] = cm[0] > 0.f ? 127.f / cm[0] : 0.f; inv[1] = cm[1] > 0.f ? 127.f / cm[1] : 0.f; inv[2] = cm[2] > 0.f ? 127.f / cm[2] : 0.f; inv[3] = cm[3] > 0.f ? 127.f / cm[3] : 0.f;
;     f32x4 v[4][4];
; #pragma unroll
;     for (int g = 0; g < 4; ++g)
; #pragma unroll
;         for (int j = 0; j < 4; ++j) v[g][j] = __builtin_nontemporal_load((const f32x4*)(src + (size_t)(k0 + 32 * g + 4 * q + j) * ld + c0 + 4 * c));
; #pragma unroll
;     for (int g = 0; g < 4; ++g)
; #pragma unroll
;         for (int i = 0; i < 4; ++i) *(unsigned*)(scr + (4 * c + i) * 132 + 32 * g + 4 * q) = pack_i8x4(v[g][0][i] * inv[i], v[g][1][i] * inv[i], v[g][2][i] * inv[i], v[g][3][i] * inv[i]);
;     asm volatile("s_waitcnt lgkmcnt(0)" ::: "memory");
; #pragma unroll
;     for (int r = 0; r < 4; ++r) { const int n = 8 * r + (lane >> 3), ch = lane & 7; const unsigned char* p = scr + n * 132 + ch * 16;
;         u32x4 o; o.x = *(const unsigned*)(p); o.y = *(const unsigned*)(p + 4); o.z = *(const unsigned*)(p + 8); o.w = *(const unsigned*)(p + 12);
;         *(u32x4*)(dst + (size_t)(drow0 + n) * Kd + k0 + 16 * ch) = o; }
;     asm volatile("s_waitcnt lgkmcnt(0)" ::: "memory");
; }
; template <int GRP>
; __device__ __forceinline__ void conv_item(Frame& F, int r) {
;     ...
;     else { constexpr int KBN = (GRP == 3) ? 16 : CMS_KB, I_E = KBN * 88; const int up = r / (8 * I_E); r %= (8 * I_E); const int e = r / I_E; r %= I_E; const int kb = r / 88, nb = r % 88, n0 = nb * 32, drow = (n0 >> 7) * 256 + up * 128 + (n0 & 127);
;         if (GRP == 3) cvt_item_i8(inptr(F, up ? IN_MU : IN_MG) + (size_t)e * D * DFE, DFE, kb * 128, n0, ws + WS_MGU + (size_t)e * 2 * DFE * D, D, drow, cmx + 2 * DFF + e * 2 * DFE + drow, scr, F.lane);
.LBB0_1405:
	s_add_i32 s0, s16, 0x1200
	s_mul_hi_i32 s1, s0, 0x2e8ba2e9
	s_lshr_b32 s6, s1, 31
	s_ashr_i32 s1, s1, 11
	s_add_i32 s1, s1, s6
	s_mul_i32 s6, s1, 0x2c00
	s_sub_i32 s0, s0, s6
	s_lshl_b32 s40, s1, 7
	s_mul_i32 s1, s0, 0xba3
	s_lshr_b32 s6, s1, 31
	s_ashr_i32 s1, s1, 22
	s_add_i32 s1, s1, s6
	s_mul_i32 s6, s1, 0x580
	s_sub_i32 s0, s0, s6
	s_sext_i32_i16 s6, s0
	s_mulk_i32 s6, 0xba3
	s_lshr_b32 s38, s6, 31
	s_ashr_i32 s6, s6, 18
	s_add_i32 s6, s6, s38
	s_sext_i32_i16 s38, s6
	s_mulk_i32 s6, 0x58
	s_sub_i32 s0, s0, s6
	s_sext_i32_i16 s6, s0
	s_lshl_b32 s0, s6, 5
	s_lshl_b32 s6, s6, 6
	s_and_b32 s6, s6, 0xffffff00
	s_and_b32 s41, s0, 0x60
	s_add_i32 s6, s6, s40
	s_add_i32 s39, s16, 0x3dff
	s_or_b32 s6, s6, s41
	s_cmpk_lt_u32 s39, 0x57ff
	s_cselect_b32 s39, s17, 0xa8
	v_or_b32_e32 v8, s6, v17
	s_add_i32 s39, s39, 0
	v_ashrrev_i32_e32 v9, 31, v8
	s_add_i32 s39, s39, 0x20200
	v_lshlrev_b64 v[98:99], 11, v[8:9]
	v_mov_b32_e32 v8, s39
	ds_read_b64 v[8:9], v8
	s_sext_i32_i16 s11, s1
	s_mul_i32 s9, s11, 0x1600000
	s_mul_hi_i32 s1, s11, 0x1600000
	s_mul_i32 s10, s11, 0xb00000
	s_waitcnt lgkmcnt(0)
	v_readfirstlane_b32 s39, v8
	v_readfirstlane_b32 s40, v9
	s_add_u32 s9, s39, s9
	s_addc_u32 s39, s40, s1
	s_lshl_b32 s38, s38, 7
	s_mul_hi_i32 s7, s11, 0xb00000
	s_add_u32 s10, s3, s10
	s_mul_hi_i32 s8, s11, 0x5800
	s_mulk_i32 s11, 0x5800
	s_addc_u32 s40, s4, s7
	s_add_u32 s1, s14, s11
	s_addc_u32 s8, s15, s8
	s_ashr_i32 s7, s6, 31
	v_or_b32_e32 v6, s6, v1
	v_or_b32_e32 v10, s6, v18
	v_or_b32_e32 v12, s6, v19
	s_lshl_b64 s[6:7], s[6:7], 2
	s_add_u32 s6, s1, s6
	s_addc_u32 s7, s8, s7
	s_ashr_i32 s1, s0, 31
	s_lshl_b64 s[0:1], s[0:1], 2
	v_or_b32_e32 v8, s38, v16
	s_add_u32 s0, s9, s0
	v_ashrrev_i32_e32 v11, 31, v10
	v_mul_i32_i24_e32 v8, 0x2c00, v8
	s_addc_u32 s1, s39, s1
	v_lshlrev_b64 v[100:101], 11, v[10:11]
	v_ashrrev_i32_e32 v9, 31, v8
	v_lshl_add_u64 v[10:11], s[0:1], 0, v[4:5]
	v_ashrrev_i32_e32 v7, 31, v6
	v_ashrrev_i32_e32 v13, 31, v12
	v_lshl_add_u64 v[10:11], v[10:11], 0, v[8:9]
	v_lshlrev_b64 v[14:15], 11, v[6:7]
	v_lshlrev_b64 v[6:7], 11, v[12:13]
	v_add_co_u32_e32 v12, vcc, s19, v10
	global_load_dwordx4 v[30:33], v4, s[6:7]
	s_nop 0
	v_addc_co_u32_e32 v13, vcc, 0, v11, vcc
	v_add_co_u32_e32 v42, vcc, s20, v10
	s_ashr_i32 s6, s38, 31
	s_nop 0
	v_addc_co_u32_e32 v43, vcc, 0, v11, vcc
	v_add_co_u32_e32 v46, vcc, s21, v10
	s_add_u32 s0, s10, s38
	s_nop 0
	v_addc_co_u32_e32 v47, vcc, 0, v11, vcc
	v_add_co_u32_e32 v50, vcc, s22, v10
	s_addc_u32 s1, s40, s6
	s_nop 0
	v_addc_co_u32_e32 v51, vcc, 0, v11, vcc
	v_add_co_u32_e32 v54, vcc, s23, v10
	v_lshl_add_u64 v[8:9], s[0:1], 0, v[2:3]
	s_nop 0
	v_addc_co_u32_e32 v55, vcc, 0, v11, vcc
	v_add_co_u32_e32 v58, vcc, s24, v10
	v_lshl_add_u64 v[6:7], v[8:9], 0, v[6:7]
	s_nop 0
	v_addc_co_u32_e32 v59, vcc, 0, v11, vcc
	v_add_co_u32_e32 v62, vcc, s25, v10
	s_addk_i32 s16, 0x200
	s_nop 0
	v_addc_co_u32_e32 v63, vcc, 0, v11, vcc
	v_add_co_u32_e32 v66, vcc, s26, v10
	s_cmpk_gt_i32 s16, 0x5ff
	s_nop 0
	v_addc_co_u32_e32 v67, vcc, 0, v11, vcc
	v_add_co_u32_e32 v70, vcc, s27, v10
	s_waitcnt vmcnt(0)
	v_div_scale_f32 v29, s[0:1], v30, v30, s18
	v_addc_co_u32_e32 v71, vcc, 0, v11, vcc
	v_add_co_u32_e32 v74, vcc, s28, v10
	v_rcp_f32_e32 v105, v29
	s_nop 0
	v_addc_co_u32_e32 v75, vcc, 0, v11, vcc
	v_add_co_u32_e32 v78, vcc, s29, v10
	v_div_scale_f32 v103, s[0:1], v33, v33, s18
	s_nop 0
	v_addc_co_u32_e32 v79, vcc, 0, v11, vcc
	v_add_co_u32_e32 v82, vcc, s30, v10
	v_fma_f32 v109, -v29, v105, 1.0
	s_nop 0
	v_addc_co_u32_e32 v83, vcc, 0, v11, vcc
	v_add_co_u32_e32 v86, vcc, s31, v10
	v_rcp_f32_e32 v108, v103
	s_nop 0
	v_addc_co_u32_e32 v87, vcc, 0, v11, vcc
	v_add_co_u32_e32 v90, vcc, s34, v10
	v_fmac_f32_e32 v105, v109, v105
	s_nop 0
	v_addc_co_u32_e32 v91, vcc, 0, v11, vcc
	v_add_co_u32_e32 v94, vcc, s35, v10
	v_div_scale_f32 v102, s[8:9], s18, v32, s18
	s_nop 0
	v_addc_co_u32_e32 v95, vcc, 0, v11, vcc
	global_load_dwordx4 v[34:37], v[10:11], off nt
	global_load_dwordx4 v[38:41], v[12:13], off offset:3072 nt
	s_nop 0
	global_load_dwordx4 v[42:45], v[42:43], off offset:2048 nt
	s_nop 0
	global_load_dwordx4 v[46:49], v[46:47], off offset:1024 nt
	s_nop 0
	global_load_dwordx4 v[50:53], v[50:51], off nt
	s_nop 0
	global_load_dwordx4 v[54:57], v[54:55], off offset:3072 nt
	s_nop 0
	global_load_dwordx4 v[58:61], v[58:59], off offset:2048 nt
	s_nop 0
	global_load_dwordx4 v[62:65], v[62:63], off offset:1024 nt
	s_nop 0
	global_load_dwordx4 v[66:69], v[66:67], off nt
	s_nop 0
	global_load_dwordx4 v[70:73], v[70:71], off offset:3072 nt
	s_nop 0
	global_load_dwordx4 v[74:77], v[74:75], off offset:2048 nt
	s_nop 0
	global_load_dwordx4 v[78:81], v[78:79], off offset:1024 nt
	s_nop 0
	global_load_dwordx4 v[82:85], v[82:83], off nt
	s_nop 0
	global_load_dwordx4 v[86:89], v[86:87], off offset:3072 nt
	s_nop 0
	global_load_dwordx4 v[90:93], v[90:91], off offset:2048 nt
	s_nop 0
	global_load_dwordx4 v[94:97], v[94:95], off offset:1024 nt
	v_lshl_add_u64 v[12:13], v[8:9], 0, v[98:99]
	v_div_scale_f32 v99, s[0:1], v31, v31, s18
	v_rcp_f32_e32 v106, v99
	v_lshl_add_u64 v[10:11], v[8:9], 0, v[14:15]
	v_lshl_add_u64 v[14:15], v[8:9], 0, v[100:101]
	v_div_scale_f32 v101, s[0:1], v32, v32, s18
	v_rcp_f32_e32 v107, v101
	v_div_scale_f32 v98, vcc, s18, v30, s18
	v_fma_f32 v110, -v99, v106, 1.0
	v_div_scale_f32 v100, s[6:7], s18, v31, s18
	v_fmac_f32_e32 v106, v110, v106
	v_mul_f32_e32 v109, v98, v105
	v_fma_f32 v111, -v101, v107, 1.0
	v_mul_f32_e32 v110, v100, v106
	v_fma_f32 v113, -v29, v109, v98
	v_fmac_f32_e32 v107, v111, v107
	v_fma_f32 v114, -v99, v110, v100
	v_fmac_f32_e32 v109, v113, v105
	v_fma_f32 v112, -v103, v108, 1.0
	v_mul_f32_e32 v111, v102, v107
	v_fmac_f32_e32 v110, v114, v106
	v_fma_f32 v29, -v29, v109, v98
	v_div_scale_f32 v104, s[10:11], s18, v33, s18
	v_fmac_f32_e32 v108, v112, v108
	v_fma_f32 v115, -v101, v111, v102
	v_fma_f32 v98, -v99, v110, v100
	v_div_fmas_f32 v29, v29, v105, v109
	s_mov_b64 vcc, s[6:7]
	v_mul_f32_e32 v112, v104, v108
	v_fmac_f32_e32 v111, v115, v107
	v_div_fixup_f32 v29, v29, v30, s18
	v_div_fmas_f32 v98, v98, v106, v110
	v_cmp_lt_f32_e32 vcc, 0, v30
	v_fma_f32 v116, -v103, v112, v104
	v_fma_f32 v99, -v101, v111, v102
	v_cndmask_b32_e32 v29, 0, v29, vcc
	s_mov_b64 vcc, s[8:9]
	v_fmac_f32_e32 v112, v116, v108
	v_div_fixup_f32 v30, v98, v31, s18
	v_div_fmas_f32 v98, v99, v107, v111
	v_cmp_lt_f32_e32 vcc, 0, v31
	v_fma_f32 v100, -v103, v112, v104
	v_div_fixup_f32 v31, v98, v32, s18
	v_cndmask_b32_e32 v30, 0, v30, vcc
	s_mov_b64 vcc, s[10:11]
	v_div_fmas_f32 v98, v100, v108, v112
	v_cmp_lt_f32_e32 vcc, 0, v32
	v_div_fixup_f32 v32, v98, v33, s18
	s_waitcnt vmcnt(0) lgkmcnt(0)
; __device__ __forceinline__ unsigned pack_i8x4(float a, float b, float c, float d) {
;     const int ia = (int)rintf(fminf(fmaxf(a, -127.f), 127.f)), ib = (int)rintf(fminf(fmaxf(b, -127.f), 127.f)), ic = (int)rintf(fminf(fmaxf(c, -127.f), 127.f)), id = (int)rintf(fminf(fmaxf(d, -127.f), 127.f));
;     return (unsigned)(ia & 0xff) | ((unsigned)(ib & 0xff) << 8) | ((unsigned)(ic & 0xff) << 16) | ((unsigned)(id & 0xff) << 24);
; }
; __device__ __forceinline__ void cvt_item_i8(const float* src, int ld, int k0, int c0, unsigned char* dst, int Kd, int drow0, const float* cmx  , unsigned char* scr, int lane) {
;     const int c = lane & 7, q = lane >> 3;
;     const f32x4 cm = *(const f32x4*)(cmx + 4 * c);
;     f32x4 inv; inv[0] = cm[0] > 0.f ? 127.f / cm[0] : 0.f; inv[1] = cm[1] > 0.f ? 127.f / cm[1] : 0.f; inv[2] = cm[2] > 0.f ? 127.f / cm[2] : 0.f; inv[3] = cm[3] > 0.f ? 127.f / cm[3] : 0.f;
;     f32x4 v[4][4];
; #pragma unroll
;     for (int g = 0; g < 4; ++g)
; #pragma unroll
;         for (int j = 0; j < 4; ++j) v[g][j] = __builtin_nontemporal_load((const f32x4*)(src + (size_t)(k0 + 32 * g + 4 * q + j) * ld + c0 + 4 * c));
; #pragma unroll
;     for (int g = 0; g < 4; ++g)
; #pragma unroll
;         for (int i = 0; i < 4; ++i) *(unsigned*)(scr + (4 * c + i) * 132 + 32 * g + 4 * q) = pack_i8x4(v[g][0][i] * inv[i], v[g][1][i] * inv[i], v[g][2][i] * inv[i], v[g][3][i] * inv[i]);
	v_mul_f32_e32 v34, v34, v29
	v_mul_f32_e32 v38, v29, v38
	v_mul_f32_e32 v42, v29, v42
	v_mul_f32_e32 v46, v29, v46
	v_mul_f32_e32 v50, v29, v50
	v_mul_f32_e32 v54, v29, v54
	v_mul_f32_e32 v58, v29, v58
	v_mul_f32_e32 v62, v29, v62
	v_mul_f32_e32 v66, v29, v66
	v_mul_f32_e32 v70, v29, v70
	v_mul_f32_e32 v74, v29, v74
	v_mul_f32_e32 v78, v29, v78
	v_mul_f32_e32 v82, v29, v82
	v_mul_f32_e32 v86, v29, v86
	v_cndmask_b32_e32 v31, 0, v31, vcc
	v_med3_f32 v34, v34, s36, v20
	v_med3_f32 v38, v38, s36, v20
	v_med3_f32 v42, v42, s36, v20
	v_med3_f32 v46, v46, s36, v20
	v_mul_f32_e32 v39, v30, v39
	v_mul_f32_e32 v43, v30, v43
	v_mul_f32_e32 v47, v30, v47
	v_med3_f32 v50, v50, s36, v20
	v_med3_f32 v54, v54, s36, v20
	v_mul_f32_e32 v55, v30, v55
	v_cmp_lt_f32_e32 vcc, 0, v33
	v_mul_f32_e32 v90, v29, v90
	v_mul_f32_e32 v35, v35, v30
	v_med3_f32 v58, v58, s36, v20
	v_med3_f32 v62, v62, s36, v20
	v_mul_f32_e32 v51, v30, v51
	v_mul_f32_e32 v59, v30, v59
	v_mul_f32_e32 v63, v30, v63
	v_med3_f32 v66, v66, s36, v20
	v_med3_f32 v70, v70, s36, v20
	v_med3_f32 v74, v74, s36, v20
	v_med3_f32 v78, v78, s36, v20
	v_mul_f32_e32 v71, v30, v71
	v_mul_f32_e32 v79, v30, v79
	v_med3_f32 v82, v82, s36, v20
	v_med3_f32 v86, v86, s36, v20
	v_mul_f32_e32 v87, v30, v87
	v_cndmask_b32_e32 v32, 0, v32, vcc
	v_rndne_f32_e32 v33, v34
	v_rndne_f32_e32 v34, v38
	v_rndne_f32_e32 v38, v42
	v_rndne_f32_e32 v42, v46
	v_med3_f32 v39, v39, s36, v20
	v_med3_f32 v43, v43, s36, v20
	v_med3_f32 v46, v47, s36, v20
	v_mul_f32_e32 v40, v31, v40
	v_mul_f32_e32 v47, v31, v48
	v_rndne_f32_e32 v48, v50
	v_rndne_f32_e32 v50, v54
	v_med3_f32 v55, v55, s36, v20
	v_mul_f32_e32 v56, v31, v56
	v_mul_f32_e32 v29, v29, v94
	v_mul_f32_e32 v67, v30, v67
	v_mul_f32_e32 v75, v30, v75
	v_med3_f32 v90, v90, s36, v20
	v_mul_f32_e32 v83, v30, v83
	v_mul_f32_e32 v91, v30, v91
	v_med3_f32 v35, v35, s36, v20
	v_mul_f32_e32 v36, v36, v31
	v_mul_f32_e32 v44, v31, v44
	v_rndne_f32_e32 v54, v58
	v_rndne_f32_e32 v58, v62
	v_med3_f32 v51, v51, s36, v20
	v_med3_f32 v59, v59, s36, v20
	v_med3_f32 v62, v63, s36, v20
	v_mul_f32_e32 v52, v31, v52
	v_mul_f32_e32 v60, v31, v60
	v_mul_f32_e32 v63, v31, v64
	v_rndne_f32_e32 v64, v66
	v_rndne_f32_e32 v66, v70
	v_rndne_f32_e32 v70, v74
	v_rndne_f32_e32 v74, v78
	v_med3_f32 v71, v71, s36, v20
	v_med3_f32 v78, v79, s36, v20
	v_mul_f32_e32 v72, v31, v72
	v_mul_f32_e32 v79, v31, v80
	v_rndne_f32_e32 v80, v82
	v_rndne_f32_e32 v82, v86
	v_med3_f32 v87, v87, s36, v20
	v_mul_f32_e32 v88, v31, v88
	v_cvt_i32_f32_e32 v34, v34
	v_rndne_f32_e32 v39, v39
	v_rndne_f32_e32 v43, v43
	v_med3_f32 v40, v40, s36, v20
	v_mul_f32_e32 v41, v32, v41
	v_cvt_i32_f32_e32 v50, v50
	v_rndne_f32_e32 v55, v55
	v_med3_f32 v56, v56, s36, v20
	v_mul_f32_e32 v57, v32, v57
	v_med3_f32 v29, v29, s36, v20
	v_mul_f32_e32 v30, v30, v95
	v_med3_f32 v67, v67, s36, v20
	v_med3_f32 v75, v75, s36, v20
	v_mul_f32_e32 v68, v31, v68
	v_mul_f32_e32 v76, v31, v76
	v_rndne_f32_e32 v86, v90
	v_med3_f32 v83, v83, s36, v20
	v_med3_f32 v90, v91, s36, v20
	v_mul_f32_e32 v84, v31, v84
	v_mul_f32_e32 v91, v31, v92
	v_cvt_i32_f32_e32 v33, v33
	v_cvt_i32_f32_sdwa v38, v38 dst_sel:WORD_1 dst_unused:UNUSED_PAD src0_sel:DWORD
	v_rndne_f32_e32 v35, v35
	v_med3_f32 v36, v36, s36, v20
	v_med3_f32 v44, v44, s36, v20
	v_mul_f32_e32 v37, v37, v32
	v_mul_f32_e32 v45, v32, v45
	v_cvt_i32_f32_e32 v48, v48
	v_cvt_i32_f32_sdwa v54, v54 dst_sel:WORD_1 dst_unused:UNUSED_PAD src0_sel:DWORD
	v_rndne_f32_e32 v51, v51
	v_rndne_f32_e32 v59, v59
	v_med3_f32 v52, v52, s36, v20
	v_med3_f32 v60, v60, s36, v20
	v_mul_f32_e32 v53, v32, v53
	v_mul_f32_e32 v61, v32, v61
	v_cvt_i32_f32_e32 v66, v66
	v_rndne_f32_e32 v71, v71
	v_med3_f32 v72, v72, s36, v20
	v_mul_f32_e32 v73, v32, v73
	v_cvt_i32_f32_e32 v82, v82
	v_rndne_f32_e32 v87, v87
	v_med3_f32 v88, v88, s36, v20
	v_mul_f32_e32 v89, v32, v89
	v_cvt_i32_f32_e32 v39, v39
	v_cvt_i32_f32_sdwa v43, v43 dst_sel:WORD_1 dst_unused:UNUSED_PAD src0_sel:DWORD
	v_rndne_f32_e32 v40, v40
	v_med3_f32 v41, v41, s36, v20
	v_cvt_i32_f32_e32 v55, v55
	v_rndne_f32_e32 v56, v56
	v_med3_f32 v57, v57, s36, v20
	v_rndne_f32_e32 v29, v29
	v_med3_f32 v30, v30, s36, v20
	v_mul_f32_e32 v31, v31, v96
	v_cvt_i32_f32_sdwa v42, v42 dst_sel:BYTE_3 dst_unused:UNUSED_PAD src0_sel:DWORD
	v_rndne_f32_e32 v46, v46
	v_med3_f32 v47, v47, s36, v20
	v_mul_f32_e32 v49, v32, v49
	v_cvt_i32_f32_sdwa v58, v58 dst_sel:BYTE_3 dst_unused:UNUSED_PAD src0_sel:DWORD
	v_rndne_f32_e32 v62, v62
	v_med3_f32 v63, v63, s36, v20
	v_mul_f32_e32 v65, v32, v65
	v_cvt_i32_f32_e32 v64, v64
	v_cvt_i32_f32_sdwa v70, v70 dst_sel:WORD_1 dst_unused:UNUSED_PAD src0_sel:DWORD
	v_rndne_f32_e32 v67, v67
	v_rndne_f32_e32 v75, v75
	v_med3_f32 v68, v68, s36, v20
	v_med3_f32 v76, v76, s36, v20
	v_mul_f32_e32 v69, v32, v69
	v_mul_f32_e32 v77, v32, v77
	v_cvt_i32_f32_e32 v80, v80
	v_cvt_i32_f32_sdwa v86, v86 dst_sel:WORD_1 dst_unused:UNUSED_PAD src0_sel:DWORD
	v_rndne_f32_e32 v83, v83
	v_rndne_f32_e32 v90, v90
	v_med3_f32 v84, v84, s36, v20
	v_med3_f32 v91, v91, s36, v20
	v_mul_f32_e32 v85, v32, v85
	v_mul_f32_e32 v92, v32, v93
	v_cvt_i32_f32_e32 v35, v35
	v_rndne_f32_e32 v36, v36
	v_rndne_f32_e32 v44, v44
	v_med3_f32 v37, v37, s36, v20
	v_med3_f32 v45, v45, s36, v20
	v_cvt_i32_f32_e32 v51, v51
	v_cvt_i32_f32_sdwa v59, v59 dst_sel:WORD_1 dst_unused:UNUSED_PAD src0_sel:DWORD
	v_rndne_f32_e32 v52, v52
	v_rndne_f32_e32 v60, v60
	v_med3_f32 v53, v53, s36, v20
	v_med3_f32 v61, v61, s36, v20
	v_cvt_i32_f32_e32 v71, v71
	v_rndne_f32_e32 v72, v72
	v_med3_f32 v73, v73, s36, v20
	v_cvt_i32_f32_e32 v87, v87
	v_rndne_f32_e32 v88, v88
	v_med3_f32 v89, v89, s36, v20
	v_cvt_i32_f32_e32 v40, v40
; __device__ __forceinline__ unsigned pack_i8x4(float a, float b, float c, float d) {
;     const int ia = (int)rintf(fminf(fmaxf(a, -127.f), 127.f)), ib = (int)rintf(fminf(fmaxf(b, -127.f), 127.f)), ic = (int)rintf(fminf(fmaxf(c, -127.f), 127.f)), id = (int)rintf(fminf(fmaxf(d, -127.f), 127.f));
;     return (unsigned)(ia & 0xff) | ((unsigned)(ib & 0xff) << 8) | ((unsigned)(ic & 0xff) << 16) | ((unsigned)(id & 0xff) << 24);
; }
; __device__ __forceinline__ void cvt_item_i8(const float* src, int ld, int k0, int c0, unsigned char* dst, int Kd, int drow0, const float* cmx  , unsigned char* scr, int lane) {
;     const int c = lane & 7, q = lane >> 3;
;     const f32x4 cm = *(const f32x4*)(cmx + 4 * c);
;     f32x4 inv; inv[0] = cm[0] > 0.f ? 127.f / cm[0] : 0.f; inv[1] = cm[1] > 0.f ? 127.f / cm[1] : 0.f; inv[2] = cm[2] > 0.f ? 127.f / cm[2] : 0.f; inv[3] = cm[3] > 0.f ? 127.f / cm[3] : 0.f;
;     f32x4 v[4][4];
; #pragma unroll
;     for (int g = 0; g < 4; ++g)
; #pragma unroll
;         for (int j = 0; j < 4; ++j) v[g][j] = __builtin_nontemporal_load((const f32x4*)(src + (size_t)(k0 + 32 * g + 4 * q + j) * ld + c0 + 4 * c));
; #pragma unroll
;     for (int g = 0; g < 4; ++g)
; #pragma unroll
;         for (int i = 0; i < 4; ++i) *(unsigned*)(scr + (4 * c + i) * 132 + 32 * g + 4 * q) = pack_i8x4(v[g][0][i] * inv[i], v[g][1][i] * inv[i], v[g][2][i] * inv[i], v[g][3][i] * inv[i]);
;     asm volatile("s_waitcnt lgkmcnt(0)" ::: "memory");
; #pragma unroll
;     for (int r = 0; r < 4; ++r) { const int n = 8 * r + (lane >> 3), ch = lane & 7; const unsigned char* p = scr + n * 132 + ch * 16;
;         u32x4 o; o.x = *(const unsigned*)(p); o.y = *(const unsigned*)(p + 4); o.z = *(const unsigned*)(p + 8); o.w = *(const unsigned*)(p + 12);
;         *(u32x4*)(dst + (size_t)(drow0 + n) * Kd + k0 + 16 * ch) = o; }
;     asm volatile("s_waitcnt lgkmcnt(0)" ::: "memory");
; }
	v_rndne_f32_e32 v41, v41
	v_cvt_i32_f32_e32 v56, v56
	v_rndne_f32_e32 v57, v57
	v_cvt_i32_f32_sdwa v74, v74 dst_sel:BYTE_3 dst_unused:UNUSED_PAD src0_sel:DWORD
	v_rndne_f32_e32 v78, v78
	v_med3_f32 v79, v79, s36, v20
	v_mul_f32_e32 v81, v32, v81
	v_cvt_i32_f32_sdwa v29, v29 dst_sel:BYTE_3 dst_unused:UNUSED_PAD src0_sel:DWORD
	v_rndne_f32_e32 v30, v30
	v_med3_f32 v31, v31, s36, v20
	v_mul_f32_e32 v32, v32, v97
	v_cvt_i32_f32_sdwa v46, v46 dst_sel:BYTE_3 dst_unused:UNUSED_PAD src0_sel:DWORD
	v_rndne_f32_e32 v47, v47
	v_med3_f32 v49, v49, s36, v20
	v_cvt_i32_f32_sdwa v62, v62 dst_sel:BYTE_3 dst_unused:UNUSED_PAD src0_sel:DWORD
	v_rndne_f32_e32 v63, v63
	v_med3_f32 v65, v65, s36, v20
	v_cvt_i32_f32_e32 v67, v67
	v_cvt_i32_f32_sdwa v75, v75 dst_sel:WORD_1 dst_unused:UNUSED_PAD src0_sel:DWORD
	v_rndne_f32_e32 v68, v68
	v_rndne_f32_e32 v76, v76
	v_med3_f32 v69, v69, s36, v20
	v_med3_f32 v77, v77, s36, v20
	v_cvt_i32_f32_e32 v83, v83
	v_cvt_i32_f32_sdwa v90, v90 dst_sel:WORD_1 dst_unused:UNUSED_PAD src0_sel:DWORD
	v_rndne_f32_e32 v84, v84
	v_rndne_f32_e32 v91, v91
	v_med3_f32 v85, v85, s36, v20
	v_med3_f32 v92, v92, s36, v20
	v_cvt_i32_f32_e32 v36, v36
	v_cvt_i32_f32_sdwa v44, v44 dst_sel:WORD_1 dst_unused:UNUSED_PAD src0_sel:DWORD
	v_rndne_f32_e32 v37, v37
	v_rndne_f32_e32 v45, v45
	v_cvt_i32_f32_e32 v52, v52
	v_cvt_i32_f32_sdwa v60, v60 dst_sel:WORD_1 dst_unused:UNUSED_PAD src0_sel:DWORD
	v_rndne_f32_e32 v53, v53
	v_rndne_f32_e32 v61, v61
	v_cvt_i32_f32_e32 v72, v72
	v_rndne_f32_e32 v73, v73
	v_cvt_i32_f32_e32 v88, v88
	v_rndne_f32_e32 v89, v89
	v_cvt_i32_f32_e32 v41, v41
	v_cvt_i32_f32_e32 v57, v57
	v_cvt_i32_f32_sdwa v78, v78 dst_sel:BYTE_3 dst_unused:UNUSED_PAD src0_sel:DWORD
	v_rndne_f32_e32 v79, v79
	v_med3_f32 v81, v81, s36, v20
	v_cvt_i32_f32_sdwa v30, v30 dst_sel:BYTE_3 dst_unused:UNUSED_PAD src0_sel:DWORD
	v_rndne_f32_e32 v31, v31
	v_med3_f32 v32, v32, s36, v20
	v_cvt_i32_f32_sdwa v47, v47 dst_sel:BYTE_3 dst_unused:UNUSED_PAD src0_sel:DWORD
	v_rndne_f32_e32 v49, v49
	v_cvt_i32_f32_sdwa v63, v63 dst_sel:BYTE_3 dst_unused:UNUSED_PAD src0_sel:DWORD
	v_rndne_f32_e32 v65, v65
	v_cvt_i32_f32_e32 v68, v68
	v_cvt_i32_f32_sdwa v76, v76 dst_sel:WORD_1 dst_unused:UNUSED_PAD src0_sel:DWORD
	v_rndne_f32_e32 v69, v69
	v_rndne_f32_e32 v77, v77
	v_cvt_i32_f32_e32 v84, v84
	v_cvt_i32_f32_sdwa v91, v91 dst_sel:WORD_1 dst_unused:UNUSED_PAD src0_sel:DWORD
	v_rndne_f32_e32 v85, v85
	v_rndne_f32_e32 v92, v92
	v_cvt_i32_f32_e32 v37, v37
	v_cvt_i32_f32_sdwa v45, v45 dst_sel:WORD_1 dst_unused:UNUSED_PAD src0_sel:DWORD
	v_cvt_i32_f32_e32 v53, v53
	v_cvt_i32_f32_sdwa v61, v61 dst_sel:WORD_1 dst_unused:UNUSED_PAD src0_sel:DWORD
	v_cvt_i32_f32_e32 v73, v73
	v_cvt_i32_f32_e32 v89, v89
	v_lshlrev_b32_e32 v34, 8, v34
	v_lshlrev_b32_e32 v50, 8, v50
	v_cvt_i32_f32_sdwa v79, v79 dst_sel:BYTE_3 dst_unused:UNUSED_PAD src0_sel:DWORD
	v_rndne_f32_e32 v81, v81
	v_cvt_i32_f32_sdwa v31, v31 dst_sel:BYTE_3 dst_unused:UNUSED_PAD src0_sel:DWORD
	v_rndne_f32_e32 v32, v32
	v_cvt_i32_f32_sdwa v49, v49 dst_sel:BYTE_3 dst_unused:UNUSED_PAD src0_sel:DWORD
	v_cvt_i32_f32_sdwa v65, v65 dst_sel:BYTE_3 dst_unused:UNUSED_PAD src0_sel:DWORD
	v_cvt_i32_f32_e32 v69, v69
	v_cvt_i32_f32_sdwa v77, v77 dst_sel:WORD_1 dst_unused:UNUSED_PAD src0_sel:DWORD
	v_cvt_i32_f32_e32 v85, v85
	v_cvt_i32_f32_sdwa v92, v92 dst_sel:WORD_1 dst_unused:UNUSED_PAD src0_sel:DWORD
	v_and_b32_e32 v38, 0xff0000, v38
	v_and_b32_e32 v54, 0xff0000, v54
	v_lshlrev_b32_e32 v66, 8, v66
	v_lshlrev_b32_e32 v82, 8, v82
	v_perm_b32 v33, v34, v33, s37
	v_lshlrev_b32_e32 v34, 8, v39
	v_and_b32_e32 v39, 0xff0000, v43
	v_perm_b32 v43, v50, v48, s37
	v_lshlrev_b32_e32 v48, 8, v55
	v_cvt_i32_f32_sdwa v81, v81 dst_sel:BYTE_3 dst_unused:UNUSED_PAD src0_sel:DWORD
	v_cvt_i32_f32_sdwa v32, v32 dst_sel:BYTE_3 dst_unused:UNUSED_PAD src0_sel:DWORD
	v_and_b32_e32 v70, 0xff0000, v70
	v_and_b32_e32 v86, 0xff0000, v86
	v_and_b32_e32 v50, 0xff0000, v59
	v_perm_b32 v55, v66, v64, s37
	v_lshlrev_b32_e32 v59, 8, v71
	v_perm_b32 v66, v82, v80, s37
	v_lshlrev_b32_e32 v71, 8, v87
	v_or3_b32 v33, v33, v38, v42
	v_perm_b32 v34, v34, v35, s37
	v_lshlrev_b32_e32 v35, 8, v40
	v_or3_b32 v40, v43, v54, v58
	v_perm_b32 v42, v48, v51, s37
	v_lshlrev_b32_e32 v43, 8, v56
	v_and_b32_e32 v64, 0xff0000, v75
	v_and_b32_e32 v75, 0xff0000, v90
	v_and_b32_e32 v38, 0xff0000, v44
	v_and_b32_e32 v44, 0xff0000, v60
	v_or3_b32 v48, v55, v70, v74
	v_perm_b32 v51, v59, v67, s37
	v_lshlrev_b32_e32 v54, 8, v72
	v_or3_b32 v29, v66, v86, v29
	v_perm_b32 v56, v71, v83, s37
	v_lshlrev_b32_e32 v58, 8, v88
	v_or3_b32 v34, v34, v39, v46
	v_perm_b32 v35, v35, v36, s37
	v_lshlrev_b32_e32 v36, 8, v41
	ds_write2_b32 v21, v33, v40 offset1:8
	v_or3_b32 v33, v42, v50, v62
	v_perm_b32 v40, v43, v52, s37
	v_lshlrev_b32_e32 v41, 8, v57
	v_and_b32_e32 v55, 0xff0000, v76
	v_and_b32_e32 v59, 0xff0000, v91
	v_and_b32_e32 v39, 0xff0000, v45
	v_and_b32_e32 v42, 0xff0000, v61
	v_or3_b32 v43, v51, v64, v78
	v_perm_b32 v45, v54, v68, s37
	v_lshlrev_b32_e32 v46, 8, v73
	ds_write2_b32 v21, v48, v29 offset0:16 offset1:24
	v_or3_b32 v29, v56, v75, v30
	v_perm_b32 v30, v58, v84, s37
	v_lshlrev_b32_e32 v48, 8, v89
	v_or3_b32 v35, v35, v38, v47
	v_perm_b32 v36, v36, v37, s37
	ds_write2_b32 v21, v34, v33 offset0:33 offset1:41
	v_or3_b32 v33, v40, v44, v63
	v_perm_b32 v34, v41, v53, s37
	v_and_b32_e32 v50, 0xff0000, v77
	v_and_b32_e32 v51, 0xff0000, v92
	v_or3_b32 v37, v45, v55, v79
	v_perm_b32 v38, v46, v69, s37
	ds_write2_b32 v21, v43, v29 offset0:49 offset1:57
	v_or3_b32 v29, v30, v59, v31
	v_perm_b32 v30, v48, v85, s37
	v_or3_b32 v31, v36, v39, v49
	ds_write2_b32 v21, v35, v33 offset0:66 offset1:74
	v_or3_b32 v33, v34, v42, v65
	v_or3_b32 v34, v38, v50, v81
	ds_write2_b32 v21, v37, v29 offset0:82 offset1:90
	v_or3_b32 v29, v30, v51, v32
	ds_write2_b32 v21, v31, v33 offset0:99 offset1:107
	ds_write2_b32 v21, v34, v29 offset0:115 offset1:123
	s_waitcnt lgkmcnt(0)
	ds_read2_b32 v[30:31], v22 offset1:1
	ds_read2_b32 v[32:33], v22 offset0:2 offset1:3
	ds_read2_b32 v[34:35], v23 offset1:1
	ds_read2_b32 v[36:37], v24 offset1:1
	ds_read2_b32 v[38:39], v25 offset1:1
	ds_read2_b32 v[40:41], v26 offset1:1
	ds_read2_b32 v[42:43], v27 offset1:1
	ds_read2_b32 v[44:45], v28 offset1:1
	s_waitcnt lgkmcnt(6)
	global_store_dwordx4 v[10:11], v[30:33], off
	s_waitcnt lgkmcnt(4)
	global_store_dwordx4 v[12:13], v[34:37], off
	s_waitcnt lgkmcnt(2)
	global_store_dwordx4 v[14:15], v[38:41], off
	s_waitcnt lgkmcnt(0)
	global_store_dwordx4 v[6:7], v[42:45], off
	s_waitcnt lgkmcnt(0)
	s_cbranch_scc0 .LBB0_1405

; __device__ __forceinline__ void cvt_item_i8(const float* src, int ld, int k0, int c0, unsigned char* dst, int Kd, int drow0, const float* cmx  , unsigned char* scr, int lane) {
;     const int c = lane & 7, q = lane >> 3;
;     const f32x4 cm = *(const f32x4*)(cmx + 4 * c);
;     f32x4 inv; inv[0] = cm[0] > 0.f ? 127.f / cm[0] : 0.f; inv[1] = cm[1] > 0.f ? 127.f / cm[1] : 0.f; inv[2] = cm[2] > 0.f ? 127.f / cm[2] : 0.f; inv[3] = cm[3] > 0.f ? 127.f / cm[3] : 0.f;
;     f32x4 v[4][4];
; #pragma unroll
;     for (int g = 0; g < 4; ++g)
; #pragma unroll
;         for (int j = 0; j < 4; ++j) v[g][j] = __builtin_nontemporal_load((const f32x4*)(src + (size_t)(k0 + 32 * g + 4 * q + j) * ld + c0 + 4 * c));
; template <int GRP>
; __device__ __forceinline__ void conv_item(Frame& F, int r) {
;     ...
;     else { constexpr int KBN = (GRP == 3) ? 16 : CMS_KB, I_E = KBN * 88; const int up = r / (8 * I_E); r %= (8 * I_E); const int e = r / I_E; r %= I_E; const int kb = r / 88, nb = r % 88, n0 = nb * 32, drow = (n0 >> 7) * 256 + up * 128 + (n0 & 127);
;         if (GRP == 3) cvt_item_i8(inptr(F, up ? IN_MU : IN_MG) + (size_t)e * D * DFE, DFE, kb * 128, n0, ws + WS_MGU + (size_t)e * 2 * DFE * D, D, drow, cmx + 2 * DFF + e * 2 * DFE + drow, scr, F.lane);
; template <int GRP>
; __device__ __forceinline__ void y_phase(Frame& F, const MW& W) {
;     ...
;         if (F.tid >= 256) {
;             if (base == (int)blockIdx.x * 256 && F.G == 256) {
; #pragma unroll 1
;                 for (int k = 0; k < YK; ++k) conv_item<GRP>(F, (int)blockIdx.x * 4 + (F.wave - 4) + k * 1024);
;             }
.LBB0_1616:
	s_add_i32 s8, s77, s16
	s_add_i32 s10, s8, 0xffc
	s_add_i32 s11, s8, 0x3bfb
	s_mul_hi_i32 s8, s10, 0x2e8ba2e9
	s_lshr_b32 s31, s8, 31
	s_ashr_i32 s8, s8, 11
	s_add_i32 s8, s8, s31
	s_mul_i32 s31, s8, 0x2c00
	s_lshl_b32 s34, s8, 7
	s_sub_i32 s8, s10, s31
	s_mul_i32 s10, s8, 0xba3
	s_lshr_b32 s31, s10, 31
	s_ashr_i32 s10, s10, 22
	s_add_i32 s10, s10, s31
	s_mul_i32 s31, s10, 0x580
	s_sext_i32_i16 s10, s10
	s_sub_i32 s8, s8, s31
	s_mul_hi_i32 s31, s10, 0x1600000
	s_mul_i32 s35, s10, 0x1600000
	s_mul_hi_i32 s36, s10, 0xb00000
	s_mul_i32 s37, s10, 0xb00000
	s_mul_hi_i32 s38, s10, 0x5800
	s_mul_i32 s39, s10, 0x5800
	s_sext_i32_i16 s10, s8
	s_mulk_i32 s10, 0xba3
	s_lshr_b32 s40, s10, 31
	s_ashr_i32 s10, s10, 18
	s_add_i32 s10, s10, s40
	s_sext_i32_i16 s40, s10
	s_mulk_i32 s10, 0x58
	s_sub_i32 s8, s8, s10
	s_sext_i32_i16 s10, s8
	s_lshl_b32 s8, s10, 5
	s_lshl_b32 s10, s10, 6
	s_and_b32 s10, s10, 0xffffff00
	s_and_b32 s41, s8, 0x60
	s_add_i32 s10, s10, s34
	s_or_b32 s10, s10, s41
	s_movk_i32 s9, 0xa0
	s_cmpk_lt_u32 s11, 0x57ff
	s_cselect_b32 s9, s9, 0xa8
	v_or_b32_e32 v128, s10, v216
	s_add_i32 s9, s9, 0
	v_ashrrev_i32_e32 v129, 31, v128
	s_add_i32 s9, s9, 0x20200
	v_lshlrev_b64 v[192:193], 11, v[128:129]
	v_mov_b32_e32 v128, s9
	ds_read_b64 v[128:129], v128
	v_or_b32_e32 v126, s10, v131
	v_or_b32_e32 v140, s10, v217
	v_or_b32_e32 v142, s10, v218
	v_ashrrev_i32_e32 v141, 31, v140
	s_waitcnt lgkmcnt(0)
	v_readfirstlane_b32 s9, v128
	v_readfirstlane_b32 s11, v129
	s_add_u32 s34, s9, s35
	s_addc_u32 s31, s11, s31
	s_lshl_b32 s35, s40, 7
	s_add_u32 s37, s4, s37
	s_addc_u32 s36, s49, s36
	s_add_u32 s9, s96, s39
	s_addc_u32 s38, s97, s38
	s_ashr_i32 s11, s10, 31
	s_lshl_b64 s[10:11], s[10:11], 2
	s_add_u32 s10, s9, s10
	s_addc_u32 s11, s38, s11
	s_ashr_i32 s9, s8, 31
	s_lshl_b64 s[8:9], s[8:9], 2
	v_or_b32_e32 v128, s35, v135
	s_add_u32 s8, s34, s8
	v_mul_i32_i24_e32 v128, 0x2c00, v128
	s_addc_u32 s9, s31, s9
	v_lshlrev_b64 v[236:237], 11, v[140:141]
	v_ashrrev_i32_e32 v129, 31, v128
	v_lshl_add_u64 v[140:141], s[8:9], 0, v[132:133]
	s_movk_i32 s12, 0x2000
	v_ashrrev_i32_e32 v127, 31, v126
	v_ashrrev_i32_e32 v143, 31, v142
	v_lshl_add_u64 v[140:141], v[140:141], 0, v[128:129]
	v_lshlrev_b64 v[144:145], 11, v[126:127]
	v_lshlrev_b64 v[126:127], 11, v[142:143]
	v_add_co_u32_e32 v142, vcc, s12, v140
	s_movk_i32 s13, 0x5000
	s_nop 0
	v_addc_co_u32_e32 v143, vcc, 0, v141, vcc
	v_add_co_u32_e32 v164, vcc, s13, v140
	s_mov_b32 s18, 0x8000
	s_nop 0
	v_addc_co_u32_e32 v165, vcc, 0, v141, vcc
	v_add_co_u32_e32 v168, vcc, s18, v140
	s_mov_b32 s19, 0x58000
	s_nop 0
	v_addc_co_u32_e32 v169, vcc, 0, v141, vcc
	v_add_co_u32_e32 v172, vcc, s19, v140
	s_mov_b32 s20, 0x5a000
	s_nop 0
	v_addc_co_u32_e32 v173, vcc, 0, v141, vcc
	v_add_co_u32_e32 v176, vcc, s20, v140
	s_mov_b32 s21, 0x5d000
	s_nop 0
	v_addc_co_u32_e32 v177, vcc, 0, v141, vcc
	v_add_co_u32_e32 v180, vcc, s21, v140
	s_mov_b32 s22, 0x60000
	s_nop 0
	v_addc_co_u32_e32 v181, vcc, 0, v141, vcc
	global_load_dwordx4 v[152:155], v132, s[10:11]
	v_add_co_u32_e32 v184, vcc, s22, v140
	s_mov_b32 s23, 0xb0000
	s_nop 0
	v_addc_co_u32_e32 v185, vcc, 0, v141, vcc
	v_add_co_u32_e32 v188, vcc, s23, v140
	s_mov_b32 s24, 0xb2000
	s_nop 0
	v_addc_co_u32_e32 v189, vcc, 0, v141, vcc
	v_add_co_u32_e32 v196, vcc, s24, v140
	s_mov_b32 s25, 0xb5000
	s_nop 0
	v_addc_co_u32_e32 v197, vcc, 0, v141, vcc
	v_add_co_u32_e32 v200, vcc, s25, v140
	s_mov_b32 s26, 0xb8000
	s_nop 0
	v_addc_co_u32_e32 v201, vcc, 0, v141, vcc
	v_add_co_u32_e32 v204, vcc, s26, v140
	s_mov_b32 s27, 0x108000
	s_nop 0
	v_addc_co_u32_e32 v205, vcc, 0, v141, vcc
	v_add_co_u32_e32 v208, vcc, s27, v140
	s_mov_b32 s28, 0x10a000
	s_nop 0
	v_addc_co_u32_e32 v209, vcc, 0, v141, vcc
	v_add_co_u32_e32 v212, vcc, s28, v140
	s_mov_b32 s29, 0x10d000
	s_nop 0
	v_addc_co_u32_e32 v213, vcc, 0, v141, vcc
	v_add_co_u32_e32 v228, vcc, s29, v140
	s_mov_b32 s30, 0x110000
	s_nop 0
	v_addc_co_u32_e32 v229, vcc, 0, v141, vcc
	v_add_co_u32_e32 v232, vcc, s30, v140
	s_ashr_i32 s10, s35, 31
	s_nop 0
	v_addc_co_u32_e32 v233, vcc, 0, v141, vcc
	global_load_dwordx4 v[156:159], v[140:141], off nt
	global_load_dwordx4 v[160:163], v[142:143], off offset:3072 nt
	s_nop 0
	global_load_dwordx4 v[164:167], v[164:165], off offset:2048 nt
	s_nop 0
	global_load_dwordx4 v[168:171], v[168:169], off offset:1024 nt
	s_nop 0
	global_load_dwordx4 v[172:175], v[172:173], off nt
	s_nop 0
	global_load_dwordx4 v[176:179], v[176:177], off offset:3072 nt
	s_nop 0
	global_load_dwordx4 v[180:183], v[180:181], off offset:2048 nt
	s_nop 0
	global_load_dwordx4 v[184:187], v[184:185], off offset:1024 nt
	s_nop 0
	global_load_dwordx4 v[188:191], v[188:189], off nt
	s_nop 0
	global_load_dwordx4 v[196:199], v[196:197], off offset:3072 nt
	s_nop 0
	global_load_dwordx4 v[200:203], v[200:201], off offset:2048 nt
	s_nop 0
	global_load_dwordx4 v[204:207], v[204:205], off offset:1024 nt
	s_nop 0
	global_load_dwordx4 v[208:211], v[208:209], off nt
	s_nop 0
	global_load_dwordx4 v[212:215], v[212:213], off offset:3072 nt
	s_nop 0
	global_load_dwordx4 v[228:231], v[228:229], off offset:2048 nt
	s_nop 0
	global_load_dwordx4 v[232:235], v[232:233], off offset:1024 nt
	s_add_u32 s8, s37, s35
	s_addc_u32 s9, s36, s10
	v_lshl_add_u64 v[128:129], s[8:9], 0, v[138:139]
	v_lshl_add_u64 v[142:143], v[128:129], 0, v[192:193]
	v_lshl_add_u64 v[140:141], v[128:129], 0, v[144:145]
	v_lshl_add_u64 v[144:145], v[128:129], 0, v[236:237]
	v_add_u32_e32 v146, 0x428, v220
	v_add_u32_e32 v147, 0x840, v220
	v_add_u32_e32 v148, 0x848, v220
	v_add_u32_e32 v149, 0xc60, v220
	v_add_u32_e32 v1, 0x420, v220
	v_add_u32_e32 v150, 0xc68, v220
	v_lshl_add_u64 v[126:127], v[128:129], 0, v[126:127]
	s_addk_i32 s16, 0x400
	s_cmp_eq_u32 s16, 0
	s_waitcnt vmcnt(0)
; __device__ __forceinline__ void cvt_item_i8(const float* src, int ld, int k0, int c0, unsigned char* dst, int Kd, int drow0, const float* cmx  , unsigned char* scr, int lane) {
;     ...
;     f32x4 inv; inv[0] = cm[0] > 0.f ? 127.f / cm[0] : 0.f; inv[1] = cm[1] > 0.f ? 127.f / cm[1] : 0.f; inv[2] = cm[2] > 0.f ? 127.f / cm[2] : 0.f; inv[3] = cm[3] > 0.f ? 127.f / cm[3] : 0.f;
;     f32x4 v[4][4];
; #pragma unroll
;     for (int g = 0; g < 4; ++g)
; #pragma unroll
;         for (int j = 0; j < 4; ++j) v[g][j] = __builtin_nontemporal_load((const f32x4*)(src + (size_t)(k0 + 32 * g + 4 * q + j) * ld + c0 + 4 * c));
; #pragma unroll
;     for (int g = 0; g < 4; ++g)
; #pragma unroll
;         for (int i = 0; i < 4; ++i) *(unsigned*)(scr + (4 * c + i) * 132 + 32 * g + 4 * q) = pack_i8x4(v[g][0][i] * inv[i], v[g][1][i] * inv[i], v[g][2][i] * inv[i], v[g][3][i] * inv[i]);
	v_div_scale_f32 v151, s[8:9], v152, v152, s15
	v_div_scale_f32 v193, s[8:9], v153, v153, s15
	v_rcp_f32_e32 v239, v151
	v_rcp_f32_e32 v240, v193
	v_div_scale_f32 v223, s[10:11], v154, v154, s15
	v_rcp_f32_e32 v241, v223
	v_div_scale_f32 v237, s[12:13], v155, v155, s15
	v_fma_f32 v243, -v151, v239, 1.0
	v_div_scale_f32 v192, vcc, s15, v152, s15
	v_rcp_f32_e32 v242, v237
	v_fma_f32 v244, -v193, v240, 1.0
	v_fmac_f32_e32 v239, v243, v239
	v_div_scale_f32 v195, s[8:9], s15, v153, s15
	v_fmac_f32_e32 v240, v244, v240
	v_mul_f32_e32 v243, v192, v239
	v_fma_f32 v245, -v223, v241, 1.0
	v_mul_f32_e32 v244, v195, v240
	v_fma_f32 v247, -v151, v243, v192
	v_div_scale_f32 v236, s[10:11], s15, v154, s15
	v_fmac_f32_e32 v241, v245, v241
	v_fma_f32 v248, -v193, v244, v195
	v_fmac_f32_e32 v243, v247, v239
	v_fma_f32 v246, -v237, v242, 1.0
	v_mul_f32_e32 v245, v236, v241
	v_fmac_f32_e32 v244, v248, v240
	v_fma_f32 v151, -v151, v243, v192
	v_div_scale_f32 v238, s[12:13], s15, v155, s15
	v_fmac_f32_e32 v242, v246, v242
	v_fma_f32 v249, -v223, v245, v236
	v_fma_f32 v192, -v193, v244, v195
	v_div_fmas_f32 v151, v151, v239, v243
	s_mov_b64 vcc, s[8:9]
	v_mul_f32_e32 v246, v238, v242
	v_fmac_f32_e32 v245, v249, v241
	v_div_fixup_f32 v151, v151, v152, s15
	v_div_fmas_f32 v192, v192, v240, v244
	v_cmp_lt_f32_e32 vcc, 0, v152
	v_fma_f32 v250, -v237, v246, v238
	v_fma_f32 v193, -v223, v245, v236
	v_cndmask_b32_e32 v151, 0, v151, vcc
	s_mov_b64 vcc, s[10:11]
	v_fmac_f32_e32 v246, v250, v242
	v_div_fixup_f32 v152, v192, v153, s15
	v_div_fmas_f32 v192, v193, v241, v245
	v_cmp_lt_f32_e32 vcc, 0, v153
	v_fma_f32 v195, -v237, v246, v238
	v_div_fixup_f32 v153, v192, v154, s15
	v_cndmask_b32_e32 v152, 0, v152, vcc
	s_mov_b64 vcc, s[12:13]
	v_div_fmas_f32 v192, v195, v242, v246
	s_waitcnt lgkmcnt(0)
	v_mul_f32_e32 v156, v156, v151
	v_mul_f32_e32 v160, v151, v160
	v_mul_f32_e32 v164, v151, v164
	v_mul_f32_e32 v168, v151, v168
	v_mul_f32_e32 v172, v151, v172
	v_mul_f32_e32 v176, v151, v176
	v_cmp_lt_f32_e32 vcc, 0, v154
	v_mul_f32_e32 v180, v151, v180
	v_mul_f32_e32 v184, v151, v184
	v_mul_f32_e32 v188, v151, v188
	v_mul_f32_e32 v193, v151, v196
	v_mul_f32_e32 v195, v151, v200
	v_mul_f32_e32 v196, v151, v204
	v_mul_f32_e32 v200, v151, v208
	v_mul_f32_e32 v204, v151, v212
	v_mul_f32_e32 v208, v151, v228
	v_cndmask_b32_e32 v153, 0, v153, vcc
	v_div_fixup_f32 v154, v192, v155, s15
	v_med3_f32 v156, v156, s3, v222
	v_med3_f32 v160, v160, s3, v222
	v_med3_f32 v164, v164, s3, v222
	v_med3_f32 v168, v168, s3, v222
	v_mul_f32_e32 v161, v152, v161
	v_mul_f32_e32 v165, v152, v165
	v_mul_f32_e32 v169, v152, v169
	v_med3_f32 v172, v172, s3, v222
	v_med3_f32 v176, v176, s3, v222
	v_mul_f32_e32 v177, v152, v177
	v_cmp_lt_f32_e32 vcc, 0, v155
	v_mul_f32_e32 v157, v157, v152
	v_med3_f32 v180, v180, s3, v222
	v_med3_f32 v184, v184, s3, v222
	v_mul_f32_e32 v173, v152, v173
	v_mul_f32_e32 v181, v152, v181
	v_mul_f32_e32 v185, v152, v185
	v_med3_f32 v188, v188, s3, v222
	v_med3_f32 v192, v193, s3, v222
	v_med3_f32 v193, v195, s3, v222
	v_med3_f32 v195, v196, s3, v222
	v_mul_f32_e32 v196, v152, v197
	v_mul_f32_e32 v197, v152, v201
	v_mul_f32_e32 v201, v152, v205
	v_med3_f32 v204, v204, s3, v222
	v_med3_f32 v205, v208, s3, v222
	v_mul_f32_e32 v208, v152, v209
	v_mul_f32_e32 v209, v152, v213
	v_mul_f32_e32 v212, v152, v229
	v_cndmask_b32_e32 v154, 0, v154, vcc
	v_rndne_f32_e32 v155, v156
	v_rndne_f32_e32 v156, v160
	v_rndne_f32_e32 v160, v164
	v_rndne_f32_e32 v164, v168
	v_med3_f32 v161, v161, s3, v222
	v_med3_f32 v165, v165, s3, v222
	v_med3_f32 v168, v169, s3, v222
	v_mul_f32_e32 v162, v153, v162
	v_mul_f32_e32 v169, v153, v170
	v_rndne_f32_e32 v170, v172
	v_rndne_f32_e32 v172, v176
	v_med3_f32 v177, v177, s3, v222
	v_mul_f32_e32 v178, v153, v178
	v_mul_f32_e32 v151, v151, v232
	v_mul_f32_e32 v189, v152, v189
	v_med3_f32 v200, v200, s3, v222
	v_med3_f32 v157, v157, s3, v222
	v_mul_f32_e32 v158, v158, v153
	v_mul_f32_e32 v166, v153, v166
	v_rndne_f32_e32 v176, v180
	v_rndne_f32_e32 v180, v184
	v_med3_f32 v173, v173, s3, v222
	v_med3_f32 v181, v181, s3, v222
	v_med3_f32 v184, v185, s3, v222
	v_mul_f32_e32 v174, v153, v174
	v_mul_f32_e32 v182, v153, v182
	v_mul_f32_e32 v185, v153, v186
	v_rndne_f32_e32 v186, v188
	v_rndne_f32_e32 v188, v192
	v_rndne_f32_e32 v192, v193
	v_rndne_f32_e32 v193, v195
	v_med3_f32 v195, v196, s3, v222
	v_med3_f32 v196, v197, s3, v222
	v_med3_f32 v197, v201, s3, v222
	v_mul_f32_e32 v198, v153, v198
	v_mul_f32_e32 v201, v153, v202
	v_mul_f32_e32 v202, v153, v206
	v_rndne_f32_e32 v204, v204
	v_med3_f32 v206, v208, s3, v222
	v_med3_f32 v208, v209, s3, v222
	v_med3_f32 v209, v212, s3, v222
	v_mul_f32_e32 v212, v153, v214
	v_cvt_i32_f32_e32 v156, v156
	v_rndne_f32_e32 v161, v161
	v_rndne_f32_e32 v165, v165
	v_med3_f32 v162, v162, s3, v222
	v_mul_f32_e32 v163, v154, v163
	v_cvt_i32_f32_e32 v172, v172
	v_rndne_f32_e32 v177, v177
	v_med3_f32 v178, v178, s3, v222
	v_mul_f32_e32 v179, v154, v179
	v_med3_f32 v151, v151, s3, v222
	v_mul_f32_e32 v152, v152, v233
	v_med3_f32 v189, v189, s3, v222
	v_mul_f32_e32 v190, v153, v190
	v_rndne_f32_e32 v200, v200
	v_rndne_f32_e32 v205, v205
	v_mul_f32_e32 v210, v153, v210
	v_mul_f32_e32 v213, v153, v230
	v_cvt_i32_f32_e32 v155, v155
	v_cvt_i32_f32_sdwa v160, v160 dst_sel:WORD_1 dst_unused:UNUSED_PAD src0_sel:DWORD
	v_rndne_f32_e32 v157, v157
	v_med3_f32 v158, v158, s3, v222
	v_med3_f32 v166, v166, s3, v222
	v_mul_f32_e32 v159, v159, v154
	v_mul_f32_e32 v167, v154, v167
	v_cvt_i32_f32_e32 v170, v170
	v_cvt_i32_f32_sdwa v176, v176 dst_sel:WORD_1 dst_unused:UNUSED_PAD src0_sel:DWORD
	v_rndne_f32_e32 v173, v173
	v_rndne_f32_e32 v181, v181
; __device__ __forceinline__ unsigned pack_i8x4(float a, float b, float c, float d) {
;     const int ia = (int)rintf(fminf(fmaxf(a, -127.f), 127.f)), ib = (int)rintf(fminf(fmaxf(b, -127.f), 127.f)), ic = (int)rintf(fminf(fmaxf(c, -127.f), 127.f)), id = (int)rintf(fminf(fmaxf(d, -127.f), 127.f));
;     return (unsigned)(ia & 0xff) | ((unsigned)(ib & 0xff) << 8) | ((unsigned)(ic & 0xff) << 16) | ((unsigned)(id & 0xff) << 24);
; }
; __device__ __forceinline__ void cvt_item_i8(const float* src, int ld, int k0, int c0, unsigned char* dst, int Kd, int drow0, const float* cmx  , unsigned char* scr, int lane) {
;     const int c = lane & 7, q = lane >> 3;
;     const f32x4 cm = *(const f32x4*)(cmx + 4 * c);
;     f32x4 inv; inv[0] = cm[0] > 0.f ? 127.f / cm[0] : 0.f; inv[1] = cm[1] > 0.f ? 127.f / cm[1] : 0.f; inv[2] = cm[2] > 0.f ? 127.f / cm[2] : 0.f; inv[3] = cm[3] > 0.f ? 127.f / cm[3] : 0.f;
;     f32x4 v[4][4];
; #pragma unroll
;     for (int g = 0; g < 4; ++g)
; #pragma unroll
;         for (int j = 0; j < 4; ++j) v[g][j] = __builtin_nontemporal_load((const f32x4*)(src + (size_t)(k0 + 32 * g + 4 * q + j) * ld + c0 + 4 * c));
; #pragma unroll
;     for (int g = 0; g < 4; ++g)
; #pragma unroll
;         for (int i = 0; i < 4; ++i) *(unsigned*)(scr + (4 * c + i) * 132 + 32 * g + 4 * q) = pack_i8x4(v[g][0][i] * inv[i], v[g][1][i] * inv[i], v[g][2][i] * inv[i], v[g][3][i] * inv[i]);
	v_med3_f32 v174, v174, s3, v222
	v_med3_f32 v182, v182, s3, v222
	v_mul_f32_e32 v175, v154, v175
	v_mul_f32_e32 v183, v154, v183
	v_cvt_i32_f32_e32 v188, v188
	v_rndne_f32_e32 v195, v195
	v_med3_f32 v198, v198, s3, v222
	v_mul_f32_e32 v199, v154, v199
	v_cvt_i32_f32_e32 v204, v204
	v_rndne_f32_e32 v208, v208
	v_med3_f32 v212, v212, s3, v222
	v_mul_f32_e32 v214, v154, v215
	v_cvt_i32_f32_e32 v161, v161
	v_cvt_i32_f32_sdwa v165, v165 dst_sel:WORD_1 dst_unused:UNUSED_PAD src0_sel:DWORD
	v_rndne_f32_e32 v162, v162
	v_med3_f32 v163, v163, s3, v222
	v_cvt_i32_f32_e32 v177, v177
	v_rndne_f32_e32 v178, v178
	v_med3_f32 v179, v179, s3, v222
	v_rndne_f32_e32 v151, v151
	v_med3_f32 v152, v152, s3, v222
	v_mul_f32_e32 v153, v153, v234
	v_cvt_i32_f32_sdwa v164, v164 dst_sel:BYTE_3 dst_unused:UNUSED_PAD src0_sel:DWORD
	v_rndne_f32_e32 v168, v168
	v_med3_f32 v169, v169, s3, v222
	v_mul_f32_e32 v171, v154, v171
	v_cvt_i32_f32_sdwa v180, v180 dst_sel:BYTE_3 dst_unused:UNUSED_PAD src0_sel:DWORD
	v_rndne_f32_e32 v184, v184
	v_med3_f32 v185, v185, s3, v222
	v_mul_f32_e32 v187, v154, v187
	v_cvt_i32_f32_e32 v186, v186
	v_cvt_i32_f32_sdwa v192, v192 dst_sel:WORD_1 dst_unused:UNUSED_PAD src0_sel:DWORD
	v_rndne_f32_e32 v189, v189
	v_rndne_f32_e32 v196, v196
	v_med3_f32 v190, v190, s3, v222
	v_med3_f32 v201, v201, s3, v222
	v_mul_f32_e32 v191, v154, v191
	v_mul_f32_e32 v203, v154, v203
	v_cvt_i32_f32_e32 v200, v200
	v_cvt_i32_f32_sdwa v205, v205 dst_sel:WORD_1 dst_unused:UNUSED_PAD src0_sel:DWORD
	v_rndne_f32_e32 v206, v206
	v_rndne_f32_e32 v209, v209
	v_med3_f32 v210, v210, s3, v222
	v_med3_f32 v213, v213, s3, v222
	v_mul_f32_e32 v211, v154, v211
	v_mul_f32_e32 v215, v154, v231
	v_cvt_i32_f32_e32 v157, v157
	v_rndne_f32_e32 v158, v158
	v_rndne_f32_e32 v166, v166
	v_med3_f32 v159, v159, s3, v222
	v_med3_f32 v167, v167, s3, v222
	v_cvt_i32_f32_e32 v173, v173
	v_cvt_i32_f32_sdwa v181, v181 dst_sel:WORD_1 dst_unused:UNUSED_PAD src0_sel:DWORD
	v_rndne_f32_e32 v174, v174
	v_rndne_f32_e32 v182, v182
	v_med3_f32 v175, v175, s3, v222
	v_med3_f32 v183, v183, s3, v222
	v_cvt_i32_f32_e32 v195, v195
	v_rndne_f32_e32 v198, v198
	v_med3_f32 v199, v199, s3, v222
	v_cvt_i32_f32_e32 v208, v208
	v_rndne_f32_e32 v212, v212
	v_med3_f32 v214, v214, s3, v222
	v_cvt_i32_f32_e32 v162, v162
	v_rndne_f32_e32 v163, v163
	v_cvt_i32_f32_e32 v178, v178
	v_rndne_f32_e32 v179, v179
	v_cvt_i32_f32_sdwa v193, v193 dst_sel:BYTE_3 dst_unused:UNUSED_PAD src0_sel:DWORD
	v_rndne_f32_e32 v197, v197
	v_med3_f32 v202, v202, s3, v222
	v_mul_f32_e32 v207, v154, v207
	v_cvt_i32_f32_sdwa v151, v151 dst_sel:BYTE_3 dst_unused:UNUSED_PAD src0_sel:DWORD
	v_rndne_f32_e32 v152, v152
	v_med3_f32 v153, v153, s3, v222
	v_mul_f32_e32 v154, v154, v235
	v_cvt_i32_f32_sdwa v168, v168 dst_sel:BYTE_3 dst_unused:UNUSED_PAD src0_sel:DWORD
	v_rndne_f32_e32 v169, v169
	v_med3_f32 v171, v171, s3, v222
	v_cvt_i32_f32_sdwa v184, v184 dst_sel:BYTE_3 dst_unused:UNUSED_PAD src0_sel:DWORD
	v_rndne_f32_e32 v185, v185
	v_med3_f32 v187, v187, s3, v222
	v_cvt_i32_f32_e32 v189, v189
	v_cvt_i32_f32_sdwa v196, v196 dst_sel:WORD_1 dst_unused:UNUSED_PAD src0_sel:DWORD
	v_rndne_f32_e32 v190, v190
	v_rndne_f32_e32 v201, v201
	v_med3_f32 v191, v191, s3, v222
	v_med3_f32 v203, v203, s3, v222
	v_cvt_i32_f32_e32 v206, v206
	v_cvt_i32_f32_sdwa v209, v209 dst_sel:WORD_1 dst_unused:UNUSED_PAD src0_sel:DWORD
	v_rndne_f32_e32 v210, v210
	v_rndne_f32_e32 v213, v213
	v_med3_f32 v211, v211, s3, v222
	v_med3_f32 v215, v215, s3, v222
	v_cvt_i32_f32_e32 v158, v158
	v_cvt_i32_f32_sdwa v166, v166 dst_sel:WORD_1 dst_unused:UNUSED_PAD src0_sel:DWORD
	v_rndne_f32_e32 v159, v159
	v_rndne_f32_e32 v167, v167
	v_cvt_i32_f32_e32 v174, v174
	v_cvt_i32_f32_sdwa v182, v182 dst_sel:WORD_1 dst_unused:UNUSED_PAD src0_sel:DWORD
	v_rndne_f32_e32 v175, v175
	v_rndne_f32_e32 v183, v183
	v_cvt_i32_f32_e32 v198, v198
	v_rndne_f32_e32 v199, v199
	v_cvt_i32_f32_e32 v212, v212
	v_rndne_f32_e32 v214, v214
	v_cvt_i32_f32_e32 v163, v163
	v_cvt_i32_f32_e32 v179, v179
	v_cvt_i32_f32_sdwa v197, v197 dst_sel:BYTE_3 dst_unused:UNUSED_PAD src0_sel:DWORD
	v_rndne_f32_e32 v202, v202
	v_med3_f32 v207, v207, s3, v222
	v_cvt_i32_f32_sdwa v152, v152 dst_sel:BYTE_3 dst_unused:UNUSED_PAD src0_sel:DWORD
	v_rndne_f32_e32 v153, v153
	v_med3_f32 v154, v154, s3, v222
	v_cvt_i32_f32_sdwa v169, v169 dst_sel:BYTE_3 dst_unused:UNUSED_PAD src0_sel:DWORD
	v_rndne_f32_e32 v171, v171
	v_cvt_i32_f32_sdwa v185, v185 dst_sel:BYTE_3 dst_unused:UNUSED_PAD src0_sel:DWORD
	v_rndne_f32_e32 v187, v187
	v_cvt_i32_f32_e32 v190, v190
	v_cvt_i32_f32_sdwa v201, v201 dst_sel:WORD_1 dst_unused:UNUSED_PAD src0_sel:DWORD
; __device__ __forceinline__ unsigned pack_i8x4(float a, float b, float c, float d) {
;     const int ia = (int)rintf(fminf(fmaxf(a, -127.f), 127.f)), ib = (int)rintf(fminf(fmaxf(b, -127.f), 127.f)), ic = (int)rintf(fminf(fmaxf(c, -127.f), 127.f)), id = (int)rintf(fminf(fmaxf(d, -127.f), 127.f));
;     return (unsigned)(ia & 0xff) | ((unsigned)(ib & 0xff) << 8) | ((unsigned)(ic & 0xff) << 16) | ((unsigned)(id & 0xff) << 24);
; }
; __device__ __forceinline__ void cvt_item_i8(const float* src, int ld, int k0, int c0, unsigned char* dst, int Kd, int drow0, const float* cmx  , unsigned char* scr, int lane) {
;     const int c = lane & 7, q = lane >> 3;
;     const f32x4 cm = *(const f32x4*)(cmx + 4 * c);
;     f32x4 inv; inv[0] = cm[0] > 0.f ? 127.f / cm[0] : 0.f; inv[1] = cm[1] > 0.f ? 127.f / cm[1] : 0.f; inv[2] = cm[2] > 0.f ? 127.f / cm[2] : 0.f; inv[3] = cm[3] > 0.f ? 127.f / cm[3] : 0.f;
;     f32x4 v[4][4];
; #pragma unroll
;     for (int g = 0; g < 4; ++g)
; #pragma unroll
;         for (int j = 0; j < 4; ++j) v[g][j] = __builtin_nontemporal_load((const f32x4*)(src + (size_t)(k0 + 32 * g + 4 * q + j) * ld + c0 + 4 * c));
; #pragma unroll
;     for (int g = 0; g < 4; ++g)
; #pragma unroll
;         for (int i = 0; i < 4; ++i) *(unsigned*)(scr + (4 * c + i) * 132 + 32 * g + 4 * q) = pack_i8x4(v[g][0][i] * inv[i], v[g][1][i] * inv[i], v[g][2][i] * inv[i], v[g][3][i] * inv[i]);
;     asm volatile("s_waitcnt lgkmcnt(0)" ::: "memory");
; #pragma unroll
;     for (int r = 0; r < 4; ++r) { const int n = 8 * r + (lane >> 3), ch = lane & 7; const unsigned char* p = scr + n * 132 + ch * 16;
;         u32x4 o; o.x = *(const unsigned*)(p); o.y = *(const unsigned*)(p + 4); o.z = *(const unsigned*)(p + 8); o.w = *(const unsigned*)(p + 12);
;         *(u32x4*)(dst + (size_t)(drow0 + n) * Kd + k0 + 16 * ch) = o; }
;     asm volatile("s_waitcnt lgkmcnt(0)" ::: "memory");
; }
	v_rndne_f32_e32 v191, v191
	v_rndne_f32_e32 v203, v203
	v_cvt_i32_f32_e32 v210, v210
	v_cvt_i32_f32_sdwa v213, v213 dst_sel:WORD_1 dst_unused:UNUSED_PAD src0_sel:DWORD
	v_rndne_f32_e32 v211, v211
	v_rndne_f32_e32 v215, v215
	v_cvt_i32_f32_e32 v159, v159
	v_cvt_i32_f32_sdwa v167, v167 dst_sel:WORD_1 dst_unused:UNUSED_PAD src0_sel:DWORD
	v_cvt_i32_f32_e32 v175, v175
	v_cvt_i32_f32_sdwa v183, v183 dst_sel:WORD_1 dst_unused:UNUSED_PAD src0_sel:DWORD
	v_cvt_i32_f32_e32 v199, v199
	v_cvt_i32_f32_e32 v214, v214
	v_lshlrev_b32_e32 v156, 8, v156
	v_lshlrev_b32_e32 v172, 8, v172
	v_cvt_i32_f32_sdwa v202, v202 dst_sel:BYTE_3 dst_unused:UNUSED_PAD src0_sel:DWORD
	v_rndne_f32_e32 v207, v207
	v_cvt_i32_f32_sdwa v153, v153 dst_sel:BYTE_3 dst_unused:UNUSED_PAD src0_sel:DWORD
	v_rndne_f32_e32 v154, v154
	v_cvt_i32_f32_sdwa v171, v171 dst_sel:BYTE_3 dst_unused:UNUSED_PAD src0_sel:DWORD
	v_cvt_i32_f32_sdwa v187, v187 dst_sel:BYTE_3 dst_unused:UNUSED_PAD src0_sel:DWORD
	v_cvt_i32_f32_e32 v191, v191
	v_cvt_i32_f32_sdwa v203, v203 dst_sel:WORD_1 dst_unused:UNUSED_PAD src0_sel:DWORD
	v_cvt_i32_f32_e32 v211, v211
	v_cvt_i32_f32_sdwa v215, v215 dst_sel:WORD_1 dst_unused:UNUSED_PAD src0_sel:DWORD
	v_and_b32_e32 v160, 0xff0000, v160
	v_and_b32_e32 v176, 0xff0000, v176
	v_lshlrev_b32_e32 v188, 8, v188
	v_lshlrev_b32_e32 v204, 8, v204
	v_perm_b32 v155, v156, v155, s6
	v_lshlrev_b32_e32 v156, 8, v161
	v_and_b32_e32 v161, 0xff0000, v165
	v_perm_b32 v165, v172, v170, s6
	v_lshlrev_b32_e32 v170, 8, v177
	v_cvt_i32_f32_sdwa v207, v207 dst_sel:BYTE_3 dst_unused:UNUSED_PAD src0_sel:DWORD
	v_cvt_i32_f32_sdwa v154, v154 dst_sel:BYTE_3 dst_unused:UNUSED_PAD src0_sel:DWORD
	v_and_b32_e32 v192, 0xff0000, v192
	v_and_b32_e32 v205, 0xff0000, v205
	v_and_b32_e32 v172, 0xff0000, v181
	v_perm_b32 v177, v188, v186, s6
	v_lshlrev_b32_e32 v181, 8, v195
	v_perm_b32 v188, v204, v200, s6
	v_lshlrev_b32_e32 v195, 8, v208
	v_or3_b32 v155, v155, v160, v164
	v_perm_b32 v156, v156, v157, s6
	v_lshlrev_b32_e32 v157, 8, v162
	v_or3_b32 v162, v165, v176, v180
	v_perm_b32 v164, v170, v173, s6
	v_lshlrev_b32_e32 v165, 8, v178
	v_and_b32_e32 v186, 0xff0000, v196
	v_and_b32_e32 v196, 0xff0000, v209
	v_and_b32_e32 v160, 0xff0000, v166
	v_and_b32_e32 v166, 0xff0000, v182
	v_or3_b32 v170, v177, v192, v193
	v_perm_b32 v173, v181, v189, s6
	v_lshlrev_b32_e32 v176, 8, v198
	v_or3_b32 v151, v188, v205, v151
	v_perm_b32 v178, v195, v206, s6
	v_lshlrev_b32_e32 v180, 8, v212
	v_or3_b32 v156, v156, v161, v168
	v_perm_b32 v157, v157, v158, s6
	v_lshlrev_b32_e32 v158, 8, v163
	ds_write2_b32 v219, v155, v162 offset1:8
	v_or3_b32 v155, v164, v172, v184
	v_perm_b32 v162, v165, v174, s6
	v_lshlrev_b32_e32 v163, 8, v179
	v_and_b32_e32 v177, 0xff0000, v201
	v_and_b32_e32 v181, 0xff0000, v213
	v_and_b32_e32 v161, 0xff0000, v167
	v_and_b32_e32 v164, 0xff0000, v183
	v_or3_b32 v165, v173, v186, v197
	v_perm_b32 v167, v176, v190, s6
	v_lshlrev_b32_e32 v168, 8, v199
	ds_write2_b32 v219, v170, v151 offset0:16 offset1:24
	v_or3_b32 v151, v178, v196, v152
	v_perm_b32 v152, v180, v210, s6
	v_lshlrev_b32_e32 v170, 8, v214
	v_or3_b32 v157, v157, v160, v169
	v_perm_b32 v158, v158, v159, s6
	ds_write2_b32 v219, v156, v155 offset0:33 offset1:41
	v_or3_b32 v155, v162, v166, v185
	v_perm_b32 v156, v163, v175, s6
	v_and_b32_e32 v172, 0xff0000, v203
	v_and_b32_e32 v173, 0xff0000, v215
	v_or3_b32 v159, v167, v177, v202
	v_perm_b32 v160, v168, v191, s6
	ds_write2_b32 v219, v165, v151 offset0:49 offset1:57
	v_or3_b32 v151, v152, v181, v153
	v_perm_b32 v152, v170, v211, s6
	v_or3_b32 v153, v158, v161, v171
	ds_write2_b32 v219, v157, v155 offset0:66 offset1:74
	v_or3_b32 v155, v156, v164, v187
	v_or3_b32 v156, v160, v172, v207
	ds_write2_b32 v219, v159, v151 offset0:82 offset1:90
	v_or3_b32 v151, v152, v173, v154
	ds_write2_b32 v219, v153, v155 offset0:99 offset1:107
	ds_write2_b32 v219, v156, v151 offset0:115 offset1:123
	s_waitcnt lgkmcnt(0)
	ds_read2_b32 v[152:153], v220 offset1:1
	ds_read2_b32 v[154:155], v220 offset0:2 offset1:3
	ds_read2_b32 v[156:157], v1 offset1:1
	ds_read2_b32 v[158:159], v146 offset1:1
	ds_read2_b32 v[160:161], v147 offset1:1
	ds_read2_b32 v[162:163], v148 offset1:1
	ds_read2_b32 v[146:147], v149 offset1:1
	ds_read2_b32 v[148:149], v150 offset1:1
	s_waitcnt lgkmcnt(6)
	global_store_dwordx4 v[140:141], v[152:155], off
	s_waitcnt lgkmcnt(4)
	global_store_dwordx4 v[142:143], v[156:159], off
	s_waitcnt lgkmcnt(2)
	global_store_dwordx4 v[144:145], v[160:163], off
	s_waitcnt lgkmcnt(0)
	global_store_dwordx4 v[126:127], v[146:149], off
	s_waitcnt lgkmcnt(0)
	s_cbranch_scc0 .LBB0_1616
	s_branch .LBB0_1543

; __device__ __forceinline__ void cvt_item_i8(const float* src, int ld, int k0, int c0, unsigned char* dst, int Kd, int drow0, const float* cmx  , unsigned char* scr, int lane) {
;     const int c = lane & 7, q = lane >> 3;
;     const f32x4 cm = *(const f32x4*)(cmx + 4 * c);
;     f32x4 inv; inv[0] = cm[0] > 0.f ? 127.f / cm[0] : 0.f; inv[1] = cm[1] > 0.f ? 127.f / cm[1] : 0.f; inv[2] = cm[2] > 0.f ? 127.f / cm[2] : 0.f; inv[3] = cm[3] > 0.f ? 127.f / cm[3] : 0.f;
;     f32x4 v[4][4];
; #pragma unroll
;     for (int g = 0; g < 4; ++g)
; #pragma unroll
;         for (int j = 0; j < 4; ++j) v[g][j] = __builtin_nontemporal_load((const f32x4*)(src + (size_t)(k0 + 32 * g + 4 * q + j) * ld + c0 + 4 * c));
; #pragma unroll
;     for (int g = 0; g < 4; ++g)
; #pragma unroll
;         for (int i = 0; i < 4; ++i) *(unsigned*)(scr + (4 * c + i) * 132 + 32 * g + 4 * q) = pack_i8x4(v[g][0][i] * inv[i], v[g][1][i] * inv[i], v[g][2][i] * inv[i], v[g][3][i] * inv[i]);
;     asm volatile("s_waitcnt lgkmcnt(0)" ::: "memory");
; #pragma unroll
;     for (int r = 0; r < 4; ++r) { const int n = 8 * r + (lane >> 3), ch = lane & 7; const unsigned char* p = scr + n * 132 + ch * 16;
;         u32x4 o; o.x = *(const unsigned*)(p); o.y = *(const unsigned*)(p + 4); o.z = *(const unsigned*)(p + 8); o.w = *(const unsigned*)(p + 12);
;         *(u32x4*)(dst + (size_t)(drow0 + n) * Kd + k0 + 16 * ch) = o; }
;     asm volatile("s_waitcnt lgkmcnt(0)" ::: "memory");
; }
; template <int GRP>
; __device__ __forceinline__ void conv_item(Frame& F, int r) {
;     ...
;     else { constexpr int KBN = (GRP == 3) ? 16 : CMS_KB, I_E = KBN * 88; const int up = r / (8 * I_E); r %= (8 * I_E); const int e = r / I_E; r %= I_E; const int kb = r / 88, nb = r % 88, n0 = nb * 32, drow = (n0 >> 7) * 256 + up * 128 + (n0 & 127);
;         if (GRP == 3) cvt_item_i8(inptr(F, up ? IN_MU : IN_MG) + (size_t)e * D * DFE, DFE, kb * 128, n0, ws + WS_MGU + (size_t)e * 2 * DFE * D, D, drow, cmx + 2 * DFF + e * 2 * DFE + drow, scr, F.lane);
;     ...
;     for (int it = first + F.gw; it < N; it += F.NGW) conv_item<GRP>(F, it);
.LBB0_1672:
	s_mul_hi_i32 s0, s3, 0x2e8ba2e9
	s_lshr_b32 s1, s0, 31
	s_ashr_i32 s0, s0, 11
	s_add_i32 s0, s0, s1
	s_mul_i32 s1, s0, 0xffffd400
	s_lshl_b32 s6, s0, 7
	s_add_i32 s0, s3, s1
	s_mul_i32 s1, s0, 0xba3
	s_lshr_b32 s7, s1, 31
	s_ashr_i32 s1, s1, 22
	s_add_i32 s1, s1, s7
	s_mul_i32 s7, s1, 0x580
	s_sub_i32 s0, s0, s7
	s_sext_i32_i16 s36, s0
	s_mulk_i32 s36, 0xba3
	s_lshr_b32 s38, s36, 31
	s_ashr_i32 s36, s36, 18
	s_add_i32 s38, s36, s38
	s_sext_i32_i16 s36, s38
	s_mulk_i32 s38, 0x58
	s_sub_i32 s0, s0, s38
	s_sext_i32_i16 s38, s0
	s_lshl_b32 s0, s38, 5
	s_lshl_b32 s38, s38, 6
	s_and_b32 s38, s38, 0xffffff00
	s_and_b32 s39, s0, 0x60
	s_add_i32 s38, s38, s6
	s_add_i32 s37, s3, 0x2bff
	s_or_b32 s6, s38, s39
	s_cmpk_lt_u32 s37, 0x57ff
	s_cselect_b32 s37, s15, 0xa8
	v_or_b32_e32 v8, s6, v17
	s_add_i32 s37, s37, 0
	v_ashrrev_i32_e32 v9, 31, v8
	s_add_i32 s37, s37, 0x20200
	v_lshlrev_b64 v[98:99], 11, v[8:9]
	v_mov_b32_e32 v8, s37
	ds_read_b64 v[8:9], v8
	s_sext_i32_i16 s11, s1
	s_mul_i32 s9, s11, 0x1600000
	s_mul_hi_i32 s1, s11, 0x1600000
	s_mul_i32 s10, s11, 0xb00000
	s_waitcnt lgkmcnt(0)
	v_readfirstlane_b32 s37, v8
	v_readfirstlane_b32 s38, v9
	s_add_u32 s9, s37, s9
	s_addc_u32 s37, s38, s1
	s_lshl_b32 s36, s36, 7
	s_mul_hi_i32 s7, s11, 0xb00000
	s_add_u32 s10, s4, s10
	s_mul_hi_i32 s8, s11, 0x5800
	s_mulk_i32 s11, 0x5800
	s_addc_u32 s38, s12, s7
	s_add_u32 s1, s13, s11
	s_addc_u32 s8, s14, s8
	s_ashr_i32 s7, s6, 31
	v_or_b32_e32 v6, s6, v1
	v_or_b32_e32 v10, s6, v18
	v_or_b32_e32 v12, s6, v19
	s_lshl_b64 s[6:7], s[6:7], 2
	s_add_u32 s6, s1, s6
	s_addc_u32 s7, s8, s7
	s_ashr_i32 s1, s0, 31
	s_lshl_b64 s[0:1], s[0:1], 2
	v_or_b32_e32 v8, s36, v16
	s_add_u32 s0, s9, s0
	v_ashrrev_i32_e32 v11, 31, v10
	v_mul_i32_i24_e32 v8, 0x2c00, v8
	s_addc_u32 s1, s37, s1
	v_lshlrev_b64 v[100:101], 11, v[10:11]
	v_ashrrev_i32_e32 v9, 31, v8
	v_lshl_add_u64 v[10:11], s[0:1], 0, v[4:5]
	v_ashrrev_i32_e32 v7, 31, v6
	v_ashrrev_i32_e32 v13, 31, v12
	v_lshl_add_u64 v[10:11], v[10:11], 0, v[8:9]
	v_lshlrev_b64 v[14:15], 11, v[6:7]
	v_lshlrev_b64 v[6:7], 11, v[12:13]
	v_add_co_u32_e32 v12, vcc, s17, v10
	global_load_dwordx4 v[30:33], v4, s[6:7]
	s_nop 0
	v_addc_co_u32_e32 v13, vcc, 0, v11, vcc
	v_add_co_u32_e32 v42, vcc, s18, v10
	s_ashr_i32 s6, s36, 31
	s_nop 0
	v_addc_co_u32_e32 v43, vcc, 0, v11, vcc
	v_add_co_u32_e32 v46, vcc, s19, v10
	s_add_u32 s0, s10, s36
	s_nop 0
	v_addc_co_u32_e32 v47, vcc, 0, v11, vcc
	v_add_co_u32_e32 v50, vcc, s20, v10
	s_addc_u32 s1, s38, s6
	s_nop 0
	v_addc_co_u32_e32 v51, vcc, 0, v11, vcc
	v_add_co_u32_e32 v54, vcc, s21, v10
	v_lshl_add_u64 v[8:9], s[0:1], 0, v[2:3]
	s_nop 0
	v_addc_co_u32_e32 v55, vcc, 0, v11, vcc
	v_add_co_u32_e32 v58, vcc, s22, v10
	v_lshl_add_u64 v[6:7], v[8:9], 0, v[6:7]
	s_nop 0
	v_addc_co_u32_e32 v59, vcc, 0, v11, vcc
	v_add_co_u32_e32 v62, vcc, s23, v10
	s_add_i32 s3, s3, s40
	s_nop 0
	v_addc_co_u32_e32 v63, vcc, 0, v11, vcc
	v_add_co_u32_e32 v66, vcc, s24, v10
	s_cmpk_lt_i32 s3, 0x5800
	s_nop 0
	v_addc_co_u32_e32 v67, vcc, 0, v11, vcc
	v_add_co_u32_e32 v70, vcc, s25, v10
	s_waitcnt vmcnt(0)
	v_div_scale_f32 v29, s[0:1], v30, v30, s16
	v_addc_co_u32_e32 v71, vcc, 0, v11, vcc
	v_add_co_u32_e32 v74, vcc, s26, v10
	v_rcp_f32_e32 v105, v29
	s_nop 0
	v_addc_co_u32_e32 v75, vcc, 0, v11, vcc
	v_add_co_u32_e32 v78, vcc, s27, v10
	v_div_scale_f32 v103, s[0:1], v33, v33, s16
	s_nop 0
	v_addc_co_u32_e32 v79, vcc, 0, v11, vcc
	v_add_co_u32_e32 v82, vcc, s28, v10
	v_fma_f32 v109, -v29, v105, 1.0
	s_nop 0
	v_addc_co_u32_e32 v83, vcc, 0, v11, vcc
	v_add_co_u32_e32 v86, vcc, s29, v10
	v_rcp_f32_e32 v108, v103
	s_nop 0
	v_addc_co_u32_e32 v87, vcc, 0, v11, vcc
	v_add_co_u32_e32 v90, vcc, s30, v10
	v_fmac_f32_e32 v105, v109, v105
	s_nop 0
	v_addc_co_u32_e32 v91, vcc, 0, v11, vcc
	v_add_co_u32_e32 v94, vcc, s31, v10
	v_div_scale_f32 v102, s[8:9], s16, v32, s16
	s_nop 0
	v_addc_co_u32_e32 v95, vcc, 0, v11, vcc
	global_load_dwordx4 v[34:37], v[10:11], off nt
	global_load_dwordx4 v[38:41], v[12:13], off offset:3072 nt
	s_nop 0
	global_load_dwordx4 v[42:45], v[42:43], off offset:2048 nt
	s_nop 0
	global_load_dwordx4 v[46:49], v[46:47], off offset:1024 nt
	s_nop 0
	global_load_dwordx4 v[50:53], v[50:51], off nt
	s_nop 0
	global_load_dwordx4 v[54:57], v[54:55], off offset:3072 nt
	s_nop 0
	global_load_dwordx4 v[58:61], v[58:59], off offset:2048 nt
	s_nop 0
	global_load_dwordx4 v[62:65], v[62:63], off offset:1024 nt
	s_nop 0
	global_load_dwordx4 v[66:69], v[66:67], off nt
	s_nop 0
	global_load_dwordx4 v[70:73], v[70:71], off offset:3072 nt
	s_nop 0
	global_load_dwordx4 v[74:77], v[74:75], off offset:2048 nt
	s_nop 0
	global_load_dwordx4 v[78:81], v[78:79], off offset:1024 nt
	s_nop 0
	global_load_dwordx4 v[82:85], v[82:83], off nt
	s_nop 0
	global_load_dwordx4 v[86:89], v[86:87], off offset:3072 nt
	s_nop 0
	global_load_dwordx4 v[90:93], v[90:91], off offset:2048 nt
	s_nop 0
	global_load_dwordx4 v[94:97], v[94:95], off offset:1024 nt
	v_lshl_add_u64 v[12:13], v[8:9], 0, v[98:99]
	v_div_scale_f32 v99, s[0:1], v31, v31, s16
	v_rcp_f32_e32 v106, v99
	v_lshl_add_u64 v[10:11], v[8:9], 0, v[14:15]
	v_lshl_add_u64 v[14:15], v[8:9], 0, v[100:101]
	v_div_scale_f32 v101, s[0:1], v32, v32, s16
	v_rcp_f32_e32 v107, v101
	v_div_scale_f32 v98, vcc, s16, v30, s16
	v_fma_f32 v110, -v99, v106, 1.0
	v_div_scale_f32 v100, s[6:7], s16, v31, s16
	v_fmac_f32_e32 v106, v110, v106
	v_mul_f32_e32 v109, v98, v105
	v_fma_f32 v111, -v101, v107, 1.0
	v_mul_f32_e32 v110, v100, v106
	v_fma_f32 v113, -v29, v109, v98
	v_fmac_f32_e32 v107, v111, v107
	v_fma_f32 v114, -v99, v110, v100
	v_fmac_f32_e32 v109, v113, v105
	v_fma_f32 v112, -v103, v108, 1.0
	v_mul_f32_e32 v111, v102, v107
	v_fmac_f32_e32 v110, v114, v106
	v_fma_f32 v29, -v29, v109, v98
	v_div_scale_f32 v104, s[10:11], s16, v33, s16
	v_fmac_f32_e32 v108, v112, v108
	v_fma_f32 v115, -v101, v111, v102
	v_fma_f32 v98, -v99, v110, v100
	v_div_fmas_f32 v29, v29, v105, v109
	s_mov_b64 vcc, s[6:7]
	v_mul_f32_e32 v112, v104, v108
	v_fmac_f32_e32 v111, v115, v107
	v_div_fixup_f32 v29, v29, v30, s16
	v_div_fmas_f32 v98, v98, v106, v110
	v_cmp_lt_f32_e32 vcc, 0, v30
	v_fma_f32 v116, -v103, v112, v104
	v_fma_f32 v99, -v101, v111, v102
	v_cndmask_b32_e32 v29, 0, v29, vcc
	s_mov_b64 vcc, s[8:9]
	v_fmac_f32_e32 v112, v116, v108
	v_div_fixup_f32 v30, v98, v31, s16
	v_div_fmas_f32 v98, v99, v107, v111
	v_cmp_lt_f32_e32 vcc, 0, v31
	v_fma_f32 v100, -v103, v112, v104
	v_div_fixup_f32 v31, v98, v32, s16
	v_cndmask_b32_e32 v30, 0, v30, vcc
	s_mov_b64 vcc, s[10:11]
	v_div_fmas_f32 v98, v100, v108, v112
	v_cmp_lt_f32_e32 vcc, 0, v32
	v_div_fixup_f32 v32, v98, v33, s16
	s_waitcnt vmcnt(0) lgkmcnt(0)
; __device__ __forceinline__ unsigned pack_i8x4(float a, float b, float c, float d) {
;     const int ia = (int)rintf(fminf(fmaxf(a, -127.f), 127.f)), ib = (int)rintf(fminf(fmaxf(b, -127.f), 127.f)), ic = (int)rintf(fminf(fmaxf(c, -127.f), 127.f)), id = (int)rintf(fminf(fmaxf(d, -127.f), 127.f));
;     return (unsigned)(ia & 0xff) | ((unsigned)(ib & 0xff) << 8) | ((unsigned)(ic & 0xff) << 16) | ((unsigned)(id & 0xff) << 24);
; }
; __device__ __forceinline__ void cvt_item_i8(const float* src, int ld, int k0, int c0, unsigned char* dst, int Kd, int drow0, const float* cmx  , unsigned char* scr, int lane) {
;     const int c = lane & 7, q = lane >> 3;
;     const f32x4 cm = *(const f32x4*)(cmx + 4 * c);
;     f32x4 inv; inv[0] = cm[0] > 0.f ? 127.f / cm[0] : 0.f; inv[1] = cm[1] > 0.f ? 127.f / cm[1] : 0.f; inv[2] = cm[2] > 0.f ? 127.f / cm[2] : 0.f; inv[3] = cm[3] > 0.f ? 127.f / cm[3] : 0.f;
;     f32x4 v[4][4];
; #pragma unroll
;     for (int g = 0; g < 4; ++g)
; #pragma unroll
;         for (int j = 0; j < 4; ++j) v[g][j] = __builtin_nontemporal_load((const f32x4*)(src + (size_t)(k0 + 32 * g + 4 * q + j) * ld + c0 + 4 * c));
; #pragma unroll
;     for (int g = 0; g < 4; ++g)
; #pragma unroll
;         for (int i = 0; i < 4; ++i) *(unsigned*)(scr + (4 * c + i) * 132 + 32 * g + 4 * q) = pack_i8x4(v[g][0][i] * inv[i], v[g][1][i] * inv[i], v[g][2][i] * inv[i], v[g][3][i] * inv[i]);
	v_mul_f32_e32 v34, v34, v29
	v_mul_f32_e32 v38, v29, v38
	v_mul_f32_e32 v42, v29, v42
	v_mul_f32_e32 v46, v29, v46
	v_mul_f32_e32 v50, v29, v50
	v_mul_f32_e32 v54, v29, v54
	v_mul_f32_e32 v58, v29, v58
	v_mul_f32_e32 v62, v29, v62
	v_mul_f32_e32 v66, v29, v66
	v_mul_f32_e32 v70, v29, v70
	v_mul_f32_e32 v74, v29, v74
	v_mul_f32_e32 v78, v29, v78
	v_mul_f32_e32 v82, v29, v82
	v_mul_f32_e32 v86, v29, v86
	v_cndmask_b32_e32 v31, 0, v31, vcc
	v_med3_f32 v34, v34, s34, v20
	v_med3_f32 v38, v38, s34, v20
	v_med3_f32 v42, v42, s34, v20
	v_med3_f32 v46, v46, s34, v20
	v_mul_f32_e32 v39, v30, v39
	v_mul_f32_e32 v43, v30, v43
	v_mul_f32_e32 v47, v30, v47
	v_med3_f32 v50, v50, s34, v20
	v_med3_f32 v54, v54, s34, v20
	v_mul_f32_e32 v55, v30, v55
	v_cmp_lt_f32_e32 vcc, 0, v33
	v_mul_f32_e32 v90, v29, v90
	v_mul_f32_e32 v35, v35, v30
	v_med3_f32 v58, v58, s34, v20
	v_med3_f32 v62, v62, s34, v20
	v_mul_f32_e32 v51, v30, v51
	v_mul_f32_e32 v59, v30, v59
	v_mul_f32_e32 v63, v30, v63
	v_med3_f32 v66, v66, s34, v20
	v_med3_f32 v70, v70, s34, v20
	v_med3_f32 v74, v74, s34, v20
	v_med3_f32 v78, v78, s34, v20
	v_mul_f32_e32 v71, v30, v71
	v_mul_f32_e32 v79, v30, v79
	v_med3_f32 v82, v82, s34, v20
	v_med3_f32 v86, v86, s34, v20
	v_mul_f32_e32 v87, v30, v87
	v_cndmask_b32_e32 v32, 0, v32, vcc
	v_rndne_f32_e32 v33, v34
	v_rndne_f32_e32 v34, v38
	v_rndne_f32_e32 v38, v42
	v_rndne_f32_e32 v42, v46
	v_med3_f32 v39, v39, s34, v20
	v_med3_f32 v43, v43, s34, v20
	v_med3_f32 v46, v47, s34, v20
	v_mul_f32_e32 v40, v31, v40
	v_mul_f32_e32 v47, v31, v48
	v_rndne_f32_e32 v48, v50
	v_rndne_f32_e32 v50, v54
	v_med3_f32 v55, v55, s34, v20
	v_mul_f32_e32 v56, v31, v56
	v_mul_f32_e32 v29, v29, v94
	v_mul_f32_e32 v67, v30, v67
	v_mul_f32_e32 v75, v30, v75
	v_med3_f32 v90, v90, s34, v20
	v_mul_f32_e32 v83, v30, v83
	v_mul_f32_e32 v91, v30, v91
	v_med3_f32 v35, v35, s34, v20
	v_mul_f32_e32 v36, v36, v31
	v_mul_f32_e32 v44, v31, v44
	v_rndne_f32_e32 v54, v58
	v_rndne_f32_e32 v58, v62
	v_med3_f32 v51, v51, s34, v20
	v_med3_f32 v59, v59, s34, v20
	v_med3_f32 v62, v63, s34, v20
	v_mul_f32_e32 v52, v31, v52
	v_mul_f32_e32 v60, v31, v60
	v_mul_f32_e32 v63, v31, v64
	v_rndne_f32_e32 v64, v66
	v_rndne_f32_e32 v66, v70
	v_rndne_f32_e32 v70, v74
	v_rndne_f32_e32 v74, v78
	v_med3_f32 v71, v71, s34, v20
	v_med3_f32 v78, v79, s34, v20
	v_mul_f32_e32 v72, v31, v72
	v_mul_f32_e32 v79, v31, v80
	v_rndne_f32_e32 v80, v82
	v_rndne_f32_e32 v82, v86
	v_med3_f32 v87, v87, s34, v20
	v_mul_f32_e32 v88, v31, v88
	v_cvt_i32_f32_e32 v34, v34
	v_rndne_f32_e32 v39, v39
	v_rndne_f32_e32 v43, v43
	v_med3_f32 v40, v40, s34, v20
	v_mul_f32_e32 v41, v32, v41
	v_cvt_i32_f32_e32 v50, v50
	v_rndne_f32_e32 v55, v55
	v_med3_f32 v56, v56, s34, v20
	v_mul_f32_e32 v57, v32, v57
	v_med3_f32 v29, v29, s34, v20
	v_mul_f32_e32 v30, v30, v95
	v_med3_f32 v67, v67, s34, v20
	v_med3_f32 v75, v75, s34, v20
	v_mul_f32_e32 v68, v31, v68
	v_mul_f32_e32 v76, v31, v76
	v_rndne_f32_e32 v86, v90
	v_med3_f32 v83, v83, s34, v20
	v_med3_f32 v90, v91, s34, v20
	v_mul_f32_e32 v84, v31, v84
	v_mul_f32_e32 v91, v31, v92
	v_cvt_i32_f32_e32 v33, v33
	v_cvt_i32_f32_sdwa v38, v38 dst_sel:WORD_1 dst_unused:UNUSED_PAD src0_sel:DWORD
	v_rndne_f32_e32 v35, v35
	v_med3_f32 v36, v36, s34, v20
	v_med3_f32 v44, v44, s34, v20
	v_mul_f32_e32 v37, v37, v32
	v_mul_f32_e32 v45, v32, v45
	v_cvt_i32_f32_e32 v48, v48
	v_cvt_i32_f32_sdwa v54, v54 dst_sel:WORD_1 dst_unused:UNUSED_PAD src0_sel:DWORD
	v_rndne_f32_e32 v51, v51
	v_rndne_f32_e32 v59, v59
	v_med3_f32 v52, v52, s34, v20
	v_med3_f32 v60, v60, s34, v20
	v_mul_f32_e32 v53, v32, v53
	v_mul_f32_e32 v61, v32, v61
	v_cvt_i32_f32_e32 v66, v66
	v_rndne_f32_e32 v71, v71
	v_med3_f32 v72, v72, s34, v20
	v_mul_f32_e32 v73, v32, v73
	v_cvt_i32_f32_e32 v82, v82
	v_rndne_f32_e32 v87, v87
	v_med3_f32 v88, v88, s34, v20
	v_mul_f32_e32 v89, v32, v89
	v_cvt_i32_f32_e32 v39, v39
	v_cvt_i32_f32_sdwa v43, v43 dst_sel:WORD_1 dst_unused:UNUSED_PAD src0_sel:DWORD
	v_rndne_f32_e32 v40, v40
	v_med3_f32 v41, v41, s34, v20
	v_cvt_i32_f32_e32 v55, v55
	v_rndne_f32_e32 v56, v56
	v_med3_f32 v57, v57, s34, v20
	v_rndne_f32_e32 v29, v29
	v_med3_f32 v30, v30, s34, v20
	v_mul_f32_e32 v31, v31, v96
	v_cvt_i32_f32_sdwa v42, v42 dst_sel:BYTE_3 dst_unused:UNUSED_PAD src0_sel:DWORD
	v_rndne_f32_e32 v46, v46
	v_med3_f32 v47, v47, s34, v20
	v_mul_f32_e32 v49, v32, v49
	v_cvt_i32_f32_sdwa v58, v58 dst_sel:BYTE_3 dst_unused:UNUSED_PAD src0_sel:DWORD
	v_rndne_f32_e32 v62, v62
	v_med3_f32 v63, v63, s34, v20
	v_mul_f32_e32 v65, v32, v65
	v_cvt_i32_f32_e32 v64, v64
	v_cvt_i32_f32_sdwa v70, v70 dst_sel:WORD_1 dst_unused:UNUSED_PAD src0_sel:DWORD
	v_rndne_f32_e32 v67, v67
	v_rndne_f32_e32 v75, v75
	v_med3_f32 v68, v68, s34, v20
	v_med3_f32 v76, v76, s34, v20
	v_mul_f32_e32 v69, v32, v69
	v_mul_f32_e32 v77, v32, v77
	v_cvt_i32_f32_e32 v80, v80
	v_cvt_i32_f32_sdwa v86, v86 dst_sel:WORD_1 dst_unused:UNUSED_PAD src0_sel:DWORD
	v_rndne_f32_e32 v83, v83
	v_rndne_f32_e32 v90, v90
	v_med3_f32 v84, v84, s34, v20
	v_med3_f32 v91, v91, s34, v20
	v_mul_f32_e32 v85, v32, v85
	v_mul_f32_e32 v92, v32, v93
	v_cvt_i32_f32_e32 v35, v35
	v_rndne_f32_e32 v36, v36
	v_rndne_f32_e32 v44, v44
	v_med3_f32 v37, v37, s34, v20
	v_med3_f32 v45, v45, s34, v20
	v_cvt_i32_f32_e32 v51, v51
	v_cvt_i32_f32_sdwa v59, v59 dst_sel:WORD_1 dst_unused:UNUSED_PAD src0_sel:DWORD
	v_rndne_f32_e32 v52, v52
	v_rndne_f32_e32 v60, v60
	v_med3_f32 v53, v53, s34, v20
	v_med3_f32 v61, v61, s34, v20
	v_cvt_i32_f32_e32 v71, v71
	v_rndne_f32_e32 v72, v72
	v_med3_f32 v73, v73, s34, v20
	v_cvt_i32_f32_e32 v87, v87
	v_rndne_f32_e32 v88, v88
	v_med3_f32 v89, v89, s34, v20
	v_cvt_i32_f32_e32 v40, v40
; __device__ __forceinline__ unsigned pack_i8x4(float a, float b, float c, float d) {
;     const int ia = (int)rintf(fminf(fmaxf(a, -127.f), 127.f)), ib = (int)rintf(fminf(fmaxf(b, -127.f), 127.f)), ic = (int)rintf(fminf(fmaxf(c, -127.f), 127.f)), id = (int)rintf(fminf(fmaxf(d, -127.f), 127.f));
;     return (unsigned)(ia & 0xff) | ((unsigned)(ib & 0xff) << 8) | ((unsigned)(ic & 0xff) << 16) | ((unsigned)(id & 0xff) << 24);
; }
; __device__ __forceinline__ void cvt_item_i8(const float* src, int ld, int k0, int c0, unsigned char* dst, int Kd, int drow0, const float* cmx  , unsigned char* scr, int lane) {
;     const int c = lane & 7, q = lane >> 3;
;     const f32x4 cm = *(const f32x4*)(cmx + 4 * c);
;     f32x4 inv; inv[0] = cm[0] > 0.f ? 127.f / cm[0] : 0.f; inv[1] = cm[1] > 0.f ? 127.f / cm[1] : 0.f; inv[2] = cm[2] > 0.f ? 127.f / cm[2] : 0.f; inv[3] = cm[3] > 0.f ? 127.f / cm[3] : 0.f;
;     f32x4 v[4][4];
; #pragma unroll
;     for (int g = 0; g < 4; ++g)
; #pragma unroll
;         for (int j = 0; j < 4; ++j) v[g][j] = __builtin_nontemporal_load((const f32x4*)(src + (size_t)(k0 + 32 * g + 4 * q + j) * ld + c0 + 4 * c));
; #pragma unroll
;     for (int g = 0; g < 4; ++g)
; #pragma unroll
;         for (int i = 0; i < 4; ++i) *(unsigned*)(scr + (4 * c + i) * 132 + 32 * g + 4 * q) = pack_i8x4(v[g][0][i] * inv[i], v[g][1][i] * inv[i], v[g][2][i] * inv[i], v[g][3][i] * inv[i]);
;     asm volatile("s_waitcnt lgkmcnt(0)" ::: "memory");
; #pragma unroll
;     for (int r = 0; r < 4; ++r) { const int n = 8 * r + (lane >> 3), ch = lane & 7; const unsigned char* p = scr + n * 132 + ch * 16;
;         u32x4 o; o.x = *(const unsigned*)(p); o.y = *(const unsigned*)(p + 4); o.z = *(const unsigned*)(p + 8); o.w = *(const unsigned*)(p + 12);
;         *(u32x4*)(dst + (size_t)(drow0 + n) * Kd + k0 + 16 * ch) = o; }
;     asm volatile("s_waitcnt lgkmcnt(0)" ::: "memory");
; }
	v_rndne_f32_e32 v41, v41
	v_cvt_i32_f32_e32 v56, v56
	v_rndne_f32_e32 v57, v57
	v_cvt_i32_f32_sdwa v74, v74 dst_sel:BYTE_3 dst_unused:UNUSED_PAD src0_sel:DWORD
	v_rndne_f32_e32 v78, v78
	v_med3_f32 v79, v79, s34, v20
	v_mul_f32_e32 v81, v32, v81
	v_cvt_i32_f32_sdwa v29, v29 dst_sel:BYTE_3 dst_unused:UNUSED_PAD src0_sel:DWORD
	v_rndne_f32_e32 v30, v30
	v_med3_f32 v31, v31, s34, v20
	v_mul_f32_e32 v32, v32, v97
	v_cvt_i32_f32_sdwa v46, v46 dst_sel:BYTE_3 dst_unused:UNUSED_PAD src0_sel:DWORD
	v_rndne_f32_e32 v47, v47
	v_med3_f32 v49, v49, s34, v20
	v_cvt_i32_f32_sdwa v62, v62 dst_sel:BYTE_3 dst_unused:UNUSED_PAD src0_sel:DWORD
	v_rndne_f32_e32 v63, v63
	v_med3_f32 v65, v65, s34, v20
	v_cvt_i32_f32_e32 v67, v67
	v_cvt_i32_f32_sdwa v75, v75 dst_sel:WORD_1 dst_unused:UNUSED_PAD src0_sel:DWORD
	v_rndne_f32_e32 v68, v68
	v_rndne_f32_e32 v76, v76
	v_med3_f32 v69, v69, s34, v20
	v_med3_f32 v77, v77, s34, v20
	v_cvt_i32_f32_e32 v83, v83
	v_cvt_i32_f32_sdwa v90, v90 dst_sel:WORD_1 dst_unused:UNUSED_PAD src0_sel:DWORD
	v_rndne_f32_e32 v84, v84
	v_rndne_f32_e32 v91, v91
	v_med3_f32 v85, v85, s34, v20
	v_med3_f32 v92, v92, s34, v20
	v_cvt_i32_f32_e32 v36, v36
	v_cvt_i32_f32_sdwa v44, v44 dst_sel:WORD_1 dst_unused:UNUSED_PAD src0_sel:DWORD
	v_rndne_f32_e32 v37, v37
	v_rndne_f32_e32 v45, v45
	v_cvt_i32_f32_e32 v52, v52
	v_cvt_i32_f32_sdwa v60, v60 dst_sel:WORD_1 dst_unused:UNUSED_PAD src0_sel:DWORD
	v_rndne_f32_e32 v53, v53
	v_rndne_f32_e32 v61, v61
	v_cvt_i32_f32_e32 v72, v72
	v_rndne_f32_e32 v73, v73
	v_cvt_i32_f32_e32 v88, v88
	v_rndne_f32_e32 v89, v89
	v_cvt_i32_f32_e32 v41, v41
	v_cvt_i32_f32_e32 v57, v57
	v_cvt_i32_f32_sdwa v78, v78 dst_sel:BYTE_3 dst_unused:UNUSED_PAD src0_sel:DWORD
	v_rndne_f32_e32 v79, v79
	v_med3_f32 v81, v81, s34, v20
	v_cvt_i32_f32_sdwa v30, v30 dst_sel:BYTE_3 dst_unused:UNUSED_PAD src0_sel:DWORD
	v_rndne_f32_e32 v31, v31
	v_med3_f32 v32, v32, s34, v20
	v_cvt_i32_f32_sdwa v47, v47 dst_sel:BYTE_3 dst_unused:UNUSED_PAD src0_sel:DWORD
	v_rndne_f32_e32 v49, v49
	v_cvt_i32_f32_sdwa v63, v63 dst_sel:BYTE_3 dst_unused:UNUSED_PAD src0_sel:DWORD
	v_rndne_f32_e32 v65, v65
	v_cvt_i32_f32_e32 v68, v68
	v_cvt_i32_f32_sdwa v76, v76 dst_sel:WORD_1 dst_unused:UNUSED_PAD src0_sel:DWORD
	v_rndne_f32_e32 v69, v69
	v_rndne_f32_e32 v77, v77
	v_cvt_i32_f32_e32 v84, v84
	v_cvt_i32_f32_sdwa v91, v91 dst_sel:WORD_1 dst_unused:UNUSED_PAD src0_sel:DWORD
	v_rndne_f32_e32 v85, v85
	v_rndne_f32_e32 v92, v92
	v_cvt_i32_f32_e32 v37, v37
	v_cvt_i32_f32_sdwa v45, v45 dst_sel:WORD_1 dst_unused:UNUSED_PAD src0_sel:DWORD
	v_cvt_i32_f32_e32 v53, v53
	v_cvt_i32_f32_sdwa v61, v61 dst_sel:WORD_1 dst_unused:UNUSED_PAD src0_sel:DWORD
	v_cvt_i32_f32_e32 v73, v73
	v_cvt_i32_f32_e32 v89, v89
	v_lshlrev_b32_e32 v34, 8, v34
	v_lshlrev_b32_e32 v50, 8, v50
	v_cvt_i32_f32_sdwa v79, v79 dst_sel:BYTE_3 dst_unused:UNUSED_PAD src0_sel:DWORD
	v_rndne_f32_e32 v81, v81
	v_cvt_i32_f32_sdwa v31, v31 dst_sel:BYTE_3 dst_unused:UNUSED_PAD src0_sel:DWORD
	v_rndne_f32_e32 v32, v32
	v_cvt_i32_f32_sdwa v49, v49 dst_sel:BYTE_3 dst_unused:UNUSED_PAD src0_sel:DWORD
	v_cvt_i32_f32_sdwa v65, v65 dst_sel:BYTE_3 dst_unused:UNUSED_PAD src0_sel:DWORD
	v_cvt_i32_f32_e32 v69, v69
	v_cvt_i32_f32_sdwa v77, v77 dst_sel:WORD_1 dst_unused:UNUSED_PAD src0_sel:DWORD
	v_cvt_i32_f32_e32 v85, v85
	v_cvt_i32_f32_sdwa v92, v92 dst_sel:WORD_1 dst_unused:UNUSED_PAD src0_sel:DWORD
	v_and_b32_e32 v38, 0xff0000, v38
	v_and_b32_e32 v54, 0xff0000, v54
	v_lshlrev_b32_e32 v66, 8, v66
	v_lshlrev_b32_e32 v82, 8, v82
	v_perm_b32 v33, v34, v33, s35
	v_lshlrev_b32_e32 v34, 8, v39
	v_and_b32_e32 v39, 0xff0000, v43
	v_perm_b32 v43, v50, v48, s35
	v_lshlrev_b32_e32 v48, 8, v55
	v_cvt_i32_f32_sdwa v81, v81 dst_sel:BYTE_3 dst_unused:UNUSED_PAD src0_sel:DWORD
	v_cvt_i32_f32_sdwa v32, v32 dst_sel:BYTE_3 dst_unused:UNUSED_PAD src0_sel:DWORD
	v_and_b32_e32 v70, 0xff0000, v70
	v_and_b32_e32 v86, 0xff0000, v86
	v_and_b32_e32 v50, 0xff0000, v59
	v_perm_b32 v55, v66, v64, s35
	v_lshlrev_b32_e32 v59, 8, v71
	v_perm_b32 v66, v82, v80, s35
	v_lshlrev_b32_e32 v71, 8, v87
	v_or3_b32 v33, v33, v38, v42
	v_perm_b32 v34, v34, v35, s35
	v_lshlrev_b32_e32 v35, 8, v40
	v_or3_b32 v40, v43, v54, v58
	v_perm_b32 v42, v48, v51, s35
	v_lshlrev_b32_e32 v43, 8, v56
	v_and_b32_e32 v64, 0xff0000, v75
	v_and_b32_e32 v75, 0xff0000, v90
	v_and_b32_e32 v38, 0xff0000, v44
	v_and_b32_e32 v44, 0xff0000, v60
	v_or3_b32 v48, v55, v70, v74
	v_perm_b32 v51, v59, v67, s35
	v_lshlrev_b32_e32 v54, 8, v72
	v_or3_b32 v29, v66, v86, v29
	v_perm_b32 v56, v71, v83, s35
	v_lshlrev_b32_e32 v58, 8, v88
	v_or3_b32 v34, v34, v39, v46
	v_perm_b32 v35, v35, v36, s35
	v_lshlrev_b32_e32 v36, 8, v41
	ds_write2_b32 v21, v33, v40 offset1:8
	v_or3_b32 v33, v42, v50, v62
	v_perm_b32 v40, v43, v52, s35
	v_lshlrev_b32_e32 v41, 8, v57
	v_and_b32_e32 v55, 0xff0000, v76
	v_and_b32_e32 v59, 0xff0000, v91
	v_and_b32_e32 v39, 0xff0000, v45
	v_and_b32_e32 v42, 0xff0000, v61
	v_or3_b32 v43, v51, v64, v78
	v_perm_b32 v45, v54, v68, s35
	v_lshlrev_b32_e32 v46, 8, v73
	ds_write2_b32 v21, v48, v29 offset0:16 offset1:24
	v_or3_b32 v29, v56, v75, v30
	v_perm_b32 v30, v58, v84, s35
	v_lshlrev_b32_e32 v48, 8, v89
	v_or3_b32 v35, v35, v38, v47
	v_perm_b32 v36, v36, v37, s35
	ds_write2_b32 v21, v34, v33 offset0:33 offset1:41
	v_or3_b32 v33, v40, v44, v63
	v_perm_b32 v34, v41, v53, s35
	v_and_b32_e32 v50, 0xff0000, v77
	v_and_b32_e32 v51, 0xff0000, v92
	v_or3_b32 v37, v45, v55, v79
	v_perm_b32 v38, v46, v69, s35
	ds_write2_b32 v21, v43, v29 offset0:49 offset1:57
	v_or3_b32 v29, v30, v59, v31
	v_perm_b32 v30, v48, v85, s35
	v_or3_b32 v31, v36, v39, v49
	ds_write2_b32 v21, v35, v33 offset0:66 offset1:74
	v_or3_b32 v33, v34, v42, v65
	v_or3_b32 v34, v38, v50, v81
	ds_write2_b32 v21, v37, v29 offset0:82 offset1:90
	v_or3_b32 v29, v30, v51, v32
	ds_write2_b32 v21, v31, v33 offset0:99 offset1:107
	ds_write2_b32 v21, v34, v29 offset0:115 offset1:123
	s_waitcnt lgkmcnt(0)
	ds_read2_b32 v[30:31], v22 offset1:1
	ds_read2_b32 v[32:33], v22 offset0:2 offset1:3
	ds_read2_b32 v[34:35], v23 offset1:1
	ds_read2_b32 v[36:37], v24 offset1:1
	ds_read2_b32 v[38:39], v25 offset1:1
	ds_read2_b32 v[40:41], v26 offset1:1
	ds_read2_b32 v[42:43], v27 offset1:1
	ds_read2_b32 v[44:45], v28 offset1:1
	s_waitcnt lgkmcnt(6)
	global_store_dwordx4 v[10:11], v[30:33], off
	s_waitcnt lgkmcnt(4)
	global_store_dwordx4 v[12:13], v[34:37], off
	s_waitcnt lgkmcnt(2)
	global_store_dwordx4 v[14:15], v[38:41], off
	s_waitcnt lgkmcnt(0)
	global_store_dwordx4 v[6:7], v[42:45], off
	s_waitcnt lgkmcnt(0)
	s_cbranch_scc1 .LBB0_1672

; #define LAS __attribute__((address_space(3)))
; __device__ __forceinline__ void prefetch(Pre& P, const bf16_t* proj, const float* gates, size_t rb, int c, int h, int tid, int lane) {
;     const int cc = tid & 31, rg = tid >> 5;
;     const int col = (cc < 16) ? (C_LQ + h * 128 + 8 * cc) : (C_LK + h * 128 + 8 * (cc - 16));
; #pragma unroll
;     for (int i = 0; i < 7; ++i) { const int pos = c * 64 + 4 * rg - 3 + i;
;         if (pos >= 0) P.raw[i] = *(const u32x4*)(proj + (rb + pos) * NIN + col); else P.raw[i] = (u32x4){0u, 0u, 0u, 0u}; }
; __device__ __forceinline__ void z_setup(Frame& F, const float* conv_w, const float* conv_b, const float* normw) {
;     __syncthreads();
;     for (int i = F.tid; i < 5 * 1024; i += NTHR) { const int j = i >> 10, ch = i & 1023; ((LAS float*)(F.lds + ZCW))[i] = (j < 4) ? conv_w[j * 1024 + ch] : conv_b[ch]; }
;     ((LAS float*)(F.lds + ZNW))[F.tid] = normw[F.tid];
;     __syncthreads();
; }
.LBB0_1773:
	s_mov_b64 s[8:9], 0x1000
	v_lshl_add_u64 v[10:11], v[4:5], 0, s[8:9]
	v_lshl_add_u64 v[12:13], v[10:11], 0, s[8:9]
	v_lshl_add_u64 v[14:15], v[12:13], 0, s[8:9]
	v_lshl_add_u64 v[16:17], s[0:1], 0, v[2:3]
	global_load_dword v20, v[4:5], off
	global_load_dword v21, v[4:5], off offset:2048
	global_load_dword v22, v[10:11], off
	global_load_dword v23, v[10:11], off offset:2048
	global_load_dword v24, v[12:13], off
	global_load_dword v25, v[12:13], off offset:2048
	global_load_dword v26, v[14:15], off
	global_load_dword v27, v[14:15], off offset:2048
	global_load_dword v28, v[16:17], off
	global_load_dword v29, v[16:17], off offset:2048
	s_waitcnt vmcnt(0)
	ds_write_b32 v1, v20
	ds_write_b32 v1, v21 offset:2048
	ds_write_b32 v1, v22 offset:4096
	ds_write_b32 v1, v23 offset:6144
	ds_write_b32 v1, v24 offset:8192
	ds_write_b32 v1, v25 offset:10240
	ds_write_b32 v1, v26 offset:12288
	ds_write_b32 v1, v27 offset:14336
	ds_write_b32 v1, v28 offset:16384
	ds_write_b32 v1, v29 offset:18432
	v_mov_b32_e32 v34, 0
	v_lshlrev_b32_e32 v110, 2, v0
	v_mov_b32_e32 v111, v34
	v_lshl_add_u64 v[2:3], s[6:7], 0, v[110:111]
	global_load_dword v1, v[2:3], off offset:2048
	v_lshl_add_u32 v2, v0, 2, 0
	s_cmpk_lt_i32 s2, 0x400
	v_add_u32_e32 v2, 0x1f300, v2
	s_cselect_b64 s[0:1], -1, 0
	s_cmpk_gt_i32 s2, 0x3ff
	s_waitcnt vmcnt(0) lgkmcnt(0)
	ds_write_b32 v2, v1
	s_waitcnt lgkmcnt(0)
	s_barrier
	s_cbranch_scc1 .LBB0_1784
	s_ashr_i32 s3, s2, 5
	s_and_b32 s4, s3, 3
	s_lshl_b32 s11, s4, 7
	v_lshlrev_b32_e32 v2, 3, v203
	v_or_b32_e32 v3, s11, v2
	v_add_u32_e32 v2, s11, v2
	s_lshl_b32 s8, s2, 6
	v_or_b32_e32 v3, 0x600, v3
	v_add_u32_e32 v2, 0x780, v2
	v_cmp_gt_u32_e32 vcc, 16, v203
	s_ashr_i32 s6, s2, 7
	s_and_b32 s10, s8, 0x7c0
	v_lshrrev_b32_e32 v1, 5, v0
	v_cndmask_b32_e32 v3, v2, v3, vcc
	s_ashr_i32 s7, s6, 31
	v_lshl_or_b32 v2, v1, 2, s10
	v_lshlrev_b32_e32 v4, 1, v3
	v_mov_b32_e32 v5, v34
	s_lshl_b64 s[6:7], s[6:7], 11
	v_add_u32_e32 v6, -3, v2
	v_lshl_add_u64 v[4:5], s[58:59], 0, v[4:5]
	v_cmp_ne_u32_e32 vcc, 0, v2
	v_mov_b32_e32 v35, 0
	v_mov_b32_e32 v36, 0
	v_mov_b32_e32 v37, 0
	s_and_saveexec_b64 s[8:9], vcc
	s_cbranch_execz .LBB0_1777
	v_mov_b32_e32 v7, 0
	v_lshl_add_u64 v[8:9], s[6:7], 0, v[6:7]
	s_movk_i32 s14, 0x2600
	v_mad_u64_u32 v[10:11], s[12:13], v8, s14, v[4:5]
	v_mad_i32_i24 v11, v9, s14, v11
	global_load_dwordx4 v[34:37], v[10:11], off

; __device__ __forceinline__ void cvt_item_i8(const float* src, int ld, int k0, int c0, unsigned char* dst, int Kd, int drow0, const float* cmx  , unsigned char* scr, int lane) {
;     const int c = lane & 7, q = lane >> 3;
;     const f32x4 cm = *(const f32x4*)(cmx + 4 * c);
;     f32x4 inv; inv[0] = cm[0] > 0.f ? 127.f / cm[0] : 0.f; inv[1] = cm[1] > 0.f ? 127.f / cm[1] : 0.f; inv[2] = cm[2] > 0.f ? 127.f / cm[2] : 0.f; inv[3] = cm[3] > 0.f ? 127.f / cm[3] : 0.f;
;     f32x4 v[4][4];
; #pragma unroll
;     for (int g = 0; g < 4; ++g)
; #pragma unroll
;         for (int j = 0; j < 4; ++j) v[g][j] = __builtin_nontemporal_load((const f32x4*)(src + (size_t)(k0 + 32 * g + 4 * q + j) * ld + c0 + 4 * c));
; #pragma unroll
;     for (int g = 0; g < 4; ++g)
; #pragma unroll
;         for (int i = 0; i < 4; ++i) *(unsigned*)(scr + (4 * c + i) * 132 + 32 * g + 4 * q) = pack_i8x4(v[g][0][i] * inv[i], v[g][1][i] * inv[i], v[g][2][i] * inv[i], v[g][3][i] * inv[i]);
;     asm volatile("s_waitcnt lgkmcnt(0)" ::: "memory");
; #pragma unroll
;     for (int r = 0; r < 4; ++r) { const int n = 8 * r + (lane >> 3), ch = lane & 7; const unsigned char* p = scr + n * 132 + ch * 16;
;         u32x4 o; o.x = *(const unsigned*)(p); o.y = *(const unsigned*)(p + 4); o.z = *(const unsigned*)(p + 8); o.w = *(const unsigned*)(p + 12);
;         *(u32x4*)(dst + (size_t)(drow0 + n) * Kd + k0 + 16 * ch) = o; }
;     asm volatile("s_waitcnt lgkmcnt(0)" ::: "memory");
; }
; template <int GRP>
; __device__ __forceinline__ void conv_item(Frame& F, int r) {
;     ...
;     else { constexpr int KBN = (GRP == 3) ? 16 : CMS_KB, I_E = KBN * 88; const int up = r / (8 * I_E); r %= (8 * I_E); const int e = r / I_E; r %= I_E; const int kb = r / 88, nb = r % 88, n0 = nb * 32, drow = (n0 >> 7) * 256 + up * 128 + (n0 & 127);
;         if (GRP == 3) cvt_item_i8(inptr(F, up ? IN_MU : IN_MG) + (size_t)e * D * DFE, DFE, kb * 128, n0, ws + WS_MGU + (size_t)e * 2 * DFE * D, D, drow, cmx + 2 * DFF + e * 2 * DFE + drow, scr, F.lane);
;     ...
;     for (int it = first + F.gw; it < N; it += F.NGW) conv_item<GRP>(F, it);
.LBB0_1909:
	s_mul_hi_i32 s0, s3, 0x2e8ba2e9
	s_lshr_b32 s1, s0, 31
	s_ashr_i32 s0, s0, 11
	s_add_i32 s0, s0, s1
	s_mul_i32 s1, s0, 0xffffd400
	s_lshl_b32 s6, s0, 7
	s_add_i32 s0, s3, s1
	s_mul_i32 s1, s0, 0xba3
	s_lshr_b32 s7, s1, 31
	s_ashr_i32 s1, s1, 22
	s_add_i32 s1, s1, s7
	s_mul_i32 s7, s1, 0x580
	s_sub_i32 s0, s0, s7
	s_sext_i32_i16 s38, s0
	s_mulk_i32 s38, 0xba3
	s_lshr_b32 s40, s38, 31
	s_ashr_i32 s38, s38, 18
	s_add_i32 s40, s38, s40
	s_sext_i32_i16 s38, s40
	s_mulk_i32 s40, 0x58
	s_sub_i32 s0, s0, s40
	s_sext_i32_i16 s40, s0
	s_lshl_b32 s0, s40, 5
	s_lshl_b32 s40, s40, 6
	s_and_b32 s40, s40, 0xffffff00
	s_and_b32 s41, s0, 0x60
	s_add_i32 s40, s40, s6
	s_add_i32 s39, s3, 0x2bff
	s_or_b32 s6, s40, s41
	s_cmpk_lt_u32 s39, 0x57ff
	s_cselect_b32 s39, s15, 0xa8
	v_or_b32_e32 v8, s6, v17
	s_add_i32 s39, s39, 0
	v_ashrrev_i32_e32 v9, 31, v8
	s_add_i32 s39, s39, 0x20200
	v_lshlrev_b64 v[98:99], 11, v[8:9]
	v_mov_b32_e32 v8, s39
	ds_read_b64 v[8:9], v8
	s_sext_i32_i16 s11, s1
	s_mul_i32 s9, s11, 0x1600000
	s_mul_hi_i32 s1, s11, 0x1600000
	s_mul_i32 s10, s11, 0xb00000
	s_waitcnt lgkmcnt(0)
	v_readfirstlane_b32 s39, v8
	v_readfirstlane_b32 s40, v9
	s_add_u32 s9, s39, s9
	s_addc_u32 s39, s40, s1
	s_lshl_b32 s38, s38, 7
	s_mul_hi_i32 s7, s11, 0xb00000
	s_add_u32 s10, s4, s10
	s_mul_hi_i32 s8, s11, 0x5800
	s_mulk_i32 s11, 0x5800
	s_addc_u32 s40, s12, s7
	s_add_u32 s1, s13, s11
	s_addc_u32 s8, s14, s8
	s_ashr_i32 s7, s6, 31
	v_or_b32_e32 v6, s6, v1
	v_or_b32_e32 v10, s6, v18
	v_or_b32_e32 v12, s6, v19
	s_lshl_b64 s[6:7], s[6:7], 2
	s_add_u32 s6, s1, s6
	s_addc_u32 s7, s8, s7
	s_ashr_i32 s1, s0, 31
	s_lshl_b64 s[0:1], s[0:1], 2
	v_or_b32_e32 v8, s38, v16
	s_add_u32 s0, s9, s0
	v_ashrrev_i32_e32 v11, 31, v10
	v_mul_i32_i24_e32 v8, 0x2c00, v8
	s_addc_u32 s1, s39, s1
	v_lshlrev_b64 v[100:101], 11, v[10:11]
	v_ashrrev_i32_e32 v9, 31, v8
	v_lshl_add_u64 v[10:11], s[0:1], 0, v[4:5]
	v_ashrrev_i32_e32 v7, 31, v6
	v_ashrrev_i32_e32 v13, 31, v12
	v_lshl_add_u64 v[10:11], v[10:11], 0, v[8:9]
	v_lshlrev_b64 v[14:15], 11, v[6:7]
	v_lshlrev_b64 v[6:7], 11, v[12:13]
	v_add_co_u32_e32 v12, vcc, s17, v10
	global_load_dwordx4 v[30:33], v4, s[6:7]
	s_nop 0
	v_addc_co_u32_e32 v13, vcc, 0, v11, vcc
	v_add_co_u32_e32 v42, vcc, s20, v10
	s_ashr_i32 s6, s38, 31
	s_nop 0
	v_addc_co_u32_e32 v43, vcc, 0, v11, vcc
	v_add_co_u32_e32 v46, vcc, s21, v10
	s_add_u32 s0, s10, s38
	s_nop 0
	v_addc_co_u32_e32 v47, vcc, 0, v11, vcc
	v_add_co_u32_e32 v50, vcc, s22, v10
	s_addc_u32 s1, s40, s6
	s_nop 0
	v_addc_co_u32_e32 v51, vcc, 0, v11, vcc
	v_add_co_u32_e32 v54, vcc, s23, v10
	v_lshl_add_u64 v[8:9], s[0:1], 0, v[2:3]
	s_nop 0
	v_addc_co_u32_e32 v55, vcc, 0, v11, vcc
	v_add_co_u32_e32 v58, vcc, s24, v10
	v_lshl_add_u64 v[6:7], v[8:9], 0, v[6:7]
	s_nop 0
	v_addc_co_u32_e32 v59, vcc, 0, v11, vcc
	v_add_co_u32_e32 v62, vcc, s25, v10
	s_add_i32 s3, s3, s42
	s_nop 0
	v_addc_co_u32_e32 v63, vcc, 0, v11, vcc
	v_add_co_u32_e32 v66, vcc, s26, v10
	s_cmpk_lt_i32 s3, 0x5800
	s_nop 0
	v_addc_co_u32_e32 v67, vcc, 0, v11, vcc
	v_add_co_u32_e32 v70, vcc, s27, v10
	s_waitcnt vmcnt(0)
	v_div_scale_f32 v29, s[0:1], v30, v30, s16
	v_addc_co_u32_e32 v71, vcc, 0, v11, vcc
	v_add_co_u32_e32 v74, vcc, s28, v10
	v_rcp_f32_e32 v105, v29
	s_nop 0
	v_addc_co_u32_e32 v75, vcc, 0, v11, vcc
	v_add_co_u32_e32 v78, vcc, s29, v10
	v_div_scale_f32 v103, s[0:1], v33, v33, s16
	s_nop 0
	v_addc_co_u32_e32 v79, vcc, 0, v11, vcc
	v_add_co_u32_e32 v82, vcc, s30, v10
	v_fma_f32 v109, -v29, v105, 1.0
	s_nop 0
	v_addc_co_u32_e32 v83, vcc, 0, v11, vcc
	v_add_co_u32_e32 v86, vcc, s31, v10
	v_rcp_f32_e32 v108, v103
	s_nop 0
	v_addc_co_u32_e32 v87, vcc, 0, v11, vcc
	v_add_co_u32_e32 v90, vcc, s34, v10
	v_fmac_f32_e32 v105, v109, v105
	s_nop 0
	v_addc_co_u32_e32 v91, vcc, 0, v11, vcc
	v_add_co_u32_e32 v94, vcc, s35, v10
	v_div_scale_f32 v102, s[8:9], s16, v32, s16
	s_nop 0
	v_addc_co_u32_e32 v95, vcc, 0, v11, vcc
	global_load_dwordx4 v[34:37], v[10:11], off nt
	global_load_dwordx4 v[38:41], v[12:13], off offset:3072 nt
	s_nop 0
	global_load_dwordx4 v[42:45], v[42:43], off offset:2048 nt
	s_nop 0
	global_load_dwordx4 v[46:49], v[46:47], off offset:1024 nt
	s_nop 0
	global_load_dwordx4 v[50:53], v[50:51], off nt
	s_nop 0
	global_load_dwordx4 v[54:57], v[54:55], off offset:3072 nt
	s_nop 0
	global_load_dwordx4 v[58:61], v[58:59], off offset:2048 nt
	s_nop 0
	global_load_dwordx4 v[62:65], v[62:63], off offset:1024 nt
	s_nop 0
	global_load_dwordx4 v[66:69], v[66:67], off nt
	s_nop 0
	global_load_dwordx4 v[70:73], v[70:71], off offset:3072 nt
	s_nop 0
	global_load_dwordx4 v[74:77], v[74:75], off offset:2048 nt
	s_nop 0
	global_load_dwordx4 v[78:81], v[78:79], off offset:1024 nt
	s_nop 0
	global_load_dwordx4 v[82:85], v[82:83], off nt
	s_nop 0
	global_load_dwordx4 v[86:89], v[86:87], off offset:3072 nt
	s_nop 0
	global_load_dwordx4 v[90:93], v[90:91], off offset:2048 nt
	s_nop 0
	global_load_dwordx4 v[94:97], v[94:95], off offset:1024 nt
	v_lshl_add_u64 v[12:13], v[8:9], 0, v[98:99]
	v_div_scale_f32 v99, s[0:1], v31, v31, s16
	v_rcp_f32_e32 v106, v99
	v_lshl_add_u64 v[10:11], v[8:9], 0, v[14:15]
	v_lshl_add_u64 v[14:15], v[8:9], 0, v[100:101]
	v_div_scale_f32 v101, s[0:1], v32, v32, s16
	v_rcp_f32_e32 v107, v101
	v_div_scale_f32 v98, vcc, s16, v30, s16
	v_fma_f32 v110, -v99, v106, 1.0
	v_div_scale_f32 v100, s[6:7], s16, v31, s16
	v_fmac_f32_e32 v106, v110, v106
	v_mul_f32_e32 v109, v98, v105
	v_fma_f32 v111, -v101, v107, 1.0
	v_mul_f32_e32 v110, v100, v106
	v_fma_f32 v113, -v29, v109, v98
	v_fmac_f32_e32 v107, v111, v107
	v_fma_f32 v114, -v99, v110, v100
	v_fmac_f32_e32 v109, v113, v105
	v_fma_f32 v112, -v103, v108, 1.0
	v_mul_f32_e32 v111, v102, v107
	v_fmac_f32_e32 v110, v114, v106
	v_fma_f32 v29, -v29, v109, v98
	v_div_scale_f32 v104, s[10:11], s16, v33, s16
	v_fmac_f32_e32 v108, v112, v108
	v_fma_f32 v115, -v101, v111, v102
	v_fma_f32 v98, -v99, v110, v100
	v_div_fmas_f32 v29, v29, v105, v109
	s_mov_b64 vcc, s[6:7]
	v_mul_f32_e32 v112, v104, v108
	v_fmac_f32_e32 v111, v115, v107
	v_div_fixup_f32 v29, v29, v30, s16
	v_div_fmas_f32 v98, v98, v106, v110
	v_cmp_lt_f32_e32 vcc, 0, v30
	v_fma_f32 v116, -v103, v112, v104
	v_fma_f32 v99, -v101, v111, v102
	v_cndmask_b32_e32 v29, 0, v29, vcc
	s_mov_b64 vcc, s[8:9]
	v_fmac_f32_e32 v112, v116, v108
	v_div_fixup_f32 v30, v98, v31, s16
	v_div_fmas_f32 v98, v99, v107, v111
	v_cmp_lt_f32_e32 vcc, 0, v31
	v_fma_f32 v100, -v103, v112, v104
	v_div_fixup_f32 v31, v98, v32, s16
	v_cndmask_b32_e32 v30, 0, v30, vcc
	s_mov_b64 vcc, s[10:11]
	v_div_fmas_f32 v98, v100, v108, v112
	v_cmp_lt_f32_e32 vcc, 0, v32
	v_div_fixup_f32 v32, v98, v33, s16
	s_waitcnt vmcnt(0) lgkmcnt(0)
; __device__ __forceinline__ unsigned pack_i8x4(float a, float b, float c, float d) {
;     const int ia = (int)rintf(fminf(fmaxf(a, -127.f), 127.f)), ib = (int)rintf(fminf(fmaxf(b, -127.f), 127.f)), ic = (int)rintf(fminf(fmaxf(c, -127.f), 127.f)), id = (int)rintf(fminf(fmaxf(d, -127.f), 127.f));
;     return (unsigned)(ia & 0xff) | ((unsigned)(ib & 0xff) << 8) | ((unsigned)(ic & 0xff) << 16) | ((unsigned)(id & 0xff) << 24);
; }
; __device__ __forceinline__ void cvt_item_i8(const float* src, int ld, int k0, int c0, unsigned char* dst, int Kd, int drow0, const float* cmx  , unsigned char* scr, int lane) {
;     const int c = lane & 7, q = lane >> 3;
;     const f32x4 cm = *(const f32x4*)(cmx + 4 * c);
;     f32x4 inv; inv[0] = cm[0] > 0.f ? 127.f / cm[0] : 0.f; inv[1] = cm[1] > 0.f ? 127.f / cm[1] : 0.f; inv[2] = cm[2] > 0.f ? 127.f / cm[2] : 0.f; inv[3] = cm[3] > 0.f ? 127.f / cm[3] : 0.f;
;     f32x4 v[4][4];
; #pragma unroll
;     for (int g = 0; g < 4; ++g)
; #pragma unroll
;         for (int j = 0; j < 4; ++j) v[g][j] = __builtin_nontemporal_load((const f32x4*)(src + (size_t)(k0 + 32 * g + 4 * q + j) * ld + c0 + 4 * c));
; #pragma unroll
;     for (int g = 0; g < 4; ++g)
; #pragma unroll
;         for (int i = 0; i < 4; ++i) *(unsigned*)(scr + (4 * c + i) * 132 + 32 * g + 4 * q) = pack_i8x4(v[g][0][i] * inv[i], v[g][1][i] * inv[i], v[g][2][i] * inv[i], v[g][3][i] * inv[i]);
	v_mul_f32_e32 v34, v34, v29
	v_mul_f32_e32 v38, v29, v38
	v_mul_f32_e32 v42, v29, v42
	v_mul_f32_e32 v46, v29, v46
	v_mul_f32_e32 v50, v29, v50
	v_mul_f32_e32 v54, v29, v54
	v_mul_f32_e32 v58, v29, v58
	v_mul_f32_e32 v62, v29, v62
	v_mul_f32_e32 v66, v29, v66
	v_mul_f32_e32 v70, v29, v70
	v_mul_f32_e32 v74, v29, v74
	v_mul_f32_e32 v78, v29, v78
	v_mul_f32_e32 v82, v29, v82
	v_mul_f32_e32 v86, v29, v86
	v_cndmask_b32_e32 v31, 0, v31, vcc
	v_med3_f32 v34, v34, s36, v20
	v_med3_f32 v38, v38, s36, v20
	v_med3_f32 v42, v42, s36, v20
	v_med3_f32 v46, v46, s36, v20
	v_mul_f32_e32 v39, v30, v39
	v_mul_f32_e32 v43, v30, v43
	v_mul_f32_e32 v47, v30, v47
	v_med3_f32 v50, v50, s36, v20
	v_med3_f32 v54, v54, s36, v20
	v_mul_f32_e32 v55, v30, v55
	v_cmp_lt_f32_e32 vcc, 0, v33
	v_mul_f32_e32 v90, v29, v90
	v_mul_f32_e32 v35, v35, v30
	v_med3_f32 v58, v58, s36, v20
	v_med3_f32 v62, v62, s36, v20
	v_mul_f32_e32 v51, v30, v51
	v_mul_f32_e32 v59, v30, v59
	v_mul_f32_e32 v63, v30, v63
	v_med3_f32 v66, v66, s36, v20
	v_med3_f32 v70, v70, s36, v20
	v_med3_f32 v74, v74, s36, v20
	v_med3_f32 v78, v78, s36, v20
	v_mul_f32_e32 v71, v30, v71
	v_mul_f32_e32 v79, v30, v79
	v_med3_f32 v82, v82, s36, v20
	v_med3_f32 v86, v86, s36, v20
	v_mul_f32_e32 v87, v30, v87
	v_cndmask_b32_e32 v32, 0, v32, vcc
	v_rndne_f32_e32 v33, v34
	v_rndne_f32_e32 v34, v38
	v_rndne_f32_e32 v38, v42
	v_rndne_f32_e32 v42, v46
	v_med3_f32 v39, v39, s36, v20
	v_med3_f32 v43, v43, s36, v20
	v_med3_f32 v46, v47, s36, v20
	v_mul_f32_e32 v40, v31, v40
	v_mul_f32_e32 v47, v31, v48
	v_rndne_f32_e32 v48, v50
	v_rndne_f32_e32 v50, v54
	v_med3_f32 v55, v55, s36, v20
	v_mul_f32_e32 v56, v31, v56
	v_mul_f32_e32 v29, v29, v94
	v_mul_f32_e32 v67, v30, v67
	v_mul_f32_e32 v75, v30, v75
	v_med3_f32 v90, v90, s36, v20
	v_mul_f32_e32 v83, v30, v83
	v_mul_f32_e32 v91, v30, v91
	v_med3_f32 v35, v35, s36, v20
	v_mul_f32_e32 v36, v36, v31
	v_mul_f32_e32 v44, v31, v44
	v_rndne_f32_e32 v54, v58
	v_rndne_f32_e32 v58, v62
	v_med3_f32 v51, v51, s36, v20
	v_med3_f32 v59, v59, s36, v20
	v_med3_f32 v62, v63, s36, v20
	v_mul_f32_e32 v52, v31, v52
	v_mul_f32_e32 v60, v31, v60
	v_mul_f32_e32 v63, v31, v64
	v_rndne_f32_e32 v64, v66
	v_rndne_f32_e32 v66, v70
	v_rndne_f32_e32 v70, v74
	v_rndne_f32_e32 v74, v78
	v_med3_f32 v71, v71, s36, v20
	v_med3_f32 v78, v79, s36, v20
	v_mul_f32_e32 v72, v31, v72
	v_mul_f32_e32 v79, v31, v80
	v_rndne_f32_e32 v80, v82
	v_rndne_f32_e32 v82, v86
	v_med3_f32 v87, v87, s36, v20
	v_mul_f32_e32 v88, v31, v88
	v_cvt_i32_f32_e32 v34, v34
	v_rndne_f32_e32 v39, v39
	v_rndne_f32_e32 v43, v43
	v_med3_f32 v40, v40, s36, v20
	v_mul_f32_e32 v41, v32, v41
	v_cvt_i32_f32_e32 v50, v50
	v_rndne_f32_e32 v55, v55
	v_med3_f32 v56, v56, s36, v20
	v_mul_f32_e32 v57, v32, v57
	v_med3_f32 v29, v29, s36, v20
	v_mul_f32_e32 v30, v30, v95
	v_med3_f32 v67, v67, s36, v20
	v_med3_f32 v75, v75, s36, v20
	v_mul_f32_e32 v68, v31, v68
	v_mul_f32_e32 v76, v31, v76
	v_rndne_f32_e32 v86, v90
	v_med3_f32 v83, v83, s36, v20
	v_med3_f32 v90, v91, s36, v20
	v_mul_f32_e32 v84, v31, v84
	v_mul_f32_e32 v91, v31, v92
	v_cvt_i32_f32_e32 v33, v33
	v_cvt_i32_f32_sdwa v38, v38 dst_sel:WORD_1 dst_unused:UNUSED_PAD src0_sel:DWORD
	v_rndne_f32_e32 v35, v35
	v_med3_f32 v36, v36, s36, v20
	v_med3_f32 v44, v44, s36, v20
	v_mul_f32_e32 v37, v37, v32
	v_mul_f32_e32 v45, v32, v45
	v_cvt_i32_f32_e32 v48, v48
	v_cvt_i32_f32_sdwa v54, v54 dst_sel:WORD_1 dst_unused:UNUSED_PAD src0_sel:DWORD
	v_rndne_f32_e32 v51, v51
	v_rndne_f32_e32 v59, v59
	v_med3_f32 v52, v52, s36, v20
	v_med3_f32 v60, v60, s36, v20
	v_mul_f32_e32 v53, v32, v53
	v_mul_f32_e32 v61, v32, v61
	v_cvt_i32_f32_e32 v66, v66
	v_rndne_f32_e32 v71, v71
	v_med3_f32 v72, v72, s36, v20
	v_mul_f32_e32 v73, v32, v73
	v_cvt_i32_f32_e32 v82, v82
	v_rndne_f32_e32 v87, v87
	v_med3_f32 v88, v88, s36, v20
	v_mul_f32_e32 v89, v32, v89
	v_cvt_i32_f32_e32 v39, v39
	v_cvt_i32_f32_sdwa v43, v43 dst_sel:WORD_1 dst_unused:UNUSED_PAD src0_sel:DWORD
	v_rndne_f32_e32 v40, v40
	v_med3_f32 v41, v41, s36, v20
	v_cvt_i32_f32_e32 v55, v55
	v_rndne_f32_e32 v56, v56
	v_med3_f32 v57, v57, s36, v20
	v_rndne_f32_e32 v29, v29
	v_med3_f32 v30, v30, s36, v20
	v_mul_f32_e32 v31, v31, v96
	v_cvt_i32_f32_sdwa v42, v42 dst_sel:BYTE_3 dst_unused:UNUSED_PAD src0_sel:DWORD
	v_rndne_f32_e32 v46, v46
	v_med3_f32 v47, v47, s36, v20
	v_mul_f32_e32 v49, v32, v49
	v_cvt_i32_f32_sdwa v58, v58 dst_sel:BYTE_3 dst_unused:UNUSED_PAD src0_sel:DWORD
	v_rndne_f32_e32 v62, v62
	v_med3_f32 v63, v63, s36, v20
	v_mul_f32_e32 v65, v32, v65
	v_cvt_i32_f32_e32 v64, v64
	v_cvt_i32_f32_sdwa v70, v70 dst_sel:WORD_1 dst_unused:UNUSED_PAD src0_sel:DWORD
	v_rndne_f32_e32 v67, v67
	v_rndne_f32_e32 v75, v75
	v_med3_f32 v68, v68, s36, v20
	v_med3_f32 v76, v76, s36, v20
	v_mul_f32_e32 v69, v32, v69
	v_mul_f32_e32 v77, v32, v77
	v_cvt_i32_f32_e32 v80, v80
	v_cvt_i32_f32_sdwa v86, v86 dst_sel:WORD_1 dst_unused:UNUSED_PAD src0_sel:DWORD
	v_rndne_f32_e32 v83, v83
	v_rndne_f32_e32 v90, v90
	v_med3_f32 v84, v84, s36, v20
	v_med3_f32 v91, v91, s36, v20
	v_mul_f32_e32 v85, v32, v85
	v_mul_f32_e32 v92, v32, v93
	v_cvt_i32_f32_e32 v35, v35
	v_rndne_f32_e32 v36, v36
	v_rndne_f32_e32 v44, v44
	v_med3_f32 v37, v37, s36, v20
	v_med3_f32 v45, v45, s36, v20
	v_cvt_i32_f32_e32 v51, v51
	v_cvt_i32_f32_sdwa v59, v59 dst_sel:WORD_1 dst_unused:UNUSED_PAD src0_sel:DWORD
	v_rndne_f32_e32 v52, v52
	v_rndne_f32_e32 v60, v60
	v_med3_f32 v53, v53, s36, v20
	v_med3_f32 v61, v61, s36, v20
	v_cvt_i32_f32_e32 v71, v71
	v_rndne_f32_e32 v72, v72
	v_med3_f32 v73, v73, s36, v20
	v_cvt_i32_f32_e32 v87, v87
	v_rndne_f32_e32 v88, v88
	v_med3_f32 v89, v89, s36, v20
	v_cvt_i32_f32_e32 v40, v40
; __device__ __forceinline__ unsigned pack_i8x4(float a, float b, float c, float d) {
;     const int ia = (int)rintf(fminf(fmaxf(a, -127.f), 127.f)), ib = (int)rintf(fminf(fmaxf(b, -127.f), 127.f)), ic = (int)rintf(fminf(fmaxf(c, -127.f), 127.f)), id = (int)rintf(fminf(fmaxf(d, -127.f), 127.f));
;     return (unsigned)(ia & 0xff) | ((unsigned)(ib & 0xff) << 8) | ((unsigned)(ic & 0xff) << 16) | ((unsigned)(id & 0xff) << 24);
; }
; __device__ __forceinline__ void cvt_item_i8(const float* src, int ld, int k0, int c0, unsigned char* dst, int Kd, int drow0, const float* cmx  , unsigned char* scr, int lane) {
;     const int c = lane & 7, q = lane >> 3;
;     const f32x4 cm = *(const f32x4*)(cmx + 4 * c);
;     f32x4 inv; inv[0] = cm[0] > 0.f ? 127.f / cm[0] : 0.f; inv[1] = cm[1] > 0.f ? 127.f / cm[1] : 0.f; inv[2] = cm[2] > 0.f ? 127.f / cm[2] : 0.f; inv[3] = cm[3] > 0.f ? 127.f / cm[3] : 0.f;
;     f32x4 v[4][4];
; #pragma unroll
;     for (int g = 0; g < 4; ++g)
; #pragma unroll
;         for (int j = 0; j < 4; ++j) v[g][j] = __builtin_nontemporal_load((const f32x4*)(src + (size_t)(k0 + 32 * g + 4 * q + j) * ld + c0 + 4 * c));
; #pragma unroll
;     for (int g = 0; g < 4; ++g)
; #pragma unroll
;         for (int i = 0; i < 4; ++i) *(unsigned*)(scr + (4 * c + i) * 132 + 32 * g + 4 * q) = pack_i8x4(v[g][0][i] * inv[i], v[g][1][i] * inv[i], v[g][2][i] * inv[i], v[g][3][i] * inv[i]);
;     asm volatile("s_waitcnt lgkmcnt(0)" ::: "memory");
; #pragma unroll
;     for (int r = 0; r < 4; ++r) { const int n = 8 * r + (lane >> 3), ch = lane & 7; const unsigned char* p = scr + n * 132 + ch * 16;
;         u32x4 o; o.x = *(const unsigned*)(p); o.y = *(const unsigned*)(p + 4); o.z = *(const unsigned*)(p + 8); o.w = *(const unsigned*)(p + 12);
;         *(u32x4*)(dst + (size_t)(drow0 + n) * Kd + k0 + 16 * ch) = o; }
;     asm volatile("s_waitcnt lgkmcnt(0)" ::: "memory");
; }
	v_rndne_f32_e32 v41, v41
	v_cvt_i32_f32_e32 v56, v56
	v_rndne_f32_e32 v57, v57
	v_cvt_i32_f32_sdwa v74, v74 dst_sel:BYTE_3 dst_unused:UNUSED_PAD src0_sel:DWORD
	v_rndne_f32_e32 v78, v78
	v_med3_f32 v79, v79, s36, v20
	v_mul_f32_e32 v81, v32, v81
	v_cvt_i32_f32_sdwa v29, v29 dst_sel:BYTE_3 dst_unused:UNUSED_PAD src0_sel:DWORD
	v_rndne_f32_e32 v30, v30
	v_med3_f32 v31, v31, s36, v20
	v_mul_f32_e32 v32, v32, v97
	v_cvt_i32_f32_sdwa v46, v46 dst_sel:BYTE_3 dst_unused:UNUSED_PAD src0_sel:DWORD
	v_rndne_f32_e32 v47, v47
	v_med3_f32 v49, v49, s36, v20
	v_cvt_i32_f32_sdwa v62, v62 dst_sel:BYTE_3 dst_unused:UNUSED_PAD src0_sel:DWORD
	v_rndne_f32_e32 v63, v63
	v_med3_f32 v65, v65, s36, v20
	v_cvt_i32_f32_e32 v67, v67
	v_cvt_i32_f32_sdwa v75, v75 dst_sel:WORD_1 dst_unused:UNUSED_PAD src0_sel:DWORD
	v_rndne_f32_e32 v68, v68
	v_rndne_f32_e32 v76, v76
	v_med3_f32 v69, v69, s36, v20
	v_med3_f32 v77, v77, s36, v20
	v_cvt_i32_f32_e32 v83, v83
	v_cvt_i32_f32_sdwa v90, v90 dst_sel:WORD_1 dst_unused:UNUSED_PAD src0_sel:DWORD
	v_rndne_f32_e32 v84, v84
	v_rndne_f32_e32 v91, v91
	v_med3_f32 v85, v85, s36, v20
	v_med3_f32 v92, v92, s36, v20
	v_cvt_i32_f32_e32 v36, v36
	v_cvt_i32_f32_sdwa v44, v44 dst_sel:WORD_1 dst_unused:UNUSED_PAD src0_sel:DWORD
	v_rndne_f32_e32 v37, v37
	v_rndne_f32_e32 v45, v45
	v_cvt_i32_f32_e32 v52, v52
	v_cvt_i32_f32_sdwa v60, v60 dst_sel:WORD_1 dst_unused:UNUSED_PAD src0_sel:DWORD
	v_rndne_f32_e32 v53, v53
	v_rndne_f32_e32 v61, v61
	v_cvt_i32_f32_e32 v72, v72
	v_rndne_f32_e32 v73, v73
	v_cvt_i32_f32_e32 v88, v88
	v_rndne_f32_e32 v89, v89
	v_cvt_i32_f32_e32 v41, v41
	v_cvt_i32_f32_e32 v57, v57
	v_cvt_i32_f32_sdwa v78, v78 dst_sel:BYTE_3 dst_unused:UNUSED_PAD src0_sel:DWORD
	v_rndne_f32_e32 v79, v79
	v_med3_f32 v81, v81, s36, v20
	v_cvt_i32_f32_sdwa v30, v30 dst_sel:BYTE_3 dst_unused:UNUSED_PAD src0_sel:DWORD
	v_rndne_f32_e32 v31, v31
	v_med3_f32 v32, v32, s36, v20
	v_cvt_i32_f32_sdwa v47, v47 dst_sel:BYTE_3 dst_unused:UNUSED_PAD src0_sel:DWORD
	v_rndne_f32_e32 v49, v49
	v_cvt_i32_f32_sdwa v63, v63 dst_sel:BYTE_3 dst_unused:UNUSED_PAD src0_sel:DWORD
	v_rndne_f32_e32 v65, v65
	v_cvt_i32_f32_e32 v68, v68
	v_cvt_i32_f32_sdwa v76, v76 dst_sel:WORD_1 dst_unused:UNUSED_PAD src0_sel:DWORD
	v_rndne_f32_e32 v69, v69
	v_rndne_f32_e32 v77, v77
	v_cvt_i32_f32_e32 v84, v84
	v_cvt_i32_f32_sdwa v91, v91 dst_sel:WORD_1 dst_unused:UNUSED_PAD src0_sel:DWORD
	v_rndne_f32_e32 v85, v85
	v_rndne_f32_e32 v92, v92
	v_cvt_i32_f32_e32 v37, v37
	v_cvt_i32_f32_sdwa v45, v45 dst_sel:WORD_1 dst_unused:UNUSED_PAD src0_sel:DWORD
	v_cvt_i32_f32_e32 v53, v53
	v_cvt_i32_f32_sdwa v61, v61 dst_sel:WORD_1 dst_unused:UNUSED_PAD src0_sel:DWORD
	v_cvt_i32_f32_e32 v73, v73
	v_cvt_i32_f32_e32 v89, v89
	v_lshlrev_b32_e32 v34, 8, v34
	v_lshlrev_b32_e32 v50, 8, v50
	v_cvt_i32_f32_sdwa v79, v79 dst_sel:BYTE_3 dst_unused:UNUSED_PAD src0_sel:DWORD
	v_rndne_f32_e32 v81, v81
	v_cvt_i32_f32_sdwa v31, v31 dst_sel:BYTE_3 dst_unused:UNUSED_PAD src0_sel:DWORD
	v_rndne_f32_e32 v32, v32
	v_cvt_i32_f32_sdwa v49, v49 dst_sel:BYTE_3 dst_unused:UNUSED_PAD src0_sel:DWORD
	v_cvt_i32_f32_sdwa v65, v65 dst_sel:BYTE_3 dst_unused:UNUSED_PAD src0_sel:DWORD
	v_cvt_i32_f32_e32 v69, v69
	v_cvt_i32_f32_sdwa v77, v77 dst_sel:WORD_1 dst_unused:UNUSED_PAD src0_sel:DWORD
	v_cvt_i32_f32_e32 v85, v85
	v_cvt_i32_f32_sdwa v92, v92 dst_sel:WORD_1 dst_unused:UNUSED_PAD src0_sel:DWORD
	v_and_b32_e32 v38, 0xff0000, v38
	v_and_b32_e32 v54, 0xff0000, v54
	v_lshlrev_b32_e32 v66, 8, v66
	v_lshlrev_b32_e32 v82, 8, v82
	v_perm_b32 v33, v34, v33, s37
	v_lshlrev_b32_e32 v34, 8, v39
	v_and_b32_e32 v39, 0xff0000, v43
	v_perm_b32 v43, v50, v48, s37
	v_lshlrev_b32_e32 v48, 8, v55
	v_cvt_i32_f32_sdwa v81, v81 dst_sel:BYTE_3 dst_unused:UNUSED_PAD src0_sel:DWORD
	v_cvt_i32_f32_sdwa v32, v32 dst_sel:BYTE_3 dst_unused:UNUSED_PAD src0_sel:DWORD
	v_and_b32_e32 v70, 0xff0000, v70
	v_and_b32_e32 v86, 0xff0000, v86
	v_and_b32_e32 v50, 0xff0000, v59
	v_perm_b32 v55, v66, v64, s37
	v_lshlrev_b32_e32 v59, 8, v71
	v_perm_b32 v66, v82, v80, s37
	v_lshlrev_b32_e32 v71, 8, v87
	v_or3_b32 v33, v33, v38, v42
	v_perm_b32 v34, v34, v35, s37
	v_lshlrev_b32_e32 v35, 8, v40
	v_or3_b32 v40, v43, v54, v58
	v_perm_b32 v42, v48, v51, s37
	v_lshlrev_b32_e32 v43, 8, v56
	v_and_b32_e32 v64, 0xff0000, v75
	v_and_b32_e32 v75, 0xff0000, v90
	v_and_b32_e32 v38, 0xff0000, v44
	v_and_b32_e32 v44, 0xff0000, v60
	v_or3_b32 v48, v55, v70, v74
	v_perm_b32 v51, v59, v67, s37
	v_lshlrev_b32_e32 v54, 8, v72
	v_or3_b32 v29, v66, v86, v29
	v_perm_b32 v56, v71, v83, s37
	v_lshlrev_b32_e32 v58, 8, v88
	v_or3_b32 v34, v34, v39, v46
	v_perm_b32 v35, v35, v36, s37
	v_lshlrev_b32_e32 v36, 8, v41
	ds_write2_b32 v21, v33, v40 offset1:8
	v_or3_b32 v33, v42, v50, v62
	v_perm_b32 v40, v43, v52, s37
	v_lshlrev_b32_e32 v41, 8, v57
	v_and_b32_e32 v55, 0xff0000, v76
	v_and_b32_e32 v59, 0xff0000, v91
	v_and_b32_e32 v39, 0xff0000, v45
	v_and_b32_e32 v42, 0xff0000, v61
	v_or3_b32 v43, v51, v64, v78
	v_perm_b32 v45, v54, v68, s37
	v_lshlrev_b32_e32 v46, 8, v73
	ds_write2_b32 v21, v48, v29 offset0:16 offset1:24
	v_or3_b32 v29, v56, v75, v30
	v_perm_b32 v30, v58, v84, s37
	v_lshlrev_b32_e32 v48, 8, v89
	v_or3_b32 v35, v35, v38, v47
	v_perm_b32 v36, v36, v37, s37
	ds_write2_b32 v21, v34, v33 offset0:33 offset1:41
	v_or3_b32 v33, v40, v44, v63
	v_perm_b32 v34, v41, v53, s37
	v_and_b32_e32 v50, 0xff0000, v77
	v_and_b32_e32 v51, 0xff0000, v92
	v_or3_b32 v37, v45, v55, v79
	v_perm_b32 v38, v46, v69, s37
	ds_write2_b32 v21, v43, v29 offset0:49 offset1:57
	v_or3_b32 v29, v30, v59, v31
	v_perm_b32 v30, v48, v85, s37
	v_or3_b32 v31, v36, v39, v49
	ds_write2_b32 v21, v35, v33 offset0:66 offset1:74
	v_or3_b32 v33, v34, v42, v65
	v_or3_b32 v34, v38, v50, v81
	ds_write2_b32 v21, v37, v29 offset0:82 offset1:90
	v_or3_b32 v29, v30, v51, v32
	ds_write2_b32 v21, v31, v33 offset0:99 offset1:107
	ds_write2_b32 v21, v34, v29 offset0:115 offset1:123
	s_waitcnt lgkmcnt(0)
	ds_read2_b32 v[30:31], v22 offset1:1
	ds_read2_b32 v[32:33], v22 offset0:2 offset1:3
	ds_read2_b32 v[34:35], v23 offset1:1
	ds_read2_b32 v[36:37], v24 offset1:1
	ds_read2_b32 v[38:39], v25 offset1:1
	ds_read2_b32 v[40:41], v26 offset1:1
	ds_read2_b32 v[42:43], v27 offset1:1
	ds_read2_b32 v[44:45], v28 offset1:1
	s_waitcnt lgkmcnt(6)
	global_store_dwordx4 v[10:11], v[30:33], off
	s_waitcnt lgkmcnt(4)
	global_store_dwordx4 v[12:13], v[34:37], off
	s_waitcnt lgkmcnt(2)
	global_store_dwordx4 v[14:15], v[38:41], off
	s_waitcnt lgkmcnt(0)
	global_store_dwordx4 v[6:7], v[42:45], off
	s_waitcnt lgkmcnt(0)
	s_cbranch_scc1 .LBB0_1909

; #define LBAR() do { asm volatile("s_waitcnt lgkmcnt(0)" ::: "memory"); __builtin_amdgcn_s_barrier(); asm volatile("" ::: "memory"); } while (0)
; __device__ __forceinline__ void swa_unit(Frame& F, const bf16_t* proj, const float* sinks, unsigned char* Y, int b, int kvh, int qb) {
;     ...
;     LBAR();
;     if (qb > 0) stage_kv(lds, kcol, vcol, rb + (size_t)qb * 128 - 128, 256, 0, F.tid);
;     else        stage_kv(lds, kcol, vcol, rb, 128, 128, F.tid);
;     LBAR();
;     const float sk = sinks[hq] * 1.4426950408889634f;
;     for (int sb = 0; sb < 4; ++sb) {
;         const int t = qb * 128 + sb * 32 + r32;
;         bf16x8 qf[4];
;         { const bf16_t* qrow = proj + (rb + t) * NIN + C_SQ + hq * 64 + hh * 8;
; #pragma unroll
;           for (int s = 0; s < 4; ++s) qf[s] = *(const bf16x8*)(qrow + s * 16); }
;         State st; init(st);
;         int kt0 = sb; if (qb == 0 && kt0 < 4) kt0 = 4;
;         if (kt0 == sb) tile<2>(lds, sb, qf, st, lane);
;         for (int kt = (kt0 > sb + 1 ? kt0 : sb + 1); kt < sb + 4; ++kt) tile<3>(lds, kt, qf, st, lane);
;         tile<1>(lds, sb + 4, qf, st, lane);
.LBB0_2014:
	s_lshl_b32 s0, s19, 3
	v_readlane_b32 s8, v255, 9
	s_add_i32 s0, s0, s8
	s_lshl_b32 s8, s0, 2
	s_add_u32 s8, s17, s8
	s_addc_u32 s9, s18, 0
	s_waitcnt lgkmcnt(0)
	s_barrier
	v_mov_b64_e32 v[4:5], s[8:9]
	global_load_dword v6, v[4:5], off offset:64
	v_ashrrev_i32_e32 v5, 5, v3
	v_and_b32_e32 v139, 31, v3
	v_ashrrev_i32_e32 v4, 2, v3
	v_ashrrev_i32_e32 v3, 3, v3
	v_lshlrev_b32_e32 v20, 2, v5
	s_lshl_b32 s0, s0, 6
	v_and_b32_e32 v140, -8, v4
	v_add_u32_e32 v7, -8, v139
	v_add_u32_e32 v8, -9, v139
	v_add_u32_e32 v9, -10, v139
	v_add_u32_e32 v10, -11, v139
	v_add_u32_e32 v11, -16, v139
	v_subrev_u32_e32 v12, 17, v139
	v_subrev_u32_e32 v13, 18, v139
	v_subrev_u32_e32 v14, 19, v139
	v_subrev_u32_e32 v15, 24, v139
	v_subrev_u32_e32 v16, 25, v139
	v_subrev_u32_e32 v17, 26, v139
	v_subrev_u32_e32 v19, 27, v139
	v_lshlrev_b32_e32 v21, 4, v5
	v_lshlrev_b32_e32 v5, 3, v5
	v_and_b32_e32 v4, -4, v3
	v_or_b32_e32 v22, 2, v20
	v_or_b32_e32 v23, 3, v20
	s_add_u32 s52, s5, s0
	v_lshl_or_b32 v154, s16, 7, v139
	v_mul_u32_u24_e32 v3, 0x90, v139
	v_cmp_gt_i32_e64 s[8:9], v20, v139
	v_cmp_lt_i32_e64 s[10:11], v20, v139
	v_cmp_gt_i32_e64 s[12:13], v20, v7
	v_cmp_gt_i32_e64 s[14:15], v20, v8
	v_cmp_gt_i32_e64 s[16:17], v20, v9
	v_cmp_gt_i32_e64 s[18:19], v20, v10
	v_cmp_gt_i32_e64 s[20:21], v20, v11
	v_cmp_gt_i32_e64 s[22:23], v20, v12
	v_cmp_gt_i32_e64 s[24:25], v20, v13
	v_cmp_gt_i32_e64 s[26:27], v20, v14
	v_cmp_gt_i32_e64 s[28:29], v20, v15
	v_cmp_gt_i32_e64 s[30:31], v20, v16
	v_cmp_gt_i32_e64 s[34:35], v20, v17
	v_cmp_gt_i32_e64 s[36:37], v20, v19
	v_mad_u32_u24 v7, v139, s66, v5
	v_ashrrev_i32_e32 v5, 31, v4
	v_cmp_gt_i32_e64 s[38:39], v22, v139
	v_cmp_gt_i32_e64 s[40:41], v23, v139
	s_addc_u32 s53, s33, 0
	s_mov_b32 s76, 0
	s_mov_b32 s75, 1
	v_ashrrev_i32_e32 v141, 31, v140
	v_cndmask_b32_e64 v34, v152, v18, s[8:9]
	v_cndmask_b32_e64 v35, v18, v152, s[10:11]
	v_cndmask_b32_e64 v38, v152, v18, s[12:13]
	v_cndmask_b32_e64 v39, v152, v18, s[14:15]
	v_cndmask_b32_e64 v40, v152, v18, s[16:17]
	v_cndmask_b32_e64 v41, v152, v18, s[18:19]
	v_cndmask_b32_e64 v42, v152, v18, s[20:21]
	v_cndmask_b32_e64 v43, v152, v18, s[22:23]
	v_cndmask_b32_e64 v44, v152, v18, s[24:25]
	v_cndmask_b32_e64 v45, v152, v18, s[26:27]
	v_cndmask_b32_e64 v46, v152, v18, s[28:29]
	v_cndmask_b32_e64 v47, v152, v18, s[30:31]
	v_cndmask_b32_e64 v48, v152, v18, s[34:35]
	v_cndmask_b32_e64 v49, v152, v18, s[36:37]
	v_add_u32_e32 v142, 0, v21
	v_add3_u32 v155, v3, v21, 0
	v_cndmask_b32_e64 v36, v152, v18, s[38:39]
	v_cndmask_b32_e64 v37, v152, v18, s[40:41]
	v_add_u32_e32 v156, 0, v7
	v_add_u32_e32 v157, s67, v7
	v_lshl_add_u64 v[144:145], s[52:53], 0, v[4:5]
	s_lshl_b32 s0, s0, 1
	s_waitcnt vmcnt(0) lgkmcnt(0)
	v_mul_f32_e32 v158, 0x3fb8aa3b, v6
	s_branch .LBB0_2016

; #define LAS __attribute__((address_space(3)))
; template <int YMODE, int EXTRA, bool NORM_OUT, bool XN8  , bool XIN_BF = false  , bool XOUT_BF = false  > ...
;     ...
;     for (int blk = blockIdx.x; blk < M / 64; blk += F.G) {
;         const int b = (blk * 64) / SEQ;
;         __syncthreads();
;         { const int col = 4 * F.tid;
;             if (YMODE) { const f32x4 g = *(const f32x4*)(gt + (size_t)b * 6 * D + col), p = *(const f32x4*)(gpost + col); *(LAS f32x4*)(vA + col) = g * p; }
;             if (NORM_OUT) { const f32x4 g = *(const f32x4*)(gpre + col), s = *(const f32x4*)(sc + (size_t)b * 6 * D + col); *(LAS f32x4*)(vB + col) = g * (1.f + s); *(LAS f32x4*)(vC + col) = *(const f32x4*)(sh + (size_t)b * 6 * D + col); } }
;         __syncthreads();
;         f32x4 xr[8]; u32x2 xrb[8], yr[8], yr2[8]; float w1n = 0.f, w2n = 0.f;
;     ...
;         RP_LOAD(0);
.LBB0_2175:
	s_ashr_i32 s39, s38, 31
	s_lshr_b32 s0, s39, 27
	s_add_i32 s0, s38, s0
	s_ashr_i32 s0, s0, 5
	s_mul_i32 s0, s0, 6
	s_ashr_i32 s1, s0, 31
	s_lshl_b64 s[0:1], s[0:1], 13
	v_lshl_add_u64 v[28:29], v[4:5], 0, s[0:1]
	s_waitcnt lgkmcnt(0)
	s_barrier
	global_load_dwordx4 v[24:27], v[6:7], off
	s_nop 0
	global_load_dwordx4 v[28:31], v[28:29], off
	v_lshl_add_u64 v[32:33], v[10:11], 0, s[0:1]
	v_lshl_add_u64 v[36:37], v[12:13], 0, s[0:1]
	global_load_dwordx4 v[32:35], v[32:33], off
	s_nop 0
	global_load_dwordx4 v[36:39], v[36:37], off
	s_lshl_b64 s[40:41], s[38:39], 6
	s_add_u32 s39, s40, s5
	s_addc_u32 s43, s41, 0
	s_and_b32 s0, s38, 7
	s_or_b32 s42, s39, s0
	s_lshl_b64 s[0:1], s[42:43], 12
	s_mov_b32 s77, 0
	s_waitcnt vmcnt(0) lgkmcnt(0)
	v_pk_mul_f32 v[26:27], v[30:31], v[26:27]
	v_pk_mul_f32 v[24:25], v[28:29], v[24:25]
	ds_write_b128 v1, v[24:27]
	global_load_dwordx4 v[24:27], v[8:9], off
	v_pk_add_f32 v[34:35], v[34:35], 1.0 op_sel_hi:[1,0]
	v_pk_add_f32 v[32:33], v[32:33], 1.0 op_sel_hi:[1,0]
	v_lshl_add_u64 v[30:31], v[16:17], 0, s[0:1]
	v_lshl_add_u64 v[28:29], v[14:15], 0, s[0:1]
	ds_write_b128 v115, v[36:39]
	s_waitcnt vmcnt(0) lgkmcnt(0)
	v_pk_mul_f32 v[26:27], v[26:27], v[34:35]
	v_pk_mul_f32 v[24:25], v[24:25], v[32:33]
	ds_write_b128 v114, v[24:27]
	s_waitcnt lgkmcnt(0)
	s_barrier
	global_load_dwordx2 v[96:97], v[30:31], off nt
	global_load_dwordx2 v[86:87], v[30:31], off offset:512 nt
	global_load_dwordx2 v[82:83], v[30:31], off offset:1024 nt
	global_load_dwordx2 v[80:81], v[30:31], off offset:1536 nt
	global_load_dwordx2 v[70:71], v[30:31], off offset:2048 nt
	global_load_dwordx2 v[68:69], v[30:31], off offset:2560 nt
	global_load_dwordx2 v[66:67], v[30:31], off offset:3072 nt
	global_load_dwordx2 v[64:65], v[30:31], off offset:3584 nt
	global_load_dwordx2 v[78:79], v[28:29], off nt
	global_load_dwordx2 v[76:77], v[28:29], off offset:512 nt
	global_load_dwordx2 v[74:75], v[28:29], off offset:1024 nt
	global_load_dwordx2 v[72:73], v[28:29], off offset:1536 nt
	global_load_dwordx2 v[62:63], v[28:29], off offset:2048 nt
	global_load_dwordx2 v[60:61], v[28:29], off offset:2560 nt
	global_load_dwordx2 v[56:57], v[28:29], off offset:3072 nt
	global_load_dwordx2 v[58:59], v[28:29], off offset:3584 nt
	s_waitcnt vmcnt(15)
	v_mov_b64_e32 v[26:27], v[96:97]
	s_waitcnt vmcnt(14)
	v_mov_b64_e32 v[30:31], v[86:87]
	s_waitcnt vmcnt(13)
	v_mov_b64_e32 v[34:35], v[82:83]
	s_waitcnt vmcnt(12)
	v_mov_b64_e32 v[38:39], v[80:81]
	s_waitcnt vmcnt(11)
	v_mov_b64_e32 v[42:43], v[70:71]
	s_waitcnt vmcnt(10)
	v_mov_b64_e32 v[46:47], v[68:69]
	s_waitcnt vmcnt(9)
	v_mov_b64_e32 v[50:51], v[66:67]
	s_waitcnt vmcnt(8)
	v_mov_b64_e32 v[54:55], v[64:65]
	s_waitcnt vmcnt(7)
	v_mov_b64_e32 v[24:25], v[78:79]
	s_waitcnt vmcnt(6)
	v_mov_b64_e32 v[28:29], v[76:77]
	s_waitcnt vmcnt(5)
	v_mov_b64_e32 v[32:33], v[74:75]
	s_waitcnt vmcnt(4)
	v_mov_b64_e32 v[36:37], v[72:73]
	s_waitcnt vmcnt(3)
	v_mov_b64_e32 v[40:41], v[62:63]
	s_waitcnt vmcnt(2)
	v_mov_b64_e32 v[44:45], v[60:61]
	s_waitcnt vmcnt(1)
	v_mov_b64_e32 v[48:49], v[56:57]
	s_waitcnt vmcnt(0)
	v_mov_b64_e32 v[52:53], v[58:59]
	s_branch .LBB0_2177

; #define LAS __attribute__((address_space(3)))
; template <int YMODE, int EXTRA, bool NORM_OUT, bool XN8  , bool XIN_BF = false  , bool XOUT_BF = false  > ...
;     ...
;     for (int blk = blockIdx.x; blk < M / 64; blk += F.G) {
;         const int b = (blk * 64) / SEQ;
;         __syncthreads();
;         { const int col = 4 * F.tid;
;             if (YMODE) { const f32x4 g = *(const f32x4*)(gt + (size_t)b * 6 * D + col), p = *(const f32x4*)(gpost + col); *(LAS f32x4*)(vA + col) = g * p; }
;             if (NORM_OUT) { const f32x4 g = *(const f32x4*)(gpre + col), s = *(const f32x4*)(sc + (size_t)b * 6 * D + col); *(LAS f32x4*)(vB + col) = g * (1.f + s); *(LAS f32x4*)(vC + col) = *(const f32x4*)(sh + (size_t)b * 6 * D + col); } }
;         __syncthreads();
;         f32x4 xr[8]; u32x2 xrb[8], yr[8], yr2[8]; float w1n = 0.f, w2n = 0.f;
.LBB0_2454:
	s_ashr_i32 s3, s2, 31
	s_lshr_b32 s0, s3, 27
	s_add_i32 s0, s2, s0
	s_ashr_i32 s0, s0, 5
	s_mul_i32 s0, s0, 6
	s_ashr_i32 s1, s0, 31
	s_lshl_b64 s[0:1], s[0:1], 13
	s_waitcnt lgkmcnt(0)
	s_barrier
	v_lshl_add_u64 v[4:5], v[8:9], 0, s[0:1]
	global_load_dwordx4 v[0:3], v[10:11], off
	global_load_dwordx4 v[16:19], v[4:5], off
	s_lshl_b64 s[8:9], s[2:3], 6
	s_add_u32 s3, s8, s12
	s_addc_u32 s11, s9, 0
	s_and_b32 s0, s2, 7
	s_or_b32 s10, s3, s0
	s_lshl_b64 s[0:1], s[10:11], 12
	s_lshl_b64 s[16:17], s[10:11], 4
	s_add_u32 s16, s28, s16
	s_addc_u32 s17, s29, s17
	s_waitcnt vmcnt(0) lgkmcnt(0)
	v_pk_mul_f32 v[2:3], v[18:19], v[2:3]
	v_pk_mul_f32 v[0:1], v[16:17], v[0:1]
	ds_write_b128 v13, v[0:3]
	s_waitcnt lgkmcnt(0)
	s_barrier
	global_load_dwordx4 v[2:5], v7, s[16:17]
	v_lshl_add_u64 v[0:1], v[14:15], 0, s[0:1]
	global_load_dwordx2 v[96:97], v[0:1], off nt
	global_load_dwordx2 v[94:95], v[0:1], off offset:512 nt
	global_load_dwordx2 v[92:93], v[0:1], off offset:1024 nt
	global_load_dwordx2 v[90:91], v[0:1], off offset:1536 nt
	global_load_dwordx2 v[86:87], v[0:1], off offset:2048 nt
	global_load_dwordx2 v[84:85], v[0:1], off offset:2560 nt
	global_load_dwordx2 v[82:83], v[0:1], off offset:3072 nt
	global_load_dwordx2 v[16:17], v[0:1], off offset:3584 nt
	s_waitcnt vmcnt(8)
	v_readfirstlane_b32 s1, v2
	v_readfirstlane_b32 s0, v3
	s_bfe_u32 s6, s1, 0x100010
	s_bfe_u32 s10, s0, 0x100010
	s_lshl_b32 s6, s6, 2
	s_lshl_b32 s10, s10, 2
	s_add_i32 s6, s13, s6
	s_add_i32 s10, s13, s10
	v_mov_b32_e32 v0, s6
	v_mov_b32_e32 v1, s10
	ds_read_b32 v0, v0
	ds_read_b32 v2, v1
	s_lshl_b32 s1, s1, 12
	s_lshl_b32 s0, s0, 12
	s_and_b32 s6, s1, 0xffff000
	s_waitcnt lgkmcnt(1)
	v_ashrrev_i32_e32 v1, 31, v0
	s_waitcnt lgkmcnt(0)
	v_ashrrev_i32_e32 v3, 31, v2
	v_lshlrev_b64 v[0:1], 20, v[0:1]
	v_lshlrev_b64 v[2:3], 20, v[2:3]
	v_lshl_add_u64 v[0:1], s[72:73], 0, v[0:1]
	v_lshl_add_u64 v[2:3], s[72:73], 0, v[2:3]
	v_lshl_add_u64 v[0:1], v[0:1], 0, s[6:7]
	s_and_b32 s6, s0, 0xffff000
	v_lshl_add_u64 v[2:3], v[2:3], 0, s[6:7]
	v_readfirstlane_b32 s0, v0
	v_readfirstlane_b32 s1, v1
	v_readfirstlane_b32 s16, v2
	v_readfirstlane_b32 s17, v3
	s_nop 2
	global_load_dwordx2 v[108:109], v126, s[0:1] nt
	global_load_dwordx2 v[106:107], v126, s[0:1] offset:512 nt
	global_load_dwordx2 v[102:103], v126, s[0:1] offset:1024 nt
	global_load_dwordx2 v[98:99], v126, s[0:1] offset:1536 nt
	global_load_dwordx2 v[104:105], v126, s[16:17] nt
	global_load_dwordx2 v[100:101], v126, s[16:17] offset:512 nt
	global_load_dwordx2 v[80:81], v126, s[16:17] offset:1024 nt
	global_load_dwordx2 v[76:77], v126, s[16:17] offset:1536 nt
	global_load_dwordx2 v[72:73], v126, s[16:17] offset:2048 nt
	global_load_dwordx2 v[68:69], v126, s[16:17] offset:2560 nt
	global_load_dwordx2 v[66:67], v126, s[16:17] offset:3072 nt
	global_load_dwordx2 v[64:65], v126, s[16:17] offset:3584 nt
	global_load_dwordx2 v[88:89], v126, s[0:1] offset:2048 nt
	global_load_dwordx2 v[78:79], v126, s[0:1] offset:2560 nt
	global_load_dwordx2 v[74:75], v126, s[0:1] offset:3072 nt
	global_load_dwordx2 v[70:71], v126, s[0:1] offset:3584 nt
	s_mov_b32 s16, s7
	s_waitcnt vmcnt(11)
	v_mov_b64_e32 v[0:1], v[104:105]
	s_waitcnt vmcnt(10)
	v_mov_b64_e32 v[18:19], v[100:101]
	s_waitcnt vmcnt(9)
	v_mov_b64_e32 v[20:21], v[80:81]
	s_waitcnt vmcnt(8)
	v_mov_b64_e32 v[22:23], v[76:77]
	s_waitcnt vmcnt(7)
	v_mov_b64_e32 v[24:25], v[72:73]
	s_waitcnt vmcnt(6)
	v_mov_b64_e32 v[26:27], v[68:69]
	s_waitcnt vmcnt(5)
	v_mov_b64_e32 v[28:29], v[66:67]
	s_waitcnt vmcnt(4)
	v_mov_b64_e32 v[30:31], v[64:65]
	s_branch .LBB0_2456
